# write-through sc1 on all global_store_dwordx4
# baseline (speedup 1.0000x reference)
.LBB0_48:
	s_waitcnt vmcnt(3)
	v_mul_f32_e32 v4, 0x42800000, v4
	s_waitcnt vmcnt(2)
	v_mul_f32_e32 v8, 0x42800000, v8
	v_med3_f32 v4, v4, s75, v91
	v_med3_f32 v8, v8, s75, v91
	v_mov_b32_e32 v67, v69
	v_cvt_pk_fp8_f32 v67, v4, v8
	s_waitcnt vmcnt(1)
	v_mul_f32_e32 v12, 0x42800000, v12
	s_waitcnt vmcnt(0)
	v_mul_f32_e32 v0, 0x42800000, v0
	v_med3_f32 v4, v12, s75, v91
	v_med3_f32 v0, v0, s75, v91
	v_cvt_pk_fp8_f32 v67, v4, v0 op_sel:[0,0,1]
	v_mul_f32_e32 v0, 0x42800000, v57
	v_mul_f32_e32 v4, 0x42800000, v53
	v_med3_f32 v0, v0, s75, v91
	v_med3_f32 v4, v4, s75, v91
	v_mov_b32_e32 v98, v69
	v_cvt_pk_fp8_f32 v98, v0, v4
	v_mul_f32_e32 v8, 0x42800000, v61
	v_mul_f32_e32 v0, 0x42800000, v45
	v_med3_f32 v4, v8, s75, v91
	v_med3_f32 v0, v0, s75, v91
	v_cvt_pk_fp8_f32 v98, v4, v0 op_sel:[0,0,1]
	v_mul_f32_e32 v0, 0x42800000, v41
	v_mul_f32_e32 v4, 0x42800000, v37
	v_med3_f32 v0, v0, s75, v91
	v_med3_f32 v4, v4, s75, v91
	v_mov_b32_e32 v99, v69
	v_cvt_pk_fp8_f32 v99, v0, v4
	v_mul_f32_e32 v8, 0x42800000, v49
	v_mul_f32_e32 v0, 0x42800000, v33
	v_med3_f32 v4, v8, s75, v91
	v_med3_f32 v0, v0, s75, v91
	v_cvt_pk_fp8_f32 v99, v4, v0 op_sel:[0,0,1]
	v_mul_f32_e32 v0, 0x42800000, v21
	v_mul_f32_e32 v4, 0x42800000, v25
	v_med3_f32 v0, v0, s75, v91
	v_med3_f32 v4, v4, s75, v91
	v_mov_b32_e32 v100, v69
	v_cvt_pk_fp8_f32 v100, v0, v4
	v_mul_f32_e32 v8, 0x42800000, v29
	v_mul_f32_e32 v0, 0x42800000, v17
	v_med3_f32 v4, v8, s75, v91
	v_med3_f32 v0, v0, s75, v91
	v_cvt_pk_fp8_f32 v100, v4, v0 op_sel:[0,0,1]
	v_mul_f32_e32 v0, 0x42800000, v5
	v_mul_f32_e32 v4, 0x42800000, v9
	v_med3_f32 v0, v0, s75, v91
	v_med3_f32 v4, v4, s75, v91
	v_mov_b32_e32 v101, v69
	v_cvt_pk_fp8_f32 v101, v0, v4
	v_mul_f32_e32 v5, 0x42800000, v13
	v_mul_f32_e32 v0, 0x42800000, v1
	v_med3_f32 v1, v5, s75, v91
	v_med3_f32 v0, v0, s75, v91
	v_cvt_pk_fp8_f32 v101, v1, v0 op_sel:[0,0,1]
	v_mul_f32_e32 v0, 0x42800000, v58
	v_mul_f32_e32 v1, 0x42800000, v54
	v_med3_f32 v0, v0, s75, v91
	v_med3_f32 v1, v1, s75, v91
	v_mov_b32_e32 v102, v69
	v_cvt_pk_fp8_f32 v102, v0, v1
	v_mul_f32_e32 v4, 0x42800000, v62
	v_mul_f32_e32 v0, 0x42800000, v46
	v_med3_f32 v1, v4, s75, v91
	v_med3_f32 v0, v0, s75, v91
	v_cvt_pk_fp8_f32 v102, v1, v0 op_sel:[0,0,1]
	v_mul_f32_e32 v0, 0x42800000, v42
	v_mul_f32_e32 v1, 0x42800000, v38
	v_med3_f32 v0, v0, s75, v91
	v_med3_f32 v1, v1, s75, v91
	v_mov_b32_e32 v103, v69
	v_cvt_pk_fp8_f32 v103, v0, v1
	v_mul_f32_e32 v4, 0x42800000, v50
	v_mul_f32_e32 v0, 0x42800000, v34
	v_med3_f32 v1, v4, s75, v91
	v_med3_f32 v0, v0, s75, v91
	v_cvt_pk_fp8_f32 v103, v1, v0 op_sel:[0,0,1]
	v_mul_f32_e32 v0, 0x42800000, v22
	v_mul_f32_e32 v1, 0x42800000, v26
	v_med3_f32 v0, v0, s75, v91
	v_med3_f32 v1, v1, s75, v91
	v_mov_b32_e32 v104, v69
	v_cvt_pk_fp8_f32 v104, v0, v1
	v_mul_f32_e32 v4, 0x42800000, v30
	v_mul_f32_e32 v0, 0x42800000, v18
	v_med3_f32 v1, v4, s75, v91
	v_med3_f32 v0, v0, s75, v91
	v_cvt_pk_fp8_f32 v104, v1, v0 op_sel:[0,0,1]
	v_mul_f32_e32 v0, 0x42800000, v6
	v_mul_f32_e32 v1, 0x42800000, v10
	v_med3_f32 v0, v0, s75, v91
	v_med3_f32 v1, v1, s75, v91
	v_mov_b32_e32 v105, v69
	v_cvt_pk_fp8_f32 v105, v0, v1
	v_mul_f32_e32 v4, 0x42800000, v14
	v_mul_f32_e32 v0, 0x42800000, v2
	v_med3_f32 v1, v4, s75, v91
	v_med3_f32 v0, v0, s75, v91
	v_cvt_pk_fp8_f32 v105, v1, v0 op_sel:[0,0,1]
	v_mul_f32_e32 v0, 0x42800000, v59
	v_mul_f32_e32 v1, 0x42800000, v55
	v_med3_f32 v0, v0, s75, v91
	v_med3_f32 v1, v1, s75, v91
	v_mov_b32_e32 v4, v69
	v_cvt_pk_fp8_f32 v4, v0, v1
	v_mul_f32_e32 v2, 0x42800000, v63
	v_mul_f32_e32 v0, 0x42800000, v47
	v_med3_f32 v1, v2, s75, v91
	v_med3_f32 v0, v0, s75, v91
	v_cvt_pk_fp8_f32 v4, v1, v0 op_sel:[0,0,1]
	v_mul_f32_e32 v0, 0x42800000, v43
	v_mul_f32_e32 v1, 0x42800000, v39
	v_med3_f32 v0, v0, s75, v91
	v_med3_f32 v1, v1, s75, v91
	v_mov_b32_e32 v5, v69
	v_cvt_pk_fp8_f32 v5, v0, v1
	v_mul_f32_e32 v2, 0x42800000, v51
	v_mul_f32_e32 v0, 0x42800000, v35
	v_med3_f32 v1, v2, s75, v91
	v_med3_f32 v0, v0, s75, v91
	v_cvt_pk_fp8_f32 v5, v1, v0 op_sel:[0,0,1]
	v_mul_f32_e32 v0, 0x42800000, v23
	v_mul_f32_e32 v1, 0x42800000, v27
	v_mul_f32_e32 v56, 0x42800000, v56
	v_mul_f32_e32 v52, 0x42800000, v52
	v_med3_f32 v0, v0, s75, v91
	v_med3_f32 v1, v1, s75, v91
	v_mov_b32_e32 v6, v69
	v_med3_f32 v56, v56, s75, v91
	v_med3_f32 v52, v52, s75, v91
	v_mov_b32_e32 v64, v69
	v_cvt_pk_fp8_f32 v6, v0, v1
	v_cvt_pk_fp8_f32 v64, v56, v52
	v_mul_f32_e32 v40, 0x42800000, v40
	v_mul_f32_e32 v36, 0x42800000, v36
	v_mul_f32_e32 v20, 0x42800000, v20
	v_mul_f32_e32 v24, 0x42800000, v24
	v_med3_f32 v40, v40, s75, v91
	v_med3_f32 v36, v36, s75, v91
	v_mov_b32_e32 v65, v69
	v_med3_f32 v20, v20, s75, v91
	v_med3_f32 v24, v24, s75, v91
	v_mov_b32_e32 v66, v69
	v_mul_f32_e32 v2, 0x42800000, v31
	v_mul_f32_e32 v0, 0x42800000, v19
	v_mul_f32_e32 v60, 0x42800000, v60
	v_mul_f32_e32 v44, 0x42800000, v44
	v_cvt_pk_fp8_f32 v65, v40, v36
	v_cvt_pk_fp8_f32 v66, v20, v24
	v_med3_f32 v1, v2, s75, v91
	v_med3_f32 v0, v0, s75, v91
	v_med3_f32 v52, v60, s75, v91
	v_med3_f32 v44, v44, s75, v91
	v_cvt_pk_fp8_f32 v6, v1, v0 op_sel:[0,0,1]
	v_mul_f32_e32 v0, 0x42800000, v7
	v_mul_f32_e32 v1, 0x42800000, v11
	v_cvt_pk_fp8_f32 v64, v52, v44 op_sel:[0,0,1]
	v_mul_f32_e32 v44, 0x42800000, v48
	v_mul_f32_e32 v32, 0x42800000, v32
	v_mul_f32_e32 v28, 0x42800000, v28
	v_mul_f32_e32 v16, 0x42800000, v16
	v_med3_f32 v0, v0, s75, v91
	v_med3_f32 v1, v1, s75, v91
	v_mov_b32_e32 v7, v69
	v_med3_f32 v36, v44, s75, v91
	v_med3_f32 v32, v32, s75, v91
	v_med3_f32 v20, v28, s75, v91
	v_med3_f32 v16, v16, s75, v91
	v_cvt_pk_fp8_f32 v7, v0, v1
	v_cvt_pk_fp8_f32 v65, v36, v32 op_sel:[0,0,1]
	v_cvt_pk_fp8_f32 v66, v20, v16 op_sel:[0,0,1]
	v_mul_f32_e32 v2, 0x42800000, v15
	v_mul_f32_e32 v0, 0x42800000, v3
	v_med3_f32 v1, v2, s75, v91
	v_med3_f32 v0, v0, s75, v91
	v_cvt_pk_fp8_f32 v7, v1, v0 op_sel:[0,0,1]
	s_mul_hi_i32 s1, s0, 0x380000
	s_mul_i32 s0, s0, 0x380000
	ds_write_b128 v88, v[64:67] offset:40960
	ds_write_b128 v88, v[98:101] offset:41040
	ds_write_b128 v88, v[102:105] offset:41120
	ds_write_b128 v88, v[4:7] offset:41200
	s_add_u32 s0, s42, s0
	s_waitcnt lgkmcnt(0)
	s_addc_u32 s1, s43, s1
	s_add_i32 s11, s11, s76
	s_ashr_i32 s2, s20, 31
	ds_read_b128 v[0:3], v89 offset:40960
	s_add_u32 s0, s0, s20
	v_add_u32_e32 v4, s11, v76
	s_addc_u32 s1, s1, s2
	v_ashrrev_i32_e32 v5, 31, v4
	v_lshl_add_u64 v[8:9], s[0:1], 0, v[70:71]
	v_lshlrev_b64 v[4:5], 9, v[4:5]
	v_lshl_add_u64 v[10:11], v[8:9], 0, v[4:5]
	ds_read_b128 v[4:7], v89 offset:42240
	s_waitcnt lgkmcnt(1)
	global_store_dwordx4 v[10:11], v[0:3], off sc1
	s_nop 1
	v_add_u32_e32 v0, s11, v77
	v_ashrrev_i32_e32 v1, 31, v0
	v_lshlrev_b64 v[0:1], 9, v[0:1]
	v_lshl_add_u64 v[0:1], v[8:9], 0, v[0:1]
	s_waitcnt lgkmcnt(0)
	global_store_dwordx4 v[0:1], v[4:7], off sc1
	ds_read_b128 v[0:3], v89 offset:43520
	s_nop 0
	v_add_u32_e32 v4, s11, v78
	v_ashrrev_i32_e32 v5, 31, v4
	v_lshlrev_b64 v[4:5], 9, v[4:5]
	v_lshl_add_u64 v[10:11], v[8:9], 0, v[4:5]
	ds_read_b128 v[4:7], v89 offset:44800
	s_waitcnt lgkmcnt(1)
	global_store_dwordx4 v[10:11], v[0:3], off sc1
	s_nop 1
	v_add_u32_e32 v0, s11, v79
	v_ashrrev_i32_e32 v1, 31, v0
	v_lshlrev_b64 v[0:1], 9, v[0:1]
	v_lshl_add_u64 v[0:1], v[8:9], 0, v[0:1]
	s_waitcnt lgkmcnt(0)
	global_store_dwordx4 v[0:1], v[4:7], off sc1
	s_waitcnt lgkmcnt(0)

.LBB0_78:
	s_cmpk_gt_i32 s78, 0x93
	s_cbranch_scc1 .LBB0_80
	s_lshl_b32 s26, s1, 6
	s_mul_i32 s27, s0, 0x1280000
	v_or_b32_e32 v0, s26, v75
	s_mul_hi_i32 s19, s0, 0x1280000
	s_add_u32 s27, s46, s27
	v_mul_hi_i32_i24_e32 v1, 0x9500, v0
	v_mul_i32_i24_e32 v0, 0x9500, v0
	s_addc_u32 s28, s47, s19
	v_lshl_add_u64 v[0:1], s[2:3], 0, v[0:1]
	s_ashr_i32 s19, s18, 31
	v_lshl_add_u64 v[0:1], s[18:19], 2, v[0:1]
	v_mov_b32_e32 v73, v69
	v_lshl_add_u64 v[32:33], v[0:1], 0, v[72:73]
	v_add_co_u32_e32 v0, vcc, s60, v32
	s_ashr_i32 s19, s26, 31
	s_nop 0
	v_addc_co_u32_e32 v1, vcc, 0, v33, vcc
	global_load_dwordx4 v[8:11], v[32:33], off nt
	global_load_dwordx4 v[12:15], v[0:1], off offset:1280 nt
	v_add_co_u32_e32 v0, vcc, s61, v32
	s_add_u32 s26, s27, s26
	s_nop 0
	v_addc_co_u32_e32 v1, vcc, 0, v33, vcc
	v_add_co_u32_e32 v2, vcc, s62, v32
	s_addc_u32 s27, s28, s19
	s_nop 0
	v_addc_co_u32_e32 v3, vcc, 0, v33, vcc
	global_load_dwordx4 v[20:23], v[0:1], off offset:2560 nt
	global_load_dwordx4 v[16:19], v[2:3], off offset:3840 nt
	v_add_co_u32_e32 v0, vcc, s63, v32
	s_mov_b64 s[28:29], 0
	s_nop 0
	v_addc_co_u32_e32 v1, vcc, 0, v33, vcc
	v_add_co_u32_e32 v2, vcc, s64, v32
	s_waitcnt vmcnt(3)
	v_mul_f32_e32 v8, 0x42800000, v8
	v_addc_co_u32_e32 v3, vcc, 0, v33, vcc
	global_load_dwordx4 v[24:27], v[0:1], off offset:1024 nt
	global_load_dwordx4 v[28:31], v[2:3], off offset:2304 nt
	v_add_co_u32_e32 v0, vcc, s65, v32
	s_waitcnt vmcnt(4)
	v_mul_f32_e32 v12, 0x42800000, v12
	v_addc_co_u32_e32 v1, vcc, 0, v33, vcc
	v_add_co_u32_e32 v2, vcc, s66, v32
	v_med3_f32 v12, v12, s75, v91
	s_nop 0
	v_addc_co_u32_e32 v3, vcc, 0, v33, vcc
	v_add_co_u32_e32 v34, vcc, s67, v32
	global_load_dwordx4 v[4:7], v[0:1], off offset:3584 nt
	s_nop 0
	global_load_dwordx4 v[0:3], v[2:3], off offset:768 nt
	v_addc_co_u32_e32 v35, vcc, 0, v33, vcc
	v_add_co_u32_e32 v38, vcc, s68, v32
	s_waitcnt vmcnt(5)
	v_mul_f32_e32 v20, 0x42800000, v20
	v_addc_co_u32_e32 v39, vcc, 0, v33, vcc
	v_add_co_u32_e32 v42, vcc, s69, v32
	global_load_dwordx4 v[34:37], v[34:35], off offset:2048 nt
	s_nop 0
	global_load_dwordx4 v[38:41], v[38:39], off offset:3328 nt
	v_addc_co_u32_e32 v43, vcc, 0, v33, vcc
	v_add_co_u32_e32 v46, vcc, s70, v32
	s_waitcnt vmcnt(6)
	v_mul_f32_e32 v16, 0x42800000, v16
	v_addc_co_u32_e32 v47, vcc, 0, v33, vcc
	v_add_co_u32_e32 v50, vcc, s71, v32
	global_load_dwordx4 v[42:45], v[42:43], off offset:512 nt
	s_nop 0
	global_load_dwordx4 v[46:49], v[46:47], off offset:1792 nt
	v_addc_co_u32_e32 v51, vcc, 0, v33, vcc
	v_add_co_u32_e32 v54, vcc, s72, v32
	global_load_dwordx4 v[50:53], v[50:51], off offset:3072 nt
	s_nop 0
	v_addc_co_u32_e32 v55, vcc, 0, v33, vcc
	v_add_co_u32_e32 v58, vcc, s73, v32
	global_load_dwordx4 v[54:57], v[54:55], off offset:256 nt
	s_nop 0
	v_addc_co_u32_e32 v59, vcc, 0, v33, vcc
	v_add_co_u32_e32 v32, vcc, s74, v32
	global_load_dwordx4 v[58:61], v[58:59], off offset:1536 nt
	s_nop 0
	v_addc_co_u32_e32 v33, vcc, 0, v33, vcc
	global_load_dwordx4 v[62:65], v[32:33], off offset:2816 nt
	v_med3_f32 v32, v8, s75, v91
	v_mov_b32_e32 v8, v69
	v_cvt_pk_fp8_f32 v8, v32, v12
	v_mul_f32_e32 v33, 0x42800000, v9
	v_mul_f32_e32 v66, 0x42800000, v10
	v_mul_f32_e32 v67, 0x42800000, v11
	v_med3_f32 v11, v20, s75, v91
	v_med3_f32 v16, v16, s75, v91
	v_cvt_pk_fp8_f32 v8, v11, v16 op_sel:[0,0,1]
	v_mul_f32_e32 v13, 0x42800000, v13
	v_mul_f32_e32 v12, 0x42800000, v21
	v_mul_f32_e32 v17, 0x42800000, v17
	v_mul_f32_e32 v73, 0x42800000, v15
	v_mul_f32_e32 v15, 0x42800000, v22
	v_mul_f32_e32 v14, 0x42800000, v14
	v_mul_f32_e32 v18, 0x42800000, v18
	v_mul_f32_e32 v21, 0x42800000, v23
	v_mul_f32_e32 v19, 0x42800000, v19
	s_waitcnt vmcnt(11)
	v_mul_f32_e32 v9, 0x42800000, v24
	s_waitcnt vmcnt(10)
	v_mul_f32_e32 v10, 0x42800000, v28
	v_med3_f32 v11, v9, s75, v91
	v_med3_f32 v10, v10, s75, v91
	v_mov_b32_e32 v9, v69
	v_cvt_pk_fp8_f32 v9, v11, v10
	v_mov_b32_e32 v10, v69
	v_mov_b32_e32 v11, v69
	v_mul_f32_e32 v22, 0x42800000, v25
	v_mul_f32_e32 v25, 0x42800000, v29
	v_mul_f32_e32 v23, 0x42800000, v26
	v_mul_f32_e32 v26, 0x42800000, v30
	v_mul_f32_e32 v24, 0x42800000, v27
	s_waitcnt vmcnt(9)
	v_mul_f32_e32 v4, 0x42800000, v4
	s_waitcnt vmcnt(8)
	v_mul_f32_e32 v0, 0x42800000, v0
	v_med3_f32 v4, v4, s75, v91
	v_med3_f32 v0, v0, s75, v91
	v_cvt_pk_fp8_f32 v9, v4, v0 op_sel:[0,0,1]
	v_mul_f32_e32 v16, 0x42800000, v6
	v_med3_f32 v6, v13, s75, v91
	v_mul_f32_e32 v20, 0x42800000, v7
	v_med3_f32 v7, v25, s75, v91
	v_mul_f32_e32 v1, 0x42800000, v1
	s_waitcnt vmcnt(7)
	v_mul_f32_e32 v0, 0x42800000, v34
	s_waitcnt vmcnt(6)
	v_mul_f32_e32 v4, 0x42800000, v38
	v_med3_f32 v0, v0, s75, v91
	v_med3_f32 v4, v4, s75, v91
	v_cvt_pk_fp8_f32 v10, v0, v4
	v_mul_f32_e32 v0, 0x42800000, v5
	v_med3_f32 v0, v0, s75, v91
	v_med3_f32 v1, v1, s75, v91
	v_mov_b32_e32 v13, v69
	v_mul_f32_e32 v27, 0x42800000, v31
	s_waitcnt vmcnt(5)
	v_mul_f32_e32 v4, 0x42800000, v42
	s_waitcnt vmcnt(4)
	v_mul_f32_e32 v5, 0x42800000, v46
	v_med3_f32 v4, v4, s75, v91
	v_med3_f32 v5, v5, s75, v91
	v_cvt_pk_fp8_f32 v10, v4, v5 op_sel:[0,0,1]
	s_waitcnt vmcnt(3)
	v_mul_f32_e32 v4, 0x42800000, v50
	v_med3_f32 v4, v4, s75, v91
	s_waitcnt vmcnt(2)
	v_mul_f32_e32 v5, 0x42800000, v54
	v_med3_f32 v5, v5, s75, v91
	v_cvt_pk_fp8_f32 v11, v4, v5
	v_med3_f32 v5, v33, s75, v91
	v_mov_b32_e32 v4, v69
	v_cvt_pk_fp8_f32 v4, v5, v6
	s_waitcnt vmcnt(1)
	v_mul_f32_e32 v5, 0x42800000, v58
	v_med3_f32 v5, v5, s75, v91
	s_waitcnt vmcnt(0)
	v_mul_f32_e32 v6, 0x42800000, v62
	v_med3_f32 v6, v6, s75, v91
	v_cvt_pk_fp8_f32 v11, v5, v6 op_sel:[0,0,1]
	v_med3_f32 v5, v12, s75, v91
	v_med3_f32 v6, v17, s75, v91
	v_cvt_pk_fp8_f32 v4, v5, v6 op_sel:[0,0,1]
	v_med3_f32 v6, v22, s75, v91
	v_mov_b32_e32 v5, v69
	v_cvt_pk_fp8_f32 v5, v6, v7
	v_mov_b32_e32 v6, v69
	v_mov_b32_e32 v7, v69
	v_mov_b32_e32 v12, v69
	v_cvt_pk_fp8_f32 v5, v0, v1 op_sel:[0,0,1]
	v_mul_f32_e32 v0, 0x42800000, v35
	v_mul_f32_e32 v1, 0x42800000, v39
	v_med3_f32 v0, v0, s75, v91
	v_med3_f32 v1, v1, s75, v91
	v_cvt_pk_fp8_f32 v6, v0, v1
	v_mul_f32_e32 v0, 0x42800000, v43
	v_mul_f32_e32 v1, 0x42800000, v47
	v_med3_f32 v0, v0, s75, v91
	v_med3_f32 v1, v1, s75, v91
	v_cvt_pk_fp8_f32 v6, v0, v1 op_sel:[0,0,1]
	v_mul_f32_e32 v0, 0x42800000, v51
	v_mul_f32_e32 v1, 0x42800000, v55
	v_med3_f32 v0, v0, s75, v91
	v_med3_f32 v1, v1, s75, v91
	v_cvt_pk_fp8_f32 v7, v0, v1
	v_med3_f32 v0, v66, s75, v91
	v_med3_f32 v1, v14, s75, v91
	v_cvt_pk_fp8_f32 v12, v0, v1
	v_mul_f32_e32 v0, 0x42800000, v59
	v_mul_f32_e32 v1, 0x42800000, v63
	v_med3_f32 v0, v0, s75, v91
	v_med3_f32 v1, v1, s75, v91
	v_cvt_pk_fp8_f32 v7, v0, v1 op_sel:[0,0,1]
	v_med3_f32 v0, v15, s75, v91
	v_med3_f32 v1, v18, s75, v91
	v_cvt_pk_fp8_f32 v12, v0, v1 op_sel:[0,0,1]
	v_med3_f32 v0, v23, s75, v91
	v_med3_f32 v1, v26, s75, v91
	v_cvt_pk_fp8_f32 v13, v0, v1
	v_mul_f32_e32 v1, 0x42800000, v2
	v_med3_f32 v0, v16, s75, v91
	v_med3_f32 v1, v1, s75, v91
	v_cvt_pk_fp8_f32 v13, v0, v1 op_sel:[0,0,1]
	v_mul_f32_e32 v0, 0x42800000, v36
	v_mul_f32_e32 v1, 0x42800000, v40
	v_med3_f32 v0, v0, s75, v91
	v_med3_f32 v1, v1, s75, v91
	v_mov_b32_e32 v14, v69
	v_cvt_pk_fp8_f32 v14, v0, v1
	v_mul_f32_e32 v0, 0x42800000, v44
	v_mul_f32_e32 v1, 0x42800000, v48
	v_med3_f32 v0, v0, s75, v91
	v_med3_f32 v1, v1, s75, v91
	v_cvt_pk_fp8_f32 v14, v0, v1 op_sel:[0,0,1]
	v_mul_f32_e32 v0, 0x42800000, v52
	v_mul_f32_e32 v1, 0x42800000, v56
	v_med3_f32 v0, v0, s75, v91
	v_med3_f32 v1, v1, s75, v91
	v_mov_b32_e32 v15, v69
	v_cvt_pk_fp8_f32 v15, v0, v1
	v_med3_f32 v1, v67, s75, v91
	v_med3_f32 v2, v73, s75, v91
	v_mov_b32_e32 v0, v69
	v_cvt_pk_fp8_f32 v0, v1, v2
	v_mul_f32_e32 v1, 0x42800000, v60
	v_mul_f32_e32 v2, 0x42800000, v64
	v_med3_f32 v1, v1, s75, v91
	v_med3_f32 v2, v2, s75, v91
	v_cvt_pk_fp8_f32 v15, v1, v2 op_sel:[0,0,1]
	v_med3_f32 v1, v21, s75, v91
	v_med3_f32 v2, v19, s75, v91
	v_cvt_pk_fp8_f32 v0, v1, v2 op_sel:[0,0,1]
	v_med3_f32 v2, v24, s75, v91
	v_med3_f32 v16, v27, s75, v91
	v_mov_b32_e32 v1, v69
	v_cvt_pk_fp8_f32 v1, v2, v16
	v_mul_f32_e32 v2, 0x42800000, v3
	v_med3_f32 v3, v20, s75, v91
	v_med3_f32 v2, v2, s75, v91
	v_cvt_pk_fp8_f32 v1, v3, v2 op_sel:[0,0,1]
	v_mul_f32_e32 v2, 0x42800000, v37
	v_mul_f32_e32 v3, 0x42800000, v41
	v_med3_f32 v17, v2, s75, v91
	v_med3_f32 v3, v3, s75, v91
	v_mov_b32_e32 v2, v69
	v_cvt_pk_fp8_f32 v2, v17, v3
	v_mul_f32_e32 v16, 0x42800000, v45
	v_mul_f32_e32 v3, 0x42800000, v49
	v_med3_f32 v16, v16, s75, v91
	v_med3_f32 v3, v3, s75, v91
	v_cvt_pk_fp8_f32 v2, v16, v3 op_sel:[0,0,1]
	v_mul_f32_e32 v3, 0x42800000, v53
	v_mul_f32_e32 v16, 0x42800000, v57
	v_med3_f32 v18, v3, s75, v91
	v_med3_f32 v16, v16, s75, v91
	v_mov_b32_e32 v3, v69
	v_cvt_pk_fp8_f32 v3, v18, v16
	v_mul_f32_e32 v17, 0x42800000, v61
	v_mul_f32_e32 v16, 0x42800000, v65
	v_med3_f32 v17, v17, s75, v91
	v_med3_f32 v16, v16, s75, v91
	v_cvt_pk_fp8_f32 v3, v17, v16 op_sel:[0,0,1]
	ds_write_b128 v88, v[8:11] offset:40960
	ds_write_b128 v88, v[4:7] offset:41040
	ds_write_b128 v88, v[12:15] offset:41120
	ds_write_b128 v88, v[0:3] offset:41200
	s_waitcnt lgkmcnt(0)
	ds_read_b128 v[0:3], v89 offset:40960
	v_or_b32_e32 v4, s11, v76
	v_ashrrev_i32_e32 v5, 31, v4
	v_lshl_add_u64 v[8:9], s[26:27], 0, v[70:71]
	v_lshlrev_b64 v[4:5], 11, v[4:5]
	v_lshl_add_u64 v[10:11], v[8:9], 0, v[4:5]
	ds_read_b128 v[4:7], v89 offset:42240
	s_waitcnt lgkmcnt(1)
	global_store_dwordx4 v[10:11], v[0:3], off sc1
	s_nop 1
	v_or_b32_e32 v0, s11, v77
	v_ashrrev_i32_e32 v1, 31, v0
	v_lshlrev_b64 v[0:1], 11, v[0:1]
	v_lshl_add_u64 v[0:1], v[8:9], 0, v[0:1]
	s_waitcnt lgkmcnt(0)
	global_store_dwordx4 v[0:1], v[4:7], off sc1
	ds_read_b128 v[0:3], v89 offset:43520
	s_nop 0
	v_or_b32_e32 v4, s11, v78
	v_ashrrev_i32_e32 v5, 31, v4
	v_lshlrev_b64 v[4:5], 11, v[4:5]
	v_lshl_add_u64 v[10:11], v[8:9], 0, v[4:5]
	ds_read_b128 v[4:7], v89 offset:44800
	s_waitcnt lgkmcnt(1)
	global_store_dwordx4 v[10:11], v[0:3], off sc1
	s_nop 1
	v_or_b32_e32 v0, s11, v79
	v_ashrrev_i32_e32 v1, 31, v0
	v_lshlrev_b64 v[0:1], 11, v[0:1]
	v_lshl_add_u64 v[0:1], v[8:9], 0, v[0:1]
	s_waitcnt lgkmcnt(0)
	global_store_dwordx4 v[0:1], v[4:7], off sc1
	s_waitcnt lgkmcnt(0)
.LBB0_80:
	s_and_b64 vcc, exec, s[28:29]
	s_cbranch_vccz .LBB0_49
	s_xor_b64 s[28:29], s[20:21], -1
	s_lshl_b32 s20, s1, 6
	s_mov_b64 s[26:27], -1
	s_and_b64 vcc, exec, s[28:29]
	s_cbranch_vccz .LBB0_111
	s_andn2_b64 vcc, exec, s[24:25]
	s_cbranch_vccnz .LBB0_85
	s_ashr_i32 s1, s0, 31
	s_lshl_b64 s[24:25], s[0:1], 22
	v_or_b32_e32 v0, s20, v75
	s_add_u32 s1, s49, s24
	v_mul_hi_i32_i24_e32 v1, s12, v0
	v_mul_i32_i24_e32 v0, s12, v0
	s_addc_u32 s21, s50, s25
	v_lshl_add_u64 v[0:1], v[0:1], 2, s[2:3]
	s_ashr_i32 s19, s18, 31
	v_lshl_add_u64 v[0:1], s[18:19], 2, v[0:1]
	v_mov_b32_e32 v73, v69
	v_lshl_add_u64 v[0:1], v[0:1], 0, v[72:73]
	s_lshl_b64 s[24:25], s[12:13], 2
	global_load_dwordx4 v[56:59], v[0:1], off nt
	v_lshl_add_u64 v[0:1], v[0:1], 0, s[24:25]
	global_load_dwordx4 v[60:63], v[0:1], off nt
	v_lshl_add_u64 v[0:1], v[0:1], 0, s[24:25]
	global_load_dwordx4 v[64:67], v[0:1], off nt
	v_lshl_add_u64 v[0:1], v[0:1], 0, s[24:25]
	global_load_dwordx4 v[52:55], v[0:1], off nt
	v_lshl_add_u64 v[0:1], v[0:1], 0, s[24:25]
	global_load_dwordx4 v[40:43], v[0:1], off nt
	v_lshl_add_u64 v[0:1], v[0:1], 0, s[24:25]
	global_load_dwordx4 v[44:47], v[0:1], off nt
	v_lshl_add_u64 v[0:1], v[0:1], 0, s[24:25]
	global_load_dwordx4 v[48:51], v[0:1], off nt
	v_lshl_add_u64 v[0:1], v[0:1], 0, s[24:25]
	global_load_dwordx4 v[36:39], v[0:1], off nt
	v_lshl_add_u64 v[0:1], v[0:1], 0, s[24:25]
	global_load_dwordx4 v[24:27], v[0:1], off nt
	v_lshl_add_u64 v[0:1], v[0:1], 0, s[24:25]
	global_load_dwordx4 v[28:31], v[0:1], off nt
	v_lshl_add_u64 v[0:1], v[0:1], 0, s[24:25]
	global_load_dwordx4 v[32:35], v[0:1], off nt
	v_lshl_add_u64 v[0:1], v[0:1], 0, s[24:25]
	global_load_dwordx4 v[20:23], v[0:1], off nt
	v_lshl_add_u64 v[0:1], v[0:1], 0, s[24:25]
	global_load_dwordx4 v[4:7], v[0:1], off nt
	v_lshl_add_u64 v[0:1], v[0:1], 0, s[24:25]
	global_load_dwordx4 v[12:15], v[0:1], off nt
	v_lshl_add_u64 v[0:1], v[0:1], 0, s[24:25]
	global_load_dwordx4 v[16:19], v[0:1], off nt
	v_lshl_add_u64 v[0:1], v[0:1], 0, s[24:25]
	global_load_dwordx4 v[0:3], v[0:1], off nt
	v_mov_b32_e32 v11, v69
	v_mov_b32_e32 v99, v69
	v_mov_b32_e32 v100, v69
	v_mov_b32_e32 v101, v69
	v_mov_b32_e32 v102, v69
	v_mov_b32_e32 v103, v69
	v_mov_b32_e32 v104, v69
	v_mov_b32_e32 v105, v69
	v_mov_b32_e32 v8, v69
	v_mov_b32_e32 v9, v69
	v_mov_b32_e32 v10, v69
	v_mov_b32_e32 v98, v69
	s_ashr_i32 s19, s20, 31
	s_add_u32 s24, s1, s20
	s_addc_u32 s25, s21, s19
	s_cmpk_gt_i32 s30, 0x8340
	s_waitcnt vmcnt(15)
	v_mul_f32_e32 v56, 0x42800000, v56
	v_mul_f32_e32 v57, 0x42800000, v57
	s_waitcnt vmcnt(14)
	v_mul_f32_e32 v60, 0x42800000, v60
	v_med3_f32 v56, v56, s75, v91
	v_mul_f32_e32 v61, 0x42800000, v61
	v_med3_f32 v60, v60, s75, v91
	v_med3_f32 v57, v57, s75, v91
	v_med3_f32 v61, v61, s75, v91
	s_waitcnt vmcnt(11)
	v_mul_f32_e32 v41, 0x42800000, v41
	v_med3_f32 v41, v41, s75, v91
	s_waitcnt vmcnt(10)
	v_mul_f32_e32 v45, 0x42800000, v45
	v_med3_f32 v45, v45, s75, v91
	v_cvt_pk_fp8_f32 v99, v41, v45
	s_waitcnt vmcnt(9)
	v_mul_f32_e32 v49, 0x42800000, v49
	v_mul_f32_e32 v40, 0x42800000, v40
	v_mul_f32_e32 v44, 0x42800000, v44
	s_waitcnt vmcnt(7)
	v_mul_f32_e32 v24, 0x42800000, v24
	v_med3_f32 v40, v40, s75, v91
	s_waitcnt vmcnt(6)
	v_mul_f32_e32 v28, 0x42800000, v28
	v_med3_f32 v44, v44, s75, v91
	v_med3_f32 v24, v24, s75, v91
	v_med3_f32 v28, v28, s75, v91
	v_cvt_pk_fp8_f32 v8, v56, v60
	v_cvt_pk_fp8_f32 v9, v40, v44
	s_waitcnt vmcnt(3)
	v_mul_f32_e32 v4, 0x42800000, v4
	v_med3_f32 v4, v4, s75, v91
	s_waitcnt vmcnt(2)
	v_mul_f32_e32 v12, 0x42800000, v12
	v_med3_f32 v12, v12, s75, v91
	v_cvt_pk_fp8_f32 v11, v4, v12
	s_waitcnt vmcnt(1)
	v_mul_f32_e32 v16, 0x42800000, v16
	s_waitcnt vmcnt(0)
	v_mul_f32_e32 v0, 0x42800000, v0
	v_med3_f32 v4, v16, s75, v91
	v_med3_f32 v0, v0, s75, v91
	v_cvt_pk_fp8_f32 v11, v4, v0 op_sel:[0,0,1]
	v_mul_f32_e32 v0, 0x42800000, v37
	v_med3_f32 v4, v49, s75, v91
	v_med3_f32 v0, v0, s75, v91
	v_cvt_pk_fp8_f32 v99, v4, v0 op_sel:[0,0,1]
	v_mul_f32_e32 v0, 0x42800000, v25
	v_mul_f32_e32 v4, 0x42800000, v29
	v_med3_f32 v0, v0, s75, v91
	v_med3_f32 v4, v4, s75, v91
	v_cvt_pk_fp8_f32 v100, v0, v4
	v_mul_f32_e32 v12, 0x42800000, v33
	v_mul_f32_e32 v0, 0x42800000, v21
	v_med3_f32 v4, v12, s75, v91
	v_med3_f32 v0, v0, s75, v91
	v_cvt_pk_fp8_f32 v100, v4, v0 op_sel:[0,0,1]
	v_mul_f32_e32 v0, 0x42800000, v5
	v_mul_f32_e32 v4, 0x42800000, v13
	v_med3_f32 v0, v0, s75, v91
	v_med3_f32 v4, v4, s75, v91
	v_cvt_pk_fp8_f32 v101, v0, v4
	v_mul_f32_e32 v5, 0x42800000, v17
	v_mul_f32_e32 v0, 0x42800000, v1
	v_med3_f32 v1, v5, s75, v91
	v_med3_f32 v0, v0, s75, v91
	v_cvt_pk_fp8_f32 v101, v1, v0 op_sel:[0,0,1]
	v_mul_f32_e32 v0, 0x42800000, v58
	v_mul_f32_e32 v1, 0x42800000, v62
	v_med3_f32 v0, v0, s75, v91
	v_med3_f32 v1, v1, s75, v91
	v_cvt_pk_fp8_f32 v102, v0, v1
	v_mul_f32_e32 v4, 0x42800000, v66
	v_mul_f32_e32 v0, 0x42800000, v54
	v_med3_f32 v1, v4, s75, v91
	v_med3_f32 v0, v0, s75, v91
	v_cvt_pk_fp8_f32 v102, v1, v0 op_sel:[0,0,1]
	v_mul_f32_e32 v0, 0x42800000, v42
	v_mul_f32_e32 v1, 0x42800000, v46
	v_med3_f32 v0, v0, s75, v91
	v_med3_f32 v1, v1, s75, v91
	v_cvt_pk_fp8_f32 v103, v0, v1
	v_mul_f32_e32 v4, 0x42800000, v50
	v_mul_f32_e32 v0, 0x42800000, v38
	v_med3_f32 v1, v4, s75, v91
	v_med3_f32 v0, v0, s75, v91
	v_cvt_pk_fp8_f32 v103, v1, v0 op_sel:[0,0,1]
	v_mul_f32_e32 v0, 0x42800000, v26
	v_mul_f32_e32 v1, 0x42800000, v30
	v_med3_f32 v0, v0, s75, v91
	v_med3_f32 v1, v1, s75, v91
	v_cvt_pk_fp8_f32 v104, v0, v1
	v_mul_f32_e32 v4, 0x42800000, v34
	v_mul_f32_e32 v0, 0x42800000, v22
	v_med3_f32 v1, v4, s75, v91
	v_med3_f32 v0, v0, s75, v91
	v_cvt_pk_fp8_f32 v104, v1, v0 op_sel:[0,0,1]
	v_mul_f32_e32 v0, 0x42800000, v6
	v_mul_f32_e32 v1, 0x42800000, v14
	v_med3_f32 v0, v0, s75, v91
	v_med3_f32 v1, v1, s75, v91
	v_cvt_pk_fp8_f32 v105, v0, v1
	v_mul_f32_e32 v4, 0x42800000, v18
	v_mul_f32_e32 v0, 0x42800000, v2
	v_med3_f32 v1, v4, s75, v91
	v_med3_f32 v0, v0, s75, v91
	v_cvt_pk_fp8_f32 v105, v1, v0 op_sel:[0,0,1]
	v_mul_f32_e32 v0, 0x42800000, v59
	v_mul_f32_e32 v1, 0x42800000, v63
	v_med3_f32 v0, v0, s75, v91
	v_med3_f32 v1, v1, s75, v91
	v_mov_b32_e32 v4, v69
	v_cvt_pk_fp8_f32 v4, v0, v1
	v_mul_f32_e32 v2, 0x42800000, v67
	v_mul_f32_e32 v0, 0x42800000, v55
	v_med3_f32 v1, v2, s75, v91
	v_med3_f32 v0, v0, s75, v91
	v_cvt_pk_fp8_f32 v4, v1, v0 op_sel:[0,0,1]
	v_mul_f32_e32 v0, 0x42800000, v43
	v_mul_f32_e32 v1, 0x42800000, v47
	v_med3_f32 v0, v0, s75, v91
	v_med3_f32 v1, v1, s75, v91
	v_mov_b32_e32 v5, v69
	v_cvt_pk_fp8_f32 v5, v0, v1
	v_mul_f32_e32 v2, 0x42800000, v51
	v_mul_f32_e32 v0, 0x42800000, v39
	v_med3_f32 v1, v2, s75, v91
	v_med3_f32 v0, v0, s75, v91
	v_cvt_pk_fp8_f32 v5, v1, v0 op_sel:[0,0,1]
	v_mul_f32_e32 v0, 0x42800000, v27
	v_mul_f32_e32 v1, 0x42800000, v31
	v_med3_f32 v0, v0, s75, v91
	v_med3_f32 v1, v1, s75, v91
	v_mov_b32_e32 v6, v69
	v_cvt_pk_fp8_f32 v6, v0, v1
	v_mul_f32_e32 v2, 0x42800000, v35
	v_mul_f32_e32 v0, 0x42800000, v23
	v_cvt_pk_fp8_f32 v10, v24, v28
	v_med3_f32 v1, v2, s75, v91
	v_med3_f32 v0, v0, s75, v91
	v_cvt_pk_fp8_f32 v98, v57, v61
	v_cvt_pk_fp8_f32 v6, v1, v0 op_sel:[0,0,1]
	v_mul_f32_e32 v0, 0x42800000, v7
	v_mul_f32_e32 v1, 0x42800000, v15
	v_mul_f32_e32 v64, 0x42800000, v64
	v_mul_f32_e32 v52, 0x42800000, v52
	v_mul_f32_e32 v48, 0x42800000, v48
	v_mul_f32_e32 v36, 0x42800000, v36
	v_mul_f32_e32 v32, 0x42800000, v32
	v_mul_f32_e32 v20, 0x42800000, v20
	v_med3_f32 v0, v0, s75, v91
	v_med3_f32 v1, v1, s75, v91
	v_mov_b32_e32 v7, v69
	v_mul_f32_e32 v65, 0x42800000, v65
	v_med3_f32 v64, v64, s75, v91
	v_mul_f32_e32 v53, 0x42800000, v53
	v_med3_f32 v52, v52, s75, v91
	v_med3_f32 v48, v48, s75, v91
	v_med3_f32 v36, v36, s75, v91
	v_med3_f32 v32, v32, s75, v91
	v_med3_f32 v20, v20, s75, v91
	v_cvt_pk_fp8_f32 v7, v0, v1
	v_med3_f32 v56, v65, s75, v91
	v_med3_f32 v53, v53, s75, v91
	v_cvt_pk_fp8_f32 v8, v64, v52 op_sel:[0,0,1]
	v_cvt_pk_fp8_f32 v9, v48, v36 op_sel:[0,0,1]
	v_cvt_pk_fp8_f32 v10, v32, v20 op_sel:[0,0,1]
	v_cvt_pk_fp8_f32 v98, v56, v53 op_sel:[0,0,1]
	v_mul_f32_e32 v2, 0x42800000, v19
	v_mul_f32_e32 v0, 0x42800000, v3
	v_med3_f32 v1, v2, s75, v91
	v_med3_f32 v0, v0, s75, v91
	v_cvt_pk_fp8_f32 v7, v1, v0 op_sel:[0,0,1]
	ds_write_b128 v88, v[8:11] offset:40960
	ds_write_b128 v88, v[98:101] offset:41040
	ds_write_b128 v88, v[102:105] offset:41120
	ds_write_b128 v88, v[4:7] offset:41200
	s_waitcnt lgkmcnt(0)
	ds_read_b128 v[0:3], v89 offset:40960
	v_or_b32_e32 v4, s11, v76
	v_ashrrev_i32_e32 v5, 31, v4
	v_lshl_add_u64 v[8:9], s[24:25], 0, v[70:71]
	v_lshlrev_b64 v[4:5], 11, v[4:5]
	v_lshl_add_u64 v[10:11], v[8:9], 0, v[4:5]
	ds_read_b128 v[4:7], v89 offset:42240
	s_waitcnt lgkmcnt(1)
	global_store_dwordx4 v[10:11], v[0:3], off sc1
	s_cselect_b64 s[24:25], -1, 0
	s_nop 0
	v_or_b32_e32 v0, s11, v77
	v_ashrrev_i32_e32 v1, 31, v0
	v_lshlrev_b64 v[0:1], 11, v[0:1]
	v_lshl_add_u64 v[0:1], v[8:9], 0, v[0:1]
	s_waitcnt lgkmcnt(0)
	global_store_dwordx4 v[0:1], v[4:7], off sc1
	ds_read_b128 v[0:3], v89 offset:43520
	s_nop 0
	v_or_b32_e32 v4, s11, v78
	v_ashrrev_i32_e32 v5, 31, v4
	v_lshlrev_b64 v[4:5], 11, v[4:5]
	v_lshl_add_u64 v[10:11], v[8:9], 0, v[4:5]
	ds_read_b128 v[4:7], v89 offset:44800
	s_waitcnt lgkmcnt(1)
	global_store_dwordx4 v[10:11], v[0:3], off sc1
	s_nop 1
	v_or_b32_e32 v0, s11, v79
	v_ashrrev_i32_e32 v1, 31, v0
	v_lshlrev_b64 v[0:1], 11, v[0:1]
	v_lshl_add_u64 v[0:1], v[8:9], 0, v[0:1]
	s_waitcnt lgkmcnt(0)
	global_store_dwordx4 v[0:1], v[4:7], off sc1
	s_waitcnt lgkmcnt(0)
	s_andn2_b64 vcc, exec, s[24:25]
	s_cbranch_vccz .LBB0_86
	s_branch .LBB0_110

.LBB0_86:
	s_andn2_b64 vcc, exec, s[22:23]
	s_cbranch_vccnz .LBB0_88
	s_ashr_i32 s1, s0, 31
	s_lshl_b64 s[22:23], s[0:1], 22
	s_add_u32 s1, s51, s22
	s_addc_u32 s19, s52, s23
	v_or_b32_e32 v0, s20, v75
	s_add_u32 s1, s1, s16
	v_mul_hi_i32_i24_e32 v1, s12, v0
	v_mul_i32_i24_e32 v0, s12, v0
	s_addc_u32 s21, s19, s17
	v_lshl_add_u64 v[0:1], v[0:1], 2, s[2:3]
	s_ashr_i32 s19, s18, 31
	v_lshl_add_u64 v[0:1], s[18:19], 2, v[0:1]
	v_mov_b32_e32 v73, v69
	v_lshl_add_u64 v[0:1], v[0:1], 0, v[72:73]
	s_lshl_b64 s[22:23], s[12:13], 2
	global_load_dwordx4 v[56:59], v[0:1], off nt
	v_lshl_add_u64 v[0:1], v[0:1], 0, s[22:23]
	global_load_dwordx4 v[60:63], v[0:1], off nt
	v_lshl_add_u64 v[0:1], v[0:1], 0, s[22:23]
	global_load_dwordx4 v[64:67], v[0:1], off nt
	v_lshl_add_u64 v[0:1], v[0:1], 0, s[22:23]
	global_load_dwordx4 v[52:55], v[0:1], off nt
	v_lshl_add_u64 v[0:1], v[0:1], 0, s[22:23]
	global_load_dwordx4 v[40:43], v[0:1], off nt
	v_lshl_add_u64 v[0:1], v[0:1], 0, s[22:23]
	global_load_dwordx4 v[44:47], v[0:1], off nt
	v_lshl_add_u64 v[0:1], v[0:1], 0, s[22:23]
	global_load_dwordx4 v[48:51], v[0:1], off nt
	v_lshl_add_u64 v[0:1], v[0:1], 0, s[22:23]
	global_load_dwordx4 v[36:39], v[0:1], off nt
	v_lshl_add_u64 v[0:1], v[0:1], 0, s[22:23]
	global_load_dwordx4 v[24:27], v[0:1], off nt
	v_lshl_add_u64 v[0:1], v[0:1], 0, s[22:23]
	global_load_dwordx4 v[28:31], v[0:1], off nt
	v_lshl_add_u64 v[0:1], v[0:1], 0, s[22:23]
	global_load_dwordx4 v[32:35], v[0:1], off nt
	v_lshl_add_u64 v[0:1], v[0:1], 0, s[22:23]
	global_load_dwordx4 v[20:23], v[0:1], off nt
	v_lshl_add_u64 v[0:1], v[0:1], 0, s[22:23]
	global_load_dwordx4 v[4:7], v[0:1], off nt
	v_lshl_add_u64 v[0:1], v[0:1], 0, s[22:23]
	global_load_dwordx4 v[12:15], v[0:1], off nt
	v_lshl_add_u64 v[0:1], v[0:1], 0, s[22:23]
	global_load_dwordx4 v[16:19], v[0:1], off nt
	v_lshl_add_u64 v[0:1], v[0:1], 0, s[22:23]
	global_load_dwordx4 v[0:3], v[0:1], off nt
	v_mov_b32_e32 v11, v69
	v_mov_b32_e32 v99, v69
	v_mov_b32_e32 v100, v69
	v_mov_b32_e32 v101, v69
	v_mov_b32_e32 v102, v69
	v_mov_b32_e32 v103, v69
	v_mov_b32_e32 v104, v69
	v_mov_b32_e32 v105, v69
	v_mov_b32_e32 v8, v69
	v_mov_b32_e32 v9, v69
	v_mov_b32_e32 v10, v69
	v_mov_b32_e32 v98, v69
	s_ashr_i32 s19, s20, 31
	s_add_u32 s22, s1, s20
	s_addc_u32 s23, s21, s19
	s_cmpk_gt_i32 s30, 0x8340
	s_waitcnt vmcnt(15)
	v_mul_f32_e32 v56, 0x42800000, v56
	v_mul_f32_e32 v57, 0x42800000, v57
	s_waitcnt vmcnt(14)
	v_mul_f32_e32 v60, 0x42800000, v60
	v_med3_f32 v56, v56, s75, v91
	v_mul_f32_e32 v61, 0x42800000, v61
	v_med3_f32 v60, v60, s75, v91
	v_med3_f32 v57, v57, s75, v91
	v_med3_f32 v61, v61, s75, v91
	s_waitcnt vmcnt(11)
	v_mul_f32_e32 v41, 0x42800000, v41
	v_med3_f32 v41, v41, s75, v91
	s_waitcnt vmcnt(10)
	v_mul_f32_e32 v45, 0x42800000, v45
	v_med3_f32 v45, v45, s75, v91
	v_cvt_pk_fp8_f32 v99, v41, v45
	s_waitcnt vmcnt(9)
	v_mul_f32_e32 v49, 0x42800000, v49
	v_mul_f32_e32 v40, 0x42800000, v40
	v_mul_f32_e32 v44, 0x42800000, v44
	s_waitcnt vmcnt(7)
	v_mul_f32_e32 v24, 0x42800000, v24
	v_med3_f32 v40, v40, s75, v91
	s_waitcnt vmcnt(6)
	v_mul_f32_e32 v28, 0x42800000, v28
	v_med3_f32 v44, v44, s75, v91
	v_med3_f32 v24, v24, s75, v91
	v_med3_f32 v28, v28, s75, v91
	v_cvt_pk_fp8_f32 v8, v56, v60
	v_cvt_pk_fp8_f32 v9, v40, v44
	s_waitcnt vmcnt(3)
	v_mul_f32_e32 v4, 0x42800000, v4
	v_med3_f32 v4, v4, s75, v91
	s_waitcnt vmcnt(2)
	v_mul_f32_e32 v12, 0x42800000, v12
	v_med3_f32 v12, v12, s75, v91
	v_cvt_pk_fp8_f32 v11, v4, v12
	s_waitcnt vmcnt(1)
	v_mul_f32_e32 v16, 0x42800000, v16
	s_waitcnt vmcnt(0)
	v_mul_f32_e32 v0, 0x42800000, v0
	v_med3_f32 v4, v16, s75, v91
	v_med3_f32 v0, v0, s75, v91
	v_cvt_pk_fp8_f32 v11, v4, v0 op_sel:[0,0,1]
	v_mul_f32_e32 v0, 0x42800000, v37
	v_med3_f32 v4, v49, s75, v91
	v_med3_f32 v0, v0, s75, v91
	v_cvt_pk_fp8_f32 v99, v4, v0 op_sel:[0,0,1]
	v_mul_f32_e32 v0, 0x42800000, v25
	v_mul_f32_e32 v4, 0x42800000, v29
	v_med3_f32 v0, v0, s75, v91
	v_med3_f32 v4, v4, s75, v91
	v_cvt_pk_fp8_f32 v100, v0, v4
	v_mul_f32_e32 v12, 0x42800000, v33
	v_mul_f32_e32 v0, 0x42800000, v21
	v_med3_f32 v4, v12, s75, v91
	v_med3_f32 v0, v0, s75, v91
	v_cvt_pk_fp8_f32 v100, v4, v0 op_sel:[0,0,1]
	v_mul_f32_e32 v0, 0x42800000, v5
	v_mul_f32_e32 v4, 0x42800000, v13
	v_med3_f32 v0, v0, s75, v91
	v_med3_f32 v4, v4, s75, v91
	v_cvt_pk_fp8_f32 v101, v0, v4
	v_mul_f32_e32 v5, 0x42800000, v17
	v_mul_f32_e32 v0, 0x42800000, v1
	v_med3_f32 v1, v5, s75, v91
	v_med3_f32 v0, v0, s75, v91
	v_cvt_pk_fp8_f32 v101, v1, v0 op_sel:[0,0,1]
	v_mul_f32_e32 v0, 0x42800000, v58
	v_mul_f32_e32 v1, 0x42800000, v62
	v_med3_f32 v0, v0, s75, v91
	v_med3_f32 v1, v1, s75, v91
	v_cvt_pk_fp8_f32 v102, v0, v1
	v_mul_f32_e32 v4, 0x42800000, v66
	v_mul_f32_e32 v0, 0x42800000, v54
	v_med3_f32 v1, v4, s75, v91
	v_med3_f32 v0, v0, s75, v91
	v_cvt_pk_fp8_f32 v102, v1, v0 op_sel:[0,0,1]
	v_mul_f32_e32 v0, 0x42800000, v42
	v_mul_f32_e32 v1, 0x42800000, v46
	v_med3_f32 v0, v0, s75, v91
	v_med3_f32 v1, v1, s75, v91
	v_cvt_pk_fp8_f32 v103, v0, v1
	v_mul_f32_e32 v4, 0x42800000, v50
	v_mul_f32_e32 v0, 0x42800000, v38
	v_med3_f32 v1, v4, s75, v91
	v_med3_f32 v0, v0, s75, v91
	v_cvt_pk_fp8_f32 v103, v1, v0 op_sel:[0,0,1]
	v_mul_f32_e32 v0, 0x42800000, v26
	v_mul_f32_e32 v1, 0x42800000, v30
	v_med3_f32 v0, v0, s75, v91
	v_med3_f32 v1, v1, s75, v91
	v_cvt_pk_fp8_f32 v104, v0, v1
	v_mul_f32_e32 v4, 0x42800000, v34
	v_mul_f32_e32 v0, 0x42800000, v22
	v_med3_f32 v1, v4, s75, v91
	v_med3_f32 v0, v0, s75, v91
	v_cvt_pk_fp8_f32 v104, v1, v0 op_sel:[0,0,1]
	v_mul_f32_e32 v0, 0x42800000, v6
	v_mul_f32_e32 v1, 0x42800000, v14
	v_med3_f32 v0, v0, s75, v91
	v_med3_f32 v1, v1, s75, v91
	v_cvt_pk_fp8_f32 v105, v0, v1
	v_mul_f32_e32 v4, 0x42800000, v18
	v_mul_f32_e32 v0, 0x42800000, v2
	v_med3_f32 v1, v4, s75, v91
	v_med3_f32 v0, v0, s75, v91
	v_cvt_pk_fp8_f32 v105, v1, v0 op_sel:[0,0,1]
	v_mul_f32_e32 v0, 0x42800000, v59
	v_mul_f32_e32 v1, 0x42800000, v63
	v_med3_f32 v0, v0, s75, v91
	v_med3_f32 v1, v1, s75, v91
	v_mov_b32_e32 v4, v69
	v_cvt_pk_fp8_f32 v4, v0, v1
	v_mul_f32_e32 v2, 0x42800000, v67
	v_mul_f32_e32 v0, 0x42800000, v55
	v_med3_f32 v1, v2, s75, v91
	v_med3_f32 v0, v0, s75, v91
	v_cvt_pk_fp8_f32 v4, v1, v0 op_sel:[0,0,1]
	v_mul_f32_e32 v0, 0x42800000, v43
	v_mul_f32_e32 v1, 0x42800000, v47
	v_med3_f32 v0, v0, s75, v91
	v_med3_f32 v1, v1, s75, v91
	v_mov_b32_e32 v5, v69
	v_cvt_pk_fp8_f32 v5, v0, v1
	v_mul_f32_e32 v2, 0x42800000, v51
	v_mul_f32_e32 v0, 0x42800000, v39
	v_med3_f32 v1, v2, s75, v91
	v_med3_f32 v0, v0, s75, v91
	v_cvt_pk_fp8_f32 v5, v1, v0 op_sel:[0,0,1]
	v_mul_f32_e32 v0, 0x42800000, v27
	v_mul_f32_e32 v1, 0x42800000, v31
	v_med3_f32 v0, v0, s75, v91
	v_med3_f32 v1, v1, s75, v91
	v_mov_b32_e32 v6, v69
	v_cvt_pk_fp8_f32 v6, v0, v1
	v_mul_f32_e32 v2, 0x42800000, v35
	v_mul_f32_e32 v0, 0x42800000, v23
	v_cvt_pk_fp8_f32 v10, v24, v28
	v_med3_f32 v1, v2, s75, v91
	v_med3_f32 v0, v0, s75, v91
	v_cvt_pk_fp8_f32 v98, v57, v61
	v_cvt_pk_fp8_f32 v6, v1, v0 op_sel:[0,0,1]
	v_mul_f32_e32 v0, 0x42800000, v7
	v_mul_f32_e32 v1, 0x42800000, v15
	v_mul_f32_e32 v64, 0x42800000, v64
	v_mul_f32_e32 v52, 0x42800000, v52
	v_mul_f32_e32 v48, 0x42800000, v48
	v_mul_f32_e32 v36, 0x42800000, v36
	v_mul_f32_e32 v32, 0x42800000, v32
	v_mul_f32_e32 v20, 0x42800000, v20
	v_med3_f32 v0, v0, s75, v91
	v_med3_f32 v1, v1, s75, v91
	v_mov_b32_e32 v7, v69
	v_mul_f32_e32 v65, 0x42800000, v65
	v_med3_f32 v64, v64, s75, v91
	v_mul_f32_e32 v53, 0x42800000, v53
	v_med3_f32 v52, v52, s75, v91
	v_med3_f32 v48, v48, s75, v91
	v_med3_f32 v36, v36, s75, v91
	v_med3_f32 v32, v32, s75, v91
	v_med3_f32 v20, v20, s75, v91
	v_cvt_pk_fp8_f32 v7, v0, v1
	v_med3_f32 v56, v65, s75, v91
	v_med3_f32 v53, v53, s75, v91
	v_cvt_pk_fp8_f32 v8, v64, v52 op_sel:[0,0,1]
	v_cvt_pk_fp8_f32 v9, v48, v36 op_sel:[0,0,1]
	v_cvt_pk_fp8_f32 v10, v32, v20 op_sel:[0,0,1]
	v_cvt_pk_fp8_f32 v98, v56, v53 op_sel:[0,0,1]
	v_mul_f32_e32 v2, 0x42800000, v19
	v_mul_f32_e32 v0, 0x42800000, v3
	v_med3_f32 v1, v2, s75, v91
	v_med3_f32 v0, v0, s75, v91
	v_cvt_pk_fp8_f32 v7, v1, v0 op_sel:[0,0,1]
	ds_write_b128 v88, v[8:11] offset:40960
	ds_write_b128 v88, v[98:101] offset:41040
	ds_write_b128 v88, v[102:105] offset:41120
	ds_write_b128 v88, v[4:7] offset:41200
	s_waitcnt lgkmcnt(0)
	ds_read_b128 v[0:3], v89 offset:40960
	v_or_b32_e32 v4, s11, v76
	v_ashrrev_i32_e32 v5, 31, v4
	v_lshl_add_u64 v[8:9], s[22:23], 0, v[70:71]
	v_lshlrev_b64 v[4:5], 11, v[4:5]
	v_lshl_add_u64 v[10:11], v[8:9], 0, v[4:5]
	ds_read_b128 v[4:7], v89 offset:42240
	s_waitcnt lgkmcnt(1)
	global_store_dwordx4 v[10:11], v[0:3], off sc1
	s_cselect_b64 s[22:23], -1, 0
	s_nop 0
	v_or_b32_e32 v0, s11, v77
	v_ashrrev_i32_e32 v1, 31, v0
	v_lshlrev_b64 v[0:1], 11, v[0:1]
	v_lshl_add_u64 v[0:1], v[8:9], 0, v[0:1]
	s_waitcnt lgkmcnt(0)
	global_store_dwordx4 v[0:1], v[4:7], off sc1
	ds_read_b128 v[0:3], v89 offset:43520
	s_nop 0
	v_or_b32_e32 v4, s11, v78
	v_ashrrev_i32_e32 v5, 31, v4
	v_lshlrev_b64 v[4:5], 11, v[4:5]
	v_lshl_add_u64 v[10:11], v[8:9], 0, v[4:5]
	ds_read_b128 v[4:7], v89 offset:44800
	s_waitcnt lgkmcnt(1)
	global_store_dwordx4 v[10:11], v[0:3], off sc1
	s_nop 1
	v_or_b32_e32 v0, s11, v79
	v_ashrrev_i32_e32 v1, 31, v0
	v_lshlrev_b64 v[0:1], 11, v[0:1]
	v_lshl_add_u64 v[0:1], v[8:9], 0, v[0:1]
	s_waitcnt lgkmcnt(0)
	global_store_dwordx4 v[0:1], v[4:7], off sc1
	s_waitcnt lgkmcnt(0)
	s_andn2_b64 vcc, exec, s[22:23]
	s_cbranch_vccz .LBB0_89
	s_branch .LBB0_110

.LBB0_93:
	s_lshl_b64 s[16:17], s[16:17], 1
	s_add_u32 s1, s8, s16
	s_addc_u32 s16, s9, s17
	s_ashr_i32 s21, s20, 31
	s_lshl_b64 s[8:9], s[20:21], 1
	s_waitcnt lgkmcnt(0)
	s_add_u32 s8, s1, s8
	s_addc_u32 s9, s16, s9
	v_or_b32_e32 v0, s11, v80
	v_lshl_add_u64 v[4:5], s[8:9], 0, v[68:69]
	s_mov_b64 s[8:9], -1
	s_and_b64 vcc, exec, s[22:23]
	v_mul_hi_i32_i24_e32 v7, s10, v0
	v_mul_i32_i24_e32 v6, s10, v0
	s_cbranch_vccz .LBB0_95
	v_lshl_add_u64 v[0:1], v[6:7], 1, v[4:5]
	global_store_dwordx4 v[0:1], v[94:97], off sc1
	s_mov_b64 s[8:9], 0
.LBB0_95:
	v_mov_b32_e32 v0, 0
	s_andn2_b64 vcc, exec, s[8:9]
	v_mov_b32_e32 v1, 0
	v_mov_b32_e32 v2, 0
	v_mov_b32_e32 v3, 0
	s_cbranch_vccnz .LBB0_97
	ds_read_b128 v[8:11], v92 offset:40960
	ds_read_b128 v[0:3], v92 offset:42112
	v_lshl_add_u64 v[6:7], v[6:7], 1, v[4:5]
	s_waitcnt lgkmcnt(1)
	global_store_dwordx4 v[6:7], v[8:11], off sc1
.LBB0_97:
	v_or_b32_e32 v6, s11, v81
	v_mul_hi_i32_i24_e32 v7, s10, v6
	v_mul_i32_i24_e32 v6, s10, v6
	v_lshl_add_u64 v[6:7], v[6:7], 1, v[4:5]
	s_waitcnt lgkmcnt(0)
	global_store_dwordx4 v[6:7], v[0:3], off sc1
	s_mov_b64 s[8:9], -1
	s_and_b64 vcc, exec, s[22:23]
	v_or_b32_e32 v0, s11, v82
	v_mul_hi_i32_i24_e32 v7, s10, v0
	v_mul_i32_i24_e32 v6, s10, v0
	s_cbranch_vccz .LBB0_99
	v_lshl_add_u64 v[0:1], v[6:7], 1, v[4:5]
	global_store_dwordx4 v[0:1], v[94:97], off sc1
	s_mov_b64 s[8:9], 0
.LBB0_99:
	v_mov_b32_e32 v0, 0
	s_andn2_b64 vcc, exec, s[8:9]
	v_mov_b32_e32 v1, 0
	v_mov_b32_e32 v2, 0
	v_mov_b32_e32 v3, 0
	s_cbranch_vccnz .LBB0_101
	ds_read_b128 v[8:11], v92 offset:43264
	ds_read_b128 v[0:3], v92 offset:44416
	v_lshl_add_u64 v[6:7], v[6:7], 1, v[4:5]
	s_waitcnt lgkmcnt(1)
	global_store_dwordx4 v[6:7], v[8:11], off sc1
.LBB0_101:
	v_or_b32_e32 v6, s11, v83
	v_mul_hi_i32_i24_e32 v7, s10, v6
	v_mul_i32_i24_e32 v6, s10, v6
	v_lshl_add_u64 v[6:7], v[6:7], 1, v[4:5]
	s_waitcnt lgkmcnt(0)
	global_store_dwordx4 v[6:7], v[0:3], off sc1
	s_mov_b64 s[8:9], -1
	s_and_b64 vcc, exec, s[22:23]
	v_or_b32_e32 v0, s11, v84
	v_mul_hi_i32_i24_e32 v7, s10, v0
	v_mul_i32_i24_e32 v6, s10, v0
	s_cbranch_vccz .LBB0_103
	v_lshl_add_u64 v[0:1], v[6:7], 1, v[4:5]
	global_store_dwordx4 v[0:1], v[94:97], off sc1
	s_mov_b64 s[8:9], 0
.LBB0_103:
	v_mov_b32_e32 v0, 0
	s_andn2_b64 vcc, exec, s[8:9]
	v_mov_b32_e32 v1, 0
	v_mov_b32_e32 v2, 0
	v_mov_b32_e32 v3, 0
	s_cbranch_vccnz .LBB0_105
	ds_read_b128 v[8:11], v92 offset:45568
	ds_read_b128 v[0:3], v92 offset:46720
	v_lshl_add_u64 v[6:7], v[6:7], 1, v[4:5]
	s_waitcnt lgkmcnt(1)
	global_store_dwordx4 v[6:7], v[8:11], off sc1
.LBB0_105:
	v_or_b32_e32 v6, s11, v85
	v_mul_hi_i32_i24_e32 v7, s10, v6
	v_mul_i32_i24_e32 v6, s10, v6
	v_lshl_add_u64 v[6:7], v[6:7], 1, v[4:5]
	s_waitcnt lgkmcnt(0)
	global_store_dwordx4 v[6:7], v[0:3], off sc1
	s_mov_b64 s[8:9], -1
	s_and_b64 vcc, exec, s[22:23]
	v_or_b32_e32 v0, s11, v86
	v_mul_hi_i32_i24_e32 v7, s10, v0
	v_mul_i32_i24_e32 v6, s10, v0
	s_cbranch_vccz .LBB0_107
	v_lshl_add_u64 v[0:1], v[6:7], 1, v[4:5]
	global_store_dwordx4 v[0:1], v[94:97], off sc1
	s_mov_b64 s[8:9], 0
.LBB0_107:
	v_mov_b32_e32 v0, 0
	s_andn2_b64 vcc, exec, s[8:9]
	v_mov_b32_e32 v1, 0
	v_mov_b32_e32 v2, 0
	v_mov_b32_e32 v3, 0
	s_cbranch_vccnz .LBB0_109
	ds_read_b128 v[8:11], v92 offset:47872
	ds_read_b128 v[0:3], v92 offset:49024
	v_lshl_add_u64 v[6:7], v[6:7], 1, v[4:5]
	s_waitcnt lgkmcnt(1)
	global_store_dwordx4 v[6:7], v[8:11], off sc1
.LBB0_109:
	v_or_b32_e32 v6, s11, v87
	v_mul_hi_i32_i24_e32 v7, s10, v6
	v_mul_i32_i24_e32 v6, s10, v6
	v_lshl_add_u64 v[4:5], v[6:7], 1, v[4:5]
	s_waitcnt lgkmcnt(0)
	global_store_dwordx4 v[4:5], v[0:3], off sc1
	s_waitcnt lgkmcnt(0)

.LBB0_267:
	v_lshl_or_b32 v152, s67, 9, v183
	s_waitcnt lgkmcnt(0)
	v_lshl_add_u64 v[2:3], s[8:9], 0, v[152:153]
	v_mad_i64_i32 v[4:5], s[22:23], v0, s55, v[2:3]
	v_cvt_pk_bf16_f32 v10, v10, v11
	v_cvt_pk_bf16_f32 v11, v6, v7
	v_cvt_pk_bf16_f32 v12, v12, v13
	v_cvt_pk_bf16_f32 v13, v8, v9
	global_store_dwordx4 v[4:5], v[10:13], off sc1
	v_pk_mul_f32 v[6:7], v[134:135], s[16:17] op_sel_hi:[1,0]
	v_pk_mul_f32 v[8:9], v[130:131], s[16:17] op_sel_hi:[1,0]
	v_pk_mul_f32 v[10:11], v[132:133], s[16:17] op_sel_hi:[1,0]
	s_and_b64 vcc, exec, s[4:5]
	v_pk_mul_f32 v[12:13], v[128:129], s[16:17] op_sel_hi:[1,0]
	s_cbranch_vccnz .LBB0_269
	v_mul_f32_e32 v1, 0xbfb8aa3b, v10
	v_exp_f32_e32 v1, v1
	v_mul_f32_e32 v10, 0xbfb8aa3b, v12
	v_exp_f32_e32 v10, v10
	v_mul_f32_e32 v6, 0xbfb8aa3b, v6
	v_add_f32_e32 v1, 1.0, v1
	v_exp_f32_e32 v6, v6
	v_add_f32_e32 v12, 1.0, v10
	v_rcp_f32_e32 v10, v1
	v_mul_f32_e32 v1, 0xbfb8aa3b, v11
	v_exp_f32_e32 v1, v1
	v_mul_f32_e32 v11, 0xbfb8aa3b, v13
	v_exp_f32_e32 v13, v11
	v_mul_f32_e32 v8, 0xbfb8aa3b, v8
	v_exp_f32_e32 v8, v8
	v_add_f32_e32 v1, 1.0, v1
	v_rcp_f32_e32 v11, v1
	v_add_f32_e32 v1, 1.0, v13
	v_rcp_f32_e32 v13, v1
	v_add_f32_e32 v1, 1.0, v6
	v_mul_f32_e32 v7, 0xbfb8aa3b, v7
	v_rcp_f32_e32 v6, v1
	v_add_f32_e32 v1, 1.0, v8
	v_exp_f32_e32 v7, v7
	v_mul_f32_e32 v8, 0xbfb8aa3b, v9
	v_exp_f32_e32 v9, v8
	v_rcp_f32_e32 v8, v1
	v_add_f32_e32 v1, 1.0, v7
	v_rcp_f32_e32 v7, v1
	v_add_f32_e32 v1, 1.0, v9
	v_rcp_f32_e32 v12, v12
	v_rcp_f32_e32 v9, v1
.LBB0_269:
	v_cvt_pk_bf16_f32 v10, v10, v11
	v_cvt_pk_bf16_f32 v11, v6, v7
	v_cvt_pk_bf16_f32 v12, v12, v13
	v_cvt_pk_bf16_f32 v13, v8, v9
	global_store_dwordx4 v[4:5], v[10:13], off offset:256 sc1
	v_pk_mul_f32 v[6:7], v[126:127], s[16:17] op_sel_hi:[1,0]
	v_pk_mul_f32 v[8:9], v[122:123], s[16:17] op_sel_hi:[1,0]
	v_pk_mul_f32 v[10:11], v[124:125], s[16:17] op_sel_hi:[1,0]
	s_and_b64 vcc, exec, s[4:5]
	v_pk_mul_f32 v[12:13], v[120:121], s[16:17] op_sel_hi:[1,0]
	s_cbranch_vccnz .LBB0_271
	v_mul_f32_e32 v1, 0xbfb8aa3b, v10
	v_exp_f32_e32 v1, v1
	v_mul_f32_e32 v4, 0xbfb8aa3b, v12
	v_exp_f32_e32 v4, v4
	v_mul_f32_e32 v5, 0xbfb8aa3b, v13
	v_add_f32_e32 v1, 1.0, v1
	v_rcp_f32_e32 v10, v1
	v_mul_f32_e32 v1, 0xbfb8aa3b, v11
	v_exp_f32_e32 v1, v1
	v_exp_f32_e32 v5, v5
	v_add_f32_e32 v4, 1.0, v4
	v_rcp_f32_e32 v12, v4
	v_add_f32_e32 v1, 1.0, v1
	v_mul_f32_e32 v4, 0xbfb8aa3b, v6
	v_rcp_f32_e32 v11, v1
	v_add_f32_e32 v1, 1.0, v5
	v_exp_f32_e32 v4, v4
	v_mul_f32_e32 v5, 0xbfb8aa3b, v8
	v_exp_f32_e32 v5, v5
	v_rcp_f32_e32 v13, v1
	v_add_f32_e32 v1, 1.0, v4
	v_mul_f32_e32 v4, 0xbfb8aa3b, v7
	v_rcp_f32_e32 v6, v1
	v_add_f32_e32 v1, 1.0, v5
	v_exp_f32_e32 v4, v4
	v_mul_f32_e32 v5, 0xbfb8aa3b, v9
	v_exp_f32_e32 v5, v5
	v_rcp_f32_e32 v8, v1
	v_add_f32_e32 v1, 1.0, v4
	v_rcp_f32_e32 v7, v1
	v_add_f32_e32 v1, 1.0, v5
	v_rcp_f32_e32 v9, v1
.LBB0_271:
	v_or_b32_e32 v1, 16, v0
	v_mad_i64_i32 v[4:5], s[22:23], v1, s55, v[2:3]
	v_cvt_pk_bf16_f32 v10, v10, v11
	v_cvt_pk_bf16_f32 v11, v6, v7
	v_cvt_pk_bf16_f32 v12, v12, v13
	v_cvt_pk_bf16_f32 v13, v8, v9
	global_store_dwordx4 v[4:5], v[10:13], off sc1
	v_pk_mul_f32 v[6:7], v[118:119], s[16:17] op_sel_hi:[1,0]
	v_pk_mul_f32 v[8:9], v[114:115], s[16:17] op_sel_hi:[1,0]
	v_pk_mul_f32 v[10:11], v[116:117], s[16:17] op_sel_hi:[1,0]
	s_and_b64 vcc, exec, s[4:5]
	v_pk_mul_f32 v[12:13], v[112:113], s[16:17] op_sel_hi:[1,0]
	s_cbranch_vccnz .LBB0_273
	v_mul_f32_e32 v1, 0xbfb8aa3b, v10
	v_exp_f32_e32 v1, v1
	v_mul_f32_e32 v10, 0xbfb8aa3b, v12
	v_exp_f32_e32 v10, v10
	v_mul_f32_e32 v6, 0xbfb8aa3b, v6
	v_add_f32_e32 v1, 1.0, v1
	v_exp_f32_e32 v6, v6
	v_add_f32_e32 v12, 1.0, v10
	v_rcp_f32_e32 v10, v1
	v_mul_f32_e32 v1, 0xbfb8aa3b, v11
	v_exp_f32_e32 v1, v1
	v_mul_f32_e32 v11, 0xbfb8aa3b, v13
	v_exp_f32_e32 v13, v11
	v_mul_f32_e32 v8, 0xbfb8aa3b, v8
	v_exp_f32_e32 v8, v8
	v_add_f32_e32 v1, 1.0, v1
	v_rcp_f32_e32 v11, v1
	v_add_f32_e32 v1, 1.0, v13
	v_rcp_f32_e32 v13, v1
	v_add_f32_e32 v1, 1.0, v6
	v_mul_f32_e32 v7, 0xbfb8aa3b, v7
	v_rcp_f32_e32 v6, v1
	v_add_f32_e32 v1, 1.0, v8
	v_exp_f32_e32 v7, v7
	v_mul_f32_e32 v8, 0xbfb8aa3b, v9
	v_exp_f32_e32 v9, v8
	v_rcp_f32_e32 v8, v1
	v_add_f32_e32 v1, 1.0, v7
	v_rcp_f32_e32 v7, v1
	v_add_f32_e32 v1, 1.0, v9
	v_rcp_f32_e32 v12, v12
	v_rcp_f32_e32 v9, v1
.LBB0_273:
	v_cvt_pk_bf16_f32 v10, v10, v11
	v_cvt_pk_bf16_f32 v11, v6, v7
	v_cvt_pk_bf16_f32 v12, v12, v13
	v_cvt_pk_bf16_f32 v13, v8, v9
	global_store_dwordx4 v[4:5], v[10:13], off offset:256 sc1
	v_pk_mul_f32 v[6:7], v[110:111], s[16:17] op_sel_hi:[1,0]
	v_pk_mul_f32 v[8:9], v[106:107], s[16:17] op_sel_hi:[1,0]
	v_pk_mul_f32 v[10:11], v[108:109], s[16:17] op_sel_hi:[1,0]
	s_and_b64 vcc, exec, s[4:5]
	v_pk_mul_f32 v[12:13], v[104:105], s[16:17] op_sel_hi:[1,0]
	s_cbranch_vccnz .LBB0_275
	v_mul_f32_e32 v1, 0xbfb8aa3b, v10
	v_exp_f32_e32 v1, v1
	v_mul_f32_e32 v4, 0xbfb8aa3b, v12
	v_exp_f32_e32 v4, v4
	v_mul_f32_e32 v5, 0xbfb8aa3b, v13
	v_add_f32_e32 v1, 1.0, v1
	v_rcp_f32_e32 v10, v1
	v_mul_f32_e32 v1, 0xbfb8aa3b, v11
	v_exp_f32_e32 v1, v1
	v_exp_f32_e32 v5, v5
	v_add_f32_e32 v4, 1.0, v4
	v_rcp_f32_e32 v12, v4
	v_add_f32_e32 v1, 1.0, v1
	v_mul_f32_e32 v4, 0xbfb8aa3b, v6
	v_rcp_f32_e32 v11, v1
	v_add_f32_e32 v1, 1.0, v5
	v_exp_f32_e32 v4, v4
	v_mul_f32_e32 v5, 0xbfb8aa3b, v8
	v_exp_f32_e32 v5, v5
	v_rcp_f32_e32 v13, v1
	v_add_f32_e32 v1, 1.0, v4
	v_mul_f32_e32 v4, 0xbfb8aa3b, v7
	v_rcp_f32_e32 v6, v1
	v_add_f32_e32 v1, 1.0, v5
	v_exp_f32_e32 v4, v4
	v_mul_f32_e32 v5, 0xbfb8aa3b, v9
	v_exp_f32_e32 v5, v5
	v_rcp_f32_e32 v8, v1
	v_add_f32_e32 v1, 1.0, v4
	v_rcp_f32_e32 v7, v1
	v_add_f32_e32 v1, 1.0, v5
	v_rcp_f32_e32 v9, v1
.LBB0_275:
	v_or_b32_e32 v1, 32, v0
	v_mad_i64_i32 v[4:5], s[22:23], v1, s55, v[2:3]
	v_cvt_pk_bf16_f32 v10, v10, v11
	v_cvt_pk_bf16_f32 v11, v6, v7
	v_cvt_pk_bf16_f32 v12, v12, v13
	v_cvt_pk_bf16_f32 v13, v8, v9
	global_store_dwordx4 v[4:5], v[10:13], off sc1
	v_pk_mul_f32 v[6:7], v[102:103], s[16:17] op_sel_hi:[1,0]
	v_pk_mul_f32 v[8:9], v[98:99], s[16:17] op_sel_hi:[1,0]
	v_pk_mul_f32 v[10:11], v[100:101], s[16:17] op_sel_hi:[1,0]
	s_and_b64 vcc, exec, s[4:5]
	v_pk_mul_f32 v[12:13], v[96:97], s[16:17] op_sel_hi:[1,0]
	s_cbranch_vccnz .LBB0_277
	v_mul_f32_e32 v1, 0xbfb8aa3b, v10
	v_exp_f32_e32 v1, v1
	v_mul_f32_e32 v10, 0xbfb8aa3b, v12
	v_exp_f32_e32 v10, v10
	v_mul_f32_e32 v6, 0xbfb8aa3b, v6
	v_add_f32_e32 v1, 1.0, v1
	v_exp_f32_e32 v6, v6
	v_add_f32_e32 v12, 1.0, v10
	v_rcp_f32_e32 v10, v1
	v_mul_f32_e32 v1, 0xbfb8aa3b, v11
	v_exp_f32_e32 v1, v1
	v_mul_f32_e32 v11, 0xbfb8aa3b, v13
	v_exp_f32_e32 v13, v11
	v_mul_f32_e32 v8, 0xbfb8aa3b, v8
	v_exp_f32_e32 v8, v8
	v_add_f32_e32 v1, 1.0, v1
	v_rcp_f32_e32 v11, v1
	v_add_f32_e32 v1, 1.0, v13
	v_rcp_f32_e32 v13, v1
	v_add_f32_e32 v1, 1.0, v6
	v_mul_f32_e32 v7, 0xbfb8aa3b, v7
	v_rcp_f32_e32 v6, v1
	v_add_f32_e32 v1, 1.0, v8
	v_exp_f32_e32 v7, v7
	v_mul_f32_e32 v8, 0xbfb8aa3b, v9
	v_exp_f32_e32 v9, v8
	v_rcp_f32_e32 v8, v1
	v_add_f32_e32 v1, 1.0, v7
	v_rcp_f32_e32 v7, v1
	v_add_f32_e32 v1, 1.0, v9
	v_rcp_f32_e32 v12, v12
	v_rcp_f32_e32 v9, v1
.LBB0_277:
	v_cvt_pk_bf16_f32 v10, v10, v11
	v_cvt_pk_bf16_f32 v11, v6, v7
	v_cvt_pk_bf16_f32 v12, v12, v13
	v_cvt_pk_bf16_f32 v13, v8, v9
	global_store_dwordx4 v[4:5], v[10:13], off offset:256 sc1
	v_pk_mul_f32 v[6:7], v[94:95], s[16:17] op_sel_hi:[1,0]
	v_pk_mul_f32 v[8:9], v[90:91], s[16:17] op_sel_hi:[1,0]
	v_pk_mul_f32 v[10:11], v[92:93], s[16:17] op_sel_hi:[1,0]
	s_and_b64 vcc, exec, s[4:5]
	v_pk_mul_f32 v[12:13], v[88:89], s[16:17] op_sel_hi:[1,0]
	s_cbranch_vccnz .LBB0_279
	v_mul_f32_e32 v1, 0xbfb8aa3b, v10
	v_exp_f32_e32 v1, v1
	v_mul_f32_e32 v4, 0xbfb8aa3b, v12
	v_exp_f32_e32 v4, v4
	v_mul_f32_e32 v5, 0xbfb8aa3b, v13
	v_add_f32_e32 v1, 1.0, v1
	v_rcp_f32_e32 v10, v1
	v_mul_f32_e32 v1, 0xbfb8aa3b, v11
	v_exp_f32_e32 v1, v1
	v_exp_f32_e32 v5, v5
	v_add_f32_e32 v4, 1.0, v4
	v_rcp_f32_e32 v12, v4
	v_add_f32_e32 v1, 1.0, v1
	v_mul_f32_e32 v4, 0xbfb8aa3b, v6
	v_rcp_f32_e32 v11, v1
	v_add_f32_e32 v1, 1.0, v5
	v_exp_f32_e32 v4, v4
	v_mul_f32_e32 v5, 0xbfb8aa3b, v8
	v_exp_f32_e32 v5, v5
	v_rcp_f32_e32 v13, v1
	v_add_f32_e32 v1, 1.0, v4
	v_mul_f32_e32 v4, 0xbfb8aa3b, v7
	v_rcp_f32_e32 v6, v1
	v_add_f32_e32 v1, 1.0, v5
	v_exp_f32_e32 v4, v4
	v_mul_f32_e32 v5, 0xbfb8aa3b, v9
	v_exp_f32_e32 v5, v5
	v_rcp_f32_e32 v8, v1
	v_add_f32_e32 v1, 1.0, v4
	v_rcp_f32_e32 v7, v1
	v_add_f32_e32 v1, 1.0, v5
	v_rcp_f32_e32 v9, v1
.LBB0_279:
	v_or_b32_e32 v1, 48, v0
	v_mad_i64_i32 v[4:5], s[22:23], v1, s55, v[2:3]
	v_cvt_pk_bf16_f32 v10, v10, v11
	v_cvt_pk_bf16_f32 v11, v6, v7
	v_cvt_pk_bf16_f32 v12, v12, v13
	v_cvt_pk_bf16_f32 v13, v8, v9
	global_store_dwordx4 v[4:5], v[10:13], off sc1
	v_pk_mul_f32 v[6:7], v[86:87], s[16:17] op_sel_hi:[1,0]
	v_pk_mul_f32 v[8:9], v[82:83], s[16:17] op_sel_hi:[1,0]
	v_pk_mul_f32 v[10:11], v[84:85], s[16:17] op_sel_hi:[1,0]
	s_and_b64 vcc, exec, s[4:5]
	v_pk_mul_f32 v[12:13], v[80:81], s[16:17] op_sel_hi:[1,0]
	s_cbranch_vccnz .LBB0_281
	v_mul_f32_e32 v1, 0xbfb8aa3b, v10
	v_exp_f32_e32 v1, v1
	v_mul_f32_e32 v10, 0xbfb8aa3b, v12
	v_exp_f32_e32 v10, v10
	v_mul_f32_e32 v6, 0xbfb8aa3b, v6
	v_add_f32_e32 v1, 1.0, v1
	v_exp_f32_e32 v6, v6
	v_add_f32_e32 v12, 1.0, v10
	v_rcp_f32_e32 v10, v1
	v_mul_f32_e32 v1, 0xbfb8aa3b, v11
	v_exp_f32_e32 v1, v1
	v_mul_f32_e32 v11, 0xbfb8aa3b, v13
	v_exp_f32_e32 v13, v11
	v_mul_f32_e32 v8, 0xbfb8aa3b, v8
	v_exp_f32_e32 v8, v8
	v_add_f32_e32 v1, 1.0, v1
	v_rcp_f32_e32 v11, v1
	v_add_f32_e32 v1, 1.0, v13
	v_rcp_f32_e32 v13, v1
	v_add_f32_e32 v1, 1.0, v6
	v_mul_f32_e32 v7, 0xbfb8aa3b, v7
	v_rcp_f32_e32 v6, v1
	v_add_f32_e32 v1, 1.0, v8
	v_exp_f32_e32 v7, v7
	v_mul_f32_e32 v8, 0xbfb8aa3b, v9
	v_exp_f32_e32 v9, v8
	v_rcp_f32_e32 v8, v1
	v_add_f32_e32 v1, 1.0, v7
	v_rcp_f32_e32 v7, v1
	v_add_f32_e32 v1, 1.0, v9
	v_rcp_f32_e32 v12, v12
	v_rcp_f32_e32 v9, v1
.LBB0_281:
	v_cvt_pk_bf16_f32 v10, v10, v11
	v_cvt_pk_bf16_f32 v11, v6, v7
	v_cvt_pk_bf16_f32 v12, v12, v13
	v_cvt_pk_bf16_f32 v13, v8, v9
	global_store_dwordx4 v[4:5], v[10:13], off offset:256 sc1
	v_pk_mul_f32 v[6:7], v[78:79], s[16:17] op_sel_hi:[1,0]
	v_pk_mul_f32 v[8:9], v[74:75], s[16:17] op_sel_hi:[1,0]
	v_pk_mul_f32 v[10:11], v[76:77], s[16:17] op_sel_hi:[1,0]
	s_and_b64 vcc, exec, s[4:5]
	v_pk_mul_f32 v[12:13], v[72:73], s[16:17] op_sel_hi:[1,0]
	s_cbranch_vccnz .LBB0_283
	v_mul_f32_e32 v1, 0xbfb8aa3b, v10
	v_exp_f32_e32 v1, v1
	v_mul_f32_e32 v4, 0xbfb8aa3b, v12
	v_exp_f32_e32 v4, v4
	v_mul_f32_e32 v5, 0xbfb8aa3b, v13
	v_add_f32_e32 v1, 1.0, v1
	v_rcp_f32_e32 v10, v1
	v_mul_f32_e32 v1, 0xbfb8aa3b, v11
	v_exp_f32_e32 v1, v1
	v_exp_f32_e32 v5, v5
	v_add_f32_e32 v4, 1.0, v4
	v_rcp_f32_e32 v12, v4
	v_add_f32_e32 v1, 1.0, v1
	v_mul_f32_e32 v4, 0xbfb8aa3b, v6
	v_rcp_f32_e32 v11, v1
	v_add_f32_e32 v1, 1.0, v5
	v_exp_f32_e32 v4, v4
	v_mul_f32_e32 v5, 0xbfb8aa3b, v8
	v_exp_f32_e32 v5, v5
	v_rcp_f32_e32 v13, v1
	v_add_f32_e32 v1, 1.0, v4
	v_mul_f32_e32 v4, 0xbfb8aa3b, v7
	v_rcp_f32_e32 v6, v1
	v_add_f32_e32 v1, 1.0, v5
	v_exp_f32_e32 v4, v4
	v_mul_f32_e32 v5, 0xbfb8aa3b, v9
	v_exp_f32_e32 v5, v5
	v_rcp_f32_e32 v8, v1
	v_add_f32_e32 v1, 1.0, v4
	v_rcp_f32_e32 v7, v1
	v_add_f32_e32 v1, 1.0, v5
	v_rcp_f32_e32 v9, v1
.LBB0_283:
	v_add_u32_e32 v1, 0x80, v0
	v_mad_i64_i32 v[4:5], s[22:23], v1, s55, v[2:3]
	v_cvt_pk_bf16_f32 v10, v10, v11
	v_cvt_pk_bf16_f32 v11, v6, v7
	v_cvt_pk_bf16_f32 v12, v12, v13
	v_cvt_pk_bf16_f32 v13, v8, v9
	global_store_dwordx4 v[4:5], v[10:13], off sc1
	v_pk_mul_f32 v[6:7], v[70:71], s[16:17] op_sel_hi:[1,0]
	v_pk_mul_f32 v[8:9], v[66:67], s[16:17] op_sel_hi:[1,0]
	v_pk_mul_f32 v[10:11], v[68:69], s[16:17] op_sel_hi:[1,0]
	s_and_b64 vcc, exec, s[4:5]
	v_pk_mul_f32 v[12:13], v[64:65], s[16:17] op_sel_hi:[1,0]
	s_cbranch_vccnz .LBB0_285
	v_mul_f32_e32 v1, 0xbfb8aa3b, v10
	v_exp_f32_e32 v1, v1
	v_mul_f32_e32 v10, 0xbfb8aa3b, v12
	v_exp_f32_e32 v10, v10
	v_mul_f32_e32 v6, 0xbfb8aa3b, v6
	v_add_f32_e32 v1, 1.0, v1
	v_exp_f32_e32 v6, v6
	v_add_f32_e32 v12, 1.0, v10
	v_rcp_f32_e32 v10, v1
	v_mul_f32_e32 v1, 0xbfb8aa3b, v11
	v_exp_f32_e32 v1, v1
	v_mul_f32_e32 v11, 0xbfb8aa3b, v13
	v_exp_f32_e32 v13, v11
	v_mul_f32_e32 v8, 0xbfb8aa3b, v8
	v_exp_f32_e32 v8, v8
	v_add_f32_e32 v1, 1.0, v1
	v_rcp_f32_e32 v11, v1
	v_add_f32_e32 v1, 1.0, v13
	v_rcp_f32_e32 v13, v1
	v_add_f32_e32 v1, 1.0, v6
	v_mul_f32_e32 v7, 0xbfb8aa3b, v7
	v_rcp_f32_e32 v6, v1
	v_add_f32_e32 v1, 1.0, v8
	v_exp_f32_e32 v7, v7
	v_mul_f32_e32 v8, 0xbfb8aa3b, v9
	v_exp_f32_e32 v9, v8
	v_rcp_f32_e32 v8, v1
	v_add_f32_e32 v1, 1.0, v7
	v_rcp_f32_e32 v7, v1
	v_add_f32_e32 v1, 1.0, v9
	v_rcp_f32_e32 v12, v12
	v_rcp_f32_e32 v9, v1
.LBB0_285:
	v_cvt_pk_bf16_f32 v10, v10, v11
	v_cvt_pk_bf16_f32 v11, v6, v7
	v_cvt_pk_bf16_f32 v12, v12, v13
	v_cvt_pk_bf16_f32 v13, v8, v9
	global_store_dwordx4 v[4:5], v[10:13], off offset:256 sc1
	v_pk_mul_f32 v[6:7], v[62:63], s[16:17] op_sel_hi:[1,0]
	v_pk_mul_f32 v[8:9], v[58:59], s[16:17] op_sel_hi:[1,0]
	v_pk_mul_f32 v[10:11], v[60:61], s[16:17] op_sel_hi:[1,0]
	s_and_b64 vcc, exec, s[4:5]
	v_pk_mul_f32 v[12:13], v[56:57], s[16:17] op_sel_hi:[1,0]
	s_cbranch_vccnz .LBB0_287
	v_mul_f32_e32 v1, 0xbfb8aa3b, v10
	v_exp_f32_e32 v1, v1
	v_mul_f32_e32 v4, 0xbfb8aa3b, v12
	v_exp_f32_e32 v4, v4
	v_mul_f32_e32 v5, 0xbfb8aa3b, v13
	v_add_f32_e32 v1, 1.0, v1
	v_rcp_f32_e32 v10, v1
	v_mul_f32_e32 v1, 0xbfb8aa3b, v11
	v_exp_f32_e32 v1, v1
	v_exp_f32_e32 v5, v5
	v_add_f32_e32 v4, 1.0, v4
	v_rcp_f32_e32 v12, v4
	v_add_f32_e32 v1, 1.0, v1
	v_mul_f32_e32 v4, 0xbfb8aa3b, v6
	v_rcp_f32_e32 v11, v1
	v_add_f32_e32 v1, 1.0, v5
	v_exp_f32_e32 v4, v4
	v_mul_f32_e32 v5, 0xbfb8aa3b, v8
	v_exp_f32_e32 v5, v5
	v_rcp_f32_e32 v13, v1
	v_add_f32_e32 v1, 1.0, v4
	v_mul_f32_e32 v4, 0xbfb8aa3b, v7
	v_rcp_f32_e32 v6, v1
	v_add_f32_e32 v1, 1.0, v5
	v_exp_f32_e32 v4, v4
	v_mul_f32_e32 v5, 0xbfb8aa3b, v9
	v_exp_f32_e32 v5, v5
	v_rcp_f32_e32 v8, v1
	v_add_f32_e32 v1, 1.0, v4
	v_rcp_f32_e32 v7, v1
	v_add_f32_e32 v1, 1.0, v5
	v_rcp_f32_e32 v9, v1
.LBB0_287:
	v_add_u32_e32 v1, 0x90, v0
	v_mad_i64_i32 v[4:5], s[22:23], v1, s55, v[2:3]
	v_cvt_pk_bf16_f32 v10, v10, v11
	v_cvt_pk_bf16_f32 v11, v6, v7
	v_cvt_pk_bf16_f32 v12, v12, v13
	v_cvt_pk_bf16_f32 v13, v8, v9
	global_store_dwordx4 v[4:5], v[10:13], off sc1
	v_pk_mul_f32 v[6:7], v[54:55], s[16:17] op_sel_hi:[1,0]
	v_pk_mul_f32 v[8:9], v[50:51], s[16:17] op_sel_hi:[1,0]
	v_pk_mul_f32 v[10:11], v[52:53], s[16:17] op_sel_hi:[1,0]
	s_and_b64 vcc, exec, s[4:5]
	v_pk_mul_f32 v[12:13], v[48:49], s[16:17] op_sel_hi:[1,0]
	s_cbranch_vccnz .LBB0_289
	v_mul_f32_e32 v1, 0xbfb8aa3b, v10
	v_exp_f32_e32 v1, v1
	v_mul_f32_e32 v10, 0xbfb8aa3b, v12
	v_exp_f32_e32 v10, v10
	v_mul_f32_e32 v6, 0xbfb8aa3b, v6
	v_add_f32_e32 v1, 1.0, v1
	v_exp_f32_e32 v6, v6
	v_add_f32_e32 v12, 1.0, v10
	v_rcp_f32_e32 v10, v1
	v_mul_f32_e32 v1, 0xbfb8aa3b, v11
	v_exp_f32_e32 v1, v1
	v_mul_f32_e32 v11, 0xbfb8aa3b, v13
	v_exp_f32_e32 v13, v11
	v_mul_f32_e32 v8, 0xbfb8aa3b, v8
	v_exp_f32_e32 v8, v8
	v_add_f32_e32 v1, 1.0, v1
	v_rcp_f32_e32 v11, v1
	v_add_f32_e32 v1, 1.0, v13
	v_rcp_f32_e32 v13, v1
	v_add_f32_e32 v1, 1.0, v6
	v_mul_f32_e32 v7, 0xbfb8aa3b, v7
	v_rcp_f32_e32 v6, v1
	v_add_f32_e32 v1, 1.0, v8
	v_exp_f32_e32 v7, v7
	v_mul_f32_e32 v8, 0xbfb8aa3b, v9
	v_exp_f32_e32 v9, v8
	v_rcp_f32_e32 v8, v1
	v_add_f32_e32 v1, 1.0, v7
	v_rcp_f32_e32 v7, v1
	v_add_f32_e32 v1, 1.0, v9
	v_rcp_f32_e32 v12, v12
	v_rcp_f32_e32 v9, v1
.LBB0_289:
	v_cvt_pk_bf16_f32 v10, v10, v11
	v_cvt_pk_bf16_f32 v11, v6, v7
	v_cvt_pk_bf16_f32 v12, v12, v13
	v_cvt_pk_bf16_f32 v13, v8, v9
	global_store_dwordx4 v[4:5], v[10:13], off offset:256 sc1
	v_pk_mul_f32 v[6:7], v[46:47], s[16:17] op_sel_hi:[1,0]
	v_pk_mul_f32 v[8:9], v[42:43], s[16:17] op_sel_hi:[1,0]
	v_pk_mul_f32 v[10:11], v[44:45], s[16:17] op_sel_hi:[1,0]
	s_and_b64 vcc, exec, s[4:5]
	v_pk_mul_f32 v[12:13], v[40:41], s[16:17] op_sel_hi:[1,0]
	s_cbranch_vccnz .LBB0_291
	v_mul_f32_e32 v1, 0xbfb8aa3b, v10
	v_exp_f32_e32 v1, v1
	v_mul_f32_e32 v4, 0xbfb8aa3b, v12
	v_exp_f32_e32 v4, v4
	v_mul_f32_e32 v5, 0xbfb8aa3b, v13
	v_add_f32_e32 v1, 1.0, v1
	v_rcp_f32_e32 v10, v1
	v_mul_f32_e32 v1, 0xbfb8aa3b, v11
	v_exp_f32_e32 v1, v1
	v_exp_f32_e32 v5, v5
	v_add_f32_e32 v4, 1.0, v4
	v_rcp_f32_e32 v12, v4
	v_add_f32_e32 v1, 1.0, v1
	v_mul_f32_e32 v4, 0xbfb8aa3b, v6
	v_rcp_f32_e32 v11, v1
	v_add_f32_e32 v1, 1.0, v5
	v_exp_f32_e32 v4, v4
	v_mul_f32_e32 v5, 0xbfb8aa3b, v8
	v_exp_f32_e32 v5, v5
	v_rcp_f32_e32 v13, v1
	v_add_f32_e32 v1, 1.0, v4
	v_mul_f32_e32 v4, 0xbfb8aa3b, v7
	v_rcp_f32_e32 v6, v1
	v_add_f32_e32 v1, 1.0, v5
	v_exp_f32_e32 v4, v4
	v_mul_f32_e32 v5, 0xbfb8aa3b, v9
	v_exp_f32_e32 v5, v5
	v_rcp_f32_e32 v8, v1
	v_add_f32_e32 v1, 1.0, v4
	v_rcp_f32_e32 v7, v1
	v_add_f32_e32 v1, 1.0, v5
	v_rcp_f32_e32 v9, v1
.LBB0_291:
	v_add_u32_e32 v1, 0xa0, v0
	v_mad_i64_i32 v[4:5], s[22:23], v1, s55, v[2:3]
	v_cvt_pk_bf16_f32 v10, v10, v11
	v_cvt_pk_bf16_f32 v11, v6, v7
	v_cvt_pk_bf16_f32 v12, v12, v13
	v_cvt_pk_bf16_f32 v13, v8, v9
	global_store_dwordx4 v[4:5], v[10:13], off sc1
	v_pk_mul_f32 v[6:7], v[38:39], s[16:17] op_sel_hi:[1,0]
	v_pk_mul_f32 v[8:9], v[34:35], s[16:17] op_sel_hi:[1,0]
	v_pk_mul_f32 v[10:11], v[36:37], s[16:17] op_sel_hi:[1,0]
	s_and_b64 vcc, exec, s[4:5]
	v_pk_mul_f32 v[12:13], v[32:33], s[16:17] op_sel_hi:[1,0]
	s_cbranch_vccnz .LBB0_293
	v_mul_f32_e32 v1, 0xbfb8aa3b, v10
	v_exp_f32_e32 v1, v1
	v_mul_f32_e32 v10, 0xbfb8aa3b, v12
	v_exp_f32_e32 v10, v10
	v_mul_f32_e32 v6, 0xbfb8aa3b, v6
	v_add_f32_e32 v1, 1.0, v1
	v_exp_f32_e32 v6, v6
	v_add_f32_e32 v12, 1.0, v10
	v_rcp_f32_e32 v10, v1
	v_mul_f32_e32 v1, 0xbfb8aa3b, v11
	v_exp_f32_e32 v1, v1
	v_mul_f32_e32 v11, 0xbfb8aa3b, v13
	v_exp_f32_e32 v13, v11
	v_mul_f32_e32 v8, 0xbfb8aa3b, v8
	v_exp_f32_e32 v8, v8
	v_add_f32_e32 v1, 1.0, v1
	v_rcp_f32_e32 v11, v1
	v_add_f32_e32 v1, 1.0, v13
	v_rcp_f32_e32 v13, v1
	v_add_f32_e32 v1, 1.0, v6
	v_mul_f32_e32 v7, 0xbfb8aa3b, v7
	v_rcp_f32_e32 v6, v1
	v_add_f32_e32 v1, 1.0, v8
	v_exp_f32_e32 v7, v7
	v_mul_f32_e32 v8, 0xbfb8aa3b, v9
	v_exp_f32_e32 v9, v8
	v_rcp_f32_e32 v8, v1
	v_add_f32_e32 v1, 1.0, v7
	v_rcp_f32_e32 v7, v1
	v_add_f32_e32 v1, 1.0, v9
	v_rcp_f32_e32 v12, v12
	v_rcp_f32_e32 v9, v1
.LBB0_293:
	v_cvt_pk_bf16_f32 v10, v10, v11
	v_cvt_pk_bf16_f32 v11, v6, v7
	v_cvt_pk_bf16_f32 v12, v12, v13
	v_cvt_pk_bf16_f32 v13, v8, v9
	global_store_dwordx4 v[4:5], v[10:13], off offset:256 sc1
	v_pk_mul_f32 v[4:5], v[30:31], s[16:17] op_sel_hi:[1,0]
	v_pk_mul_f32 v[8:9], v[28:29], s[16:17] op_sel_hi:[1,0]
	v_pk_mul_f32 v[6:7], v[26:27], s[16:17] op_sel_hi:[1,0]
	s_and_b64 vcc, exec, s[4:5]
	v_pk_mul_f32 v[10:11], v[24:25], s[16:17] op_sel_hi:[1,0]
	s_cbranch_vccnz .LBB0_295
	v_mul_f32_e32 v1, 0xbfb8aa3b, v8
	v_exp_f32_e32 v1, v1
	v_mul_f32_e32 v8, 0xbfb8aa3b, v10
	v_exp_f32_e32 v8, v8
	v_mul_f32_e32 v4, 0xbfb8aa3b, v4
	v_add_f32_e32 v1, 1.0, v1
	v_exp_f32_e32 v4, v4
	v_add_f32_e32 v10, 1.0, v8
	v_rcp_f32_e32 v8, v1
	v_mul_f32_e32 v1, 0xbfb8aa3b, v9
	v_exp_f32_e32 v1, v1
	v_mul_f32_e32 v9, 0xbfb8aa3b, v11
	v_exp_f32_e32 v11, v9
	v_mul_f32_e32 v6, 0xbfb8aa3b, v6
	v_exp_f32_e32 v6, v6
	v_add_f32_e32 v1, 1.0, v1
	v_rcp_f32_e32 v9, v1
	v_add_f32_e32 v1, 1.0, v11
	v_rcp_f32_e32 v11, v1
	v_add_f32_e32 v1, 1.0, v4
	v_mul_f32_e32 v5, 0xbfb8aa3b, v5
	v_rcp_f32_e32 v4, v1
	v_add_f32_e32 v1, 1.0, v6
	v_exp_f32_e32 v5, v5
	v_mul_f32_e32 v6, 0xbfb8aa3b, v7
	v_exp_f32_e32 v7, v6
	v_rcp_f32_e32 v6, v1
	v_add_f32_e32 v1, 1.0, v5
	v_rcp_f32_e32 v5, v1
	v_add_f32_e32 v1, 1.0, v7
	v_rcp_f32_e32 v10, v10
	v_rcp_f32_e32 v7, v1
.LBB0_295:
	v_add_u32_e32 v1, 0xb0, v0
	v_mad_i64_i32 v[2:3], s[22:23], v1, s55, v[2:3]
	v_cvt_pk_bf16_f32 v8, v8, v9
	v_cvt_pk_bf16_f32 v9, v4, v5
	v_cvt_pk_bf16_f32 v10, v10, v11
	v_cvt_pk_bf16_f32 v11, v6, v7
	global_store_dwordx4 v[2:3], v[8:11], off sc1
	v_pk_mul_f32 v[6:7], v[22:23], s[16:17] op_sel_hi:[1,0]
	v_pk_mul_f32 v[4:5], v[18:19], s[16:17] op_sel_hi:[1,0]
	v_pk_mul_f32 v[8:9], v[20:21], s[16:17] op_sel_hi:[1,0]
	s_and_b64 vcc, exec, s[4:5]
	v_pk_mul_f32 v[10:11], v[16:17], s[16:17] op_sel_hi:[1,0]
	s_cbranch_vccnz .LBB0_297
	v_mul_f32_e32 v1, 0xbfb8aa3b, v8
	v_exp_f32_e32 v1, v1
	v_mul_f32_e32 v8, 0xbfb8aa3b, v10
	v_exp_f32_e32 v8, v8
	v_mul_f32_e32 v6, 0xbfb8aa3b, v6
	v_add_f32_e32 v1, 1.0, v1
	v_exp_f32_e32 v6, v6
	v_add_f32_e32 v10, 1.0, v8
	v_rcp_f32_e32 v8, v1
	v_mul_f32_e32 v1, 0xbfb8aa3b, v9
	v_exp_f32_e32 v1, v1
	v_mul_f32_e32 v9, 0xbfb8aa3b, v11
	v_exp_f32_e32 v11, v9
	v_mul_f32_e32 v4, 0xbfb8aa3b, v4
	v_exp_f32_e32 v4, v4
	v_add_f32_e32 v1, 1.0, v1
	v_rcp_f32_e32 v9, v1
	v_add_f32_e32 v1, 1.0, v11
	v_rcp_f32_e32 v11, v1
	v_add_f32_e32 v1, 1.0, v6
	v_rcp_f32_e32 v6, v1
	v_add_f32_e32 v1, 1.0, v4
	v_mul_f32_e32 v4, 0xbfb8aa3b, v7
	v_exp_f32_e32 v7, v4
	v_mul_f32_e32 v4, 0xbfb8aa3b, v5
	v_exp_f32_e32 v5, v4
	v_rcp_f32_e32 v4, v1
	v_add_f32_e32 v1, 1.0, v7
	v_rcp_f32_e32 v7, v1
	v_add_f32_e32 v1, 1.0, v5
	v_rcp_f32_e32 v10, v10
	v_rcp_f32_e32 v5, v1
.LBB0_297:
	v_cvt_pk_bf16_f32 v8, v8, v9
	v_cvt_pk_bf16_f32 v9, v6, v7
	v_cvt_pk_bf16_f32 v10, v10, v11
	v_cvt_pk_bf16_f32 v11, v4, v5
	global_store_dwordx4 v[2:3], v[8:11], off offset:256 sc1
	s_mov_b64 s[4:5], 0

.LBB0_365:
	ds_read_b128 v[12:15], v176
	ds_read_b128 v[16:19], v176 offset:1024
	ds_read_b128 v[28:31], v176 offset:2048
	ds_read_b128 v[32:35], v176 offset:3072
	s_add_u32 s18, s29, s57
	v_cmp_lt_i64_e32 vcc, s[6:7], v[144:145]
	s_addc_u32 s19, s30, 0
	s_and_b64 s[2:3], vcc, exec
	s_cselect_b32 s25, s19, s23
	s_cselect_b32 s24, s18, s22
	s_add_u32 s20, s31, s58
	s_addc_u32 s21, s38, 0
	s_and_b64 s[2:3], vcc, exec
	s_cselect_b32 s3, s21, s27
	s_cselect_b32 s2, s20, s26
	s_add_u32 s62, s22, 0x20080
	s_addc_u32 s63, s23, 0
	s_add_i32 s67, s40, 0xc000
	v_lshl_add_u64 v[44:45], s[62:63], 0, v[136:137]
	s_mov_b32 m0, s67
	s_add_i32 s61, s40, 0xe000
	ds_read_b128 v[4:7], v177
	ds_read_b128 v[8:11], v177 offset:1024
	ds_read_b128 v[20:23], v177 offset:2048
	ds_read_b128 v[24:27], v177 offset:3072
	ds_read_b128 v[36:39], v177 offset:4096
	ds_read_b128 v[40:43], v177 offset:5120
	ds_read_b128 v[52:55], v177 offset:6144
	ds_read_b128 v[56:59], v177 offset:7168
	global_load_lds_dwordx4 v[44:45], off
	v_lshl_add_u64 v[44:45], s[62:63], 0, v[140:141]
	s_mov_b32 m0, s61
	s_nop 0
	global_load_lds_dwordx4 v[44:45], off
	s_waitcnt lgkmcnt(8)
	s_barrier
	s_waitcnt lgkmcnt(0)
	s_setprio 1
	v_mov_b64_e32 v[110:111], v[2:3]
	v_mov_b64_e32 v[114:115], v[2:3]
	v_mov_b64_e32 v[106:107], v[2:3]
	v_mov_b64_e32 v[102:103], v[2:3]
	v_mov_b64_e32 v[82:83], v[2:3]
	v_mov_b64_e32 v[78:79], v[2:3]
	v_mov_b64_e32 v[50:51], v[2:3]
	v_mov_b64_e32 v[46:47], v[2:3]
	v_mov_b64_e32 v[108:109], v[0:1]
	v_mov_b64_e32 v[112:113], v[0:1]
	v_mov_b64_e32 v[104:105], v[0:1]
	v_mov_b64_e32 v[100:101], v[0:1]
	v_mov_b64_e32 v[80:81], v[0:1]
	v_mov_b64_e32 v[76:77], v[0:1]
	v_mov_b64_e32 v[48:49], v[0:1]
	v_mov_b64_e32 v[44:45], v[0:1]
	s_waitcnt lgkmcnt(0)
	v_mfma_scale_f32_16x16x128_f8f6f4 v[108:111], v[12:19], v[4:11], v[108:111], v171, v171 op_sel_hi:[0,0,0]
	v_mfma_scale_f32_16x16x128_f8f6f4 v[112:115], v[28:35], v[4:11], v[112:115], v171, v171 op_sel_hi:[0,0,0]
	v_mfma_scale_f32_16x16x128_f8f6f4 v[104:107], v[12:19], v[20:27], v[104:107], v171, v171 op_sel_hi:[0,0,0]
	v_mfma_scale_f32_16x16x128_f8f6f4 v[100:103], v[28:35], v[20:27], v[100:103], v171, v171 op_sel_hi:[0,0,0]
	v_mfma_scale_f32_16x16x128_f8f6f4 v[80:83], v[12:19], v[36:43], v[80:83], v171, v171 op_sel_hi:[0,0,0]
	v_mfma_scale_f32_16x16x128_f8f6f4 v[76:79], v[28:35], v[36:43], v[76:79], v171, v171 op_sel_hi:[0,0,0]
	v_mfma_scale_f32_16x16x128_f8f6f4 v[48:51], v[12:19], v[52:59], v[48:51], v171, v171 op_sel_hi:[0,0,0]
	v_mfma_scale_f32_16x16x128_f8f6f4 v[44:47], v[28:35], v[52:59], v[44:47], v171, v171 op_sel_hi:[0,0,0]
	s_setprio 0
	s_barrier
	v_lshl_add_u64 v[132:133], s[26:27], 0, v[138:139]
	s_add_i32 s64, s50, s39
	v_lshl_add_u64 v[60:61], v[132:133], 0, s[10:11]
	s_mov_b32 m0, s64
	v_lshl_add_u64 v[134:135], s[26:27], 0, v[142:143]
	s_add_i32 s62, s64, 0x2000
	ds_read_b128 v[154:157], v178
	ds_read_b128 v[158:161], v178 offset:1024
	ds_read_b128 v[180:183], v178 offset:2048
	ds_read_b128 v[184:187], v178 offset:3072
	global_load_lds_dwordx4 v[60:61], off
	v_lshl_add_u64 v[60:61], v[134:135], 0, s[10:11]
	s_mov_b32 m0, s62
	s_nop 0
	global_load_lds_dwordx4 v[60:61], off
	s_barrier
	s_waitcnt lgkmcnt(0)
	s_setprio 1
	v_mov_b64_e32 v[126:127], v[2:3]
	v_mov_b64_e32 v[130:131], v[2:3]
	v_mov_b64_e32 v[122:123], v[2:3]
	v_mov_b64_e32 v[118:119], v[2:3]
	v_mov_b64_e32 v[98:99], v[2:3]
	v_mov_b64_e32 v[94:95], v[2:3]
	v_mov_b64_e32 v[66:67], v[2:3]
	v_mov_b64_e32 v[62:63], v[2:3]
	v_mov_b64_e32 v[124:125], v[0:1]
	v_mov_b64_e32 v[128:129], v[0:1]
	v_mov_b64_e32 v[120:121], v[0:1]
	v_mov_b64_e32 v[116:117], v[0:1]
	v_mov_b64_e32 v[96:97], v[0:1]
	v_mov_b64_e32 v[92:93], v[0:1]
	v_mov_b64_e32 v[64:65], v[0:1]
	v_mov_b64_e32 v[60:61], v[0:1]
	s_waitcnt lgkmcnt(0)
	v_mfma_scale_f32_16x16x128_f8f6f4 v[124:127], v[154:161], v[4:11], v[124:127], v171, v171 op_sel_hi:[0,0,0]
	v_mfma_scale_f32_16x16x128_f8f6f4 v[128:131], v[180:187], v[4:11], v[128:131], v171, v171 op_sel_hi:[0,0,0]
	v_mfma_scale_f32_16x16x128_f8f6f4 v[120:123], v[154:161], v[20:27], v[120:123], v171, v171 op_sel_hi:[0,0,0]
	v_mfma_scale_f32_16x16x128_f8f6f4 v[116:119], v[180:187], v[20:27], v[116:119], v171, v171 op_sel_hi:[0,0,0]
	v_mfma_scale_f32_16x16x128_f8f6f4 v[96:99], v[154:161], v[36:43], v[96:99], v171, v171 op_sel_hi:[0,0,0]
	v_mfma_scale_f32_16x16x128_f8f6f4 v[92:95], v[180:187], v[36:43], v[92:95], v171, v171 op_sel_hi:[0,0,0]
	v_mfma_scale_f32_16x16x128_f8f6f4 v[64:67], v[154:161], v[52:59], v[64:67], v171, v171 op_sel_hi:[0,0,0]
	v_mfma_scale_f32_16x16x128_f8f6f4 v[60:63], v[180:187], v[52:59], v[60:63], v171, v171 op_sel_hi:[0,0,0]
	s_setprio 0
	v_lshl_add_u64 v[150:151], s[22:23], 0, v[136:137]
	s_mov_b32 m0, s40
	v_lshl_add_u64 v[4:5], v[150:151], 0, s[10:11]
	v_lshl_add_u64 v[152:153], s[22:23], 0, v[140:141]
	s_barrier
	ds_read_b128 v[52:55], v177 offset:16384
	ds_read_b128 v[56:59], v177 offset:17408
	ds_read_b128 v[188:191], v177 offset:18432
	ds_read_b128 v[192:195], v177 offset:19456
	ds_read_b128 v[196:199], v177 offset:20480
	ds_read_b128 v[200:203], v177 offset:21504
	ds_read_b128 v[204:207], v177 offset:22528
	ds_read_b128 v[208:211], v177 offset:23552
	global_load_lds_dwordx4 v[4:5], off
	v_lshl_add_u64 v[4:5], v[152:153], 0, s[10:11]
	s_mov_b32 m0, s41
	s_nop 0
	global_load_lds_dwordx4 v[4:5], off
	s_barrier
	s_waitcnt lgkmcnt(0)
	s_setprio 1
	v_mov_b64_e32 v[74:75], v[2:3]
	v_mov_b64_e32 v[70:71], v[2:3]
	v_mov_b64_e32 v[42:43], v[2:3]
	v_mov_b64_e32 v[38:39], v[2:3]
	v_mov_b64_e32 v[26:27], v[2:3]
	v_mov_b64_e32 v[22:23], v[2:3]
	v_mov_b64_e32 v[10:11], v[2:3]
	v_mov_b64_e32 v[6:7], v[2:3]
	v_mov_b64_e32 v[72:73], v[0:1]
	v_mov_b64_e32 v[68:69], v[0:1]
	v_mov_b64_e32 v[40:41], v[0:1]
	v_mov_b64_e32 v[36:37], v[0:1]
	v_mov_b64_e32 v[24:25], v[0:1]
	v_mov_b64_e32 v[20:21], v[0:1]
	v_mov_b64_e32 v[8:9], v[0:1]
	v_mov_b64_e32 v[4:5], v[0:1]
	s_waitcnt lgkmcnt(0)
	v_mfma_scale_f32_16x16x128_f8f6f4 v[72:75], v[12:19], v[52:59], v[72:75], v171, v171 op_sel_hi:[0,0,0]
	v_mfma_scale_f32_16x16x128_f8f6f4 v[68:71], v[28:35], v[52:59], v[68:71], v171, v171 op_sel_hi:[0,0,0]
	v_mfma_scale_f32_16x16x128_f8f6f4 v[40:43], v[12:19], v[188:195], v[40:43], v171, v171 op_sel_hi:[0,0,0]
	v_mfma_scale_f32_16x16x128_f8f6f4 v[36:39], v[28:35], v[188:195], v[36:39], v171, v171 op_sel_hi:[0,0,0]
	v_mfma_scale_f32_16x16x128_f8f6f4 v[24:27], v[12:19], v[196:203], v[24:27], v171, v171 op_sel_hi:[0,0,0]
	v_mfma_scale_f32_16x16x128_f8f6f4 v[20:23], v[28:35], v[196:203], v[20:23], v171, v171 op_sel_hi:[0,0,0]
	v_mfma_scale_f32_16x16x128_f8f6f4 v[8:11], v[12:19], v[204:211], v[8:11], v171, v171 op_sel_hi:[0,0,0]
	v_mfma_scale_f32_16x16x128_f8f6f4 v[4:7], v[28:35], v[204:211], v[4:7], v171, v171 op_sel_hi:[0,0,0]
	s_setprio 0
	s_barrier
	s_add_u32 s68, s26, 0x10100
	s_addc_u32 s69, s27, 0
	s_add_i32 s65, s51, s39
	v_lshl_add_u64 v[12:13], s[68:69], 0, v[138:139]
	s_mov_b32 m0, s65
	s_add_i32 s63, s65, 0x2000
	global_load_lds_dwordx4 v[12:13], off
	v_lshl_add_u64 v[12:13], s[68:69], 0, v[142:143]
	s_mov_b32 m0, s63
	s_nop 0
	global_load_lds_dwordx4 v[12:13], off
	s_waitcnt vmcnt(6)
	s_barrier
	s_setprio 1
	v_mov_b64_e32 v[90:91], v[2:3]
	v_mov_b64_e32 v[86:87], v[2:3]
	v_mov_b64_e32 v[88:89], v[0:1]
	v_mov_b64_e32 v[84:85], v[0:1]
	v_mfma_scale_f32_16x16x128_f8f6f4 v[88:91], v[154:161], v[52:59], v[88:91], v171, v171 op_sel_hi:[0,0,0]
	v_mfma_scale_f32_16x16x128_f8f6f4 v[84:87], v[180:187], v[52:59], v[84:87], v171, v171 op_sel_hi:[0,0,0]
	v_mov_b64_e32 v[58:59], v[2:3]
	v_mov_b64_e32 v[54:55], v[2:3]
	v_mov_b64_e32 v[34:35], v[2:3]
	v_mov_b64_e32 v[30:31], v[2:3]
	v_mov_b64_e32 v[18:19], v[2:3]
	v_mov_b64_e32 v[14:15], v[2:3]
	v_mov_b64_e32 v[56:57], v[0:1]
	v_mov_b64_e32 v[52:53], v[0:1]
	v_mov_b64_e32 v[32:33], v[0:1]
	v_mov_b64_e32 v[28:29], v[0:1]
	v_mov_b64_e32 v[16:17], v[0:1]
	v_mov_b64_e32 v[12:13], v[0:1]
	v_mfma_scale_f32_16x16x128_f8f6f4 v[56:59], v[154:161], v[188:195], v[56:59], v171, v171 op_sel_hi:[0,0,0]
	v_mfma_scale_f32_16x16x128_f8f6f4 v[52:55], v[180:187], v[188:195], v[52:55], v171, v171 op_sel_hi:[0,0,0]
	v_mfma_scale_f32_16x16x128_f8f6f4 v[32:35], v[154:161], v[196:203], v[32:35], v171, v171 op_sel_hi:[0,0,0]
	v_mfma_scale_f32_16x16x128_f8f6f4 v[28:31], v[180:187], v[196:203], v[28:31], v171, v171 op_sel_hi:[0,0,0]
	v_mfma_scale_f32_16x16x128_f8f6f4 v[16:19], v[154:161], v[204:211], v[16:19], v171, v171 op_sel_hi:[0,0,0]
	v_mfma_scale_f32_16x16x128_f8f6f4 v[12:15], v[180:187], v[204:211], v[12:15], v171, v171 op_sel_hi:[0,0,0]
	s_setprio 0
	s_add_i32 s66, 0, 0x18000
	v_add_u32_e32 v154, s66, v174
	s_barrier
	ds_read_b128 v[156:159], v154
	ds_read_b128 v[160:163], v154 offset:1024
	ds_read_b128 v[180:183], v154 offset:2048
	ds_read_b128 v[184:187], v154 offset:3072
	s_add_u32 s68, s22, 0x20100
	s_addc_u32 s69, s23, 0
	s_mov_b32 m0, s42
	v_lshl_add_u64 v[164:165], s[68:69], 0, v[136:137]
	ds_read_b128 v[188:191], v177 offset:32768
	ds_read_b128 v[192:195], v177 offset:33792
	ds_read_b128 v[196:199], v177 offset:34816
	ds_read_b128 v[200:203], v177 offset:35840
	ds_read_b128 v[204:207], v177 offset:36864
	ds_read_b128 v[208:211], v177 offset:37888
	ds_read_b128 v[212:215], v177 offset:38912
	ds_read_b128 v[216:219], v177 offset:39936
	global_load_lds_dwordx4 v[164:165], off
	v_lshl_add_u64 v[164:165], s[68:69], 0, v[140:141]
	s_mov_b32 m0, s43
	s_nop 0
	global_load_lds_dwordx4 v[164:165], off
	s_waitcnt lgkmcnt(8)
	s_barrier
	s_waitcnt lgkmcnt(0)
	s_setprio 1
	s_waitcnt lgkmcnt(0)
	v_mfma_scale_f32_16x16x128_f8f6f4 v[108:111], v[156:163], v[188:195], v[108:111], v171, v171 op_sel_hi:[0,0,0]
	v_mfma_scale_f32_16x16x128_f8f6f4 v[112:115], v[180:187], v[188:195], v[112:115], v171, v171 op_sel_hi:[0,0,0]
	v_mfma_scale_f32_16x16x128_f8f6f4 v[104:107], v[156:163], v[196:203], v[104:107], v171, v171 op_sel_hi:[0,0,0]
	v_mfma_scale_f32_16x16x128_f8f6f4 v[100:103], v[180:187], v[196:203], v[100:103], v171, v171 op_sel_hi:[0,0,0]
	v_mfma_scale_f32_16x16x128_f8f6f4 v[80:83], v[156:163], v[204:211], v[80:83], v171, v171 op_sel_hi:[0,0,0]
	v_mfma_scale_f32_16x16x128_f8f6f4 v[76:79], v[180:187], v[204:211], v[76:79], v171, v171 op_sel_hi:[0,0,0]
	v_mfma_scale_f32_16x16x128_f8f6f4 v[48:51], v[156:163], v[212:219], v[48:51], v171, v171 op_sel_hi:[0,0,0]
	v_mfma_scale_f32_16x16x128_f8f6f4 v[44:47], v[180:187], v[212:219], v[44:47], v171, v171 op_sel_hi:[0,0,0]
	s_setprio 0
	s_barrier
	s_add_i32 s69, 0, 0x1c000
	s_add_i32 s68, s66, s39
	v_add_u32_e32 v155, s69, v174
	v_lshl_add_u64 v[132:133], v[132:133], 0, s[12:13]
	s_mov_b32 m0, s68
	s_add_i32 s66, s68, 0x2000
	ds_read_b128 v[224:227], v155
	ds_read_b128 v[228:231], v155 offset:1024
	ds_read_b128 v[232:235], v155 offset:2048
	ds_read_b128 v[236:239], v155 offset:3072
	global_load_lds_dwordx4 v[132:133], off
	v_lshl_add_u64 v[132:133], v[134:135], 0, s[12:13]
	s_mov_b32 m0, s66
	s_nop 0
	global_load_lds_dwordx4 v[132:133], off
	s_barrier
	s_waitcnt lgkmcnt(0)
	s_setprio 1
	s_waitcnt lgkmcnt(0)
	v_mfma_scale_f32_16x16x128_f8f6f4 v[124:127], v[224:231], v[188:195], v[124:127], v171, v171 op_sel_hi:[0,0,0]
	v_mfma_scale_f32_16x16x128_f8f6f4 v[128:131], v[232:239], v[188:195], v[128:131], v171, v171 op_sel_hi:[0,0,0]
	v_mfma_scale_f32_16x16x128_f8f6f4 v[120:123], v[224:231], v[196:203], v[120:123], v171, v171 op_sel_hi:[0,0,0]
	v_mfma_scale_f32_16x16x128_f8f6f4 v[116:119], v[232:239], v[196:203], v[116:119], v171, v171 op_sel_hi:[0,0,0]
	v_mfma_scale_f32_16x16x128_f8f6f4 v[96:99], v[224:231], v[204:211], v[96:99], v171, v171 op_sel_hi:[0,0,0]
	v_mfma_scale_f32_16x16x128_f8f6f4 v[92:95], v[232:239], v[204:211], v[92:95], v171, v171 op_sel_hi:[0,0,0]
	v_mfma_scale_f32_16x16x128_f8f6f4 v[64:67], v[224:231], v[212:219], v[64:67], v171, v171 op_sel_hi:[0,0,0]
	v_mfma_scale_f32_16x16x128_f8f6f4 v[60:63], v[232:239], v[212:219], v[60:63], v171, v171 op_sel_hi:[0,0,0]
	s_setprio 0
	s_mov_b32 m0, s46
	v_lshl_add_u64 v[132:133], v[150:151], 0, s[12:13]
	s_barrier
	ds_read_b128 v[188:191], v177 offset:49152
	ds_read_b128 v[192:195], v177 offset:50176
	ds_read_b128 v[196:199], v177 offset:51200
	ds_read_b128 v[200:203], v177 offset:52224
	ds_read_b128 v[204:207], v177 offset:53248
	ds_read_b128 v[208:211], v177 offset:54272
	ds_read_b128 v[212:215], v177 offset:55296
	ds_read_b128 v[216:219], v177 offset:56320
	global_load_lds_dwordx4 v[132:133], off
	v_lshl_add_u64 v[132:133], v[152:153], 0, s[12:13]
	s_mov_b32 m0, s47
	s_nop 0
	global_load_lds_dwordx4 v[132:133], off
	s_barrier
	s_waitcnt lgkmcnt(0)
	s_setprio 1
	s_waitcnt lgkmcnt(0)
	v_mfma_scale_f32_16x16x128_f8f6f4 v[72:75], v[156:163], v[188:195], v[72:75], v171, v171 op_sel_hi:[0,0,0]
	v_mfma_scale_f32_16x16x128_f8f6f4 v[68:71], v[180:187], v[188:195], v[68:71], v171, v171 op_sel_hi:[0,0,0]
	v_mfma_scale_f32_16x16x128_f8f6f4 v[40:43], v[156:163], v[196:203], v[40:43], v171, v171 op_sel_hi:[0,0,0]
	v_mfma_scale_f32_16x16x128_f8f6f4 v[36:39], v[180:187], v[196:203], v[36:39], v171, v171 op_sel_hi:[0,0,0]
	v_mfma_scale_f32_16x16x128_f8f6f4 v[24:27], v[156:163], v[204:211], v[24:27], v171, v171 op_sel_hi:[0,0,0]
	v_mfma_scale_f32_16x16x128_f8f6f4 v[20:23], v[180:187], v[204:211], v[20:23], v171, v171 op_sel_hi:[0,0,0]
	v_mfma_scale_f32_16x16x128_f8f6f4 v[8:11], v[156:163], v[212:219], v[8:11], v171, v171 op_sel_hi:[0,0,0]
	v_mfma_scale_f32_16x16x128_f8f6f4 v[4:7], v[180:187], v[212:219], v[4:7], v171, v171 op_sel_hi:[0,0,0]
	s_setprio 0
	s_barrier
	s_add_u32 s70, s26, 0x10180
	s_addc_u32 s71, s27, 0
	s_add_i32 s27, s69, s39
	v_lshl_add_u64 v[132:133], s[70:71], 0, v[138:139]
	s_mov_b32 m0, s27
	s_add_i32 s26, s27, 0x2000
	global_load_lds_dwordx4 v[132:133], off
	v_lshl_add_u64 v[132:133], s[70:71], 0, v[142:143]
	s_mov_b32 m0, s26
	s_nop 0
	global_load_lds_dwordx4 v[132:133], off
	s_waitcnt vmcnt(6)
	s_barrier
	s_setprio 1
	v_mfma_scale_f32_16x16x128_f8f6f4 v[88:91], v[224:231], v[188:195], v[88:91], v171, v171 op_sel_hi:[0,0,0]
	v_mfma_scale_f32_16x16x128_f8f6f4 v[84:87], v[232:239], v[188:195], v[84:87], v171, v171 op_sel_hi:[0,0,0]
	v_mfma_scale_f32_16x16x128_f8f6f4 v[56:59], v[224:231], v[196:203], v[56:59], v171, v171 op_sel_hi:[0,0,0]
	v_mfma_scale_f32_16x16x128_f8f6f4 v[52:55], v[232:239], v[196:203], v[52:55], v171, v171 op_sel_hi:[0,0,0]
	v_mfma_scale_f32_16x16x128_f8f6f4 v[32:35], v[224:231], v[204:211], v[32:35], v171, v171 op_sel_hi:[0,0,0]
	v_mfma_scale_f32_16x16x128_f8f6f4 v[28:31], v[232:239], v[204:211], v[28:31], v171, v171 op_sel_hi:[0,0,0]
	v_mfma_scale_f32_16x16x128_f8f6f4 v[16:19], v[224:231], v[212:219], v[16:19], v171, v171 op_sel_hi:[0,0,0]
	v_mfma_scale_f32_16x16x128_f8f6f4 v[12:15], v[232:239], v[212:219], v[12:15], v171, v171 op_sel_hi:[0,0,0]
	s_setprio 0
	s_barrier
	ds_read_b128 v[156:159], v176
	ds_read_b128 v[160:163], v176 offset:1024
	ds_read_b128 v[180:183], v176 offset:2048
	ds_read_b128 v[184:187], v176 offset:3072
	s_add_u32 s22, s22, 0x20180
	s_addc_u32 s23, s23, 0
	s_mov_b32 m0, s67
	v_lshl_add_u64 v[132:133], s[22:23], 0, v[136:137]
	ds_read_b128 v[188:191], v177
	ds_read_b128 v[192:195], v177 offset:1024
	ds_read_b128 v[196:199], v177 offset:2048
	ds_read_b128 v[200:203], v177 offset:3072
	ds_read_b128 v[204:207], v177 offset:4096
	ds_read_b128 v[208:211], v177 offset:5120
	ds_read_b128 v[212:215], v177 offset:6144
	ds_read_b128 v[216:219], v177 offset:7168
	global_load_lds_dwordx4 v[132:133], off
	v_lshl_add_u64 v[132:133], s[22:23], 0, v[140:141]
	s_mov_b32 m0, s61
	s_nop 0
	global_load_lds_dwordx4 v[132:133], off
	s_waitcnt lgkmcnt(8)
	s_barrier
	s_waitcnt lgkmcnt(0)
	s_setprio 1
	s_waitcnt lgkmcnt(0)
	v_mfma_scale_f32_16x16x128_f8f6f4 v[108:111], v[156:163], v[188:195], v[108:111], v171, v171 op_sel_hi:[0,0,0]
	v_mfma_scale_f32_16x16x128_f8f6f4 v[112:115], v[180:187], v[188:195], v[112:115], v171, v171 op_sel_hi:[0,0,0]
	v_mfma_scale_f32_16x16x128_f8f6f4 v[104:107], v[156:163], v[196:203], v[104:107], v171, v171 op_sel_hi:[0,0,0]
	v_mfma_scale_f32_16x16x128_f8f6f4 v[100:103], v[180:187], v[196:203], v[100:103], v171, v171 op_sel_hi:[0,0,0]
	v_mfma_scale_f32_16x16x128_f8f6f4 v[80:83], v[156:163], v[204:211], v[80:83], v171, v171 op_sel_hi:[0,0,0]
	v_mfma_scale_f32_16x16x128_f8f6f4 v[76:79], v[180:187], v[204:211], v[76:79], v171, v171 op_sel_hi:[0,0,0]
	v_mfma_scale_f32_16x16x128_f8f6f4 v[48:51], v[156:163], v[212:219], v[48:51], v171, v171 op_sel_hi:[0,0,0]
	v_mfma_scale_f32_16x16x128_f8f6f4 v[44:47], v[180:187], v[212:219], v[44:47], v171, v171 op_sel_hi:[0,0,0]
	s_setprio 0
	s_barrier
	s_mov_b32 m0, s64
	v_lshl_add_u64 v[132:133], s[2:3], 0, v[138:139]
	ds_read_b128 v[224:227], v178
	ds_read_b128 v[228:231], v178 offset:1024
	ds_read_b128 v[232:235], v178 offset:2048
	ds_read_b128 v[236:239], v178 offset:3072
	global_load_lds_dwordx4 v[132:133], off
	v_lshl_add_u64 v[134:135], s[2:3], 0, v[142:143]
	s_mov_b32 m0, s62
	s_nop 0
	global_load_lds_dwordx4 v[134:135], off
	s_barrier
	s_waitcnt lgkmcnt(0)
	s_setprio 1
	s_waitcnt lgkmcnt(0)
	v_mfma_scale_f32_16x16x128_f8f6f4 v[124:127], v[224:231], v[188:195], v[124:127], v171, v171 op_sel_hi:[0,0,0]
	v_mfma_scale_f32_16x16x128_f8f6f4 v[128:131], v[232:239], v[188:195], v[128:131], v171, v171 op_sel_hi:[0,0,0]
	v_mfma_scale_f32_16x16x128_f8f6f4 v[120:123], v[224:231], v[196:203], v[120:123], v171, v171 op_sel_hi:[0,0,0]
	v_mfma_scale_f32_16x16x128_f8f6f4 v[116:119], v[232:239], v[196:203], v[116:119], v171, v171 op_sel_hi:[0,0,0]
	v_mfma_scale_f32_16x16x128_f8f6f4 v[96:99], v[224:231], v[204:211], v[96:99], v171, v171 op_sel_hi:[0,0,0]
	v_mfma_scale_f32_16x16x128_f8f6f4 v[92:95], v[232:239], v[204:211], v[92:95], v171, v171 op_sel_hi:[0,0,0]
	v_mfma_scale_f32_16x16x128_f8f6f4 v[64:67], v[224:231], v[212:219], v[64:67], v171, v171 op_sel_hi:[0,0,0]
	v_mfma_scale_f32_16x16x128_f8f6f4 v[60:63], v[232:239], v[212:219], v[60:63], v171, v171 op_sel_hi:[0,0,0]
	s_setprio 0
	s_mov_b32 m0, s40
	v_lshl_add_u64 v[150:151], s[24:25], 0, v[136:137]
	s_barrier
	ds_read_b128 v[188:191], v177 offset:16384
	ds_read_b128 v[192:195], v177 offset:17408
	ds_read_b128 v[196:199], v177 offset:18432
	ds_read_b128 v[200:203], v177 offset:19456
	ds_read_b128 v[204:207], v177 offset:20480
	ds_read_b128 v[208:211], v177 offset:21504
	ds_read_b128 v[212:215], v177 offset:22528
	ds_read_b128 v[216:219], v177 offset:23552
	global_load_lds_dwordx4 v[150:151], off
	v_lshl_add_u64 v[152:153], s[24:25], 0, v[140:141]
	s_mov_b32 m0, s41
	s_nop 0
	global_load_lds_dwordx4 v[152:153], off
	s_barrier
	s_waitcnt lgkmcnt(0)
	s_setprio 1
	s_waitcnt lgkmcnt(0)
	v_mfma_scale_f32_16x16x128_f8f6f4 v[72:75], v[156:163], v[188:195], v[72:75], v171, v171 op_sel_hi:[0,0,0]
	v_mfma_scale_f32_16x16x128_f8f6f4 v[68:71], v[180:187], v[188:195], v[68:71], v171, v171 op_sel_hi:[0,0,0]
	v_mfma_scale_f32_16x16x128_f8f6f4 v[40:43], v[156:163], v[196:203], v[40:43], v171, v171 op_sel_hi:[0,0,0]
	v_mfma_scale_f32_16x16x128_f8f6f4 v[36:39], v[180:187], v[196:203], v[36:39], v171, v171 op_sel_hi:[0,0,0]
	v_mfma_scale_f32_16x16x128_f8f6f4 v[24:27], v[156:163], v[204:211], v[24:27], v171, v171 op_sel_hi:[0,0,0]
	v_mfma_scale_f32_16x16x128_f8f6f4 v[20:23], v[180:187], v[204:211], v[20:23], v171, v171 op_sel_hi:[0,0,0]
	v_mfma_scale_f32_16x16x128_f8f6f4 v[8:11], v[156:163], v[212:219], v[8:11], v171, v171 op_sel_hi:[0,0,0]
	v_mfma_scale_f32_16x16x128_f8f6f4 v[4:7], v[180:187], v[212:219], v[4:7], v171, v171 op_sel_hi:[0,0,0]
	s_setprio 0
	s_barrier
	s_add_u32 s22, s2, 0x10000
	s_addc_u32 s23, s3, 0
	s_mov_b32 m0, s65
	v_lshl_add_u64 v[156:157], s[22:23], 0, v[138:139]
	global_load_lds_dwordx4 v[156:157], off
	v_lshl_add_u64 v[156:157], s[22:23], 0, v[142:143]
	s_mov_b32 m0, s63
	s_nop 0
	global_load_lds_dwordx4 v[156:157], off
	s_waitcnt vmcnt(6)
	s_barrier
	s_setprio 1
	v_mfma_scale_f32_16x16x128_f8f6f4 v[88:91], v[224:231], v[188:195], v[88:91], v171, v171 op_sel_hi:[0,0,0]
	v_mfma_scale_f32_16x16x128_f8f6f4 v[84:87], v[232:239], v[188:195], v[84:87], v171, v171 op_sel_hi:[0,0,0]
	v_mfma_scale_f32_16x16x128_f8f6f4 v[56:59], v[224:231], v[196:203], v[56:59], v171, v171 op_sel_hi:[0,0,0]
	v_mfma_scale_f32_16x16x128_f8f6f4 v[52:55], v[232:239], v[196:203], v[52:55], v171, v171 op_sel_hi:[0,0,0]
	v_mfma_scale_f32_16x16x128_f8f6f4 v[32:35], v[224:231], v[204:211], v[32:35], v171, v171 op_sel_hi:[0,0,0]
	v_mfma_scale_f32_16x16x128_f8f6f4 v[28:31], v[232:239], v[204:211], v[28:31], v171, v171 op_sel_hi:[0,0,0]
	v_mfma_scale_f32_16x16x128_f8f6f4 v[16:19], v[224:231], v[212:219], v[16:19], v171, v171 op_sel_hi:[0,0,0]
	v_mfma_scale_f32_16x16x128_f8f6f4 v[12:15], v[232:239], v[212:219], v[12:15], v171, v171 op_sel_hi:[0,0,0]
	s_setprio 0
	s_barrier
	ds_read_b128 v[156:159], v154
	ds_read_b128 v[160:163], v154 offset:1024
	ds_read_b128 v[180:183], v154 offset:2048
	ds_read_b128 v[184:187], v154 offset:3072
	s_add_u32 s22, s24, 0x20000
	s_addc_u32 s23, s25, 0
	s_mov_b32 m0, s42
	v_lshl_add_u64 v[164:165], s[22:23], 0, v[136:137]
	ds_read_b128 v[188:191], v177 offset:32768
	ds_read_b128 v[192:195], v177 offset:33792
	ds_read_b128 v[196:199], v177 offset:34816
	ds_read_b128 v[200:203], v177 offset:35840
	ds_read_b128 v[204:207], v177 offset:36864
	ds_read_b128 v[208:211], v177 offset:37888
	ds_read_b128 v[212:215], v177 offset:38912
	ds_read_b128 v[216:219], v177 offset:39936
	global_load_lds_dwordx4 v[164:165], off
	v_lshl_add_u64 v[164:165], s[22:23], 0, v[140:141]
	s_mov_b32 m0, s43
	s_nop 0
	global_load_lds_dwordx4 v[164:165], off
	s_waitcnt lgkmcnt(8)
	s_barrier
	s_waitcnt lgkmcnt(0)
	s_setprio 1
	s_waitcnt lgkmcnt(0)
	v_mfma_scale_f32_16x16x128_f8f6f4 v[108:111], v[156:163], v[188:195], v[108:111], v171, v171 op_sel_hi:[0,0,0]
	v_mfma_scale_f32_16x16x128_f8f6f4 v[112:115], v[180:187], v[188:195], v[112:115], v171, v171 op_sel_hi:[0,0,0]
	v_mfma_scale_f32_16x16x128_f8f6f4 v[104:107], v[156:163], v[196:203], v[104:107], v171, v171 op_sel_hi:[0,0,0]
	v_mfma_scale_f32_16x16x128_f8f6f4 v[100:103], v[180:187], v[196:203], v[100:103], v171, v171 op_sel_hi:[0,0,0]
	v_mfma_scale_f32_16x16x128_f8f6f4 v[80:83], v[156:163], v[204:211], v[80:83], v171, v171 op_sel_hi:[0,0,0]
	v_mfma_scale_f32_16x16x128_f8f6f4 v[76:79], v[180:187], v[204:211], v[76:79], v171, v171 op_sel_hi:[0,0,0]
	v_mfma_scale_f32_16x16x128_f8f6f4 v[48:51], v[156:163], v[212:219], v[48:51], v171, v171 op_sel_hi:[0,0,0]
	v_mfma_scale_f32_16x16x128_f8f6f4 v[44:47], v[180:187], v[212:219], v[44:47], v171, v171 op_sel_hi:[0,0,0]
	s_setprio 0
	s_barrier
	s_mov_b32 m0, s68
	v_lshl_add_u64 v[132:133], v[132:133], 0, s[8:9]
	ds_read_b128 v[224:227], v155
	ds_read_b128 v[228:231], v155 offset:1024
	ds_read_b128 v[232:235], v155 offset:2048
	ds_read_b128 v[236:239], v155 offset:3072
	global_load_lds_dwordx4 v[132:133], off
	v_lshl_add_u64 v[132:133], v[134:135], 0, s[8:9]
	s_mov_b32 m0, s66
	s_nop 0
	global_load_lds_dwordx4 v[132:133], off
	s_barrier
	s_waitcnt lgkmcnt(0)
	s_setprio 1
	s_waitcnt lgkmcnt(0)
	v_mfma_scale_f32_16x16x128_f8f6f4 v[124:127], v[224:231], v[188:195], v[124:127], v171, v171 op_sel_hi:[0,0,0]
	v_mfma_scale_f32_16x16x128_f8f6f4 v[128:131], v[232:239], v[188:195], v[128:131], v171, v171 op_sel_hi:[0,0,0]
	v_mfma_scale_f32_16x16x128_f8f6f4 v[120:123], v[224:231], v[196:203], v[120:123], v171, v171 op_sel_hi:[0,0,0]
	v_mfma_scale_f32_16x16x128_f8f6f4 v[116:119], v[232:239], v[196:203], v[116:119], v171, v171 op_sel_hi:[0,0,0]
	v_mfma_scale_f32_16x16x128_f8f6f4 v[96:99], v[224:231], v[204:211], v[96:99], v171, v171 op_sel_hi:[0,0,0]
	v_mfma_scale_f32_16x16x128_f8f6f4 v[92:95], v[232:239], v[204:211], v[92:95], v171, v171 op_sel_hi:[0,0,0]
	v_mfma_scale_f32_16x16x128_f8f6f4 v[64:67], v[224:231], v[212:219], v[64:67], v171, v171 op_sel_hi:[0,0,0]
	v_mfma_scale_f32_16x16x128_f8f6f4 v[60:63], v[232:239], v[212:219], v[60:63], v171, v171 op_sel_hi:[0,0,0]
	s_setprio 0
	s_mov_b32 m0, s46
	v_lshl_add_u64 v[132:133], v[150:151], 0, s[8:9]
	s_barrier
	ds_read_b128 v[188:191], v177 offset:49152
	ds_read_b128 v[192:195], v177 offset:50176
	ds_read_b128 v[196:199], v177 offset:51200
	ds_read_b128 v[200:203], v177 offset:52224
	ds_read_b128 v[204:207], v177 offset:53248
	ds_read_b128 v[208:211], v177 offset:54272
	ds_read_b128 v[212:215], v177 offset:55296
	ds_read_b128 v[216:219], v177 offset:56320
	global_load_lds_dwordx4 v[132:133], off
	v_lshl_add_u64 v[132:133], v[152:153], 0, s[8:9]
	s_mov_b32 m0, s47
	s_nop 0
	global_load_lds_dwordx4 v[132:133], off
	s_barrier
	s_waitcnt lgkmcnt(0)
	s_setprio 1
	s_waitcnt lgkmcnt(0)
	v_mfma_scale_f32_16x16x128_f8f6f4 v[72:75], v[156:163], v[188:195], v[72:75], v171, v171 op_sel_hi:[0,0,0]
	v_mfma_scale_f32_16x16x128_f8f6f4 v[68:71], v[180:187], v[188:195], v[68:71], v171, v171 op_sel_hi:[0,0,0]
	v_mfma_scale_f32_16x16x128_f8f6f4 v[40:43], v[156:163], v[196:203], v[40:43], v171, v171 op_sel_hi:[0,0,0]
	v_mfma_scale_f32_16x16x128_f8f6f4 v[36:39], v[180:187], v[196:203], v[36:39], v171, v171 op_sel_hi:[0,0,0]
	v_mfma_scale_f32_16x16x128_f8f6f4 v[24:27], v[156:163], v[204:211], v[24:27], v171, v171 op_sel_hi:[0,0,0]
	v_mfma_scale_f32_16x16x128_f8f6f4 v[20:23], v[180:187], v[204:211], v[20:23], v171, v171 op_sel_hi:[0,0,0]
	v_mfma_scale_f32_16x16x128_f8f6f4 v[8:11], v[156:163], v[212:219], v[8:11], v171, v171 op_sel_hi:[0,0,0]
	v_mfma_scale_f32_16x16x128_f8f6f4 v[4:7], v[180:187], v[212:219], v[4:7], v171, v171 op_sel_hi:[0,0,0]
	s_setprio 0
	s_barrier
	s_add_u32 s2, s2, 0x10080
	s_addc_u32 s3, s3, 0
	s_mov_b32 m0, s27
	v_lshl_add_u64 v[132:133], s[2:3], 0, v[138:139]
	global_load_lds_dwordx4 v[132:133], off
	v_lshl_add_u64 v[132:133], s[2:3], 0, v[142:143]
	s_mov_b32 m0, s26
	s_nop 0
	global_load_lds_dwordx4 v[132:133], off
	s_waitcnt vmcnt(6)
	s_barrier
	s_setprio 1
	v_mfma_scale_f32_16x16x128_f8f6f4 v[88:91], v[224:231], v[188:195], v[88:91], v171, v171 op_sel_hi:[0,0,0]
	v_mfma_scale_f32_16x16x128_f8f6f4 v[84:87], v[232:239], v[188:195], v[84:87], v171, v171 op_sel_hi:[0,0,0]
	v_mfma_scale_f32_16x16x128_f8f6f4 v[56:59], v[224:231], v[196:203], v[56:59], v171, v171 op_sel_hi:[0,0,0]
	v_mfma_scale_f32_16x16x128_f8f6f4 v[52:55], v[232:239], v[196:203], v[52:55], v171, v171 op_sel_hi:[0,0,0]
	v_mfma_scale_f32_16x16x128_f8f6f4 v[32:35], v[224:231], v[204:211], v[32:35], v171, v171 op_sel_hi:[0,0,0]
	v_mfma_scale_f32_16x16x128_f8f6f4 v[28:31], v[232:239], v[204:211], v[28:31], v171, v171 op_sel_hi:[0,0,0]
	v_mfma_scale_f32_16x16x128_f8f6f4 v[16:19], v[224:231], v[212:219], v[16:19], v171, v171 op_sel_hi:[0,0,0]
	v_mfma_scale_f32_16x16x128_f8f6f4 v[12:15], v[232:239], v[212:219], v[12:15], v171, v171 op_sel_hi:[0,0,0]
	s_setprio 0
	v_lshl_add_u32 v164, s60, 8, v173
	s_cmp_lt_i32 s59, 6
	s_cselect_b32 s2, 0, 32
	v_or_b32_e32 v162, 16, v164
	s_cselect_b32 s24, s52, 0x47b1c000
	s_cselect_b32 s22, s53, 0x800
	s_cselect_b32 s23, 0, -6
	s_add_u32 s2, s44, s2
	v_ashrrev_i32_e32 v165, 31, v164
	v_ashrrev_i32_e32 v163, 31, v162
	s_addc_u32 s3, s45, 0
	v_lshlrev_b64 v[132:133], 6, v[164:165]
	v_lshlrev_b64 v[150:151], 6, v[162:163]
	s_barrier
	s_nop 7
	s_nop 7
	s_nop 7
	v_lshl_add_u64 v[132:133], s[2:3], 0, v[132:133]
	v_lshl_add_u64 v[150:151], s[2:3], 0, v[150:151]
	global_load_dwordx4 v[180:183], v[132:133], off
	s_nop 0
	global_load_dwordx4 v[132:135], v[132:133], off offset:16
	s_nop 0
	global_load_dwordx4 v[184:187], v[150:151], off
	global_load_dwordx4 v[188:191], v[150:151], off offset:16
	v_or_b32_e32 v160, 32, v164
	v_ashrrev_i32_e32 v161, 31, v160
	v_lshlrev_b64 v[150:151], 6, v[160:161]
	v_or_b32_e32 v158, 48, v164
	v_lshl_add_u64 v[150:151], s[2:3], 0, v[150:151]
	v_ashrrev_i32_e32 v159, 31, v158
	global_load_dwordx4 v[192:195], v[150:151], off
	global_load_dwordx4 v[196:199], v[150:151], off offset:16
	v_lshlrev_b64 v[150:151], 6, v[158:159]
	v_lshl_add_u64 v[150:151], s[2:3], 0, v[150:151]
	global_load_dwordx4 v[200:203], v[150:151], off
	global_load_dwordx4 v[204:207], v[150:151], off offset:16
	v_add_u32_e32 v156, 0x80, v164
	v_add_u32_e32 v152, 0xa0, v164
	v_add_u32_e32 v150, 0xb0, v164
	v_add_u32_e32 v154, 0x90, v164
	v_ashrrev_i32_e32 v157, 31, v156
	v_ashrrev_i32_e32 v153, 31, v152
	v_ashrrev_i32_e32 v151, 31, v150
	v_ashrrev_i32_e32 v155, 31, v154
	v_lshlrev_b64 v[208:209], 6, v[156:157]
	v_lshlrev_b64 v[212:213], 6, v[152:153]
	v_lshlrev_b64 v[214:215], 6, v[150:151]
	v_lshlrev_b64 v[210:211], 6, v[154:155]
	v_lshl_add_u64 v[216:217], s[2:3], 0, v[208:209]
	v_lshl_add_u64 v[232:233], s[2:3], 0, v[212:213]
	v_lshl_add_u64 v[240:241], s[2:3], 0, v[214:215]
	v_lshl_add_u64 v[220:221], s[2:3], 0, v[210:211]
	global_load_dwordx4 v[208:211], v[216:217], off
	global_load_dwordx4 v[212:215], v[216:217], off offset:16
	s_nop 0
	global_load_dwordx4 v[216:219], v[220:221], off
	global_load_dwordx4 v[224:227], v[220:221], off offset:16
	global_load_dwordx4 v[228:231], v[232:233], off
	s_nop 0
	global_load_dwordx4 v[232:235], v[232:233], off offset:16
	s_nop 0
	global_load_dwordx4 v[236:239], v[240:241], off
	s_nop 0
	global_load_dwordx4 v[240:243], v[240:241], off offset:16
	s_mov_b32 s60, s56
	s_mov_b64 s[26:27], s[20:21]
	s_waitcnt vmcnt(0)
	v_mov_b32_e32 v220, v180
	v_mov_b32_e32 v221, v132
	v_mov_b32_e32 v132, v181
	v_mov_b32_e32 v180, v182
	v_mov_b32_e32 v181, v134
	v_mov_b32_e32 v134, v183
	v_mov_b32_e32 v182, v184
	v_mov_b32_e32 v183, v188
	v_mov_b32_e32 v188, v185
	v_mov_b32_e32 v184, v186
	v_mov_b32_e32 v185, v190
	v_mov_b32_e32 v190, v187
	v_pk_add_f32 v[132:133], v[220:221], v[132:133]
	v_pk_add_f32 v[134:135], v[180:181], v[134:135]
	v_pk_add_f32 v[180:181], v[182:183], v[188:189]
	v_pk_add_f32 v[182:183], v[184:185], v[190:191]
	v_pk_add_f32 v[132:133], v[132:133], v[134:135]
	v_pk_add_f32 v[134:135], v[180:181], v[182:183]
	v_mov_b32_e32 v181, v132
	v_mov_b32_e32 v180, v134
	v_mov_b32_e32 v132, v135
	v_pk_add_f32 v[132:133], v[180:181], v[132:133]
	v_mov_b32_e32 v186, v192
	v_pk_fma_f32 v[132:133], v[132:133], s[16:17], v[148:149] op_sel_hi:[1,0,0]
	v_mov_b32_e32 v187, v196
	v_mul_f32_e32 v134, 0x4b800000, v133
	v_mul_f32_e32 v135, 0x4b800000, v132
	v_cmp_gt_f32_e32 vcc, s54, v133
	v_cmp_gt_f32_e64 s[2:3], s54, v132
	v_mov_b32_e32 v196, v193
	v_cndmask_b32_e32 v133, v133, v134, vcc
	v_cndmask_b32_e64 v132, v132, v135, s[2:3]
	v_rsq_f32_e32 v134, v133
	v_rsq_f32_e32 v135, v132
	v_mov_b32_e32 v192, v194
	v_mov_b32_e32 v193, v198
	v_mul_f32_e32 v151, 0x45800000, v134
	v_mul_f32_e32 v153, 0x45800000, v135
	v_cndmask_b32_e32 v134, v134, v151, vcc
	v_cndmask_b32_e64 v135, v135, v153, s[2:3]
	v_mov_b32_e32 v198, v195
	v_pk_add_f32 v[132:133], v[186:187], v[196:197]
	v_mul_f32_e32 v180, 0x3c800000, v134
	v_mul_f32_e32 v182, 0x3c800000, v135
	v_pk_add_f32 v[134:135], v[192:193], v[198:199]
	v_mov_b32_e32 v184, v202
	v_pk_add_f32 v[132:133], v[132:133], v[134:135]
	v_mov_b32_e32 v134, v200
	v_mov_b32_e32 v135, v204
	v_mov_b32_e32 v204, v201
	v_mov_b32_e32 v185, v206
	v_mov_b32_e32 v206, v203
	v_pk_add_f32 v[134:135], v[134:135], v[204:205]
	v_pk_add_f32 v[184:185], v[184:185], v[206:207]
	v_mov_b32_e32 v186, v218
	v_pk_add_f32 v[134:135], v[134:135], v[184:185]
	v_mov_b32_e32 v185, v132
	v_mov_b32_e32 v184, v134
	v_mov_b32_e32 v132, v135
	v_pk_add_f32 v[132:133], v[184:185], v[132:133]
	v_mov_b32_e32 v135, v214
	v_pk_fma_f32 v[132:133], v[132:133], s[16:17], v[148:149] op_sel_hi:[1,0,0]
	v_mov_b32_e32 v214, v211
	v_mul_f32_e32 v134, 0x4b800000, v133
	v_cmp_gt_f32_e32 vcc, s54, v133
	v_cmp_gt_f32_e64 s[2:3], s54, v132
	v_mov_b32_e32 v187, v226
	v_cndmask_b32_e32 v133, v133, v134, vcc
	v_rsq_f32_e32 v133, v133
	v_mul_f32_e32 v134, 0x4b800000, v132
	v_cndmask_b32_e64 v132, v132, v134, s[2:3]
	v_rsq_f32_e32 v132, v132
	v_mul_f32_e32 v134, 0x45800000, v133
	v_cndmask_b32_e32 v133, v133, v134, vcc
	v_mul_f32_e32 v184, 0x3c800000, v133
	v_mul_f32_e32 v133, 0x45800000, v132
	v_cndmask_b32_e64 v132, v132, v133, s[2:3]
	v_mul_f32_e32 v172, 0x3c800000, v132
	v_mov_b32_e32 v132, v208
	v_mov_b32_e32 v133, v212
	v_mov_b32_e32 v212, v209
	v_mov_b32_e32 v134, v210
	v_pk_add_f32 v[132:133], v[132:133], v[212:213]
	v_pk_add_f32 v[134:135], v[134:135], v[214:215]
	v_mov_b32_e32 v226, v219
	v_pk_add_f32 v[132:133], v[132:133], v[134:135]
	v_mov_b32_e32 v134, v216
	v_mov_b32_e32 v135, v224
	v_mov_b32_e32 v224, v217
	v_pk_add_f32 v[134:135], v[134:135], v[224:225]
	v_pk_add_f32 v[186:187], v[186:187], v[226:227]
	v_pk_mul_f32 v[108:109], v[108:109], v[180:181] op_sel_hi:[1,0]
	v_pk_add_f32 v[134:135], v[134:135], v[186:187]
	v_mov_b32_e32 v187, v132
	v_mov_b32_e32 v186, v134
	v_mov_b32_e32 v132, v135
	v_pk_add_f32 v[132:133], v[186:187], v[132:133]
	v_mov_b32_e32 v135, v234
	v_pk_fma_f32 v[132:133], v[132:133], s[16:17], v[148:149] op_sel_hi:[1,0,0]
	v_mov_b32_e32 v234, v231
	v_mul_f32_e32 v134, 0x4b800000, v133
	v_cmp_gt_f32_e32 vcc, s54, v133
	v_cmp_gt_f32_e64 s[2:3], s54, v132
	v_mov_b32_e32 v186, v238
	v_cndmask_b32_e32 v133, v133, v134, vcc
	v_rsq_f32_e32 v133, v133
	v_mul_f32_e32 v134, 0x4b800000, v132
	v_cndmask_b32_e64 v132, v132, v134, s[2:3]
	v_rsq_f32_e32 v132, v132
	v_mul_f32_e32 v134, 0x45800000, v133
	v_cndmask_b32_e32 v133, v133, v134, vcc
	v_mul_f32_e32 v170, 0x3c800000, v133
	v_mul_f32_e32 v133, 0x45800000, v132
	v_cndmask_b32_e64 v132, v132, v133, s[2:3]
	v_mul_f32_e32 v168, 0x3c800000, v132
	v_mov_b32_e32 v132, v228
	v_mov_b32_e32 v133, v232
	v_mov_b32_e32 v232, v229
	v_mov_b32_e32 v134, v230
	v_pk_add_f32 v[132:133], v[132:133], v[232:233]
	v_pk_add_f32 v[134:135], v[134:135], v[234:235]
	v_mov_b32_e32 v187, v242
	v_pk_add_f32 v[132:133], v[132:133], v[134:135]
	v_mov_b32_e32 v134, v236
	v_mov_b32_e32 v135, v240
	v_mov_b32_e32 v240, v237
	v_mov_b32_e32 v242, v239
	v_pk_add_f32 v[134:135], v[134:135], v[240:241]
	v_pk_add_f32 v[186:187], v[186:187], v[242:243]
	v_pk_mul_f32 v[110:111], v[110:111], v[180:181] op_sel_hi:[1,0]
	v_pk_add_f32 v[134:135], v[134:135], v[186:187]
	v_mov_b32_e32 v187, v132
	v_mov_b32_e32 v186, v134
	v_mov_b32_e32 v132, v135
	v_pk_add_f32 v[132:133], v[186:187], v[132:133]
	v_cvt_pk_bf16_f32 v108, v108, v109
	v_cvt_pk_bf16_f32 v109, v110, v111
	v_pk_mul_f32 v[114:115], v[114:115], v[180:181] op_sel_hi:[1,0]
	v_pk_fma_f32 v[132:133], v[132:133], s[16:17], v[148:149] op_sel_hi:[1,0,0]
	v_pk_mul_f32 v[112:113], v[112:113], v[180:181] op_sel_hi:[1,0]
	v_mul_f32_e32 v134, 0x4b800000, v133
	v_cmp_gt_f32_e32 vcc, s54, v133
	v_cmp_gt_f32_e64 s[2:3], s54, v132
	v_cvt_pk_bf16_f32 v110, v112, v113
	v_cvt_pk_bf16_f32 v111, v114, v115
	v_pk_mul_f32 v[112:113], v[130:131], v[180:181] op_sel_hi:[1,0]
	v_cndmask_b32_e32 v133, v133, v134, vcc
	v_rsq_f32_e32 v133, v133
	v_mul_f32_e32 v134, 0x4b800000, v132
	v_cndmask_b32_e64 v132, v132, v134, s[2:3]
	v_rsq_f32_e32 v132, v132
	v_mul_f32_e32 v134, 0x45800000, v133
	v_cndmask_b32_e32 v133, v133, v134, vcc
	v_mul_f32_e32 v166, 0x3c800000, v133
	v_mul_f32_e32 v133, 0x45800000, v132
	v_cndmask_b32_e64 v132, v132, v133, s[2:3]
	s_add_u32 s2, s4, s24
	s_addc_u32 s3, s5, 0
	s_add_i32 s23, s23, s59
	v_lshl_or_b32 v134, s23, 8, v175
	v_ashrrev_i32_e32 v135, 31, v134
	v_lshl_add_u64 v[134:135], v[134:135], 1, s[2:3]
	v_mad_i64_i32 v[164:165], s[2:3], s22, v164, 0
	v_lshl_add_u64 v[164:165], v[164:165], 1, v[134:135]
	global_store_dwordx4 v[164:165], v[108:111], off sc1
	v_pk_mul_f32 v[114:115], v[128:129], v[180:181] op_sel_hi:[1,0]
	v_pk_mul_f32 v[106:107], v[106:107], v[182:183] op_sel_hi:[1,0]
	v_pk_mul_f32 v[108:109], v[124:125], v[180:181] op_sel_hi:[1,0]
	v_pk_mul_f32 v[110:111], v[126:127], v[180:181] op_sel_hi:[1,0]
	v_cvt_pk_bf16_f32 v108, v108, v109
	v_pk_mul_f32 v[104:105], v[104:105], v[182:183] op_sel_hi:[1,0]
	v_cvt_pk_bf16_f32 v109, v110, v111
	v_cvt_pk_bf16_f32 v110, v114, v115
	v_cvt_pk_bf16_f32 v111, v112, v113
	global_store_dwordx4 v[164:165], v[108:111], off offset:256 sc1
	v_pk_mul_f32 v[82:83], v[82:83], v[184:185] op_sel_hi:[1,0]
	v_pk_mul_f32 v[80:81], v[80:81], v[184:185] op_sel_hi:[1,0]
	v_mad_i64_i32 v[108:109], s[2:3], s22, v162, 0
	v_lshl_add_u64 v[108:109], v[108:109], 1, v[134:135]
	v_pk_mul_f32 v[110:111], v[102:103], v[182:183] op_sel_hi:[1,0]
	v_pk_mul_f32 v[102:103], v[100:101], v[182:183] op_sel_hi:[1,0]
	v_cvt_pk_bf16_f32 v100, v104, v105
	v_cvt_pk_bf16_f32 v101, v106, v107
	v_pk_mul_f32 v[104:105], v[118:119], v[182:183] op_sel_hi:[1,0]
	v_cvt_pk_bf16_f32 v102, v102, v103
	v_cvt_pk_bf16_f32 v103, v110, v111
	global_store_dwordx4 v[108:109], v[100:103], off sc1
	v_pk_mul_f32 v[106:107], v[116:117], v[182:183] op_sel_hi:[1,0]
	v_pk_mul_f32 v[50:51], v[50:51], v[172:173] op_sel_hi:[1,0]
	v_pk_mul_f32 v[100:101], v[120:121], v[182:183] op_sel_hi:[1,0]
	v_pk_mul_f32 v[102:103], v[122:123], v[182:183] op_sel_hi:[1,0]
	v_cvt_pk_bf16_f32 v100, v100, v101
	v_pk_mul_f32 v[48:49], v[48:49], v[172:173] op_sel_hi:[1,0]
	v_cvt_pk_bf16_f32 v101, v102, v103
	v_cvt_pk_bf16_f32 v102, v106, v107
	v_cvt_pk_bf16_f32 v103, v104, v105
	global_store_dwordx4 v[108:109], v[100:103], off offset:256 sc1
	v_pk_mul_f32 v[42:43], v[42:43], v[168:169] op_sel_hi:[1,0]
	v_pk_mul_f32 v[40:41], v[40:41], v[168:169] op_sel_hi:[1,0]
	v_mad_i64_i32 v[100:101], s[2:3], s22, v160, 0
	v_lshl_add_u64 v[100:101], v[100:101], 1, v[134:135]
	v_pk_mul_f32 v[102:103], v[78:79], v[184:185] op_sel_hi:[1,0]
	v_pk_mul_f32 v[78:79], v[76:77], v[184:185] op_sel_hi:[1,0]
	v_cvt_pk_bf16_f32 v76, v80, v81
	v_cvt_pk_bf16_f32 v77, v82, v83
	v_pk_mul_f32 v[80:81], v[94:95], v[184:185] op_sel_hi:[1,0]
	v_cvt_pk_bf16_f32 v78, v78, v79
	v_cvt_pk_bf16_f32 v79, v102, v103
	global_store_dwordx4 v[100:101], v[76:79], off sc1
	v_pk_mul_f32 v[82:83], v[92:93], v[184:185] op_sel_hi:[1,0]
	v_pk_mul_f32 v[26:27], v[26:27], v[166:167] op_sel_hi:[1,0]
	v_pk_mul_f32 v[76:77], v[96:97], v[184:185] op_sel_hi:[1,0]
	v_pk_mul_f32 v[78:79], v[98:99], v[184:185] op_sel_hi:[1,0]
	v_cvt_pk_bf16_f32 v76, v76, v77
	v_pk_mul_f32 v[24:25], v[24:25], v[166:167] op_sel_hi:[1,0]
	v_cvt_pk_bf16_f32 v77, v78, v79
	v_cvt_pk_bf16_f32 v78, v82, v83
	v_cvt_pk_bf16_f32 v79, v80, v81
	global_store_dwordx4 v[100:101], v[76:79], off offset:256 sc1
	v_mul_f32_e32 v132, 0x3c800000, v132
	v_pk_mul_f32 v[10:11], v[10:11], v[132:133] op_sel_hi:[1,0]
	v_mad_i64_i32 v[76:77], s[2:3], s22, v158, 0
	v_lshl_add_u64 v[76:77], v[76:77], 1, v[134:135]
	v_pk_mul_f32 v[78:79], v[46:47], v[172:173] op_sel_hi:[1,0]
	v_pk_mul_f32 v[46:47], v[44:45], v[172:173] op_sel_hi:[1,0]
	v_cvt_pk_bf16_f32 v44, v48, v49
	v_cvt_pk_bf16_f32 v45, v50, v51
	v_pk_mul_f32 v[48:49], v[62:63], v[172:173] op_sel_hi:[1,0]
	v_cvt_pk_bf16_f32 v46, v46, v47
	v_cvt_pk_bf16_f32 v47, v78, v79
	global_store_dwordx4 v[76:77], v[44:47], off sc1
	v_pk_mul_f32 v[50:51], v[60:61], v[172:173] op_sel_hi:[1,0]
	v_pk_mul_f32 v[60:61], v[68:69], v[170:171] op_sel_hi:[1,0]
	v_pk_mul_f32 v[44:45], v[64:65], v[172:173] op_sel_hi:[1,0]
	v_pk_mul_f32 v[46:47], v[66:67], v[172:173] op_sel_hi:[1,0]
	v_cvt_pk_bf16_f32 v44, v44, v45
	v_pk_mul_f32 v[8:9], v[8:9], v[132:133] op_sel_hi:[1,0]
	v_cvt_pk_bf16_f32 v45, v46, v47
	v_cvt_pk_bf16_f32 v46, v50, v51
	v_cvt_pk_bf16_f32 v47, v48, v49
	global_store_dwordx4 v[76:77], v[44:47], off offset:256 sc1
	v_pk_mul_f32 v[50:51], v[70:71], v[170:171] op_sel_hi:[1,0]
	s_add_i32 s49, s49, s17
	v_mad_i64_i32 v[44:45], s[2:3], s22, v156, 0
	v_lshl_add_u64 v[48:49], v[44:45], 1, v[134:135]
	v_pk_mul_f32 v[46:47], v[74:75], v[170:171] op_sel_hi:[1,0]
	v_pk_mul_f32 v[44:45], v[72:73], v[170:171] op_sel_hi:[1,0]
	s_andn2_b64 vcc, exec, s[0:1]
	v_cvt_pk_bf16_f32 v44, v44, v45
	v_cvt_pk_bf16_f32 v45, v46, v47
	v_cvt_pk_bf16_f32 v46, v60, v61
	v_cvt_pk_bf16_f32 v47, v50, v51
	global_store_dwordx4 v[48:49], v[44:47], off sc1
	v_pk_mul_f32 v[50:51], v[86:87], v[170:171] op_sel_hi:[1,0]
	v_pk_mul_f32 v[60:61], v[84:85], v[170:171] op_sel_hi:[1,0]
	v_pk_mul_f32 v[46:47], v[90:91], v[170:171] op_sel_hi:[1,0]
	v_pk_mul_f32 v[44:45], v[88:89], v[170:171] op_sel_hi:[1,0]
	s_mov_b32 s59, s55
	v_cvt_pk_bf16_f32 v44, v44, v45
	v_cvt_pk_bf16_f32 v45, v46, v47
	v_cvt_pk_bf16_f32 v46, v60, v61
	v_cvt_pk_bf16_f32 v47, v50, v51
	global_store_dwordx4 v[48:49], v[44:47], off offset:256 sc1
	s_nop 1
	v_mad_i64_i32 v[44:45], s[2:3], s22, v154, 0
	v_pk_mul_f32 v[46:47], v[38:39], v[168:169] op_sel_hi:[1,0]
	v_pk_mul_f32 v[38:39], v[36:37], v[168:169] op_sel_hi:[1,0]
	v_lshl_add_u64 v[44:45], v[44:45], 1, v[134:135]
	v_cvt_pk_bf16_f32 v36, v40, v41
	v_cvt_pk_bf16_f32 v37, v42, v43
	v_cvt_pk_bf16_f32 v38, v38, v39
	v_cvt_pk_bf16_f32 v39, v46, v47
	global_store_dwordx4 v[44:45], v[36:39], off sc1
	v_pk_mul_f32 v[40:41], v[54:55], v[168:169] op_sel_hi:[1,0]
	v_pk_mul_f32 v[42:43], v[52:53], v[168:169] op_sel_hi:[1,0]
	v_pk_mul_f32 v[38:39], v[58:59], v[168:169] op_sel_hi:[1,0]
	v_pk_mul_f32 v[36:37], v[56:57], v[168:169] op_sel_hi:[1,0]
	s_nop 0
	v_cvt_pk_bf16_f32 v36, v36, v37
	v_cvt_pk_bf16_f32 v37, v38, v39
	v_cvt_pk_bf16_f32 v38, v42, v43
	v_cvt_pk_bf16_f32 v39, v40, v41
	global_store_dwordx4 v[44:45], v[36:39], off offset:256 sc1
	s_nop 1
	v_mad_i64_i32 v[36:37], s[2:3], s22, v152, 0
	v_pk_mul_f32 v[38:39], v[22:23], v[166:167] op_sel_hi:[1,0]
	v_pk_mul_f32 v[22:23], v[20:21], v[166:167] op_sel_hi:[1,0]
	v_lshl_add_u64 v[36:37], v[36:37], 1, v[134:135]
	v_cvt_pk_bf16_f32 v20, v24, v25
	v_cvt_pk_bf16_f32 v21, v26, v27
	v_cvt_pk_bf16_f32 v22, v22, v23
	v_cvt_pk_bf16_f32 v23, v38, v39
	global_store_dwordx4 v[36:37], v[20:23], off sc1
	v_pk_mul_f32 v[24:25], v[30:31], v[166:167] op_sel_hi:[1,0]
	v_pk_mul_f32 v[26:27], v[28:29], v[166:167] op_sel_hi:[1,0]
	v_pk_mul_f32 v[22:23], v[34:35], v[166:167] op_sel_hi:[1,0]
	v_pk_mul_f32 v[20:21], v[32:33], v[166:167] op_sel_hi:[1,0]
	s_nop 0
	v_cvt_pk_bf16_f32 v20, v20, v21
	v_cvt_pk_bf16_f32 v21, v22, v23
	v_cvt_pk_bf16_f32 v22, v26, v27
	v_cvt_pk_bf16_f32 v23, v24, v25
	global_store_dwordx4 v[36:37], v[20:23], off offset:256 sc1
	s_nop 1
	v_mad_i64_i32 v[20:21], s[2:3], s22, v150, 0
	v_pk_mul_f32 v[22:23], v[6:7], v[132:133] op_sel_hi:[1,0]
	v_pk_mul_f32 v[6:7], v[4:5], v[132:133] op_sel_hi:[1,0]
	v_lshl_add_u64 v[20:21], v[20:21], 1, v[134:135]
	v_cvt_pk_bf16_f32 v4, v8, v9
	v_cvt_pk_bf16_f32 v5, v10, v11
	v_cvt_pk_bf16_f32 v6, v6, v7
	v_cvt_pk_bf16_f32 v7, v22, v23
	global_store_dwordx4 v[20:21], v[4:7], off sc1
	s_mov_b64 s[22:23], s[18:19]
	v_pk_mul_f32 v[8:9], v[14:15], v[132:133] op_sel_hi:[1,0]
	v_pk_mul_f32 v[6:7], v[18:19], v[132:133] op_sel_hi:[1,0]
	v_pk_mul_f32 v[4:5], v[16:17], v[132:133] op_sel_hi:[1,0]
	v_pk_mul_f32 v[10:11], v[12:13], v[132:133] op_sel_hi:[1,0]
	v_cvt_pk_bf16_f32 v4, v4, v5
	v_cvt_pk_bf16_f32 v5, v6, v7
	s_nop 0
	v_cvt_pk_bf16_f32 v6, v10, v11
	v_cvt_pk_bf16_f32 v7, v8, v9
	global_store_dwordx4 v[20:21], v[4:7], off offset:256 sc1
	s_cbranch_vccz .LBB0_371

.LBB0_381:
	v_lshl_add_u64 v[64:65], s[6:7], 0, v[44:45]
	global_load_dwordx4 v[0:3], v[64:65], off
	global_load_dwordx4 v[50:53], v[34:35], off offset:16
	global_load_dwordx4 v[54:57], v[34:35], off
	s_add_i32 s47, s23, s22
	s_cmpk_lt_i32 s47, 0x2200
	s_cselect_b64 s[20:21], -1, 0
	s_and_b64 s[4:5], s[20:21], exec
	s_cselect_b32 s4, s47, s22
	s_mul_hi_i32 s5, s4, 0x4c00
	s_mulk_i32 s4, 0x4c00
	s_add_u32 s4, s8, s4
	s_addc_u32 s5, s9, s5
	s_add_i32 s46, s27, s22
	s_cmpk_lt_i32 s46, 0x2200
	s_cselect_b64 s[18:19], -1, 0
	s_and_b64 s[12:13], s[18:19], exec
	v_lshl_add_u64 v[48:49], s[6:7], 0, v[46:47]
	s_cselect_b32 s10, s46, s22
	global_load_dwordx4 v[60:63], v[48:49], off
	s_mul_hi_i32 s13, s10, 0x4c00
	s_mulk_i32 s10, 0x4c00
	s_add_u32 s12, s8, s10
	s_addc_u32 s13, s9, s13
	s_add_i32 s45, s29, s22
	s_cmpk_lt_i32 s45, 0x2200
	s_cselect_b64 s[16:17], -1, 0
	v_lshl_add_u64 v[4:5], s[4:5], 0, v[32:33]
	global_load_dwordx4 v[28:31], v58, s[4:5] offset:3072
	global_load_dwordx4 v[20:23], v58, s[12:13] offset:3072
	s_and_b64 s[4:5], s[16:17], exec
	s_cselect_b32 s4, s45, s22
	v_add_co_u32_e32 v4, vcc, s42, v4
	s_mul_hi_i32 s5, s4, 0x4c00
	s_mulk_i32 s4, 0x4c00
	v_addc_co_u32_e32 v5, vcc, 0, v5, vcc
	v_lshl_add_u64 v[6:7], s[12:13], 0, v[32:33]
	s_add_u32 s4, s8, s4
	v_add_co_u32_e32 v6, vcc, s42, v6
	s_addc_u32 s5, s9, s5
	s_nop 0
	v_addc_co_u32_e32 v7, vcc, 0, v7, vcc
	global_load_dwordx4 v[24:27], v[4:5], off offset:2048
	global_load_dwordx4 v[16:19], v[6:7], off offset:2048
	v_lshl_add_u64 v[4:5], s[4:5], 0, v[32:33]
	v_add_co_u32_e32 v8, vcc, s42, v4
	s_add_i32 s44, s31, s22
	s_nop 0
	v_addc_co_u32_e32 v9, vcc, 0, v5, vcc
	s_cmpk_lt_i32 s44, 0x2200
	s_cselect_b64 s[12:13], -1, 0
	s_and_b64 s[48:49], s[12:13], exec
	s_cselect_b32 s10, s44, s22
	s_mul_hi_i32 s49, s10, 0x4c00
	s_mulk_i32 s10, 0x4c00
	s_add_u32 s48, s8, s10
	s_addc_u32 s49, s9, s49
	v_lshl_add_u64 v[10:11], s[48:49], 0, v[32:33]
	global_load_dwordx4 v[12:15], v58, s[4:5] offset:3072
	global_load_dwordx4 v[4:7], v58, s[48:49] offset:3072
	s_cmpk_gt_i32 s22, 0x1fff
	s_waitcnt vmcnt(0)
	v_and_b32_e32 v75, 0xffff0000, v0
	v_lshlrev_b32_e32 v74, 16, v0
	v_and_b32_e32 v66, 0xffff0000, v1
	v_lshlrev_b32_e32 v67, 16, v1
	v_mul_f32_e32 v76, v75, v75
	v_pk_mul_f32 v[0:1], v[66:67], v[66:67]
	v_fmac_f32_e32 v76, v74, v74
	v_and_b32_e32 v68, 0xffff0000, v2
	v_lshlrev_b32_e32 v69, 16, v2
	v_add_f32_e32 v1, v1, v76
	v_and_b32_e32 v70, 0xffff0000, v3
	v_lshlrev_b32_e32 v71, 16, v3
	v_pk_mul_f32 v[2:3], v[68:69], v[68:69]
	v_add_f32_e32 v0, v0, v1
	v_add_f32_e32 v0, v3, v0
	v_pk_mul_f32 v[72:73], v[70:71], v[70:71]
	v_add_f32_e32 v0, v2, v0
	v_add_f32_e32 v0, v73, v0
	v_add_f32_e32 v0, v72, v0
	v_mov_b32_e32 v1, v0
	s_nop 1
	v_mov_b32_dpp v1, v1 quad_perm:[1,0,3,2] row_mask:0xf bank_mask:0xf
	v_add_f32_e32 v0, v0, v1
	v_mov_b32_e32 v1, v0
	s_nop 1
	v_mov_b32_dpp v1, v1 quad_perm:[2,3,0,1] row_mask:0xf bank_mask:0xf
	v_add_f32_e32 v0, v0, v1
	v_mov_b32_e32 v1, v0
	s_nop 1
	v_mov_b32_dpp v1, v1 row_half_mirror row_mask:0xf bank_mask:0xf
	v_add_f32_e32 v0, v0, v1
	v_mov_b32_e32 v1, v0
	s_nop 1
	v_mov_b32_dpp v1, v1 row_mirror row_mask:0xf bank_mask:0xf
	v_add_f32_e32 v0, v0, v1
	v_fmamk_f32 v0, v0, 0x3c000000, v59
	v_mul_f32_e32 v1, 0x4b800000, v0
	v_cmp_gt_f32_e32 vcc, s43, v0
	s_nop 1
	v_cndmask_b32_e32 v0, v0, v1, vcc
	v_rsq_f32_e32 v72, v0
	v_add_co_u32_e64 v0, s[4:5], s42, v10
	v_mul_f32_e32 v73, 0x45800000, v72
	v_cndmask_b32_e32 v72, v72, v73, vcc
	v_mul_f32_e32 v66, v72, v66
	v_mul_f32_e32 v57, v57, v66
	v_mul_f32_e32 v66, v72, v69
	v_mul_f32_e32 v67, v72, v67
	v_mul_f32_e32 v66, v50, v66
	v_mul_f32_e32 v50, v72, v68
	v_mul_f32_e32 v56, v56, v67
	v_mul_f32_e32 v67, v51, v50
	v_mul_f32_e32 v50, v72, v71
	v_mul_f32_e32 v68, v52, v50
	v_mul_f32_e32 v50, v72, v70
	v_addc_co_u32_e64 v1, s[4:5], 0, v11, s[4:5]
	v_mul_f32_e32 v73, v72, v74
	v_mul_f32_e32 v74, v72, v75
	v_mul_f32_e32 v53, v53, v50
	global_load_dwordx4 v[8:11], v[8:9], off offset:2048
	s_nop 0
	global_load_dwordx4 v[0:3], v[0:1], off offset:2048
	v_mul_f32_e32 v54, v54, v73
	v_mul_f32_e32 v55, v55, v74
	v_cvt_pk_bf16_f32 v50, v54, v55
	v_cvt_pk_bf16_f32 v51, v56, v57
	v_cvt_pk_bf16_f32 v52, v66, v67
	v_cvt_pk_bf16_f32 v53, v68, v53
	global_store_dwordx4 v[64:65], v[50:53], off sc1
	global_load_dwordx4 v[50:53], v[36:37], off
	s_nop 0
	global_load_dwordx4 v[64:67], v[36:37], off offset:16
	v_lshlrev_b32_e32 v56, 16, v60
	v_and_b32_e32 v57, 0xffff0000, v60
	v_lshlrev_b32_e32 v60, 16, v61
	v_and_b32_e32 v61, 0xffff0000, v61
	v_pk_mul_f32 v[70:71], v[56:57], v[56:57]
	v_pk_mul_f32 v[72:73], v[60:61], v[60:61]
	v_add_f32_e32 v70, v70, v71
	v_lshlrev_b32_e32 v68, 16, v62
	v_and_b32_e32 v69, 0xffff0000, v62
	v_add_f32_e32 v70, v72, v70
	v_pk_mul_f32 v[74:75], v[68:69], v[68:69]
	v_add_f32_e32 v70, v73, v70
	v_and_b32_e32 v54, 0xffff0000, v63
	v_lshlrev_b32_e32 v55, 16, v63
	v_add_f32_e32 v70, v74, v70
	v_pk_mul_f32 v[62:63], v[54:55], v[54:55]
	v_add_f32_e32 v70, v75, v70
	v_add_f32_e32 v63, v63, v70
	v_add_f32_e32 v62, v62, v63
	v_mov_b32_e32 v63, v62
	s_nop 1
	v_mov_b32_dpp v63, v63 quad_perm:[1,0,3,2] row_mask:0xf bank_mask:0xf
	v_add_f32_e32 v62, v62, v63
	v_mov_b32_e32 v63, v62
	s_nop 1
	v_mov_b32_dpp v63, v63 quad_perm:[2,3,0,1] row_mask:0xf bank_mask:0xf
	v_add_f32_e32 v62, v62, v63
	v_mov_b32_e32 v63, v62
	s_nop 1
	v_mov_b32_dpp v63, v63 row_half_mirror row_mask:0xf bank_mask:0xf
	v_add_f32_e32 v62, v62, v63
	v_fmamk_f32 v62, v62, 0x3c800000, v59
	v_mul_f32_e32 v63, 0x4b800000, v62
	v_cmp_gt_f32_e32 vcc, s43, v62
	s_nop 1
	v_cndmask_b32_e32 v62, v62, v63, vcc
	v_rsq_f32_e32 v62, v62
	s_nop 0
	v_mul_f32_e32 v63, 0x45800000, v62
	v_cndmask_b32_e32 v62, v62, v63, vcc
	v_pk_mul_f32 v[56:57], v[62:63], v[56:57] op_sel_hi:[0,1]
	v_pk_mul_f32 v[60:61], v[62:63], v[60:61] op_sel_hi:[0,1]
	v_pk_mul_f32 v[68:69], v[62:63], v[68:69] op_sel_hi:[0,1]
	v_pk_mul_f32 v[62:63], v[62:63], v[54:55] op_sel_hi:[0,1]
	s_waitcnt vmcnt(1)
	v_pk_mul_f32 v[56:57], v[50:51], v[56:57]
	v_pk_mul_f32 v[54:55], v[52:53], v[60:61]
	s_waitcnt vmcnt(0)
	v_pk_mul_f32 v[52:53], v[64:65], v[68:69]
	v_pk_mul_f32 v[50:51], v[66:67], v[62:63] op_sel:[0,1] op_sel_hi:[1,0]
	s_cbranch_scc0 .LBB0_387
	s_and_saveexec_b64 s[4:5], s[2:3]
	s_cbranch_execnz .LBB0_388

.LBB0_388:
	v_cvt_pk_bf16_f32 v60, v56, v57
	v_cvt_pk_bf16_f32 v61, v54, v55
	v_cvt_pk_bf16_f32 v62, v52, v53
	v_cvt_pk_bf16_f32 v63, v50, v51
	global_store_dwordx4 v[48:49], v[60:63], off sc1
	s_or_b64 exec, exec, s[4:5]
	s_andn2_b64 vcc, exec, s[20:21]
	s_cbranch_vccnz .LBB0_384
.LBB0_389:
	global_load_dwordx4 v[48:51], v[34:35], off
	global_load_dwordx4 v[52:55], v[34:35], off offset:16
	v_and_b32_e32 v67, 0xffff0000, v28
	v_lshlrev_b32_e32 v66, 16, v28
	v_and_b32_e32 v28, 0xffff0000, v29
	v_lshlrev_b32_e32 v29, 16, v29
	v_mul_f32_e32 v68, v67, v67
	v_pk_mul_f32 v[60:61], v[28:29], v[28:29]
	v_fmac_f32_e32 v68, v66, v66
	v_and_b32_e32 v56, 0xffff0000, v30
	v_lshlrev_b32_e32 v57, 16, v30
	v_add_f32_e32 v61, v61, v68
	v_pk_mul_f32 v[62:63], v[56:57], v[56:57]
	v_add_f32_e32 v60, v60, v61
	v_and_b32_e32 v30, 0xffff0000, v31
	v_lshlrev_b32_e32 v31, 16, v31
	v_add_f32_e32 v60, v63, v60
	v_pk_mul_f32 v[64:65], v[30:31], v[30:31]
	v_add_f32_e32 v60, v62, v60
	v_add_f32_e32 v60, v65, v60
	v_add_f32_e32 v60, v64, v60
	v_mov_b32_e32 v61, v60
	s_cmpk_gt_i32 s47, 0x1fff
	s_nop 0
	v_mov_b32_dpp v61, v61 quad_perm:[1,0,3,2] row_mask:0xf bank_mask:0xf
	v_add_f32_e32 v60, v60, v61
	v_mov_b32_e32 v61, v60
	s_nop 1
	v_mov_b32_dpp v61, v61 quad_perm:[2,3,0,1] row_mask:0xf bank_mask:0xf
	v_add_f32_e32 v60, v60, v61
	v_mov_b32_e32 v61, v60
	s_nop 1
	v_mov_b32_dpp v61, v61 row_half_mirror row_mask:0xf bank_mask:0xf
	v_add_f32_e32 v60, v60, v61
	v_mov_b32_e32 v61, v60
	s_nop 1
	v_mov_b32_dpp v61, v61 row_mirror row_mask:0xf bank_mask:0xf
	v_add_f32_e32 v60, v60, v61
	v_fmamk_f32 v60, v60, 0x3c000000, v59
	v_mul_f32_e32 v61, 0x4b800000, v60
	v_cmp_gt_f32_e32 vcc, s43, v60
	s_nop 1
	v_cndmask_b32_e32 v60, v60, v61, vcc
	v_rsq_f32_e32 v62, v60
	v_lshl_add_u64 v[60:61], s[6:7], 0, v[40:41]
	v_mul_f32_e32 v63, 0x45800000, v62
	v_cndmask_b32_e32 v62, v62, v63, vcc
	v_mul_f32_e32 v29, v62, v29
	v_mul_f32_e32 v31, v62, v31
	v_mul_f32_e32 v63, v62, v66
	v_mul_f32_e32 v64, v62, v67
	v_mul_f32_e32 v28, v62, v28
	v_mul_f32_e32 v57, v62, v57
	v_mul_f32_e32 v56, v62, v56
	v_mul_f32_e32 v30, v62, v30
	s_waitcnt vmcnt(1)
	v_mul_f32_e32 v29, v50, v29
	s_waitcnt vmcnt(0)
	v_mul_f32_e32 v31, v54, v31
	v_mul_f32_e32 v48, v48, v63
	v_mul_f32_e32 v49, v49, v64
	v_mul_f32_e32 v50, v51, v28
	v_mul_f32_e32 v51, v52, v57
	v_mul_f32_e32 v52, v53, v56
	v_mul_f32_e32 v53, v55, v30
	v_cvt_pk_bf16_f32 v28, v48, v49
	v_cvt_pk_bf16_f32 v29, v29, v50
	v_cvt_pk_bf16_f32 v30, v51, v52
	v_cvt_pk_bf16_f32 v31, v31, v53
	global_store_dwordx4 v[60:61], v[28:31], off sc1
	global_load_dwordx4 v[48:51], v[36:37], off
	global_load_dwordx4 v[52:55], v[36:37], off offset:16
	v_lshlrev_b32_e32 v30, 16, v24
	v_and_b32_e32 v31, 0xffff0000, v24
	v_lshlrev_b32_e32 v24, 16, v25
	v_and_b32_e32 v25, 0xffff0000, v25
	v_pk_mul_f32 v[60:61], v[30:31], v[30:31]
	v_pk_mul_f32 v[62:63], v[24:25], v[24:25]
	v_add_f32_e32 v60, v60, v61
	v_lshlrev_b32_e32 v56, 16, v26
	v_and_b32_e32 v57, 0xffff0000, v26
	v_add_f32_e32 v60, v62, v60
	v_pk_mul_f32 v[64:65], v[56:57], v[56:57]
	v_add_f32_e32 v60, v63, v60
	v_and_b32_e32 v28, 0xffff0000, v27
	v_lshlrev_b32_e32 v29, 16, v27
	v_add_f32_e32 v60, v64, v60
	v_pk_mul_f32 v[26:27], v[28:29], v[28:29]
	v_add_f32_e32 v60, v65, v60
	v_add_f32_e32 v27, v27, v60
	v_add_f32_e32 v26, v26, v27
	v_mov_b32_e32 v27, v26
	s_nop 1
	v_mov_b32_dpp v27, v27 quad_perm:[1,0,3,2] row_mask:0xf bank_mask:0xf
	v_add_f32_e32 v26, v26, v27
	v_mov_b32_e32 v27, v26
	s_nop 1
	v_mov_b32_dpp v27, v27 quad_perm:[2,3,0,1] row_mask:0xf bank_mask:0xf
	v_add_f32_e32 v26, v26, v27
	v_mov_b32_e32 v27, v26
	s_nop 1
	v_mov_b32_dpp v27, v27 row_half_mirror row_mask:0xf bank_mask:0xf
	v_add_f32_e32 v26, v26, v27
	v_fmamk_f32 v26, v26, 0x3c800000, v59
	v_mul_f32_e32 v27, 0x4b800000, v26
	v_cmp_gt_f32_e32 vcc, s43, v26
	s_nop 1
	v_cndmask_b32_e32 v26, v26, v27, vcc
	v_rsq_f32_e32 v26, v26
	s_nop 0
	v_mul_f32_e32 v27, 0x45800000, v26
	v_cndmask_b32_e32 v26, v26, v27, vcc
	v_pk_mul_f32 v[30:31], v[26:27], v[30:31] op_sel_hi:[0,1]
	v_pk_mul_f32 v[24:25], v[26:27], v[24:25] op_sel_hi:[0,1]
	v_pk_mul_f32 v[56:57], v[26:27], v[56:57] op_sel_hi:[0,1]
	v_pk_mul_f32 v[60:61], v[26:27], v[28:29] op_sel_hi:[0,1]
	s_waitcnt vmcnt(1)
	v_pk_mul_f32 v[30:31], v[48:49], v[30:31]
	v_pk_mul_f32 v[28:29], v[50:51], v[24:25]
	s_waitcnt vmcnt(0)
	v_pk_mul_f32 v[26:27], v[52:53], v[56:57]
	v_pk_mul_f32 v[24:25], v[54:55], v[60:61] op_sel:[0,1] op_sel_hi:[1,0]
	s_cbranch_scc1 .LBB0_391
	s_add_i32 s4, s39, s25
	s_and_b32 s4, s4, 0x1ffe0
	s_lshl_b32 s10, s4, 3
	v_lshl_add_u64 v[56:57], v[38:39], 0, s[10:11]
	global_load_dwordx4 v[48:51], v[56:57], off
	global_load_dwordx4 v[52:55], v[56:57], off offset:16
	global_load_dwordx4 v[60:63], v[56:57], off offset:32
	global_load_dwordx4 v[64:67], v[56:57], off offset:48
	v_mov_b32_e32 v56, v30
	v_mov_b32_e32 v57, v31
	v_mov_b32_e32 v68, v28
	v_mov_b32_e32 v69, v29
	v_mov_b32_e32 v70, v26
	v_mov_b32_e32 v71, v27
	v_mov_b32_e32 v72, v24
	v_mov_b32_e32 v73, v25
	v_mov_b32_dpp v56, v56 row_shl:4 row_mask:0xf bank_mask:0x5
	v_mov_b32_dpp v57, v57 row_shl:4 row_mask:0xf bank_mask:0x5
	v_mov_b32_dpp v68, v68 row_shl:4 row_mask:0xf bank_mask:0x5
	v_mov_b32_dpp v69, v69 row_shl:4 row_mask:0xf bank_mask:0x5
	v_mov_b32_dpp v70, v70 row_shl:4 row_mask:0xf bank_mask:0x5
	v_mov_b32_dpp v71, v71 row_shl:4 row_mask:0xf bank_mask:0x5
	v_mov_b32_dpp v72, v72 row_shl:4 row_mask:0xf bank_mask:0x5
	v_mov_b32_dpp v73, v73 row_shl:4 row_mask:0xf bank_mask:0x5
	v_mov_b32_dpp v56, v30 row_shr:4 row_mask:0xf bank_mask:0xa
	v_mov_b32_dpp v57, v31 row_shr:4 row_mask:0xf bank_mask:0xa
	v_mov_b32_dpp v68, v28 row_shr:4 row_mask:0xf bank_mask:0xa
	v_mov_b32_dpp v69, v29 row_shr:4 row_mask:0xf bank_mask:0xa
	v_mov_b32_dpp v70, v26 row_shr:4 row_mask:0xf bank_mask:0xa
	v_mov_b32_dpp v71, v27 row_shr:4 row_mask:0xf bank_mask:0xa
	v_mov_b32_dpp v72, v24 row_shr:4 row_mask:0xf bank_mask:0xa
	v_mov_b32_dpp v73, v25 row_shr:4 row_mask:0xf bank_mask:0xa
	s_waitcnt vmcnt(3)
	v_mov_b32_e32 v75, v50
	v_mov_b32_e32 v50, v49
	s_waitcnt vmcnt(2)
	v_mov_b32_e32 v49, v54
	v_mov_b32_e32 v54, v53
	s_waitcnt vmcnt(1)
	v_mov_b32_e32 v53, v62
	v_mov_b32_e32 v62, v61
	s_waitcnt vmcnt(0)
	v_mov_b32_e32 v61, v66
	v_mov_b32_e32 v66, v65
	v_pk_mul_f32 v[50:51], v[50:51], v[56:57]
	v_pk_mul_f32 v[54:55], v[54:55], v[68:69]
	v_pk_mul_f32 v[56:57], v[62:63], v[70:71]
	v_pk_mul_f32 v[62:63], v[66:67], v[72:73]
	v_mov_b32_e32 v74, v48
	v_mov_b32_e32 v48, v52
	v_mov_b32_e32 v52, v60
	v_mov_b32_e32 v60, v64
	v_cndmask_b32_e64 v51, v51, -v51, s[0:1]
	v_cndmask_b32_e64 v50, v50, -v50, s[0:1]
	v_cndmask_b32_e64 v55, v55, -v55, s[0:1]
	v_cndmask_b32_e64 v54, v54, -v54, s[0:1]
	v_cndmask_b32_e64 v57, v57, -v57, s[0:1]
	v_cndmask_b32_e64 v56, v56, -v56, s[0:1]
	v_cndmask_b32_e64 v63, v63, -v63, s[0:1]
	v_cndmask_b32_e64 v62, v62, -v62, s[0:1]
	v_pk_fma_f32 v[30:31], v[30:31], v[74:75], v[50:51]
	v_pk_fma_f32 v[28:29], v[28:29], v[48:49], v[54:55]
	v_pk_fma_f32 v[26:27], v[26:27], v[52:53], v[56:57]
	v_pk_fma_f32 v[24:25], v[24:25], v[60:61], v[62:63]
.LBB0_391:
	s_and_saveexec_b64 s[4:5], s[2:3]
	s_cbranch_execz .LBB0_393
	v_cvt_pk_bf16_f32 v48, v30, v31
	v_cvt_pk_bf16_f32 v49, v28, v29
	v_cvt_pk_bf16_f32 v50, v26, v27
	v_cvt_pk_bf16_f32 v51, v24, v25
	v_lshl_add_u64 v[24:25], s[6:7], 0, v[42:43]
	global_store_dwordx4 v[24:25], v[48:51], off sc1

.LBB0_394:
	global_load_dwordx4 v[24:27], v[34:35], off
	global_load_dwordx4 v[28:31], v[34:35], off offset:16
	v_and_b32_e32 v57, 0xffff0000, v20
	v_lshlrev_b32_e32 v56, 16, v20
	v_and_b32_e32 v20, 0xffff0000, v21
	v_lshlrev_b32_e32 v21, 16, v21
	v_mul_f32_e32 v60, v57, v57
	v_pk_mul_f32 v[50:51], v[20:21], v[20:21]
	v_fmac_f32_e32 v60, v56, v56
	v_and_b32_e32 v48, 0xffff0000, v22
	v_lshlrev_b32_e32 v49, 16, v22
	v_add_f32_e32 v51, v51, v60
	v_pk_mul_f32 v[52:53], v[48:49], v[48:49]
	v_add_f32_e32 v50, v50, v51
	v_and_b32_e32 v22, 0xffff0000, v23
	v_lshlrev_b32_e32 v23, 16, v23
	v_add_f32_e32 v50, v53, v50
	v_pk_mul_f32 v[54:55], v[22:23], v[22:23]
	v_add_f32_e32 v50, v52, v50
	v_add_f32_e32 v50, v55, v50
	v_add_f32_e32 v50, v54, v50
	v_mov_b32_e32 v51, v50
	s_mul_i32 s4, s46, 0x4c00
	s_mul_hi_i32 s5, s46, 0x4c00
	v_mov_b32_dpp v51, v51 quad_perm:[1,0,3,2] row_mask:0xf bank_mask:0xf
	v_add_f32_e32 v50, v50, v51
	v_mov_b32_e32 v51, v50
	s_add_u32 s4, s8, s4
	s_addc_u32 s5, s9, s5
	v_mov_b32_dpp v51, v51 quad_perm:[2,3,0,1] row_mask:0xf bank_mask:0xf
	v_add_f32_e32 v50, v50, v51
	v_mov_b32_e32 v51, v50
	s_cmpk_gt_i32 s46, 0x1fff
	s_nop 0
	v_mov_b32_dpp v51, v51 row_half_mirror row_mask:0xf bank_mask:0xf
	v_add_f32_e32 v50, v50, v51
	v_mov_b32_e32 v51, v50
	s_nop 1
	v_mov_b32_dpp v51, v51 row_mirror row_mask:0xf bank_mask:0xf
	v_add_f32_e32 v50, v50, v51
	v_fmamk_f32 v50, v50, 0x3c000000, v59
	v_mul_f32_e32 v51, 0x4b800000, v50
	v_cmp_gt_f32_e32 vcc, s43, v50
	s_nop 1
	v_cndmask_b32_e32 v50, v50, v51, vcc
	v_rsq_f32_e32 v50, v50
	s_nop 0
	v_mul_f32_e32 v51, 0x45800000, v50
	v_cndmask_b32_e32 v50, v50, v51, vcc
	v_mul_f32_e32 v21, v50, v21
	v_mul_f32_e32 v23, v50, v23
	v_mul_f32_e32 v51, v50, v56
	v_mul_f32_e32 v52, v50, v57
	v_mul_f32_e32 v20, v50, v20
	v_mul_f32_e32 v49, v50, v49
	v_mul_f32_e32 v48, v50, v48
	v_mul_f32_e32 v22, v50, v22
	s_waitcnt vmcnt(1)
	v_mul_f32_e32 v21, v26, v21
	s_waitcnt vmcnt(0)
	v_mul_f32_e32 v23, v30, v23
	v_mul_f32_e32 v24, v24, v51
	v_mul_f32_e32 v25, v25, v52
	v_mul_f32_e32 v26, v27, v20
	v_mul_f32_e32 v27, v28, v49
	v_mul_f32_e32 v28, v29, v48
	v_mul_f32_e32 v29, v31, v22
	v_cvt_pk_bf16_f32 v20, v24, v25
	v_cvt_pk_bf16_f32 v21, v21, v26
	v_cvt_pk_bf16_f32 v22, v27, v28
	v_cvt_pk_bf16_f32 v23, v23, v29
	global_store_dwordx4 v58, v[20:23], s[4:5] offset:3072 sc1
	global_load_dwordx4 v[22:25], v[36:37], off
	s_nop 0
	global_load_dwordx4 v[26:29], v[36:37], off offset:16
	v_lshlrev_b32_e32 v30, 16, v16
	v_and_b32_e32 v31, 0xffff0000, v16
	v_lshlrev_b32_e32 v16, 16, v17
	v_and_b32_e32 v17, 0xffff0000, v17
	v_pk_mul_f32 v[50:51], v[30:31], v[30:31]
	v_pk_mul_f32 v[52:53], v[16:17], v[16:17]
	v_add_f32_e32 v50, v50, v51
	v_lshlrev_b32_e32 v48, 16, v18
	v_and_b32_e32 v49, 0xffff0000, v18
	v_add_f32_e32 v50, v52, v50
	v_pk_mul_f32 v[54:55], v[48:49], v[48:49]
	v_add_f32_e32 v50, v53, v50
	v_and_b32_e32 v20, 0xffff0000, v19
	v_lshlrev_b32_e32 v21, 16, v19
	v_add_f32_e32 v50, v54, v50
	v_pk_mul_f32 v[18:19], v[20:21], v[20:21]
	v_add_f32_e32 v50, v55, v50
	v_add_f32_e32 v19, v19, v50
	v_add_f32_e32 v18, v18, v19
	v_mov_b32_e32 v19, v18
	s_nop 1
	v_mov_b32_dpp v19, v19 quad_perm:[1,0,3,2] row_mask:0xf bank_mask:0xf
	v_add_f32_e32 v18, v18, v19
	v_mov_b32_e32 v19, v18
	s_nop 1
	v_mov_b32_dpp v19, v19 quad_perm:[2,3,0,1] row_mask:0xf bank_mask:0xf
	v_add_f32_e32 v18, v18, v19
	v_mov_b32_e32 v19, v18
	s_nop 1
	v_mov_b32_dpp v19, v19 row_half_mirror row_mask:0xf bank_mask:0xf
	v_add_f32_e32 v18, v18, v19
	v_fmamk_f32 v18, v18, 0x3c800000, v59
	v_mul_f32_e32 v19, 0x4b800000, v18
	v_cmp_gt_f32_e32 vcc, s43, v18
	s_nop 1
	v_cndmask_b32_e32 v18, v18, v19, vcc
	v_rsq_f32_e32 v18, v18
	s_nop 0
	v_mul_f32_e32 v19, 0x45800000, v18
	v_cndmask_b32_e32 v18, v18, v19, vcc
	v_pk_mul_f32 v[30:31], v[18:19], v[30:31] op_sel_hi:[0,1]
	v_pk_mul_f32 v[16:17], v[18:19], v[16:17] op_sel_hi:[0,1]
	v_pk_mul_f32 v[48:49], v[18:19], v[48:49] op_sel_hi:[0,1]
	v_pk_mul_f32 v[50:51], v[18:19], v[20:21] op_sel_hi:[0,1]
	s_waitcnt vmcnt(1)
	v_pk_mul_f32 v[22:23], v[22:23], v[30:31]
	v_pk_mul_f32 v[20:21], v[24:25], v[16:17]
	s_waitcnt vmcnt(0)
	v_pk_mul_f32 v[18:19], v[26:27], v[48:49]
	v_pk_mul_f32 v[16:17], v[28:29], v[50:51] op_sel:[0,1] op_sel_hi:[1,0]
	s_cbranch_scc1 .LBB0_396
	s_add_i32 s10, s28, s25
	s_and_b32 s10, s10, 0x1ffe0
	s_lshl_b32 s10, s10, 3
	v_lshl_add_u64 v[56:57], v[38:39], 0, s[10:11]
	global_load_dwordx4 v[24:27], v[56:57], off
	global_load_dwordx4 v[28:31], v[56:57], off offset:16
	global_load_dwordx4 v[48:51], v[56:57], off offset:32
	global_load_dwordx4 v[52:55], v[56:57], off offset:48
	v_mov_b32_e32 v56, v22
	v_mov_b32_e32 v57, v23
	v_mov_b32_e32 v60, v20
	v_mov_b32_e32 v61, v21
	v_mov_b32_e32 v62, v18
	v_mov_b32_e32 v63, v19
	v_mov_b32_e32 v64, v16
	v_mov_b32_e32 v65, v17
	v_mov_b32_dpp v56, v56 row_shl:4 row_mask:0xf bank_mask:0x5
	v_mov_b32_dpp v57, v57 row_shl:4 row_mask:0xf bank_mask:0x5
	v_mov_b32_dpp v60, v60 row_shl:4 row_mask:0xf bank_mask:0x5
	v_mov_b32_dpp v61, v61 row_shl:4 row_mask:0xf bank_mask:0x5
	v_mov_b32_dpp v62, v62 row_shl:4 row_mask:0xf bank_mask:0x5
	v_mov_b32_dpp v63, v63 row_shl:4 row_mask:0xf bank_mask:0x5
	v_mov_b32_dpp v64, v64 row_shl:4 row_mask:0xf bank_mask:0x5
	v_mov_b32_dpp v65, v65 row_shl:4 row_mask:0xf bank_mask:0x5
	v_mov_b32_dpp v56, v22 row_shr:4 row_mask:0xf bank_mask:0xa
	v_mov_b32_dpp v57, v23 row_shr:4 row_mask:0xf bank_mask:0xa
	v_mov_b32_dpp v60, v20 row_shr:4 row_mask:0xf bank_mask:0xa
	v_mov_b32_dpp v61, v21 row_shr:4 row_mask:0xf bank_mask:0xa
	v_mov_b32_dpp v62, v18 row_shr:4 row_mask:0xf bank_mask:0xa
	v_mov_b32_dpp v63, v19 row_shr:4 row_mask:0xf bank_mask:0xa
	v_mov_b32_dpp v64, v16 row_shr:4 row_mask:0xf bank_mask:0xa
	v_mov_b32_dpp v65, v17 row_shr:4 row_mask:0xf bank_mask:0xa
	s_waitcnt vmcnt(3)
	v_mov_b32_e32 v67, v26
	v_mov_b32_e32 v26, v25
	s_waitcnt vmcnt(2)
	v_mov_b32_e32 v25, v30
	v_mov_b32_e32 v30, v29
	s_waitcnt vmcnt(1)
	v_mov_b32_e32 v29, v50
	v_mov_b32_e32 v50, v49
	s_waitcnt vmcnt(0)
	v_mov_b32_e32 v49, v54
	v_mov_b32_e32 v54, v53
	v_mov_b32_e32 v66, v24
	v_mov_b32_e32 v24, v28
	v_mov_b32_e32 v28, v48
	v_mov_b32_e32 v48, v52
	v_pk_mul_f32 v[26:27], v[26:27], v[56:57]
	v_pk_mul_f32 v[30:31], v[30:31], v[60:61]
	v_pk_mul_f32 v[50:51], v[50:51], v[62:63]
	v_pk_mul_f32 v[52:53], v[54:55], v[64:65]
	v_cndmask_b32_e64 v27, v27, -v27, s[0:1]
	v_cndmask_b32_e64 v26, v26, -v26, s[0:1]
	v_cndmask_b32_e64 v31, v31, -v31, s[0:1]
	v_cndmask_b32_e64 v30, v30, -v30, s[0:1]
	v_cndmask_b32_e64 v51, v51, -v51, s[0:1]
	v_cndmask_b32_e64 v50, v50, -v50, s[0:1]
	v_cndmask_b32_e64 v53, v53, -v53, s[0:1]
	v_cndmask_b32_e64 v52, v52, -v52, s[0:1]
	v_pk_fma_f32 v[22:23], v[22:23], v[66:67], v[26:27]
	v_pk_fma_f32 v[20:21], v[20:21], v[24:25], v[30:31]
	v_pk_fma_f32 v[18:19], v[18:19], v[28:29], v[50:51]
	v_pk_fma_f32 v[16:17], v[16:17], v[48:49], v[52:53]
.LBB0_396:
	s_and_saveexec_b64 s[18:19], s[2:3]
	s_cbranch_execz .LBB0_398
	v_cvt_pk_bf16_f32 v22, v22, v23
	v_cvt_pk_bf16_f32 v23, v20, v21
	v_cvt_pk_bf16_f32 v24, v18, v19
	v_cvt_pk_bf16_f32 v25, v16, v17
	v_lshl_add_u64 v[16:17], s[4:5], 0, v[32:33]
	v_add_co_u32_e32 v16, vcc, 0x1000, v16
	s_nop 1
	v_addc_co_u32_e32 v17, vcc, 0, v17, vcc
	global_store_dwordx4 v[16:17], v[22:25], off offset:2048 sc1

.LBB0_399:
	global_load_dwordx4 v[16:19], v[34:35], off
	global_load_dwordx4 v[20:23], v[34:35], off offset:16
	v_and_b32_e32 v49, 0xffff0000, v12
	v_lshlrev_b32_e32 v48, 16, v12
	v_and_b32_e32 v12, 0xffff0000, v13
	v_lshlrev_b32_e32 v13, 16, v13
	v_mul_f32_e32 v50, v49, v49
	v_pk_mul_f32 v[26:27], v[12:13], v[12:13]
	v_fmac_f32_e32 v50, v48, v48
	v_and_b32_e32 v24, 0xffff0000, v14
	v_lshlrev_b32_e32 v25, 16, v14
	v_add_f32_e32 v27, v27, v50
	v_pk_mul_f32 v[28:29], v[24:25], v[24:25]
	v_add_f32_e32 v26, v26, v27
	v_and_b32_e32 v14, 0xffff0000, v15
	v_lshlrev_b32_e32 v15, 16, v15
	v_add_f32_e32 v26, v29, v26
	v_pk_mul_f32 v[30:31], v[14:15], v[14:15]
	v_add_f32_e32 v26, v28, v26
	v_add_f32_e32 v26, v31, v26
	v_add_f32_e32 v26, v30, v26
	v_mov_b32_e32 v27, v26
	s_mul_i32 s4, s45, 0x4c00
	s_mul_hi_i32 s5, s45, 0x4c00
	v_mov_b32_dpp v27, v27 quad_perm:[1,0,3,2] row_mask:0xf bank_mask:0xf
	v_add_f32_e32 v26, v26, v27
	v_mov_b32_e32 v27, v26
	s_add_u32 s4, s8, s4
	s_addc_u32 s5, s9, s5
	v_mov_b32_dpp v27, v27 quad_perm:[2,3,0,1] row_mask:0xf bank_mask:0xf
	v_add_f32_e32 v26, v26, v27
	v_mov_b32_e32 v27, v26
	s_cmpk_gt_i32 s45, 0x1fff
	s_nop 0
	v_mov_b32_dpp v27, v27 row_half_mirror row_mask:0xf bank_mask:0xf
	v_add_f32_e32 v26, v26, v27
	v_mov_b32_e32 v27, v26
	s_nop 1
	v_mov_b32_dpp v27, v27 row_mirror row_mask:0xf bank_mask:0xf
	v_add_f32_e32 v26, v26, v27
	v_fmamk_f32 v26, v26, 0x3c000000, v59
	v_mul_f32_e32 v27, 0x4b800000, v26
	v_cmp_gt_f32_e32 vcc, s43, v26
	s_nop 1
	v_cndmask_b32_e32 v26, v26, v27, vcc
	v_rsq_f32_e32 v26, v26
	s_nop 0
	v_mul_f32_e32 v27, 0x45800000, v26
	v_cndmask_b32_e32 v26, v26, v27, vcc
	v_mul_f32_e32 v13, v26, v13
	v_mul_f32_e32 v15, v26, v15
	v_mul_f32_e32 v27, v26, v48
	v_mul_f32_e32 v28, v26, v49
	v_mul_f32_e32 v12, v26, v12
	v_mul_f32_e32 v25, v26, v25
	v_mul_f32_e32 v24, v26, v24
	v_mul_f32_e32 v14, v26, v14
	s_waitcnt vmcnt(1)
	v_mul_f32_e32 v13, v18, v13
	s_waitcnt vmcnt(0)
	v_mul_f32_e32 v15, v22, v15
	v_mul_f32_e32 v16, v16, v27
	v_mul_f32_e32 v17, v17, v28
	v_mul_f32_e32 v18, v19, v12
	v_mul_f32_e32 v19, v20, v25
	v_mul_f32_e32 v20, v21, v24
	v_mul_f32_e32 v21, v23, v14
	v_cvt_pk_bf16_f32 v12, v16, v17
	v_cvt_pk_bf16_f32 v13, v13, v18
	v_cvt_pk_bf16_f32 v14, v19, v20
	v_cvt_pk_bf16_f32 v15, v15, v21
	global_store_dwordx4 v58, v[12:15], s[4:5] offset:3072 sc1
	global_load_dwordx4 v[14:17], v[36:37], off
	s_nop 0
	global_load_dwordx4 v[18:21], v[36:37], off offset:16
	v_lshlrev_b32_e32 v22, 16, v8
	v_and_b32_e32 v23, 0xffff0000, v8
	v_lshlrev_b32_e32 v8, 16, v9
	v_and_b32_e32 v9, 0xffff0000, v9
	v_pk_mul_f32 v[26:27], v[22:23], v[22:23]
	v_pk_mul_f32 v[28:29], v[8:9], v[8:9]
	v_add_f32_e32 v26, v26, v27
	v_lshlrev_b32_e32 v24, 16, v10
	v_and_b32_e32 v25, 0xffff0000, v10
	v_add_f32_e32 v26, v28, v26
	v_pk_mul_f32 v[30:31], v[24:25], v[24:25]
	v_add_f32_e32 v26, v29, v26
	v_and_b32_e32 v12, 0xffff0000, v11
	v_lshlrev_b32_e32 v13, 16, v11
	v_add_f32_e32 v26, v30, v26
	v_pk_mul_f32 v[10:11], v[12:13], v[12:13]
	v_add_f32_e32 v26, v31, v26
	v_add_f32_e32 v11, v11, v26
	v_add_f32_e32 v10, v10, v11
	v_mov_b32_e32 v11, v10
	s_nop 1
	v_mov_b32_dpp v11, v11 quad_perm:[1,0,3,2] row_mask:0xf bank_mask:0xf
	v_add_f32_e32 v10, v10, v11
	v_mov_b32_e32 v11, v10
	s_nop 1
	v_mov_b32_dpp v11, v11 quad_perm:[2,3,0,1] row_mask:0xf bank_mask:0xf
	v_add_f32_e32 v10, v10, v11
	v_mov_b32_e32 v11, v10
	s_nop 1
	v_mov_b32_dpp v11, v11 row_half_mirror row_mask:0xf bank_mask:0xf
	v_add_f32_e32 v10, v10, v11
	v_fmamk_f32 v10, v10, 0x3c800000, v59
	v_mul_f32_e32 v11, 0x4b800000, v10
	v_cmp_gt_f32_e32 vcc, s43, v10
	s_nop 1
	v_cndmask_b32_e32 v10, v10, v11, vcc
	v_rsq_f32_e32 v10, v10
	s_nop 0
	v_mul_f32_e32 v11, 0x45800000, v10
	v_cndmask_b32_e32 v10, v10, v11, vcc
	v_pk_mul_f32 v[22:23], v[10:11], v[22:23] op_sel_hi:[0,1]
	v_pk_mul_f32 v[8:9], v[10:11], v[8:9] op_sel_hi:[0,1]
	v_pk_mul_f32 v[24:25], v[10:11], v[24:25] op_sel_hi:[0,1]
	v_pk_mul_f32 v[26:27], v[10:11], v[12:13] op_sel_hi:[0,1]
	s_waitcnt vmcnt(1)
	v_pk_mul_f32 v[14:15], v[14:15], v[22:23]
	v_pk_mul_f32 v[12:13], v[16:17], v[8:9]
	s_waitcnt vmcnt(0)
	v_pk_mul_f32 v[10:11], v[18:19], v[24:25]
	v_pk_mul_f32 v[8:9], v[20:21], v[26:27] op_sel:[0,1] op_sel_hi:[1,0]
	s_cbranch_scc1 .LBB0_401
	s_add_i32 s10, s30, s25
	s_and_b32 s10, s10, 0x1ffe0
	s_lshl_b32 s10, s10, 3
	v_lshl_add_u64 v[48:49], v[38:39], 0, s[10:11]
	global_load_dwordx4 v[16:19], v[48:49], off
	global_load_dwordx4 v[20:23], v[48:49], off offset:16
	global_load_dwordx4 v[24:27], v[48:49], off offset:32
	global_load_dwordx4 v[28:31], v[48:49], off offset:48
	v_mov_b32_e32 v48, v14
	v_mov_b32_e32 v49, v15
	v_mov_b32_e32 v50, v12
	v_mov_b32_e32 v51, v13
	v_mov_b32_e32 v52, v10
	v_mov_b32_e32 v53, v11
	v_mov_b32_e32 v54, v8
	v_mov_b32_e32 v55, v9
	v_mov_b32_dpp v48, v48 row_shl:4 row_mask:0xf bank_mask:0x5
	v_mov_b32_dpp v49, v49 row_shl:4 row_mask:0xf bank_mask:0x5
	v_mov_b32_dpp v50, v50 row_shl:4 row_mask:0xf bank_mask:0x5
	v_mov_b32_dpp v51, v51 row_shl:4 row_mask:0xf bank_mask:0x5
	v_mov_b32_dpp v52, v52 row_shl:4 row_mask:0xf bank_mask:0x5
	v_mov_b32_dpp v53, v53 row_shl:4 row_mask:0xf bank_mask:0x5
	v_mov_b32_dpp v54, v54 row_shl:4 row_mask:0xf bank_mask:0x5
	v_mov_b32_dpp v55, v55 row_shl:4 row_mask:0xf bank_mask:0x5
	v_mov_b32_dpp v48, v14 row_shr:4 row_mask:0xf bank_mask:0xa
	v_mov_b32_dpp v49, v15 row_shr:4 row_mask:0xf bank_mask:0xa
	v_mov_b32_dpp v50, v12 row_shr:4 row_mask:0xf bank_mask:0xa
	v_mov_b32_dpp v51, v13 row_shr:4 row_mask:0xf bank_mask:0xa
	v_mov_b32_dpp v52, v10 row_shr:4 row_mask:0xf bank_mask:0xa
	v_mov_b32_dpp v53, v11 row_shr:4 row_mask:0xf bank_mask:0xa
	v_mov_b32_dpp v54, v8 row_shr:4 row_mask:0xf bank_mask:0xa
	v_mov_b32_dpp v55, v9 row_shr:4 row_mask:0xf bank_mask:0xa
	s_waitcnt vmcnt(3)
	v_mov_b32_e32 v57, v18
	v_mov_b32_e32 v18, v17
	s_waitcnt vmcnt(2)
	v_mov_b32_e32 v17, v22
	v_mov_b32_e32 v22, v21
	s_waitcnt vmcnt(1)
	v_mov_b32_e32 v21, v26
	v_mov_b32_e32 v26, v25
	s_waitcnt vmcnt(0)
	v_mov_b32_e32 v25, v30
	v_mov_b32_e32 v30, v29
	v_mov_b32_e32 v56, v16
	v_mov_b32_e32 v16, v20
	v_mov_b32_e32 v20, v24
	v_mov_b32_e32 v24, v28
	v_pk_mul_f32 v[18:19], v[18:19], v[48:49]
	v_pk_mul_f32 v[22:23], v[22:23], v[50:51]
	v_pk_mul_f32 v[26:27], v[26:27], v[52:53]
	v_pk_mul_f32 v[28:29], v[30:31], v[54:55]
	v_cndmask_b32_e64 v19, v19, -v19, s[0:1]
	v_cndmask_b32_e64 v18, v18, -v18, s[0:1]
	v_cndmask_b32_e64 v23, v23, -v23, s[0:1]
	v_cndmask_b32_e64 v22, v22, -v22, s[0:1]
	v_cndmask_b32_e64 v27, v27, -v27, s[0:1]
	v_cndmask_b32_e64 v26, v26, -v26, s[0:1]
	v_cndmask_b32_e64 v29, v29, -v29, s[0:1]
	v_cndmask_b32_e64 v28, v28, -v28, s[0:1]
	v_pk_fma_f32 v[14:15], v[14:15], v[56:57], v[18:19]
	v_pk_fma_f32 v[12:13], v[12:13], v[16:17], v[22:23]
	v_pk_fma_f32 v[10:11], v[10:11], v[20:21], v[26:27]
	v_pk_fma_f32 v[8:9], v[8:9], v[24:25], v[28:29]
.LBB0_401:
	s_and_saveexec_b64 s[16:17], s[2:3]
	s_cbranch_execz .LBB0_403
	v_cvt_pk_bf16_f32 v14, v14, v15
	v_cvt_pk_bf16_f32 v15, v12, v13
	v_cvt_pk_bf16_f32 v16, v10, v11
	v_cvt_pk_bf16_f32 v17, v8, v9
	v_lshl_add_u64 v[8:9], s[4:5], 0, v[32:33]
	v_add_co_u32_e32 v8, vcc, 0x1000, v8
	s_nop 1
	v_addc_co_u32_e32 v9, vcc, 0, v9, vcc
	global_store_dwordx4 v[8:9], v[14:17], off offset:2048 sc1

.LBB0_404:
	global_load_dwordx4 v[8:11], v[34:35], off
	global_load_dwordx4 v[12:15], v[34:35], off offset:16
	v_and_b32_e32 v25, 0xffff0000, v4
	v_lshlrev_b32_e32 v24, 16, v4
	v_and_b32_e32 v4, 0xffff0000, v5
	v_lshlrev_b32_e32 v5, 16, v5
	v_mul_f32_e32 v26, v25, v25
	v_pk_mul_f32 v[18:19], v[4:5], v[4:5]
	v_fmac_f32_e32 v26, v24, v24
	v_and_b32_e32 v16, 0xffff0000, v6
	v_lshlrev_b32_e32 v17, 16, v6
	v_add_f32_e32 v19, v19, v26
	v_pk_mul_f32 v[20:21], v[16:17], v[16:17]
	v_add_f32_e32 v18, v18, v19
	v_and_b32_e32 v6, 0xffff0000, v7
	v_lshlrev_b32_e32 v7, 16, v7
	v_add_f32_e32 v18, v21, v18
	v_pk_mul_f32 v[22:23], v[6:7], v[6:7]
	v_add_f32_e32 v18, v20, v18
	v_add_f32_e32 v18, v23, v18
	v_add_f32_e32 v18, v22, v18
	v_mov_b32_e32 v19, v18
	s_mul_i32 s4, s44, 0x4c00
	s_mul_hi_i32 s5, s44, 0x4c00
	v_mov_b32_dpp v19, v19 quad_perm:[1,0,3,2] row_mask:0xf bank_mask:0xf
	v_add_f32_e32 v18, v18, v19
	v_mov_b32_e32 v19, v18
	s_add_u32 s4, s8, s4
	s_addc_u32 s5, s9, s5
	v_mov_b32_dpp v19, v19 quad_perm:[2,3,0,1] row_mask:0xf bank_mask:0xf
	v_add_f32_e32 v18, v18, v19
	v_mov_b32_e32 v19, v18
	s_cmpk_gt_i32 s44, 0x1fff
	s_nop 0
	v_mov_b32_dpp v19, v19 row_half_mirror row_mask:0xf bank_mask:0xf
	v_add_f32_e32 v18, v18, v19
	v_mov_b32_e32 v19, v18
	s_nop 1
	v_mov_b32_dpp v19, v19 row_mirror row_mask:0xf bank_mask:0xf
	v_add_f32_e32 v18, v18, v19
	v_fmamk_f32 v18, v18, 0x3c000000, v59
	v_mul_f32_e32 v19, 0x4b800000, v18
	v_cmp_gt_f32_e32 vcc, s43, v18
	s_nop 1
	v_cndmask_b32_e32 v18, v18, v19, vcc
	v_rsq_f32_e32 v18, v18
	s_nop 0
	v_mul_f32_e32 v19, 0x45800000, v18
	v_cndmask_b32_e32 v18, v18, v19, vcc
	v_mul_f32_e32 v5, v18, v5
	v_mul_f32_e32 v7, v18, v7
	v_mul_f32_e32 v19, v18, v24
	v_mul_f32_e32 v20, v18, v25
	v_mul_f32_e32 v4, v18, v4
	v_mul_f32_e32 v17, v18, v17
	v_mul_f32_e32 v16, v18, v16
	v_mul_f32_e32 v6, v18, v6
	s_waitcnt vmcnt(1)
	v_mul_f32_e32 v5, v10, v5
	s_waitcnt vmcnt(0)
	v_mul_f32_e32 v7, v14, v7
	v_mul_f32_e32 v8, v8, v19
	v_mul_f32_e32 v9, v9, v20
	v_mul_f32_e32 v10, v11, v4
	v_mul_f32_e32 v11, v12, v17
	v_mul_f32_e32 v12, v13, v16
	v_mul_f32_e32 v13, v15, v6
	v_cvt_pk_bf16_f32 v4, v8, v9
	v_cvt_pk_bf16_f32 v5, v5, v10
	v_cvt_pk_bf16_f32 v6, v11, v12
	v_cvt_pk_bf16_f32 v7, v7, v13
	global_store_dwordx4 v58, v[4:7], s[4:5] offset:3072 sc1
	global_load_dwordx4 v[6:9], v[36:37], off
	s_nop 0
	global_load_dwordx4 v[10:13], v[36:37], off offset:16
	v_lshlrev_b32_e32 v14, 16, v0
	v_and_b32_e32 v15, 0xffff0000, v0
	v_lshlrev_b32_e32 v0, 16, v1
	v_and_b32_e32 v1, 0xffff0000, v1
	v_pk_mul_f32 v[18:19], v[14:15], v[14:15]
	v_pk_mul_f32 v[20:21], v[0:1], v[0:1]
	v_add_f32_e32 v18, v18, v19
	v_lshlrev_b32_e32 v16, 16, v2
	v_and_b32_e32 v17, 0xffff0000, v2
	v_add_f32_e32 v18, v20, v18
	v_pk_mul_f32 v[22:23], v[16:17], v[16:17]
	v_add_f32_e32 v18, v21, v18
	v_and_b32_e32 v4, 0xffff0000, v3
	v_lshlrev_b32_e32 v5, 16, v3
	v_add_f32_e32 v18, v22, v18
	v_pk_mul_f32 v[2:3], v[4:5], v[4:5]
	v_add_f32_e32 v18, v23, v18
	v_add_f32_e32 v3, v3, v18
	v_add_f32_e32 v2, v2, v3
	v_mov_b32_e32 v3, v2
	s_nop 1
	v_mov_b32_dpp v3, v3 quad_perm:[1,0,3,2] row_mask:0xf bank_mask:0xf
	v_add_f32_e32 v2, v2, v3
	v_mov_b32_e32 v3, v2
	s_nop 1
	v_mov_b32_dpp v3, v3 quad_perm:[2,3,0,1] row_mask:0xf bank_mask:0xf
	v_add_f32_e32 v2, v2, v3
	v_mov_b32_e32 v3, v2
	s_nop 1
	v_mov_b32_dpp v3, v3 row_half_mirror row_mask:0xf bank_mask:0xf
	v_add_f32_e32 v2, v2, v3
	v_fmamk_f32 v2, v2, 0x3c800000, v59
	v_mul_f32_e32 v3, 0x4b800000, v2
	v_cmp_gt_f32_e32 vcc, s43, v2
	s_nop 1
	v_cndmask_b32_e32 v2, v2, v3, vcc
	v_rsq_f32_e32 v2, v2
	s_nop 0
	v_mul_f32_e32 v3, 0x45800000, v2
	v_cndmask_b32_e32 v2, v2, v3, vcc
	v_pk_mul_f32 v[14:15], v[2:3], v[14:15] op_sel_hi:[0,1]
	v_pk_mul_f32 v[0:1], v[2:3], v[0:1] op_sel_hi:[0,1]
	v_pk_mul_f32 v[16:17], v[2:3], v[16:17] op_sel_hi:[0,1]
	v_pk_mul_f32 v[18:19], v[2:3], v[4:5] op_sel_hi:[0,1]
	s_waitcnt vmcnt(1)
	v_pk_mul_f32 v[6:7], v[6:7], v[14:15]
	v_pk_mul_f32 v[4:5], v[8:9], v[0:1]
	s_waitcnt vmcnt(0)
	v_pk_mul_f32 v[2:3], v[10:11], v[16:17]
	v_pk_mul_f32 v[0:1], v[12:13], v[18:19] op_sel:[0,1] op_sel_hi:[1,0]
	s_cbranch_scc1 .LBB0_406
	s_add_i32 s10, s38, s25
	s_and_b32 s10, s10, 0x1ffe0
	s_lshl_b32 s10, s10, 3
	v_lshl_add_u64 v[24:25], v[38:39], 0, s[10:11]
	global_load_dwordx4 v[8:11], v[24:25], off
	global_load_dwordx4 v[12:15], v[24:25], off offset:16
	global_load_dwordx4 v[16:19], v[24:25], off offset:32
	global_load_dwordx4 v[20:23], v[24:25], off offset:48
	v_mov_b32_e32 v24, v6
	v_mov_b32_e32 v25, v7
	v_mov_b32_e32 v26, v4
	v_mov_b32_e32 v27, v5
	v_mov_b32_e32 v28, v2
	v_mov_b32_e32 v29, v3
	v_mov_b32_e32 v30, v0
	v_mov_b32_e32 v31, v1
	v_mov_b32_dpp v24, v24 row_shl:4 row_mask:0xf bank_mask:0x5
	v_mov_b32_dpp v25, v25 row_shl:4 row_mask:0xf bank_mask:0x5
	v_mov_b32_dpp v26, v26 row_shl:4 row_mask:0xf bank_mask:0x5
	v_mov_b32_dpp v27, v27 row_shl:4 row_mask:0xf bank_mask:0x5
	v_mov_b32_dpp v28, v28 row_shl:4 row_mask:0xf bank_mask:0x5
	v_mov_b32_dpp v29, v29 row_shl:4 row_mask:0xf bank_mask:0x5
	v_mov_b32_dpp v30, v30 row_shl:4 row_mask:0xf bank_mask:0x5
	v_mov_b32_dpp v31, v31 row_shl:4 row_mask:0xf bank_mask:0x5
	v_mov_b32_dpp v24, v6 row_shr:4 row_mask:0xf bank_mask:0xa
	v_mov_b32_dpp v25, v7 row_shr:4 row_mask:0xf bank_mask:0xa
	v_mov_b32_dpp v26, v4 row_shr:4 row_mask:0xf bank_mask:0xa
	v_mov_b32_dpp v27, v5 row_shr:4 row_mask:0xf bank_mask:0xa
	v_mov_b32_dpp v28, v2 row_shr:4 row_mask:0xf bank_mask:0xa
	v_mov_b32_dpp v29, v3 row_shr:4 row_mask:0xf bank_mask:0xa
	v_mov_b32_dpp v30, v0 row_shr:4 row_mask:0xf bank_mask:0xa
	v_mov_b32_dpp v31, v1 row_shr:4 row_mask:0xf bank_mask:0xa
	s_waitcnt vmcnt(3)
	v_mov_b32_e32 v49, v10
	v_mov_b32_e32 v10, v9
	s_waitcnt vmcnt(2)
	v_mov_b32_e32 v9, v14
	v_mov_b32_e32 v14, v13
	s_waitcnt vmcnt(1)
	v_mov_b32_e32 v13, v18
	v_mov_b32_e32 v18, v17
	s_waitcnt vmcnt(0)
	v_mov_b32_e32 v17, v22
	v_mov_b32_e32 v22, v21
	v_mov_b32_e32 v48, v8
	v_mov_b32_e32 v8, v12
	v_mov_b32_e32 v12, v16
	v_mov_b32_e32 v16, v20
	v_pk_mul_f32 v[10:11], v[10:11], v[24:25]
	v_pk_mul_f32 v[14:15], v[14:15], v[26:27]
	v_pk_mul_f32 v[18:19], v[18:19], v[28:29]
	v_pk_mul_f32 v[20:21], v[22:23], v[30:31]
	v_cndmask_b32_e64 v11, v11, -v11, s[0:1]
	v_cndmask_b32_e64 v10, v10, -v10, s[0:1]
	v_cndmask_b32_e64 v15, v15, -v15, s[0:1]
	v_cndmask_b32_e64 v14, v14, -v14, s[0:1]
	v_cndmask_b32_e64 v19, v19, -v19, s[0:1]
	v_cndmask_b32_e64 v18, v18, -v18, s[0:1]
	v_cndmask_b32_e64 v21, v21, -v21, s[0:1]
	v_cndmask_b32_e64 v20, v20, -v20, s[0:1]
	v_pk_fma_f32 v[6:7], v[6:7], v[48:49], v[10:11]
	v_pk_fma_f32 v[4:5], v[4:5], v[8:9], v[14:15]
	v_pk_fma_f32 v[2:3], v[2:3], v[12:13], v[18:19]
	v_pk_fma_f32 v[0:1], v[0:1], v[16:17], v[20:21]
.LBB0_406:
	s_and_saveexec_b64 s[12:13], s[2:3]
	s_cbranch_execz .LBB0_379
	v_cvt_pk_bf16_f32 v6, v6, v7
	v_cvt_pk_bf16_f32 v7, v4, v5
	v_cvt_pk_bf16_f32 v8, v2, v3
	v_cvt_pk_bf16_f32 v9, v0, v1
	v_lshl_add_u64 v[0:1], s[4:5], 0, v[32:33]
	v_add_co_u32_e32 v0, vcc, 0x1000, v0
	s_nop 1
	v_addc_co_u32_e32 v1, vcc, 0, v1, vcc
	global_store_dwordx4 v[0:1], v[6:9], off offset:2048 sc1
	s_branch .LBB0_379

.LBB0_492:
	s_and_b32 s2, s11, 0xffffffc0
	v_or_b32_e32 v0, s2, v108
	v_ashrrev_i32_e32 v1, 31, v0
	v_lshlrev_b64 v[0:1], 12, v[0:1]
	s_and_b32 s2, s13, 0x700
	v_lshl_add_u64 v[0:1], s[4:5], 0, v[0:1]
	s_lshl_b32 s2, s2, 1
	v_lshl_add_u64 v[70:71], v[0:1], 0, s[2:3]
	global_load_dwordx4 v[50:53], v[70:71], off offset:256
	global_load_dwordx4 v[54:57], v[70:71], off offset:272
	global_load_dwordx4 v[58:61], v[70:71], off offset:304
	global_load_dwordx4 v[62:65], v[70:71], off offset:288
	global_load_dwordx4 v[32:35], v[70:71], off offset:368
	global_load_dwordx4 v[36:39], v[70:71], off offset:352
	global_load_dwordx4 v[40:43], v[70:71], off offset:336
	global_load_dwordx4 v[66:69], v[70:71], off offset:320
	global_load_dwordx4 v[16:19], v[70:71], off offset:432
	global_load_dwordx4 v[20:23], v[70:71], off offset:416
	global_load_dwordx4 v[24:27], v[70:71], off offset:400
	global_load_dwordx4 v[28:31], v[70:71], off offset:384
	global_load_dwordx4 v[0:3], v[70:71], off offset:496
	global_load_dwordx4 v[4:7], v[70:71], off offset:480
	global_load_dwordx4 v[8:11], v[70:71], off offset:464
	global_load_dwordx4 v[12:15], v[70:71], off offset:448
	v_mov_b32_e32 v49, 0
	v_mov_b32_e32 v72, 0
	v_mov_b32_e32 v73, 0
	v_mov_b32_e32 v74, 0
	s_and_b64 vcc, exec, s[0:1]
	s_waitcnt vmcnt(15)
	v_lshlrev_b32_e32 v70, 16, v50
	v_and_b32_e32 v50, 0xffff0000, v50
	v_lshlrev_b32_e32 v75, 16, v52
	v_and_b32_e32 v52, 0xffff0000, v52
	s_waitcnt vmcnt(14)
	v_lshlrev_b32_e32 v77, 16, v54
	v_and_b32_e32 v54, 0xffff0000, v54
	v_lshlrev_b32_e32 v79, 16, v56
	v_and_b32_e32 v56, 0xffff0000, v56
	v_max_f32_e32 v70, v70, v70
	v_max_f32_e32 v50, v50, v50
	v_max_f32_e32 v75, v75, v75
	v_max_f32_e32 v52, v52, v52
	v_max_f32_e32 v77, v77, v77
	v_max_f32_e32 v54, v54, v54
	v_max_f32_e32 v79, v79, v79
	v_max_f32_e32 v56, v56, v56
	v_med3_f32 v70, v70, s7, v45
	v_med3_f32 v50, v50, s7, v45
	v_med3_f32 v75, v75, s7, v45
	v_med3_f32 v52, v52, s7, v45
	v_med3_f32 v77, v77, s7, v45
	v_med3_f32 v54, v54, s7, v45
	v_med3_f32 v79, v79, s7, v45
	v_med3_f32 v56, v56, s7, v45
	v_cvt_pk_fp8_f32 v49, v70, v50
	v_lshlrev_b32_e32 v71, 16, v51
	v_and_b32_e32 v51, 0xffff0000, v51
	v_cvt_pk_fp8_f32 v72, v75, v52
	v_cvt_pk_fp8_f32 v73, v77, v54
	v_cvt_pk_fp8_f32 v74, v79, v56
	v_lshlrev_b32_e32 v76, 16, v53
	v_and_b32_e32 v53, 0xffff0000, v53
	v_lshlrev_b32_e32 v78, 16, v55
	v_and_b32_e32 v55, 0xffff0000, v55
	v_lshlrev_b32_e32 v80, 16, v57
	v_and_b32_e32 v57, 0xffff0000, v57
	v_max_f32_e32 v71, v71, v71
	v_max_f32_e32 v51, v51, v51
	v_max_f32_e32 v76, v76, v76
	v_max_f32_e32 v53, v53, v53
	v_max_f32_e32 v78, v78, v78
	v_max_f32_e32 v55, v55, v55
	v_max_f32_e32 v80, v80, v80
	v_max_f32_e32 v57, v57, v57
	v_med3_f32 v71, v71, s7, v45
	v_med3_f32 v51, v51, s7, v45
	v_med3_f32 v76, v76, s7, v45
	v_med3_f32 v53, v53, s7, v45
	v_med3_f32 v78, v78, s7, v45
	v_med3_f32 v55, v55, s7, v45
	v_med3_f32 v80, v80, s7, v45
	v_med3_f32 v57, v57, s7, v45
	v_cvt_pk_fp8_f32 v49, v71, v51 op_sel:[0,0,1]
	v_cvt_pk_fp8_f32 v72, v76, v53 op_sel:[0,0,1]
	v_cvt_pk_fp8_f32 v73, v78, v55 op_sel:[0,0,1]
	v_cvt_pk_fp8_f32 v74, v80, v57 op_sel:[0,0,1]
	ds_write_b8 v48, v49
	ds_write_b8 v48, v72 offset:256
	v_lshrrev_b32_e32 v50, 8, v49
	ds_write_b8_d16_hi v48, v49 offset:128
	ds_write_b8_d16_hi v48, v72 offset:384
	v_lshrrev_b32_e32 v49, 24, v49
	v_lshrrev_b32_e32 v51, 8, v72
	v_lshrrev_b32_e32 v52, 24, v72
	ds_write_b8 v48, v73 offset:512
	ds_write_b8 v48, v74 offset:768
	v_lshrrev_b32_e32 v53, 8, v73
	ds_write_b8 v48, v50 offset:64
	ds_write_b8 v48, v51 offset:320
	ds_write_b8 v48, v49 offset:192
	ds_write_b8 v48, v52 offset:448
	ds_write_b8 v48, v53 offset:576
	v_lshrrev_b32_e32 v49, 8, v74
	ds_write_b8 v48, v49 offset:832
	ds_write_b8_d16_hi v48, v73 offset:640
	ds_write_b8_d16_hi v48, v74 offset:896
	v_lshrrev_b32_e32 v49, 24, v73
	ds_write_b8 v48, v49 offset:704
	s_waitcnt vmcnt(12)
	v_lshlrev_b32_e32 v49, 16, v62
	v_and_b32_e32 v50, 0xffff0000, v62
	v_max_f32_e32 v49, v49, v49
	v_max_f32_e32 v50, v50, v50
	v_med3_f32 v49, v49, s7, v45
	v_med3_f32 v50, v50, s7, v45
	v_mov_b32_e32 v57, 0
	v_cvt_pk_fp8_f32 v57, v49, v50
	v_lshlrev_b32_e32 v51, 16, v63
	v_and_b32_e32 v52, 0xffff0000, v63
	v_max_f32_e32 v51, v51, v51
	v_max_f32_e32 v50, v52, v52
	v_lshlrev_b32_e32 v53, 16, v64
	v_and_b32_e32 v54, 0xffff0000, v64
	v_med3_f32 v49, v51, s7, v45
	v_med3_f32 v50, v50, s7, v45
	v_cvt_pk_fp8_f32 v57, v49, v50 op_sel:[0,0,1]
	v_max_f32_e32 v49, v53, v53
	v_max_f32_e32 v50, v54, v54
	v_med3_f32 v49, v49, s7, v45
	v_med3_f32 v50, v50, s7, v45
	v_mov_b32_e32 v52, 0
	v_cvt_pk_fp8_f32 v52, v49, v50
	v_lshlrev_b32_e32 v55, 16, v65
	v_and_b32_e32 v56, 0xffff0000, v65
	v_max_f32_e32 v51, v55, v55
	v_max_f32_e32 v50, v56, v56
	v_med3_f32 v49, v51, s7, v45
	v_med3_f32 v50, v50, s7, v45
	v_cvt_pk_fp8_f32 v52, v49, v50 op_sel:[0,0,1]
	v_lshrrev_b32_e32 v49, 24, v74
	ds_write_b8 v48, v49 offset:960
	ds_write_b8 v48, v57 offset:1024
	ds_write_b8 v48, v52 offset:1280
	v_lshrrev_b32_e32 v49, 8, v57
	ds_write_b8 v48, v49 offset:1088
	v_lshrrev_b32_e32 v49, 8, v52
	ds_write_b8 v48, v49 offset:1344
	ds_write_b8_d16_hi v48, v57 offset:1152
	ds_write_b8_d16_hi v48, v52 offset:1408
	v_lshrrev_b32_e32 v49, 24, v57
	ds_write_b8 v48, v49 offset:1216
	v_lshlrev_b32_e32 v49, 16, v58
	v_and_b32_e32 v50, 0xffff0000, v58
	v_max_f32_e32 v49, v49, v49
	v_max_f32_e32 v50, v50, v50
	v_med3_f32 v49, v49, s7, v45
	v_med3_f32 v50, v50, s7, v45
	v_mov_b32_e32 v58, 0
	v_cvt_pk_fp8_f32 v58, v49, v50
	v_lshlrev_b32_e32 v51, 16, v59
	v_and_b32_e32 v53, 0xffff0000, v59
	v_max_f32_e32 v51, v51, v51
	v_max_f32_e32 v50, v53, v53
	v_lshlrev_b32_e32 v54, 16, v60
	v_and_b32_e32 v55, 0xffff0000, v60
	v_med3_f32 v49, v51, s7, v45
	v_med3_f32 v50, v50, s7, v45
	v_cvt_pk_fp8_f32 v58, v49, v50 op_sel:[0,0,1]
	v_max_f32_e32 v49, v54, v54
	v_max_f32_e32 v50, v55, v55
	v_med3_f32 v49, v49, s7, v45
	v_med3_f32 v50, v50, s7, v45
	v_mov_b32_e32 v53, 0
	v_cvt_pk_fp8_f32 v53, v49, v50
	v_lshlrev_b32_e32 v56, 16, v61
	v_and_b32_e32 v57, 0xffff0000, v61
	v_max_f32_e32 v51, v56, v56
	v_max_f32_e32 v50, v57, v57
	v_med3_f32 v49, v51, s7, v45
	v_med3_f32 v50, v50, s7, v45
	v_cvt_pk_fp8_f32 v53, v49, v50 op_sel:[0,0,1]
	v_lshrrev_b32_e32 v49, 24, v52
	ds_write_b8 v48, v49 offset:1472
	ds_write_b8 v48, v58 offset:1536
	ds_write_b8 v48, v53 offset:1792
	v_lshrrev_b32_e32 v49, 8, v58
	ds_write_b8 v48, v49 offset:1600
	v_lshrrev_b32_e32 v49, 8, v53
	ds_write_b8 v48, v49 offset:1856
	ds_write_b8_d16_hi v48, v58 offset:1664
	ds_write_b8_d16_hi v48, v53 offset:1920
	v_lshrrev_b32_e32 v49, 24, v58
	ds_write_b8 v48, v49 offset:1728
	s_waitcnt vmcnt(8)
	v_lshlrev_b32_e32 v49, 16, v66
	v_and_b32_e32 v50, 0xffff0000, v66
	v_max_f32_e32 v49, v49, v49
	v_max_f32_e32 v50, v50, v50
	v_med3_f32 v49, v49, s7, v45
	v_med3_f32 v50, v50, s7, v45
	v_mov_b32_e32 v58, 0
	v_cvt_pk_fp8_f32 v58, v49, v50
	v_lshlrev_b32_e32 v51, 16, v67
	v_and_b32_e32 v52, 0xffff0000, v67
	v_max_f32_e32 v51, v51, v51
	v_max_f32_e32 v50, v52, v52
	v_lshlrev_b32_e32 v54, 16, v68
	v_and_b32_e32 v55, 0xffff0000, v68
	v_med3_f32 v49, v51, s7, v45
	v_med3_f32 v50, v50, s7, v45
	v_cvt_pk_fp8_f32 v58, v49, v50 op_sel:[0,0,1]
	v_max_f32_e32 v49, v54, v54
	v_max_f32_e32 v50, v55, v55
	v_med3_f32 v49, v49, s7, v45
	v_med3_f32 v50, v50, s7, v45
	v_mov_b32_e32 v52, 0
	v_cvt_pk_fp8_f32 v52, v49, v50
	v_lshlrev_b32_e32 v56, 16, v69
	v_and_b32_e32 v57, 0xffff0000, v69
	v_max_f32_e32 v51, v56, v56
	v_max_f32_e32 v50, v57, v57
	v_med3_f32 v49, v51, s7, v45
	v_med3_f32 v50, v50, s7, v45
	v_cvt_pk_fp8_f32 v52, v49, v50 op_sel:[0,0,1]
	v_lshrrev_b32_e32 v49, 24, v53
	ds_write_b8 v48, v49 offset:1984
	ds_write_b8 v48, v58 offset:2048
	ds_write_b8 v48, v52 offset:2304
	v_lshrrev_b32_e32 v49, 8, v58
	ds_write_b8 v48, v49 offset:2112
	v_lshrrev_b32_e32 v49, 8, v52
	ds_write_b8 v48, v49 offset:2368
	ds_write_b8_d16_hi v48, v58 offset:2176
	ds_write_b8_d16_hi v48, v52 offset:2432
	v_lshrrev_b32_e32 v49, 24, v58
	ds_write_b8 v48, v49 offset:2240
	v_lshlrev_b32_e32 v49, 16, v40
	v_and_b32_e32 v40, 0xffff0000, v40
	v_max_f32_e32 v49, v49, v49
	v_max_f32_e32 v40, v40, v40
	v_med3_f32 v49, v49, s7, v45
	v_med3_f32 v40, v40, s7, v45
	v_mov_b32_e32 v54, 0
	v_cvt_pk_fp8_f32 v54, v49, v40
	v_lshlrev_b32_e32 v50, 16, v41
	v_and_b32_e32 v41, 0xffff0000, v41
	v_max_f32_e32 v50, v50, v50
	v_max_f32_e32 v41, v41, v41
	v_lshlrev_b32_e32 v51, 16, v42
	v_and_b32_e32 v42, 0xffff0000, v42
	v_med3_f32 v40, v50, s7, v45
	v_med3_f32 v41, v41, s7, v45
	v_cvt_pk_fp8_f32 v54, v40, v41 op_sel:[0,0,1]
	v_max_f32_e32 v40, v51, v51
	v_max_f32_e32 v41, v42, v42
	v_med3_f32 v40, v40, s7, v45
	v_med3_f32 v41, v41, s7, v45
	v_mov_b32_e32 v49, 0
	v_cvt_pk_fp8_f32 v49, v40, v41
	v_lshlrev_b32_e32 v53, 16, v43
	v_and_b32_e32 v43, 0xffff0000, v43
	v_max_f32_e32 v42, v53, v53
	v_max_f32_e32 v41, v43, v43
	v_med3_f32 v40, v42, s7, v45
	v_med3_f32 v41, v41, s7, v45
	v_cvt_pk_fp8_f32 v49, v40, v41 op_sel:[0,0,1]
	v_lshrrev_b32_e32 v40, 24, v52
	ds_write_b8 v48, v40 offset:2496
	ds_write_b8 v48, v54 offset:2560
	ds_write_b8 v48, v49 offset:2816
	v_lshrrev_b32_e32 v40, 8, v54
	ds_write_b8 v48, v40 offset:2624
	v_lshrrev_b32_e32 v40, 8, v49
	ds_write_b8 v48, v40 offset:2880
	ds_write_b8_d16_hi v48, v54 offset:2688
	ds_write_b8_d16_hi v48, v49 offset:2944
	v_lshrrev_b32_e32 v40, 24, v54
	ds_write_b8 v48, v40 offset:2752
	v_lshlrev_b32_e32 v40, 16, v36
	v_and_b32_e32 v36, 0xffff0000, v36
	v_max_f32_e32 v40, v40, v40
	v_max_f32_e32 v36, v36, v36
	v_med3_f32 v40, v40, s7, v45
	v_med3_f32 v36, v36, s7, v45
	v_mov_b32_e32 v50, 0
	v_cvt_pk_fp8_f32 v50, v40, v36
	v_lshlrev_b32_e32 v41, 16, v37
	v_and_b32_e32 v37, 0xffff0000, v37
	v_max_f32_e32 v41, v41, v41
	v_max_f32_e32 v37, v37, v37
	v_lshlrev_b32_e32 v42, 16, v38
	v_and_b32_e32 v38, 0xffff0000, v38
	v_med3_f32 v36, v41, s7, v45
	v_med3_f32 v37, v37, s7, v45
	v_cvt_pk_fp8_f32 v50, v36, v37 op_sel:[0,0,1]
	v_max_f32_e32 v36, v42, v42
	v_max_f32_e32 v37, v38, v38
	v_med3_f32 v36, v36, s7, v45
	v_med3_f32 v37, v37, s7, v45
	v_mov_b32_e32 v40, 0
	v_cvt_pk_fp8_f32 v40, v36, v37
	v_lshlrev_b32_e32 v43, 16, v39
	v_and_b32_e32 v39, 0xffff0000, v39
	v_max_f32_e32 v38, v43, v43
	v_max_f32_e32 v37, v39, v39
	v_med3_f32 v36, v38, s7, v45
	v_med3_f32 v37, v37, s7, v45
	v_cvt_pk_fp8_f32 v40, v36, v37 op_sel:[0,0,1]
	v_lshrrev_b32_e32 v36, 24, v49
	ds_write_b8 v48, v36 offset:3008
	ds_write_b8 v48, v50 offset:3072
	ds_write_b8 v48, v40 offset:3328
	v_lshrrev_b32_e32 v36, 8, v50
	ds_write_b8 v48, v36 offset:3136
	v_lshrrev_b32_e32 v36, 8, v40
	ds_write_b8 v48, v36 offset:3392
	ds_write_b8_d16_hi v48, v50 offset:3200
	ds_write_b8_d16_hi v48, v40 offset:3456
	v_lshrrev_b32_e32 v36, 24, v50
	ds_write_b8 v48, v36 offset:3264
	v_lshlrev_b32_e32 v36, 16, v32
	v_and_b32_e32 v32, 0xffff0000, v32
	v_max_f32_e32 v36, v36, v36
	v_max_f32_e32 v32, v32, v32
	v_med3_f32 v36, v36, s7, v45
	v_med3_f32 v32, v32, s7, v45
	v_mov_b32_e32 v41, 0
	v_cvt_pk_fp8_f32 v41, v36, v32
	v_lshlrev_b32_e32 v37, 16, v33
	v_and_b32_e32 v33, 0xffff0000, v33
	v_max_f32_e32 v37, v37, v37
	v_max_f32_e32 v33, v33, v33
	v_lshlrev_b32_e32 v38, 16, v34
	v_and_b32_e32 v34, 0xffff0000, v34
	v_med3_f32 v32, v37, s7, v45
	v_med3_f32 v33, v33, s7, v45
	v_cvt_pk_fp8_f32 v41, v32, v33 op_sel:[0,0,1]
	v_max_f32_e32 v32, v38, v38
	v_max_f32_e32 v33, v34, v34
	v_med3_f32 v32, v32, s7, v45
	v_med3_f32 v33, v33, s7, v45
	v_mov_b32_e32 v36, 0
	v_cvt_pk_fp8_f32 v36, v32, v33
	v_lshlrev_b32_e32 v39, 16, v35
	v_and_b32_e32 v35, 0xffff0000, v35
	v_max_f32_e32 v34, v39, v39
	v_max_f32_e32 v33, v35, v35
	v_med3_f32 v32, v34, s7, v45
	v_med3_f32 v33, v33, s7, v45
	v_cvt_pk_fp8_f32 v36, v32, v33 op_sel:[0,0,1]
	v_lshrrev_b32_e32 v32, 24, v40
	ds_write_b8 v48, v32 offset:3520
	ds_write_b8 v48, v41 offset:3584
	ds_write_b8 v48, v36 offset:3840
	v_lshrrev_b32_e32 v32, 8, v41
	ds_write_b8 v48, v32 offset:3648
	v_lshrrev_b32_e32 v32, 8, v36
	ds_write_b8 v48, v32 offset:3904
	ds_write_b8_d16_hi v48, v41 offset:3712
	ds_write_b8_d16_hi v48, v36 offset:3968
	v_lshrrev_b32_e32 v32, 24, v41
	ds_write_b8 v48, v32 offset:3776
	s_waitcnt vmcnt(4)
	v_lshlrev_b32_e32 v32, 16, v28
	v_and_b32_e32 v28, 0xffff0000, v28
	v_max_f32_e32 v32, v32, v32
	v_max_f32_e32 v28, v28, v28
	v_med3_f32 v32, v32, s7, v45
	v_med3_f32 v28, v28, s7, v45
	v_mov_b32_e32 v37, 0
	v_cvt_pk_fp8_f32 v37, v32, v28
	v_lshlrev_b32_e32 v33, 16, v29
	v_and_b32_e32 v29, 0xffff0000, v29
	v_max_f32_e32 v33, v33, v33
	v_max_f32_e32 v29, v29, v29
	v_lshlrev_b32_e32 v34, 16, v30
	v_and_b32_e32 v30, 0xffff0000, v30
	v_med3_f32 v28, v33, s7, v45
	v_med3_f32 v29, v29, s7, v45
	v_cvt_pk_fp8_f32 v37, v28, v29 op_sel:[0,0,1]
	v_max_f32_e32 v28, v34, v34
	v_max_f32_e32 v29, v30, v30
	v_med3_f32 v28, v28, s7, v45
	v_med3_f32 v29, v29, s7, v45
	v_mov_b32_e32 v32, 0
	v_cvt_pk_fp8_f32 v32, v28, v29
	v_lshlrev_b32_e32 v35, 16, v31
	v_and_b32_e32 v31, 0xffff0000, v31
	v_max_f32_e32 v30, v35, v35
	v_max_f32_e32 v29, v31, v31
	v_med3_f32 v28, v30, s7, v45
	v_med3_f32 v29, v29, s7, v45
	v_cvt_pk_fp8_f32 v32, v28, v29 op_sel:[0,0,1]
	v_lshrrev_b32_e32 v28, 24, v36
	ds_write_b8 v48, v28 offset:4032
	ds_write_b8 v48, v37 offset:4096
	ds_write_b8 v48, v32 offset:4352
	v_lshrrev_b32_e32 v28, 8, v37
	ds_write_b8 v48, v28 offset:4160
	v_lshrrev_b32_e32 v28, 8, v32
	ds_write_b8 v48, v28 offset:4416
	ds_write_b8_d16_hi v48, v37 offset:4224
	ds_write_b8_d16_hi v48, v32 offset:4480
	v_lshrrev_b32_e32 v28, 24, v37
	ds_write_b8 v48, v28 offset:4288
	v_lshlrev_b32_e32 v28, 16, v24
	v_and_b32_e32 v24, 0xffff0000, v24
	v_max_f32_e32 v28, v28, v28
	v_max_f32_e32 v24, v24, v24
	v_med3_f32 v28, v28, s7, v45
	v_med3_f32 v24, v24, s7, v45
	v_mov_b32_e32 v33, 0
	v_cvt_pk_fp8_f32 v33, v28, v24
	v_lshlrev_b32_e32 v29, 16, v25
	v_and_b32_e32 v25, 0xffff0000, v25
	v_max_f32_e32 v29, v29, v29
	v_max_f32_e32 v25, v25, v25
	v_lshlrev_b32_e32 v30, 16, v26
	v_and_b32_e32 v26, 0xffff0000, v26
	v_med3_f32 v24, v29, s7, v45
	v_med3_f32 v25, v25, s7, v45
	v_cvt_pk_fp8_f32 v33, v24, v25 op_sel:[0,0,1]
	v_max_f32_e32 v24, v30, v30
	v_max_f32_e32 v25, v26, v26
	v_med3_f32 v24, v24, s7, v45
	v_med3_f32 v25, v25, s7, v45
	v_mov_b32_e32 v28, 0
	v_cvt_pk_fp8_f32 v28, v24, v25
	v_lshlrev_b32_e32 v31, 16, v27
	v_and_b32_e32 v27, 0xffff0000, v27
	v_max_f32_e32 v26, v31, v31
	v_max_f32_e32 v25, v27, v27
	v_med3_f32 v24, v26, s7, v45
	v_med3_f32 v25, v25, s7, v45
	v_cvt_pk_fp8_f32 v28, v24, v25 op_sel:[0,0,1]
	v_lshrrev_b32_e32 v24, 24, v32
	ds_write_b8 v48, v24 offset:4544
	ds_write_b8 v48, v33 offset:4608
	ds_write_b8 v48, v28 offset:4864
	v_lshrrev_b32_e32 v24, 8, v33
	ds_write_b8 v48, v24 offset:4672
	v_lshrrev_b32_e32 v24, 8, v28
	ds_write_b8 v48, v24 offset:4928
	ds_write_b8_d16_hi v48, v33 offset:4736
	ds_write_b8_d16_hi v48, v28 offset:4992
	v_lshrrev_b32_e32 v24, 24, v33
	ds_write_b8 v48, v24 offset:4800
	v_lshlrev_b32_e32 v24, 16, v20
	v_and_b32_e32 v20, 0xffff0000, v20
	v_max_f32_e32 v24, v24, v24
	v_max_f32_e32 v20, v20, v20
	v_med3_f32 v24, v24, s7, v45
	v_med3_f32 v20, v20, s7, v45
	v_mov_b32_e32 v29, 0
	v_cvt_pk_fp8_f32 v29, v24, v20
	v_lshlrev_b32_e32 v25, 16, v21
	v_and_b32_e32 v21, 0xffff0000, v21
	v_max_f32_e32 v25, v25, v25
	v_max_f32_e32 v21, v21, v21
	v_lshlrev_b32_e32 v26, 16, v22
	v_and_b32_e32 v22, 0xffff0000, v22
	v_med3_f32 v20, v25, s7, v45
	v_med3_f32 v21, v21, s7, v45
	v_cvt_pk_fp8_f32 v29, v20, v21 op_sel:[0,0,1]
	v_max_f32_e32 v20, v26, v26
	v_max_f32_e32 v21, v22, v22
	v_med3_f32 v20, v20, s7, v45
	v_med3_f32 v21, v21, s7, v45
	v_mov_b32_e32 v24, 0
	v_cvt_pk_fp8_f32 v24, v20, v21
	v_lshlrev_b32_e32 v27, 16, v23
	v_and_b32_e32 v23, 0xffff0000, v23
	v_max_f32_e32 v22, v27, v27
	v_max_f32_e32 v21, v23, v23
	v_med3_f32 v20, v22, s7, v45
	v_med3_f32 v21, v21, s7, v45
	v_cvt_pk_fp8_f32 v24, v20, v21 op_sel:[0,0,1]
	v_lshrrev_b32_e32 v20, 24, v28
	ds_write_b8 v48, v20 offset:5056
	ds_write_b8 v48, v29 offset:5120
	ds_write_b8 v48, v24 offset:5376
	v_lshrrev_b32_e32 v20, 8, v29
	ds_write_b8 v48, v20 offset:5184
	v_lshrrev_b32_e32 v20, 8, v24
	ds_write_b8 v48, v20 offset:5440
	ds_write_b8_d16_hi v48, v29 offset:5248
	ds_write_b8_d16_hi v48, v24 offset:5504
	v_lshrrev_b32_e32 v20, 24, v29
	ds_write_b8 v48, v20 offset:5312
	v_lshlrev_b32_e32 v20, 16, v16
	v_and_b32_e32 v16, 0xffff0000, v16
	v_max_f32_e32 v20, v20, v20
	v_max_f32_e32 v16, v16, v16
	v_med3_f32 v20, v20, s7, v45
	v_med3_f32 v16, v16, s7, v45
	v_mov_b32_e32 v25, 0
	v_cvt_pk_fp8_f32 v25, v20, v16
	v_lshlrev_b32_e32 v21, 16, v17
	v_and_b32_e32 v17, 0xffff0000, v17
	v_max_f32_e32 v21, v21, v21
	v_max_f32_e32 v17, v17, v17
	v_lshlrev_b32_e32 v22, 16, v18
	v_and_b32_e32 v18, 0xffff0000, v18
	v_med3_f32 v16, v21, s7, v45
	v_med3_f32 v17, v17, s7, v45
	v_cvt_pk_fp8_f32 v25, v16, v17 op_sel:[0,0,1]
	v_max_f32_e32 v16, v22, v22
	v_max_f32_e32 v17, v18, v18
	v_med3_f32 v16, v16, s7, v45
	v_med3_f32 v17, v17, s7, v45
	v_mov_b32_e32 v20, 0
	v_cvt_pk_fp8_f32 v20, v16, v17
	v_lshlrev_b32_e32 v23, 16, v19
	v_and_b32_e32 v19, 0xffff0000, v19
	v_max_f32_e32 v18, v23, v23
	v_max_f32_e32 v17, v19, v19
	v_med3_f32 v16, v18, s7, v45
	v_med3_f32 v17, v17, s7, v45
	v_cvt_pk_fp8_f32 v20, v16, v17 op_sel:[0,0,1]
	v_lshrrev_b32_e32 v16, 24, v24
	ds_write_b8 v48, v16 offset:5568
	ds_write_b8 v48, v25 offset:5632
	ds_write_b8 v48, v20 offset:5888
	v_lshrrev_b32_e32 v16, 8, v25
	ds_write_b8 v48, v16 offset:5696
	v_lshrrev_b32_e32 v16, 8, v20
	ds_write_b8 v48, v16 offset:5952
	ds_write_b8_d16_hi v48, v25 offset:5760
	ds_write_b8_d16_hi v48, v20 offset:6016
	v_lshrrev_b32_e32 v16, 24, v25
	ds_write_b8 v48, v16 offset:5824
	s_waitcnt vmcnt(0)
	v_lshlrev_b32_e32 v16, 16, v12
	v_and_b32_e32 v12, 0xffff0000, v12
	v_max_f32_e32 v16, v16, v16
	v_max_f32_e32 v12, v12, v12
	v_med3_f32 v16, v16, s7, v45
	v_med3_f32 v12, v12, s7, v45
	v_mov_b32_e32 v21, 0
	v_cvt_pk_fp8_f32 v21, v16, v12
	v_lshlrev_b32_e32 v17, 16, v13
	v_and_b32_e32 v13, 0xffff0000, v13
	v_max_f32_e32 v17, v17, v17
	v_max_f32_e32 v13, v13, v13
	v_lshlrev_b32_e32 v18, 16, v14
	v_and_b32_e32 v14, 0xffff0000, v14
	v_med3_f32 v12, v17, s7, v45
	v_med3_f32 v13, v13, s7, v45
	v_cvt_pk_fp8_f32 v21, v12, v13 op_sel:[0,0,1]
	v_max_f32_e32 v12, v18, v18
	v_max_f32_e32 v13, v14, v14
	v_med3_f32 v12, v12, s7, v45
	v_med3_f32 v13, v13, s7, v45
	v_mov_b32_e32 v16, 0
	v_cvt_pk_fp8_f32 v16, v12, v13
	v_lshlrev_b32_e32 v19, 16, v15
	v_and_b32_e32 v15, 0xffff0000, v15
	v_max_f32_e32 v14, v19, v19
	v_max_f32_e32 v13, v15, v15
	v_med3_f32 v12, v14, s7, v45
	v_med3_f32 v13, v13, s7, v45
	v_cvt_pk_fp8_f32 v16, v12, v13 op_sel:[0,0,1]
	v_lshrrev_b32_e32 v12, 24, v20
	ds_write_b8 v48, v12 offset:6080
	ds_write_b8 v48, v21 offset:6144
	ds_write_b8 v48, v16 offset:6400
	v_lshrrev_b32_e32 v12, 8, v21
	ds_write_b8 v48, v12 offset:6208
	v_lshrrev_b32_e32 v12, 8, v16
	ds_write_b8 v48, v12 offset:6464
	ds_write_b8_d16_hi v48, v21 offset:6272
	ds_write_b8_d16_hi v48, v16 offset:6528
	v_lshrrev_b32_e32 v12, 24, v21
	ds_write_b8 v48, v12 offset:6336
	v_lshlrev_b32_e32 v12, 16, v8
	v_and_b32_e32 v8, 0xffff0000, v8
	v_max_f32_e32 v12, v12, v12
	v_max_f32_e32 v8, v8, v8
	v_med3_f32 v12, v12, s7, v45
	v_med3_f32 v8, v8, s7, v45
	v_mov_b32_e32 v17, 0
	v_cvt_pk_fp8_f32 v17, v12, v8
	v_lshlrev_b32_e32 v13, 16, v9
	v_and_b32_e32 v9, 0xffff0000, v9
	v_max_f32_e32 v13, v13, v13
	v_max_f32_e32 v9, v9, v9
	v_lshlrev_b32_e32 v14, 16, v10
	v_and_b32_e32 v10, 0xffff0000, v10
	v_med3_f32 v8, v13, s7, v45
	v_med3_f32 v9, v9, s7, v45
	v_cvt_pk_fp8_f32 v17, v8, v9 op_sel:[0,0,1]
	v_max_f32_e32 v8, v14, v14
	v_max_f32_e32 v9, v10, v10
	v_med3_f32 v8, v8, s7, v45
	v_med3_f32 v9, v9, s7, v45
	v_mov_b32_e32 v12, 0
	v_cvt_pk_fp8_f32 v12, v8, v9
	v_lshlrev_b32_e32 v15, 16, v11
	v_and_b32_e32 v11, 0xffff0000, v11
	v_max_f32_e32 v10, v15, v15
	v_max_f32_e32 v9, v11, v11
	v_med3_f32 v8, v10, s7, v45
	v_med3_f32 v9, v9, s7, v45
	v_cvt_pk_fp8_f32 v12, v8, v9 op_sel:[0,0,1]
	v_lshrrev_b32_e32 v8, 24, v16
	ds_write_b8 v48, v8 offset:6592
	ds_write_b8 v48, v17 offset:6656
	ds_write_b8 v48, v12 offset:6912
	v_lshrrev_b32_e32 v8, 8, v17
	ds_write_b8 v48, v8 offset:6720
	v_lshrrev_b32_e32 v8, 8, v12
	ds_write_b8 v48, v8 offset:6976
	ds_write_b8_d16_hi v48, v17 offset:6784
	ds_write_b8_d16_hi v48, v12 offset:7040
	v_lshrrev_b32_e32 v8, 24, v17
	ds_write_b8 v48, v8 offset:6848
	v_lshlrev_b32_e32 v8, 16, v4
	v_and_b32_e32 v4, 0xffff0000, v4
	v_max_f32_e32 v8, v8, v8
	v_max_f32_e32 v4, v4, v4
	v_med3_f32 v8, v8, s7, v45
	v_med3_f32 v4, v4, s7, v45
	v_mov_b32_e32 v13, 0
	v_cvt_pk_fp8_f32 v13, v8, v4
	v_lshlrev_b32_e32 v9, 16, v5
	v_and_b32_e32 v5, 0xffff0000, v5
	v_max_f32_e32 v9, v9, v9
	v_max_f32_e32 v5, v5, v5
	v_lshlrev_b32_e32 v10, 16, v6
	v_and_b32_e32 v6, 0xffff0000, v6
	v_med3_f32 v4, v9, s7, v45
	v_med3_f32 v5, v5, s7, v45
	v_cvt_pk_fp8_f32 v13, v4, v5 op_sel:[0,0,1]
	v_max_f32_e32 v4, v10, v10
	v_max_f32_e32 v5, v6, v6
	v_med3_f32 v4, v4, s7, v45
	v_med3_f32 v5, v5, s7, v45
	v_mov_b32_e32 v8, 0
	v_cvt_pk_fp8_f32 v8, v4, v5
	v_lshlrev_b32_e32 v11, 16, v7
	v_and_b32_e32 v7, 0xffff0000, v7
	v_max_f32_e32 v6, v11, v11
	v_max_f32_e32 v5, v7, v7
	v_med3_f32 v4, v6, s7, v45
	v_med3_f32 v5, v5, s7, v45
	v_cvt_pk_fp8_f32 v8, v4, v5 op_sel:[0,0,1]
	v_lshrrev_b32_e32 v4, 24, v12
	ds_write_b8 v48, v4 offset:7104
	ds_write_b8 v48, v13 offset:7168
	ds_write_b8 v48, v8 offset:7424
	v_lshrrev_b32_e32 v4, 8, v13
	ds_write_b8 v48, v4 offset:7232
	v_lshrrev_b32_e32 v4, 8, v8
	ds_write_b8 v48, v4 offset:7488
	ds_write_b8_d16_hi v48, v13 offset:7296
	ds_write_b8_d16_hi v48, v8 offset:7552
	v_lshrrev_b32_e32 v4, 24, v13
	ds_write_b8 v48, v4 offset:7360
	v_lshlrev_b32_e32 v4, 16, v0
	v_and_b32_e32 v0, 0xffff0000, v0
	v_max_f32_e32 v4, v4, v4
	v_max_f32_e32 v0, v0, v0
	v_med3_f32 v4, v4, s7, v45
	v_med3_f32 v0, v0, s7, v45
	v_mov_b32_e32 v9, 0
	v_cvt_pk_fp8_f32 v9, v4, v0
	v_lshlrev_b32_e32 v5, 16, v1
	v_and_b32_e32 v1, 0xffff0000, v1
	v_max_f32_e32 v5, v5, v5
	v_max_f32_e32 v1, v1, v1
	v_lshlrev_b32_e32 v6, 16, v2
	v_and_b32_e32 v2, 0xffff0000, v2
	v_med3_f32 v0, v5, s7, v45
	v_med3_f32 v1, v1, s7, v45
	v_cvt_pk_fp8_f32 v9, v0, v1 op_sel:[0,0,1]
	v_max_f32_e32 v0, v6, v6
	v_max_f32_e32 v1, v2, v2
	v_med3_f32 v0, v0, s7, v45
	v_med3_f32 v1, v1, s7, v45
	v_mov_b32_e32 v4, 0
	v_cvt_pk_fp8_f32 v4, v0, v1
	v_lshlrev_b32_e32 v7, 16, v3
	v_and_b32_e32 v3, 0xffff0000, v3
	v_max_f32_e32 v2, v7, v7
	v_max_f32_e32 v1, v3, v3
	v_med3_f32 v0, v2, s7, v45
	v_med3_f32 v1, v1, s7, v45
	v_cvt_pk_fp8_f32 v4, v0, v1 op_sel:[0,0,1]
	v_lshrrev_b32_e32 v0, 24, v8
	ds_write_b8 v48, v0 offset:7616
	ds_write_b8 v48, v9 offset:7680
	ds_write_b8 v48, v4 offset:7936
	v_lshrrev_b32_e32 v0, 8, v9
	ds_write_b8 v48, v0 offset:7744
	v_lshrrev_b32_e32 v0, 8, v4
	ds_write_b8 v48, v0 offset:8000
	ds_write_b8_d16_hi v48, v9 offset:7808
	ds_write_b8_d16_hi v48, v4 offset:8064
	v_lshrrev_b32_e32 v0, 24, v9
	ds_write_b8 v48, v0 offset:7872
	v_lshrrev_b32_e32 v0, 24, v4
	ds_write_b8 v48, v0 offset:8128
	s_waitcnt lgkmcnt(0)
	s_cbranch_vccnz .LBB0_491
	v_add_u32_e32 v16, s10, v44
	ds_read_b128 v[0:3], v16
	ds_read_b128 v[4:7], v16 offset:1024
	ds_read_b128 v[8:11], v16 offset:2048
	v_add_co_u32_e32 v12, vcc, 0xfffff000, v46
	s_nop 1
	v_addc_co_u32_e32 v13, vcc, -1, v47, vcc
	s_waitcnt lgkmcnt(2)
	global_store_dwordx4 v[12:13], v[0:3], off offset:-3072 sc1
	s_waitcnt lgkmcnt(1)
	global_store_dwordx4 v[12:13], v[4:7], off offset:-2048 sc1
	s_waitcnt lgkmcnt(0)
	global_store_dwordx4 v[12:13], v[8:11], off offset:-1024 sc1
	ds_read_b128 v[0:3], v16 offset:3072
	ds_read_b128 v[4:7], v16 offset:4096
	ds_read_b128 v[8:11], v16 offset:5120
	ds_read_b128 v[12:15], v16 offset:6144
	ds_read_b128 v[16:19], v16 offset:7168
	s_waitcnt lgkmcnt(4)
	global_store_dwordx4 v[46:47], v[0:3], off offset:-4096 sc1
	s_waitcnt lgkmcnt(3)
	global_store_dwordx4 v[46:47], v[4:7], off offset:-3072 sc1
	s_waitcnt lgkmcnt(2)
	global_store_dwordx4 v[46:47], v[8:11], off offset:-2048 sc1
	s_waitcnt lgkmcnt(1)
	global_store_dwordx4 v[46:47], v[12:15], off offset:-1024 sc1
	s_waitcnt lgkmcnt(0)
	global_store_dwordx4 v[46:47], v[16:19], off sc1
	s_branch .LBB0_491

.LBB0_645:
	s_waitcnt vmcnt(3)
	v_mul_f32_e32 v4, 0x42800000, v4
	s_waitcnt vmcnt(2)
	v_mul_f32_e32 v8, 0x42800000, v8
	v_med3_f32 v4, v4, s67, v98
	v_med3_f32 v8, v8, s67, v98
	v_mov_b32_e32 v67, v77
	v_cvt_pk_fp8_f32 v67, v4, v8
	s_waitcnt vmcnt(1)
	v_mul_f32_e32 v12, 0x42800000, v12
	s_waitcnt vmcnt(0)
	v_mul_f32_e32 v0, 0x42800000, v0
	v_med3_f32 v4, v12, s67, v98
	v_med3_f32 v0, v0, s67, v98
	v_cvt_pk_fp8_f32 v67, v4, v0 op_sel:[0,0,1]
	v_mul_f32_e32 v0, 0x42800000, v57
	v_mul_f32_e32 v4, 0x42800000, v53
	v_med3_f32 v0, v0, s67, v98
	v_med3_f32 v4, v4, s67, v98
	v_mov_b32_e32 v68, v77
	v_cvt_pk_fp8_f32 v68, v0, v4
	v_mul_f32_e32 v8, 0x42800000, v61
	v_mul_f32_e32 v0, 0x42800000, v45
	v_med3_f32 v4, v8, s67, v98
	v_med3_f32 v0, v0, s67, v98
	v_cvt_pk_fp8_f32 v68, v4, v0 op_sel:[0,0,1]
	v_mul_f32_e32 v0, 0x42800000, v41
	v_mul_f32_e32 v4, 0x42800000, v37
	v_med3_f32 v0, v0, s67, v98
	v_med3_f32 v4, v4, s67, v98
	v_mov_b32_e32 v69, v77
	v_cvt_pk_fp8_f32 v69, v0, v4
	v_mul_f32_e32 v8, 0x42800000, v49
	v_mul_f32_e32 v0, 0x42800000, v33
	v_med3_f32 v4, v8, s67, v98
	v_med3_f32 v0, v0, s67, v98
	v_cvt_pk_fp8_f32 v69, v4, v0 op_sel:[0,0,1]
	v_mul_f32_e32 v0, 0x42800000, v21
	v_mul_f32_e32 v4, 0x42800000, v25
	v_med3_f32 v0, v0, s67, v98
	v_med3_f32 v4, v4, s67, v98
	v_mov_b32_e32 v70, v77
	v_cvt_pk_fp8_f32 v70, v0, v4
	v_mul_f32_e32 v8, 0x42800000, v29
	v_mul_f32_e32 v0, 0x42800000, v17
	v_med3_f32 v4, v8, s67, v98
	v_med3_f32 v0, v0, s67, v98
	v_cvt_pk_fp8_f32 v70, v4, v0 op_sel:[0,0,1]
	v_mul_f32_e32 v0, 0x42800000, v5
	v_mul_f32_e32 v4, 0x42800000, v9
	v_med3_f32 v0, v0, s67, v98
	v_med3_f32 v4, v4, s67, v98
	v_mov_b32_e32 v71, v77
	v_cvt_pk_fp8_f32 v71, v0, v4
	v_mul_f32_e32 v5, 0x42800000, v13
	v_mul_f32_e32 v0, 0x42800000, v1
	v_med3_f32 v1, v5, s67, v98
	v_med3_f32 v0, v0, s67, v98
	v_cvt_pk_fp8_f32 v71, v1, v0 op_sel:[0,0,1]
	v_mul_f32_e32 v0, 0x42800000, v58
	v_mul_f32_e32 v1, 0x42800000, v54
	v_med3_f32 v0, v0, s67, v98
	v_med3_f32 v1, v1, s67, v98
	v_mov_b32_e32 v72, v77
	v_cvt_pk_fp8_f32 v72, v0, v1
	v_mul_f32_e32 v4, 0x42800000, v62
	v_mul_f32_e32 v0, 0x42800000, v46
	v_med3_f32 v1, v4, s67, v98
	v_med3_f32 v0, v0, s67, v98
	v_cvt_pk_fp8_f32 v72, v1, v0 op_sel:[0,0,1]
	v_mul_f32_e32 v0, 0x42800000, v42
	v_mul_f32_e32 v1, 0x42800000, v38
	v_med3_f32 v0, v0, s67, v98
	v_med3_f32 v1, v1, s67, v98
	v_mov_b32_e32 v73, v77
	v_cvt_pk_fp8_f32 v73, v0, v1
	v_mul_f32_e32 v4, 0x42800000, v50
	v_mul_f32_e32 v0, 0x42800000, v34
	v_med3_f32 v1, v4, s67, v98
	v_med3_f32 v0, v0, s67, v98
	v_cvt_pk_fp8_f32 v73, v1, v0 op_sel:[0,0,1]
	v_mul_f32_e32 v0, 0x42800000, v22
	v_mul_f32_e32 v1, 0x42800000, v26
	v_med3_f32 v0, v0, s67, v98
	v_med3_f32 v1, v1, s67, v98
	v_mov_b32_e32 v74, v77
	v_cvt_pk_fp8_f32 v74, v0, v1
	v_mul_f32_e32 v4, 0x42800000, v30
	v_mul_f32_e32 v0, 0x42800000, v18
	v_med3_f32 v1, v4, s67, v98
	v_med3_f32 v0, v0, s67, v98
	v_cvt_pk_fp8_f32 v74, v1, v0 op_sel:[0,0,1]
	v_mul_f32_e32 v0, 0x42800000, v6
	v_mul_f32_e32 v1, 0x42800000, v10
	v_med3_f32 v0, v0, s67, v98
	v_med3_f32 v1, v1, s67, v98
	v_mov_b32_e32 v75, v77
	v_cvt_pk_fp8_f32 v75, v0, v1
	v_mul_f32_e32 v4, 0x42800000, v14
	v_mul_f32_e32 v0, 0x42800000, v2
	v_med3_f32 v1, v4, s67, v98
	v_med3_f32 v0, v0, s67, v98
	v_cvt_pk_fp8_f32 v75, v1, v0 op_sel:[0,0,1]
	v_mul_f32_e32 v0, 0x42800000, v59
	v_mul_f32_e32 v1, 0x42800000, v55
	v_med3_f32 v0, v0, s67, v98
	v_med3_f32 v1, v1, s67, v98
	v_mov_b32_e32 v4, v77
	v_cvt_pk_fp8_f32 v4, v0, v1
	v_mul_f32_e32 v2, 0x42800000, v63
	v_mul_f32_e32 v0, 0x42800000, v47
	v_med3_f32 v1, v2, s67, v98
	v_med3_f32 v0, v0, s67, v98
	v_cvt_pk_fp8_f32 v4, v1, v0 op_sel:[0,0,1]
	v_mul_f32_e32 v0, 0x42800000, v43
	v_mul_f32_e32 v1, 0x42800000, v39
	v_med3_f32 v0, v0, s67, v98
	v_med3_f32 v1, v1, s67, v98
	v_mov_b32_e32 v5, v77
	v_cvt_pk_fp8_f32 v5, v0, v1
	v_mul_f32_e32 v2, 0x42800000, v51
	v_mul_f32_e32 v0, 0x42800000, v35
	v_med3_f32 v1, v2, s67, v98
	v_med3_f32 v0, v0, s67, v98
	v_cvt_pk_fp8_f32 v5, v1, v0 op_sel:[0,0,1]
	v_mul_f32_e32 v0, 0x42800000, v23
	v_mul_f32_e32 v1, 0x42800000, v27
	v_mul_f32_e32 v56, 0x42800000, v56
	v_mul_f32_e32 v52, 0x42800000, v52
	v_med3_f32 v0, v0, s67, v98
	v_med3_f32 v1, v1, s67, v98
	v_mov_b32_e32 v6, v77
	v_med3_f32 v56, v56, s67, v98
	v_med3_f32 v52, v52, s67, v98
	v_mov_b32_e32 v64, v77
	v_cvt_pk_fp8_f32 v6, v0, v1
	v_cvt_pk_fp8_f32 v64, v56, v52
	v_mul_f32_e32 v40, 0x42800000, v40
	v_mul_f32_e32 v36, 0x42800000, v36
	v_mul_f32_e32 v20, 0x42800000, v20
	v_mul_f32_e32 v24, 0x42800000, v24
	v_med3_f32 v40, v40, s67, v98
	v_med3_f32 v36, v36, s67, v98
	v_mov_b32_e32 v65, v77
	v_med3_f32 v20, v20, s67, v98
	v_med3_f32 v24, v24, s67, v98
	v_mov_b32_e32 v66, v77
	v_mul_f32_e32 v2, 0x42800000, v31
	v_mul_f32_e32 v0, 0x42800000, v19
	v_mul_f32_e32 v60, 0x42800000, v60
	v_mul_f32_e32 v44, 0x42800000, v44
	v_cvt_pk_fp8_f32 v65, v40, v36
	v_cvt_pk_fp8_f32 v66, v20, v24
	v_med3_f32 v1, v2, s67, v98
	v_med3_f32 v0, v0, s67, v98
	v_med3_f32 v52, v60, s67, v98
	v_med3_f32 v44, v44, s67, v98
	v_cvt_pk_fp8_f32 v6, v1, v0 op_sel:[0,0,1]
	v_mul_f32_e32 v0, 0x42800000, v7
	v_mul_f32_e32 v1, 0x42800000, v11
	v_cvt_pk_fp8_f32 v64, v52, v44 op_sel:[0,0,1]
	v_mul_f32_e32 v44, 0x42800000, v48
	v_mul_f32_e32 v32, 0x42800000, v32
	v_mul_f32_e32 v28, 0x42800000, v28
	v_mul_f32_e32 v16, 0x42800000, v16
	v_med3_f32 v0, v0, s67, v98
	v_med3_f32 v1, v1, s67, v98
	v_mov_b32_e32 v7, v77
	v_med3_f32 v36, v44, s67, v98
	v_med3_f32 v32, v32, s67, v98
	v_med3_f32 v20, v28, s67, v98
	v_med3_f32 v16, v16, s67, v98
	v_cvt_pk_fp8_f32 v7, v0, v1
	v_cvt_pk_fp8_f32 v65, v36, v32 op_sel:[0,0,1]
	v_cvt_pk_fp8_f32 v66, v20, v16 op_sel:[0,0,1]
	v_mul_f32_e32 v2, 0x42800000, v15
	v_mul_f32_e32 v0, 0x42800000, v3
	v_med3_f32 v1, v2, s67, v98
	v_med3_f32 v0, v0, s67, v98
	v_cvt_pk_fp8_f32 v7, v1, v0 op_sel:[0,0,1]
	s_mul_hi_i32 s3, s2, 0x380000
	s_mul_i32 s2, s2, 0x380000
	ds_write_b128 v95, v[64:67] offset:40960
	ds_write_b128 v95, v[68:71] offset:41040
	ds_write_b128 v95, v[72:75] offset:41120
	ds_write_b128 v95, v[4:7] offset:41200
	s_add_u32 s2, s51, s2
	s_waitcnt lgkmcnt(0)
	s_addc_u32 s3, s52, s3
	s_add_i32 s13, s13, s0
	s_ashr_i32 s0, s22, 31
	ds_read_b128 v[0:3], v96 offset:40960
	s_add_u32 s2, s2, s22
	v_add_u32_e32 v4, s13, v83
	s_addc_u32 s3, s3, s0
	v_ashrrev_i32_e32 v5, 31, v4
	v_lshl_add_u64 v[8:9], s[2:3], 0, v[78:79]
	v_lshlrev_b64 v[4:5], 9, v[4:5]
	v_lshl_add_u64 v[10:11], v[8:9], 0, v[4:5]
	ds_read_b128 v[4:7], v96 offset:42240
	s_waitcnt lgkmcnt(1)
	global_store_dwordx4 v[10:11], v[0:3], off sc1
	s_nop 1
	v_add_u32_e32 v0, s13, v84
	v_ashrrev_i32_e32 v1, 31, v0
	v_lshlrev_b64 v[0:1], 9, v[0:1]
	v_lshl_add_u64 v[0:1], v[8:9], 0, v[0:1]
	s_waitcnt lgkmcnt(0)
	global_store_dwordx4 v[0:1], v[4:7], off sc1
	ds_read_b128 v[0:3], v96 offset:43520
	s_nop 0
	v_add_u32_e32 v4, s13, v85
	v_ashrrev_i32_e32 v5, 31, v4
	v_lshlrev_b64 v[4:5], 9, v[4:5]
	v_lshl_add_u64 v[10:11], v[8:9], 0, v[4:5]
	ds_read_b128 v[4:7], v96 offset:44800
	s_waitcnt lgkmcnt(1)
	global_store_dwordx4 v[10:11], v[0:3], off sc1
	s_nop 1
	v_add_u32_e32 v0, s13, v86
	v_ashrrev_i32_e32 v1, 31, v0
	v_lshlrev_b64 v[0:1], 9, v[0:1]
	v_lshl_add_u64 v[0:1], v[8:9], 0, v[0:1]
	s_waitcnt lgkmcnt(0)
	global_store_dwordx4 v[0:1], v[4:7], off sc1
	s_waitcnt lgkmcnt(0)

.LBB0_647:
	s_add_i32 s92, s40, s65
	s_add_i32 s0, s92, 0x1cc9
	s_mul_hi_i32 s2, s0, 0x20d56b39
	s_lshr_b32 s3, s2, 31
	s_ashr_i32 s2, s2, 12
	s_add_i32 s2, s2, s3
	s_mul_i32 s3, s2, 0x7cc0
	s_sub_i32 s30, s0, s3
	s_cmpk_gt_i32 s30, 0x1cbf
	s_mov_b64 s[4:5], -1
	s_cbranch_scc0 .LBB0_653
	s_add_i32 s9, s30, 0xffffe340
	s_and_b32 s8, s9, 0xff
	s_cmpk_gt_u32 s30, 0x5cbf
	s_cbranch_scc0 .LBB0_650
	v_mov_b32_e32 v0, s61
	s_add_i32 s0, s30, 0xffffa340
	s_ashr_i32 s3, s2, 31
	ds_read_b64 v[0:1], v0
	s_lshr_b32 s0, s0, 8
	s_lshl_b64 s[4:5], s[2:3], 26
	s_add_u32 s10, s41, s4
	s_addc_u32 s11, s43, s5
	s_lshl_b64 s[4:5], s[0:1], 20
	s_add_u32 s4, s10, s4
	s_addc_u32 s5, s11, s5
	s_waitcnt lgkmcnt(0)
	v_readfirstlane_b32 s12, v0
	s_lshl_b64 s[10:11], s[2:3], 27
	v_readfirstlane_b32 s13, v1
	s_add_u32 s3, s12, s10
	s_addc_u32 s13, s13, s11
	s_lshl_b64 s[10:11], s[0:1], 22
	s_add_u32 s12, s3, s10
	s_addc_u32 s13, s13, s11
	s_lshl_b32 s0, s8, 3
	s_and_b32 s3, s0, 0x7c0
	s_lshl_b32 s0, s30, 6
	s_and_b32 s10, s0, 0x1c0
	v_or_b32_e32 v0, s10, v82
	v_lshlrev_b32_e32 v0, 13, v0
	v_mov_b32_e32 v1, v77
	v_lshl_add_u64 v[0:1], s[12:13], 0, v[0:1]
	s_lshl_b32 s0, s3, 2
	v_lshl_add_u64 v[0:1], v[0:1], 0, s[0:1]
	v_mov_b32_e32 v81, v77
	v_lshl_add_u64 v[60:61], v[0:1], 0, v[80:81]
	v_add_co_u32_e32 v4, vcc, s62, v60
	s_mov_b32 s0, 0x8000
	s_nop 0
	v_addc_co_u32_e32 v5, vcc, 0, v61, vcc
	v_add_co_u32_e32 v8, vcc, s63, v60
	global_load_dwordx4 v[0:3], v[60:61], off nt
	s_nop 0
	global_load_dwordx4 v[4:7], v[4:5], off nt
	v_addc_co_u32_e32 v9, vcc, 0, v61, vcc
	v_add_co_u32_e32 v10, vcc, s64, v60
	v_mov_b32_e32 v64, v77
	s_nop 0
	v_addc_co_u32_e32 v11, vcc, 0, v61, vcc
	v_add_co_u32_e32 v16, vcc, s0, v60
	s_mov_b32 s0, 0xa000
	s_nop 0
	v_addc_co_u32_e32 v17, vcc, 0, v61, vcc
	v_add_co_u32_e32 v20, vcc, s0, v60
	s_mov_b32 s0, 0xc000
	s_nop 0
	v_addc_co_u32_e32 v21, vcc, 0, v61, vcc
	v_add_co_u32_e32 v24, vcc, s0, v60
	s_mov_b32 s0, 0xe000
	s_nop 0
	v_addc_co_u32_e32 v25, vcc, 0, v61, vcc
	global_load_dwordx4 v[12:15], v[8:9], off nt
	s_nop 0
	global_load_dwordx4 v[8:11], v[10:11], off nt
	v_add_co_u32_e32 v26, vcc, s0, v60
	s_mov_b32 s0, 0x10000
	s_nop 0
	v_addc_co_u32_e32 v27, vcc, 0, v61, vcc
	global_load_dwordx4 v[16:19], v[16:17], off nt
	s_nop 0
	global_load_dwordx4 v[20:23], v[20:21], off nt
	v_add_co_u32_e32 v28, vcc, s0, v60
	s_mov_b32 s0, 0x14000
	s_nop 0
	v_addc_co_u32_e32 v29, vcc, 0, v61, vcc
	v_add_co_u32_e32 v36, vcc, s66, v60
	global_load_dwordx4 v[32:35], v[24:25], off nt
	s_nop 0
	global_load_dwordx4 v[24:27], v[26:27], off nt
	v_addc_co_u32_e32 v37, vcc, 0, v61, vcc
	v_add_co_u32_e32 v40, vcc, s0, v60
	s_mov_b32 s0, 0x16000
	s_nop 0
	v_addc_co_u32_e32 v41, vcc, 0, v61, vcc
	global_load_dwordx4 v[28:31], v[28:29], off nt
	s_nop 0
	global_load_dwordx4 v[36:39], v[36:37], off nt
	v_add_co_u32_e32 v42, vcc, s0, v60
	s_mov_b32 s0, 0x18000
	s_nop 0
	v_addc_co_u32_e32 v43, vcc, 0, v61, vcc
	v_add_co_u32_e32 v48, vcc, s0, v60
	s_mov_b32 s0, 0x1a000
	s_nop 0
	v_addc_co_u32_e32 v49, vcc, 0, v61, vcc
	global_load_dwordx4 v[44:47], v[40:41], off nt
	s_nop 0
	global_load_dwordx4 v[40:43], v[42:43], off nt
	v_add_co_u32_e32 v52, vcc, s0, v60
	s_mov_b32 s0, 0x1c000
	s_nop 0
	v_addc_co_u32_e32 v53, vcc, 0, v61, vcc
	global_load_dwordx4 v[48:51], v[48:49], off nt
	s_nop 0
	global_load_dwordx4 v[52:55], v[52:53], off nt
	v_add_co_u32_e32 v56, vcc, s0, v60
	s_mov_b32 s0, 0x1e000
	s_nop 0
	v_addc_co_u32_e32 v57, vcc, 0, v61, vcc
	v_add_co_u32_e32 v60, vcc, s0, v60
	global_load_dwordx4 v[56:59], v[56:57], off nt
	s_nop 0
	v_addc_co_u32_e32 v61, vcc, 0, v61, vcc
	global_load_dwordx4 v[60:63], v[60:61], off nt
	v_mov_b32_e32 v65, v77
	v_mov_b32_e32 v66, v77
	v_mov_b32_e32 v67, v77
	v_mov_b32_e32 v68, v77
	v_mov_b32_e32 v69, v77
	s_waitcnt vmcnt(15)
	v_mul_f32_e32 v0, 0x42000000, v0
	s_waitcnt vmcnt(14)
	v_mul_f32_e32 v4, 0x42000000, v4
	v_med3_f32 v0, v0, s67, v98
	v_med3_f32 v4, v4, s67, v98
	v_cvt_pk_fp8_f32 v64, v0, v4
	v_mov_b32_e32 v70, v77
	v_mov_b32_e32 v71, v77
	v_mov_b32_e32 v72, v77
	v_mov_b32_e32 v73, v77
	v_mov_b32_e32 v74, v77
	v_mov_b32_e32 v75, v77
	s_add_u32 s4, s4, s10
	s_addc_u32 s5, s5, 0
	s_waitcnt vmcnt(13)
	v_mul_f32_e32 v12, 0x42000000, v12
	s_waitcnt vmcnt(12)
	v_mul_f32_e32 v0, 0x42000000, v8
	v_med3_f32 v4, v12, s67, v98
	v_med3_f32 v0, v0, s67, v98
	v_cvt_pk_fp8_f32 v64, v4, v0 op_sel:[0,0,1]
	s_waitcnt vmcnt(11)
	v_mul_f32_e32 v0, 0x42000000, v16
	s_waitcnt vmcnt(10)
	v_mul_f32_e32 v4, 0x42000000, v20
	v_med3_f32 v0, v0, s67, v98
	v_med3_f32 v4, v4, s67, v98
	v_cvt_pk_fp8_f32 v65, v0, v4
	s_waitcnt vmcnt(9)
	v_mul_f32_e32 v8, 0x42000000, v32
	s_waitcnt vmcnt(8)
	v_mul_f32_e32 v0, 0x42000000, v24
	v_med3_f32 v4, v8, s67, v98
	v_med3_f32 v0, v0, s67, v98
	v_cvt_pk_fp8_f32 v65, v4, v0 op_sel:[0,0,1]
	s_waitcnt vmcnt(7)
	v_mul_f32_e32 v0, 0x42000000, v28
	s_waitcnt vmcnt(6)
	v_mul_f32_e32 v4, 0x42000000, v36
	v_med3_f32 v0, v0, s67, v98
	v_med3_f32 v4, v4, s67, v98
	v_cvt_pk_fp8_f32 v66, v0, v4
	s_waitcnt vmcnt(5)
	v_mul_f32_e32 v8, 0x42000000, v44
	s_waitcnt vmcnt(4)
	v_mul_f32_e32 v0, 0x42000000, v40
	v_med3_f32 v4, v8, s67, v98
	v_med3_f32 v0, v0, s67, v98
	v_cvt_pk_fp8_f32 v66, v4, v0 op_sel:[0,0,1]
	s_waitcnt vmcnt(3)
	v_mul_f32_e32 v0, 0x42000000, v48
	s_waitcnt vmcnt(2)
	v_mul_f32_e32 v4, 0x42000000, v52
	v_med3_f32 v0, v0, s67, v98
	v_med3_f32 v4, v4, s67, v98
	v_cvt_pk_fp8_f32 v67, v0, v4
	s_waitcnt vmcnt(1)
	v_mul_f32_e32 v8, 0x42000000, v56
	v_med3_f32 v4, v8, s67, v98
	s_waitcnt vmcnt(0)
	v_mul_f32_e32 v0, 0x42000000, v60
	v_med3_f32 v0, v0, s67, v98
	v_cvt_pk_fp8_f32 v67, v4, v0 op_sel:[0,0,1]
	v_mul_f32_e32 v0, 0x42000000, v1
	v_mul_f32_e32 v1, 0x42000000, v5
	v_med3_f32 v0, v0, s67, v98
	v_med3_f32 v1, v1, s67, v98
	v_cvt_pk_fp8_f32 v68, v0, v1
	v_mul_f32_e32 v4, 0x42000000, v13
	v_mul_f32_e32 v0, 0x42000000, v9
	v_med3_f32 v1, v4, s67, v98
	v_med3_f32 v0, v0, s67, v98
	v_cvt_pk_fp8_f32 v68, v1, v0 op_sel:[0,0,1]
	v_mul_f32_e32 v0, 0x42000000, v17
	v_mul_f32_e32 v1, 0x42000000, v21
	v_med3_f32 v0, v0, s67, v98
	v_med3_f32 v1, v1, s67, v98
	v_cvt_pk_fp8_f32 v69, v0, v1
	v_mul_f32_e32 v4, 0x42000000, v33
	v_mul_f32_e32 v0, 0x42000000, v25
	v_med3_f32 v1, v4, s67, v98
	v_med3_f32 v0, v0, s67, v98
	v_cvt_pk_fp8_f32 v69, v1, v0 op_sel:[0,0,1]
	v_mul_f32_e32 v0, 0x42000000, v29
	v_mul_f32_e32 v1, 0x42000000, v37
	v_med3_f32 v0, v0, s67, v98
	v_med3_f32 v1, v1, s67, v98
	v_cvt_pk_fp8_f32 v70, v0, v1
	v_mul_f32_e32 v4, 0x42000000, v45
	v_mul_f32_e32 v0, 0x42000000, v41
	v_med3_f32 v1, v4, s67, v98
	v_med3_f32 v0, v0, s67, v98
	v_cvt_pk_fp8_f32 v70, v1, v0 op_sel:[0,0,1]
	v_mul_f32_e32 v0, 0x42000000, v49
	v_mul_f32_e32 v1, 0x42000000, v53
	v_med3_f32 v0, v0, s67, v98
	v_med3_f32 v1, v1, s67, v98
	v_cvt_pk_fp8_f32 v71, v0, v1
	v_mul_f32_e32 v4, 0x42000000, v57
	v_mul_f32_e32 v0, 0x42000000, v61
	v_med3_f32 v1, v4, s67, v98
	v_med3_f32 v0, v0, s67, v98
	v_cvt_pk_fp8_f32 v71, v1, v0 op_sel:[0,0,1]
	v_mul_f32_e32 v0, 0x42000000, v2
	v_mul_f32_e32 v1, 0x42000000, v6
	v_med3_f32 v0, v0, s67, v98
	v_med3_f32 v1, v1, s67, v98
	v_cvt_pk_fp8_f32 v72, v0, v1
	v_mul_f32_e32 v2, 0x42000000, v14
	v_mul_f32_e32 v0, 0x42000000, v10
	v_med3_f32 v1, v2, s67, v98
	v_med3_f32 v0, v0, s67, v98
	v_cvt_pk_fp8_f32 v72, v1, v0 op_sel:[0,0,1]
	v_mul_f32_e32 v0, 0x42000000, v18
	v_mul_f32_e32 v1, 0x42000000, v22
	v_med3_f32 v0, v0, s67, v98
	v_med3_f32 v1, v1, s67, v98
	v_cvt_pk_fp8_f32 v73, v0, v1
	v_mul_f32_e32 v2, 0x42000000, v34
	v_mul_f32_e32 v0, 0x42000000, v26
	v_med3_f32 v1, v2, s67, v98
	v_med3_f32 v0, v0, s67, v98
	v_cvt_pk_fp8_f32 v73, v1, v0 op_sel:[0,0,1]
	v_mul_f32_e32 v0, 0x42000000, v30
	v_mul_f32_e32 v1, 0x42000000, v38
	v_med3_f32 v0, v0, s67, v98
	v_med3_f32 v1, v1, s67, v98
	v_cvt_pk_fp8_f32 v74, v0, v1
	v_mul_f32_e32 v2, 0x42000000, v46
	v_mul_f32_e32 v0, 0x42000000, v42
	v_med3_f32 v1, v2, s67, v98
	v_med3_f32 v0, v0, s67, v98
	v_cvt_pk_fp8_f32 v74, v1, v0 op_sel:[0,0,1]
	v_mul_f32_e32 v0, 0x42000000, v50
	v_mul_f32_e32 v1, 0x42000000, v54
	v_med3_f32 v0, v0, s67, v98
	v_med3_f32 v1, v1, s67, v98
	v_cvt_pk_fp8_f32 v75, v0, v1
	v_mul_f32_e32 v2, 0x42000000, v58
	v_mul_f32_e32 v0, 0x42000000, v62
	v_med3_f32 v1, v2, s67, v98
	v_med3_f32 v0, v0, s67, v98
	v_cvt_pk_fp8_f32 v75, v1, v0 op_sel:[0,0,1]
	v_mul_f32_e32 v0, 0x42000000, v3
	v_mul_f32_e32 v1, 0x42000000, v7
	v_med3_f32 v3, v0, s67, v98
	v_med3_f32 v1, v1, s67, v98
	v_mov_b32_e32 v0, v77
	v_cvt_pk_fp8_f32 v0, v3, v1
	v_mul_f32_e32 v2, 0x42000000, v15
	v_mul_f32_e32 v1, 0x42000000, v11
	v_med3_f32 v2, v2, s67, v98
	v_med3_f32 v1, v1, s67, v98
	v_cvt_pk_fp8_f32 v0, v2, v1 op_sel:[0,0,1]
	v_mul_f32_e32 v1, 0x42000000, v19
	v_mul_f32_e32 v2, 0x42000000, v23
	v_med3_f32 v4, v1, s67, v98
	v_med3_f32 v2, v2, s67, v98
	v_mov_b32_e32 v1, v77
	v_cvt_pk_fp8_f32 v1, v4, v2
	v_mul_f32_e32 v3, 0x42000000, v35
	v_mul_f32_e32 v2, 0x42000000, v27
	v_med3_f32 v3, v3, s67, v98
	v_med3_f32 v2, v2, s67, v98
	v_cvt_pk_fp8_f32 v1, v3, v2 op_sel:[0,0,1]
	v_mul_f32_e32 v2, 0x42000000, v31
	v_mul_f32_e32 v3, 0x42000000, v39
	v_med3_f32 v5, v2, s67, v98
	v_med3_f32 v3, v3, s67, v98
	v_mov_b32_e32 v2, v77
	v_cvt_pk_fp8_f32 v2, v5, v3
	v_mul_f32_e32 v4, 0x42000000, v47
	v_mul_f32_e32 v3, 0x42000000, v43
	v_med3_f32 v4, v4, s67, v98
	v_med3_f32 v3, v3, s67, v98
	v_cvt_pk_fp8_f32 v2, v4, v3 op_sel:[0,0,1]
	v_mul_f32_e32 v3, 0x42000000, v51
	v_mul_f32_e32 v4, 0x42000000, v55
	v_med3_f32 v6, v3, s67, v98
	v_med3_f32 v4, v4, s67, v98
	v_mov_b32_e32 v3, v77
	v_cvt_pk_fp8_f32 v3, v6, v4
	v_mul_f32_e32 v5, 0x42000000, v59
	v_mul_f32_e32 v4, 0x42000000, v63
	v_med3_f32 v5, v5, s67, v98
	v_med3_f32 v4, v4, s67, v98
	v_cvt_pk_fp8_f32 v3, v5, v4 op_sel:[0,0,1]
	ds_write_b128 v95, v[64:67] offset:40960
	ds_write_b128 v95, v[68:71] offset:41040
	ds_write_b128 v95, v[72:75] offset:41120
	ds_write_b128 v95, v[0:3] offset:41200
	s_waitcnt lgkmcnt(0)
	ds_read_b128 v[0:3], v96 offset:40960
	v_or_b32_e32 v4, s3, v83
	v_lshl_add_u64 v[8:9], s[4:5], 0, v[78:79]
	v_lshlrev_b32_e32 v4, 9, v4
	v_mov_b32_e32 v5, v77
	v_lshl_add_u64 v[10:11], v[8:9], 0, v[4:5]
	ds_read_b128 v[4:7], v96 offset:42240
	s_waitcnt lgkmcnt(1)
	global_store_dwordx4 v[10:11], v[0:3], off sc1
	s_mov_b64 s[4:5], 0
	s_nop 0
	v_or_b32_e32 v0, s3, v84
	v_lshlrev_b32_e32 v0, 9, v0
	v_mov_b32_e32 v1, v77
	v_lshl_add_u64 v[0:1], v[8:9], 0, v[0:1]
	s_waitcnt lgkmcnt(0)
	global_store_dwordx4 v[0:1], v[4:7], off sc1
	ds_read_b128 v[0:3], v96 offset:43520
	s_nop 0
	v_or_b32_e32 v4, s3, v85
	v_lshlrev_b32_e32 v4, 9, v4
	v_mov_b32_e32 v5, v77
	v_lshl_add_u64 v[10:11], v[8:9], 0, v[4:5]
	ds_read_b128 v[4:7], v96 offset:44800
	s_waitcnt lgkmcnt(1)
	global_store_dwordx4 v[10:11], v[0:3], off sc1
	s_nop 1
	v_or_b32_e32 v0, s3, v86
	v_lshlrev_b32_e32 v0, 9, v0
	v_mov_b32_e32 v1, v77
	v_lshl_add_u64 v[0:1], v[8:9], 0, v[0:1]
	s_waitcnt lgkmcnt(0)
	global_store_dwordx4 v[0:1], v[4:7], off sc1
	s_waitcnt lgkmcnt(0)
.LBB0_650:
	s_andn2_b64 vcc, exec, s[4:5]
	s_cbranch_vccnz .LBB0_652
	s_ashr_i32 s3, s2, 31
	s_lshr_b32 s0, s9, 9
	s_bfe_u32 s9, s9, 0x10008
	s_lshl_b64 s[10:11], s[2:3], 27
	s_add_u32 s3, s44, s10
	s_addc_u32 s12, s45, s11
	s_lshl_b32 s13, s9, 18
	s_lshl_b64 s[4:5], s[0:1], 21
	s_add_u32 s3, s3, s4
	s_addc_u32 s4, s12, s5
	s_add_u32 s3, s3, s13
	s_addc_u32 s4, s4, 0
	s_lshl_b32 s5, s9, 3
	s_add_i32 s5, s5, 0
	s_add_i32 s5, s5, 0x204e8
	v_mov_b32_e32 v0, s5
	ds_read_b64 v[0:1], v0
	v_mov_b32_e32 v81, v77
	v_mov_b32_e32 v12, v77
	v_mov_b32_e32 v14, v77
	v_mov_b32_e32 v13, v77
	s_waitcnt lgkmcnt(0)
	v_readfirstlane_b32 s5, v0
	v_readfirstlane_b32 s9, v1
	s_add_u32 s5, s5, s10
	s_addc_u32 s9, s9, s11
	s_lshl_b64 s[10:11], s[0:1], 22
	s_add_u32 s10, s5, s10
	s_addc_u32 s11, s9, s11
	s_lshl_b32 s0, s30, 6
	s_and_b32 s5, s0, 0x7c0
	v_or_b32_e32 v0, s5, v82
	v_lshlrev_b32_e32 v0, 11, v0
	v_mov_b32_e32 v1, v77
	s_lshl_b32 s0, s8, 3
	v_lshl_add_u64 v[0:1], s[10:11], 0, v[0:1]
	s_and_b32 s0, s0, 0x700
	v_lshl_add_u64 v[0:1], v[0:1], 0, s[0:1]
	v_lshl_add_u64 v[0:1], v[0:1], 0, v[80:81]
	s_movk_i32 s0, 0x1000
	v_add_co_u32_e32 v2, vcc, s0, v0
	global_load_dwordx4 v[36:39], v[0:1], off nt
	global_load_dwordx4 v[40:43], v[0:1], off offset:2048 nt
	v_addc_co_u32_e32 v3, vcc, 0, v1, vcc
	v_add_co_u32_e32 v4, vcc, s62, v0
	v_mov_b32_e32 v68, v77
	s_nop 0
	v_addc_co_u32_e32 v5, vcc, 0, v1, vcc
	global_load_dwordx4 v[56:59], v[4:5], off offset:-4096 nt
	global_load_dwordx4 v[20:23], v[4:5], off nt
	global_load_dwordx4 v[24:27], v[4:5], off offset:2048 nt
	v_add_co_u32_e32 v4, vcc, s68, v0
	v_mov_b32_e32 v69, v77
	s_nop 0
	v_addc_co_u32_e32 v5, vcc, 0, v1, vcc
	v_add_co_u32_e32 v6, vcc, s63, v0
	v_mov_b32_e32 v70, v77
	s_nop 0
	v_addc_co_u32_e32 v7, vcc, 0, v1, vcc
	global_load_dwordx4 v[64:67], v[2:3], off offset:2048 nt
	global_load_dwordx4 v[44:47], v[4:5], off offset:2048 nt
	global_load_dwordx4 v[60:63], v[6:7], off offset:-4096 nt
	global_load_dwordx4 v[16:19], v[6:7], off nt
	v_add_co_u32_e32 v2, vcc, s69, v0
	v_mov_b32_e32 v71, v77
	s_nop 0
	v_addc_co_u32_e32 v3, vcc, 0, v1, vcc
	v_add_co_u32_e32 v8, vcc, s64, v0
	v_mov_b32_e32 v72, v77
	s_nop 0
	v_addc_co_u32_e32 v9, vcc, 0, v1, vcc
	global_load_dwordx4 v[48:51], v[6:7], off offset:2048 nt
	global_load_dwordx4 v[52:55], v[8:9], off offset:-4096 nt
	global_load_dwordx4 v[28:31], v[2:3], off offset:2048 nt
	s_nop 0
	global_load_dwordx4 v[4:7], v[8:9], off nt
	s_nop 0
	global_load_dwordx4 v[8:11], v[8:9], off offset:2048 nt
	v_add_co_u32_e32 v0, vcc, s70, v0
	v_mov_b32_e32 v73, v77
	s_nop 0
	v_addc_co_u32_e32 v1, vcc, 0, v1, vcc
	global_load_dwordx4 v[32:35], v[0:1], off nt
	s_nop 0
	global_load_dwordx4 v[0:3], v[0:1], off offset:2048 nt
	v_mov_b32_e32 v74, v77
	v_mov_b32_e32 v75, v77
	s_lshl_b32 s0, s8, 1
	s_add_u32 s10, s3, s5
	s_addc_u32 s11, s4, 0
	s_lshl_b32 s3, s8, 2
	s_and_b32 s3, s3, 0x300
	s_and_b32 s0, s0, 64
	s_or_b32 s0, s0, s3
	s_waitcnt vmcnt(15)
	v_mul_f32_e32 v15, 0x42800000, v36
	s_waitcnt vmcnt(14)
	v_mul_f32_e32 v36, 0x42800000, v40
	v_med3_f32 v15, v15, s67, v98
	v_med3_f32 v36, v36, s67, v98
	v_cvt_pk_fp8_f32 v12, v15, v36
	s_waitcnt vmcnt(13)
	v_mul_f32_e32 v40, 0x42800000, v56
	s_waitcnt vmcnt(12)
	v_mul_f32_e32 v20, 0x42800000, v20
	s_waitcnt vmcnt(11)
	v_mul_f32_e32 v24, 0x42800000, v24
	v_med3_f32 v15, v20, s67, v98
	v_med3_f32 v20, v24, s67, v98
	v_cvt_pk_fp8_f32 v13, v15, v20
	v_med3_f32 v40, v40, s67, v98
	s_waitcnt vmcnt(10)
	v_mul_f32_e32 v56, 0x42800000, v64
	s_waitcnt vmcnt(9)
	v_mul_f32_e32 v44, 0x42800000, v44
	v_med3_f32 v36, v44, s67, v98
	s_waitcnt vmcnt(7)
	v_mul_f32_e32 v16, 0x42800000, v16
	v_med3_f32 v16, v16, s67, v98
	v_mul_f32_e32 v60, 0x42800000, v60
	v_med3_f32 v56, v56, s67, v98
	v_med3_f32 v24, v60, s67, v98
	v_cvt_pk_fp8_f32 v12, v40, v56 op_sel:[0,0,1]
	v_cvt_pk_fp8_f32 v13, v24, v36 op_sel:[0,0,1]
	s_waitcnt vmcnt(6)
	v_mul_f32_e32 v48, 0x42800000, v48
	v_med3_f32 v44, v48, s67, v98
	v_cvt_pk_fp8_f32 v14, v16, v44
	s_waitcnt vmcnt(5)
	v_mul_f32_e32 v52, 0x42800000, v52
	s_waitcnt vmcnt(4)
	v_mul_f32_e32 v28, 0x42800000, v28
	s_waitcnt vmcnt(3)
	v_mul_f32_e32 v4, 0x42800000, v4
	s_waitcnt vmcnt(2)
	v_mul_f32_e32 v8, 0x42800000, v8
	v_med3_f32 v48, v52, s67, v98
	v_med3_f32 v15, v28, s67, v98
	v_cvt_pk_fp8_f32 v14, v48, v15 op_sel:[0,0,1]
	v_med3_f32 v4, v4, s67, v98
	v_med3_f32 v8, v8, s67, v98
	v_mov_b32_e32 v15, v77
	v_cvt_pk_fp8_f32 v15, v4, v8
	s_waitcnt vmcnt(1)
	v_mul_f32_e32 v16, 0x42800000, v32
	s_waitcnt vmcnt(0)
	v_mul_f32_e32 v0, 0x42800000, v0
	v_med3_f32 v4, v16, s67, v98
	v_med3_f32 v0, v0, s67, v98
	v_cvt_pk_fp8_f32 v15, v4, v0 op_sel:[0,0,1]
	v_mul_f32_e32 v0, 0x42800000, v37
	v_mul_f32_e32 v4, 0x42800000, v41
	v_med3_f32 v0, v0, s67, v98
	v_med3_f32 v4, v4, s67, v98
	v_cvt_pk_fp8_f32 v68, v0, v4
	v_mul_f32_e32 v8, 0x42800000, v57
	v_mul_f32_e32 v0, 0x42800000, v65
	v_med3_f32 v4, v8, s67, v98
	v_med3_f32 v0, v0, s67, v98
	v_cvt_pk_fp8_f32 v68, v4, v0 op_sel:[0,0,1]
	v_mul_f32_e32 v0, 0x42800000, v21
	v_mul_f32_e32 v4, 0x42800000, v25
	v_med3_f32 v0, v0, s67, v98
	v_med3_f32 v4, v4, s67, v98
	v_cvt_pk_fp8_f32 v69, v0, v4
	v_mul_f32_e32 v8, 0x42800000, v61
	v_mul_f32_e32 v0, 0x42800000, v45
	v_med3_f32 v4, v8, s67, v98
	v_med3_f32 v0, v0, s67, v98
	v_cvt_pk_fp8_f32 v69, v4, v0 op_sel:[0,0,1]
	v_mul_f32_e32 v0, 0x42800000, v17
	v_mul_f32_e32 v4, 0x42800000, v49
	v_med3_f32 v0, v0, s67, v98
	v_med3_f32 v4, v4, s67, v98
	v_cvt_pk_fp8_f32 v70, v0, v4
	v_mul_f32_e32 v8, 0x42800000, v53
	v_mul_f32_e32 v0, 0x42800000, v29
	v_med3_f32 v4, v8, s67, v98
	v_med3_f32 v0, v0, s67, v98
	v_cvt_pk_fp8_f32 v70, v4, v0 op_sel:[0,0,1]
	v_mul_f32_e32 v0, 0x42800000, v5
	v_mul_f32_e32 v4, 0x42800000, v9
	v_med3_f32 v0, v0, s67, v98
	v_med3_f32 v4, v4, s67, v98
	v_cvt_pk_fp8_f32 v71, v0, v4
	v_mul_f32_e32 v5, 0x42800000, v33
	v_mul_f32_e32 v0, 0x42800000, v1
	v_med3_f32 v1, v5, s67, v98
	v_med3_f32 v0, v0, s67, v98
	v_cvt_pk_fp8_f32 v71, v1, v0 op_sel:[0,0,1]
	v_mul_f32_e32 v0, 0x42800000, v38
	v_mul_f32_e32 v1, 0x42800000, v42
	v_med3_f32 v0, v0, s67, v98
	v_med3_f32 v1, v1, s67, v98
	v_cvt_pk_fp8_f32 v72, v0, v1
	v_mul_f32_e32 v4, 0x42800000, v58
	v_mul_f32_e32 v0, 0x42800000, v66
	v_med3_f32 v1, v4, s67, v98
	v_med3_f32 v0, v0, s67, v98
	v_cvt_pk_fp8_f32 v72, v1, v0 op_sel:[0,0,1]
	v_mul_f32_e32 v0, 0x42800000, v22
	v_mul_f32_e32 v1, 0x42800000, v26
	v_med3_f32 v0, v0, s67, v98
	v_med3_f32 v1, v1, s67, v98
	v_cvt_pk_fp8_f32 v73, v0, v1
	v_mul_f32_e32 v4, 0x42800000, v62
	v_mul_f32_e32 v0, 0x42800000, v46
	v_med3_f32 v1, v4, s67, v98
	v_med3_f32 v0, v0, s67, v98
	v_cvt_pk_fp8_f32 v73, v1, v0 op_sel:[0,0,1]
	v_mul_f32_e32 v0, 0x42800000, v18
	v_mul_f32_e32 v1, 0x42800000, v50
	v_med3_f32 v0, v0, s67, v98
	v_med3_f32 v1, v1, s67, v98
	v_cvt_pk_fp8_f32 v74, v0, v1
	v_mul_f32_e32 v4, 0x42800000, v54
	v_mul_f32_e32 v0, 0x42800000, v30
	v_med3_f32 v1, v4, s67, v98
	v_med3_f32 v0, v0, s67, v98
	v_cvt_pk_fp8_f32 v74, v1, v0 op_sel:[0,0,1]
	v_mul_f32_e32 v0, 0x42800000, v6
	v_mul_f32_e32 v1, 0x42800000, v10
	v_med3_f32 v0, v0, s67, v98
	v_med3_f32 v1, v1, s67, v98
	v_cvt_pk_fp8_f32 v75, v0, v1
	v_mul_f32_e32 v4, 0x42800000, v34
	v_mul_f32_e32 v0, 0x42800000, v2
	v_med3_f32 v1, v4, s67, v98
	v_med3_f32 v0, v0, s67, v98
	v_cvt_pk_fp8_f32 v75, v1, v0 op_sel:[0,0,1]
	v_mul_f32_e32 v0, 0x42800000, v39
	v_mul_f32_e32 v1, 0x42800000, v43
	v_med3_f32 v0, v0, s67, v98
	v_med3_f32 v1, v1, s67, v98
	v_mov_b32_e32 v4, v77
	v_cvt_pk_fp8_f32 v4, v0, v1
	v_mul_f32_e32 v2, 0x42800000, v59
	v_mul_f32_e32 v0, 0x42800000, v67
	v_med3_f32 v1, v2, s67, v98
	v_med3_f32 v0, v0, s67, v98
	v_cvt_pk_fp8_f32 v4, v1, v0 op_sel:[0,0,1]
	v_mul_f32_e32 v0, 0x42800000, v23
	v_mul_f32_e32 v1, 0x42800000, v27
	v_med3_f32 v0, v0, s67, v98
	v_med3_f32 v1, v1, s67, v98
	v_mov_b32_e32 v5, v77
	v_cvt_pk_fp8_f32 v5, v0, v1
	v_mul_f32_e32 v2, 0x42800000, v63
	v_mul_f32_e32 v0, 0x42800000, v47
	v_med3_f32 v1, v2, s67, v98
	v_med3_f32 v0, v0, s67, v98
	v_cvt_pk_fp8_f32 v5, v1, v0 op_sel:[0,0,1]
	v_mul_f32_e32 v0, 0x42800000, v19
	v_mul_f32_e32 v1, 0x42800000, v51
	v_med3_f32 v0, v0, s67, v98
	v_med3_f32 v1, v1, s67, v98
	v_mov_b32_e32 v6, v77
	v_cvt_pk_fp8_f32 v6, v0, v1
	v_mul_f32_e32 v2, 0x42800000, v55
	v_mul_f32_e32 v0, 0x42800000, v31
	v_med3_f32 v1, v2, s67, v98
	v_med3_f32 v0, v0, s67, v98
	v_cvt_pk_fp8_f32 v6, v1, v0 op_sel:[0,0,1]
	v_mul_f32_e32 v0, 0x42800000, v7
	v_mul_f32_e32 v1, 0x42800000, v11
	v_med3_f32 v0, v0, s67, v98
	v_med3_f32 v1, v1, s67, v98
	v_mov_b32_e32 v7, v77
	v_cvt_pk_fp8_f32 v7, v0, v1
	v_mul_f32_e32 v2, 0x42800000, v35
	v_mul_f32_e32 v0, 0x42800000, v3
	v_med3_f32 v1, v2, s67, v98
	v_med3_f32 v0, v0, s67, v98
	v_cvt_pk_fp8_f32 v7, v1, v0 op_sel:[0,0,1]
	ds_write_b128 v95, v[12:15] offset:40960
	ds_write_b128 v95, v[68:71] offset:41040
	ds_write_b128 v95, v[72:75] offset:41120
	ds_write_b128 v95, v[4:7] offset:41200
	s_waitcnt lgkmcnt(0)
	ds_read_b128 v[0:3], v96 offset:40960
	v_or_b32_e32 v4, s0, v83
	v_lshl_add_u64 v[8:9], s[10:11], 0, v[78:79]
	v_lshlrev_b32_e32 v4, 11, v4
	v_mov_b32_e32 v5, v77
	v_lshl_add_u64 v[10:11], v[8:9], 0, v[4:5]
	ds_read_b128 v[4:7], v96 offset:42240
	s_waitcnt lgkmcnt(1)
	global_store_dwordx4 v[10:11], v[0:3], off sc1
	s_nop 1
	v_or_b32_e32 v0, s0, v84
	v_lshlrev_b32_e32 v0, 11, v0
	v_mov_b32_e32 v1, v77
	v_lshl_add_u64 v[0:1], v[8:9], 0, v[0:1]
	s_waitcnt lgkmcnt(0)
	global_store_dwordx4 v[0:1], v[4:7], off sc1
	ds_read_b128 v[0:3], v96 offset:43520
	s_nop 0
	v_or_b32_e32 v4, s0, v85
	v_lshlrev_b32_e32 v4, 11, v4
	v_mov_b32_e32 v5, v77
	v_lshl_add_u64 v[10:11], v[8:9], 0, v[4:5]
	ds_read_b128 v[4:7], v96 offset:44800
	s_waitcnt lgkmcnt(1)
	global_store_dwordx4 v[10:11], v[0:3], off sc1
	s_nop 1
	v_or_b32_e32 v0, s0, v86
	v_lshlrev_b32_e32 v0, 11, v0
	v_mov_b32_e32 v1, v77
	v_lshl_add_u64 v[0:1], v[8:9], 0, v[0:1]
	s_waitcnt lgkmcnt(0)
	global_store_dwordx4 v[0:1], v[4:7], off sc1
	s_waitcnt lgkmcnt(0)

.LBB0_682:
	s_cmpk_gt_i32 s94, 0x93
	s_cbranch_scc1 .LBB0_684
	s_lshl_b32 s28, s3, 6
	s_mul_i32 s29, s2, 0x1280000
	v_or_b32_e32 v0, s28, v82
	s_mul_hi_i32 s21, s2, 0x1280000
	s_add_u32 s29, s55, s29
	v_mul_hi_i32_i24_e32 v1, 0x9500, v0
	v_mul_i32_i24_e32 v0, 0x9500, v0
	s_addc_u32 s30, s56, s21
	v_lshl_add_u64 v[0:1], s[4:5], 0, v[0:1]
	s_ashr_i32 s21, s20, 31
	v_lshl_add_u64 v[0:1], s[20:21], 2, v[0:1]
	v_mov_b32_e32 v81, v77
	v_lshl_add_u64 v[56:57], v[0:1], 0, v[80:81]
	v_add_co_u32_e32 v4, vcc, s78, v56
	global_load_dwordx4 v[0:3], v[56:57], off nt
	s_nop 0
	v_addc_co_u32_e32 v5, vcc, 0, v57, vcc
	global_load_dwordx4 v[16:19], v[4:5], off offset:1280 nt
	v_add_co_u32_e32 v4, vcc, s66, v56
	v_mov_b32_e32 v64, v77
	s_nop 0
	v_addc_co_u32_e32 v5, vcc, 0, v57, vcc
	global_load_dwordx4 v[20:23], v[4:5], off offset:2560 nt
	v_add_co_u32_e32 v4, vcc, s79, v56
	v_mov_b32_e32 v65, v77
	s_nop 0
	v_addc_co_u32_e32 v5, vcc, 0, v57, vcc
	global_load_dwordx4 v[44:47], v[4:5], off offset:3840 nt
	v_add_co_u32_e32 v4, vcc, s80, v56
	v_mov_b32_e32 v66, v77
	s_nop 0
	v_addc_co_u32_e32 v5, vcc, 0, v57, vcc
	v_add_co_u32_e32 v8, vcc, s81, v56
	global_load_dwordx4 v[4:7], v[4:5], off offset:1024 nt
	s_nop 0
	v_addc_co_u32_e32 v9, vcc, 0, v57, vcc
	global_load_dwordx4 v[24:27], v[8:9], off offset:2304 nt
	v_add_co_u32_e32 v8, vcc, s82, v56
	v_mov_b32_e32 v67, v77
	s_nop 0
	v_addc_co_u32_e32 v9, vcc, 0, v57, vcc
	global_load_dwordx4 v[28:31], v[8:9], off offset:3584 nt
	v_add_co_u32_e32 v8, vcc, s83, v56
	s_ashr_i32 s21, s28, 31
	s_nop 0
	v_addc_co_u32_e32 v9, vcc, 0, v57, vcc
	global_load_dwordx4 v[52:55], v[8:9], off offset:768 nt
	v_add_co_u32_e32 v8, vcc, s84, v56
	s_add_u32 s28, s29, s28
	s_nop 0
	v_addc_co_u32_e32 v9, vcc, 0, v57, vcc
	v_add_co_u32_e32 v12, vcc, s85, v56
	global_load_dwordx4 v[8:11], v[8:9], off offset:2048 nt
	s_nop 0
	v_addc_co_u32_e32 v13, vcc, 0, v57, vcc
	global_load_dwordx4 v[32:35], v[12:13], off offset:3328 nt
	v_add_co_u32_e32 v12, vcc, s86, v56
	s_addc_u32 s29, s30, s21
	s_nop 0
	v_addc_co_u32_e32 v13, vcc, 0, v57, vcc
	global_load_dwordx4 v[36:39], v[12:13], off offset:512 nt
	v_add_co_u32_e32 v12, vcc, s87, v56
	s_mov_b64 s[30:31], 0
	s_nop 0
	v_addc_co_u32_e32 v13, vcc, 0, v57, vcc
	global_load_dwordx4 v[60:63], v[12:13], off offset:1792 nt
	v_add_co_u32_e32 v12, vcc, s88, v56
	s_waitcnt vmcnt(11)
	v_mul_f32_e32 v0, 0x42800000, v0
	v_addc_co_u32_e32 v13, vcc, 0, v57, vcc
	v_add_co_u32_e32 v40, vcc, s89, v56
	global_load_dwordx4 v[12:15], v[12:13], off offset:3072 nt
	s_nop 0
	v_addc_co_u32_e32 v41, vcc, 0, v57, vcc
	global_load_dwordx4 v[40:43], v[40:41], off offset:256 nt
	v_add_co_u32_e32 v48, vcc, s90, v56
	s_waitcnt vmcnt(12)
	v_mul_f32_e32 v16, 0x42800000, v16
	v_addc_co_u32_e32 v49, vcc, 0, v57, vcc
	v_add_co_u32_e32 v56, vcc, s91, v56
	global_load_dwordx4 v[48:51], v[48:49], off offset:1536 nt
	s_nop 0
	v_addc_co_u32_e32 v57, vcc, 0, v57, vcc
	global_load_dwordx4 v[56:59], v[56:57], off offset:2816 nt
	v_med3_f32 v0, v0, s67, v98
	v_med3_f32 v16, v16, s67, v98
	v_cvt_pk_fp8_f32 v64, v0, v16
	s_waitcnt vmcnt(11)
	v_mul_f32_e32 v0, 0x42800000, v4
	v_med3_f32 v0, v0, s67, v98
	v_mul_f32_e32 v20, 0x42800000, v20
	s_waitcnt vmcnt(10)
	v_mul_f32_e32 v4, 0x42800000, v24
	v_med3_f32 v4, v4, s67, v98
	v_mul_f32_e32 v44, 0x42800000, v44
	v_cvt_pk_fp8_f32 v65, v0, v4
	v_med3_f32 v20, v20, s67, v98
	v_med3_f32 v44, v44, s67, v98
	v_cvt_pk_fp8_f32 v64, v20, v44 op_sel:[0,0,1]
	s_waitcnt vmcnt(9)
	v_mul_f32_e32 v16, 0x42800000, v28
	v_med3_f32 v16, v16, s67, v98
	s_waitcnt vmcnt(8)
	v_mul_f32_e32 v20, 0x42800000, v52
	v_med3_f32 v20, v20, s67, v98
	v_cvt_pk_fp8_f32 v65, v16, v20 op_sel:[0,0,1]
	s_waitcnt vmcnt(7)
	v_mul_f32_e32 v0, 0x42800000, v8
	v_med3_f32 v0, v0, s67, v98
	s_waitcnt vmcnt(6)
	v_mul_f32_e32 v4, 0x42800000, v32
	v_med3_f32 v4, v4, s67, v98
	v_cvt_pk_fp8_f32 v66, v0, v4
	s_waitcnt vmcnt(5)
	v_mul_f32_e32 v8, 0x42800000, v36
	v_med3_f32 v8, v8, s67, v98
	s_waitcnt vmcnt(4)
	v_mul_f32_e32 v16, 0x42800000, v60
	v_med3_f32 v16, v16, s67, v98
	v_cvt_pk_fp8_f32 v66, v8, v16 op_sel:[0,0,1]
	s_waitcnt vmcnt(3)
	v_mul_f32_e32 v0, 0x42800000, v12
	v_med3_f32 v0, v0, s67, v98
	s_waitcnt vmcnt(2)
	v_mul_f32_e32 v4, 0x42800000, v40
	v_med3_f32 v4, v4, s67, v98
	v_cvt_pk_fp8_f32 v67, v0, v4
	v_mul_f32_e32 v0, 0x42800000, v1
	v_mul_f32_e32 v1, 0x42800000, v17
	v_med3_f32 v0, v0, s67, v98
	v_med3_f32 v1, v1, s67, v98
	v_mul_f32_e32 v4, 0x42800000, v21
	s_waitcnt vmcnt(1)
	v_mul_f32_e32 v8, 0x42800000, v48
	v_med3_f32 v8, v8, s67, v98
	v_med3_f32 v4, v4, s67, v98
	s_waitcnt vmcnt(0)
	v_mul_f32_e32 v12, 0x42800000, v56
	v_med3_f32 v12, v12, s67, v98
	v_cvt_pk_fp8_f32 v67, v8, v12 op_sel:[0,0,1]
	v_mul_f32_e32 v8, 0x42800000, v45
	v_med3_f32 v8, v8, s67, v98
	ds_write_b128 v95, v[64:67] offset:40960
	v_mov_b32_e32 v64, v77
	v_cvt_pk_fp8_f32 v64, v0, v1
	v_mul_f32_e32 v0, 0x42800000, v5
	v_mul_f32_e32 v1, 0x42800000, v25
	v_med3_f32 v0, v0, s67, v98
	v_med3_f32 v1, v1, s67, v98
	v_mov_b32_e32 v65, v77
	v_cvt_pk_fp8_f32 v65, v0, v1
	v_mul_f32_e32 v0, 0x42800000, v9
	v_mul_f32_e32 v1, 0x42800000, v33
	v_med3_f32 v0, v0, s67, v98
	v_med3_f32 v1, v1, s67, v98
	v_mov_b32_e32 v66, v77
	v_cvt_pk_fp8_f32 v64, v4, v8 op_sel:[0,0,1]
	v_mul_f32_e32 v4, 0x42800000, v29
	v_mul_f32_e32 v5, 0x42800000, v53
	v_cvt_pk_fp8_f32 v66, v0, v1
	v_mul_f32_e32 v0, 0x42800000, v13
	v_mul_f32_e32 v1, 0x42800000, v41
	v_med3_f32 v4, v4, s67, v98
	v_med3_f32 v5, v5, s67, v98
	v_med3_f32 v0, v0, s67, v98
	v_med3_f32 v1, v1, s67, v98
	v_mov_b32_e32 v67, v77
	v_cvt_pk_fp8_f32 v65, v4, v5 op_sel:[0,0,1]
	v_mul_f32_e32 v4, 0x42800000, v37
	v_mul_f32_e32 v5, 0x42800000, v61
	v_cvt_pk_fp8_f32 v67, v0, v1
	v_med3_f32 v4, v4, s67, v98
	v_med3_f32 v5, v5, s67, v98
	v_cvt_pk_fp8_f32 v66, v4, v5 op_sel:[0,0,1]
	v_mul_f32_e32 v4, 0x42800000, v49
	v_mul_f32_e32 v5, 0x42800000, v57
	v_med3_f32 v4, v4, s67, v98
	v_med3_f32 v5, v5, s67, v98
	v_cvt_pk_fp8_f32 v67, v4, v5 op_sel:[0,0,1]
	v_mul_f32_e32 v0, 0x42800000, v2
	v_mul_f32_e32 v1, 0x42800000, v18
	v_med3_f32 v0, v0, s67, v98
	ds_write_b128 v95, v[64:67] offset:41040
	v_med3_f32 v1, v1, s67, v98
	v_mov_b32_e32 v64, v77
	v_cvt_pk_fp8_f32 v64, v0, v1
	v_mul_f32_e32 v0, 0x42800000, v6
	v_mul_f32_e32 v1, 0x42800000, v26
	v_med3_f32 v0, v0, s67, v98
	v_med3_f32 v1, v1, s67, v98
	v_mov_b32_e32 v65, v77
	v_mul_f32_e32 v2, 0x42800000, v22
	v_mul_f32_e32 v4, 0x42800000, v46
	v_cvt_pk_fp8_f32 v65, v0, v1
	v_mul_f32_e32 v0, 0x42800000, v10
	v_mul_f32_e32 v1, 0x42800000, v34
	v_med3_f32 v2, v2, s67, v98
	v_med3_f32 v4, v4, s67, v98
	v_med3_f32 v0, v0, s67, v98
	v_med3_f32 v1, v1, s67, v98
	v_mov_b32_e32 v66, v77
	v_cvt_pk_fp8_f32 v64, v2, v4 op_sel:[0,0,1]
	v_mul_f32_e32 v2, 0x42800000, v30
	v_mul_f32_e32 v4, 0x42800000, v54
	v_cvt_pk_fp8_f32 v66, v0, v1
	v_mul_f32_e32 v0, 0x42800000, v14
	v_mul_f32_e32 v1, 0x42800000, v42
	v_med3_f32 v2, v2, s67, v98
	v_med3_f32 v4, v4, s67, v98
	v_med3_f32 v0, v0, s67, v98
	v_med3_f32 v1, v1, s67, v98
	v_mov_b32_e32 v67, v77
	v_cvt_pk_fp8_f32 v65, v2, v4 op_sel:[0,0,1]
	v_mul_f32_e32 v2, 0x42800000, v38
	v_mul_f32_e32 v4, 0x42800000, v62
	v_cvt_pk_fp8_f32 v67, v0, v1
	v_med3_f32 v2, v2, s67, v98
	v_med3_f32 v4, v4, s67, v98
	v_cvt_pk_fp8_f32 v66, v2, v4 op_sel:[0,0,1]
	v_mul_f32_e32 v2, 0x42800000, v50
	v_mul_f32_e32 v4, 0x42800000, v58
	v_med3_f32 v2, v2, s67, v98
	v_med3_f32 v4, v4, s67, v98
	v_mul_f32_e32 v0, 0x42800000, v3
	v_mul_f32_e32 v1, 0x42800000, v19
	v_cvt_pk_fp8_f32 v67, v2, v4 op_sel:[0,0,1]
	v_med3_f32 v4, v0, s67, v98
	v_med3_f32 v1, v1, s67, v98
	v_mov_b32_e32 v0, v77
	v_cvt_pk_fp8_f32 v0, v4, v1
	v_mul_f32_e32 v2, 0x42800000, v23
	v_mul_f32_e32 v3, 0x42800000, v47
	v_med3_f32 v2, v2, s67, v98
	v_med3_f32 v3, v3, s67, v98
	v_cvt_pk_fp8_f32 v0, v2, v3 op_sel:[0,0,1]
	v_mul_f32_e32 v1, 0x42800000, v7
	v_mul_f32_e32 v2, 0x42800000, v27
	v_med3_f32 v5, v1, s67, v98
	v_med3_f32 v2, v2, s67, v98
	v_mov_b32_e32 v1, v77
	v_cvt_pk_fp8_f32 v1, v5, v2
	v_mul_f32_e32 v3, 0x42800000, v31
	v_mul_f32_e32 v4, 0x42800000, v55
	v_med3_f32 v3, v3, s67, v98
	v_med3_f32 v4, v4, s67, v98
	v_cvt_pk_fp8_f32 v1, v3, v4 op_sel:[0,0,1]
	v_mul_f32_e32 v2, 0x42800000, v11
	v_mul_f32_e32 v3, 0x42800000, v35
	v_med3_f32 v6, v2, s67, v98
	v_med3_f32 v3, v3, s67, v98
	v_mov_b32_e32 v2, v77
	v_cvt_pk_fp8_f32 v2, v6, v3
	v_mul_f32_e32 v4, 0x42800000, v39
	v_mul_f32_e32 v5, 0x42800000, v63
	v_med3_f32 v4, v4, s67, v98
	v_med3_f32 v5, v5, s67, v98
	v_cvt_pk_fp8_f32 v2, v4, v5 op_sel:[0,0,1]
	v_mul_f32_e32 v3, 0x42800000, v15
	v_mul_f32_e32 v4, 0x42800000, v43
	v_med3_f32 v7, v3, s67, v98
	v_med3_f32 v4, v4, s67, v98
	v_mov_b32_e32 v3, v77
	v_cvt_pk_fp8_f32 v3, v7, v4
	v_mul_f32_e32 v5, 0x42800000, v51
	v_mul_f32_e32 v6, 0x42800000, v59
	v_med3_f32 v5, v5, s67, v98
	v_med3_f32 v6, v6, s67, v98
	v_cvt_pk_fp8_f32 v3, v5, v6 op_sel:[0,0,1]
	ds_write_b128 v95, v[64:67] offset:41120
	v_or_b32_e32 v6, s13, v83
	v_ashrrev_i32_e32 v7, 31, v6
	ds_write_b128 v95, v[0:3] offset:41200
	s_waitcnt lgkmcnt(0)
	ds_read_b128 v[0:3], v96 offset:40960
	v_lshl_add_u64 v[4:5], s[28:29], 0, v[78:79]
	v_lshlrev_b64 v[6:7], 11, v[6:7]
	v_lshl_add_u64 v[6:7], v[4:5], 0, v[6:7]
	s_waitcnt lgkmcnt(0)
	global_store_dwordx4 v[6:7], v[0:3], off sc1
	ds_read_b128 v[0:3], v96 offset:42240
	v_or_b32_e32 v6, s13, v84
	v_ashrrev_i32_e32 v7, 31, v6
	v_lshlrev_b64 v[6:7], 11, v[6:7]
	v_lshl_add_u64 v[6:7], v[4:5], 0, v[6:7]
	s_waitcnt lgkmcnt(0)
	global_store_dwordx4 v[6:7], v[0:3], off sc1
	ds_read_b128 v[0:3], v96 offset:43520
	v_or_b32_e32 v6, s13, v85
	v_ashrrev_i32_e32 v7, 31, v6
	v_lshlrev_b64 v[6:7], 11, v[6:7]
	v_lshl_add_u64 v[6:7], v[4:5], 0, v[6:7]
	s_waitcnt lgkmcnt(0)
	global_store_dwordx4 v[6:7], v[0:3], off sc1
	ds_read_b128 v[0:3], v96 offset:44800
	v_or_b32_e32 v6, s13, v86
	v_ashrrev_i32_e32 v7, 31, v6
	v_lshlrev_b64 v[6:7], 11, v[6:7]
	v_lshl_add_u64 v[4:5], v[4:5], 0, v[6:7]
	s_waitcnt lgkmcnt(0)
	global_store_dwordx4 v[4:5], v[0:3], off sc1
	s_waitcnt lgkmcnt(0)
.LBB0_684:
	s_and_b64 vcc, exec, s[30:31]
	s_cbranch_vccz .LBB0_646
	s_xor_b64 s[30:31], s[22:23], -1
	s_lshl_b32 s22, s3, 6
	s_mov_b64 s[28:29], -1
	s_and_b64 vcc, exec, s[30:31]
	s_cbranch_vccz .LBB0_715
	s_andn2_b64 vcc, exec, s[26:27]
	s_cbranch_vccnz .LBB0_689
	s_ashr_i32 s3, s2, 31
	s_lshl_b64 s[26:27], s[2:3], 22
	v_or_b32_e32 v0, s22, v82
	s_add_u32 s3, s57, s26
	v_mul_hi_i32_i24_e32 v1, s16, v0
	v_mul_i32_i24_e32 v0, s16, v0
	s_addc_u32 s23, s58, s27
	v_lshl_add_u64 v[0:1], v[0:1], 2, s[4:5]
	s_ashr_i32 s21, s20, 31
	v_lshl_add_u64 v[0:1], s[20:21], 2, v[0:1]
	v_mov_b32_e32 v81, v77
	v_lshl_add_u64 v[0:1], v[0:1], 0, v[80:81]
	s_lshl_b64 s[26:27], s[16:17], 2
	global_load_dwordx4 v[56:59], v[0:1], off nt
	v_lshl_add_u64 v[0:1], v[0:1], 0, s[26:27]
	global_load_dwordx4 v[60:63], v[0:1], off nt
	v_lshl_add_u64 v[0:1], v[0:1], 0, s[26:27]
	global_load_dwordx4 v[64:67], v[0:1], off nt
	v_lshl_add_u64 v[0:1], v[0:1], 0, s[26:27]
	global_load_dwordx4 v[52:55], v[0:1], off nt
	v_lshl_add_u64 v[0:1], v[0:1], 0, s[26:27]
	global_load_dwordx4 v[40:43], v[0:1], off nt
	v_lshl_add_u64 v[0:1], v[0:1], 0, s[26:27]
	global_load_dwordx4 v[44:47], v[0:1], off nt
	v_lshl_add_u64 v[0:1], v[0:1], 0, s[26:27]
	global_load_dwordx4 v[48:51], v[0:1], off nt
	v_lshl_add_u64 v[0:1], v[0:1], 0, s[26:27]
	global_load_dwordx4 v[36:39], v[0:1], off nt
	v_lshl_add_u64 v[0:1], v[0:1], 0, s[26:27]
	global_load_dwordx4 v[24:27], v[0:1], off nt
	v_lshl_add_u64 v[0:1], v[0:1], 0, s[26:27]
	global_load_dwordx4 v[28:31], v[0:1], off nt
	v_lshl_add_u64 v[0:1], v[0:1], 0, s[26:27]
	global_load_dwordx4 v[32:35], v[0:1], off nt
	v_lshl_add_u64 v[0:1], v[0:1], 0, s[26:27]
	global_load_dwordx4 v[20:23], v[0:1], off nt
	v_lshl_add_u64 v[0:1], v[0:1], 0, s[26:27]
	global_load_dwordx4 v[4:7], v[0:1], off nt
	v_lshl_add_u64 v[0:1], v[0:1], 0, s[26:27]
	global_load_dwordx4 v[8:11], v[0:1], off nt
	v_lshl_add_u64 v[0:1], v[0:1], 0, s[26:27]
	global_load_dwordx4 v[12:15], v[0:1], off nt
	v_lshl_add_u64 v[0:1], v[0:1], 0, s[26:27]
	global_load_dwordx4 v[0:3], v[0:1], off nt
	v_mov_b32_e32 v19, v77
	v_mov_b32_e32 v69, v77
	v_mov_b32_e32 v70, v77
	v_mov_b32_e32 v71, v77
	v_mov_b32_e32 v72, v77
	v_mov_b32_e32 v73, v77
	v_mov_b32_e32 v74, v77
	v_mov_b32_e32 v75, v77
	v_mov_b32_e32 v16, v77
	v_mov_b32_e32 v17, v77
	v_mov_b32_e32 v18, v77
	v_mov_b32_e32 v68, v77
	s_ashr_i32 s21, s22, 31
	s_add_u32 s26, s3, s22
	s_addc_u32 s27, s23, s21
	s_add_i32 s3, s92, 0x9988
	s_cmpk_lt_u32 s3, 0xf97f
	s_waitcnt vmcnt(15)
	v_mul_f32_e32 v56, 0x42800000, v56
	v_mul_f32_e32 v57, 0x42800000, v57
	s_waitcnt vmcnt(14)
	v_mul_f32_e32 v60, 0x42800000, v60
	v_med3_f32 v56, v56, s67, v98
	v_mul_f32_e32 v61, 0x42800000, v61
	v_med3_f32 v60, v60, s67, v98
	v_med3_f32 v57, v57, s67, v98
	v_med3_f32 v61, v61, s67, v98
	s_waitcnt vmcnt(11)
	v_mul_f32_e32 v41, 0x42800000, v41
	v_med3_f32 v41, v41, s67, v98
	s_waitcnt vmcnt(10)
	v_mul_f32_e32 v45, 0x42800000, v45
	v_med3_f32 v45, v45, s67, v98
	v_cvt_pk_fp8_f32 v69, v41, v45
	s_waitcnt vmcnt(9)
	v_mul_f32_e32 v49, 0x42800000, v49
	v_mul_f32_e32 v40, 0x42800000, v40
	v_mul_f32_e32 v44, 0x42800000, v44
	s_waitcnt vmcnt(7)
	v_mul_f32_e32 v24, 0x42800000, v24
	v_med3_f32 v40, v40, s67, v98
	s_waitcnt vmcnt(6)
	v_mul_f32_e32 v28, 0x42800000, v28
	v_med3_f32 v44, v44, s67, v98
	v_med3_f32 v24, v24, s67, v98
	v_med3_f32 v28, v28, s67, v98
	v_cvt_pk_fp8_f32 v16, v56, v60
	v_cvt_pk_fp8_f32 v17, v40, v44
	s_waitcnt vmcnt(3)
	v_mul_f32_e32 v4, 0x42800000, v4
	v_med3_f32 v4, v4, s67, v98
	s_waitcnt vmcnt(2)
	v_mul_f32_e32 v8, 0x42800000, v8
	v_med3_f32 v8, v8, s67, v98
	v_cvt_pk_fp8_f32 v19, v4, v8
	s_waitcnt vmcnt(1)
	v_mul_f32_e32 v12, 0x42800000, v12
	s_waitcnt vmcnt(0)
	v_mul_f32_e32 v0, 0x42800000, v0
	v_med3_f32 v4, v12, s67, v98
	v_med3_f32 v0, v0, s67, v98
	v_cvt_pk_fp8_f32 v19, v4, v0 op_sel:[0,0,1]
	v_mul_f32_e32 v0, 0x42800000, v37
	v_med3_f32 v4, v49, s67, v98
	v_med3_f32 v0, v0, s67, v98
	v_cvt_pk_fp8_f32 v69, v4, v0 op_sel:[0,0,1]
	v_mul_f32_e32 v0, 0x42800000, v25
	v_mul_f32_e32 v4, 0x42800000, v29
	v_med3_f32 v0, v0, s67, v98
	v_med3_f32 v4, v4, s67, v98
	v_cvt_pk_fp8_f32 v70, v0, v4
	v_mul_f32_e32 v8, 0x42800000, v33
	v_mul_f32_e32 v0, 0x42800000, v21
	v_med3_f32 v4, v8, s67, v98
	v_med3_f32 v0, v0, s67, v98
	v_cvt_pk_fp8_f32 v70, v4, v0 op_sel:[0,0,1]
	v_mul_f32_e32 v0, 0x42800000, v5
	v_mul_f32_e32 v4, 0x42800000, v9
	v_med3_f32 v0, v0, s67, v98
	v_med3_f32 v4, v4, s67, v98
	v_cvt_pk_fp8_f32 v71, v0, v4
	v_mul_f32_e32 v5, 0x42800000, v13
	v_mul_f32_e32 v0, 0x42800000, v1
	v_med3_f32 v1, v5, s67, v98
	v_med3_f32 v0, v0, s67, v98
	v_cvt_pk_fp8_f32 v71, v1, v0 op_sel:[0,0,1]
	v_mul_f32_e32 v0, 0x42800000, v58
	v_mul_f32_e32 v1, 0x42800000, v62
	v_med3_f32 v0, v0, s67, v98
	v_med3_f32 v1, v1, s67, v98
	v_cvt_pk_fp8_f32 v72, v0, v1
	v_mul_f32_e32 v4, 0x42800000, v66
	v_mul_f32_e32 v0, 0x42800000, v54
	v_med3_f32 v1, v4, s67, v98
	v_med3_f32 v0, v0, s67, v98
	v_cvt_pk_fp8_f32 v72, v1, v0 op_sel:[0,0,1]
	v_mul_f32_e32 v0, 0x42800000, v42
	v_mul_f32_e32 v1, 0x42800000, v46
	v_med3_f32 v0, v0, s67, v98
	v_med3_f32 v1, v1, s67, v98
	v_cvt_pk_fp8_f32 v73, v0, v1
	v_mul_f32_e32 v4, 0x42800000, v50
	v_mul_f32_e32 v0, 0x42800000, v38
	v_med3_f32 v1, v4, s67, v98
	v_med3_f32 v0, v0, s67, v98
	v_cvt_pk_fp8_f32 v73, v1, v0 op_sel:[0,0,1]
	v_mul_f32_e32 v0, 0x42800000, v26
	v_mul_f32_e32 v1, 0x42800000, v30
	v_med3_f32 v0, v0, s67, v98
	v_med3_f32 v1, v1, s67, v98
	v_cvt_pk_fp8_f32 v74, v0, v1
	v_mul_f32_e32 v4, 0x42800000, v34
	v_mul_f32_e32 v0, 0x42800000, v22
	v_med3_f32 v1, v4, s67, v98
	v_med3_f32 v0, v0, s67, v98
	v_cvt_pk_fp8_f32 v74, v1, v0 op_sel:[0,0,1]
	v_mul_f32_e32 v0, 0x42800000, v6
	v_mul_f32_e32 v1, 0x42800000, v10
	v_med3_f32 v0, v0, s67, v98
	v_med3_f32 v1, v1, s67, v98
	v_cvt_pk_fp8_f32 v75, v0, v1
	v_mul_f32_e32 v4, 0x42800000, v14
	v_mul_f32_e32 v0, 0x42800000, v2
	v_med3_f32 v1, v4, s67, v98
	v_med3_f32 v0, v0, s67, v98
	v_cvt_pk_fp8_f32 v75, v1, v0 op_sel:[0,0,1]
	v_mul_f32_e32 v0, 0x42800000, v59
	v_mul_f32_e32 v1, 0x42800000, v63
	v_med3_f32 v0, v0, s67, v98
	v_med3_f32 v1, v1, s67, v98
	v_mov_b32_e32 v4, v77
	v_cvt_pk_fp8_f32 v4, v0, v1
	v_mul_f32_e32 v2, 0x42800000, v67
	v_mul_f32_e32 v0, 0x42800000, v55
	v_med3_f32 v1, v2, s67, v98
	v_med3_f32 v0, v0, s67, v98
	v_cvt_pk_fp8_f32 v4, v1, v0 op_sel:[0,0,1]
	v_mul_f32_e32 v0, 0x42800000, v43
	v_mul_f32_e32 v1, 0x42800000, v47
	v_med3_f32 v0, v0, s67, v98
	v_med3_f32 v1, v1, s67, v98
	v_mov_b32_e32 v5, v77
	v_cvt_pk_fp8_f32 v5, v0, v1
	v_mul_f32_e32 v2, 0x42800000, v51
	v_mul_f32_e32 v0, 0x42800000, v39
	v_med3_f32 v1, v2, s67, v98
	v_med3_f32 v0, v0, s67, v98
	v_cvt_pk_fp8_f32 v5, v1, v0 op_sel:[0,0,1]
	v_mul_f32_e32 v0, 0x42800000, v27
	v_mul_f32_e32 v1, 0x42800000, v31
	v_med3_f32 v0, v0, s67, v98
	v_med3_f32 v1, v1, s67, v98
	v_mov_b32_e32 v6, v77
	v_cvt_pk_fp8_f32 v6, v0, v1
	v_mul_f32_e32 v2, 0x42800000, v35
	v_mul_f32_e32 v0, 0x42800000, v23
	v_cvt_pk_fp8_f32 v18, v24, v28
	v_med3_f32 v1, v2, s67, v98
	v_med3_f32 v0, v0, s67, v98
	v_cvt_pk_fp8_f32 v68, v57, v61
	v_cvt_pk_fp8_f32 v6, v1, v0 op_sel:[0,0,1]
	v_mul_f32_e32 v0, 0x42800000, v7
	v_mul_f32_e32 v1, 0x42800000, v11
	v_mul_f32_e32 v64, 0x42800000, v64
	v_mul_f32_e32 v52, 0x42800000, v52
	v_mul_f32_e32 v48, 0x42800000, v48
	v_mul_f32_e32 v36, 0x42800000, v36
	v_mul_f32_e32 v32, 0x42800000, v32
	v_mul_f32_e32 v20, 0x42800000, v20
	v_med3_f32 v0, v0, s67, v98
	v_med3_f32 v1, v1, s67, v98
	v_mov_b32_e32 v7, v77
	v_mul_f32_e32 v65, 0x42800000, v65
	v_med3_f32 v64, v64, s67, v98
	v_mul_f32_e32 v53, 0x42800000, v53
	v_med3_f32 v52, v52, s67, v98
	v_med3_f32 v48, v48, s67, v98
	v_med3_f32 v36, v36, s67, v98
	v_med3_f32 v32, v32, s67, v98
	v_med3_f32 v20, v20, s67, v98
	v_cvt_pk_fp8_f32 v7, v0, v1
	v_med3_f32 v56, v65, s67, v98
	v_med3_f32 v53, v53, s67, v98
	v_cvt_pk_fp8_f32 v16, v64, v52 op_sel:[0,0,1]
	v_cvt_pk_fp8_f32 v17, v48, v36 op_sel:[0,0,1]
	v_cvt_pk_fp8_f32 v18, v32, v20 op_sel:[0,0,1]
	v_cvt_pk_fp8_f32 v68, v56, v53 op_sel:[0,0,1]
	v_mul_f32_e32 v2, 0x42800000, v15
	v_mul_f32_e32 v0, 0x42800000, v3
	v_med3_f32 v1, v2, s67, v98
	v_med3_f32 v0, v0, s67, v98
	v_cvt_pk_fp8_f32 v7, v1, v0 op_sel:[0,0,1]
	ds_write_b128 v95, v[16:19] offset:40960
	ds_write_b128 v95, v[68:71] offset:41040
	ds_write_b128 v95, v[72:75] offset:41120
	ds_write_b128 v95, v[4:7] offset:41200
	s_waitcnt lgkmcnt(0)
	ds_read_b128 v[0:3], v96 offset:40960
	v_or_b32_e32 v4, s13, v83
	v_ashrrev_i32_e32 v5, 31, v4
	v_lshl_add_u64 v[8:9], s[26:27], 0, v[78:79]
	v_lshlrev_b64 v[4:5], 11, v[4:5]
	v_lshl_add_u64 v[10:11], v[8:9], 0, v[4:5]
	ds_read_b128 v[4:7], v96 offset:42240
	s_waitcnt lgkmcnt(1)
	global_store_dwordx4 v[10:11], v[0:3], off sc1
	s_cselect_b64 s[26:27], -1, 0
	s_nop 0
	v_or_b32_e32 v0, s13, v84
	v_ashrrev_i32_e32 v1, 31, v0
	v_lshlrev_b64 v[0:1], 11, v[0:1]
	v_lshl_add_u64 v[0:1], v[8:9], 0, v[0:1]
	s_waitcnt lgkmcnt(0)
	global_store_dwordx4 v[0:1], v[4:7], off sc1
	ds_read_b128 v[0:3], v96 offset:43520
	s_nop 0
	v_or_b32_e32 v4, s13, v85
	v_ashrrev_i32_e32 v5, 31, v4
	v_lshlrev_b64 v[4:5], 11, v[4:5]
	v_lshl_add_u64 v[10:11], v[8:9], 0, v[4:5]
	ds_read_b128 v[4:7], v96 offset:44800
	s_waitcnt lgkmcnt(1)
	global_store_dwordx4 v[10:11], v[0:3], off sc1
	s_nop 1
	v_or_b32_e32 v0, s13, v86
	v_ashrrev_i32_e32 v1, 31, v0
	v_lshlrev_b64 v[0:1], 11, v[0:1]
	v_lshl_add_u64 v[0:1], v[8:9], 0, v[0:1]
	s_waitcnt lgkmcnt(0)
	global_store_dwordx4 v[0:1], v[4:7], off sc1
	s_waitcnt lgkmcnt(0)
	s_andn2_b64 vcc, exec, s[26:27]
	s_cbranch_vccz .LBB0_690
	s_branch .LBB0_714

.LBB0_690:
	s_andn2_b64 vcc, exec, s[24:25]
	s_cbranch_vccnz .LBB0_692
	s_ashr_i32 s3, s2, 31
	s_lshl_b64 s[24:25], s[2:3], 22
	s_add_u32 s3, s59, s24
	s_addc_u32 s21, s60, s25
	v_or_b32_e32 v0, s22, v82
	s_add_u32 s3, s3, s18
	v_mul_hi_i32_i24_e32 v1, s16, v0
	v_mul_i32_i24_e32 v0, s16, v0
	s_addc_u32 s23, s21, s19
	v_lshl_add_u64 v[0:1], v[0:1], 2, s[4:5]
	s_ashr_i32 s21, s20, 31
	v_lshl_add_u64 v[0:1], s[20:21], 2, v[0:1]
	v_mov_b32_e32 v81, v77
	v_lshl_add_u64 v[0:1], v[0:1], 0, v[80:81]
	s_lshl_b64 s[24:25], s[16:17], 2
	global_load_dwordx4 v[56:59], v[0:1], off nt
	v_lshl_add_u64 v[0:1], v[0:1], 0, s[24:25]
	global_load_dwordx4 v[60:63], v[0:1], off nt
	v_lshl_add_u64 v[0:1], v[0:1], 0, s[24:25]
	global_load_dwordx4 v[64:67], v[0:1], off nt
	v_lshl_add_u64 v[0:1], v[0:1], 0, s[24:25]
	global_load_dwordx4 v[52:55], v[0:1], off nt
	v_lshl_add_u64 v[0:1], v[0:1], 0, s[24:25]
	global_load_dwordx4 v[40:43], v[0:1], off nt
	v_lshl_add_u64 v[0:1], v[0:1], 0, s[24:25]
	global_load_dwordx4 v[44:47], v[0:1], off nt
	v_lshl_add_u64 v[0:1], v[0:1], 0, s[24:25]
	global_load_dwordx4 v[48:51], v[0:1], off nt
	v_lshl_add_u64 v[0:1], v[0:1], 0, s[24:25]
	global_load_dwordx4 v[36:39], v[0:1], off nt
	v_lshl_add_u64 v[0:1], v[0:1], 0, s[24:25]
	global_load_dwordx4 v[24:27], v[0:1], off nt
	v_lshl_add_u64 v[0:1], v[0:1], 0, s[24:25]
	global_load_dwordx4 v[28:31], v[0:1], off nt
	v_lshl_add_u64 v[0:1], v[0:1], 0, s[24:25]
	global_load_dwordx4 v[32:35], v[0:1], off nt
	v_lshl_add_u64 v[0:1], v[0:1], 0, s[24:25]
	global_load_dwordx4 v[20:23], v[0:1], off nt
	v_lshl_add_u64 v[0:1], v[0:1], 0, s[24:25]
	global_load_dwordx4 v[4:7], v[0:1], off nt
	v_lshl_add_u64 v[0:1], v[0:1], 0, s[24:25]
	global_load_dwordx4 v[12:15], v[0:1], off nt
	v_lshl_add_u64 v[0:1], v[0:1], 0, s[24:25]
	global_load_dwordx4 v[16:19], v[0:1], off nt
	v_lshl_add_u64 v[0:1], v[0:1], 0, s[24:25]
	global_load_dwordx4 v[0:3], v[0:1], off nt
	v_mov_b32_e32 v11, v77
	v_mov_b32_e32 v69, v77
	v_mov_b32_e32 v70, v77
	v_mov_b32_e32 v71, v77
	v_mov_b32_e32 v72, v77
	v_mov_b32_e32 v73, v77
	v_mov_b32_e32 v74, v77
	v_mov_b32_e32 v75, v77
	v_mov_b32_e32 v8, v77
	v_mov_b32_e32 v9, v77
	v_mov_b32_e32 v10, v77
	v_mov_b32_e32 v68, v77
	s_ashr_i32 s21, s22, 31
	s_add_u32 s24, s3, s22
	s_addc_u32 s25, s23, s21
	s_add_i32 s92, s92, 0x9988
	s_cmpk_lt_u32 s92, 0xf97f
	s_waitcnt vmcnt(15)
	v_mul_f32_e32 v56, 0x42800000, v56
	v_mul_f32_e32 v57, 0x42800000, v57
	s_waitcnt vmcnt(14)
	v_mul_f32_e32 v60, 0x42800000, v60
	v_med3_f32 v56, v56, s67, v98
	v_mul_f32_e32 v61, 0x42800000, v61
	v_med3_f32 v60, v60, s67, v98
	v_med3_f32 v57, v57, s67, v98
	v_med3_f32 v61, v61, s67, v98
	s_waitcnt vmcnt(11)
	v_mul_f32_e32 v41, 0x42800000, v41
	v_med3_f32 v41, v41, s67, v98
	s_waitcnt vmcnt(10)
	v_mul_f32_e32 v45, 0x42800000, v45
	v_med3_f32 v45, v45, s67, v98
	v_cvt_pk_fp8_f32 v69, v41, v45
	s_waitcnt vmcnt(9)
	v_mul_f32_e32 v49, 0x42800000, v49
	v_mul_f32_e32 v40, 0x42800000, v40
	v_mul_f32_e32 v44, 0x42800000, v44
	s_waitcnt vmcnt(7)
	v_mul_f32_e32 v24, 0x42800000, v24
	v_med3_f32 v40, v40, s67, v98
	s_waitcnt vmcnt(6)
	v_mul_f32_e32 v28, 0x42800000, v28
	v_med3_f32 v44, v44, s67, v98
	v_med3_f32 v24, v24, s67, v98
	v_med3_f32 v28, v28, s67, v98
	v_cvt_pk_fp8_f32 v8, v56, v60
	v_cvt_pk_fp8_f32 v9, v40, v44
	s_waitcnt vmcnt(3)
	v_mul_f32_e32 v4, 0x42800000, v4
	v_med3_f32 v4, v4, s67, v98
	s_waitcnt vmcnt(2)
	v_mul_f32_e32 v12, 0x42800000, v12
	v_med3_f32 v12, v12, s67, v98
	v_cvt_pk_fp8_f32 v11, v4, v12
	s_waitcnt vmcnt(1)
	v_mul_f32_e32 v16, 0x42800000, v16
	s_waitcnt vmcnt(0)
	v_mul_f32_e32 v0, 0x42800000, v0
	v_med3_f32 v4, v16, s67, v98
	v_med3_f32 v0, v0, s67, v98
	v_cvt_pk_fp8_f32 v11, v4, v0 op_sel:[0,0,1]
	v_mul_f32_e32 v0, 0x42800000, v37
	v_med3_f32 v4, v49, s67, v98
	v_med3_f32 v0, v0, s67, v98
	v_cvt_pk_fp8_f32 v69, v4, v0 op_sel:[0,0,1]
	v_mul_f32_e32 v0, 0x42800000, v25
	v_mul_f32_e32 v4, 0x42800000, v29
	v_med3_f32 v0, v0, s67, v98
	v_med3_f32 v4, v4, s67, v98
	v_cvt_pk_fp8_f32 v70, v0, v4
	v_mul_f32_e32 v12, 0x42800000, v33
	v_mul_f32_e32 v0, 0x42800000, v21
	v_med3_f32 v4, v12, s67, v98
	v_med3_f32 v0, v0, s67, v98
	v_cvt_pk_fp8_f32 v70, v4, v0 op_sel:[0,0,1]
	v_mul_f32_e32 v0, 0x42800000, v5
	v_mul_f32_e32 v4, 0x42800000, v13
	v_med3_f32 v0, v0, s67, v98
	v_med3_f32 v4, v4, s67, v98
	v_cvt_pk_fp8_f32 v71, v0, v4
	v_mul_f32_e32 v5, 0x42800000, v17
	v_mul_f32_e32 v0, 0x42800000, v1
	v_med3_f32 v1, v5, s67, v98
	v_med3_f32 v0, v0, s67, v98
	v_cvt_pk_fp8_f32 v71, v1, v0 op_sel:[0,0,1]
	v_mul_f32_e32 v0, 0x42800000, v58
	v_mul_f32_e32 v1, 0x42800000, v62
	v_med3_f32 v0, v0, s67, v98
	v_med3_f32 v1, v1, s67, v98
	v_cvt_pk_fp8_f32 v72, v0, v1
	v_mul_f32_e32 v4, 0x42800000, v66
	v_mul_f32_e32 v0, 0x42800000, v54
	v_med3_f32 v1, v4, s67, v98
	v_med3_f32 v0, v0, s67, v98
	v_cvt_pk_fp8_f32 v72, v1, v0 op_sel:[0,0,1]
	v_mul_f32_e32 v0, 0x42800000, v42
	v_mul_f32_e32 v1, 0x42800000, v46
	v_med3_f32 v0, v0, s67, v98
	v_med3_f32 v1, v1, s67, v98
	v_cvt_pk_fp8_f32 v73, v0, v1
	v_mul_f32_e32 v4, 0x42800000, v50
	v_mul_f32_e32 v0, 0x42800000, v38
	v_med3_f32 v1, v4, s67, v98
	v_med3_f32 v0, v0, s67, v98
	v_cvt_pk_fp8_f32 v73, v1, v0 op_sel:[0,0,1]
	v_mul_f32_e32 v0, 0x42800000, v26
	v_mul_f32_e32 v1, 0x42800000, v30
	v_med3_f32 v0, v0, s67, v98
	v_med3_f32 v1, v1, s67, v98
	v_cvt_pk_fp8_f32 v74, v0, v1
	v_mul_f32_e32 v4, 0x42800000, v34
	v_mul_f32_e32 v0, 0x42800000, v22
	v_med3_f32 v1, v4, s67, v98
	v_med3_f32 v0, v0, s67, v98
	v_cvt_pk_fp8_f32 v74, v1, v0 op_sel:[0,0,1]
	v_mul_f32_e32 v0, 0x42800000, v6
	v_mul_f32_e32 v1, 0x42800000, v14
	v_med3_f32 v0, v0, s67, v98
	v_med3_f32 v1, v1, s67, v98
	v_cvt_pk_fp8_f32 v75, v0, v1
	v_mul_f32_e32 v4, 0x42800000, v18
	v_mul_f32_e32 v0, 0x42800000, v2
	v_med3_f32 v1, v4, s67, v98
	v_med3_f32 v0, v0, s67, v98
	v_cvt_pk_fp8_f32 v75, v1, v0 op_sel:[0,0,1]
	v_mul_f32_e32 v0, 0x42800000, v59
	v_mul_f32_e32 v1, 0x42800000, v63
	v_med3_f32 v0, v0, s67, v98
	v_med3_f32 v1, v1, s67, v98
	v_mov_b32_e32 v4, v77
	v_cvt_pk_fp8_f32 v4, v0, v1
	v_mul_f32_e32 v2, 0x42800000, v67
	v_mul_f32_e32 v0, 0x42800000, v55
	v_med3_f32 v1, v2, s67, v98
	v_med3_f32 v0, v0, s67, v98
	v_cvt_pk_fp8_f32 v4, v1, v0 op_sel:[0,0,1]
	v_mul_f32_e32 v0, 0x42800000, v43
	v_mul_f32_e32 v1, 0x42800000, v47
	v_med3_f32 v0, v0, s67, v98
	v_med3_f32 v1, v1, s67, v98
	v_mov_b32_e32 v5, v77
	v_cvt_pk_fp8_f32 v5, v0, v1
	v_mul_f32_e32 v2, 0x42800000, v51
	v_mul_f32_e32 v0, 0x42800000, v39
	v_med3_f32 v1, v2, s67, v98
	v_med3_f32 v0, v0, s67, v98
	v_cvt_pk_fp8_f32 v5, v1, v0 op_sel:[0,0,1]
	v_mul_f32_e32 v0, 0x42800000, v27
	v_mul_f32_e32 v1, 0x42800000, v31
	v_med3_f32 v0, v0, s67, v98
	v_med3_f32 v1, v1, s67, v98
	v_mov_b32_e32 v6, v77
	v_cvt_pk_fp8_f32 v6, v0, v1
	v_mul_f32_e32 v2, 0x42800000, v35
	v_mul_f32_e32 v0, 0x42800000, v23
	v_cvt_pk_fp8_f32 v10, v24, v28
	v_med3_f32 v1, v2, s67, v98
	v_med3_f32 v0, v0, s67, v98
	v_cvt_pk_fp8_f32 v68, v57, v61
	v_cvt_pk_fp8_f32 v6, v1, v0 op_sel:[0,0,1]
	v_mul_f32_e32 v0, 0x42800000, v7
	v_mul_f32_e32 v1, 0x42800000, v15
	v_mul_f32_e32 v64, 0x42800000, v64
	v_mul_f32_e32 v52, 0x42800000, v52
	v_mul_f32_e32 v48, 0x42800000, v48
	v_mul_f32_e32 v36, 0x42800000, v36
	v_mul_f32_e32 v32, 0x42800000, v32
	v_mul_f32_e32 v20, 0x42800000, v20
	v_med3_f32 v0, v0, s67, v98
	v_med3_f32 v1, v1, s67, v98
	v_mov_b32_e32 v7, v77
	v_mul_f32_e32 v65, 0x42800000, v65
	v_med3_f32 v64, v64, s67, v98
	v_mul_f32_e32 v53, 0x42800000, v53
	v_med3_f32 v52, v52, s67, v98
	v_med3_f32 v48, v48, s67, v98
	v_med3_f32 v36, v36, s67, v98
	v_med3_f32 v32, v32, s67, v98
	v_med3_f32 v20, v20, s67, v98
	v_cvt_pk_fp8_f32 v7, v0, v1
	v_med3_f32 v56, v65, s67, v98
	v_med3_f32 v53, v53, s67, v98
	v_cvt_pk_fp8_f32 v8, v64, v52 op_sel:[0,0,1]
	v_cvt_pk_fp8_f32 v9, v48, v36 op_sel:[0,0,1]
	v_cvt_pk_fp8_f32 v10, v32, v20 op_sel:[0,0,1]
	v_cvt_pk_fp8_f32 v68, v56, v53 op_sel:[0,0,1]
	v_mul_f32_e32 v2, 0x42800000, v19
	v_mul_f32_e32 v0, 0x42800000, v3
	v_med3_f32 v1, v2, s67, v98
	v_med3_f32 v0, v0, s67, v98
	v_cvt_pk_fp8_f32 v7, v1, v0 op_sel:[0,0,1]
	ds_write_b128 v95, v[8:11] offset:40960
	ds_write_b128 v95, v[68:71] offset:41040
	ds_write_b128 v95, v[72:75] offset:41120
	ds_write_b128 v95, v[4:7] offset:41200
	s_waitcnt lgkmcnt(0)
	ds_read_b128 v[0:3], v96 offset:40960
	v_or_b32_e32 v4, s13, v83
	v_ashrrev_i32_e32 v5, 31, v4
	v_lshl_add_u64 v[8:9], s[24:25], 0, v[78:79]
	v_lshlrev_b64 v[4:5], 11, v[4:5]
	v_lshl_add_u64 v[10:11], v[8:9], 0, v[4:5]
	ds_read_b128 v[4:7], v96 offset:42240
	s_waitcnt lgkmcnt(1)
	global_store_dwordx4 v[10:11], v[0:3], off sc1
	s_cselect_b64 s[24:25], -1, 0
	s_nop 0
	v_or_b32_e32 v0, s13, v84
	v_ashrrev_i32_e32 v1, 31, v0
	v_lshlrev_b64 v[0:1], 11, v[0:1]
	v_lshl_add_u64 v[0:1], v[8:9], 0, v[0:1]
	s_waitcnt lgkmcnt(0)
	global_store_dwordx4 v[0:1], v[4:7], off sc1
	ds_read_b128 v[0:3], v96 offset:43520
	s_nop 0
	v_or_b32_e32 v4, s13, v85
	v_ashrrev_i32_e32 v5, 31, v4
	v_lshlrev_b64 v[4:5], 11, v[4:5]
	v_lshl_add_u64 v[10:11], v[8:9], 0, v[4:5]
	ds_read_b128 v[4:7], v96 offset:44800
	s_waitcnt lgkmcnt(1)
	global_store_dwordx4 v[10:11], v[0:3], off sc1
	s_nop 1
	v_or_b32_e32 v0, s13, v86
	v_ashrrev_i32_e32 v1, 31, v0
	v_lshlrev_b64 v[0:1], 11, v[0:1]
	v_lshl_add_u64 v[0:1], v[8:9], 0, v[0:1]
	s_waitcnt lgkmcnt(0)
	global_store_dwordx4 v[0:1], v[4:7], off sc1
	s_waitcnt lgkmcnt(0)
	s_andn2_b64 vcc, exec, s[24:25]
	s_cbranch_vccz .LBB0_693
	s_branch .LBB0_714

.LBB0_697:
	s_lshl_b64 s[18:19], s[18:19], 1
	s_add_u32 s3, s10, s18
	s_addc_u32 s18, s11, s19
	s_ashr_i32 s23, s22, 31
	s_lshl_b64 s[10:11], s[22:23], 1
	s_waitcnt lgkmcnt(0)
	s_add_u32 s10, s3, s10
	s_addc_u32 s11, s18, s11
	v_or_b32_e32 v0, s13, v87
	v_lshl_add_u64 v[4:5], s[10:11], 0, v[76:77]
	s_mov_b64 s[10:11], -1
	s_and_b64 vcc, exec, s[24:25]
	v_mul_hi_i32_i24_e32 v7, s12, v0
	v_mul_i32_i24_e32 v6, s12, v0
	s_cbranch_vccz .LBB0_699
	v_lshl_add_u64 v[0:1], v[6:7], 1, v[4:5]
	global_store_dwordx4 v[0:1], v[100:103], off sc1
	s_mov_b64 s[10:11], 0
.LBB0_699:
	v_mov_b32_e32 v0, 0
	s_andn2_b64 vcc, exec, s[10:11]
	v_mov_b32_e32 v1, 0
	v_mov_b32_e32 v2, 0
	v_mov_b32_e32 v3, 0
	s_cbranch_vccnz .LBB0_701
	ds_read_b128 v[8:11], v99 offset:40960
	ds_read_b128 v[0:3], v99 offset:42112
	v_lshl_add_u64 v[6:7], v[6:7], 1, v[4:5]
	s_waitcnt lgkmcnt(1)
	global_store_dwordx4 v[6:7], v[8:11], off sc1
.LBB0_701:
	v_or_b32_e32 v6, s13, v88
	v_mul_hi_i32_i24_e32 v7, s12, v6
	v_mul_i32_i24_e32 v6, s12, v6
	v_lshl_add_u64 v[6:7], v[6:7], 1, v[4:5]
	s_waitcnt lgkmcnt(0)
	global_store_dwordx4 v[6:7], v[0:3], off sc1
	s_mov_b64 s[10:11], -1
	s_and_b64 vcc, exec, s[24:25]
	v_or_b32_e32 v0, s13, v89
	v_mul_hi_i32_i24_e32 v7, s12, v0
	v_mul_i32_i24_e32 v6, s12, v0
	s_cbranch_vccz .LBB0_703
	v_lshl_add_u64 v[0:1], v[6:7], 1, v[4:5]
	global_store_dwordx4 v[0:1], v[100:103], off sc1
	s_mov_b64 s[10:11], 0
.LBB0_703:
	v_mov_b32_e32 v0, 0
	s_andn2_b64 vcc, exec, s[10:11]
	v_mov_b32_e32 v1, 0
	v_mov_b32_e32 v2, 0
	v_mov_b32_e32 v3, 0
	s_cbranch_vccnz .LBB0_705
	ds_read_b128 v[8:11], v99 offset:43264
	ds_read_b128 v[0:3], v99 offset:44416
	v_lshl_add_u64 v[6:7], v[6:7], 1, v[4:5]
	s_waitcnt lgkmcnt(1)
	global_store_dwordx4 v[6:7], v[8:11], off sc1
.LBB0_705:
	v_or_b32_e32 v6, s13, v90
	v_mul_hi_i32_i24_e32 v7, s12, v6
	v_mul_i32_i24_e32 v6, s12, v6
	v_lshl_add_u64 v[6:7], v[6:7], 1, v[4:5]
	s_waitcnt lgkmcnt(0)
	global_store_dwordx4 v[6:7], v[0:3], off sc1
	s_mov_b64 s[10:11], -1
	s_and_b64 vcc, exec, s[24:25]
	v_or_b32_e32 v0, s13, v91
	v_mul_hi_i32_i24_e32 v7, s12, v0
	v_mul_i32_i24_e32 v6, s12, v0
	s_cbranch_vccz .LBB0_707
	v_lshl_add_u64 v[0:1], v[6:7], 1, v[4:5]
	global_store_dwordx4 v[0:1], v[100:103], off sc1
	s_mov_b64 s[10:11], 0
.LBB0_707:
	v_mov_b32_e32 v0, 0
	s_andn2_b64 vcc, exec, s[10:11]
	v_mov_b32_e32 v1, 0
	v_mov_b32_e32 v2, 0
	v_mov_b32_e32 v3, 0
	s_cbranch_vccnz .LBB0_709
	ds_read_b128 v[8:11], v99 offset:45568
	ds_read_b128 v[0:3], v99 offset:46720
	v_lshl_add_u64 v[6:7], v[6:7], 1, v[4:5]
	s_waitcnt lgkmcnt(1)
	global_store_dwordx4 v[6:7], v[8:11], off sc1
.LBB0_709:
	v_or_b32_e32 v6, s13, v92
	v_mul_hi_i32_i24_e32 v7, s12, v6
	v_mul_i32_i24_e32 v6, s12, v6
	v_lshl_add_u64 v[6:7], v[6:7], 1, v[4:5]
	s_waitcnt lgkmcnt(0)
	global_store_dwordx4 v[6:7], v[0:3], off sc1
	s_mov_b64 s[10:11], -1
	s_and_b64 vcc, exec, s[24:25]
	v_or_b32_e32 v0, s13, v93
	v_mul_hi_i32_i24_e32 v7, s12, v0
	v_mul_i32_i24_e32 v6, s12, v0
	s_cbranch_vccz .LBB0_711
	v_lshl_add_u64 v[0:1], v[6:7], 1, v[4:5]
	global_store_dwordx4 v[0:1], v[100:103], off sc1
	s_mov_b64 s[10:11], 0
.LBB0_711:
	v_mov_b32_e32 v0, 0
	s_andn2_b64 vcc, exec, s[10:11]
	v_mov_b32_e32 v1, 0
	v_mov_b32_e32 v2, 0
	v_mov_b32_e32 v3, 0
	s_cbranch_vccnz .LBB0_713
	ds_read_b128 v[8:11], v99 offset:47872
	ds_read_b128 v[0:3], v99 offset:49024
	v_lshl_add_u64 v[6:7], v[6:7], 1, v[4:5]
	s_waitcnt lgkmcnt(1)
	global_store_dwordx4 v[6:7], v[8:11], off sc1
.LBB0_713:
	v_or_b32_e32 v6, s13, v94
	v_mul_hi_i32_i24_e32 v7, s12, v6
	v_mul_i32_i24_e32 v6, s12, v6
	v_lshl_add_u64 v[4:5], v[6:7], 1, v[4:5]
	s_waitcnt lgkmcnt(0)
	global_store_dwordx4 v[4:5], v[0:3], off sc1
	s_waitcnt lgkmcnt(0)

.LBB0_985:
	ds_read_b128 v[8:11], v176
	ds_read_b128 v[12:15], v176 offset:1024
	ds_read_b128 v[0:3], v176 offset:2048
	ds_read_b128 v[4:7], v176 offset:3072
	s_add_u32 s20, s18, 0xfffc0080
	s_addc_u32 s21, s19, -1
	s_cmp_eq_u32 s67, 12
	s_cselect_b32 s23, s61, s21
	s_cselect_b32 s22, s62, s20
	s_cselect_b32 s21, s63, s66
	s_cselect_b32 s20, s64, s65
	v_lshl_add_u64 v[158:159], s[18:19], 0, v[156:157]
	s_add_i32 m0, s44, 0xc000
	ds_read_b128 v[180:183], v177
	ds_read_b128 v[184:187], v177 offset:1024
	ds_read_b128 v[188:191], v177 offset:2048
	ds_read_b128 v[192:195], v177 offset:3072
	ds_read_b128 v[196:199], v177 offset:4096
	ds_read_b128 v[200:203], v177 offset:5120
	ds_read_b128 v[204:207], v177 offset:6144
	ds_read_b128 v[208:211], v177 offset:7168
	global_load_lds_dwordx4 v[158:159], off
	v_lshl_add_u64 v[158:159], s[18:19], 0, v[154:155]
	s_add_i32 m0, s44, 0xe000
	s_nop 0
	global_load_lds_dwordx4 v[158:159], off
	s_waitcnt lgkmcnt(8)
	s_barrier
	s_waitcnt lgkmcnt(0)
	s_setprio 1
	s_waitcnt lgkmcnt(0)
	v_mfma_scale_f32_16x16x128_f8f6f4 v[140:143], v[8:15], v[180:187], v[140:143], v172, v172 op_sel_hi:[0,0,0]
	v_mfma_scale_f32_16x16x128_f8f6f4 v[136:139], v[0:7], v[180:187], v[136:139], v172, v172 op_sel_hi:[0,0,0]
	v_mfma_scale_f32_16x16x128_f8f6f4 v[128:131], v[8:15], v[188:195], v[128:131], v172, v172 op_sel_hi:[0,0,0]
	v_mfma_scale_f32_16x16x128_f8f6f4 v[120:123], v[0:7], v[188:195], v[120:123], v172, v172 op_sel_hi:[0,0,0]
	v_mfma_scale_f32_16x16x128_f8f6f4 v[112:115], v[8:15], v[196:203], v[112:115], v172, v172 op_sel_hi:[0,0,0]
	v_mfma_scale_f32_16x16x128_f8f6f4 v[104:107], v[0:7], v[196:203], v[104:107], v172, v172 op_sel_hi:[0,0,0]
	v_mfma_scale_f32_16x16x128_f8f6f4 v[96:99], v[8:15], v[204:211], v[96:99], v172, v172 op_sel_hi:[0,0,0]
	v_mfma_scale_f32_16x16x128_f8f6f4 v[88:91], v[0:7], v[204:211], v[88:91], v172, v172 op_sel_hi:[0,0,0]
	s_setprio 0
	s_barrier
	s_add_i32 s68, s53, s43
	v_lshl_add_u64 v[162:163], s[20:21], 0, v[146:147]
	s_mov_b32 m0, s68
	ds_read_b128 v[212:215], v178
	ds_read_b128 v[216:219], v178 offset:1024
	ds_read_b128 v[224:227], v178 offset:2048
	ds_read_b128 v[228:231], v178 offset:3072
	global_load_lds_dwordx4 v[162:163], off
	v_lshl_add_u64 v[164:165], s[20:21], 0, v[150:151]
	s_add_i32 m0, s68, 0x2000
	s_nop 0
	global_load_lds_dwordx4 v[164:165], off
	s_barrier
	s_waitcnt lgkmcnt(0)
	s_setprio 1
	s_waitcnt lgkmcnt(0)
	v_mfma_scale_f32_16x16x128_f8f6f4 v[132:135], v[212:219], v[180:187], v[132:135], v172, v172 op_sel_hi:[0,0,0]
	v_mfma_scale_f32_16x16x128_f8f6f4 v[124:127], v[224:231], v[180:187], v[124:127], v172, v172 op_sel_hi:[0,0,0]
	v_mfma_scale_f32_16x16x128_f8f6f4 v[116:119], v[212:219], v[188:195], v[116:119], v172, v172 op_sel_hi:[0,0,0]
	v_mfma_scale_f32_16x16x128_f8f6f4 v[108:111], v[224:231], v[188:195], v[108:111], v172, v172 op_sel_hi:[0,0,0]
	v_mfma_scale_f32_16x16x128_f8f6f4 v[100:103], v[212:219], v[196:203], v[100:103], v172, v172 op_sel_hi:[0,0,0]
	v_mfma_scale_f32_16x16x128_f8f6f4 v[92:95], v[224:231], v[196:203], v[92:95], v172, v172 op_sel_hi:[0,0,0]
	v_mfma_scale_f32_16x16x128_f8f6f4 v[84:87], v[212:219], v[204:211], v[84:87], v172, v172 op_sel_hi:[0,0,0]
	v_mfma_scale_f32_16x16x128_f8f6f4 v[80:83], v[224:231], v[204:211], v[80:83], v172, v172 op_sel_hi:[0,0,0]
	s_setprio 0
	s_mov_b32 m0, s44
	v_lshl_add_u64 v[166:167], s[22:23], 0, v[144:145]
	s_barrier
	ds_read_b128 v[180:183], v177 offset:16384
	ds_read_b128 v[184:187], v177 offset:17408
	ds_read_b128 v[188:191], v177 offset:18432
	ds_read_b128 v[192:195], v177 offset:19456
	ds_read_b128 v[196:199], v177 offset:20480
	ds_read_b128 v[200:203], v177 offset:21504
	ds_read_b128 v[204:207], v177 offset:22528
	ds_read_b128 v[208:211], v177 offset:23552
	global_load_lds_dwordx4 v[166:167], off
	v_lshl_add_u64 v[168:169], s[22:23], 0, v[148:149]
	s_mov_b32 m0, s45
	s_nop 0
	global_load_lds_dwordx4 v[168:169], off
	s_barrier
	s_waitcnt lgkmcnt(0)
	s_setprio 1
	s_waitcnt lgkmcnt(0)
	v_mfma_scale_f32_16x16x128_f8f6f4 v[76:79], v[8:15], v[180:187], v[76:79], v172, v172 op_sel_hi:[0,0,0]
	v_mfma_scale_f32_16x16x128_f8f6f4 v[72:75], v[0:7], v[180:187], v[72:75], v172, v172 op_sel_hi:[0,0,0]
	v_mfma_scale_f32_16x16x128_f8f6f4 v[64:67], v[8:15], v[188:195], v[64:67], v172, v172 op_sel_hi:[0,0,0]
	v_mfma_scale_f32_16x16x128_f8f6f4 v[56:59], v[0:7], v[188:195], v[56:59], v172, v172 op_sel_hi:[0,0,0]
	v_mfma_scale_f32_16x16x128_f8f6f4 v[48:51], v[8:15], v[196:203], v[48:51], v172, v172 op_sel_hi:[0,0,0]
	v_mfma_scale_f32_16x16x128_f8f6f4 v[40:43], v[0:7], v[196:203], v[40:43], v172, v172 op_sel_hi:[0,0,0]
	v_mfma_scale_f32_16x16x128_f8f6f4 v[32:35], v[8:15], v[204:211], v[32:35], v172, v172 op_sel_hi:[0,0,0]
	v_mfma_scale_f32_16x16x128_f8f6f4 v[24:27], v[0:7], v[204:211], v[24:27], v172, v172 op_sel_hi:[0,0,0]
	s_setprio 0
	s_barrier
	s_add_u32 s68, s20, 0x40000
	s_addc_u32 s69, s21, 0
	s_add_i32 s70, s54, s43
	v_lshl_add_u64 v[0:1], s[68:69], 0, v[146:147]
	s_mov_b32 m0, s70
	s_nop 0
	global_load_lds_dwordx4 v[0:1], off
	v_lshl_add_u64 v[0:1], s[68:69], 0, v[150:151]
	s_add_i32 m0, s70, 0x2000
	s_nop 0
	global_load_lds_dwordx4 v[0:1], off
	s_waitcnt vmcnt(6)
	s_barrier
	s_setprio 1
	v_mfma_scale_f32_16x16x128_f8f6f4 v[68:71], v[212:219], v[180:187], v[68:71], v172, v172 op_sel_hi:[0,0,0]
	v_mfma_scale_f32_16x16x128_f8f6f4 v[60:63], v[224:231], v[180:187], v[60:63], v172, v172 op_sel_hi:[0,0,0]
	v_mfma_scale_f32_16x16x128_f8f6f4 v[52:55], v[212:219], v[188:195], v[52:55], v172, v172 op_sel_hi:[0,0,0]
	v_mfma_scale_f32_16x16x128_f8f6f4 v[44:47], v[224:231], v[188:195], v[44:47], v172, v172 op_sel_hi:[0,0,0]
	v_mfma_scale_f32_16x16x128_f8f6f4 v[36:39], v[212:219], v[196:203], v[36:39], v172, v172 op_sel_hi:[0,0,0]
	v_mfma_scale_f32_16x16x128_f8f6f4 v[28:31], v[224:231], v[196:203], v[28:31], v172, v172 op_sel_hi:[0,0,0]
	v_mfma_scale_f32_16x16x128_f8f6f4 v[20:23], v[212:219], v[204:211], v[20:23], v172, v172 op_sel_hi:[0,0,0]
	v_mfma_scale_f32_16x16x128_f8f6f4 v[16:19], v[224:231], v[204:211], v[16:19], v172, v172 op_sel_hi:[0,0,0]
	s_setprio 0
	s_add_i32 s68, 0, 0x18000
	v_add_u32_e32 v12, s68, v173
	s_barrier
	ds_read_b128 v[0:3], v12
	ds_read_b128 v[4:7], v12 offset:1024
	ds_read_b128 v[8:11], v12 offset:2048
	ds_read_b128 v[12:15], v12 offset:3072
	s_add_u32 s22, s22, 0x40000
	s_addc_u32 s23, s23, 0
	s_mov_b32 m0, s46
	v_lshl_add_u64 v[158:159], s[22:23], 0, v[144:145]
	ds_read_b128 v[180:183], v177 offset:32768
	ds_read_b128 v[184:187], v177 offset:33792
	ds_read_b128 v[188:191], v177 offset:34816
	ds_read_b128 v[192:195], v177 offset:35840
	ds_read_b128 v[196:199], v177 offset:36864
	ds_read_b128 v[200:203], v177 offset:37888
	ds_read_b128 v[204:207], v177 offset:38912
	ds_read_b128 v[208:211], v177 offset:39936
	global_load_lds_dwordx4 v[158:159], off
	v_lshl_add_u64 v[158:159], s[22:23], 0, v[148:149]
	s_mov_b32 m0, s47
	s_nop 0
	global_load_lds_dwordx4 v[158:159], off
	s_waitcnt lgkmcnt(8)
	s_barrier
	s_waitcnt lgkmcnt(0)
	s_setprio 1
	s_waitcnt lgkmcnt(0)
	v_mfma_scale_f32_16x16x128_f8f6f4 v[140:143], v[0:7], v[180:187], v[140:143], v172, v172 op_sel_hi:[0,0,0]
	v_mfma_scale_f32_16x16x128_f8f6f4 v[136:139], v[8:15], v[180:187], v[136:139], v172, v172 op_sel_hi:[0,0,0]
	v_mfma_scale_f32_16x16x128_f8f6f4 v[128:131], v[0:7], v[188:195], v[128:131], v172, v172 op_sel_hi:[0,0,0]
	v_mfma_scale_f32_16x16x128_f8f6f4 v[120:123], v[8:15], v[188:195], v[120:123], v172, v172 op_sel_hi:[0,0,0]
	v_mfma_scale_f32_16x16x128_f8f6f4 v[112:115], v[0:7], v[196:203], v[112:115], v172, v172 op_sel_hi:[0,0,0]
	v_mfma_scale_f32_16x16x128_f8f6f4 v[104:107], v[8:15], v[196:203], v[104:107], v172, v172 op_sel_hi:[0,0,0]
	v_mfma_scale_f32_16x16x128_f8f6f4 v[96:99], v[0:7], v[204:211], v[96:99], v172, v172 op_sel_hi:[0,0,0]
	v_mfma_scale_f32_16x16x128_f8f6f4 v[88:91], v[8:15], v[204:211], v[88:91], v172, v172 op_sel_hi:[0,0,0]
	s_setprio 0
	s_barrier
	s_add_i32 s22, 0, 0x1c000
	s_add_i32 s23, s68, s43
	v_add_u32_e32 v152, s22, v173
	v_lshl_add_u64 v[158:159], v[162:163], 0, s[6:7]
	s_mov_b32 m0, s23
	ds_read_b128 v[212:215], v152
	ds_read_b128 v[216:219], v152 offset:1024
	ds_read_b128 v[224:227], v152 offset:2048
	ds_read_b128 v[228:231], v152 offset:3072
	global_load_lds_dwordx4 v[158:159], off
	v_lshl_add_u64 v[158:159], v[164:165], 0, s[6:7]
	s_add_i32 m0, s23, 0x2000
	s_nop 0
	global_load_lds_dwordx4 v[158:159], off
	s_barrier
	s_waitcnt lgkmcnt(0)
	s_setprio 1
	s_waitcnt lgkmcnt(0)
	v_mfma_scale_f32_16x16x128_f8f6f4 v[132:135], v[212:219], v[180:187], v[132:135], v172, v172 op_sel_hi:[0,0,0]
	v_mfma_scale_f32_16x16x128_f8f6f4 v[124:127], v[224:231], v[180:187], v[124:127], v172, v172 op_sel_hi:[0,0,0]
	v_mfma_scale_f32_16x16x128_f8f6f4 v[116:119], v[212:219], v[188:195], v[116:119], v172, v172 op_sel_hi:[0,0,0]
	v_mfma_scale_f32_16x16x128_f8f6f4 v[108:111], v[224:231], v[188:195], v[108:111], v172, v172 op_sel_hi:[0,0,0]
	v_mfma_scale_f32_16x16x128_f8f6f4 v[100:103], v[212:219], v[196:203], v[100:103], v172, v172 op_sel_hi:[0,0,0]
	v_mfma_scale_f32_16x16x128_f8f6f4 v[92:95], v[224:231], v[196:203], v[92:95], v172, v172 op_sel_hi:[0,0,0]
	v_mfma_scale_f32_16x16x128_f8f6f4 v[84:87], v[212:219], v[204:211], v[84:87], v172, v172 op_sel_hi:[0,0,0]
	v_mfma_scale_f32_16x16x128_f8f6f4 v[80:83], v[224:231], v[204:211], v[80:83], v172, v172 op_sel_hi:[0,0,0]
	s_setprio 0
	s_mov_b32 m0, s50
	v_lshl_add_u64 v[158:159], v[166:167], 0, s[6:7]
	s_barrier
	ds_read_b128 v[180:183], v177 offset:49152
	ds_read_b128 v[184:187], v177 offset:50176
	ds_read_b128 v[188:191], v177 offset:51200
	ds_read_b128 v[192:195], v177 offset:52224
	ds_read_b128 v[196:199], v177 offset:53248
	ds_read_b128 v[200:203], v177 offset:54272
	ds_read_b128 v[204:207], v177 offset:55296
	ds_read_b128 v[208:211], v177 offset:56320
	global_load_lds_dwordx4 v[158:159], off
	v_lshl_add_u64 v[158:159], v[168:169], 0, s[6:7]
	s_mov_b32 m0, s51
	s_nop 0
	global_load_lds_dwordx4 v[158:159], off
	s_barrier
	s_waitcnt lgkmcnt(0)
	s_setprio 1
	s_waitcnt lgkmcnt(0)
	v_mfma_scale_f32_16x16x128_f8f6f4 v[76:79], v[0:7], v[180:187], v[76:79], v172, v172 op_sel_hi:[0,0,0]
	v_mfma_scale_f32_16x16x128_f8f6f4 v[72:75], v[8:15], v[180:187], v[72:75], v172, v172 op_sel_hi:[0,0,0]
	v_mfma_scale_f32_16x16x128_f8f6f4 v[64:67], v[0:7], v[188:195], v[64:67], v172, v172 op_sel_hi:[0,0,0]
	v_mfma_scale_f32_16x16x128_f8f6f4 v[56:59], v[8:15], v[188:195], v[56:59], v172, v172 op_sel_hi:[0,0,0]
	v_mfma_scale_f32_16x16x128_f8f6f4 v[48:51], v[0:7], v[196:203], v[48:51], v172, v172 op_sel_hi:[0,0,0]
	v_mfma_scale_f32_16x16x128_f8f6f4 v[40:43], v[8:15], v[196:203], v[40:43], v172, v172 op_sel_hi:[0,0,0]
	v_mfma_scale_f32_16x16x128_f8f6f4 v[32:35], v[0:7], v[204:211], v[32:35], v172, v172 op_sel_hi:[0,0,0]
	v_mfma_scale_f32_16x16x128_f8f6f4 v[24:27], v[8:15], v[204:211], v[24:27], v172, v172 op_sel_hi:[0,0,0]
	s_setprio 0
	s_barrier
	s_add_u32 s20, s20, 0x40080
	s_addc_u32 s21, s21, 0
	s_add_i32 s22, s22, s43
	v_lshl_add_u64 v[0:1], s[20:21], 0, v[146:147]
	s_mov_b32 m0, s22
	s_nop 0
	global_load_lds_dwordx4 v[0:1], off
	v_lshl_add_u64 v[0:1], s[20:21], 0, v[150:151]
	s_add_i32 m0, s22, 0x2000
	s_nop 0
	global_load_lds_dwordx4 v[0:1], off
	s_waitcnt vmcnt(6)
	s_barrier
	s_setprio 1
	v_mfma_scale_f32_16x16x128_f8f6f4 v[68:71], v[212:219], v[180:187], v[68:71], v172, v172 op_sel_hi:[0,0,0]
	v_mfma_scale_f32_16x16x128_f8f6f4 v[60:63], v[224:231], v[180:187], v[60:63], v172, v172 op_sel_hi:[0,0,0]
	v_mfma_scale_f32_16x16x128_f8f6f4 v[52:55], v[212:219], v[188:195], v[52:55], v172, v172 op_sel_hi:[0,0,0]
	v_mfma_scale_f32_16x16x128_f8f6f4 v[44:47], v[224:231], v[188:195], v[44:47], v172, v172 op_sel_hi:[0,0,0]
	v_mfma_scale_f32_16x16x128_f8f6f4 v[36:39], v[212:219], v[196:203], v[36:39], v172, v172 op_sel_hi:[0,0,0]
	v_mfma_scale_f32_16x16x128_f8f6f4 v[28:31], v[224:231], v[196:203], v[28:31], v172, v172 op_sel_hi:[0,0,0]
	v_mfma_scale_f32_16x16x128_f8f6f4 v[20:23], v[212:219], v[204:211], v[20:23], v172, v172 op_sel_hi:[0,0,0]
	v_mfma_scale_f32_16x16x128_f8f6f4 v[16:19], v[224:231], v[204:211], v[16:19], v172, v172 op_sel_hi:[0,0,0]
	s_setprio 0
	s_add_i32 s67, s67, 2
	s_add_u32 s65, s65, 0x100
	s_addc_u32 s66, s66, 0
	s_add_u32 s18, s18, 0x100
	s_addc_u32 s19, s19, 0
	s_cmp_gt_u32 s67, 13
	s_barrier
	s_cbranch_scc0 .LBB0_985
	s_lshl_b32 s18, s60, 8
	s_min_i32 s19, s60, 32
	s_ashr_i32 s22, s19, 4
	s_add_i32 s19, s18, 0xffffe000
	s_cmp_lt_i32 s60, 32
	s_cselect_b32 s20, s18, s19
	s_mul_i32 s22, s22, 6
	s_cselect_b32 s60, s28, s30
	s_cselect_b32 s61, s27, s29
	s_ashr_i32 s21, s20, 31
	s_ashr_i32 s19, s18, 31
	s_ashr_i32 s23, s22, 31
	s_lshl_b64 s[20:21], s[20:21], 13
	s_lshl_b64 s[18:19], s[18:19], 12
	s_lshl_b64 s[22:23], s[22:23], 13
	v_lshl_or_b32 v8, s59, 8, v175
	s_add_u32 s22, s4, s22
	s_addc_u32 s23, s5, s23
	v_ashrrev_i32_e32 v9, 31, v8
	v_lshl_add_u64 v[0:1], v[8:9], 2, s[22:23]
	v_lshl_add_u64 v[10:11], v[0:1], 0, s[8:9]
	v_add_co_u32_e32 v0, vcc, s49, v0
	s_add_u32 s20, s61, s20
	s_nop 7
	s_nop 7
	s_nop 7
	s_nop 0
	v_addc_co_u32_e32 v1, vcc, 0, v1, vcc
	s_addc_u32 s21, s60, s21
	v_add_u32_e32 v152, v174, v8
	global_load_dwordx4 v[0:3], v[0:1], off
	s_nop 0
	global_load_dwordx4 v[164:167], v[10:11], off offset:528
	global_load_dwordx4 v[4:7], v[10:11], off offset:16
	global_load_dwordx4 v[180:183], v[10:11], off offset:512
	v_mov_b32_e32 v169, v153
	v_lshl_add_u64 v[8:9], v[152:153], 2, s[20:21]
	v_add_u32_e32 v168, 0x80, v152
	global_load_dwordx4 v[184:187], v[8:9], off
	global_load_dwordx4 v[188:191], v[8:9], off offset:16
	v_lshl_add_u64 v[8:9], v[168:169], 2, s[20:21]
	global_load_dwordx4 v[192:195], v[8:9], off
	global_load_dwordx4 v[196:199], v[8:9], off offset:16
	v_add_u32_e32 v220, 0x8000, v152
	v_mov_b32_e32 v221, v153
	v_lshl_add_u64 v[8:9], v[220:221], 2, s[20:21]
	v_add_u32_e32 v252, 0x8080, v152
	v_mov_b32_e32 v253, v153
	global_load_dwordx4 v[200:203], v[8:9], off
	global_load_dwordx4 v[204:207], v[8:9], off offset:16
	v_lshl_add_u64 v[8:9], v[252:253], 2, s[20:21]
	global_load_dwordx4 v[208:211], v[8:9], off
	global_load_dwordx4 v[212:215], v[8:9], off offset:16
	v_mov_b32_e32 v223, v153
	v_add_u32_e32 v222, 0x10000, v152
	v_lshl_add_u64 v[8:9], v[222:223], 2, s[20:21]
	v_mov_b32_e32 v171, v153
	v_add_u32_e32 v170, 0x10080, v152
	global_load_dwordx4 v[216:219], v[8:9], off
	global_load_dwordx4 v[224:227], v[8:9], off offset:16
	v_lshl_add_u64 v[8:9], v[170:171], 2, s[20:21]
	v_mov_b32_e32 v159, v153
	v_add_u32_e32 v158, 0x18000, v152
	global_load_dwordx4 v[228:231], v[8:9], off
	global_load_dwordx4 v[232:235], v[8:9], off offset:16
	v_lshl_add_u64 v[8:9], v[158:159], 2, s[20:21]
	v_mov_b32_e32 v163, v153
	v_add_u32_e32 v162, 0x18080, v152
	global_load_dwordx4 v[236:239], v[8:9], off
	global_load_dwordx4 v[240:243], v[8:9], off offset:16
	v_lshl_add_u64 v[8:9], v[162:163], 2, s[20:21]
	global_load_dwordx4 v[244:247], v[8:9], off offset:16
	global_load_dwordx4 v[248:251], v[8:9], off
	s_add_u32 s18, s2, s18
	s_addc_u32 s19, s3, s19
	v_lshl_add_u64 v[160:161], v[152:153], 1, s[18:19]
	s_and_b64 vcc, exec, s[0:1]
	s_mov_b32 s59, s55
	s_mov_b32 s60, s56
	s_waitcnt vmcnt(0)
	v_pk_mul_f32 v[14:15], v[0:1], s[10:11] op_sel_hi:[1,0]
	v_pk_mul_f32 v[12:13], v[2:3], s[10:11] op_sel_hi:[1,0]
	v_pk_mul_f32 v[8:9], v[6:7], s[10:11] op_sel_hi:[1,0]
	v_pk_mul_f32 v[10:11], v[4:5], s[10:11] op_sel_hi:[1,0]
	v_pk_mul_f32 v[6:7], v[180:181], s[10:11] op_sel_hi:[1,0]
	v_pk_mul_f32 v[4:5], v[182:183], s[10:11] op_sel_hi:[1,0]
	v_pk_mul_f32 v[0:1], v[166:167], s[10:11] op_sel_hi:[1,0]
	v_pk_mul_f32 v[2:3], v[164:165], s[10:11] op_sel_hi:[1,0]
	v_pk_fma_f32 v[140:141], v[140:141], v[14:15], v[184:185]
	v_pk_fma_f32 v[164:165], v[138:139], v[8:9], v[190:191]
	v_pk_fma_f32 v[138:139], v[136:137], v[10:11], v[188:189]
	v_pk_fma_f32 v[132:133], v[132:133], v[6:7], v[192:193]
	v_pk_fma_f32 v[142:143], v[142:143], v[12:13], v[186:187]
	v_cvt_pk_bf16_f32 v136, v140, v141
	v_pk_fma_f32 v[134:135], v[134:135], v[4:5], v[194:195]
	v_cvt_pk_bf16_f32 v137, v142, v143
	v_cvt_pk_bf16_f32 v138, v138, v139
	v_cvt_pk_bf16_f32 v139, v164, v165
	v_pk_fma_f32 v[140:141], v[126:127], v[0:1], v[198:199]
	global_store_dwordx4 v[160:161], v[136:139], off sc1
	v_pk_fma_f32 v[126:127], v[124:125], v[2:3], v[196:197]
	v_cvt_pk_bf16_f32 v124, v132, v133
	v_cvt_pk_bf16_f32 v125, v134, v135
	v_lshl_add_u64 v[132:133], v[168:169], 1, s[18:19]
	v_cvt_pk_bf16_f32 v126, v126, v127
	v_cvt_pk_bf16_f32 v127, v140, v141
	global_store_dwordx4 v[132:133], v[124:127], off sc1
	v_pk_fma_f32 v[116:117], v[116:117], v[6:7], v[208:209]
	v_pk_fma_f32 v[118:119], v[118:119], v[4:5], v[210:211]
	v_pk_fma_f32 v[124:125], v[130:131], v[12:13], v[202:203]
	v_pk_fma_f32 v[126:127], v[128:129], v[14:15], v[200:201]
	v_pk_fma_f32 v[128:129], v[122:123], v[8:9], v[206:207]
	v_pk_fma_f32 v[122:123], v[120:121], v[10:11], v[204:205]
	v_cvt_pk_bf16_f32 v120, v126, v127
	v_cvt_pk_bf16_f32 v121, v124, v125
	v_lshl_add_u64 v[124:125], v[220:221], 1, s[18:19]
	v_cvt_pk_bf16_f32 v122, v122, v123
	v_cvt_pk_bf16_f32 v123, v128, v129
	global_store_dwordx4 v[124:125], v[120:123], off sc1
	v_pk_fma_f32 v[100:101], v[100:101], v[6:7], v[228:229]
	v_pk_fma_f32 v[102:103], v[102:103], v[4:5], v[230:231]
	v_pk_fma_f32 v[120:121], v[110:111], v[0:1], v[214:215]
	v_pk_fma_f32 v[110:111], v[108:109], v[2:3], v[212:213]
	v_cvt_pk_bf16_f32 v108, v116, v117
	v_cvt_pk_bf16_f32 v109, v118, v119
	v_lshl_add_u64 v[116:117], v[252:253], 1, s[18:19]
	v_cvt_pk_bf16_f32 v110, v110, v111
	v_cvt_pk_bf16_f32 v111, v120, v121
	global_store_dwordx4 v[116:117], v[108:111], off sc1
	v_pk_fma_f32 v[84:85], v[84:85], v[6:7], v[248:249]
	v_pk_fma_f32 v[86:87], v[86:87], v[4:5], v[250:251]
	v_pk_fma_f32 v[108:109], v[114:115], v[12:13], v[218:219]
	v_pk_fma_f32 v[110:111], v[112:113], v[14:15], v[216:217]
	v_pk_fma_f32 v[112:113], v[106:107], v[8:9], v[226:227]
	v_pk_fma_f32 v[106:107], v[104:105], v[10:11], v[224:225]
	v_cvt_pk_bf16_f32 v104, v110, v111
	v_cvt_pk_bf16_f32 v105, v108, v109
	v_lshl_add_u64 v[108:109], v[222:223], 1, s[18:19]
	v_cvt_pk_bf16_f32 v106, v106, v107
	v_cvt_pk_bf16_f32 v107, v112, v113
	global_store_dwordx4 v[108:109], v[104:107], off sc1
	v_add_u32_e32 v160, 0x40080, v152
	v_mov_b32_e32 v161, v153
	v_pk_fma_f32 v[104:105], v[94:95], v[0:1], v[234:235]
	v_pk_fma_f32 v[94:95], v[92:93], v[2:3], v[232:233]
	v_cvt_pk_bf16_f32 v92, v100, v101
	v_cvt_pk_bf16_f32 v93, v102, v103
	v_lshl_add_u64 v[100:101], v[170:171], 1, s[18:19]
	v_cvt_pk_bf16_f32 v94, v94, v95
	v_cvt_pk_bf16_f32 v95, v104, v105
	global_store_dwordx4 v[100:101], v[92:95], off sc1
	v_add_u32_e32 v164, 0x48080, v152
	v_mov_b32_e32 v165, v153
	v_pk_fma_f32 v[92:93], v[98:99], v[12:13], v[238:239]
	v_pk_fma_f32 v[94:95], v[96:97], v[14:15], v[236:237]
	v_pk_fma_f32 v[96:97], v[90:91], v[8:9], v[242:243]
	v_pk_fma_f32 v[90:91], v[88:89], v[10:11], v[240:241]
	v_cvt_pk_bf16_f32 v88, v94, v95
	v_cvt_pk_bf16_f32 v89, v92, v93
	v_lshl_add_u64 v[92:93], v[158:159], 1, s[18:19]
	v_cvt_pk_bf16_f32 v90, v90, v91
	v_cvt_pk_bf16_f32 v91, v96, v97
	global_store_dwordx4 v[92:93], v[88:91], off sc1
	v_add_u32_e32 v158, 0x40000, v152
	v_lshl_add_u64 v[92:93], v[160:161], 2, s[20:21]
	v_pk_fma_f32 v[88:89], v[82:83], v[0:1], v[246:247]
	v_pk_fma_f32 v[82:83], v[80:81], v[2:3], v[244:245]
	v_cvt_pk_bf16_f32 v80, v84, v85
	v_lshl_add_u64 v[84:85], v[162:163], 1, s[18:19]
	v_cvt_pk_bf16_f32 v81, v86, v87
	v_cvt_pk_bf16_f32 v82, v82, v83
	v_cvt_pk_bf16_f32 v83, v88, v89
	global_store_dwordx4 v[84:85], v[80:83], off sc1
	v_lshl_add_u64 v[84:85], v[158:159], 2, s[20:21]
	global_load_dwordx4 v[80:83], v[84:85], off
	s_nop 0
	global_load_dwordx4 v[84:87], v[84:85], off offset:16
	s_nop 0
	global_load_dwordx4 v[88:91], v[92:93], off
	s_nop 0
	global_load_dwordx4 v[92:95], v[92:93], off offset:16
	v_add_u32_e32 v162, 0x48000, v152
	v_lshl_add_u64 v[100:101], v[162:163], 2, s[20:21]
	global_load_dwordx4 v[96:99], v[100:101], off
	s_nop 0
	global_load_dwordx4 v[100:103], v[100:101], off offset:16
	v_lshl_add_u64 v[108:109], v[164:165], 2, s[20:21]
	global_load_dwordx4 v[104:107], v[108:109], off
	s_nop 0
	global_load_dwordx4 v[108:111], v[108:109], off offset:16
	v_add_u32_e32 v166, 0x50000, v152
	v_mov_b32_e32 v167, v153
	v_lshl_add_u64 v[116:117], v[166:167], 2, s[20:21]
	v_add_u32_e32 v168, 0x50080, v152
	global_load_dwordx4 v[112:115], v[116:117], off
	s_nop 0
	global_load_dwordx4 v[116:119], v[116:117], off offset:16
	v_lshl_add_u64 v[124:125], v[168:169], 2, s[20:21]
	v_add_u32_e32 v170, 0x58000, v152
	global_load_dwordx4 v[120:123], v[124:125], off
	s_nop 0
	global_load_dwordx4 v[124:127], v[124:125], off offset:16
	v_lshl_add_u64 v[132:133], v[170:171], 2, s[20:21]
	v_add_u32_e32 v152, 0x58080, v152
	global_load_dwordx4 v[128:131], v[132:133], off
	s_nop 0
	global_load_dwordx4 v[132:135], v[132:133], off offset:16
	v_lshl_add_u64 v[140:141], v[152:153], 2, s[20:21]
	global_load_dwordx4 v[136:139], v[140:141], off
	s_nop 0
	global_load_dwordx4 v[140:143], v[140:141], off offset:16
	s_mov_b64 s[20:21], s[12:13]
	s_waitcnt vmcnt(0)
	v_pk_fma_f32 v[76:77], v[76:77], v[14:15], v[80:81]
	v_pk_fma_f32 v[78:79], v[78:79], v[12:13], v[82:83]
	v_pk_fma_f32 v[80:81], v[74:75], v[8:9], v[86:87]
	v_pk_fma_f32 v[74:75], v[72:73], v[10:11], v[84:85]
	v_cvt_pk_bf16_f32 v72, v76, v77
	v_cvt_pk_bf16_f32 v73, v78, v79
	v_lshl_add_u64 v[76:77], v[158:159], 1, s[18:19]
	v_pk_fma_f32 v[68:69], v[68:69], v[6:7], v[88:89]
	v_cvt_pk_bf16_f32 v74, v74, v75
	v_cvt_pk_bf16_f32 v75, v80, v81
	global_store_dwordx4 v[76:77], v[72:75], off sc1
	v_pk_fma_f32 v[70:71], v[70:71], v[4:5], v[90:91]
	v_pk_fma_f32 v[52:53], v[52:53], v[6:7], v[104:105]
	v_pk_fma_f32 v[72:73], v[62:63], v[0:1], v[94:95]
	v_pk_fma_f32 v[62:63], v[60:61], v[2:3], v[92:93]
	v_cvt_pk_bf16_f32 v60, v68, v69
	v_cvt_pk_bf16_f32 v61, v70, v71
	v_lshl_add_u64 v[68:69], v[160:161], 1, s[18:19]
	v_cvt_pk_bf16_f32 v62, v62, v63
	v_cvt_pk_bf16_f32 v63, v72, v73
	global_store_dwordx4 v[68:69], v[60:63], off sc1
	v_pk_fma_f32 v[54:55], v[54:55], v[4:5], v[106:107]
	v_pk_fma_f32 v[36:37], v[36:37], v[6:7], v[120:121]
	v_pk_fma_f32 v[60:61], v[66:67], v[12:13], v[98:99]
	v_pk_fma_f32 v[62:63], v[64:65], v[14:15], v[96:97]
	v_pk_fma_f32 v[64:65], v[58:59], v[8:9], v[102:103]
	v_pk_fma_f32 v[58:59], v[56:57], v[10:11], v[100:101]
	v_cvt_pk_bf16_f32 v56, v62, v63
	v_cvt_pk_bf16_f32 v57, v60, v61
	v_lshl_add_u64 v[60:61], v[162:163], 1, s[18:19]
	v_cvt_pk_bf16_f32 v58, v58, v59
	v_cvt_pk_bf16_f32 v59, v64, v65
	global_store_dwordx4 v[60:61], v[56:59], off sc1
	v_pk_fma_f32 v[38:39], v[38:39], v[4:5], v[122:123]
	v_pk_fma_f32 v[26:27], v[26:27], v[8:9], v[134:135]
	v_pk_fma_f32 v[56:57], v[46:47], v[0:1], v[110:111]
	v_pk_fma_f32 v[46:47], v[44:45], v[2:3], v[108:109]
	v_cvt_pk_bf16_f32 v44, v52, v53
	v_cvt_pk_bf16_f32 v45, v54, v55
	v_lshl_add_u64 v[52:53], v[164:165], 1, s[18:19]
	v_cvt_pk_bf16_f32 v46, v46, v47
	v_cvt_pk_bf16_f32 v47, v56, v57
	global_store_dwordx4 v[52:53], v[44:47], off sc1
	v_pk_fma_f32 v[4:5], v[22:23], v[4:5], v[138:139]
	v_pk_fma_f32 v[6:7], v[20:21], v[6:7], v[136:137]
	v_pk_fma_f32 v[44:45], v[50:51], v[12:13], v[114:115]
	v_pk_fma_f32 v[46:47], v[48:49], v[14:15], v[112:113]
	v_pk_fma_f32 v[48:49], v[42:43], v[8:9], v[118:119]
	v_pk_fma_f32 v[42:43], v[40:41], v[10:11], v[116:117]
	v_cvt_pk_bf16_f32 v40, v46, v47
	v_cvt_pk_bf16_f32 v41, v44, v45
	v_lshl_add_u64 v[44:45], v[166:167], 1, s[18:19]
	v_cvt_pk_bf16_f32 v42, v42, v43
	v_cvt_pk_bf16_f32 v43, v48, v49
	global_store_dwordx4 v[44:45], v[40:43], off sc1
	v_pk_fma_f32 v[12:13], v[34:35], v[12:13], v[130:131]
	v_pk_fma_f32 v[14:15], v[32:33], v[14:15], v[128:129]
	v_pk_fma_f32 v[40:41], v[30:31], v[0:1], v[126:127]
	v_pk_fma_f32 v[30:31], v[28:29], v[2:3], v[124:125]
	v_cvt_pk_bf16_f32 v28, v36, v37
	v_lshl_add_u64 v[36:37], v[168:169], 1, s[18:19]
	v_cvt_pk_bf16_f32 v29, v38, v39
	v_cvt_pk_bf16_f32 v30, v30, v31
	v_cvt_pk_bf16_f32 v31, v40, v41
	global_store_dwordx4 v[36:37], v[28:31], off sc1
	v_pk_fma_f32 v[10:11], v[24:25], v[10:11], v[132:133]
	v_cvt_pk_bf16_f32 v8, v14, v15
	v_cvt_pk_bf16_f32 v9, v12, v13
	v_lshl_add_u64 v[12:13], v[170:171], 1, s[18:19]
	v_cvt_pk_bf16_f32 v10, v10, v11
	v_cvt_pk_bf16_f32 v11, v26, v27
	global_store_dwordx4 v[12:13], v[8:11], off sc1
	v_pk_fma_f32 v[2:3], v[16:17], v[2:3], v[140:141]
	s_nop 0
	v_pk_fma_f32 v[8:9], v[18:19], v[0:1], v[142:143]
	v_cvt_pk_bf16_f32 v0, v6, v7
	v_cvt_pk_bf16_f32 v1, v4, v5
	v_lshl_add_u64 v[4:5], v[152:153], 1, s[18:19]
	v_cvt_pk_bf16_f32 v2, v2, v3
	v_cvt_pk_bf16_f32 v3, v8, v9
	global_store_dwordx4 v[4:5], v[0:3], off sc1
	s_mov_b64 s[18:19], s[16:17]
	s_cbranch_vccz .LBB0_978
	s_waitcnt vmcnt(0)
	s_cmpk_gt_u32 s31, 0xff
	s_cbranch_scc1 .LBB0_989
	s_barrier

.LBB0_1060:
	s_waitcnt vmcnt(3)
	v_mul_f32_e32 v4, 0x42800000, v4
	s_waitcnt vmcnt(2)
	v_mul_f32_e32 v8, 0x42800000, v8
	v_med3_f32 v4, v4, s68, v101
	v_med3_f32 v8, v8, s68, v101
	v_mov_b32_e32 v67, v79
	v_cvt_pk_fp8_f32 v67, v4, v8
	s_waitcnt vmcnt(1)
	v_mul_f32_e32 v12, 0x42800000, v12
	s_waitcnt vmcnt(0)
	v_mul_f32_e32 v0, 0x42800000, v0
	v_med3_f32 v4, v12, s68, v101
	v_med3_f32 v0, v0, s68, v101
	v_cvt_pk_fp8_f32 v67, v4, v0 op_sel:[0,0,1]
	v_mul_f32_e32 v0, 0x42800000, v57
	v_mul_f32_e32 v4, 0x42800000, v53
	v_med3_f32 v0, v0, s68, v101
	v_med3_f32 v4, v4, s68, v101
	v_mov_b32_e32 v68, v79
	v_cvt_pk_fp8_f32 v68, v0, v4
	v_mul_f32_e32 v8, 0x42800000, v61
	v_mul_f32_e32 v0, 0x42800000, v45
	v_med3_f32 v4, v8, s68, v101
	v_med3_f32 v0, v0, s68, v101
	v_cvt_pk_fp8_f32 v68, v4, v0 op_sel:[0,0,1]
	v_mul_f32_e32 v0, 0x42800000, v41
	v_mul_f32_e32 v4, 0x42800000, v37
	v_med3_f32 v0, v0, s68, v101
	v_med3_f32 v4, v4, s68, v101
	v_mov_b32_e32 v69, v79
	v_cvt_pk_fp8_f32 v69, v0, v4
	v_mul_f32_e32 v8, 0x42800000, v49
	v_mul_f32_e32 v0, 0x42800000, v33
	v_med3_f32 v4, v8, s68, v101
	v_med3_f32 v0, v0, s68, v101
	v_cvt_pk_fp8_f32 v69, v4, v0 op_sel:[0,0,1]
	v_mul_f32_e32 v0, 0x42800000, v21
	v_mul_f32_e32 v4, 0x42800000, v25
	v_med3_f32 v0, v0, s68, v101
	v_med3_f32 v4, v4, s68, v101
	v_mov_b32_e32 v70, v79
	v_cvt_pk_fp8_f32 v70, v0, v4
	v_mul_f32_e32 v8, 0x42800000, v29
	v_mul_f32_e32 v0, 0x42800000, v17
	v_med3_f32 v4, v8, s68, v101
	v_med3_f32 v0, v0, s68, v101
	v_cvt_pk_fp8_f32 v70, v4, v0 op_sel:[0,0,1]
	v_mul_f32_e32 v0, 0x42800000, v5
	v_mul_f32_e32 v4, 0x42800000, v9
	v_med3_f32 v0, v0, s68, v101
	v_med3_f32 v4, v4, s68, v101
	v_mov_b32_e32 v71, v79
	v_cvt_pk_fp8_f32 v71, v0, v4
	v_mul_f32_e32 v5, 0x42800000, v13
	v_mul_f32_e32 v0, 0x42800000, v1
	v_med3_f32 v1, v5, s68, v101
	v_med3_f32 v0, v0, s68, v101
	v_cvt_pk_fp8_f32 v71, v1, v0 op_sel:[0,0,1]
	v_mul_f32_e32 v0, 0x42800000, v58
	v_mul_f32_e32 v1, 0x42800000, v54
	v_med3_f32 v0, v0, s68, v101
	v_med3_f32 v1, v1, s68, v101
	v_mov_b32_e32 v72, v79
	v_cvt_pk_fp8_f32 v72, v0, v1
	v_mul_f32_e32 v4, 0x42800000, v62
	v_mul_f32_e32 v0, 0x42800000, v46
	v_med3_f32 v1, v4, s68, v101
	v_med3_f32 v0, v0, s68, v101
	v_cvt_pk_fp8_f32 v72, v1, v0 op_sel:[0,0,1]
	v_mul_f32_e32 v0, 0x42800000, v42
	v_mul_f32_e32 v1, 0x42800000, v38
	v_med3_f32 v0, v0, s68, v101
	v_med3_f32 v1, v1, s68, v101
	v_mov_b32_e32 v73, v79
	v_cvt_pk_fp8_f32 v73, v0, v1
	v_mul_f32_e32 v4, 0x42800000, v50
	v_mul_f32_e32 v0, 0x42800000, v34
	v_med3_f32 v1, v4, s68, v101
	v_med3_f32 v0, v0, s68, v101
	v_cvt_pk_fp8_f32 v73, v1, v0 op_sel:[0,0,1]
	v_mul_f32_e32 v0, 0x42800000, v22
	v_mul_f32_e32 v1, 0x42800000, v26
	v_med3_f32 v0, v0, s68, v101
	v_med3_f32 v1, v1, s68, v101
	v_mov_b32_e32 v74, v79
	v_cvt_pk_fp8_f32 v74, v0, v1
	v_mul_f32_e32 v4, 0x42800000, v30
	v_mul_f32_e32 v0, 0x42800000, v18
	v_med3_f32 v1, v4, s68, v101
	v_med3_f32 v0, v0, s68, v101
	v_cvt_pk_fp8_f32 v74, v1, v0 op_sel:[0,0,1]
	v_mul_f32_e32 v0, 0x42800000, v6
	v_mul_f32_e32 v1, 0x42800000, v10
	v_med3_f32 v0, v0, s68, v101
	v_med3_f32 v1, v1, s68, v101
	v_mov_b32_e32 v75, v79
	v_cvt_pk_fp8_f32 v75, v0, v1
	v_mul_f32_e32 v4, 0x42800000, v14
	v_mul_f32_e32 v0, 0x42800000, v2
	v_med3_f32 v1, v4, s68, v101
	v_med3_f32 v0, v0, s68, v101
	v_cvt_pk_fp8_f32 v75, v1, v0 op_sel:[0,0,1]
	v_mul_f32_e32 v0, 0x42800000, v59
	v_mul_f32_e32 v1, 0x42800000, v55
	v_med3_f32 v0, v0, s68, v101
	v_med3_f32 v1, v1, s68, v101
	v_mov_b32_e32 v4, v79
	v_cvt_pk_fp8_f32 v4, v0, v1
	v_mul_f32_e32 v2, 0x42800000, v63
	v_mul_f32_e32 v0, 0x42800000, v47
	v_med3_f32 v1, v2, s68, v101
	v_med3_f32 v0, v0, s68, v101
	v_cvt_pk_fp8_f32 v4, v1, v0 op_sel:[0,0,1]
	v_mul_f32_e32 v0, 0x42800000, v43
	v_mul_f32_e32 v1, 0x42800000, v39
	v_med3_f32 v0, v0, s68, v101
	v_med3_f32 v1, v1, s68, v101
	v_mov_b32_e32 v5, v79
	v_cvt_pk_fp8_f32 v5, v0, v1
	v_mul_f32_e32 v2, 0x42800000, v51
	v_mul_f32_e32 v0, 0x42800000, v35
	v_med3_f32 v1, v2, s68, v101
	v_med3_f32 v0, v0, s68, v101
	v_cvt_pk_fp8_f32 v5, v1, v0 op_sel:[0,0,1]
	v_mul_f32_e32 v0, 0x42800000, v23
	v_mul_f32_e32 v1, 0x42800000, v27
	v_mul_f32_e32 v56, 0x42800000, v56
	v_mul_f32_e32 v52, 0x42800000, v52
	v_med3_f32 v0, v0, s68, v101
	v_med3_f32 v1, v1, s68, v101
	v_mov_b32_e32 v6, v79
	v_med3_f32 v56, v56, s68, v101
	v_med3_f32 v52, v52, s68, v101
	v_mov_b32_e32 v64, v79
	v_cvt_pk_fp8_f32 v6, v0, v1
	v_cvt_pk_fp8_f32 v64, v56, v52
	v_mul_f32_e32 v40, 0x42800000, v40
	v_mul_f32_e32 v36, 0x42800000, v36
	v_mul_f32_e32 v20, 0x42800000, v20
	v_mul_f32_e32 v24, 0x42800000, v24
	v_med3_f32 v40, v40, s68, v101
	v_med3_f32 v36, v36, s68, v101
	v_mov_b32_e32 v65, v79
	v_med3_f32 v20, v20, s68, v101
	v_med3_f32 v24, v24, s68, v101
	v_mov_b32_e32 v66, v79
	v_mul_f32_e32 v2, 0x42800000, v31
	v_mul_f32_e32 v0, 0x42800000, v19
	v_mul_f32_e32 v60, 0x42800000, v60
	v_mul_f32_e32 v44, 0x42800000, v44
	v_cvt_pk_fp8_f32 v65, v40, v36
	v_cvt_pk_fp8_f32 v66, v20, v24
	v_med3_f32 v1, v2, s68, v101
	v_med3_f32 v0, v0, s68, v101
	v_med3_f32 v52, v60, s68, v101
	v_med3_f32 v44, v44, s68, v101
	v_cvt_pk_fp8_f32 v6, v1, v0 op_sel:[0,0,1]
	v_mul_f32_e32 v0, 0x42800000, v7
	v_mul_f32_e32 v1, 0x42800000, v11
	v_cvt_pk_fp8_f32 v64, v52, v44 op_sel:[0,0,1]
	v_mul_f32_e32 v44, 0x42800000, v48
	v_mul_f32_e32 v32, 0x42800000, v32
	v_mul_f32_e32 v28, 0x42800000, v28
	v_mul_f32_e32 v16, 0x42800000, v16
	v_med3_f32 v0, v0, s68, v101
	v_med3_f32 v1, v1, s68, v101
	v_mov_b32_e32 v7, v79
	v_med3_f32 v36, v44, s68, v101
	v_med3_f32 v32, v32, s68, v101
	v_med3_f32 v20, v28, s68, v101
	v_med3_f32 v16, v16, s68, v101
	v_cvt_pk_fp8_f32 v7, v0, v1
	v_cvt_pk_fp8_f32 v65, v36, v32 op_sel:[0,0,1]
	v_cvt_pk_fp8_f32 v66, v20, v16 op_sel:[0,0,1]
	v_mul_f32_e32 v2, 0x42800000, v15
	v_mul_f32_e32 v0, 0x42800000, v3
	v_med3_f32 v1, v2, s68, v101
	v_med3_f32 v0, v0, s68, v101
	v_cvt_pk_fp8_f32 v7, v1, v0 op_sel:[0,0,1]
	s_mul_hi_i32 s3, s2, 0x380000
	s_mul_i32 s2, s2, 0x380000
	ds_write_b128 v98, v[64:67] offset:40960
	ds_write_b128 v98, v[68:71] offset:41040
	ds_write_b128 v98, v[72:75] offset:41120
	ds_write_b128 v98, v[4:7] offset:41200
	s_add_u32 s2, s53, s2
	s_waitcnt lgkmcnt(0)
	s_addc_u32 s3, s54, s3
	s_add_i32 s17, s17, s0
	s_ashr_i32 s0, s24, 31
	ds_read_b128 v[0:3], v99 offset:40960
	s_add_u32 s2, s2, s24
	v_add_u32_e32 v4, s17, v87
	s_addc_u32 s3, s3, s0
	v_ashrrev_i32_e32 v5, 31, v4
	v_lshl_add_u64 v[8:9], s[2:3], 0, v[80:81]
	v_lshlrev_b64 v[4:5], 9, v[4:5]
	v_lshl_add_u64 v[10:11], v[8:9], 0, v[4:5]
	ds_read_b128 v[4:7], v99 offset:42240
	s_waitcnt lgkmcnt(1)
	global_store_dwordx4 v[10:11], v[0:3], off sc1
	s_nop 1
	v_add_u32_e32 v0, s17, v77
	v_ashrrev_i32_e32 v1, 31, v0
	v_lshlrev_b64 v[0:1], 9, v[0:1]
	v_lshl_add_u64 v[0:1], v[8:9], 0, v[0:1]
	s_waitcnt lgkmcnt(0)
	global_store_dwordx4 v[0:1], v[4:7], off sc1
	ds_read_b128 v[0:3], v99 offset:43520
	s_nop 0
	v_add_u32_e32 v4, s17, v88
	v_ashrrev_i32_e32 v5, 31, v4
	v_lshlrev_b64 v[4:5], 9, v[4:5]
	v_lshl_add_u64 v[10:11], v[8:9], 0, v[4:5]
	ds_read_b128 v[4:7], v99 offset:44800
	s_waitcnt lgkmcnt(1)
	global_store_dwordx4 v[10:11], v[0:3], off sc1
	s_nop 1
	v_add_u32_e32 v0, s17, v89
	v_ashrrev_i32_e32 v1, 31, v0
	v_lshlrev_b64 v[0:1], 9, v[0:1]
	v_lshl_add_u64 v[0:1], v[8:9], 0, v[0:1]
	s_waitcnt lgkmcnt(0)
	global_store_dwordx4 v[0:1], v[4:7], off sc1
	s_waitcnt lgkmcnt(0)

.LBB0_1062:
	s_add_i32 s0, s43, 0x1cc0
	s_mul_hi_i32 s2, s0, 0x20d56b39
	s_lshr_b32 s3, s2, 31
	s_ashr_i32 s2, s2, 12
	s_add_i32 s2, s2, s3
	s_mul_i32 s3, s2, 0x7cc0
	s_sub_i32 s38, s0, s3
	s_cmpk_gt_i32 s38, 0x1cbf
	s_mov_b64 s[4:5], -1
	s_cbranch_scc0 .LBB0_1068
	s_add_i32 s7, s38, 0xffffe340
	s_and_b32 s6, s7, 0xff
	s_cmpk_gt_u32 s38, 0x5cbf
	s_cbranch_scc0 .LBB0_1065
	v_mov_b32_e32 v0, s63
	s_add_i32 s0, s38, 0xffffa340
	s_ashr_i32 s3, s2, 31
	ds_read_b64 v[0:1], v0
	s_lshr_b32 s0, s0, 8
	s_lshl_b64 s[4:5], s[2:3], 26
	s_add_u32 s8, s45, s4
	s_addc_u32 s9, s46, s5
	s_lshl_b64 s[4:5], s[0:1], 20
	s_add_u32 s4, s8, s4
	s_addc_u32 s5, s9, s5
	s_waitcnt lgkmcnt(0)
	v_readfirstlane_b32 s16, v0
	s_lshl_b64 s[8:9], s[2:3], 27
	v_readfirstlane_b32 s17, v1
	s_add_u32 s3, s16, s8
	s_addc_u32 s17, s17, s9
	s_lshl_b64 s[8:9], s[0:1], 22
	s_add_u32 s16, s3, s8
	s_addc_u32 s17, s17, s9
	s_lshl_b32 s0, s6, 3
	s_and_b32 s3, s0, 0x7c0
	s_lshl_b32 s0, s38, 6
	s_and_b32 s8, s0, 0x1c0
	v_or_b32_e32 v0, s8, v76
	v_lshlrev_b32_e32 v0, 13, v0
	v_mov_b32_e32 v1, v79
	v_lshl_add_u64 v[0:1], s[16:17], 0, v[0:1]
	s_lshl_b32 s0, s3, 2
	v_lshl_add_u64 v[0:1], v[0:1], 0, s[0:1]
	v_mov_b32_e32 v83, v79
	v_lshl_add_u64 v[60:61], v[0:1], 0, v[82:83]
	v_add_co_u32_e32 v4, vcc, s64, v60
	s_mov_b32 s0, 0x8000
	s_nop 0
	v_addc_co_u32_e32 v5, vcc, 0, v61, vcc
	v_add_co_u32_e32 v8, vcc, s65, v60
	global_load_dwordx4 v[0:3], v[60:61], off nt
	s_nop 0
	global_load_dwordx4 v[4:7], v[4:5], off nt
	v_addc_co_u32_e32 v9, vcc, 0, v61, vcc
	v_add_co_u32_e32 v10, vcc, s66, v60
	v_mov_b32_e32 v64, v79
	s_nop 0
	v_addc_co_u32_e32 v11, vcc, 0, v61, vcc
	v_add_co_u32_e32 v16, vcc, s0, v60
	s_mov_b32 s0, 0xa000
	s_nop 0
	v_addc_co_u32_e32 v17, vcc, 0, v61, vcc
	v_add_co_u32_e32 v20, vcc, s0, v60
	s_mov_b32 s0, 0xc000
	s_nop 0
	v_addc_co_u32_e32 v21, vcc, 0, v61, vcc
	v_add_co_u32_e32 v24, vcc, s0, v60
	s_mov_b32 s0, 0xe000
	s_nop 0
	v_addc_co_u32_e32 v25, vcc, 0, v61, vcc
	global_load_dwordx4 v[12:15], v[8:9], off nt
	s_nop 0
	global_load_dwordx4 v[8:11], v[10:11], off nt
	v_add_co_u32_e32 v26, vcc, s0, v60
	s_mov_b32 s0, 0x10000
	s_nop 0
	v_addc_co_u32_e32 v27, vcc, 0, v61, vcc
	global_load_dwordx4 v[16:19], v[16:17], off nt
	s_nop 0
	global_load_dwordx4 v[20:23], v[20:21], off nt
	v_add_co_u32_e32 v28, vcc, s0, v60
	s_mov_b32 s0, 0x14000
	s_nop 0
	v_addc_co_u32_e32 v29, vcc, 0, v61, vcc
	v_add_co_u32_e32 v36, vcc, s67, v60
	global_load_dwordx4 v[32:35], v[24:25], off nt
	s_nop 0
	global_load_dwordx4 v[24:27], v[26:27], off nt
	v_addc_co_u32_e32 v37, vcc, 0, v61, vcc
	v_add_co_u32_e32 v40, vcc, s0, v60
	s_mov_b32 s0, 0x16000
	s_nop 0
	v_addc_co_u32_e32 v41, vcc, 0, v61, vcc
	global_load_dwordx4 v[28:31], v[28:29], off nt
	s_nop 0
	global_load_dwordx4 v[36:39], v[36:37], off nt
	v_add_co_u32_e32 v42, vcc, s0, v60
	s_mov_b32 s0, 0x18000
	s_nop 0
	v_addc_co_u32_e32 v43, vcc, 0, v61, vcc
	v_add_co_u32_e32 v48, vcc, s0, v60
	s_mov_b32 s0, 0x1a000
	s_nop 0
	v_addc_co_u32_e32 v49, vcc, 0, v61, vcc
	global_load_dwordx4 v[44:47], v[40:41], off nt
	s_nop 0
	global_load_dwordx4 v[40:43], v[42:43], off nt
	v_add_co_u32_e32 v52, vcc, s0, v60
	s_mov_b32 s0, 0x1c000
	s_nop 0
	v_addc_co_u32_e32 v53, vcc, 0, v61, vcc
	global_load_dwordx4 v[48:51], v[48:49], off nt
	s_nop 0
	global_load_dwordx4 v[52:55], v[52:53], off nt
	v_add_co_u32_e32 v56, vcc, s0, v60
	s_mov_b32 s0, 0x1e000
	s_nop 0
	v_addc_co_u32_e32 v57, vcc, 0, v61, vcc
	v_add_co_u32_e32 v60, vcc, s0, v60
	global_load_dwordx4 v[56:59], v[56:57], off nt
	s_nop 0
	v_addc_co_u32_e32 v61, vcc, 0, v61, vcc
	global_load_dwordx4 v[60:63], v[60:61], off nt
	v_mov_b32_e32 v65, v79
	v_mov_b32_e32 v66, v79
	v_mov_b32_e32 v67, v79
	v_mov_b32_e32 v68, v79
	v_mov_b32_e32 v69, v79
	s_waitcnt vmcnt(15)
	v_mul_f32_e32 v0, 0x42000000, v0
	s_waitcnt vmcnt(14)
	v_mul_f32_e32 v4, 0x42000000, v4
	v_med3_f32 v0, v0, s68, v101
	v_med3_f32 v4, v4, s68, v101
	v_cvt_pk_fp8_f32 v64, v0, v4
	v_mov_b32_e32 v70, v79
	v_mov_b32_e32 v71, v79
	v_mov_b32_e32 v72, v79
	v_mov_b32_e32 v73, v79
	v_mov_b32_e32 v74, v79
	v_mov_b32_e32 v75, v79
	s_add_u32 s4, s4, s8
	s_addc_u32 s5, s5, 0
	s_waitcnt vmcnt(13)
	v_mul_f32_e32 v12, 0x42000000, v12
	s_waitcnt vmcnt(12)
	v_mul_f32_e32 v0, 0x42000000, v8
	v_med3_f32 v4, v12, s68, v101
	v_med3_f32 v0, v0, s68, v101
	v_cvt_pk_fp8_f32 v64, v4, v0 op_sel:[0,0,1]
	s_waitcnt vmcnt(11)
	v_mul_f32_e32 v0, 0x42000000, v16
	s_waitcnt vmcnt(10)
	v_mul_f32_e32 v4, 0x42000000, v20
	v_med3_f32 v0, v0, s68, v101
	v_med3_f32 v4, v4, s68, v101
	v_cvt_pk_fp8_f32 v65, v0, v4
	s_waitcnt vmcnt(9)
	v_mul_f32_e32 v8, 0x42000000, v32
	s_waitcnt vmcnt(8)
	v_mul_f32_e32 v0, 0x42000000, v24
	v_med3_f32 v4, v8, s68, v101
	v_med3_f32 v0, v0, s68, v101
	v_cvt_pk_fp8_f32 v65, v4, v0 op_sel:[0,0,1]
	s_waitcnt vmcnt(7)
	v_mul_f32_e32 v0, 0x42000000, v28
	s_waitcnt vmcnt(6)
	v_mul_f32_e32 v4, 0x42000000, v36
	v_med3_f32 v0, v0, s68, v101
	v_med3_f32 v4, v4, s68, v101
	v_cvt_pk_fp8_f32 v66, v0, v4
	s_waitcnt vmcnt(5)
	v_mul_f32_e32 v8, 0x42000000, v44
	s_waitcnt vmcnt(4)
	v_mul_f32_e32 v0, 0x42000000, v40
	v_med3_f32 v4, v8, s68, v101
	v_med3_f32 v0, v0, s68, v101
	v_cvt_pk_fp8_f32 v66, v4, v0 op_sel:[0,0,1]
	s_waitcnt vmcnt(3)
	v_mul_f32_e32 v0, 0x42000000, v48
	s_waitcnt vmcnt(2)
	v_mul_f32_e32 v4, 0x42000000, v52
	v_med3_f32 v0, v0, s68, v101
	v_med3_f32 v4, v4, s68, v101
	v_cvt_pk_fp8_f32 v67, v0, v4
	s_waitcnt vmcnt(1)
	v_mul_f32_e32 v8, 0x42000000, v56
	v_med3_f32 v4, v8, s68, v101
	s_waitcnt vmcnt(0)
	v_mul_f32_e32 v0, 0x42000000, v60
	v_med3_f32 v0, v0, s68, v101
	v_cvt_pk_fp8_f32 v67, v4, v0 op_sel:[0,0,1]
	v_mul_f32_e32 v0, 0x42000000, v1
	v_mul_f32_e32 v1, 0x42000000, v5
	v_med3_f32 v0, v0, s68, v101
	v_med3_f32 v1, v1, s68, v101
	v_cvt_pk_fp8_f32 v68, v0, v1
	v_mul_f32_e32 v4, 0x42000000, v13
	v_mul_f32_e32 v0, 0x42000000, v9
	v_med3_f32 v1, v4, s68, v101
	v_med3_f32 v0, v0, s68, v101
	v_cvt_pk_fp8_f32 v68, v1, v0 op_sel:[0,0,1]
	v_mul_f32_e32 v0, 0x42000000, v17
	v_mul_f32_e32 v1, 0x42000000, v21
	v_med3_f32 v0, v0, s68, v101
	v_med3_f32 v1, v1, s68, v101
	v_cvt_pk_fp8_f32 v69, v0, v1
	v_mul_f32_e32 v4, 0x42000000, v33
	v_mul_f32_e32 v0, 0x42000000, v25
	v_med3_f32 v1, v4, s68, v101
	v_med3_f32 v0, v0, s68, v101
	v_cvt_pk_fp8_f32 v69, v1, v0 op_sel:[0,0,1]
	v_mul_f32_e32 v0, 0x42000000, v29
	v_mul_f32_e32 v1, 0x42000000, v37
	v_med3_f32 v0, v0, s68, v101
	v_med3_f32 v1, v1, s68, v101
	v_cvt_pk_fp8_f32 v70, v0, v1
	v_mul_f32_e32 v4, 0x42000000, v45
	v_mul_f32_e32 v0, 0x42000000, v41
	v_med3_f32 v1, v4, s68, v101
	v_med3_f32 v0, v0, s68, v101
	v_cvt_pk_fp8_f32 v70, v1, v0 op_sel:[0,0,1]
	v_mul_f32_e32 v0, 0x42000000, v49
	v_mul_f32_e32 v1, 0x42000000, v53
	v_med3_f32 v0, v0, s68, v101
	v_med3_f32 v1, v1, s68, v101
	v_cvt_pk_fp8_f32 v71, v0, v1
	v_mul_f32_e32 v4, 0x42000000, v57
	v_mul_f32_e32 v0, 0x42000000, v61
	v_med3_f32 v1, v4, s68, v101
	v_med3_f32 v0, v0, s68, v101
	v_cvt_pk_fp8_f32 v71, v1, v0 op_sel:[0,0,1]
	v_mul_f32_e32 v0, 0x42000000, v2
	v_mul_f32_e32 v1, 0x42000000, v6
	v_med3_f32 v0, v0, s68, v101
	v_med3_f32 v1, v1, s68, v101
	v_cvt_pk_fp8_f32 v72, v0, v1
	v_mul_f32_e32 v2, 0x42000000, v14
	v_mul_f32_e32 v0, 0x42000000, v10
	v_med3_f32 v1, v2, s68, v101
	v_med3_f32 v0, v0, s68, v101
	v_cvt_pk_fp8_f32 v72, v1, v0 op_sel:[0,0,1]
	v_mul_f32_e32 v0, 0x42000000, v18
	v_mul_f32_e32 v1, 0x42000000, v22
	v_med3_f32 v0, v0, s68, v101
	v_med3_f32 v1, v1, s68, v101
	v_cvt_pk_fp8_f32 v73, v0, v1
	v_mul_f32_e32 v2, 0x42000000, v34
	v_mul_f32_e32 v0, 0x42000000, v26
	v_med3_f32 v1, v2, s68, v101
	v_med3_f32 v0, v0, s68, v101
	v_cvt_pk_fp8_f32 v73, v1, v0 op_sel:[0,0,1]
	v_mul_f32_e32 v0, 0x42000000, v30
	v_mul_f32_e32 v1, 0x42000000, v38
	v_med3_f32 v0, v0, s68, v101
	v_med3_f32 v1, v1, s68, v101
	v_cvt_pk_fp8_f32 v74, v0, v1
	v_mul_f32_e32 v2, 0x42000000, v46
	v_mul_f32_e32 v0, 0x42000000, v42
	v_med3_f32 v1, v2, s68, v101
	v_med3_f32 v0, v0, s68, v101
	v_cvt_pk_fp8_f32 v74, v1, v0 op_sel:[0,0,1]
	v_mul_f32_e32 v0, 0x42000000, v50
	v_mul_f32_e32 v1, 0x42000000, v54
	v_med3_f32 v0, v0, s68, v101
	v_med3_f32 v1, v1, s68, v101
	v_cvt_pk_fp8_f32 v75, v0, v1
	v_mul_f32_e32 v2, 0x42000000, v58
	v_mul_f32_e32 v0, 0x42000000, v62
	v_med3_f32 v1, v2, s68, v101
	v_med3_f32 v0, v0, s68, v101
	v_cvt_pk_fp8_f32 v75, v1, v0 op_sel:[0,0,1]
	v_mul_f32_e32 v0, 0x42000000, v3
	v_mul_f32_e32 v1, 0x42000000, v7
	v_med3_f32 v3, v0, s68, v101
	v_med3_f32 v1, v1, s68, v101
	v_mov_b32_e32 v0, v79
	v_cvt_pk_fp8_f32 v0, v3, v1
	v_mul_f32_e32 v2, 0x42000000, v15
	v_mul_f32_e32 v1, 0x42000000, v11
	v_med3_f32 v2, v2, s68, v101
	v_med3_f32 v1, v1, s68, v101
	v_cvt_pk_fp8_f32 v0, v2, v1 op_sel:[0,0,1]
	v_mul_f32_e32 v1, 0x42000000, v19
	v_mul_f32_e32 v2, 0x42000000, v23
	v_med3_f32 v4, v1, s68, v101
	v_med3_f32 v2, v2, s68, v101
	v_mov_b32_e32 v1, v79
	v_cvt_pk_fp8_f32 v1, v4, v2
	v_mul_f32_e32 v3, 0x42000000, v35
	v_mul_f32_e32 v2, 0x42000000, v27
	v_med3_f32 v3, v3, s68, v101
	v_med3_f32 v2, v2, s68, v101
	v_cvt_pk_fp8_f32 v1, v3, v2 op_sel:[0,0,1]
	v_mul_f32_e32 v2, 0x42000000, v31
	v_mul_f32_e32 v3, 0x42000000, v39
	v_med3_f32 v5, v2, s68, v101
	v_med3_f32 v3, v3, s68, v101
	v_mov_b32_e32 v2, v79
	v_cvt_pk_fp8_f32 v2, v5, v3
	v_mul_f32_e32 v4, 0x42000000, v47
	v_mul_f32_e32 v3, 0x42000000, v43
	v_med3_f32 v4, v4, s68, v101
	v_med3_f32 v3, v3, s68, v101
	v_cvt_pk_fp8_f32 v2, v4, v3 op_sel:[0,0,1]
	v_mul_f32_e32 v3, 0x42000000, v51
	v_mul_f32_e32 v4, 0x42000000, v55
	v_med3_f32 v6, v3, s68, v101
	v_med3_f32 v4, v4, s68, v101
	v_mov_b32_e32 v3, v79
	v_cvt_pk_fp8_f32 v3, v6, v4
	v_mul_f32_e32 v5, 0x42000000, v59
	v_mul_f32_e32 v4, 0x42000000, v63
	v_med3_f32 v5, v5, s68, v101
	v_med3_f32 v4, v4, s68, v101
	v_cvt_pk_fp8_f32 v3, v5, v4 op_sel:[0,0,1]
	ds_write_b128 v98, v[64:67] offset:40960
	ds_write_b128 v98, v[68:71] offset:41040
	ds_write_b128 v98, v[72:75] offset:41120
	ds_write_b128 v98, v[0:3] offset:41200
	s_waitcnt lgkmcnt(0)
	ds_read_b128 v[0:3], v99 offset:40960
	v_or_b32_e32 v4, s3, v87
	v_lshl_add_u64 v[8:9], s[4:5], 0, v[80:81]
	v_lshlrev_b32_e32 v4, 9, v4
	v_mov_b32_e32 v5, v79
	v_lshl_add_u64 v[10:11], v[8:9], 0, v[4:5]
	ds_read_b128 v[4:7], v99 offset:42240
	s_waitcnt lgkmcnt(1)
	global_store_dwordx4 v[10:11], v[0:3], off sc1
	s_mov_b64 s[4:5], 0
	s_nop 0
	v_or_b32_e32 v0, s3, v77
	v_lshlrev_b32_e32 v0, 9, v0
	v_mov_b32_e32 v1, v79
	v_lshl_add_u64 v[0:1], v[8:9], 0, v[0:1]
	s_waitcnt lgkmcnt(0)
	global_store_dwordx4 v[0:1], v[4:7], off sc1
	ds_read_b128 v[0:3], v99 offset:43520
	s_nop 0
	v_or_b32_e32 v4, s3, v88
	v_lshlrev_b32_e32 v4, 9, v4
	v_mov_b32_e32 v5, v79
	v_lshl_add_u64 v[10:11], v[8:9], 0, v[4:5]
	ds_read_b128 v[4:7], v99 offset:44800
	s_waitcnt lgkmcnt(1)
	global_store_dwordx4 v[10:11], v[0:3], off sc1
	s_nop 1
	v_or_b32_e32 v0, s3, v89
	v_lshlrev_b32_e32 v0, 9, v0
	v_mov_b32_e32 v1, v79
	v_lshl_add_u64 v[0:1], v[8:9], 0, v[0:1]
	s_waitcnt lgkmcnt(0)
	global_store_dwordx4 v[0:1], v[4:7], off sc1
	s_waitcnt lgkmcnt(0)
.LBB0_1065:
	s_andn2_b64 vcc, exec, s[4:5]
	s_cbranch_vccnz .LBB0_1067
	s_ashr_i32 s3, s2, 31
	s_lshr_b32 s0, s7, 9
	s_bfe_u32 s7, s7, 0x10008
	s_lshl_b64 s[8:9], s[2:3], 27
	s_add_u32 s3, s47, s8
	s_addc_u32 s16, s48, s9
	s_lshl_b32 s17, s7, 18
	s_lshl_b64 s[4:5], s[0:1], 21
	s_add_u32 s3, s3, s4
	s_addc_u32 s4, s16, s5
	s_add_u32 s3, s3, s17
	s_addc_u32 s4, s4, 0
	s_lshl_b32 s5, s7, 3
	s_add_i32 s5, s5, 0
	s_add_i32 s5, s5, 0x204e8
	v_mov_b32_e32 v0, s5
	ds_read_b64 v[0:1], v0
	v_mov_b32_e32 v83, v79
	v_mov_b32_e32 v12, v79
	v_mov_b32_e32 v14, v79
	v_mov_b32_e32 v13, v79
	s_waitcnt lgkmcnt(0)
	v_readfirstlane_b32 s5, v0
	v_readfirstlane_b32 s7, v1
	s_add_u32 s5, s5, s8
	s_addc_u32 s7, s7, s9
	s_lshl_b64 s[8:9], s[0:1], 22
	s_add_u32 s8, s5, s8
	s_addc_u32 s9, s7, s9
	s_lshl_b32 s0, s38, 6
	s_and_b32 s5, s0, 0x7c0
	v_or_b32_e32 v0, s5, v76
	v_lshlrev_b32_e32 v0, 11, v0
	v_mov_b32_e32 v1, v79
	s_lshl_b32 s0, s6, 3
	v_lshl_add_u64 v[0:1], s[8:9], 0, v[0:1]
	s_and_b32 s0, s0, 0x700
	v_lshl_add_u64 v[0:1], v[0:1], 0, s[0:1]
	v_lshl_add_u64 v[0:1], v[0:1], 0, v[82:83]
	s_movk_i32 s0, 0x1000
	v_add_co_u32_e32 v2, vcc, s0, v0
	global_load_dwordx4 v[36:39], v[0:1], off nt
	global_load_dwordx4 v[40:43], v[0:1], off offset:2048 nt
	v_addc_co_u32_e32 v3, vcc, 0, v1, vcc
	v_add_co_u32_e32 v4, vcc, s64, v0
	v_mov_b32_e32 v68, v79
	s_nop 0
	v_addc_co_u32_e32 v5, vcc, 0, v1, vcc
	global_load_dwordx4 v[56:59], v[4:5], off offset:-4096 nt
	global_load_dwordx4 v[20:23], v[4:5], off nt
	global_load_dwordx4 v[24:27], v[4:5], off offset:2048 nt
	v_add_co_u32_e32 v4, vcc, s69, v0
	v_mov_b32_e32 v69, v79
	s_nop 0
	v_addc_co_u32_e32 v5, vcc, 0, v1, vcc
	v_add_co_u32_e32 v6, vcc, s65, v0
	v_mov_b32_e32 v70, v79
	s_nop 0
	v_addc_co_u32_e32 v7, vcc, 0, v1, vcc
	global_load_dwordx4 v[64:67], v[2:3], off offset:2048 nt
	global_load_dwordx4 v[44:47], v[4:5], off offset:2048 nt
	global_load_dwordx4 v[60:63], v[6:7], off offset:-4096 nt
	global_load_dwordx4 v[16:19], v[6:7], off nt
	v_add_co_u32_e32 v2, vcc, s70, v0
	v_mov_b32_e32 v71, v79
	s_nop 0
	v_addc_co_u32_e32 v3, vcc, 0, v1, vcc
	v_add_co_u32_e32 v8, vcc, s66, v0
	v_mov_b32_e32 v72, v79
	s_nop 0
	v_addc_co_u32_e32 v9, vcc, 0, v1, vcc
	global_load_dwordx4 v[48:51], v[6:7], off offset:2048 nt
	global_load_dwordx4 v[52:55], v[8:9], off offset:-4096 nt
	global_load_dwordx4 v[28:31], v[2:3], off offset:2048 nt
	s_nop 0
	global_load_dwordx4 v[4:7], v[8:9], off nt
	s_nop 0
	global_load_dwordx4 v[8:11], v[8:9], off offset:2048 nt
	v_add_co_u32_e32 v0, vcc, s71, v0
	v_mov_b32_e32 v73, v79
	s_nop 0
	v_addc_co_u32_e32 v1, vcc, 0, v1, vcc
	global_load_dwordx4 v[32:35], v[0:1], off nt
	s_nop 0
	global_load_dwordx4 v[0:3], v[0:1], off offset:2048 nt
	v_mov_b32_e32 v74, v79
	v_mov_b32_e32 v75, v79
	s_lshl_b32 s0, s6, 1
	s_add_u32 s8, s3, s5
	s_addc_u32 s9, s4, 0
	s_lshl_b32 s3, s6, 2
	s_and_b32 s3, s3, 0x300
	s_and_b32 s0, s0, 64
	s_or_b32 s0, s0, s3
	s_waitcnt vmcnt(15)
	v_mul_f32_e32 v15, 0x42800000, v36
	s_waitcnt vmcnt(14)
	v_mul_f32_e32 v36, 0x42800000, v40
	v_med3_f32 v15, v15, s68, v101
	v_med3_f32 v36, v36, s68, v101
	v_cvt_pk_fp8_f32 v12, v15, v36
	s_waitcnt vmcnt(13)
	v_mul_f32_e32 v40, 0x42800000, v56
	s_waitcnt vmcnt(12)
	v_mul_f32_e32 v20, 0x42800000, v20
	s_waitcnt vmcnt(11)
	v_mul_f32_e32 v24, 0x42800000, v24
	v_med3_f32 v15, v20, s68, v101
	v_med3_f32 v20, v24, s68, v101
	v_cvt_pk_fp8_f32 v13, v15, v20
	v_med3_f32 v40, v40, s68, v101
	s_waitcnt vmcnt(10)
	v_mul_f32_e32 v56, 0x42800000, v64
	s_waitcnt vmcnt(9)
	v_mul_f32_e32 v44, 0x42800000, v44
	v_med3_f32 v36, v44, s68, v101
	s_waitcnt vmcnt(7)
	v_mul_f32_e32 v16, 0x42800000, v16
	v_med3_f32 v16, v16, s68, v101
	v_mul_f32_e32 v60, 0x42800000, v60
	v_med3_f32 v56, v56, s68, v101
	v_med3_f32 v24, v60, s68, v101
	v_cvt_pk_fp8_f32 v12, v40, v56 op_sel:[0,0,1]
	v_cvt_pk_fp8_f32 v13, v24, v36 op_sel:[0,0,1]
	s_waitcnt vmcnt(6)
	v_mul_f32_e32 v48, 0x42800000, v48
	v_med3_f32 v44, v48, s68, v101
	v_cvt_pk_fp8_f32 v14, v16, v44
	s_waitcnt vmcnt(5)
	v_mul_f32_e32 v52, 0x42800000, v52
	s_waitcnt vmcnt(4)
	v_mul_f32_e32 v28, 0x42800000, v28
	s_waitcnt vmcnt(3)
	v_mul_f32_e32 v4, 0x42800000, v4
	s_waitcnt vmcnt(2)
	v_mul_f32_e32 v8, 0x42800000, v8
	v_med3_f32 v48, v52, s68, v101
	v_med3_f32 v15, v28, s68, v101
	v_cvt_pk_fp8_f32 v14, v48, v15 op_sel:[0,0,1]
	v_med3_f32 v4, v4, s68, v101
	v_med3_f32 v8, v8, s68, v101
	v_mov_b32_e32 v15, v79
	v_cvt_pk_fp8_f32 v15, v4, v8
	s_waitcnt vmcnt(1)
	v_mul_f32_e32 v16, 0x42800000, v32
	s_waitcnt vmcnt(0)
	v_mul_f32_e32 v0, 0x42800000, v0
	v_med3_f32 v4, v16, s68, v101
	v_med3_f32 v0, v0, s68, v101
	v_cvt_pk_fp8_f32 v15, v4, v0 op_sel:[0,0,1]
	v_mul_f32_e32 v0, 0x42800000, v37
	v_mul_f32_e32 v4, 0x42800000, v41
	v_med3_f32 v0, v0, s68, v101
	v_med3_f32 v4, v4, s68, v101
	v_cvt_pk_fp8_f32 v68, v0, v4
	v_mul_f32_e32 v8, 0x42800000, v57
	v_mul_f32_e32 v0, 0x42800000, v65
	v_med3_f32 v4, v8, s68, v101
	v_med3_f32 v0, v0, s68, v101
	v_cvt_pk_fp8_f32 v68, v4, v0 op_sel:[0,0,1]
	v_mul_f32_e32 v0, 0x42800000, v21
	v_mul_f32_e32 v4, 0x42800000, v25
	v_med3_f32 v0, v0, s68, v101
	v_med3_f32 v4, v4, s68, v101
	v_cvt_pk_fp8_f32 v69, v0, v4
	v_mul_f32_e32 v8, 0x42800000, v61
	v_mul_f32_e32 v0, 0x42800000, v45
	v_med3_f32 v4, v8, s68, v101
	v_med3_f32 v0, v0, s68, v101
	v_cvt_pk_fp8_f32 v69, v4, v0 op_sel:[0,0,1]
	v_mul_f32_e32 v0, 0x42800000, v17
	v_mul_f32_e32 v4, 0x42800000, v49
	v_med3_f32 v0, v0, s68, v101
	v_med3_f32 v4, v4, s68, v101
	v_cvt_pk_fp8_f32 v70, v0, v4
	v_mul_f32_e32 v8, 0x42800000, v53
	v_mul_f32_e32 v0, 0x42800000, v29
	v_med3_f32 v4, v8, s68, v101
	v_med3_f32 v0, v0, s68, v101
	v_cvt_pk_fp8_f32 v70, v4, v0 op_sel:[0,0,1]
	v_mul_f32_e32 v0, 0x42800000, v5
	v_mul_f32_e32 v4, 0x42800000, v9
	v_med3_f32 v0, v0, s68, v101
	v_med3_f32 v4, v4, s68, v101
	v_cvt_pk_fp8_f32 v71, v0, v4
	v_mul_f32_e32 v5, 0x42800000, v33
	v_mul_f32_e32 v0, 0x42800000, v1
	v_med3_f32 v1, v5, s68, v101
	v_med3_f32 v0, v0, s68, v101
	v_cvt_pk_fp8_f32 v71, v1, v0 op_sel:[0,0,1]
	v_mul_f32_e32 v0, 0x42800000, v38
	v_mul_f32_e32 v1, 0x42800000, v42
	v_med3_f32 v0, v0, s68, v101
	v_med3_f32 v1, v1, s68, v101
	v_cvt_pk_fp8_f32 v72, v0, v1
	v_mul_f32_e32 v4, 0x42800000, v58
	v_mul_f32_e32 v0, 0x42800000, v66
	v_med3_f32 v1, v4, s68, v101
	v_med3_f32 v0, v0, s68, v101
	v_cvt_pk_fp8_f32 v72, v1, v0 op_sel:[0,0,1]
	v_mul_f32_e32 v0, 0x42800000, v22
	v_mul_f32_e32 v1, 0x42800000, v26
	v_med3_f32 v0, v0, s68, v101
	v_med3_f32 v1, v1, s68, v101
	v_cvt_pk_fp8_f32 v73, v0, v1
	v_mul_f32_e32 v4, 0x42800000, v62
	v_mul_f32_e32 v0, 0x42800000, v46
	v_med3_f32 v1, v4, s68, v101
	v_med3_f32 v0, v0, s68, v101
	v_cvt_pk_fp8_f32 v73, v1, v0 op_sel:[0,0,1]
	v_mul_f32_e32 v0, 0x42800000, v18
	v_mul_f32_e32 v1, 0x42800000, v50
	v_med3_f32 v0, v0, s68, v101
	v_med3_f32 v1, v1, s68, v101
	v_cvt_pk_fp8_f32 v74, v0, v1
	v_mul_f32_e32 v4, 0x42800000, v54
	v_mul_f32_e32 v0, 0x42800000, v30
	v_med3_f32 v1, v4, s68, v101
	v_med3_f32 v0, v0, s68, v101
	v_cvt_pk_fp8_f32 v74, v1, v0 op_sel:[0,0,1]
	v_mul_f32_e32 v0, 0x42800000, v6
	v_mul_f32_e32 v1, 0x42800000, v10
	v_med3_f32 v0, v0, s68, v101
	v_med3_f32 v1, v1, s68, v101
	v_cvt_pk_fp8_f32 v75, v0, v1
	v_mul_f32_e32 v4, 0x42800000, v34
	v_mul_f32_e32 v0, 0x42800000, v2
	v_med3_f32 v1, v4, s68, v101
	v_med3_f32 v0, v0, s68, v101
	v_cvt_pk_fp8_f32 v75, v1, v0 op_sel:[0,0,1]
	v_mul_f32_e32 v0, 0x42800000, v39
	v_mul_f32_e32 v1, 0x42800000, v43
	v_med3_f32 v0, v0, s68, v101
	v_med3_f32 v1, v1, s68, v101
	v_mov_b32_e32 v4, v79
	v_cvt_pk_fp8_f32 v4, v0, v1
	v_mul_f32_e32 v2, 0x42800000, v59
	v_mul_f32_e32 v0, 0x42800000, v67
	v_med3_f32 v1, v2, s68, v101
	v_med3_f32 v0, v0, s68, v101
	v_cvt_pk_fp8_f32 v4, v1, v0 op_sel:[0,0,1]
	v_mul_f32_e32 v0, 0x42800000, v23
	v_mul_f32_e32 v1, 0x42800000, v27
	v_med3_f32 v0, v0, s68, v101
	v_med3_f32 v1, v1, s68, v101
	v_mov_b32_e32 v5, v79
	v_cvt_pk_fp8_f32 v5, v0, v1
	v_mul_f32_e32 v2, 0x42800000, v63
	v_mul_f32_e32 v0, 0x42800000, v47
	v_med3_f32 v1, v2, s68, v101
	v_med3_f32 v0, v0, s68, v101
	v_cvt_pk_fp8_f32 v5, v1, v0 op_sel:[0,0,1]
	v_mul_f32_e32 v0, 0x42800000, v19
	v_mul_f32_e32 v1, 0x42800000, v51
	v_med3_f32 v0, v0, s68, v101
	v_med3_f32 v1, v1, s68, v101
	v_mov_b32_e32 v6, v79
	v_cvt_pk_fp8_f32 v6, v0, v1
	v_mul_f32_e32 v2, 0x42800000, v55
	v_mul_f32_e32 v0, 0x42800000, v31
	v_med3_f32 v1, v2, s68, v101
	v_med3_f32 v0, v0, s68, v101
	v_cvt_pk_fp8_f32 v6, v1, v0 op_sel:[0,0,1]
	v_mul_f32_e32 v0, 0x42800000, v7
	v_mul_f32_e32 v1, 0x42800000, v11
	v_med3_f32 v0, v0, s68, v101
	v_med3_f32 v1, v1, s68, v101
	v_mov_b32_e32 v7, v79
	v_cvt_pk_fp8_f32 v7, v0, v1
	v_mul_f32_e32 v2, 0x42800000, v35
	v_mul_f32_e32 v0, 0x42800000, v3
	v_med3_f32 v1, v2, s68, v101
	v_med3_f32 v0, v0, s68, v101
	v_cvt_pk_fp8_f32 v7, v1, v0 op_sel:[0,0,1]
	ds_write_b128 v98, v[12:15] offset:40960
	ds_write_b128 v98, v[68:71] offset:41040
	ds_write_b128 v98, v[72:75] offset:41120
	ds_write_b128 v98, v[4:7] offset:41200
	s_waitcnt lgkmcnt(0)
	ds_read_b128 v[0:3], v99 offset:40960
	v_or_b32_e32 v4, s0, v87
	v_lshl_add_u64 v[8:9], s[8:9], 0, v[80:81]
	v_lshlrev_b32_e32 v4, 11, v4
	v_mov_b32_e32 v5, v79
	v_lshl_add_u64 v[10:11], v[8:9], 0, v[4:5]
	ds_read_b128 v[4:7], v99 offset:42240
	s_waitcnt lgkmcnt(1)
	global_store_dwordx4 v[10:11], v[0:3], off sc1
	s_nop 1
	v_or_b32_e32 v0, s0, v77
	v_lshlrev_b32_e32 v0, 11, v0
	v_mov_b32_e32 v1, v79
	v_lshl_add_u64 v[0:1], v[8:9], 0, v[0:1]
	s_waitcnt lgkmcnt(0)
	global_store_dwordx4 v[0:1], v[4:7], off sc1
	ds_read_b128 v[0:3], v99 offset:43520
	s_nop 0
	v_or_b32_e32 v4, s0, v88
	v_lshlrev_b32_e32 v4, 11, v4
	v_mov_b32_e32 v5, v79
	v_lshl_add_u64 v[10:11], v[8:9], 0, v[4:5]
	ds_read_b128 v[4:7], v99 offset:44800
	s_waitcnt lgkmcnt(1)
	global_store_dwordx4 v[10:11], v[0:3], off sc1
	s_nop 1
	v_or_b32_e32 v0, s0, v89
	v_lshlrev_b32_e32 v0, 11, v0
	v_mov_b32_e32 v1, v79
	v_lshl_add_u64 v[0:1], v[8:9], 0, v[0:1]
	s_waitcnt lgkmcnt(0)
	global_store_dwordx4 v[0:1], v[4:7], off sc1
	s_waitcnt lgkmcnt(0)

.LBB0_1097:
	s_cmpk_gt_i32 s94, 0x93
	s_cbranch_scc1 .LBB0_1099
	s_lshl_b32 s30, s3, 6
	s_mul_i32 s31, s2, 0x1280000
	v_or_b32_e32 v0, s30, v76
	s_mul_hi_i32 s23, s2, 0x1280000
	s_add_u32 s31, s57, s31
	v_mul_hi_i32_i24_e32 v1, 0x9500, v0
	v_mul_i32_i24_e32 v0, 0x9500, v0
	s_addc_u32 s38, s58, s23
	v_lshl_add_u64 v[0:1], s[4:5], 0, v[0:1]
	s_ashr_i32 s23, s22, 31
	v_lshl_add_u64 v[0:1], s[22:23], 2, v[0:1]
	v_mov_b32_e32 v83, v79
	v_lshl_add_u64 v[56:57], v[0:1], 0, v[82:83]
	v_add_co_u32_e32 v4, vcc, s79, v56
	global_load_dwordx4 v[0:3], v[56:57], off nt
	s_nop 0
	v_addc_co_u32_e32 v5, vcc, 0, v57, vcc
	global_load_dwordx4 v[16:19], v[4:5], off offset:1280 nt
	v_add_co_u32_e32 v4, vcc, s67, v56
	v_mov_b32_e32 v64, v79
	s_nop 0
	v_addc_co_u32_e32 v5, vcc, 0, v57, vcc
	global_load_dwordx4 v[20:23], v[4:5], off offset:2560 nt
	v_add_co_u32_e32 v4, vcc, s80, v56
	v_mov_b32_e32 v65, v79
	s_nop 0
	v_addc_co_u32_e32 v5, vcc, 0, v57, vcc
	global_load_dwordx4 v[44:47], v[4:5], off offset:3840 nt
	v_add_co_u32_e32 v4, vcc, s81, v56
	v_mov_b32_e32 v66, v79
	s_nop 0
	v_addc_co_u32_e32 v5, vcc, 0, v57, vcc
	v_add_co_u32_e32 v8, vcc, s82, v56
	global_load_dwordx4 v[4:7], v[4:5], off offset:1024 nt
	s_nop 0
	v_addc_co_u32_e32 v9, vcc, 0, v57, vcc
	global_load_dwordx4 v[24:27], v[8:9], off offset:2304 nt
	v_add_co_u32_e32 v8, vcc, s83, v56
	v_mov_b32_e32 v67, v79
	s_nop 0
	v_addc_co_u32_e32 v9, vcc, 0, v57, vcc
	global_load_dwordx4 v[28:31], v[8:9], off offset:3584 nt
	v_add_co_u32_e32 v8, vcc, s84, v56
	s_ashr_i32 s23, s30, 31
	s_nop 0
	v_addc_co_u32_e32 v9, vcc, 0, v57, vcc
	global_load_dwordx4 v[52:55], v[8:9], off offset:768 nt
	v_add_co_u32_e32 v8, vcc, s85, v56
	s_add_u32 s30, s31, s30
	s_nop 0
	v_addc_co_u32_e32 v9, vcc, 0, v57, vcc
	v_add_co_u32_e32 v12, vcc, s86, v56
	global_load_dwordx4 v[8:11], v[8:9], off offset:2048 nt
	s_nop 0
	v_addc_co_u32_e32 v13, vcc, 0, v57, vcc
	global_load_dwordx4 v[32:35], v[12:13], off offset:3328 nt
	v_add_co_u32_e32 v12, vcc, s87, v56
	s_addc_u32 s31, s38, s23
	s_nop 0
	v_addc_co_u32_e32 v13, vcc, 0, v57, vcc
	global_load_dwordx4 v[36:39], v[12:13], off offset:512 nt
	v_add_co_u32_e32 v12, vcc, s88, v56
	s_mov_b64 s[38:39], 0
	s_nop 0
	v_addc_co_u32_e32 v13, vcc, 0, v57, vcc
	global_load_dwordx4 v[60:63], v[12:13], off offset:1792 nt
	v_add_co_u32_e32 v12, vcc, s89, v56
	s_waitcnt vmcnt(11)
	v_mul_f32_e32 v0, 0x42800000, v0
	v_addc_co_u32_e32 v13, vcc, 0, v57, vcc
	v_add_co_u32_e32 v40, vcc, s90, v56
	global_load_dwordx4 v[12:15], v[12:13], off offset:3072 nt
	s_nop 0
	v_addc_co_u32_e32 v41, vcc, 0, v57, vcc
	global_load_dwordx4 v[40:43], v[40:41], off offset:256 nt
	v_add_co_u32_e32 v48, vcc, s91, v56
	s_waitcnt vmcnt(12)
	v_mul_f32_e32 v16, 0x42800000, v16
	v_addc_co_u32_e32 v49, vcc, 0, v57, vcc
	v_add_co_u32_e32 v56, vcc, s92, v56
	global_load_dwordx4 v[48:51], v[48:49], off offset:1536 nt
	s_nop 0
	v_addc_co_u32_e32 v57, vcc, 0, v57, vcc
	global_load_dwordx4 v[56:59], v[56:57], off offset:2816 nt
	v_med3_f32 v0, v0, s68, v101
	v_med3_f32 v16, v16, s68, v101
	v_cvt_pk_fp8_f32 v64, v0, v16
	s_waitcnt vmcnt(11)
	v_mul_f32_e32 v0, 0x42800000, v4
	v_med3_f32 v0, v0, s68, v101
	v_mul_f32_e32 v20, 0x42800000, v20
	s_waitcnt vmcnt(10)
	v_mul_f32_e32 v4, 0x42800000, v24
	v_med3_f32 v4, v4, s68, v101
	v_mul_f32_e32 v44, 0x42800000, v44
	v_cvt_pk_fp8_f32 v65, v0, v4
	v_med3_f32 v20, v20, s68, v101
	v_med3_f32 v44, v44, s68, v101
	v_cvt_pk_fp8_f32 v64, v20, v44 op_sel:[0,0,1]
	s_waitcnt vmcnt(9)
	v_mul_f32_e32 v16, 0x42800000, v28
	v_med3_f32 v16, v16, s68, v101
	s_waitcnt vmcnt(8)
	v_mul_f32_e32 v20, 0x42800000, v52
	v_med3_f32 v20, v20, s68, v101
	v_cvt_pk_fp8_f32 v65, v16, v20 op_sel:[0,0,1]
	s_waitcnt vmcnt(7)
	v_mul_f32_e32 v0, 0x42800000, v8
	v_med3_f32 v0, v0, s68, v101
	s_waitcnt vmcnt(6)
	v_mul_f32_e32 v4, 0x42800000, v32
	v_med3_f32 v4, v4, s68, v101
	v_cvt_pk_fp8_f32 v66, v0, v4
	s_waitcnt vmcnt(5)
	v_mul_f32_e32 v8, 0x42800000, v36
	v_med3_f32 v8, v8, s68, v101
	s_waitcnt vmcnt(4)
	v_mul_f32_e32 v16, 0x42800000, v60
	v_med3_f32 v16, v16, s68, v101
	v_cvt_pk_fp8_f32 v66, v8, v16 op_sel:[0,0,1]
	s_waitcnt vmcnt(3)
	v_mul_f32_e32 v0, 0x42800000, v12
	v_med3_f32 v0, v0, s68, v101
	s_waitcnt vmcnt(2)
	v_mul_f32_e32 v4, 0x42800000, v40
	v_med3_f32 v4, v4, s68, v101
	v_cvt_pk_fp8_f32 v67, v0, v4
	v_mul_f32_e32 v0, 0x42800000, v1
	v_mul_f32_e32 v1, 0x42800000, v17
	v_med3_f32 v0, v0, s68, v101
	v_med3_f32 v1, v1, s68, v101
	v_mul_f32_e32 v4, 0x42800000, v21
	s_waitcnt vmcnt(1)
	v_mul_f32_e32 v8, 0x42800000, v48
	v_med3_f32 v8, v8, s68, v101
	v_med3_f32 v4, v4, s68, v101
	s_waitcnt vmcnt(0)
	v_mul_f32_e32 v12, 0x42800000, v56
	v_med3_f32 v12, v12, s68, v101
	v_cvt_pk_fp8_f32 v67, v8, v12 op_sel:[0,0,1]
	v_mul_f32_e32 v8, 0x42800000, v45
	v_med3_f32 v8, v8, s68, v101
	ds_write_b128 v98, v[64:67] offset:40960
	v_mov_b32_e32 v64, v79
	v_cvt_pk_fp8_f32 v64, v0, v1
	v_mul_f32_e32 v0, 0x42800000, v5
	v_mul_f32_e32 v1, 0x42800000, v25
	v_med3_f32 v0, v0, s68, v101
	v_med3_f32 v1, v1, s68, v101
	v_mov_b32_e32 v65, v79
	v_cvt_pk_fp8_f32 v65, v0, v1
	v_mul_f32_e32 v0, 0x42800000, v9
	v_mul_f32_e32 v1, 0x42800000, v33
	v_med3_f32 v0, v0, s68, v101
	v_med3_f32 v1, v1, s68, v101
	v_mov_b32_e32 v66, v79
	v_cvt_pk_fp8_f32 v64, v4, v8 op_sel:[0,0,1]
	v_mul_f32_e32 v4, 0x42800000, v29
	v_mul_f32_e32 v5, 0x42800000, v53
	v_cvt_pk_fp8_f32 v66, v0, v1
	v_mul_f32_e32 v0, 0x42800000, v13
	v_mul_f32_e32 v1, 0x42800000, v41
	v_med3_f32 v4, v4, s68, v101
	v_med3_f32 v5, v5, s68, v101
	v_med3_f32 v0, v0, s68, v101
	v_med3_f32 v1, v1, s68, v101
	v_mov_b32_e32 v67, v79
	v_cvt_pk_fp8_f32 v65, v4, v5 op_sel:[0,0,1]
	v_mul_f32_e32 v4, 0x42800000, v37
	v_mul_f32_e32 v5, 0x42800000, v61
	v_cvt_pk_fp8_f32 v67, v0, v1
	v_med3_f32 v4, v4, s68, v101
	v_med3_f32 v5, v5, s68, v101
	v_cvt_pk_fp8_f32 v66, v4, v5 op_sel:[0,0,1]
	v_mul_f32_e32 v4, 0x42800000, v49
	v_mul_f32_e32 v5, 0x42800000, v57
	v_med3_f32 v4, v4, s68, v101
	v_med3_f32 v5, v5, s68, v101
	v_cvt_pk_fp8_f32 v67, v4, v5 op_sel:[0,0,1]
	v_mul_f32_e32 v0, 0x42800000, v2
	v_mul_f32_e32 v1, 0x42800000, v18
	v_med3_f32 v0, v0, s68, v101
	ds_write_b128 v98, v[64:67] offset:41040
	v_med3_f32 v1, v1, s68, v101
	v_mov_b32_e32 v64, v79
	v_cvt_pk_fp8_f32 v64, v0, v1
	v_mul_f32_e32 v0, 0x42800000, v6
	v_mul_f32_e32 v1, 0x42800000, v26
	v_med3_f32 v0, v0, s68, v101
	v_med3_f32 v1, v1, s68, v101
	v_mov_b32_e32 v65, v79
	v_mul_f32_e32 v2, 0x42800000, v22
	v_mul_f32_e32 v4, 0x42800000, v46
	v_cvt_pk_fp8_f32 v65, v0, v1
	v_mul_f32_e32 v0, 0x42800000, v10
	v_mul_f32_e32 v1, 0x42800000, v34
	v_med3_f32 v2, v2, s68, v101
	v_med3_f32 v4, v4, s68, v101
	v_med3_f32 v0, v0, s68, v101
	v_med3_f32 v1, v1, s68, v101
	v_mov_b32_e32 v66, v79
	v_cvt_pk_fp8_f32 v64, v2, v4 op_sel:[0,0,1]
	v_mul_f32_e32 v2, 0x42800000, v30
	v_mul_f32_e32 v4, 0x42800000, v54
	v_cvt_pk_fp8_f32 v66, v0, v1
	v_mul_f32_e32 v0, 0x42800000, v14
	v_mul_f32_e32 v1, 0x42800000, v42
	v_med3_f32 v2, v2, s68, v101
	v_med3_f32 v4, v4, s68, v101
	v_med3_f32 v0, v0, s68, v101
	v_med3_f32 v1, v1, s68, v101
	v_mov_b32_e32 v67, v79
	v_cvt_pk_fp8_f32 v65, v2, v4 op_sel:[0,0,1]
	v_mul_f32_e32 v2, 0x42800000, v38
	v_mul_f32_e32 v4, 0x42800000, v62
	v_cvt_pk_fp8_f32 v67, v0, v1
	v_med3_f32 v2, v2, s68, v101
	v_med3_f32 v4, v4, s68, v101
	v_cvt_pk_fp8_f32 v66, v2, v4 op_sel:[0,0,1]
	v_mul_f32_e32 v2, 0x42800000, v50
	v_mul_f32_e32 v4, 0x42800000, v58
	v_med3_f32 v2, v2, s68, v101
	v_med3_f32 v4, v4, s68, v101
	v_mul_f32_e32 v0, 0x42800000, v3
	v_mul_f32_e32 v1, 0x42800000, v19
	v_cvt_pk_fp8_f32 v67, v2, v4 op_sel:[0,0,1]
	v_med3_f32 v4, v0, s68, v101
	v_med3_f32 v1, v1, s68, v101
	v_mov_b32_e32 v0, v79
	v_cvt_pk_fp8_f32 v0, v4, v1
	v_mul_f32_e32 v2, 0x42800000, v23
	v_mul_f32_e32 v3, 0x42800000, v47
	v_med3_f32 v2, v2, s68, v101
	v_med3_f32 v3, v3, s68, v101
	v_cvt_pk_fp8_f32 v0, v2, v3 op_sel:[0,0,1]
	v_mul_f32_e32 v1, 0x42800000, v7
	v_mul_f32_e32 v2, 0x42800000, v27
	v_med3_f32 v5, v1, s68, v101
	v_med3_f32 v2, v2, s68, v101
	v_mov_b32_e32 v1, v79
	v_cvt_pk_fp8_f32 v1, v5, v2
	v_mul_f32_e32 v3, 0x42800000, v31
	v_mul_f32_e32 v4, 0x42800000, v55
	v_med3_f32 v3, v3, s68, v101
	v_med3_f32 v4, v4, s68, v101
	v_cvt_pk_fp8_f32 v1, v3, v4 op_sel:[0,0,1]
	v_mul_f32_e32 v2, 0x42800000, v11
	v_mul_f32_e32 v3, 0x42800000, v35
	v_med3_f32 v6, v2, s68, v101
	v_med3_f32 v3, v3, s68, v101
	v_mov_b32_e32 v2, v79
	v_cvt_pk_fp8_f32 v2, v6, v3
	v_mul_f32_e32 v4, 0x42800000, v39
	v_mul_f32_e32 v5, 0x42800000, v63
	v_med3_f32 v4, v4, s68, v101
	v_med3_f32 v5, v5, s68, v101
	v_cvt_pk_fp8_f32 v2, v4, v5 op_sel:[0,0,1]
	v_mul_f32_e32 v3, 0x42800000, v15
	v_mul_f32_e32 v4, 0x42800000, v43
	v_med3_f32 v7, v3, s68, v101
	v_med3_f32 v4, v4, s68, v101
	v_mov_b32_e32 v3, v79
	v_cvt_pk_fp8_f32 v3, v7, v4
	v_mul_f32_e32 v5, 0x42800000, v51
	v_mul_f32_e32 v6, 0x42800000, v59
	v_med3_f32 v5, v5, s68, v101
	v_med3_f32 v6, v6, s68, v101
	v_cvt_pk_fp8_f32 v3, v5, v6 op_sel:[0,0,1]
	ds_write_b128 v98, v[64:67] offset:41120
	v_or_b32_e32 v6, s17, v87
	v_ashrrev_i32_e32 v7, 31, v6
	ds_write_b128 v98, v[0:3] offset:41200
	s_waitcnt lgkmcnt(0)
	ds_read_b128 v[0:3], v99 offset:40960
	v_lshl_add_u64 v[4:5], s[30:31], 0, v[80:81]
	v_lshlrev_b64 v[6:7], 11, v[6:7]
	v_lshl_add_u64 v[6:7], v[4:5], 0, v[6:7]
	s_waitcnt lgkmcnt(0)
	global_store_dwordx4 v[6:7], v[0:3], off sc1
	ds_read_b128 v[0:3], v99 offset:42240
	v_or_b32_e32 v6, s17, v77
	v_ashrrev_i32_e32 v7, 31, v6
	v_lshlrev_b64 v[6:7], 11, v[6:7]
	v_lshl_add_u64 v[6:7], v[4:5], 0, v[6:7]
	s_waitcnt lgkmcnt(0)
	global_store_dwordx4 v[6:7], v[0:3], off sc1
	ds_read_b128 v[0:3], v99 offset:43520
	v_or_b32_e32 v6, s17, v88
	v_ashrrev_i32_e32 v7, 31, v6
	v_lshlrev_b64 v[6:7], 11, v[6:7]
	v_lshl_add_u64 v[6:7], v[4:5], 0, v[6:7]
	s_waitcnt lgkmcnt(0)
	global_store_dwordx4 v[6:7], v[0:3], off sc1
	ds_read_b128 v[0:3], v99 offset:44800
	v_or_b32_e32 v6, s17, v89
	v_ashrrev_i32_e32 v7, 31, v6
	v_lshlrev_b64 v[6:7], 11, v[6:7]
	v_lshl_add_u64 v[4:5], v[4:5], 0, v[6:7]
	s_waitcnt lgkmcnt(0)
	global_store_dwordx4 v[4:5], v[0:3], off sc1
	s_waitcnt lgkmcnt(0)
.LBB0_1099:
	s_and_b64 vcc, exec, s[38:39]
	s_cbranch_vccz .LBB0_1061
	s_xor_b64 s[38:39], s[24:25], -1
	s_lshl_b32 s24, s3, 6
	s_mov_b64 s[30:31], -1
	s_and_b64 vcc, exec, s[38:39]
	s_cbranch_vccz .LBB0_1130
	s_andn2_b64 vcc, exec, s[28:29]
	s_cbranch_vccnz .LBB0_1104
	s_ashr_i32 s3, s2, 31
	s_lshl_b64 s[28:29], s[2:3], 22
	v_or_b32_e32 v0, s24, v76
	s_add_u32 s3, s59, s28
	v_mul_hi_i32_i24_e32 v1, s18, v0
	v_mul_i32_i24_e32 v0, s18, v0
	s_addc_u32 s25, s60, s29
	v_lshl_add_u64 v[0:1], v[0:1], 2, s[4:5]
	s_ashr_i32 s23, s22, 31
	v_lshl_add_u64 v[0:1], s[22:23], 2, v[0:1]
	v_mov_b32_e32 v83, v79
	v_lshl_add_u64 v[0:1], v[0:1], 0, v[82:83]
	s_lshl_b64 s[28:29], s[18:19], 2
	global_load_dwordx4 v[56:59], v[0:1], off nt
	v_lshl_add_u64 v[0:1], v[0:1], 0, s[28:29]
	global_load_dwordx4 v[60:63], v[0:1], off nt
	v_lshl_add_u64 v[0:1], v[0:1], 0, s[28:29]
	global_load_dwordx4 v[64:67], v[0:1], off nt
	v_lshl_add_u64 v[0:1], v[0:1], 0, s[28:29]
	global_load_dwordx4 v[52:55], v[0:1], off nt
	v_lshl_add_u64 v[0:1], v[0:1], 0, s[28:29]
	global_load_dwordx4 v[40:43], v[0:1], off nt
	v_lshl_add_u64 v[0:1], v[0:1], 0, s[28:29]
	global_load_dwordx4 v[44:47], v[0:1], off nt
	v_lshl_add_u64 v[0:1], v[0:1], 0, s[28:29]
	global_load_dwordx4 v[48:51], v[0:1], off nt
	v_lshl_add_u64 v[0:1], v[0:1], 0, s[28:29]
	global_load_dwordx4 v[36:39], v[0:1], off nt
	v_lshl_add_u64 v[0:1], v[0:1], 0, s[28:29]
	global_load_dwordx4 v[24:27], v[0:1], off nt
	v_lshl_add_u64 v[0:1], v[0:1], 0, s[28:29]
	global_load_dwordx4 v[28:31], v[0:1], off nt
	v_lshl_add_u64 v[0:1], v[0:1], 0, s[28:29]
	global_load_dwordx4 v[32:35], v[0:1], off nt
	v_lshl_add_u64 v[0:1], v[0:1], 0, s[28:29]
	global_load_dwordx4 v[20:23], v[0:1], off nt
	v_lshl_add_u64 v[0:1], v[0:1], 0, s[28:29]
	global_load_dwordx4 v[4:7], v[0:1], off nt
	v_lshl_add_u64 v[0:1], v[0:1], 0, s[28:29]
	global_load_dwordx4 v[8:11], v[0:1], off nt
	v_lshl_add_u64 v[0:1], v[0:1], 0, s[28:29]
	global_load_dwordx4 v[12:15], v[0:1], off nt
	v_lshl_add_u64 v[0:1], v[0:1], 0, s[28:29]
	global_load_dwordx4 v[0:3], v[0:1], off nt
	v_mov_b32_e32 v19, v79
	v_mov_b32_e32 v69, v79
	v_mov_b32_e32 v70, v79
	v_mov_b32_e32 v71, v79
	v_mov_b32_e32 v72, v79
	v_mov_b32_e32 v73, v79
	v_mov_b32_e32 v74, v79
	v_mov_b32_e32 v75, v79
	v_mov_b32_e32 v16, v79
	v_mov_b32_e32 v17, v79
	v_mov_b32_e32 v18, v79
	v_mov_b32_e32 v68, v79
	s_ashr_i32 s23, s24, 31
	s_add_u32 s28, s3, s24
	s_addc_u32 s29, s25, s23
	s_cmp_gt_i32 s43, 0xffff6680
	s_waitcnt vmcnt(15)
	v_mul_f32_e32 v56, 0x42800000, v56
	v_mul_f32_e32 v57, 0x42800000, v57
	s_waitcnt vmcnt(14)
	v_mul_f32_e32 v60, 0x42800000, v60
	v_med3_f32 v56, v56, s68, v101
	v_mul_f32_e32 v61, 0x42800000, v61
	v_med3_f32 v60, v60, s68, v101
	v_med3_f32 v57, v57, s68, v101
	v_med3_f32 v61, v61, s68, v101
	s_waitcnt vmcnt(11)
	v_mul_f32_e32 v41, 0x42800000, v41
	v_med3_f32 v41, v41, s68, v101
	s_waitcnt vmcnt(10)
	v_mul_f32_e32 v45, 0x42800000, v45
	v_med3_f32 v45, v45, s68, v101
	v_cvt_pk_fp8_f32 v69, v41, v45
	s_waitcnt vmcnt(9)
	v_mul_f32_e32 v49, 0x42800000, v49
	v_mul_f32_e32 v40, 0x42800000, v40
	v_mul_f32_e32 v44, 0x42800000, v44
	s_waitcnt vmcnt(7)
	v_mul_f32_e32 v24, 0x42800000, v24
	v_med3_f32 v40, v40, s68, v101
	s_waitcnt vmcnt(6)
	v_mul_f32_e32 v28, 0x42800000, v28
	v_med3_f32 v44, v44, s68, v101
	v_med3_f32 v24, v24, s68, v101
	v_med3_f32 v28, v28, s68, v101
	v_cvt_pk_fp8_f32 v16, v56, v60
	v_cvt_pk_fp8_f32 v17, v40, v44
	s_waitcnt vmcnt(3)
	v_mul_f32_e32 v4, 0x42800000, v4
	v_med3_f32 v4, v4, s68, v101
	s_waitcnt vmcnt(2)
	v_mul_f32_e32 v8, 0x42800000, v8
	v_med3_f32 v8, v8, s68, v101
	v_cvt_pk_fp8_f32 v19, v4, v8
	s_waitcnt vmcnt(1)
	v_mul_f32_e32 v12, 0x42800000, v12
	s_waitcnt vmcnt(0)
	v_mul_f32_e32 v0, 0x42800000, v0
	v_med3_f32 v4, v12, s68, v101
	v_med3_f32 v0, v0, s68, v101
	v_cvt_pk_fp8_f32 v19, v4, v0 op_sel:[0,0,1]
	v_mul_f32_e32 v0, 0x42800000, v37
	v_med3_f32 v4, v49, s68, v101
	v_med3_f32 v0, v0, s68, v101
	v_cvt_pk_fp8_f32 v69, v4, v0 op_sel:[0,0,1]
	v_mul_f32_e32 v0, 0x42800000, v25
	v_mul_f32_e32 v4, 0x42800000, v29
	v_med3_f32 v0, v0, s68, v101
	v_med3_f32 v4, v4, s68, v101
	v_cvt_pk_fp8_f32 v70, v0, v4
	v_mul_f32_e32 v8, 0x42800000, v33
	v_mul_f32_e32 v0, 0x42800000, v21
	v_med3_f32 v4, v8, s68, v101
	v_med3_f32 v0, v0, s68, v101
	v_cvt_pk_fp8_f32 v70, v4, v0 op_sel:[0,0,1]
	v_mul_f32_e32 v0, 0x42800000, v5
	v_mul_f32_e32 v4, 0x42800000, v9
	v_med3_f32 v0, v0, s68, v101
	v_med3_f32 v4, v4, s68, v101
	v_cvt_pk_fp8_f32 v71, v0, v4
	v_mul_f32_e32 v5, 0x42800000, v13
	v_mul_f32_e32 v0, 0x42800000, v1
	v_med3_f32 v1, v5, s68, v101
	v_med3_f32 v0, v0, s68, v101
	v_cvt_pk_fp8_f32 v71, v1, v0 op_sel:[0,0,1]
	v_mul_f32_e32 v0, 0x42800000, v58
	v_mul_f32_e32 v1, 0x42800000, v62
	v_med3_f32 v0, v0, s68, v101
	v_med3_f32 v1, v1, s68, v101
	v_cvt_pk_fp8_f32 v72, v0, v1
	v_mul_f32_e32 v4, 0x42800000, v66
	v_mul_f32_e32 v0, 0x42800000, v54
	v_med3_f32 v1, v4, s68, v101
	v_med3_f32 v0, v0, s68, v101
	v_cvt_pk_fp8_f32 v72, v1, v0 op_sel:[0,0,1]
	v_mul_f32_e32 v0, 0x42800000, v42
	v_mul_f32_e32 v1, 0x42800000, v46
	v_med3_f32 v0, v0, s68, v101
	v_med3_f32 v1, v1, s68, v101
	v_cvt_pk_fp8_f32 v73, v0, v1
	v_mul_f32_e32 v4, 0x42800000, v50
	v_mul_f32_e32 v0, 0x42800000, v38
	v_med3_f32 v1, v4, s68, v101
	v_med3_f32 v0, v0, s68, v101
	v_cvt_pk_fp8_f32 v73, v1, v0 op_sel:[0,0,1]
	v_mul_f32_e32 v0, 0x42800000, v26
	v_mul_f32_e32 v1, 0x42800000, v30
	v_med3_f32 v0, v0, s68, v101
	v_med3_f32 v1, v1, s68, v101
	v_cvt_pk_fp8_f32 v74, v0, v1
	v_mul_f32_e32 v4, 0x42800000, v34
	v_mul_f32_e32 v0, 0x42800000, v22
	v_med3_f32 v1, v4, s68, v101
	v_med3_f32 v0, v0, s68, v101
	v_cvt_pk_fp8_f32 v74, v1, v0 op_sel:[0,0,1]
	v_mul_f32_e32 v0, 0x42800000, v6
	v_mul_f32_e32 v1, 0x42800000, v10
	v_med3_f32 v0, v0, s68, v101
	v_med3_f32 v1, v1, s68, v101
	v_cvt_pk_fp8_f32 v75, v0, v1
	v_mul_f32_e32 v4, 0x42800000, v14
	v_mul_f32_e32 v0, 0x42800000, v2
	v_med3_f32 v1, v4, s68, v101
	v_med3_f32 v0, v0, s68, v101
	v_cvt_pk_fp8_f32 v75, v1, v0 op_sel:[0,0,1]
	v_mul_f32_e32 v0, 0x42800000, v59
	v_mul_f32_e32 v1, 0x42800000, v63
	v_med3_f32 v0, v0, s68, v101
	v_med3_f32 v1, v1, s68, v101
	v_mov_b32_e32 v4, v79
	v_cvt_pk_fp8_f32 v4, v0, v1
	v_mul_f32_e32 v2, 0x42800000, v67
	v_mul_f32_e32 v0, 0x42800000, v55
	v_med3_f32 v1, v2, s68, v101
	v_med3_f32 v0, v0, s68, v101
	v_cvt_pk_fp8_f32 v4, v1, v0 op_sel:[0,0,1]
	v_mul_f32_e32 v0, 0x42800000, v43
	v_mul_f32_e32 v1, 0x42800000, v47
	v_med3_f32 v0, v0, s68, v101
	v_med3_f32 v1, v1, s68, v101
	v_mov_b32_e32 v5, v79
	v_cvt_pk_fp8_f32 v5, v0, v1
	v_mul_f32_e32 v2, 0x42800000, v51
	v_mul_f32_e32 v0, 0x42800000, v39
	v_med3_f32 v1, v2, s68, v101
	v_med3_f32 v0, v0, s68, v101
	v_cvt_pk_fp8_f32 v5, v1, v0 op_sel:[0,0,1]
	v_mul_f32_e32 v0, 0x42800000, v27
	v_mul_f32_e32 v1, 0x42800000, v31
	v_med3_f32 v0, v0, s68, v101
	v_med3_f32 v1, v1, s68, v101
	v_mov_b32_e32 v6, v79
	v_cvt_pk_fp8_f32 v6, v0, v1
	v_mul_f32_e32 v2, 0x42800000, v35
	v_mul_f32_e32 v0, 0x42800000, v23
	v_cvt_pk_fp8_f32 v18, v24, v28
	v_med3_f32 v1, v2, s68, v101
	v_med3_f32 v0, v0, s68, v101
	v_cvt_pk_fp8_f32 v68, v57, v61
	v_cvt_pk_fp8_f32 v6, v1, v0 op_sel:[0,0,1]
	v_mul_f32_e32 v0, 0x42800000, v7
	v_mul_f32_e32 v1, 0x42800000, v11
	v_mul_f32_e32 v64, 0x42800000, v64
	v_mul_f32_e32 v52, 0x42800000, v52
	v_mul_f32_e32 v48, 0x42800000, v48
	v_mul_f32_e32 v36, 0x42800000, v36
	v_mul_f32_e32 v32, 0x42800000, v32
	v_mul_f32_e32 v20, 0x42800000, v20
	v_med3_f32 v0, v0, s68, v101
	v_med3_f32 v1, v1, s68, v101
	v_mov_b32_e32 v7, v79
	v_mul_f32_e32 v65, 0x42800000, v65
	v_med3_f32 v64, v64, s68, v101
	v_mul_f32_e32 v53, 0x42800000, v53
	v_med3_f32 v52, v52, s68, v101
	v_med3_f32 v48, v48, s68, v101
	v_med3_f32 v36, v36, s68, v101
	v_med3_f32 v32, v32, s68, v101
	v_med3_f32 v20, v20, s68, v101
	v_cvt_pk_fp8_f32 v7, v0, v1
	v_med3_f32 v56, v65, s68, v101
	v_med3_f32 v53, v53, s68, v101
	v_cvt_pk_fp8_f32 v16, v64, v52 op_sel:[0,0,1]
	v_cvt_pk_fp8_f32 v17, v48, v36 op_sel:[0,0,1]
	v_cvt_pk_fp8_f32 v18, v32, v20 op_sel:[0,0,1]
	v_cvt_pk_fp8_f32 v68, v56, v53 op_sel:[0,0,1]
	v_mul_f32_e32 v2, 0x42800000, v15
	v_mul_f32_e32 v0, 0x42800000, v3
	v_med3_f32 v1, v2, s68, v101
	v_med3_f32 v0, v0, s68, v101
	v_cvt_pk_fp8_f32 v7, v1, v0 op_sel:[0,0,1]
	ds_write_b128 v98, v[16:19] offset:40960
	ds_write_b128 v98, v[68:71] offset:41040
	ds_write_b128 v98, v[72:75] offset:41120
	ds_write_b128 v98, v[4:7] offset:41200
	s_waitcnt lgkmcnt(0)
	ds_read_b128 v[0:3], v99 offset:40960
	v_or_b32_e32 v4, s17, v87
	v_ashrrev_i32_e32 v5, 31, v4
	v_lshl_add_u64 v[8:9], s[28:29], 0, v[80:81]
	v_lshlrev_b64 v[4:5], 11, v[4:5]
	v_lshl_add_u64 v[10:11], v[8:9], 0, v[4:5]
	ds_read_b128 v[4:7], v99 offset:42240
	s_waitcnt lgkmcnt(1)
	global_store_dwordx4 v[10:11], v[0:3], off sc1
	s_cselect_b64 s[28:29], -1, 0
	s_nop 0
	v_or_b32_e32 v0, s17, v77
	v_ashrrev_i32_e32 v1, 31, v0
	v_lshlrev_b64 v[0:1], 11, v[0:1]
	v_lshl_add_u64 v[0:1], v[8:9], 0, v[0:1]
	s_waitcnt lgkmcnt(0)
	global_store_dwordx4 v[0:1], v[4:7], off sc1
	ds_read_b128 v[0:3], v99 offset:43520
	s_nop 0
	v_or_b32_e32 v4, s17, v88
	v_ashrrev_i32_e32 v5, 31, v4
	v_lshlrev_b64 v[4:5], 11, v[4:5]
	v_lshl_add_u64 v[10:11], v[8:9], 0, v[4:5]
	ds_read_b128 v[4:7], v99 offset:44800
	s_waitcnt lgkmcnt(1)
	global_store_dwordx4 v[10:11], v[0:3], off sc1
	s_nop 1
	v_or_b32_e32 v0, s17, v89
	v_ashrrev_i32_e32 v1, 31, v0
	v_lshlrev_b64 v[0:1], 11, v[0:1]
	v_lshl_add_u64 v[0:1], v[8:9], 0, v[0:1]
	s_waitcnt lgkmcnt(0)
	global_store_dwordx4 v[0:1], v[4:7], off sc1
	s_waitcnt lgkmcnt(0)
	s_andn2_b64 vcc, exec, s[28:29]
	s_cbranch_vccz .LBB0_1105
	s_branch .LBB0_1129

.LBB0_1105:
	s_andn2_b64 vcc, exec, s[26:27]
	s_cbranch_vccnz .LBB0_1107
	s_ashr_i32 s3, s2, 31
	s_lshl_b64 s[26:27], s[2:3], 22
	s_add_u32 s3, s61, s26
	s_addc_u32 s23, s62, s27
	v_or_b32_e32 v0, s24, v76
	s_add_u32 s3, s3, s20
	v_mul_hi_i32_i24_e32 v1, s18, v0
	v_mul_i32_i24_e32 v0, s18, v0
	s_addc_u32 s25, s23, s21
	v_lshl_add_u64 v[0:1], v[0:1], 2, s[4:5]
	s_ashr_i32 s23, s22, 31
	v_lshl_add_u64 v[0:1], s[22:23], 2, v[0:1]
	v_mov_b32_e32 v83, v79
	v_lshl_add_u64 v[0:1], v[0:1], 0, v[82:83]
	s_lshl_b64 s[26:27], s[18:19], 2
	global_load_dwordx4 v[56:59], v[0:1], off nt
	v_lshl_add_u64 v[0:1], v[0:1], 0, s[26:27]
	global_load_dwordx4 v[60:63], v[0:1], off nt
	v_lshl_add_u64 v[0:1], v[0:1], 0, s[26:27]
	global_load_dwordx4 v[64:67], v[0:1], off nt
	v_lshl_add_u64 v[0:1], v[0:1], 0, s[26:27]
	global_load_dwordx4 v[52:55], v[0:1], off nt
	v_lshl_add_u64 v[0:1], v[0:1], 0, s[26:27]
	global_load_dwordx4 v[40:43], v[0:1], off nt
	v_lshl_add_u64 v[0:1], v[0:1], 0, s[26:27]
	global_load_dwordx4 v[44:47], v[0:1], off nt
	v_lshl_add_u64 v[0:1], v[0:1], 0, s[26:27]
	global_load_dwordx4 v[48:51], v[0:1], off nt
	v_lshl_add_u64 v[0:1], v[0:1], 0, s[26:27]
	global_load_dwordx4 v[36:39], v[0:1], off nt
	v_lshl_add_u64 v[0:1], v[0:1], 0, s[26:27]
	global_load_dwordx4 v[24:27], v[0:1], off nt
	v_lshl_add_u64 v[0:1], v[0:1], 0, s[26:27]
	global_load_dwordx4 v[28:31], v[0:1], off nt
	v_lshl_add_u64 v[0:1], v[0:1], 0, s[26:27]
	global_load_dwordx4 v[32:35], v[0:1], off nt
	v_lshl_add_u64 v[0:1], v[0:1], 0, s[26:27]
	global_load_dwordx4 v[20:23], v[0:1], off nt
	v_lshl_add_u64 v[0:1], v[0:1], 0, s[26:27]
	global_load_dwordx4 v[4:7], v[0:1], off nt
	v_lshl_add_u64 v[0:1], v[0:1], 0, s[26:27]
	global_load_dwordx4 v[12:15], v[0:1], off nt
	v_lshl_add_u64 v[0:1], v[0:1], 0, s[26:27]
	global_load_dwordx4 v[16:19], v[0:1], off nt
	v_lshl_add_u64 v[0:1], v[0:1], 0, s[26:27]
	global_load_dwordx4 v[0:3], v[0:1], off nt
	v_mov_b32_e32 v11, v79
	v_mov_b32_e32 v69, v79
	v_mov_b32_e32 v70, v79
	v_mov_b32_e32 v71, v79
	v_mov_b32_e32 v72, v79
	v_mov_b32_e32 v73, v79
	v_mov_b32_e32 v74, v79
	v_mov_b32_e32 v75, v79
	v_mov_b32_e32 v8, v79
	v_mov_b32_e32 v9, v79
	v_mov_b32_e32 v10, v79
	v_mov_b32_e32 v68, v79
	s_ashr_i32 s23, s24, 31
	s_add_u32 s26, s3, s24
	s_addc_u32 s27, s25, s23
	s_cmp_gt_i32 s43, 0xffff6680
	s_waitcnt vmcnt(15)
	v_mul_f32_e32 v56, 0x42800000, v56
	v_mul_f32_e32 v57, 0x42800000, v57
	s_waitcnt vmcnt(14)
	v_mul_f32_e32 v60, 0x42800000, v60
	v_med3_f32 v56, v56, s68, v101
	v_mul_f32_e32 v61, 0x42800000, v61
	v_med3_f32 v60, v60, s68, v101
	v_med3_f32 v57, v57, s68, v101
	v_med3_f32 v61, v61, s68, v101
	s_waitcnt vmcnt(11)
	v_mul_f32_e32 v41, 0x42800000, v41
	v_med3_f32 v41, v41, s68, v101
	s_waitcnt vmcnt(10)
	v_mul_f32_e32 v45, 0x42800000, v45
	v_med3_f32 v45, v45, s68, v101
	v_cvt_pk_fp8_f32 v69, v41, v45
	s_waitcnt vmcnt(9)
	v_mul_f32_e32 v49, 0x42800000, v49
	v_mul_f32_e32 v40, 0x42800000, v40
	v_mul_f32_e32 v44, 0x42800000, v44
	s_waitcnt vmcnt(7)
	v_mul_f32_e32 v24, 0x42800000, v24
	v_med3_f32 v40, v40, s68, v101
	s_waitcnt vmcnt(6)
	v_mul_f32_e32 v28, 0x42800000, v28
	v_med3_f32 v44, v44, s68, v101
	v_med3_f32 v24, v24, s68, v101
	v_med3_f32 v28, v28, s68, v101
	v_cvt_pk_fp8_f32 v8, v56, v60
	v_cvt_pk_fp8_f32 v9, v40, v44
	s_waitcnt vmcnt(3)
	v_mul_f32_e32 v4, 0x42800000, v4
	v_med3_f32 v4, v4, s68, v101
	s_waitcnt vmcnt(2)
	v_mul_f32_e32 v12, 0x42800000, v12
	v_med3_f32 v12, v12, s68, v101
	v_cvt_pk_fp8_f32 v11, v4, v12
	s_waitcnt vmcnt(1)
	v_mul_f32_e32 v16, 0x42800000, v16
	s_waitcnt vmcnt(0)
	v_mul_f32_e32 v0, 0x42800000, v0
	v_med3_f32 v4, v16, s68, v101
	v_med3_f32 v0, v0, s68, v101
	v_cvt_pk_fp8_f32 v11, v4, v0 op_sel:[0,0,1]
	v_mul_f32_e32 v0, 0x42800000, v37
	v_med3_f32 v4, v49, s68, v101
	v_med3_f32 v0, v0, s68, v101
	v_cvt_pk_fp8_f32 v69, v4, v0 op_sel:[0,0,1]
	v_mul_f32_e32 v0, 0x42800000, v25
	v_mul_f32_e32 v4, 0x42800000, v29
	v_med3_f32 v0, v0, s68, v101
	v_med3_f32 v4, v4, s68, v101
	v_cvt_pk_fp8_f32 v70, v0, v4
	v_mul_f32_e32 v12, 0x42800000, v33
	v_mul_f32_e32 v0, 0x42800000, v21
	v_med3_f32 v4, v12, s68, v101
	v_med3_f32 v0, v0, s68, v101
	v_cvt_pk_fp8_f32 v70, v4, v0 op_sel:[0,0,1]
	v_mul_f32_e32 v0, 0x42800000, v5
	v_mul_f32_e32 v4, 0x42800000, v13
	v_med3_f32 v0, v0, s68, v101
	v_med3_f32 v4, v4, s68, v101
	v_cvt_pk_fp8_f32 v71, v0, v4
	v_mul_f32_e32 v5, 0x42800000, v17
	v_mul_f32_e32 v0, 0x42800000, v1
	v_med3_f32 v1, v5, s68, v101
	v_med3_f32 v0, v0, s68, v101
	v_cvt_pk_fp8_f32 v71, v1, v0 op_sel:[0,0,1]
	v_mul_f32_e32 v0, 0x42800000, v58
	v_mul_f32_e32 v1, 0x42800000, v62
	v_med3_f32 v0, v0, s68, v101
	v_med3_f32 v1, v1, s68, v101
	v_cvt_pk_fp8_f32 v72, v0, v1
	v_mul_f32_e32 v4, 0x42800000, v66
	v_mul_f32_e32 v0, 0x42800000, v54
	v_med3_f32 v1, v4, s68, v101
	v_med3_f32 v0, v0, s68, v101
	v_cvt_pk_fp8_f32 v72, v1, v0 op_sel:[0,0,1]
	v_mul_f32_e32 v0, 0x42800000, v42
	v_mul_f32_e32 v1, 0x42800000, v46
	v_med3_f32 v0, v0, s68, v101
	v_med3_f32 v1, v1, s68, v101
	v_cvt_pk_fp8_f32 v73, v0, v1
	v_mul_f32_e32 v4, 0x42800000, v50
	v_mul_f32_e32 v0, 0x42800000, v38
	v_med3_f32 v1, v4, s68, v101
	v_med3_f32 v0, v0, s68, v101
	v_cvt_pk_fp8_f32 v73, v1, v0 op_sel:[0,0,1]
	v_mul_f32_e32 v0, 0x42800000, v26
	v_mul_f32_e32 v1, 0x42800000, v30
	v_med3_f32 v0, v0, s68, v101
	v_med3_f32 v1, v1, s68, v101
	v_cvt_pk_fp8_f32 v74, v0, v1
	v_mul_f32_e32 v4, 0x42800000, v34
	v_mul_f32_e32 v0, 0x42800000, v22
	v_med3_f32 v1, v4, s68, v101
	v_med3_f32 v0, v0, s68, v101
	v_cvt_pk_fp8_f32 v74, v1, v0 op_sel:[0,0,1]
	v_mul_f32_e32 v0, 0x42800000, v6
	v_mul_f32_e32 v1, 0x42800000, v14
	v_med3_f32 v0, v0, s68, v101
	v_med3_f32 v1, v1, s68, v101
	v_cvt_pk_fp8_f32 v75, v0, v1
	v_mul_f32_e32 v4, 0x42800000, v18
	v_mul_f32_e32 v0, 0x42800000, v2
	v_med3_f32 v1, v4, s68, v101
	v_med3_f32 v0, v0, s68, v101
	v_cvt_pk_fp8_f32 v75, v1, v0 op_sel:[0,0,1]
	v_mul_f32_e32 v0, 0x42800000, v59
	v_mul_f32_e32 v1, 0x42800000, v63
	v_med3_f32 v0, v0, s68, v101
	v_med3_f32 v1, v1, s68, v101
	v_mov_b32_e32 v4, v79
	v_cvt_pk_fp8_f32 v4, v0, v1
	v_mul_f32_e32 v2, 0x42800000, v67
	v_mul_f32_e32 v0, 0x42800000, v55
	v_med3_f32 v1, v2, s68, v101
	v_med3_f32 v0, v0, s68, v101
	v_cvt_pk_fp8_f32 v4, v1, v0 op_sel:[0,0,1]
	v_mul_f32_e32 v0, 0x42800000, v43
	v_mul_f32_e32 v1, 0x42800000, v47
	v_med3_f32 v0, v0, s68, v101
	v_med3_f32 v1, v1, s68, v101
	v_mov_b32_e32 v5, v79
	v_cvt_pk_fp8_f32 v5, v0, v1
	v_mul_f32_e32 v2, 0x42800000, v51
	v_mul_f32_e32 v0, 0x42800000, v39
	v_med3_f32 v1, v2, s68, v101
	v_med3_f32 v0, v0, s68, v101
	v_cvt_pk_fp8_f32 v5, v1, v0 op_sel:[0,0,1]
	v_mul_f32_e32 v0, 0x42800000, v27
	v_mul_f32_e32 v1, 0x42800000, v31
	v_med3_f32 v0, v0, s68, v101
	v_med3_f32 v1, v1, s68, v101
	v_mov_b32_e32 v6, v79
	v_cvt_pk_fp8_f32 v6, v0, v1
	v_mul_f32_e32 v2, 0x42800000, v35
	v_mul_f32_e32 v0, 0x42800000, v23
	v_cvt_pk_fp8_f32 v10, v24, v28
	v_med3_f32 v1, v2, s68, v101
	v_med3_f32 v0, v0, s68, v101
	v_cvt_pk_fp8_f32 v68, v57, v61
	v_cvt_pk_fp8_f32 v6, v1, v0 op_sel:[0,0,1]
	v_mul_f32_e32 v0, 0x42800000, v7
	v_mul_f32_e32 v1, 0x42800000, v15
	v_mul_f32_e32 v64, 0x42800000, v64
	v_mul_f32_e32 v52, 0x42800000, v52
	v_mul_f32_e32 v48, 0x42800000, v48
	v_mul_f32_e32 v36, 0x42800000, v36
	v_mul_f32_e32 v32, 0x42800000, v32
	v_mul_f32_e32 v20, 0x42800000, v20
	v_med3_f32 v0, v0, s68, v101
	v_med3_f32 v1, v1, s68, v101
	v_mov_b32_e32 v7, v79
	v_mul_f32_e32 v65, 0x42800000, v65
	v_med3_f32 v64, v64, s68, v101
	v_mul_f32_e32 v53, 0x42800000, v53
	v_med3_f32 v52, v52, s68, v101
	v_med3_f32 v48, v48, s68, v101
	v_med3_f32 v36, v36, s68, v101
	v_med3_f32 v32, v32, s68, v101
	v_med3_f32 v20, v20, s68, v101
	v_cvt_pk_fp8_f32 v7, v0, v1
	v_med3_f32 v56, v65, s68, v101
	v_med3_f32 v53, v53, s68, v101
	v_cvt_pk_fp8_f32 v8, v64, v52 op_sel:[0,0,1]
	v_cvt_pk_fp8_f32 v9, v48, v36 op_sel:[0,0,1]
	v_cvt_pk_fp8_f32 v10, v32, v20 op_sel:[0,0,1]
	v_cvt_pk_fp8_f32 v68, v56, v53 op_sel:[0,0,1]
	v_mul_f32_e32 v2, 0x42800000, v19
	v_mul_f32_e32 v0, 0x42800000, v3
	v_med3_f32 v1, v2, s68, v101
	v_med3_f32 v0, v0, s68, v101
	v_cvt_pk_fp8_f32 v7, v1, v0 op_sel:[0,0,1]
	ds_write_b128 v98, v[8:11] offset:40960
	ds_write_b128 v98, v[68:71] offset:41040
	ds_write_b128 v98, v[72:75] offset:41120
	ds_write_b128 v98, v[4:7] offset:41200
	s_waitcnt lgkmcnt(0)
	ds_read_b128 v[0:3], v99 offset:40960
	v_or_b32_e32 v4, s17, v87
	v_ashrrev_i32_e32 v5, 31, v4
	v_lshl_add_u64 v[8:9], s[26:27], 0, v[80:81]
	v_lshlrev_b64 v[4:5], 11, v[4:5]
	v_lshl_add_u64 v[10:11], v[8:9], 0, v[4:5]
	ds_read_b128 v[4:7], v99 offset:42240
	s_waitcnt lgkmcnt(1)
	global_store_dwordx4 v[10:11], v[0:3], off sc1
	s_cselect_b64 s[26:27], -1, 0
	s_nop 0
	v_or_b32_e32 v0, s17, v77
	v_ashrrev_i32_e32 v1, 31, v0
	v_lshlrev_b64 v[0:1], 11, v[0:1]
	v_lshl_add_u64 v[0:1], v[8:9], 0, v[0:1]
	s_waitcnt lgkmcnt(0)
	global_store_dwordx4 v[0:1], v[4:7], off sc1
	ds_read_b128 v[0:3], v99 offset:43520
	s_nop 0
	v_or_b32_e32 v4, s17, v88
	v_ashrrev_i32_e32 v5, 31, v4
	v_lshlrev_b64 v[4:5], 11, v[4:5]
	v_lshl_add_u64 v[10:11], v[8:9], 0, v[4:5]
	ds_read_b128 v[4:7], v99 offset:44800
	s_waitcnt lgkmcnt(1)
	global_store_dwordx4 v[10:11], v[0:3], off sc1
	s_nop 1
	v_or_b32_e32 v0, s17, v89
	v_ashrrev_i32_e32 v1, 31, v0
	v_lshlrev_b64 v[0:1], 11, v[0:1]
	v_lshl_add_u64 v[0:1], v[8:9], 0, v[0:1]
	s_waitcnt lgkmcnt(0)
	global_store_dwordx4 v[0:1], v[4:7], off sc1
	s_waitcnt lgkmcnt(0)
	s_andn2_b64 vcc, exec, s[26:27]
	s_cbranch_vccz .LBB0_1108
	s_branch .LBB0_1129

.LBB0_1112:
	s_lshl_b64 s[20:21], s[20:21], 1
	s_add_u32 s3, s8, s20
	s_addc_u32 s20, s9, s21
	s_ashr_i32 s25, s24, 31
	s_lshl_b64 s[8:9], s[24:25], 1
	s_waitcnt lgkmcnt(0)
	s_add_u32 s8, s3, s8
	s_addc_u32 s9, s20, s9
	v_or_b32_e32 v0, s17, v90
	v_lshl_add_u64 v[4:5], s[8:9], 0, v[78:79]
	s_mov_b64 s[8:9], -1
	s_and_b64 vcc, exec, s[26:27]
	v_mul_hi_i32_i24_e32 v7, s16, v0
	v_mul_i32_i24_e32 v6, s16, v0
	s_cbranch_vccz .LBB0_1114
	v_lshl_add_u64 v[0:1], v[6:7], 1, v[4:5]
	global_store_dwordx4 v[0:1], v[104:107], off sc1
	s_mov_b64 s[8:9], 0
.LBB0_1114:
	v_mov_b32_e32 v0, 0
	s_andn2_b64 vcc, exec, s[8:9]
	v_mov_b32_e32 v1, 0
	v_mov_b32_e32 v2, 0
	v_mov_b32_e32 v3, 0
	s_cbranch_vccnz .LBB0_1116
	ds_read_b128 v[8:11], v102 offset:40960
	ds_read_b128 v[0:3], v102 offset:42112
	v_lshl_add_u64 v[6:7], v[6:7], 1, v[4:5]
	s_waitcnt lgkmcnt(1)
	global_store_dwordx4 v[6:7], v[8:11], off sc1
.LBB0_1116:
	v_or_b32_e32 v6, s17, v91
	v_mul_hi_i32_i24_e32 v7, s16, v6
	v_mul_i32_i24_e32 v6, s16, v6
	v_lshl_add_u64 v[6:7], v[6:7], 1, v[4:5]
	s_waitcnt lgkmcnt(0)
	global_store_dwordx4 v[6:7], v[0:3], off sc1
	s_mov_b64 s[8:9], -1
	s_and_b64 vcc, exec, s[26:27]
	v_or_b32_e32 v0, s17, v92
	v_mul_hi_i32_i24_e32 v7, s16, v0
	v_mul_i32_i24_e32 v6, s16, v0
	s_cbranch_vccz .LBB0_1118
	v_lshl_add_u64 v[0:1], v[6:7], 1, v[4:5]
	global_store_dwordx4 v[0:1], v[104:107], off sc1
	s_mov_b64 s[8:9], 0
.LBB0_1118:
	v_mov_b32_e32 v0, 0
	s_andn2_b64 vcc, exec, s[8:9]
	v_mov_b32_e32 v1, 0
	v_mov_b32_e32 v2, 0
	v_mov_b32_e32 v3, 0
	s_cbranch_vccnz .LBB0_1120
	ds_read_b128 v[8:11], v102 offset:43264
	ds_read_b128 v[0:3], v102 offset:44416
	v_lshl_add_u64 v[6:7], v[6:7], 1, v[4:5]
	s_waitcnt lgkmcnt(1)
	global_store_dwordx4 v[6:7], v[8:11], off sc1
.LBB0_1120:
	v_or_b32_e32 v6, s17, v93
	v_mul_hi_i32_i24_e32 v7, s16, v6
	v_mul_i32_i24_e32 v6, s16, v6
	v_lshl_add_u64 v[6:7], v[6:7], 1, v[4:5]
	s_waitcnt lgkmcnt(0)
	global_store_dwordx4 v[6:7], v[0:3], off sc1
	s_mov_b64 s[8:9], -1
	s_and_b64 vcc, exec, s[26:27]
	v_or_b32_e32 v0, s17, v94
	v_mul_hi_i32_i24_e32 v7, s16, v0
	v_mul_i32_i24_e32 v6, s16, v0
	s_cbranch_vccz .LBB0_1122
	v_lshl_add_u64 v[0:1], v[6:7], 1, v[4:5]
	global_store_dwordx4 v[0:1], v[104:107], off sc1
	s_mov_b64 s[8:9], 0
.LBB0_1122:
	v_mov_b32_e32 v0, 0
	s_andn2_b64 vcc, exec, s[8:9]
	v_mov_b32_e32 v1, 0
	v_mov_b32_e32 v2, 0
	v_mov_b32_e32 v3, 0
	s_cbranch_vccnz .LBB0_1124
	ds_read_b128 v[8:11], v102 offset:45568
	ds_read_b128 v[0:3], v102 offset:46720
	v_lshl_add_u64 v[6:7], v[6:7], 1, v[4:5]
	s_waitcnt lgkmcnt(1)
	global_store_dwordx4 v[6:7], v[8:11], off sc1
.LBB0_1124:
	v_or_b32_e32 v6, s17, v95
	v_mul_hi_i32_i24_e32 v7, s16, v6
	v_mul_i32_i24_e32 v6, s16, v6
	v_lshl_add_u64 v[6:7], v[6:7], 1, v[4:5]
	s_waitcnt lgkmcnt(0)
	global_store_dwordx4 v[6:7], v[0:3], off sc1
	s_mov_b64 s[8:9], -1
	s_and_b64 vcc, exec, s[26:27]
	v_or_b32_e32 v0, s17, v96
	v_mul_hi_i32_i24_e32 v7, s16, v0
	v_mul_i32_i24_e32 v6, s16, v0
	s_cbranch_vccz .LBB0_1126
	v_lshl_add_u64 v[0:1], v[6:7], 1, v[4:5]
	global_store_dwordx4 v[0:1], v[104:107], off sc1
	s_mov_b64 s[8:9], 0
.LBB0_1126:
	v_mov_b32_e32 v0, 0
	s_andn2_b64 vcc, exec, s[8:9]
	v_mov_b32_e32 v1, 0
	v_mov_b32_e32 v2, 0
	v_mov_b32_e32 v3, 0
	s_cbranch_vccnz .LBB0_1128
	ds_read_b128 v[8:11], v102 offset:47872
	ds_read_b128 v[0:3], v102 offset:49024
	v_lshl_add_u64 v[6:7], v[6:7], 1, v[4:5]
	s_waitcnt lgkmcnt(1)
	global_store_dwordx4 v[6:7], v[8:11], off sc1
.LBB0_1128:
	v_or_b32_e32 v6, s17, v97
	v_mul_hi_i32_i24_e32 v7, s16, v6
	v_mul_i32_i24_e32 v6, s16, v6
	v_lshl_add_u64 v[4:5], v[6:7], 1, v[4:5]
	s_waitcnt lgkmcnt(0)
	global_store_dwordx4 v[4:5], v[0:3], off sc1
	s_waitcnt lgkmcnt(0)

.LBB0_1217:
	s_waitcnt vmcnt(0)
	v_mul_f32_e32 v4, 0x42800000, v4
	v_mul_f32_e32 v8, 0x42800000, v8
	v_med3_f32 v4, v4, s66, v90
	v_med3_f32 v8, v8, s66, v90
	v_mov_b32_e32 v67, v69
	v_cvt_pk_fp8_f32 v67, v4, v8
	v_mul_f32_e32 v12, 0x42800000, v12
	v_mul_f32_e32 v0, 0x42800000, v0
	v_med3_f32 v4, v12, s66, v90
	v_med3_f32 v0, v0, s66, v90
	v_cvt_pk_fp8_f32 v67, v4, v0 op_sel:[0,0,1]
	v_mul_f32_e32 v0, 0x42800000, v57
	v_mul_f32_e32 v4, 0x42800000, v53
	v_med3_f32 v0, v0, s66, v90
	v_med3_f32 v4, v4, s66, v90
	v_mov_b32_e32 v96, v69
	v_cvt_pk_fp8_f32 v96, v0, v4
	v_mul_f32_e32 v8, 0x42800000, v61
	v_mul_f32_e32 v0, 0x42800000, v45
	v_med3_f32 v4, v8, s66, v90
	v_med3_f32 v0, v0, s66, v90
	v_cvt_pk_fp8_f32 v96, v4, v0 op_sel:[0,0,1]
	v_mul_f32_e32 v0, 0x42800000, v41
	v_mul_f32_e32 v4, 0x42800000, v37
	v_med3_f32 v0, v0, s66, v90
	v_med3_f32 v4, v4, s66, v90
	v_mov_b32_e32 v97, v69
	v_cvt_pk_fp8_f32 v97, v0, v4
	v_mul_f32_e32 v8, 0x42800000, v49
	v_mul_f32_e32 v0, 0x42800000, v33
	v_med3_f32 v4, v8, s66, v90
	v_med3_f32 v0, v0, s66, v90
	v_cvt_pk_fp8_f32 v97, v4, v0 op_sel:[0,0,1]
	v_mul_f32_e32 v0, 0x42800000, v21
	v_mul_f32_e32 v4, 0x42800000, v25
	v_med3_f32 v0, v0, s66, v90
	v_med3_f32 v4, v4, s66, v90
	v_mov_b32_e32 v98, v69
	v_cvt_pk_fp8_f32 v98, v0, v4
	v_mul_f32_e32 v8, 0x42800000, v29
	v_mul_f32_e32 v0, 0x42800000, v17
	v_med3_f32 v4, v8, s66, v90
	v_med3_f32 v0, v0, s66, v90
	v_cvt_pk_fp8_f32 v98, v4, v0 op_sel:[0,0,1]
	v_mul_f32_e32 v0, 0x42800000, v5
	v_mul_f32_e32 v4, 0x42800000, v9
	v_med3_f32 v0, v0, s66, v90
	v_med3_f32 v4, v4, s66, v90
	v_mov_b32_e32 v99, v69
	v_cvt_pk_fp8_f32 v99, v0, v4
	v_mul_f32_e32 v5, 0x42800000, v13
	v_mul_f32_e32 v0, 0x42800000, v1
	v_med3_f32 v1, v5, s66, v90
	v_med3_f32 v0, v0, s66, v90
	v_cvt_pk_fp8_f32 v99, v1, v0 op_sel:[0,0,1]
	v_mul_f32_e32 v0, 0x42800000, v58
	v_mul_f32_e32 v1, 0x42800000, v54
	v_med3_f32 v0, v0, s66, v90
	v_med3_f32 v1, v1, s66, v90
	v_mov_b32_e32 v100, v69
	v_cvt_pk_fp8_f32 v100, v0, v1
	v_mul_f32_e32 v4, 0x42800000, v62
	v_mul_f32_e32 v0, 0x42800000, v46
	v_med3_f32 v1, v4, s66, v90
	v_med3_f32 v0, v0, s66, v90
	v_cvt_pk_fp8_f32 v100, v1, v0 op_sel:[0,0,1]
	v_mul_f32_e32 v0, 0x42800000, v42
	v_mul_f32_e32 v1, 0x42800000, v38
	v_med3_f32 v0, v0, s66, v90
	v_med3_f32 v1, v1, s66, v90
	v_mov_b32_e32 v101, v69
	v_cvt_pk_fp8_f32 v101, v0, v1
	v_mul_f32_e32 v4, 0x42800000, v50
	v_mul_f32_e32 v0, 0x42800000, v34
	v_med3_f32 v1, v4, s66, v90
	v_med3_f32 v0, v0, s66, v90
	v_cvt_pk_fp8_f32 v101, v1, v0 op_sel:[0,0,1]
	v_mul_f32_e32 v0, 0x42800000, v22
	v_mul_f32_e32 v1, 0x42800000, v26
	v_med3_f32 v0, v0, s66, v90
	v_med3_f32 v1, v1, s66, v90
	v_mov_b32_e32 v102, v69
	v_cvt_pk_fp8_f32 v102, v0, v1
	v_mul_f32_e32 v4, 0x42800000, v30
	v_mul_f32_e32 v0, 0x42800000, v18
	v_med3_f32 v1, v4, s66, v90
	v_med3_f32 v0, v0, s66, v90
	v_cvt_pk_fp8_f32 v102, v1, v0 op_sel:[0,0,1]
	v_mul_f32_e32 v0, 0x42800000, v6
	v_mul_f32_e32 v1, 0x42800000, v10
	v_med3_f32 v0, v0, s66, v90
	v_med3_f32 v1, v1, s66, v90
	v_mov_b32_e32 v103, v69
	v_cvt_pk_fp8_f32 v103, v0, v1
	v_mul_f32_e32 v4, 0x42800000, v14
	v_mul_f32_e32 v0, 0x42800000, v2
	v_med3_f32 v1, v4, s66, v90
	v_med3_f32 v0, v0, s66, v90
	v_cvt_pk_fp8_f32 v103, v1, v0 op_sel:[0,0,1]
	v_mul_f32_e32 v0, 0x42800000, v59
	v_mul_f32_e32 v1, 0x42800000, v55
	v_med3_f32 v0, v0, s66, v90
	v_med3_f32 v1, v1, s66, v90
	v_mov_b32_e32 v4, v69
	v_cvt_pk_fp8_f32 v4, v0, v1
	v_mul_f32_e32 v2, 0x42800000, v63
	v_mul_f32_e32 v0, 0x42800000, v47
	v_med3_f32 v1, v2, s66, v90
	v_med3_f32 v0, v0, s66, v90
	v_cvt_pk_fp8_f32 v4, v1, v0 op_sel:[0,0,1]
	v_mul_f32_e32 v0, 0x42800000, v43
	v_mul_f32_e32 v1, 0x42800000, v39
	v_med3_f32 v0, v0, s66, v90
	v_med3_f32 v1, v1, s66, v90
	v_mov_b32_e32 v5, v69
	v_cvt_pk_fp8_f32 v5, v0, v1
	v_mul_f32_e32 v2, 0x42800000, v51
	v_mul_f32_e32 v0, 0x42800000, v35
	v_med3_f32 v1, v2, s66, v90
	v_med3_f32 v0, v0, s66, v90
	v_cvt_pk_fp8_f32 v5, v1, v0 op_sel:[0,0,1]
	v_mul_f32_e32 v0, 0x42800000, v23
	v_mul_f32_e32 v1, 0x42800000, v27
	v_mul_f32_e32 v56, 0x42800000, v56
	v_mul_f32_e32 v52, 0x42800000, v52
	v_med3_f32 v0, v0, s66, v90
	v_med3_f32 v1, v1, s66, v90
	v_mov_b32_e32 v6, v69
	v_med3_f32 v56, v56, s66, v90
	v_med3_f32 v52, v52, s66, v90
	v_mov_b32_e32 v64, v69
	v_cvt_pk_fp8_f32 v6, v0, v1
	v_cvt_pk_fp8_f32 v64, v56, v52
	v_mul_f32_e32 v40, 0x42800000, v40
	v_mul_f32_e32 v36, 0x42800000, v36
	v_mul_f32_e32 v20, 0x42800000, v20
	v_mul_f32_e32 v24, 0x42800000, v24
	v_med3_f32 v40, v40, s66, v90
	v_med3_f32 v36, v36, s66, v90
	v_mov_b32_e32 v65, v69
	v_med3_f32 v20, v20, s66, v90
	v_med3_f32 v24, v24, s66, v90
	v_mov_b32_e32 v66, v69
	v_mul_f32_e32 v2, 0x42800000, v31
	v_mul_f32_e32 v0, 0x42800000, v19
	v_mul_f32_e32 v60, 0x42800000, v60
	v_mul_f32_e32 v44, 0x42800000, v44
	v_cvt_pk_fp8_f32 v65, v40, v36
	v_cvt_pk_fp8_f32 v66, v20, v24
	v_med3_f32 v1, v2, s66, v90
	v_med3_f32 v0, v0, s66, v90
	v_med3_f32 v52, v60, s66, v90
	v_med3_f32 v44, v44, s66, v90
	v_cvt_pk_fp8_f32 v6, v1, v0 op_sel:[0,0,1]
	v_mul_f32_e32 v0, 0x42800000, v7
	v_mul_f32_e32 v1, 0x42800000, v11
	v_cvt_pk_fp8_f32 v64, v52, v44 op_sel:[0,0,1]
	v_mul_f32_e32 v44, 0x42800000, v48
	v_mul_f32_e32 v32, 0x42800000, v32
	v_mul_f32_e32 v28, 0x42800000, v28
	v_mul_f32_e32 v16, 0x42800000, v16
	v_med3_f32 v0, v0, s66, v90
	v_med3_f32 v1, v1, s66, v90
	v_mov_b32_e32 v7, v69
	v_med3_f32 v36, v44, s66, v90
	v_med3_f32 v32, v32, s66, v90
	v_med3_f32 v20, v28, s66, v90
	v_med3_f32 v16, v16, s66, v90
	v_cvt_pk_fp8_f32 v7, v0, v1
	v_cvt_pk_fp8_f32 v65, v36, v32 op_sel:[0,0,1]
	v_cvt_pk_fp8_f32 v66, v20, v16 op_sel:[0,0,1]
	v_mul_f32_e32 v2, 0x42800000, v15
	v_mul_f32_e32 v0, 0x42800000, v3
	v_med3_f32 v1, v2, s66, v90
	v_med3_f32 v0, v0, s66, v90
	v_cvt_pk_fp8_f32 v7, v1, v0 op_sel:[0,0,1]
	s_mul_hi_i32 s3, s2, 0x380000
	s_mul_i32 s2, s2, 0x380000
	ds_write_b128 v87, v[64:67] offset:40960
	ds_write_b128 v87, v[96:99] offset:41040
	ds_write_b128 v87, v[100:103] offset:41120
	ds_write_b128 v87, v[4:7] offset:41200
	s_add_u32 s2, s46, s2
	s_waitcnt lgkmcnt(0)
	s_addc_u32 s3, s47, s3
	s_add_i32 s13, s13, s0
	s_ashr_i32 s0, s22, 31
	ds_read_b128 v[0:3], v88 offset:40960
	s_add_u32 s2, s2, s22
	v_add_u32_e32 v4, s13, v75
	s_addc_u32 s3, s3, s0
	v_ashrrev_i32_e32 v5, 31, v4
	v_lshl_add_u64 v[8:9], s[2:3], 0, v[70:71]
	v_lshlrev_b64 v[4:5], 9, v[4:5]
	v_lshl_add_u64 v[10:11], v[8:9], 0, v[4:5]
	ds_read_b128 v[4:7], v88 offset:42240
	s_waitcnt lgkmcnt(0)
	global_store_dwordx4 v[10:11], v[0:3], off sc1
	s_nop 1
	v_add_u32_e32 v0, s13, v76
	v_ashrrev_i32_e32 v1, 31, v0
	v_lshlrev_b64 v[0:1], 9, v[0:1]
	v_lshl_add_u64 v[0:1], v[8:9], 0, v[0:1]
	global_store_dwordx4 v[0:1], v[4:7], off sc1
	ds_read_b128 v[0:3], v88 offset:43520
	s_nop 0
	v_add_u32_e32 v4, s13, v77
	v_ashrrev_i32_e32 v5, 31, v4
	v_lshlrev_b64 v[4:5], 9, v[4:5]
	v_lshl_add_u64 v[10:11], v[8:9], 0, v[4:5]
	ds_read_b128 v[4:7], v88 offset:44800
	s_waitcnt lgkmcnt(1)
	global_store_dwordx4 v[10:11], v[0:3], off sc1
	s_nop 1
	v_add_u32_e32 v0, s13, v78
	v_ashrrev_i32_e32 v1, 31, v0
	v_lshlrev_b64 v[0:1], 9, v[0:1]
	v_lshl_add_u64 v[0:1], v[8:9], 0, v[0:1]
	s_waitcnt lgkmcnt(0)
	global_store_dwordx4 v[0:1], v[4:7], off sc1
	s_waitcnt lgkmcnt(0)

.LBB0_1219:
	s_add_i32 s92, s56, s61
	s_add_i32 s0, s92, 0x9509
	s_mul_hi_i32 s2, s0, 0x20d56b39
	s_lshr_b32 s3, s2, 31
	s_ashr_i32 s2, s2, 12
	s_add_i32 s2, s2, s3
	s_mul_i32 s3, s2, 0x7cc0
	s_sub_i32 s30, s0, s3
	s_cmpk_gt_i32 s30, 0x1cbf
	s_mov_b64 s[6:7], -1
	s_cbranch_scc0 .LBB0_1225
	s_add_i32 s9, s30, 0xffffe340
	s_and_b32 s8, s9, 0xff
	s_cmpk_gt_u32 s30, 0x5cbf
	s_cbranch_scc0 .LBB0_1222
	v_mov_b32_e32 v0, s57
	s_add_i32 s0, s30, 0xffffa340
	s_ashr_i32 s3, s2, 31
	ds_read_b64 v[0:1], v0
	s_lshr_b32 s0, s0, 8
	s_lshl_b64 s[6:7], s[2:3], 26
	s_add_u32 s10, s38, s6
	s_addc_u32 s11, s39, s7
	s_lshl_b64 s[6:7], s[0:1], 20
	s_add_u32 s6, s10, s6
	s_addc_u32 s7, s11, s7
	s_waitcnt lgkmcnt(0)
	v_readfirstlane_b32 s12, v0
	s_lshl_b64 s[10:11], s[2:3], 27
	v_readfirstlane_b32 s13, v1
	s_add_u32 s3, s12, s10
	s_addc_u32 s13, s13, s11
	s_lshl_b64 s[10:11], s[0:1], 22
	s_add_u32 s12, s3, s10
	s_addc_u32 s13, s13, s11
	s_lshl_b32 s0, s8, 3
	s_and_b32 s3, s0, 0x7c0
	s_lshl_b32 s0, s30, 6
	s_and_b32 s10, s0, 0x1c0
	v_or_b32_e32 v0, s10, v74
	v_lshlrev_b32_e32 v0, 13, v0
	v_mov_b32_e32 v1, v69
	v_lshl_add_u64 v[0:1], s[12:13], 0, v[0:1]
	s_lshl_b32 s0, s3, 2
	v_lshl_add_u64 v[0:1], v[0:1], 0, s[0:1]
	v_mov_b32_e32 v73, v69
	v_lshl_add_u64 v[60:61], v[0:1], 0, v[72:73]
	v_add_co_u32_e32 v4, vcc, s58, v60
	s_mov_b32 s0, 0x8000
	s_nop 0
	v_addc_co_u32_e32 v5, vcc, 0, v61, vcc
	v_add_co_u32_e32 v8, vcc, s59, v60
	global_load_dwordx4 v[0:3], v[60:61], off nt
	s_nop 0
	global_load_dwordx4 v[4:7], v[4:5], off nt
	v_addc_co_u32_e32 v9, vcc, 0, v61, vcc
	v_add_co_u32_e32 v10, vcc, s60, v60
	v_mov_b32_e32 v64, v69
	s_nop 0
	v_addc_co_u32_e32 v11, vcc, 0, v61, vcc
	v_add_co_u32_e32 v16, vcc, s0, v60
	s_mov_b32 s0, 0xa000
	s_nop 0
	v_addc_co_u32_e32 v17, vcc, 0, v61, vcc
	v_add_co_u32_e32 v20, vcc, s0, v60
	s_mov_b32 s0, 0xc000
	s_nop 0
	v_addc_co_u32_e32 v21, vcc, 0, v61, vcc
	v_add_co_u32_e32 v24, vcc, s0, v60
	s_mov_b32 s0, 0xe000
	s_nop 0
	v_addc_co_u32_e32 v25, vcc, 0, v61, vcc
	global_load_dwordx4 v[12:15], v[8:9], off nt
	s_nop 0
	global_load_dwordx4 v[8:11], v[10:11], off nt
	v_add_co_u32_e32 v26, vcc, s0, v60
	s_mov_b32 s0, 0x10000
	s_nop 0
	v_addc_co_u32_e32 v27, vcc, 0, v61, vcc
	global_load_dwordx4 v[16:19], v[16:17], off nt
	s_nop 0
	global_load_dwordx4 v[20:23], v[20:21], off nt
	v_add_co_u32_e32 v28, vcc, s0, v60
	s_mov_b32 s0, 0x14000
	s_nop 0
	v_addc_co_u32_e32 v29, vcc, 0, v61, vcc
	v_add_co_u32_e32 v36, vcc, s62, v60
	global_load_dwordx4 v[32:35], v[24:25], off nt
	s_nop 0
	global_load_dwordx4 v[24:27], v[26:27], off nt
	v_addc_co_u32_e32 v37, vcc, 0, v61, vcc
	v_add_co_u32_e32 v40, vcc, s0, v60
	s_mov_b32 s0, 0x16000
	s_nop 0
	v_addc_co_u32_e32 v41, vcc, 0, v61, vcc
	global_load_dwordx4 v[28:31], v[28:29], off nt
	s_nop 0
	global_load_dwordx4 v[36:39], v[36:37], off nt
	v_add_co_u32_e32 v42, vcc, s0, v60
	s_mov_b32 s0, 0x18000
	s_nop 0
	v_addc_co_u32_e32 v43, vcc, 0, v61, vcc
	v_add_co_u32_e32 v44, vcc, s0, v60
	global_load_dwordx4 v[48:51], v[40:41], off nt
	s_nop 0
	global_load_dwordx4 v[40:43], v[42:43], off nt
	v_addc_co_u32_e32 v45, vcc, 0, v61, vcc
	v_add_co_u32_e32 v52, vcc, s63, v60
	v_mov_b32_e32 v65, v69
	s_nop 0
	v_addc_co_u32_e32 v53, vcc, 0, v61, vcc
	global_load_dwordx4 v[44:47], v[44:45], off nt
	s_nop 0
	global_load_dwordx4 v[52:55], v[52:53], off nt
	v_add_co_u32_e32 v56, vcc, s64, v60
	v_mov_b32_e32 v66, v69
	s_nop 0
	v_addc_co_u32_e32 v57, vcc, 0, v61, vcc
	v_add_co_u32_e32 v60, vcc, s65, v60
	global_load_dwordx4 v[56:59], v[56:57], off nt
	s_nop 0
	v_addc_co_u32_e32 v61, vcc, 0, v61, vcc
	global_load_dwordx4 v[60:63], v[60:61], off nt
	v_mov_b32_e32 v67, v69
	v_mov_b32_e32 v96, v69
	v_mov_b32_e32 v97, v69
	v_mov_b32_e32 v98, v69
	v_mov_b32_e32 v99, v69
	v_mov_b32_e32 v100, v69
	s_waitcnt vmcnt(0)
	v_mul_f32_e32 v0, 0x42000000, v0
	v_mul_f32_e32 v4, 0x42000000, v4
	v_med3_f32 v0, v0, s66, v90
	v_med3_f32 v4, v4, s66, v90
	v_cvt_pk_fp8_f32 v64, v0, v4
	v_mov_b32_e32 v101, v69
	v_mov_b32_e32 v102, v69
	v_mov_b32_e32 v103, v69
	s_add_u32 s6, s6, s10
	s_addc_u32 s7, s7, 0
	v_mul_f32_e32 v12, 0x42000000, v12
	v_mul_f32_e32 v0, 0x42000000, v8
	v_med3_f32 v4, v12, s66, v90
	v_med3_f32 v0, v0, s66, v90
	v_cvt_pk_fp8_f32 v64, v4, v0 op_sel:[0,0,1]
	v_mul_f32_e32 v0, 0x42000000, v16
	v_mul_f32_e32 v4, 0x42000000, v20
	v_med3_f32 v0, v0, s66, v90
	v_med3_f32 v4, v4, s66, v90
	v_cvt_pk_fp8_f32 v65, v0, v4
	v_mul_f32_e32 v8, 0x42000000, v32
	v_mul_f32_e32 v0, 0x42000000, v24
	v_med3_f32 v4, v8, s66, v90
	v_med3_f32 v0, v0, s66, v90
	v_cvt_pk_fp8_f32 v65, v4, v0 op_sel:[0,0,1]
	v_mul_f32_e32 v0, 0x42000000, v28
	v_mul_f32_e32 v4, 0x42000000, v36
	v_med3_f32 v0, v0, s66, v90
	v_med3_f32 v4, v4, s66, v90
	v_cvt_pk_fp8_f32 v66, v0, v4
	v_mul_f32_e32 v8, 0x42000000, v48
	v_mul_f32_e32 v0, 0x42000000, v40
	v_med3_f32 v4, v8, s66, v90
	v_med3_f32 v0, v0, s66, v90
	v_cvt_pk_fp8_f32 v66, v4, v0 op_sel:[0,0,1]
	v_mul_f32_e32 v0, 0x42000000, v44
	v_mul_f32_e32 v4, 0x42000000, v52
	v_med3_f32 v0, v0, s66, v90
	v_med3_f32 v4, v4, s66, v90
	v_cvt_pk_fp8_f32 v67, v0, v4
	v_mul_f32_e32 v8, 0x42000000, v56
	v_med3_f32 v4, v8, s66, v90
	v_mul_f32_e32 v0, 0x42000000, v60
	v_med3_f32 v0, v0, s66, v90
	v_cvt_pk_fp8_f32 v67, v4, v0 op_sel:[0,0,1]
	v_mul_f32_e32 v0, 0x42000000, v1
	v_mul_f32_e32 v1, 0x42000000, v5
	v_med3_f32 v0, v0, s66, v90
	v_med3_f32 v1, v1, s66, v90
	v_cvt_pk_fp8_f32 v96, v0, v1
	v_mul_f32_e32 v4, 0x42000000, v13
	v_mul_f32_e32 v0, 0x42000000, v9
	v_med3_f32 v1, v4, s66, v90
	v_med3_f32 v0, v0, s66, v90
	v_cvt_pk_fp8_f32 v96, v1, v0 op_sel:[0,0,1]
	v_mul_f32_e32 v0, 0x42000000, v17
	v_mul_f32_e32 v1, 0x42000000, v21
	v_med3_f32 v0, v0, s66, v90
	v_med3_f32 v1, v1, s66, v90
	v_cvt_pk_fp8_f32 v97, v0, v1
	v_mul_f32_e32 v4, 0x42000000, v33
	v_mul_f32_e32 v0, 0x42000000, v25
	v_med3_f32 v1, v4, s66, v90
	v_med3_f32 v0, v0, s66, v90
	v_cvt_pk_fp8_f32 v97, v1, v0 op_sel:[0,0,1]
	v_mul_f32_e32 v0, 0x42000000, v29
	v_mul_f32_e32 v1, 0x42000000, v37
	v_med3_f32 v0, v0, s66, v90
	v_med3_f32 v1, v1, s66, v90
	v_cvt_pk_fp8_f32 v98, v0, v1
	v_mul_f32_e32 v4, 0x42000000, v49
	v_mul_f32_e32 v0, 0x42000000, v41
	v_med3_f32 v1, v4, s66, v90
	v_med3_f32 v0, v0, s66, v90
	v_cvt_pk_fp8_f32 v98, v1, v0 op_sel:[0,0,1]
	v_mul_f32_e32 v0, 0x42000000, v45
	v_mul_f32_e32 v1, 0x42000000, v53
	v_med3_f32 v0, v0, s66, v90
	v_med3_f32 v1, v1, s66, v90
	v_cvt_pk_fp8_f32 v99, v0, v1
	v_mul_f32_e32 v4, 0x42000000, v57
	v_mul_f32_e32 v0, 0x42000000, v61
	v_med3_f32 v1, v4, s66, v90
	v_med3_f32 v0, v0, s66, v90
	v_cvt_pk_fp8_f32 v99, v1, v0 op_sel:[0,0,1]
	v_mul_f32_e32 v0, 0x42000000, v2
	v_mul_f32_e32 v1, 0x42000000, v6
	v_med3_f32 v0, v0, s66, v90
	v_med3_f32 v1, v1, s66, v90
	v_cvt_pk_fp8_f32 v100, v0, v1
	v_mul_f32_e32 v2, 0x42000000, v14
	v_mul_f32_e32 v0, 0x42000000, v10
	v_med3_f32 v1, v2, s66, v90
	v_med3_f32 v0, v0, s66, v90
	v_cvt_pk_fp8_f32 v100, v1, v0 op_sel:[0,0,1]
	v_mul_f32_e32 v0, 0x42000000, v18
	v_mul_f32_e32 v1, 0x42000000, v22
	v_med3_f32 v0, v0, s66, v90
	v_med3_f32 v1, v1, s66, v90
	v_cvt_pk_fp8_f32 v101, v0, v1
	v_mul_f32_e32 v2, 0x42000000, v34
	v_mul_f32_e32 v0, 0x42000000, v26
	v_med3_f32 v1, v2, s66, v90
	v_med3_f32 v0, v0, s66, v90
	v_cvt_pk_fp8_f32 v101, v1, v0 op_sel:[0,0,1]
	v_mul_f32_e32 v0, 0x42000000, v30
	v_mul_f32_e32 v1, 0x42000000, v38
	v_med3_f32 v0, v0, s66, v90
	v_med3_f32 v1, v1, s66, v90
	v_cvt_pk_fp8_f32 v102, v0, v1
	v_mul_f32_e32 v2, 0x42000000, v50
	v_mul_f32_e32 v0, 0x42000000, v42
	v_med3_f32 v1, v2, s66, v90
	v_med3_f32 v0, v0, s66, v90
	v_cvt_pk_fp8_f32 v102, v1, v0 op_sel:[0,0,1]
	v_mul_f32_e32 v0, 0x42000000, v46
	v_mul_f32_e32 v1, 0x42000000, v54
	v_med3_f32 v0, v0, s66, v90
	v_med3_f32 v1, v1, s66, v90
	v_cvt_pk_fp8_f32 v103, v0, v1
	v_mul_f32_e32 v2, 0x42000000, v58
	v_mul_f32_e32 v0, 0x42000000, v62
	v_med3_f32 v1, v2, s66, v90
	v_med3_f32 v0, v0, s66, v90
	v_cvt_pk_fp8_f32 v103, v1, v0 op_sel:[0,0,1]
	v_mul_f32_e32 v0, 0x42000000, v3
	v_mul_f32_e32 v1, 0x42000000, v7
	v_med3_f32 v3, v0, s66, v90
	v_med3_f32 v1, v1, s66, v90
	v_mov_b32_e32 v0, v69
	v_cvt_pk_fp8_f32 v0, v3, v1
	v_mul_f32_e32 v2, 0x42000000, v15
	v_mul_f32_e32 v1, 0x42000000, v11
	v_med3_f32 v2, v2, s66, v90
	v_med3_f32 v1, v1, s66, v90
	v_cvt_pk_fp8_f32 v0, v2, v1 op_sel:[0,0,1]
	v_mul_f32_e32 v1, 0x42000000, v19
	v_mul_f32_e32 v2, 0x42000000, v23
	v_med3_f32 v4, v1, s66, v90
	v_med3_f32 v2, v2, s66, v90
	v_mov_b32_e32 v1, v69
	v_cvt_pk_fp8_f32 v1, v4, v2
	v_mul_f32_e32 v3, 0x42000000, v35
	v_mul_f32_e32 v2, 0x42000000, v27
	v_med3_f32 v3, v3, s66, v90
	v_med3_f32 v2, v2, s66, v90
	v_cvt_pk_fp8_f32 v1, v3, v2 op_sel:[0,0,1]
	v_mul_f32_e32 v2, 0x42000000, v31
	v_mul_f32_e32 v3, 0x42000000, v39
	v_med3_f32 v5, v2, s66, v90
	v_med3_f32 v3, v3, s66, v90
	v_mov_b32_e32 v2, v69
	v_cvt_pk_fp8_f32 v2, v5, v3
	v_mul_f32_e32 v4, 0x42000000, v51
	v_mul_f32_e32 v3, 0x42000000, v43
	v_med3_f32 v4, v4, s66, v90
	v_med3_f32 v3, v3, s66, v90
	v_cvt_pk_fp8_f32 v2, v4, v3 op_sel:[0,0,1]
	v_mul_f32_e32 v3, 0x42000000, v47
	v_mul_f32_e32 v4, 0x42000000, v55
	v_med3_f32 v6, v3, s66, v90
	v_med3_f32 v4, v4, s66, v90
	v_mov_b32_e32 v3, v69
	v_cvt_pk_fp8_f32 v3, v6, v4
	v_mul_f32_e32 v5, 0x42000000, v59
	v_mul_f32_e32 v4, 0x42000000, v63
	v_med3_f32 v5, v5, s66, v90
	v_med3_f32 v4, v4, s66, v90
	v_cvt_pk_fp8_f32 v3, v5, v4 op_sel:[0,0,1]
	ds_write_b128 v87, v[64:67] offset:40960
	ds_write_b128 v87, v[96:99] offset:41040
	ds_write_b128 v87, v[100:103] offset:41120
	ds_write_b128 v87, v[0:3] offset:41200
	s_waitcnt lgkmcnt(0)
	ds_read_b128 v[0:3], v88 offset:40960
	v_or_b32_e32 v4, s3, v75
	v_lshl_add_u64 v[8:9], s[6:7], 0, v[70:71]
	v_lshlrev_b32_e32 v4, 9, v4
	v_mov_b32_e32 v5, v69
	v_lshl_add_u64 v[10:11], v[8:9], 0, v[4:5]
	ds_read_b128 v[4:7], v88 offset:42240
	s_waitcnt lgkmcnt(1)
	global_store_dwordx4 v[10:11], v[0:3], off sc1
	s_mov_b64 s[6:7], 0
	s_nop 0
	v_or_b32_e32 v0, s3, v76
	v_lshlrev_b32_e32 v0, 9, v0
	v_mov_b32_e32 v1, v69
	v_lshl_add_u64 v[0:1], v[8:9], 0, v[0:1]
	s_waitcnt lgkmcnt(0)
	global_store_dwordx4 v[0:1], v[4:7], off sc1
	ds_read_b128 v[0:3], v88 offset:43520
	s_nop 0
	v_or_b32_e32 v4, s3, v77
	v_lshlrev_b32_e32 v4, 9, v4
	v_mov_b32_e32 v5, v69
	v_lshl_add_u64 v[10:11], v[8:9], 0, v[4:5]
	ds_read_b128 v[4:7], v88 offset:44800
	s_waitcnt lgkmcnt(1)
	global_store_dwordx4 v[10:11], v[0:3], off sc1
	s_nop 1
	v_or_b32_e32 v0, s3, v78
	v_lshlrev_b32_e32 v0, 9, v0
	v_mov_b32_e32 v1, v69
	v_lshl_add_u64 v[0:1], v[8:9], 0, v[0:1]
	s_waitcnt lgkmcnt(0)
	global_store_dwordx4 v[0:1], v[4:7], off sc1
	s_waitcnt lgkmcnt(0)
.LBB0_1222:
	s_andn2_b64 vcc, exec, s[6:7]
	s_cbranch_vccnz .LBB0_1224
	s_ashr_i32 s3, s2, 31
	s_lshr_b32 s0, s9, 9
	s_bfe_u32 s9, s9, 0x10008
	s_lshl_b64 s[10:11], s[2:3], 27
	s_add_u32 s3, s40, s10
	s_addc_u32 s12, s41, s11
	s_lshl_b32 s13, s9, 18
	s_lshl_b64 s[6:7], s[0:1], 21
	s_add_u32 s3, s3, s6
	s_addc_u32 s6, s12, s7
	s_add_u32 s3, s3, s13
	s_addc_u32 s6, s6, 0
	s_lshl_b32 s7, s9, 3
	s_add_i32 s7, s7, 0
	s_add_i32 s7, s7, 0x204e8
	v_mov_b32_e32 v0, s7
	ds_read_b64 v[0:1], v0
	v_mov_b32_e32 v73, v69
	v_mov_b32_e32 v12, v69
	v_mov_b32_e32 v14, v69
	v_mov_b32_e32 v13, v69
	s_waitcnt lgkmcnt(0)
	v_readfirstlane_b32 s7, v0
	v_readfirstlane_b32 s9, v1
	s_add_u32 s7, s7, s10
	s_addc_u32 s9, s9, s11
	s_lshl_b64 s[10:11], s[0:1], 22
	s_add_u32 s10, s7, s10
	s_addc_u32 s11, s9, s11
	s_lshl_b32 s0, s30, 6
	s_and_b32 s7, s0, 0x7c0
	v_or_b32_e32 v0, s7, v74
	v_lshlrev_b32_e32 v0, 11, v0
	v_mov_b32_e32 v1, v69
	s_lshl_b32 s0, s8, 3
	v_lshl_add_u64 v[0:1], s[10:11], 0, v[0:1]
	s_and_b32 s0, s0, 0x700
	v_lshl_add_u64 v[0:1], v[0:1], 0, s[0:1]
	v_lshl_add_u64 v[0:1], v[0:1], 0, v[72:73]
	v_add_co_u32_e32 v2, vcc, s67, v0
	global_load_dwordx4 v[40:43], v[0:1], off nt
	global_load_dwordx4 v[44:47], v[0:1], off offset:2048 nt
	v_addc_co_u32_e32 v3, vcc, 0, v1, vcc
	v_add_co_u32_e32 v4, vcc, s58, v0
	v_mov_b32_e32 v96, v69
	s_nop 0
	v_addc_co_u32_e32 v5, vcc, 0, v1, vcc
	global_load_dwordx4 v[56:59], v[4:5], off offset:-4096 nt
	global_load_dwordx4 v[20:23], v[4:5], off nt
	global_load_dwordx4 v[24:27], v[4:5], off offset:2048 nt
	v_add_co_u32_e32 v4, vcc, s68, v0
	v_mov_b32_e32 v97, v69
	s_nop 0
	v_addc_co_u32_e32 v5, vcc, 0, v1, vcc
	v_add_co_u32_e32 v6, vcc, s59, v0
	v_mov_b32_e32 v98, v69
	s_nop 0
	v_addc_co_u32_e32 v7, vcc, 0, v1, vcc
	global_load_dwordx4 v[64:67], v[2:3], off offset:2048 nt
	global_load_dwordx4 v[36:39], v[4:5], off offset:2048 nt
	global_load_dwordx4 v[60:63], v[6:7], off offset:-4096 nt
	global_load_dwordx4 v[16:19], v[6:7], off nt
	v_add_co_u32_e32 v2, vcc, s69, v0
	v_mov_b32_e32 v99, v69
	s_nop 0
	v_addc_co_u32_e32 v3, vcc, 0, v1, vcc
	v_add_co_u32_e32 v8, vcc, s60, v0
	v_mov_b32_e32 v100, v69
	s_nop 0
	v_addc_co_u32_e32 v9, vcc, 0, v1, vcc
	global_load_dwordx4 v[48:51], v[6:7], off offset:2048 nt
	global_load_dwordx4 v[52:55], v[8:9], off offset:-4096 nt
	global_load_dwordx4 v[28:31], v[2:3], off offset:2048 nt
	s_nop 0
	global_load_dwordx4 v[4:7], v[8:9], off nt
	s_nop 0
	global_load_dwordx4 v[8:11], v[8:9], off offset:2048 nt
	v_add_co_u32_e32 v0, vcc, s70, v0
	v_mov_b32_e32 v101, v69
	s_nop 0
	v_addc_co_u32_e32 v1, vcc, 0, v1, vcc
	global_load_dwordx4 v[32:35], v[0:1], off nt
	s_nop 0
	global_load_dwordx4 v[0:3], v[0:1], off offset:2048 nt
	v_mov_b32_e32 v102, v69
	v_mov_b32_e32 v103, v69
	s_lshl_b32 s0, s8, 1
	s_add_u32 s10, s3, s7
	s_addc_u32 s11, s6, 0
	s_lshl_b32 s3, s8, 2
	s_and_b32 s3, s3, 0x300
	s_and_b32 s0, s0, 64
	s_or_b32 s0, s0, s3
	s_waitcnt vmcnt(0)
	v_mul_f32_e32 v15, 0x42800000, v40
	v_mul_f32_e32 v40, 0x42800000, v44
	v_med3_f32 v15, v15, s66, v90
	v_med3_f32 v40, v40, s66, v90
	v_cvt_pk_fp8_f32 v12, v15, v40
	v_mul_f32_e32 v44, 0x42800000, v56
	v_mul_f32_e32 v20, 0x42800000, v20
	v_mul_f32_e32 v24, 0x42800000, v24
	v_med3_f32 v15, v20, s66, v90
	v_med3_f32 v20, v24, s66, v90
	v_cvt_pk_fp8_f32 v13, v15, v20
	v_med3_f32 v44, v44, s66, v90
	v_mul_f32_e32 v56, 0x42800000, v64
	v_mul_f32_e32 v36, 0x42800000, v36
	v_mul_f32_e32 v60, 0x42800000, v60
	v_mul_f32_e32 v16, 0x42800000, v16
	v_med3_f32 v16, v16, s66, v90
	v_med3_f32 v56, v56, s66, v90
	v_med3_f32 v24, v60, s66, v90
	v_med3_f32 v36, v36, s66, v90
	v_cvt_pk_fp8_f32 v12, v44, v56 op_sel:[0,0,1]
	v_cvt_pk_fp8_f32 v13, v24, v36 op_sel:[0,0,1]
	v_mul_f32_e32 v48, 0x42800000, v48
	v_med3_f32 v40, v48, s66, v90
	v_cvt_pk_fp8_f32 v14, v16, v40
	v_mul_f32_e32 v52, 0x42800000, v52
	v_mul_f32_e32 v28, 0x42800000, v28
	v_mul_f32_e32 v4, 0x42800000, v4
	v_mul_f32_e32 v8, 0x42800000, v8
	v_med3_f32 v48, v52, s66, v90
	v_med3_f32 v15, v28, s66, v90
	v_cvt_pk_fp8_f32 v14, v48, v15 op_sel:[0,0,1]
	v_med3_f32 v4, v4, s66, v90
	v_med3_f32 v8, v8, s66, v90
	v_mov_b32_e32 v15, v69
	v_cvt_pk_fp8_f32 v15, v4, v8
	v_mul_f32_e32 v16, 0x42800000, v32
	v_mul_f32_e32 v0, 0x42800000, v0
	v_med3_f32 v4, v16, s66, v90
	v_med3_f32 v0, v0, s66, v90
	v_cvt_pk_fp8_f32 v15, v4, v0 op_sel:[0,0,1]
	v_mul_f32_e32 v0, 0x42800000, v41
	v_mul_f32_e32 v4, 0x42800000, v45
	v_med3_f32 v0, v0, s66, v90
	v_med3_f32 v4, v4, s66, v90
	v_cvt_pk_fp8_f32 v96, v0, v4
	v_mul_f32_e32 v8, 0x42800000, v57
	v_mul_f32_e32 v0, 0x42800000, v65
	v_med3_f32 v4, v8, s66, v90
	v_med3_f32 v0, v0, s66, v90
	v_cvt_pk_fp8_f32 v96, v4, v0 op_sel:[0,0,1]
	v_mul_f32_e32 v0, 0x42800000, v21
	v_mul_f32_e32 v4, 0x42800000, v25
	v_med3_f32 v0, v0, s66, v90
	v_med3_f32 v4, v4, s66, v90
	v_cvt_pk_fp8_f32 v97, v0, v4
	v_mul_f32_e32 v8, 0x42800000, v61
	v_mul_f32_e32 v0, 0x42800000, v37
	v_med3_f32 v4, v8, s66, v90
	v_med3_f32 v0, v0, s66, v90
	v_cvt_pk_fp8_f32 v97, v4, v0 op_sel:[0,0,1]
	v_mul_f32_e32 v0, 0x42800000, v17
	v_mul_f32_e32 v4, 0x42800000, v49
	v_med3_f32 v0, v0, s66, v90
	v_med3_f32 v4, v4, s66, v90
	v_cvt_pk_fp8_f32 v98, v0, v4
	v_mul_f32_e32 v8, 0x42800000, v53
	v_mul_f32_e32 v0, 0x42800000, v29
	v_med3_f32 v4, v8, s66, v90
	v_med3_f32 v0, v0, s66, v90
	v_cvt_pk_fp8_f32 v98, v4, v0 op_sel:[0,0,1]
	v_mul_f32_e32 v0, 0x42800000, v5
	v_mul_f32_e32 v4, 0x42800000, v9
	v_med3_f32 v0, v0, s66, v90
	v_med3_f32 v4, v4, s66, v90
	v_cvt_pk_fp8_f32 v99, v0, v4
	v_mul_f32_e32 v5, 0x42800000, v33
	v_mul_f32_e32 v0, 0x42800000, v1
	v_med3_f32 v1, v5, s66, v90
	v_med3_f32 v0, v0, s66, v90
	v_cvt_pk_fp8_f32 v99, v1, v0 op_sel:[0,0,1]
	v_mul_f32_e32 v0, 0x42800000, v42
	v_mul_f32_e32 v1, 0x42800000, v46
	v_med3_f32 v0, v0, s66, v90
	v_med3_f32 v1, v1, s66, v90
	v_cvt_pk_fp8_f32 v100, v0, v1
	v_mul_f32_e32 v4, 0x42800000, v58
	v_mul_f32_e32 v0, 0x42800000, v66
	v_med3_f32 v1, v4, s66, v90
	v_med3_f32 v0, v0, s66, v90
	v_cvt_pk_fp8_f32 v100, v1, v0 op_sel:[0,0,1]
	v_mul_f32_e32 v0, 0x42800000, v22
	v_mul_f32_e32 v1, 0x42800000, v26
	v_med3_f32 v0, v0, s66, v90
	v_med3_f32 v1, v1, s66, v90
	v_cvt_pk_fp8_f32 v101, v0, v1
	v_mul_f32_e32 v4, 0x42800000, v62
	v_mul_f32_e32 v0, 0x42800000, v38
	v_med3_f32 v1, v4, s66, v90
	v_med3_f32 v0, v0, s66, v90
	v_cvt_pk_fp8_f32 v101, v1, v0 op_sel:[0,0,1]
	v_mul_f32_e32 v0, 0x42800000, v18
	v_mul_f32_e32 v1, 0x42800000, v50
	v_med3_f32 v0, v0, s66, v90
	v_med3_f32 v1, v1, s66, v90
	v_cvt_pk_fp8_f32 v102, v0, v1
	v_mul_f32_e32 v4, 0x42800000, v54
	v_mul_f32_e32 v0, 0x42800000, v30
	v_med3_f32 v1, v4, s66, v90
	v_med3_f32 v0, v0, s66, v90
	v_cvt_pk_fp8_f32 v102, v1, v0 op_sel:[0,0,1]
	v_mul_f32_e32 v0, 0x42800000, v6
	v_mul_f32_e32 v1, 0x42800000, v10
	v_med3_f32 v0, v0, s66, v90
	v_med3_f32 v1, v1, s66, v90
	v_cvt_pk_fp8_f32 v103, v0, v1
	v_mul_f32_e32 v4, 0x42800000, v34
	v_mul_f32_e32 v0, 0x42800000, v2
	v_med3_f32 v1, v4, s66, v90
	v_med3_f32 v0, v0, s66, v90
	v_cvt_pk_fp8_f32 v103, v1, v0 op_sel:[0,0,1]
	v_mul_f32_e32 v0, 0x42800000, v43
	v_mul_f32_e32 v1, 0x42800000, v47
	v_med3_f32 v0, v0, s66, v90
	v_med3_f32 v1, v1, s66, v90
	v_mov_b32_e32 v4, v69
	v_cvt_pk_fp8_f32 v4, v0, v1
	v_mul_f32_e32 v2, 0x42800000, v59
	v_mul_f32_e32 v0, 0x42800000, v67
	v_med3_f32 v1, v2, s66, v90
	v_med3_f32 v0, v0, s66, v90
	v_cvt_pk_fp8_f32 v4, v1, v0 op_sel:[0,0,1]
	v_mul_f32_e32 v0, 0x42800000, v23
	v_mul_f32_e32 v1, 0x42800000, v27
	v_med3_f32 v0, v0, s66, v90
	v_med3_f32 v1, v1, s66, v90
	v_mov_b32_e32 v5, v69
	v_cvt_pk_fp8_f32 v5, v0, v1
	v_mul_f32_e32 v2, 0x42800000, v63
	v_mul_f32_e32 v0, 0x42800000, v39
	v_med3_f32 v1, v2, s66, v90
	v_med3_f32 v0, v0, s66, v90
	v_cvt_pk_fp8_f32 v5, v1, v0 op_sel:[0,0,1]
	v_mul_f32_e32 v0, 0x42800000, v19
	v_mul_f32_e32 v1, 0x42800000, v51
	v_med3_f32 v0, v0, s66, v90
	v_med3_f32 v1, v1, s66, v90
	v_mov_b32_e32 v6, v69
	v_cvt_pk_fp8_f32 v6, v0, v1
	v_mul_f32_e32 v2, 0x42800000, v55
	v_mul_f32_e32 v0, 0x42800000, v31
	v_med3_f32 v1, v2, s66, v90
	v_med3_f32 v0, v0, s66, v90
	v_cvt_pk_fp8_f32 v6, v1, v0 op_sel:[0,0,1]
	v_mul_f32_e32 v0, 0x42800000, v7
	v_mul_f32_e32 v1, 0x42800000, v11
	v_med3_f32 v0, v0, s66, v90
	v_med3_f32 v1, v1, s66, v90
	v_mov_b32_e32 v7, v69
	v_cvt_pk_fp8_f32 v7, v0, v1
	v_mul_f32_e32 v2, 0x42800000, v35
	v_mul_f32_e32 v0, 0x42800000, v3
	v_med3_f32 v1, v2, s66, v90
	v_med3_f32 v0, v0, s66, v90
	v_cvt_pk_fp8_f32 v7, v1, v0 op_sel:[0,0,1]
	ds_write_b128 v87, v[12:15] offset:40960
	ds_write_b128 v87, v[96:99] offset:41040
	ds_write_b128 v87, v[100:103] offset:41120
	ds_write_b128 v87, v[4:7] offset:41200
	s_waitcnt lgkmcnt(0)
	ds_read_b128 v[0:3], v88 offset:40960
	v_or_b32_e32 v4, s0, v75
	v_lshl_add_u64 v[8:9], s[10:11], 0, v[70:71]
	v_lshlrev_b32_e32 v4, 11, v4
	v_mov_b32_e32 v5, v69
	v_lshl_add_u64 v[10:11], v[8:9], 0, v[4:5]
	ds_read_b128 v[4:7], v88 offset:42240
	s_waitcnt lgkmcnt(1)
	global_store_dwordx4 v[10:11], v[0:3], off sc1
	s_nop 1
	v_or_b32_e32 v0, s0, v76
	v_lshlrev_b32_e32 v0, 11, v0
	v_mov_b32_e32 v1, v69
	v_lshl_add_u64 v[0:1], v[8:9], 0, v[0:1]
	s_waitcnt lgkmcnt(0)
	global_store_dwordx4 v[0:1], v[4:7], off sc1
	ds_read_b128 v[0:3], v88 offset:43520
	s_nop 0
	v_or_b32_e32 v4, s0, v77
	v_lshlrev_b32_e32 v4, 11, v4
	v_mov_b32_e32 v5, v69
	v_lshl_add_u64 v[10:11], v[8:9], 0, v[4:5]
	ds_read_b128 v[4:7], v88 offset:44800
	s_waitcnt lgkmcnt(1)
	global_store_dwordx4 v[10:11], v[0:3], off sc1
	s_nop 1
	v_or_b32_e32 v0, s0, v78
	v_lshlrev_b32_e32 v0, 11, v0
	v_mov_b32_e32 v1, v69
	v_lshl_add_u64 v[0:1], v[8:9], 0, v[0:1]
	s_waitcnt lgkmcnt(0)
	global_store_dwordx4 v[0:1], v[4:7], off sc1
	s_waitcnt lgkmcnt(0)

.LBB0_1254:
	s_cmpk_gt_i32 s94, 0x93
	s_cbranch_scc1 .LBB0_1256
	s_lshl_b32 s28, s3, 6
	s_mul_i32 s29, s2, 0x1280000
	v_or_b32_e32 v0, s28, v74
	s_mul_hi_i32 s21, s2, 0x1280000
	s_add_u32 s29, s50, s29
	v_mul_hi_i32_i24_e32 v1, 0x9500, v0
	v_mul_i32_i24_e32 v0, 0x9500, v0
	s_addc_u32 s30, s51, s21
	v_lshl_add_u64 v[0:1], s[6:7], 0, v[0:1]
	s_ashr_i32 s21, s20, 31
	v_lshl_add_u64 v[0:1], s[20:21], 2, v[0:1]
	v_mov_b32_e32 v73, v69
	v_lshl_add_u64 v[56:57], v[0:1], 0, v[72:73]
	v_add_co_u32_e32 v4, vcc, s78, v56
	global_load_dwordx4 v[0:3], v[56:57], off nt
	s_nop 0
	v_addc_co_u32_e32 v5, vcc, 0, v57, vcc
	global_load_dwordx4 v[16:19], v[4:5], off offset:1280 nt
	v_add_co_u32_e32 v4, vcc, s62, v56
	v_mov_b32_e32 v64, v69
	s_nop 0
	v_addc_co_u32_e32 v5, vcc, 0, v57, vcc
	global_load_dwordx4 v[20:23], v[4:5], off offset:2560 nt
	v_add_co_u32_e32 v4, vcc, s79, v56
	v_mov_b32_e32 v65, v69
	s_nop 0
	v_addc_co_u32_e32 v5, vcc, 0, v57, vcc
	global_load_dwordx4 v[44:47], v[4:5], off offset:3840 nt
	v_add_co_u32_e32 v4, vcc, s80, v56
	v_mov_b32_e32 v66, v69
	s_nop 0
	v_addc_co_u32_e32 v5, vcc, 0, v57, vcc
	v_add_co_u32_e32 v8, vcc, s81, v56
	global_load_dwordx4 v[4:7], v[4:5], off offset:1024 nt
	s_nop 0
	v_addc_co_u32_e32 v9, vcc, 0, v57, vcc
	global_load_dwordx4 v[24:27], v[8:9], off offset:2304 nt
	v_add_co_u32_e32 v8, vcc, s82, v56
	v_mov_b32_e32 v67, v69
	s_nop 0
	v_addc_co_u32_e32 v9, vcc, 0, v57, vcc
	global_load_dwordx4 v[28:31], v[8:9], off offset:3584 nt
	v_add_co_u32_e32 v8, vcc, s83, v56
	s_ashr_i32 s21, s28, 31
	s_nop 0
	v_addc_co_u32_e32 v9, vcc, 0, v57, vcc
	global_load_dwordx4 v[52:55], v[8:9], off offset:768 nt
	v_add_co_u32_e32 v8, vcc, s84, v56
	s_add_u32 s28, s29, s28
	s_nop 0
	v_addc_co_u32_e32 v9, vcc, 0, v57, vcc
	v_add_co_u32_e32 v12, vcc, s85, v56
	global_load_dwordx4 v[8:11], v[8:9], off offset:2048 nt
	s_nop 0
	v_addc_co_u32_e32 v13, vcc, 0, v57, vcc
	global_load_dwordx4 v[32:35], v[12:13], off offset:3328 nt
	v_add_co_u32_e32 v12, vcc, s86, v56
	s_addc_u32 s29, s30, s21
	s_nop 0
	v_addc_co_u32_e32 v13, vcc, 0, v57, vcc
	global_load_dwordx4 v[36:39], v[12:13], off offset:512 nt
	v_add_co_u32_e32 v12, vcc, s87, v56
	s_mov_b64 s[30:31], 0
	s_nop 0
	v_addc_co_u32_e32 v13, vcc, 0, v57, vcc
	global_load_dwordx4 v[60:63], v[12:13], off offset:1792 nt
	v_add_co_u32_e32 v12, vcc, s88, v56
	s_waitcnt vmcnt(0)
	v_mul_f32_e32 v0, 0x42800000, v0
	v_addc_co_u32_e32 v13, vcc, 0, v57, vcc
	v_add_co_u32_e32 v40, vcc, s89, v56
	global_load_dwordx4 v[12:15], v[12:13], off offset:3072 nt
	s_nop 0
	v_addc_co_u32_e32 v41, vcc, 0, v57, vcc
	global_load_dwordx4 v[40:43], v[40:41], off offset:256 nt
	v_add_co_u32_e32 v48, vcc, s90, v56
	v_mul_f32_e32 v16, 0x42800000, v16
	s_nop 0
	v_addc_co_u32_e32 v49, vcc, 0, v57, vcc
	v_add_co_u32_e32 v56, vcc, s91, v56
	global_load_dwordx4 v[48:51], v[48:49], off offset:1536 nt
	s_nop 0
	v_addc_co_u32_e32 v57, vcc, 0, v57, vcc
	global_load_dwordx4 v[56:59], v[56:57], off offset:2816 nt
	v_med3_f32 v0, v0, s66, v90
	v_med3_f32 v16, v16, s66, v90
	v_cvt_pk_fp8_f32 v64, v0, v16
	v_mul_f32_e32 v0, 0x42800000, v4
	v_med3_f32 v0, v0, s66, v90
	v_mul_f32_e32 v20, 0x42800000, v20
	v_mul_f32_e32 v4, 0x42800000, v24
	v_med3_f32 v4, v4, s66, v90
	v_mul_f32_e32 v44, 0x42800000, v44
	v_cvt_pk_fp8_f32 v65, v0, v4
	v_med3_f32 v20, v20, s66, v90
	v_med3_f32 v44, v44, s66, v90
	v_cvt_pk_fp8_f32 v64, v20, v44 op_sel:[0,0,1]
	v_mul_f32_e32 v16, 0x42800000, v28
	v_med3_f32 v16, v16, s66, v90
	v_mul_f32_e32 v20, 0x42800000, v52
	v_med3_f32 v20, v20, s66, v90
	v_cvt_pk_fp8_f32 v65, v16, v20 op_sel:[0,0,1]
	v_mul_f32_e32 v0, 0x42800000, v8
	v_med3_f32 v0, v0, s66, v90
	v_mul_f32_e32 v4, 0x42800000, v32
	v_med3_f32 v4, v4, s66, v90
	v_cvt_pk_fp8_f32 v66, v0, v4
	v_mul_f32_e32 v8, 0x42800000, v36
	v_med3_f32 v8, v8, s66, v90
	v_mul_f32_e32 v16, 0x42800000, v60
	v_med3_f32 v16, v16, s66, v90
	v_cvt_pk_fp8_f32 v66, v8, v16 op_sel:[0,0,1]
	s_waitcnt vmcnt(0)
	v_mul_f32_e32 v0, 0x42800000, v12
	v_med3_f32 v0, v0, s66, v90
	v_mul_f32_e32 v4, 0x42800000, v40
	v_med3_f32 v4, v4, s66, v90
	v_cvt_pk_fp8_f32 v67, v0, v4
	v_mul_f32_e32 v0, 0x42800000, v1
	v_mul_f32_e32 v1, 0x42800000, v17
	v_med3_f32 v0, v0, s66, v90
	v_med3_f32 v1, v1, s66, v90
	v_mul_f32_e32 v4, 0x42800000, v21
	v_mul_f32_e32 v8, 0x42800000, v48
	v_med3_f32 v8, v8, s66, v90
	v_med3_f32 v4, v4, s66, v90
	v_mul_f32_e32 v12, 0x42800000, v56
	v_med3_f32 v12, v12, s66, v90
	v_cvt_pk_fp8_f32 v67, v8, v12 op_sel:[0,0,1]
	v_mul_f32_e32 v8, 0x42800000, v45
	v_med3_f32 v8, v8, s66, v90
	ds_write_b128 v87, v[64:67] offset:40960
	v_mov_b32_e32 v64, v69
	v_cvt_pk_fp8_f32 v64, v0, v1
	v_mul_f32_e32 v0, 0x42800000, v5
	v_mul_f32_e32 v1, 0x42800000, v25
	v_med3_f32 v0, v0, s66, v90
	v_med3_f32 v1, v1, s66, v90
	v_mov_b32_e32 v65, v69
	v_cvt_pk_fp8_f32 v65, v0, v1
	v_mul_f32_e32 v0, 0x42800000, v9
	v_mul_f32_e32 v1, 0x42800000, v33
	v_med3_f32 v0, v0, s66, v90
	v_med3_f32 v1, v1, s66, v90
	v_mov_b32_e32 v66, v69
	v_cvt_pk_fp8_f32 v64, v4, v8 op_sel:[0,0,1]
	v_mul_f32_e32 v4, 0x42800000, v29
	v_mul_f32_e32 v5, 0x42800000, v53
	v_cvt_pk_fp8_f32 v66, v0, v1
	v_mul_f32_e32 v0, 0x42800000, v13
	v_mul_f32_e32 v1, 0x42800000, v41
	v_med3_f32 v4, v4, s66, v90
	v_med3_f32 v5, v5, s66, v90
	v_med3_f32 v0, v0, s66, v90
	v_med3_f32 v1, v1, s66, v90
	v_mov_b32_e32 v67, v69
	v_cvt_pk_fp8_f32 v65, v4, v5 op_sel:[0,0,1]
	v_mul_f32_e32 v4, 0x42800000, v37
	v_mul_f32_e32 v5, 0x42800000, v61
	v_cvt_pk_fp8_f32 v67, v0, v1
	v_med3_f32 v4, v4, s66, v90
	v_med3_f32 v5, v5, s66, v90
	v_cvt_pk_fp8_f32 v66, v4, v5 op_sel:[0,0,1]
	v_mul_f32_e32 v4, 0x42800000, v49
	v_mul_f32_e32 v5, 0x42800000, v57
	v_med3_f32 v4, v4, s66, v90
	v_med3_f32 v5, v5, s66, v90
	v_cvt_pk_fp8_f32 v67, v4, v5 op_sel:[0,0,1]
	v_mul_f32_e32 v0, 0x42800000, v2
	v_mul_f32_e32 v1, 0x42800000, v18
	v_med3_f32 v0, v0, s66, v90
	ds_write_b128 v87, v[64:67] offset:41040
	v_med3_f32 v1, v1, s66, v90
	v_mov_b32_e32 v64, v69
	v_cvt_pk_fp8_f32 v64, v0, v1
	v_mul_f32_e32 v0, 0x42800000, v6
	v_mul_f32_e32 v1, 0x42800000, v26
	v_med3_f32 v0, v0, s66, v90
	v_med3_f32 v1, v1, s66, v90
	v_mov_b32_e32 v65, v69
	v_mul_f32_e32 v2, 0x42800000, v22
	v_mul_f32_e32 v4, 0x42800000, v46
	v_cvt_pk_fp8_f32 v65, v0, v1
	v_mul_f32_e32 v0, 0x42800000, v10
	v_mul_f32_e32 v1, 0x42800000, v34
	v_med3_f32 v2, v2, s66, v90
	v_med3_f32 v4, v4, s66, v90
	v_med3_f32 v0, v0, s66, v90
	v_med3_f32 v1, v1, s66, v90
	v_mov_b32_e32 v66, v69
	v_cvt_pk_fp8_f32 v64, v2, v4 op_sel:[0,0,1]
	v_mul_f32_e32 v2, 0x42800000, v30
	v_mul_f32_e32 v4, 0x42800000, v54
	v_cvt_pk_fp8_f32 v66, v0, v1
	v_mul_f32_e32 v0, 0x42800000, v14
	v_mul_f32_e32 v1, 0x42800000, v42
	v_med3_f32 v2, v2, s66, v90
	v_med3_f32 v4, v4, s66, v90
	v_med3_f32 v0, v0, s66, v90
	v_med3_f32 v1, v1, s66, v90
	v_mov_b32_e32 v67, v69
	v_cvt_pk_fp8_f32 v65, v2, v4 op_sel:[0,0,1]
	v_mul_f32_e32 v2, 0x42800000, v38
	v_mul_f32_e32 v4, 0x42800000, v62
	v_cvt_pk_fp8_f32 v67, v0, v1
	v_med3_f32 v2, v2, s66, v90
	v_med3_f32 v4, v4, s66, v90
	v_cvt_pk_fp8_f32 v66, v2, v4 op_sel:[0,0,1]
	v_mul_f32_e32 v2, 0x42800000, v50
	v_mul_f32_e32 v4, 0x42800000, v58
	v_med3_f32 v2, v2, s66, v90
	v_med3_f32 v4, v4, s66, v90
	v_mul_f32_e32 v0, 0x42800000, v3
	v_mul_f32_e32 v1, 0x42800000, v19
	v_cvt_pk_fp8_f32 v67, v2, v4 op_sel:[0,0,1]
	v_med3_f32 v4, v0, s66, v90
	v_med3_f32 v1, v1, s66, v90
	v_mov_b32_e32 v0, v69
	v_cvt_pk_fp8_f32 v0, v4, v1
	v_mul_f32_e32 v2, 0x42800000, v23
	v_mul_f32_e32 v3, 0x42800000, v47
	v_med3_f32 v2, v2, s66, v90
	v_med3_f32 v3, v3, s66, v90
	v_cvt_pk_fp8_f32 v0, v2, v3 op_sel:[0,0,1]
	v_mul_f32_e32 v1, 0x42800000, v7
	v_mul_f32_e32 v2, 0x42800000, v27
	v_med3_f32 v5, v1, s66, v90
	v_med3_f32 v2, v2, s66, v90
	v_mov_b32_e32 v1, v69
	v_cvt_pk_fp8_f32 v1, v5, v2
	v_mul_f32_e32 v3, 0x42800000, v31
	v_mul_f32_e32 v4, 0x42800000, v55
	v_med3_f32 v3, v3, s66, v90
	v_med3_f32 v4, v4, s66, v90
	v_cvt_pk_fp8_f32 v1, v3, v4 op_sel:[0,0,1]
	v_mul_f32_e32 v2, 0x42800000, v11
	v_mul_f32_e32 v3, 0x42800000, v35
	v_med3_f32 v6, v2, s66, v90
	v_med3_f32 v3, v3, s66, v90
	v_mov_b32_e32 v2, v69
	v_cvt_pk_fp8_f32 v2, v6, v3
	v_mul_f32_e32 v4, 0x42800000, v39
	v_mul_f32_e32 v5, 0x42800000, v63
	v_med3_f32 v4, v4, s66, v90
	v_med3_f32 v5, v5, s66, v90
	v_cvt_pk_fp8_f32 v2, v4, v5 op_sel:[0,0,1]
	v_mul_f32_e32 v3, 0x42800000, v15
	v_mul_f32_e32 v4, 0x42800000, v43
	v_med3_f32 v7, v3, s66, v90
	v_med3_f32 v4, v4, s66, v90
	v_mov_b32_e32 v3, v69
	v_cvt_pk_fp8_f32 v3, v7, v4
	v_mul_f32_e32 v5, 0x42800000, v51
	v_mul_f32_e32 v6, 0x42800000, v59
	v_med3_f32 v5, v5, s66, v90
	v_med3_f32 v6, v6, s66, v90
	v_cvt_pk_fp8_f32 v3, v5, v6 op_sel:[0,0,1]
	ds_write_b128 v87, v[64:67] offset:41120
	v_or_b32_e32 v6, s13, v75
	v_ashrrev_i32_e32 v7, 31, v6
	ds_write_b128 v87, v[0:3] offset:41200
	s_waitcnt lgkmcnt(0)
	ds_read_b128 v[0:3], v88 offset:40960
	v_lshl_add_u64 v[4:5], s[28:29], 0, v[70:71]
	v_lshlrev_b64 v[6:7], 11, v[6:7]
	v_lshl_add_u64 v[6:7], v[4:5], 0, v[6:7]
	s_waitcnt lgkmcnt(0)
	global_store_dwordx4 v[6:7], v[0:3], off sc1
	ds_read_b128 v[0:3], v88 offset:42240
	v_or_b32_e32 v6, s13, v76
	v_ashrrev_i32_e32 v7, 31, v6
	v_lshlrev_b64 v[6:7], 11, v[6:7]
	v_lshl_add_u64 v[6:7], v[4:5], 0, v[6:7]
	s_waitcnt lgkmcnt(0)
	global_store_dwordx4 v[6:7], v[0:3], off sc1
	ds_read_b128 v[0:3], v88 offset:43520
	v_or_b32_e32 v6, s13, v77
	v_ashrrev_i32_e32 v7, 31, v6
	v_lshlrev_b64 v[6:7], 11, v[6:7]
	v_lshl_add_u64 v[6:7], v[4:5], 0, v[6:7]
	s_waitcnt lgkmcnt(0)
	global_store_dwordx4 v[6:7], v[0:3], off sc1
	ds_read_b128 v[0:3], v88 offset:44800
	v_or_b32_e32 v6, s13, v78
	v_ashrrev_i32_e32 v7, 31, v6
	v_lshlrev_b64 v[6:7], 11, v[6:7]
	v_lshl_add_u64 v[4:5], v[4:5], 0, v[6:7]
	s_waitcnt lgkmcnt(0)
	global_store_dwordx4 v[4:5], v[0:3], off sc1
	s_waitcnt lgkmcnt(0)
.LBB0_1256:
	s_and_b64 vcc, exec, s[30:31]
	s_cbranch_vccz .LBB0_1218
	s_xor_b64 s[30:31], s[22:23], -1
	s_lshl_b32 s22, s3, 6
	s_mov_b64 s[28:29], -1
	s_and_b64 vcc, exec, s[30:31]
	s_cbranch_vccz .LBB0_1287
	s_andn2_b64 vcc, exec, s[26:27]
	s_cbranch_vccnz .LBB0_1261
	s_ashr_i32 s3, s2, 31
	s_lshl_b64 s[26:27], s[2:3], 22
	v_or_b32_e32 v0, s22, v74
	s_add_u32 s3, s52, s26
	v_mul_hi_i32_i24_e32 v1, s16, v0
	v_mul_i32_i24_e32 v0, s16, v0
	s_addc_u32 s23, s53, s27
	v_lshl_add_u64 v[0:1], v[0:1], 2, s[6:7]
	s_ashr_i32 s21, s20, 31
	v_lshl_add_u64 v[0:1], s[20:21], 2, v[0:1]
	v_mov_b32_e32 v73, v69
	v_lshl_add_u64 v[0:1], v[0:1], 0, v[72:73]
	s_lshl_b64 s[26:27], s[16:17], 2
	global_load_dwordx4 v[56:59], v[0:1], off nt
	v_lshl_add_u64 v[0:1], v[0:1], 0, s[26:27]
	global_load_dwordx4 v[60:63], v[0:1], off nt
	v_lshl_add_u64 v[0:1], v[0:1], 0, s[26:27]
	global_load_dwordx4 v[64:67], v[0:1], off nt
	v_lshl_add_u64 v[0:1], v[0:1], 0, s[26:27]
	global_load_dwordx4 v[52:55], v[0:1], off nt
	v_lshl_add_u64 v[0:1], v[0:1], 0, s[26:27]
	global_load_dwordx4 v[40:43], v[0:1], off nt
	v_lshl_add_u64 v[0:1], v[0:1], 0, s[26:27]
	global_load_dwordx4 v[44:47], v[0:1], off nt
	v_lshl_add_u64 v[0:1], v[0:1], 0, s[26:27]
	global_load_dwordx4 v[48:51], v[0:1], off nt
	v_lshl_add_u64 v[0:1], v[0:1], 0, s[26:27]
	global_load_dwordx4 v[36:39], v[0:1], off nt
	v_lshl_add_u64 v[0:1], v[0:1], 0, s[26:27]
	global_load_dwordx4 v[24:27], v[0:1], off nt
	v_lshl_add_u64 v[0:1], v[0:1], 0, s[26:27]
	global_load_dwordx4 v[28:31], v[0:1], off nt
	v_lshl_add_u64 v[0:1], v[0:1], 0, s[26:27]
	global_load_dwordx4 v[32:35], v[0:1], off nt
	v_lshl_add_u64 v[0:1], v[0:1], 0, s[26:27]
	global_load_dwordx4 v[20:23], v[0:1], off nt
	v_lshl_add_u64 v[0:1], v[0:1], 0, s[26:27]
	global_load_dwordx4 v[4:7], v[0:1], off nt
	v_lshl_add_u64 v[0:1], v[0:1], 0, s[26:27]
	global_load_dwordx4 v[12:15], v[0:1], off nt
	v_lshl_add_u64 v[0:1], v[0:1], 0, s[26:27]
	global_load_dwordx4 v[16:19], v[0:1], off nt
	v_lshl_add_u64 v[0:1], v[0:1], 0, s[26:27]
	global_load_dwordx4 v[0:3], v[0:1], off nt
	v_mov_b32_e32 v11, v69
	v_mov_b32_e32 v97, v69
	v_mov_b32_e32 v98, v69
	v_mov_b32_e32 v99, v69
	v_mov_b32_e32 v100, v69
	v_mov_b32_e32 v101, v69
	v_mov_b32_e32 v102, v69
	v_mov_b32_e32 v103, v69
	v_mov_b32_e32 v8, v69
	v_mov_b32_e32 v9, v69
	v_mov_b32_e32 v10, v69
	v_mov_b32_e32 v96, v69
	s_ashr_i32 s21, s22, 31
	s_add_u32 s26, s3, s22
	s_addc_u32 s27, s23, s21
	s_add_i32 s3, s92, 0x111c8
	s_cmpk_lt_u32 s3, 0xf97f
	s_waitcnt vmcnt(0)
	v_mul_f32_e32 v56, 0x42800000, v56
	v_mul_f32_e32 v57, 0x42800000, v57
	v_mul_f32_e32 v60, 0x42800000, v60
	v_med3_f32 v56, v56, s66, v90
	v_mul_f32_e32 v61, 0x42800000, v61
	v_med3_f32 v60, v60, s66, v90
	v_med3_f32 v57, v57, s66, v90
	v_med3_f32 v61, v61, s66, v90
	v_mul_f32_e32 v41, 0x42800000, v41
	v_med3_f32 v41, v41, s66, v90
	v_mul_f32_e32 v45, 0x42800000, v45
	v_med3_f32 v45, v45, s66, v90
	v_cvt_pk_fp8_f32 v97, v41, v45
	v_mul_f32_e32 v49, 0x42800000, v49
	v_mul_f32_e32 v40, 0x42800000, v40
	v_mul_f32_e32 v44, 0x42800000, v44
	v_mul_f32_e32 v24, 0x42800000, v24
	v_med3_f32 v40, v40, s66, v90
	v_mul_f32_e32 v28, 0x42800000, v28
	v_med3_f32 v44, v44, s66, v90
	v_med3_f32 v24, v24, s66, v90
	v_med3_f32 v28, v28, s66, v90
	v_cvt_pk_fp8_f32 v8, v56, v60
	v_cvt_pk_fp8_f32 v9, v40, v44
	v_mul_f32_e32 v4, 0x42800000, v4
	v_med3_f32 v4, v4, s66, v90
	v_mul_f32_e32 v12, 0x42800000, v12
	v_med3_f32 v12, v12, s66, v90
	v_cvt_pk_fp8_f32 v11, v4, v12
	v_mul_f32_e32 v16, 0x42800000, v16
	v_mul_f32_e32 v0, 0x42800000, v0
	v_med3_f32 v4, v16, s66, v90
	v_med3_f32 v0, v0, s66, v90
	v_cvt_pk_fp8_f32 v11, v4, v0 op_sel:[0,0,1]
	v_mul_f32_e32 v0, 0x42800000, v37
	v_med3_f32 v4, v49, s66, v90
	v_med3_f32 v0, v0, s66, v90
	v_cvt_pk_fp8_f32 v97, v4, v0 op_sel:[0,0,1]
	v_mul_f32_e32 v0, 0x42800000, v25
	v_mul_f32_e32 v4, 0x42800000, v29
	v_med3_f32 v0, v0, s66, v90
	v_med3_f32 v4, v4, s66, v90
	v_cvt_pk_fp8_f32 v98, v0, v4
	v_mul_f32_e32 v12, 0x42800000, v33
	v_mul_f32_e32 v0, 0x42800000, v21
	v_med3_f32 v4, v12, s66, v90
	v_med3_f32 v0, v0, s66, v90
	v_cvt_pk_fp8_f32 v98, v4, v0 op_sel:[0,0,1]
	v_mul_f32_e32 v0, 0x42800000, v5
	v_mul_f32_e32 v4, 0x42800000, v13
	v_med3_f32 v0, v0, s66, v90
	v_med3_f32 v4, v4, s66, v90
	v_cvt_pk_fp8_f32 v99, v0, v4
	v_mul_f32_e32 v5, 0x42800000, v17
	v_mul_f32_e32 v0, 0x42800000, v1
	v_med3_f32 v1, v5, s66, v90
	v_med3_f32 v0, v0, s66, v90
	v_cvt_pk_fp8_f32 v99, v1, v0 op_sel:[0,0,1]
	v_mul_f32_e32 v0, 0x42800000, v58
	v_mul_f32_e32 v1, 0x42800000, v62
	v_med3_f32 v0, v0, s66, v90
	v_med3_f32 v1, v1, s66, v90
	v_cvt_pk_fp8_f32 v100, v0, v1
	v_mul_f32_e32 v4, 0x42800000, v66
	v_mul_f32_e32 v0, 0x42800000, v54
	v_med3_f32 v1, v4, s66, v90
	v_med3_f32 v0, v0, s66, v90
	v_cvt_pk_fp8_f32 v100, v1, v0 op_sel:[0,0,1]
	v_mul_f32_e32 v0, 0x42800000, v42
	v_mul_f32_e32 v1, 0x42800000, v46
	v_med3_f32 v0, v0, s66, v90
	v_med3_f32 v1, v1, s66, v90
	v_cvt_pk_fp8_f32 v101, v0, v1
	v_mul_f32_e32 v4, 0x42800000, v50
	v_mul_f32_e32 v0, 0x42800000, v38
	v_med3_f32 v1, v4, s66, v90
	v_med3_f32 v0, v0, s66, v90
	v_cvt_pk_fp8_f32 v101, v1, v0 op_sel:[0,0,1]
	v_mul_f32_e32 v0, 0x42800000, v26
	v_mul_f32_e32 v1, 0x42800000, v30
	v_med3_f32 v0, v0, s66, v90
	v_med3_f32 v1, v1, s66, v90
	v_cvt_pk_fp8_f32 v102, v0, v1
	v_mul_f32_e32 v4, 0x42800000, v34
	v_mul_f32_e32 v0, 0x42800000, v22
	v_med3_f32 v1, v4, s66, v90
	v_med3_f32 v0, v0, s66, v90
	v_cvt_pk_fp8_f32 v102, v1, v0 op_sel:[0,0,1]
	v_mul_f32_e32 v0, 0x42800000, v6
	v_mul_f32_e32 v1, 0x42800000, v14
	v_med3_f32 v0, v0, s66, v90
	v_med3_f32 v1, v1, s66, v90
	v_cvt_pk_fp8_f32 v103, v0, v1
	v_mul_f32_e32 v4, 0x42800000, v18
	v_mul_f32_e32 v0, 0x42800000, v2
	v_med3_f32 v1, v4, s66, v90
	v_med3_f32 v0, v0, s66, v90
	v_cvt_pk_fp8_f32 v103, v1, v0 op_sel:[0,0,1]
	v_mul_f32_e32 v0, 0x42800000, v59
	v_mul_f32_e32 v1, 0x42800000, v63
	v_med3_f32 v0, v0, s66, v90
	v_med3_f32 v1, v1, s66, v90
	v_mov_b32_e32 v4, v69
	v_cvt_pk_fp8_f32 v4, v0, v1
	v_mul_f32_e32 v2, 0x42800000, v67
	v_mul_f32_e32 v0, 0x42800000, v55
	v_med3_f32 v1, v2, s66, v90
	v_med3_f32 v0, v0, s66, v90
	v_cvt_pk_fp8_f32 v4, v1, v0 op_sel:[0,0,1]
	v_mul_f32_e32 v0, 0x42800000, v43
	v_mul_f32_e32 v1, 0x42800000, v47
	v_med3_f32 v0, v0, s66, v90
	v_med3_f32 v1, v1, s66, v90
	v_mov_b32_e32 v5, v69
	v_cvt_pk_fp8_f32 v5, v0, v1
	v_mul_f32_e32 v2, 0x42800000, v51
	v_mul_f32_e32 v0, 0x42800000, v39
	v_med3_f32 v1, v2, s66, v90
	v_med3_f32 v0, v0, s66, v90
	v_cvt_pk_fp8_f32 v5, v1, v0 op_sel:[0,0,1]
	v_mul_f32_e32 v0, 0x42800000, v27
	v_mul_f32_e32 v1, 0x42800000, v31
	v_med3_f32 v0, v0, s66, v90
	v_med3_f32 v1, v1, s66, v90
	v_mov_b32_e32 v6, v69
	v_cvt_pk_fp8_f32 v6, v0, v1
	v_mul_f32_e32 v2, 0x42800000, v35
	v_mul_f32_e32 v0, 0x42800000, v23
	v_cvt_pk_fp8_f32 v10, v24, v28
	v_med3_f32 v1, v2, s66, v90
	v_med3_f32 v0, v0, s66, v90
	v_cvt_pk_fp8_f32 v96, v57, v61
	v_cvt_pk_fp8_f32 v6, v1, v0 op_sel:[0,0,1]
	v_mul_f32_e32 v0, 0x42800000, v7
	v_mul_f32_e32 v1, 0x42800000, v15
	v_mul_f32_e32 v64, 0x42800000, v64
	v_mul_f32_e32 v52, 0x42800000, v52
	v_mul_f32_e32 v48, 0x42800000, v48
	v_mul_f32_e32 v36, 0x42800000, v36
	v_mul_f32_e32 v32, 0x42800000, v32
	v_mul_f32_e32 v20, 0x42800000, v20
	v_med3_f32 v0, v0, s66, v90
	v_med3_f32 v1, v1, s66, v90
	v_mov_b32_e32 v7, v69
	v_mul_f32_e32 v65, 0x42800000, v65
	v_med3_f32 v64, v64, s66, v90
	v_mul_f32_e32 v53, 0x42800000, v53
	v_med3_f32 v52, v52, s66, v90
	v_med3_f32 v48, v48, s66, v90
	v_med3_f32 v36, v36, s66, v90
	v_med3_f32 v32, v32, s66, v90
	v_med3_f32 v20, v20, s66, v90
	v_cvt_pk_fp8_f32 v7, v0, v1
	v_med3_f32 v56, v65, s66, v90
	v_med3_f32 v53, v53, s66, v90
	v_cvt_pk_fp8_f32 v8, v64, v52 op_sel:[0,0,1]
	v_cvt_pk_fp8_f32 v9, v48, v36 op_sel:[0,0,1]
	v_cvt_pk_fp8_f32 v10, v32, v20 op_sel:[0,0,1]
	v_cvt_pk_fp8_f32 v96, v56, v53 op_sel:[0,0,1]
	v_mul_f32_e32 v2, 0x42800000, v19
	v_mul_f32_e32 v0, 0x42800000, v3
	v_med3_f32 v1, v2, s66, v90
	v_med3_f32 v0, v0, s66, v90
	v_cvt_pk_fp8_f32 v7, v1, v0 op_sel:[0,0,1]
	ds_write_b128 v87, v[8:11] offset:40960
	ds_write_b128 v87, v[96:99] offset:41040
	ds_write_b128 v87, v[100:103] offset:41120
	ds_write_b128 v87, v[4:7] offset:41200
	s_waitcnt lgkmcnt(0)
	ds_read_b128 v[0:3], v88 offset:40960
	v_or_b32_e32 v4, s13, v75
	v_ashrrev_i32_e32 v5, 31, v4
	v_lshl_add_u64 v[8:9], s[26:27], 0, v[70:71]
	v_lshlrev_b64 v[4:5], 11, v[4:5]
	v_lshl_add_u64 v[10:11], v[8:9], 0, v[4:5]
	ds_read_b128 v[4:7], v88 offset:42240
	s_waitcnt lgkmcnt(0)
	global_store_dwordx4 v[10:11], v[0:3], off sc1
	s_cselect_b64 s[26:27], -1, 0
	s_nop 0
	v_or_b32_e32 v0, s13, v76
	v_ashrrev_i32_e32 v1, 31, v0
	v_lshlrev_b64 v[0:1], 11, v[0:1]
	v_lshl_add_u64 v[0:1], v[8:9], 0, v[0:1]
	global_store_dwordx4 v[0:1], v[4:7], off sc1
	ds_read_b128 v[0:3], v88 offset:43520
	s_nop 0
	v_or_b32_e32 v4, s13, v77
	v_ashrrev_i32_e32 v5, 31, v4
	v_lshlrev_b64 v[4:5], 11, v[4:5]
	v_lshl_add_u64 v[10:11], v[8:9], 0, v[4:5]
	ds_read_b128 v[4:7], v88 offset:44800
	s_waitcnt lgkmcnt(1)
	global_store_dwordx4 v[10:11], v[0:3], off sc1
	s_nop 1
	v_or_b32_e32 v0, s13, v78
	v_ashrrev_i32_e32 v1, 31, v0
	v_lshlrev_b64 v[0:1], 11, v[0:1]
	v_lshl_add_u64 v[0:1], v[8:9], 0, v[0:1]
	s_waitcnt lgkmcnt(0)
	global_store_dwordx4 v[0:1], v[4:7], off sc1
	s_waitcnt lgkmcnt(0)
	s_andn2_b64 vcc, exec, s[26:27]
	s_cbranch_vccz .LBB0_1262
	s_branch .LBB0_1286

.LBB0_1262:
	s_andn2_b64 vcc, exec, s[24:25]
	s_cbranch_vccnz .LBB0_1264
	s_ashr_i32 s3, s2, 31
	s_lshl_b64 s[24:25], s[2:3], 22
	s_add_u32 s3, s54, s24
	s_addc_u32 s21, s55, s25
	v_or_b32_e32 v0, s22, v74
	s_add_u32 s3, s3, s18
	v_mul_hi_i32_i24_e32 v1, s16, v0
	v_mul_i32_i24_e32 v0, s16, v0
	s_addc_u32 s23, s21, s19
	v_lshl_add_u64 v[0:1], v[0:1], 2, s[6:7]
	s_ashr_i32 s21, s20, 31
	v_lshl_add_u64 v[0:1], s[20:21], 2, v[0:1]
	v_mov_b32_e32 v73, v69
	v_lshl_add_u64 v[0:1], v[0:1], 0, v[72:73]
	s_lshl_b64 s[24:25], s[16:17], 2
	global_load_dwordx4 v[56:59], v[0:1], off nt
	v_lshl_add_u64 v[0:1], v[0:1], 0, s[24:25]
	global_load_dwordx4 v[60:63], v[0:1], off nt
	v_lshl_add_u64 v[0:1], v[0:1], 0, s[24:25]
	global_load_dwordx4 v[64:67], v[0:1], off nt
	v_lshl_add_u64 v[0:1], v[0:1], 0, s[24:25]
	global_load_dwordx4 v[52:55], v[0:1], off nt
	v_lshl_add_u64 v[0:1], v[0:1], 0, s[24:25]
	global_load_dwordx4 v[40:43], v[0:1], off nt
	v_lshl_add_u64 v[0:1], v[0:1], 0, s[24:25]
	global_load_dwordx4 v[44:47], v[0:1], off nt
	v_lshl_add_u64 v[0:1], v[0:1], 0, s[24:25]
	global_load_dwordx4 v[48:51], v[0:1], off nt
	v_lshl_add_u64 v[0:1], v[0:1], 0, s[24:25]
	global_load_dwordx4 v[36:39], v[0:1], off nt
	v_lshl_add_u64 v[0:1], v[0:1], 0, s[24:25]
	global_load_dwordx4 v[24:27], v[0:1], off nt
	v_lshl_add_u64 v[0:1], v[0:1], 0, s[24:25]
	global_load_dwordx4 v[28:31], v[0:1], off nt
	v_lshl_add_u64 v[0:1], v[0:1], 0, s[24:25]
	global_load_dwordx4 v[32:35], v[0:1], off nt
	v_lshl_add_u64 v[0:1], v[0:1], 0, s[24:25]
	global_load_dwordx4 v[20:23], v[0:1], off nt
	v_lshl_add_u64 v[0:1], v[0:1], 0, s[24:25]
	global_load_dwordx4 v[4:7], v[0:1], off nt
	v_lshl_add_u64 v[0:1], v[0:1], 0, s[24:25]
	global_load_dwordx4 v[12:15], v[0:1], off nt
	v_lshl_add_u64 v[0:1], v[0:1], 0, s[24:25]
	global_load_dwordx4 v[16:19], v[0:1], off nt
	v_lshl_add_u64 v[0:1], v[0:1], 0, s[24:25]
	global_load_dwordx4 v[0:3], v[0:1], off nt
	v_mov_b32_e32 v11, v69
	v_mov_b32_e32 v97, v69
	v_mov_b32_e32 v98, v69
	v_mov_b32_e32 v99, v69
	v_mov_b32_e32 v100, v69
	v_mov_b32_e32 v101, v69
	v_mov_b32_e32 v102, v69
	v_mov_b32_e32 v103, v69
	v_mov_b32_e32 v8, v69
	v_mov_b32_e32 v9, v69
	v_mov_b32_e32 v10, v69
	v_mov_b32_e32 v96, v69
	s_ashr_i32 s21, s22, 31
	s_add_u32 s24, s3, s22
	s_addc_u32 s25, s23, s21
	s_add_i32 s92, s92, 0x111c8
	s_cmpk_lt_u32 s92, 0xf97f
	s_waitcnt vmcnt(0)
	v_mul_f32_e32 v56, 0x42800000, v56
	v_mul_f32_e32 v57, 0x42800000, v57
	v_mul_f32_e32 v60, 0x42800000, v60
	v_med3_f32 v56, v56, s66, v90
	v_mul_f32_e32 v61, 0x42800000, v61
	v_med3_f32 v60, v60, s66, v90
	v_med3_f32 v57, v57, s66, v90
	v_med3_f32 v61, v61, s66, v90
	v_mul_f32_e32 v41, 0x42800000, v41
	v_med3_f32 v41, v41, s66, v90
	v_mul_f32_e32 v45, 0x42800000, v45
	v_med3_f32 v45, v45, s66, v90
	v_cvt_pk_fp8_f32 v97, v41, v45
	v_mul_f32_e32 v49, 0x42800000, v49
	v_mul_f32_e32 v40, 0x42800000, v40
	v_mul_f32_e32 v44, 0x42800000, v44
	v_mul_f32_e32 v24, 0x42800000, v24
	v_med3_f32 v40, v40, s66, v90
	v_mul_f32_e32 v28, 0x42800000, v28
	v_med3_f32 v44, v44, s66, v90
	v_med3_f32 v24, v24, s66, v90
	v_med3_f32 v28, v28, s66, v90
	v_cvt_pk_fp8_f32 v8, v56, v60
	v_cvt_pk_fp8_f32 v9, v40, v44
	v_mul_f32_e32 v4, 0x42800000, v4
	v_med3_f32 v4, v4, s66, v90
	v_mul_f32_e32 v12, 0x42800000, v12
	v_med3_f32 v12, v12, s66, v90
	v_cvt_pk_fp8_f32 v11, v4, v12
	v_mul_f32_e32 v16, 0x42800000, v16
	v_mul_f32_e32 v0, 0x42800000, v0
	v_med3_f32 v4, v16, s66, v90
	v_med3_f32 v0, v0, s66, v90
	v_cvt_pk_fp8_f32 v11, v4, v0 op_sel:[0,0,1]
	v_mul_f32_e32 v0, 0x42800000, v37
	v_med3_f32 v4, v49, s66, v90
	v_med3_f32 v0, v0, s66, v90
	v_cvt_pk_fp8_f32 v97, v4, v0 op_sel:[0,0,1]
	v_mul_f32_e32 v0, 0x42800000, v25
	v_mul_f32_e32 v4, 0x42800000, v29
	v_med3_f32 v0, v0, s66, v90
	v_med3_f32 v4, v4, s66, v90
	v_cvt_pk_fp8_f32 v98, v0, v4
	v_mul_f32_e32 v12, 0x42800000, v33
	v_mul_f32_e32 v0, 0x42800000, v21
	v_med3_f32 v4, v12, s66, v90
	v_med3_f32 v0, v0, s66, v90
	v_cvt_pk_fp8_f32 v98, v4, v0 op_sel:[0,0,1]
	v_mul_f32_e32 v0, 0x42800000, v5
	v_mul_f32_e32 v4, 0x42800000, v13
	v_med3_f32 v0, v0, s66, v90
	v_med3_f32 v4, v4, s66, v90
	v_cvt_pk_fp8_f32 v99, v0, v4
	v_mul_f32_e32 v5, 0x42800000, v17
	v_mul_f32_e32 v0, 0x42800000, v1
	v_med3_f32 v1, v5, s66, v90
	v_med3_f32 v0, v0, s66, v90
	v_cvt_pk_fp8_f32 v99, v1, v0 op_sel:[0,0,1]
	v_mul_f32_e32 v0, 0x42800000, v58
	v_mul_f32_e32 v1, 0x42800000, v62
	v_med3_f32 v0, v0, s66, v90
	v_med3_f32 v1, v1, s66, v90
	v_cvt_pk_fp8_f32 v100, v0, v1
	v_mul_f32_e32 v4, 0x42800000, v66
	v_mul_f32_e32 v0, 0x42800000, v54
	v_med3_f32 v1, v4, s66, v90
	v_med3_f32 v0, v0, s66, v90
	v_cvt_pk_fp8_f32 v100, v1, v0 op_sel:[0,0,1]
	v_mul_f32_e32 v0, 0x42800000, v42
	v_mul_f32_e32 v1, 0x42800000, v46
	v_med3_f32 v0, v0, s66, v90
	v_med3_f32 v1, v1, s66, v90
	v_cvt_pk_fp8_f32 v101, v0, v1
	v_mul_f32_e32 v4, 0x42800000, v50
	v_mul_f32_e32 v0, 0x42800000, v38
	v_med3_f32 v1, v4, s66, v90
	v_med3_f32 v0, v0, s66, v90
	v_cvt_pk_fp8_f32 v101, v1, v0 op_sel:[0,0,1]
	v_mul_f32_e32 v0, 0x42800000, v26
	v_mul_f32_e32 v1, 0x42800000, v30
	v_med3_f32 v0, v0, s66, v90
	v_med3_f32 v1, v1, s66, v90
	v_cvt_pk_fp8_f32 v102, v0, v1
	v_mul_f32_e32 v4, 0x42800000, v34
	v_mul_f32_e32 v0, 0x42800000, v22
	v_med3_f32 v1, v4, s66, v90
	v_med3_f32 v0, v0, s66, v90
	v_cvt_pk_fp8_f32 v102, v1, v0 op_sel:[0,0,1]
	v_mul_f32_e32 v0, 0x42800000, v6
	v_mul_f32_e32 v1, 0x42800000, v14
	v_med3_f32 v0, v0, s66, v90
	v_med3_f32 v1, v1, s66, v90
	v_cvt_pk_fp8_f32 v103, v0, v1
	v_mul_f32_e32 v4, 0x42800000, v18
	v_mul_f32_e32 v0, 0x42800000, v2
	v_med3_f32 v1, v4, s66, v90
	v_med3_f32 v0, v0, s66, v90
	v_cvt_pk_fp8_f32 v103, v1, v0 op_sel:[0,0,1]
	v_mul_f32_e32 v0, 0x42800000, v59
	v_mul_f32_e32 v1, 0x42800000, v63
	v_med3_f32 v0, v0, s66, v90
	v_med3_f32 v1, v1, s66, v90
	v_mov_b32_e32 v4, v69
	v_cvt_pk_fp8_f32 v4, v0, v1
	v_mul_f32_e32 v2, 0x42800000, v67
	v_mul_f32_e32 v0, 0x42800000, v55
	v_med3_f32 v1, v2, s66, v90
	v_med3_f32 v0, v0, s66, v90
	v_cvt_pk_fp8_f32 v4, v1, v0 op_sel:[0,0,1]
	v_mul_f32_e32 v0, 0x42800000, v43
	v_mul_f32_e32 v1, 0x42800000, v47
	v_med3_f32 v0, v0, s66, v90
	v_med3_f32 v1, v1, s66, v90
	v_mov_b32_e32 v5, v69
	v_cvt_pk_fp8_f32 v5, v0, v1
	v_mul_f32_e32 v2, 0x42800000, v51
	v_mul_f32_e32 v0, 0x42800000, v39
	v_med3_f32 v1, v2, s66, v90
	v_med3_f32 v0, v0, s66, v90
	v_cvt_pk_fp8_f32 v5, v1, v0 op_sel:[0,0,1]
	v_mul_f32_e32 v0, 0x42800000, v27
	v_mul_f32_e32 v1, 0x42800000, v31
	v_med3_f32 v0, v0, s66, v90
	v_med3_f32 v1, v1, s66, v90
	v_mov_b32_e32 v6, v69
	v_cvt_pk_fp8_f32 v6, v0, v1
	v_mul_f32_e32 v2, 0x42800000, v35
	v_mul_f32_e32 v0, 0x42800000, v23
	v_cvt_pk_fp8_f32 v10, v24, v28
	v_med3_f32 v1, v2, s66, v90
	v_med3_f32 v0, v0, s66, v90
	v_cvt_pk_fp8_f32 v96, v57, v61
	v_cvt_pk_fp8_f32 v6, v1, v0 op_sel:[0,0,1]
	v_mul_f32_e32 v0, 0x42800000, v7
	v_mul_f32_e32 v1, 0x42800000, v15
	v_mul_f32_e32 v64, 0x42800000, v64
	v_mul_f32_e32 v52, 0x42800000, v52
	v_mul_f32_e32 v48, 0x42800000, v48
	v_mul_f32_e32 v36, 0x42800000, v36
	v_mul_f32_e32 v32, 0x42800000, v32
	v_mul_f32_e32 v20, 0x42800000, v20
	v_med3_f32 v0, v0, s66, v90
	v_med3_f32 v1, v1, s66, v90
	v_mov_b32_e32 v7, v69
	v_mul_f32_e32 v65, 0x42800000, v65
	v_med3_f32 v64, v64, s66, v90
	v_mul_f32_e32 v53, 0x42800000, v53
	v_med3_f32 v52, v52, s66, v90
	v_med3_f32 v48, v48, s66, v90
	v_med3_f32 v36, v36, s66, v90
	v_med3_f32 v32, v32, s66, v90
	v_med3_f32 v20, v20, s66, v90
	v_cvt_pk_fp8_f32 v7, v0, v1
	v_med3_f32 v56, v65, s66, v90
	v_med3_f32 v53, v53, s66, v90
	v_cvt_pk_fp8_f32 v8, v64, v52 op_sel:[0,0,1]
	v_cvt_pk_fp8_f32 v9, v48, v36 op_sel:[0,0,1]
	v_cvt_pk_fp8_f32 v10, v32, v20 op_sel:[0,0,1]
	v_cvt_pk_fp8_f32 v96, v56, v53 op_sel:[0,0,1]
	v_mul_f32_e32 v2, 0x42800000, v19
	v_mul_f32_e32 v0, 0x42800000, v3
	v_med3_f32 v1, v2, s66, v90
	v_med3_f32 v0, v0, s66, v90
	v_cvt_pk_fp8_f32 v7, v1, v0 op_sel:[0,0,1]
	ds_write_b128 v87, v[8:11] offset:40960
	ds_write_b128 v87, v[96:99] offset:41040
	ds_write_b128 v87, v[100:103] offset:41120
	ds_write_b128 v87, v[4:7] offset:41200
	s_waitcnt lgkmcnt(0)
	ds_read_b128 v[0:3], v88 offset:40960
	v_or_b32_e32 v4, s13, v75
	v_ashrrev_i32_e32 v5, 31, v4
	v_lshl_add_u64 v[8:9], s[24:25], 0, v[70:71]
	v_lshlrev_b64 v[4:5], 11, v[4:5]
	v_lshl_add_u64 v[10:11], v[8:9], 0, v[4:5]
	ds_read_b128 v[4:7], v88 offset:42240
	s_waitcnt lgkmcnt(0)
	global_store_dwordx4 v[10:11], v[0:3], off sc1
	s_cselect_b64 s[24:25], -1, 0
	s_nop 0
	v_or_b32_e32 v0, s13, v76
	v_ashrrev_i32_e32 v1, 31, v0
	v_lshlrev_b64 v[0:1], 11, v[0:1]
	v_lshl_add_u64 v[0:1], v[8:9], 0, v[0:1]
	global_store_dwordx4 v[0:1], v[4:7], off sc1
	ds_read_b128 v[0:3], v88 offset:43520
	s_nop 0
	v_or_b32_e32 v4, s13, v77
	v_ashrrev_i32_e32 v5, 31, v4
	v_lshlrev_b64 v[4:5], 11, v[4:5]
	v_lshl_add_u64 v[10:11], v[8:9], 0, v[4:5]
	ds_read_b128 v[4:7], v88 offset:44800
	s_waitcnt lgkmcnt(1)
	global_store_dwordx4 v[10:11], v[0:3], off sc1
	s_nop 1
	v_or_b32_e32 v0, s13, v78
	v_ashrrev_i32_e32 v1, 31, v0
	v_lshlrev_b64 v[0:1], 11, v[0:1]
	v_lshl_add_u64 v[0:1], v[8:9], 0, v[0:1]
	s_waitcnt lgkmcnt(0)
	global_store_dwordx4 v[0:1], v[4:7], off sc1
	s_waitcnt lgkmcnt(0)
	s_andn2_b64 vcc, exec, s[24:25]
	s_cbranch_vccz .LBB0_1265
	s_branch .LBB0_1286

.LBB0_1269:
	s_lshl_b64 s[18:19], s[18:19], 1
	s_add_u32 s3, s10, s18
	s_addc_u32 s18, s11, s19
	s_ashr_i32 s23, s22, 31
	s_lshl_b64 s[10:11], s[22:23], 1
	s_waitcnt lgkmcnt(0)
	s_add_u32 s10, s3, s10
	s_addc_u32 s11, s18, s11
	v_or_b32_e32 v0, s13, v79
	v_lshl_add_u64 v[4:5], s[10:11], 0, v[68:69]
	s_mov_b64 s[10:11], -1
	s_and_b64 vcc, exec, s[24:25]
	v_mul_hi_i32_i24_e32 v7, s12, v0
	v_mul_i32_i24_e32 v6, s12, v0
	s_cbranch_vccz .LBB0_1271
	v_lshl_add_u64 v[0:1], v[6:7], 1, v[4:5]
	global_store_dwordx4 v[0:1], v[92:95], off sc1
	s_mov_b64 s[10:11], 0
.LBB0_1271:
	v_mov_b32_e32 v0, 0
	s_andn2_b64 vcc, exec, s[10:11]
	v_mov_b32_e32 v1, 0
	v_mov_b32_e32 v2, 0
	v_mov_b32_e32 v3, 0
	s_cbranch_vccnz .LBB0_1273
	ds_read_b128 v[8:11], v91 offset:40960
	ds_read_b128 v[0:3], v91 offset:42112
	v_lshl_add_u64 v[6:7], v[6:7], 1, v[4:5]
	s_waitcnt lgkmcnt(0)
	global_store_dwordx4 v[6:7], v[8:11], off sc1
.LBB0_1273:
	v_or_b32_e32 v6, s13, v80
	v_mul_hi_i32_i24_e32 v7, s12, v6
	v_mul_i32_i24_e32 v6, s12, v6
	v_lshl_add_u64 v[6:7], v[6:7], 1, v[4:5]
	global_store_dwordx4 v[6:7], v[0:3], off sc1
	s_mov_b64 s[10:11], -1
	s_and_b64 vcc, exec, s[24:25]
	v_or_b32_e32 v0, s13, v81
	v_mul_hi_i32_i24_e32 v7, s12, v0
	v_mul_i32_i24_e32 v6, s12, v0
	s_cbranch_vccz .LBB0_1275
	v_lshl_add_u64 v[0:1], v[6:7], 1, v[4:5]
	global_store_dwordx4 v[0:1], v[92:95], off sc1
	s_mov_b64 s[10:11], 0
.LBB0_1275:
	v_mov_b32_e32 v0, 0
	s_andn2_b64 vcc, exec, s[10:11]
	v_mov_b32_e32 v1, 0
	v_mov_b32_e32 v2, 0
	v_mov_b32_e32 v3, 0
	s_cbranch_vccnz .LBB0_1277
	ds_read_b128 v[8:11], v91 offset:43264
	ds_read_b128 v[0:3], v91 offset:44416
	v_lshl_add_u64 v[6:7], v[6:7], 1, v[4:5]
	s_waitcnt lgkmcnt(0)
	global_store_dwordx4 v[6:7], v[8:11], off sc1
.LBB0_1277:
	v_or_b32_e32 v6, s13, v82
	v_mul_hi_i32_i24_e32 v7, s12, v6
	v_mul_i32_i24_e32 v6, s12, v6
	v_lshl_add_u64 v[6:7], v[6:7], 1, v[4:5]
	global_store_dwordx4 v[6:7], v[0:3], off sc1
	s_mov_b64 s[10:11], -1
	s_and_b64 vcc, exec, s[24:25]
	v_or_b32_e32 v0, s13, v83
	v_mul_hi_i32_i24_e32 v7, s12, v0
	v_mul_i32_i24_e32 v6, s12, v0
	s_cbranch_vccz .LBB0_1279
	v_lshl_add_u64 v[0:1], v[6:7], 1, v[4:5]
	global_store_dwordx4 v[0:1], v[92:95], off sc1
	s_mov_b64 s[10:11], 0
.LBB0_1279:
	v_mov_b32_e32 v0, 0
	s_andn2_b64 vcc, exec, s[10:11]
	v_mov_b32_e32 v1, 0
	v_mov_b32_e32 v2, 0
	v_mov_b32_e32 v3, 0
	s_cbranch_vccnz .LBB0_1281
	ds_read_b128 v[8:11], v91 offset:45568
	ds_read_b128 v[0:3], v91 offset:46720
	v_lshl_add_u64 v[6:7], v[6:7], 1, v[4:5]
	s_waitcnt lgkmcnt(0)
	global_store_dwordx4 v[6:7], v[8:11], off sc1
.LBB0_1281:
	v_or_b32_e32 v6, s13, v84
	v_mul_hi_i32_i24_e32 v7, s12, v6
	v_mul_i32_i24_e32 v6, s12, v6
	v_lshl_add_u64 v[6:7], v[6:7], 1, v[4:5]
	global_store_dwordx4 v[6:7], v[0:3], off sc1
	s_mov_b64 s[10:11], -1
	s_and_b64 vcc, exec, s[24:25]
	v_or_b32_e32 v0, s13, v85
	v_mul_hi_i32_i24_e32 v7, s12, v0
	v_mul_i32_i24_e32 v6, s12, v0
	s_cbranch_vccz .LBB0_1283
	v_lshl_add_u64 v[0:1], v[6:7], 1, v[4:5]
	global_store_dwordx4 v[0:1], v[92:95], off sc1
	s_mov_b64 s[10:11], 0
.LBB0_1283:
	v_mov_b32_e32 v0, 0
	s_andn2_b64 vcc, exec, s[10:11]
	v_mov_b32_e32 v1, 0
	v_mov_b32_e32 v2, 0
	v_mov_b32_e32 v3, 0
	s_cbranch_vccnz .LBB0_1285
	ds_read_b128 v[8:11], v91 offset:47872
	ds_read_b128 v[0:3], v91 offset:49024
	v_lshl_add_u64 v[6:7], v[6:7], 1, v[4:5]
	s_waitcnt lgkmcnt(0)
	global_store_dwordx4 v[6:7], v[8:11], off sc1
.LBB0_1285:
	v_or_b32_e32 v6, s13, v86
	v_mul_hi_i32_i24_e32 v7, s12, v6
	v_mul_i32_i24_e32 v6, s12, v6
	v_lshl_add_u64 v[4:5], v[6:7], 1, v[4:5]
	global_store_dwordx4 v[4:5], v[0:3], off sc1
	s_waitcnt lgkmcnt(0)

.LBB0_1347:
	ds_read_b128 v[12:15], v156
	ds_read_b128 v[16:19], v156 offset:1024
	ds_read_b128 v[28:31], v156 offset:2048
	ds_read_b128 v[32:35], v156 offset:3072
	s_add_u32 s22, s43, s21
	s_addc_u32 s23, s44, 0
	s_and_b64 s[24:25], s[2:3], exec
	s_cselect_b32 s29, s23, s31
	s_cselect_b32 s28, s22, s30
	s_add_u32 s24, s45, s67
	s_addc_u32 s25, s46, 0
	s_and_b64 s[2:3], s[2:3], exec
	s_cselect_b32 s3, s25, s39
	s_cselect_b32 s2, s24, s38
	s_add_u32 s70, s30, 0x10080
	s_addc_u32 s71, s31, 0
	s_mov_b32 m0, s57
	v_lshl_add_u64 v[44:45], s[70:71], 0, v[134:135]
	ds_read_b128 v[4:7], v157
	ds_read_b128 v[8:11], v157 offset:1024
	ds_read_b128 v[20:23], v157 offset:2048
	ds_read_b128 v[24:27], v157 offset:3072
	ds_read_b128 v[36:39], v157 offset:4096
	ds_read_b128 v[40:43], v157 offset:5120
	ds_read_b128 v[52:55], v157 offset:6144
	ds_read_b128 v[56:59], v157 offset:7168
	global_load_lds_dwordx4 v[44:45], off
	v_lshl_add_u64 v[44:45], s[70:71], 0, v[138:139]
	s_mov_b32 m0, s58
	s_nop 0
	global_load_lds_dwordx4 v[44:45], off
	s_waitcnt lgkmcnt(8)
	s_barrier
	s_waitcnt lgkmcnt(0)
	s_setprio 1
	v_mov_b64_e32 v[110:111], v[2:3]
	v_mov_b64_e32 v[114:115], v[2:3]
	v_mov_b64_e32 v[106:107], v[2:3]
	v_mov_b64_e32 v[102:103], v[2:3]
	v_mov_b64_e32 v[82:83], v[2:3]
	v_mov_b64_e32 v[78:79], v[2:3]
	v_mov_b64_e32 v[50:51], v[2:3]
	v_mov_b64_e32 v[46:47], v[2:3]
	v_mov_b64_e32 v[108:109], v[0:1]
	v_mov_b64_e32 v[112:113], v[0:1]
	v_mov_b64_e32 v[104:105], v[0:1]
	v_mov_b64_e32 v[100:101], v[0:1]
	v_mov_b64_e32 v[80:81], v[0:1]
	v_mov_b64_e32 v[76:77], v[0:1]
	v_mov_b64_e32 v[48:49], v[0:1]
	v_mov_b64_e32 v[44:45], v[0:1]
	s_waitcnt lgkmcnt(0)
	v_mfma_scale_f32_16x16x128_f8f6f4 v[108:111], v[12:19], v[4:11], v[108:111], v153, v153 op_sel_hi:[0,0,0]
	v_mfma_scale_f32_16x16x128_f8f6f4 v[112:115], v[28:35], v[4:11], v[112:115], v153, v153 op_sel_hi:[0,0,0]
	v_mfma_scale_f32_16x16x128_f8f6f4 v[104:107], v[12:19], v[20:27], v[104:107], v153, v153 op_sel_hi:[0,0,0]
	v_mfma_scale_f32_16x16x128_f8f6f4 v[100:103], v[28:35], v[20:27], v[100:103], v153, v153 op_sel_hi:[0,0,0]
	v_mfma_scale_f32_16x16x128_f8f6f4 v[80:83], v[12:19], v[36:43], v[80:83], v153, v153 op_sel_hi:[0,0,0]
	v_mfma_scale_f32_16x16x128_f8f6f4 v[76:79], v[28:35], v[36:43], v[76:79], v153, v153 op_sel_hi:[0,0,0]
	v_mfma_scale_f32_16x16x128_f8f6f4 v[48:51], v[12:19], v[52:59], v[48:51], v153, v153 op_sel_hi:[0,0,0]
	v_mfma_scale_f32_16x16x128_f8f6f4 v[44:47], v[28:35], v[52:59], v[44:47], v153, v153 op_sel_hi:[0,0,0]
	s_setprio 0
	s_barrier
	v_lshl_add_u64 v[144:145], s[38:39], 0, v[132:133]
	s_add_i32 s71, s56, s47
	v_lshl_add_u64 v[60:61], v[144:145], 0, s[6:7]
	s_mov_b32 m0, s71
	v_lshl_add_u64 v[146:147], s[38:39], 0, v[136:137]
	s_add_i32 s69, s71, 0x2000
	ds_read_b128 v[160:163], v158
	ds_read_b128 v[164:167], v158 offset:1024
	ds_read_b128 v[168:171], v158 offset:2048
	ds_read_b128 v[172:175], v158 offset:3072
	global_load_lds_dwordx4 v[60:61], off
	v_lshl_add_u64 v[60:61], v[146:147], 0, s[6:7]
	s_mov_b32 m0, s69
	s_nop 0
	global_load_lds_dwordx4 v[60:61], off
	s_barrier
	s_waitcnt lgkmcnt(0)
	s_setprio 1
	v_mov_b64_e32 v[126:127], v[2:3]
	v_mov_b64_e32 v[130:131], v[2:3]
	v_mov_b64_e32 v[122:123], v[2:3]
	v_mov_b64_e32 v[118:119], v[2:3]
	v_mov_b64_e32 v[98:99], v[2:3]
	v_mov_b64_e32 v[94:95], v[2:3]
	v_mov_b64_e32 v[66:67], v[2:3]
	v_mov_b64_e32 v[62:63], v[2:3]
	v_mov_b64_e32 v[124:125], v[0:1]
	v_mov_b64_e32 v[128:129], v[0:1]
	v_mov_b64_e32 v[120:121], v[0:1]
	v_mov_b64_e32 v[116:117], v[0:1]
	v_mov_b64_e32 v[96:97], v[0:1]
	v_mov_b64_e32 v[92:93], v[0:1]
	v_mov_b64_e32 v[64:65], v[0:1]
	v_mov_b64_e32 v[60:61], v[0:1]
	s_waitcnt lgkmcnt(0)
	v_mfma_scale_f32_16x16x128_f8f6f4 v[124:127], v[160:167], v[4:11], v[124:127], v153, v153 op_sel_hi:[0,0,0]
	v_mfma_scale_f32_16x16x128_f8f6f4 v[128:131], v[168:175], v[4:11], v[128:131], v153, v153 op_sel_hi:[0,0,0]
	v_mfma_scale_f32_16x16x128_f8f6f4 v[120:123], v[160:167], v[20:27], v[120:123], v153, v153 op_sel_hi:[0,0,0]
	v_mfma_scale_f32_16x16x128_f8f6f4 v[116:119], v[168:175], v[20:27], v[116:119], v153, v153 op_sel_hi:[0,0,0]
	v_mfma_scale_f32_16x16x128_f8f6f4 v[96:99], v[160:167], v[36:43], v[96:99], v153, v153 op_sel_hi:[0,0,0]
	v_mfma_scale_f32_16x16x128_f8f6f4 v[92:95], v[168:175], v[36:43], v[92:95], v153, v153 op_sel_hi:[0,0,0]
	v_mfma_scale_f32_16x16x128_f8f6f4 v[64:67], v[160:167], v[52:59], v[64:67], v153, v153 op_sel_hi:[0,0,0]
	v_mfma_scale_f32_16x16x128_f8f6f4 v[60:63], v[168:175], v[52:59], v[60:63], v153, v153 op_sel_hi:[0,0,0]
	s_setprio 0
	v_lshl_add_u64 v[148:149], s[30:31], 0, v[134:135]
	s_mov_b32 m0, s27
	v_lshl_add_u64 v[4:5], v[148:149], 0, s[6:7]
	v_lshl_add_u64 v[150:151], s[30:31], 0, v[138:139]
	s_barrier
	ds_read_b128 v[52:55], v157 offset:16384
	ds_read_b128 v[56:59], v157 offset:17408
	ds_read_b128 v[176:179], v157 offset:18432
	ds_read_b128 v[180:183], v157 offset:19456
	ds_read_b128 v[184:187], v157 offset:20480
	ds_read_b128 v[188:191], v157 offset:21504
	ds_read_b128 v[192:195], v157 offset:22528
	ds_read_b128 v[196:199], v157 offset:23552
	global_load_lds_dwordx4 v[4:5], off
	v_lshl_add_u64 v[4:5], v[150:151], 0, s[6:7]
	s_mov_b32 m0, s48
	s_nop 0
	global_load_lds_dwordx4 v[4:5], off
	s_barrier
	s_waitcnt lgkmcnt(0)
	s_setprio 1
	v_mov_b64_e32 v[74:75], v[2:3]
	v_mov_b64_e32 v[70:71], v[2:3]
	v_mov_b64_e32 v[42:43], v[2:3]
	v_mov_b64_e32 v[38:39], v[2:3]
	v_mov_b64_e32 v[26:27], v[2:3]
	v_mov_b64_e32 v[22:23], v[2:3]
	v_mov_b64_e32 v[10:11], v[2:3]
	v_mov_b64_e32 v[6:7], v[2:3]
	v_mov_b64_e32 v[72:73], v[0:1]
	v_mov_b64_e32 v[68:69], v[0:1]
	v_mov_b64_e32 v[40:41], v[0:1]
	v_mov_b64_e32 v[36:37], v[0:1]
	v_mov_b64_e32 v[24:25], v[0:1]
	v_mov_b64_e32 v[20:21], v[0:1]
	v_mov_b64_e32 v[8:9], v[0:1]
	v_mov_b64_e32 v[4:5], v[0:1]
	s_waitcnt lgkmcnt(0)
	v_mfma_scale_f32_16x16x128_f8f6f4 v[72:75], v[12:19], v[52:59], v[72:75], v153, v153 op_sel_hi:[0,0,0]
	v_mfma_scale_f32_16x16x128_f8f6f4 v[68:71], v[28:35], v[52:59], v[68:71], v153, v153 op_sel_hi:[0,0,0]
	v_mfma_scale_f32_16x16x128_f8f6f4 v[40:43], v[12:19], v[176:183], v[40:43], v153, v153 op_sel_hi:[0,0,0]
	v_mfma_scale_f32_16x16x128_f8f6f4 v[36:39], v[28:35], v[176:183], v[36:39], v153, v153 op_sel_hi:[0,0,0]
	v_mfma_scale_f32_16x16x128_f8f6f4 v[24:27], v[12:19], v[184:191], v[24:27], v153, v153 op_sel_hi:[0,0,0]
	v_mfma_scale_f32_16x16x128_f8f6f4 v[20:23], v[28:35], v[184:191], v[20:23], v153, v153 op_sel_hi:[0,0,0]
	v_mfma_scale_f32_16x16x128_f8f6f4 v[8:11], v[12:19], v[192:199], v[8:11], v153, v153 op_sel_hi:[0,0,0]
	v_mfma_scale_f32_16x16x128_f8f6f4 v[4:7], v[28:35], v[192:199], v[4:7], v153, v153 op_sel_hi:[0,0,0]
	s_setprio 0
	s_barrier
	s_add_u32 s74, s38, 0x10100
	s_addc_u32 s75, s39, 0
	s_add_i32 s72, s59, s47
	v_lshl_add_u64 v[12:13], s[74:75], 0, v[132:133]
	s_mov_b32 m0, s72
	s_add_i32 s70, s72, 0x2000
	global_load_lds_dwordx4 v[12:13], off
	v_lshl_add_u64 v[12:13], s[74:75], 0, v[136:137]
	s_mov_b32 m0, s70
	s_nop 0
	global_load_lds_dwordx4 v[12:13], off
	s_waitcnt vmcnt(6)
	s_barrier
	s_setprio 1
	v_mov_b64_e32 v[90:91], v[2:3]
	v_mov_b64_e32 v[86:87], v[2:3]
	v_mov_b64_e32 v[88:89], v[0:1]
	v_mov_b64_e32 v[84:85], v[0:1]
	v_mfma_scale_f32_16x16x128_f8f6f4 v[88:91], v[160:167], v[52:59], v[88:91], v153, v153 op_sel_hi:[0,0,0]
	v_mfma_scale_f32_16x16x128_f8f6f4 v[84:87], v[168:175], v[52:59], v[84:87], v153, v153 op_sel_hi:[0,0,0]
	v_mov_b64_e32 v[58:59], v[2:3]
	v_mov_b64_e32 v[54:55], v[2:3]
	v_mov_b64_e32 v[34:35], v[2:3]
	v_mov_b64_e32 v[30:31], v[2:3]
	v_mov_b64_e32 v[18:19], v[2:3]
	v_mov_b64_e32 v[14:15], v[2:3]
	v_mov_b64_e32 v[56:57], v[0:1]
	v_mov_b64_e32 v[52:53], v[0:1]
	v_mov_b64_e32 v[32:33], v[0:1]
	v_mov_b64_e32 v[28:29], v[0:1]
	v_mov_b64_e32 v[16:17], v[0:1]
	v_mov_b64_e32 v[12:13], v[0:1]
	v_mfma_scale_f32_16x16x128_f8f6f4 v[56:59], v[160:167], v[176:183], v[56:59], v153, v153 op_sel_hi:[0,0,0]
	v_mfma_scale_f32_16x16x128_f8f6f4 v[52:55], v[168:175], v[176:183], v[52:55], v153, v153 op_sel_hi:[0,0,0]
	v_mfma_scale_f32_16x16x128_f8f6f4 v[32:35], v[160:167], v[184:191], v[32:35], v153, v153 op_sel_hi:[0,0,0]
	v_mfma_scale_f32_16x16x128_f8f6f4 v[28:31], v[168:175], v[184:191], v[28:31], v153, v153 op_sel_hi:[0,0,0]
	v_mfma_scale_f32_16x16x128_f8f6f4 v[16:19], v[160:167], v[192:199], v[16:19], v153, v153 op_sel_hi:[0,0,0]
	v_mfma_scale_f32_16x16x128_f8f6f4 v[12:15], v[168:175], v[192:199], v[12:15], v153, v153 op_sel_hi:[0,0,0]
	s_setprio 0
	s_add_i32 s73, 0, 0x18000
	v_add_u32_e32 v159, s73, v155
	s_barrier
	ds_read_b128 v[162:165], v159
	ds_read_b128 v[166:169], v159 offset:1024
	ds_read_b128 v[170:173], v159 offset:2048
	ds_read_b128 v[174:177], v159 offset:3072
	s_add_u32 s74, s30, 0x10100
	s_addc_u32 s75, s31, 0
	s_mov_b32 m0, s49
	v_lshl_add_u64 v[160:161], s[74:75], 0, v[134:135]
	ds_read_b128 v[178:181], v157 offset:32768
	ds_read_b128 v[182:185], v157 offset:33792
	ds_read_b128 v[186:189], v157 offset:34816
	ds_read_b128 v[190:193], v157 offset:35840
	ds_read_b128 v[194:197], v157 offset:36864
	ds_read_b128 v[198:201], v157 offset:37888
	ds_read_b128 v[202:205], v157 offset:38912
	ds_read_b128 v[206:209], v157 offset:39936
	global_load_lds_dwordx4 v[160:161], off
	v_lshl_add_u64 v[160:161], s[74:75], 0, v[138:139]
	s_mov_b32 m0, s50
	s_nop 0
	global_load_lds_dwordx4 v[160:161], off
	s_waitcnt lgkmcnt(8)
	s_barrier
	s_waitcnt lgkmcnt(0)
	s_setprio 1
	s_waitcnt lgkmcnt(0)
	v_mfma_scale_f32_16x16x128_f8f6f4 v[108:111], v[162:169], v[178:185], v[108:111], v153, v153 op_sel_hi:[0,0,0]
	v_mfma_scale_f32_16x16x128_f8f6f4 v[112:115], v[170:177], v[178:185], v[112:115], v153, v153 op_sel_hi:[0,0,0]
	v_mfma_scale_f32_16x16x128_f8f6f4 v[104:107], v[162:169], v[186:193], v[104:107], v153, v153 op_sel_hi:[0,0,0]
	v_mfma_scale_f32_16x16x128_f8f6f4 v[100:103], v[170:177], v[186:193], v[100:103], v153, v153 op_sel_hi:[0,0,0]
	v_mfma_scale_f32_16x16x128_f8f6f4 v[80:83], v[162:169], v[194:201], v[80:83], v153, v153 op_sel_hi:[0,0,0]
	v_mfma_scale_f32_16x16x128_f8f6f4 v[76:79], v[170:177], v[194:201], v[76:79], v153, v153 op_sel_hi:[0,0,0]
	v_mfma_scale_f32_16x16x128_f8f6f4 v[48:51], v[162:169], v[202:209], v[48:51], v153, v153 op_sel_hi:[0,0,0]
	v_mfma_scale_f32_16x16x128_f8f6f4 v[44:47], v[170:177], v[202:209], v[44:47], v153, v153 op_sel_hi:[0,0,0]
	s_setprio 0
	s_barrier
	s_add_i32 s75, 0, 0x1c000
	s_add_i32 s74, s73, s47
	v_add_u32_e32 v160, s75, v155
	v_lshl_add_u64 v[144:145], v[144:145], 0, s[16:17]
	s_mov_b32 m0, s74
	s_add_i32 s73, s74, 0x2000
	ds_read_b128 v[210:213], v160
	ds_read_b128 v[214:217], v160 offset:1024
	ds_read_b128 v[224:227], v160 offset:2048
	ds_read_b128 v[228:231], v160 offset:3072
	global_load_lds_dwordx4 v[144:145], off
	v_lshl_add_u64 v[144:145], v[146:147], 0, s[16:17]
	s_mov_b32 m0, s73
	s_nop 0
	global_load_lds_dwordx4 v[144:145], off
	s_barrier
	s_waitcnt lgkmcnt(0)
	s_setprio 1
	s_waitcnt lgkmcnt(0)
	v_mfma_scale_f32_16x16x128_f8f6f4 v[124:127], v[210:217], v[178:185], v[124:127], v153, v153 op_sel_hi:[0,0,0]
	v_mfma_scale_f32_16x16x128_f8f6f4 v[128:131], v[224:231], v[178:185], v[128:131], v153, v153 op_sel_hi:[0,0,0]
	v_mfma_scale_f32_16x16x128_f8f6f4 v[120:123], v[210:217], v[186:193], v[120:123], v153, v153 op_sel_hi:[0,0,0]
	v_mfma_scale_f32_16x16x128_f8f6f4 v[116:119], v[224:231], v[186:193], v[116:119], v153, v153 op_sel_hi:[0,0,0]
	v_mfma_scale_f32_16x16x128_f8f6f4 v[96:99], v[210:217], v[194:201], v[96:99], v153, v153 op_sel_hi:[0,0,0]
	v_mfma_scale_f32_16x16x128_f8f6f4 v[92:95], v[224:231], v[194:201], v[92:95], v153, v153 op_sel_hi:[0,0,0]
	v_mfma_scale_f32_16x16x128_f8f6f4 v[64:67], v[210:217], v[202:209], v[64:67], v153, v153 op_sel_hi:[0,0,0]
	v_mfma_scale_f32_16x16x128_f8f6f4 v[60:63], v[224:231], v[202:209], v[60:63], v153, v153 op_sel_hi:[0,0,0]
	s_setprio 0
	s_mov_b32 m0, s52
	v_lshl_add_u64 v[144:145], v[148:149], 0, s[16:17]
	s_barrier
	ds_read_b128 v[178:181], v157 offset:49152
	ds_read_b128 v[182:185], v157 offset:50176
	ds_read_b128 v[186:189], v157 offset:51200
	ds_read_b128 v[190:193], v157 offset:52224
	ds_read_b128 v[194:197], v157 offset:53248
	ds_read_b128 v[198:201], v157 offset:54272
	ds_read_b128 v[202:205], v157 offset:55296
	ds_read_b128 v[206:209], v157 offset:56320
	global_load_lds_dwordx4 v[144:145], off
	v_lshl_add_u64 v[144:145], v[150:151], 0, s[16:17]
	s_mov_b32 m0, s53
	s_nop 0
	global_load_lds_dwordx4 v[144:145], off
	s_barrier
	s_waitcnt lgkmcnt(0)
	s_setprio 1
	s_waitcnt lgkmcnt(0)
	v_mfma_scale_f32_16x16x128_f8f6f4 v[72:75], v[162:169], v[178:185], v[72:75], v153, v153 op_sel_hi:[0,0,0]
	v_mfma_scale_f32_16x16x128_f8f6f4 v[68:71], v[170:177], v[178:185], v[68:71], v153, v153 op_sel_hi:[0,0,0]
	v_mfma_scale_f32_16x16x128_f8f6f4 v[40:43], v[162:169], v[186:193], v[40:43], v153, v153 op_sel_hi:[0,0,0]
	v_mfma_scale_f32_16x16x128_f8f6f4 v[36:39], v[170:177], v[186:193], v[36:39], v153, v153 op_sel_hi:[0,0,0]
	v_mfma_scale_f32_16x16x128_f8f6f4 v[24:27], v[162:169], v[194:201], v[24:27], v153, v153 op_sel_hi:[0,0,0]
	v_mfma_scale_f32_16x16x128_f8f6f4 v[20:23], v[170:177], v[194:201], v[20:23], v153, v153 op_sel_hi:[0,0,0]
	v_mfma_scale_f32_16x16x128_f8f6f4 v[8:11], v[162:169], v[202:209], v[8:11], v153, v153 op_sel_hi:[0,0,0]
	v_mfma_scale_f32_16x16x128_f8f6f4 v[4:7], v[170:177], v[202:209], v[4:7], v153, v153 op_sel_hi:[0,0,0]
	s_setprio 0
	s_barrier
	s_add_u32 s76, s38, 0x10180
	s_addc_u32 s77, s39, 0
	s_add_i32 s39, s75, s47
	v_lshl_add_u64 v[144:145], s[76:77], 0, v[132:133]
	s_mov_b32 m0, s39
	s_add_i32 s38, s39, 0x2000
	global_load_lds_dwordx4 v[144:145], off
	v_lshl_add_u64 v[144:145], s[76:77], 0, v[136:137]
	s_mov_b32 m0, s38
	s_nop 0
	global_load_lds_dwordx4 v[144:145], off
	s_waitcnt vmcnt(6)
	s_barrier
	s_setprio 1
	v_mfma_scale_f32_16x16x128_f8f6f4 v[88:91], v[210:217], v[178:185], v[88:91], v153, v153 op_sel_hi:[0,0,0]
	v_mfma_scale_f32_16x16x128_f8f6f4 v[84:87], v[224:231], v[178:185], v[84:87], v153, v153 op_sel_hi:[0,0,0]
	v_mfma_scale_f32_16x16x128_f8f6f4 v[56:59], v[210:217], v[186:193], v[56:59], v153, v153 op_sel_hi:[0,0,0]
	v_mfma_scale_f32_16x16x128_f8f6f4 v[52:55], v[224:231], v[186:193], v[52:55], v153, v153 op_sel_hi:[0,0,0]
	v_mfma_scale_f32_16x16x128_f8f6f4 v[32:35], v[210:217], v[194:201], v[32:35], v153, v153 op_sel_hi:[0,0,0]
	v_mfma_scale_f32_16x16x128_f8f6f4 v[28:31], v[224:231], v[194:201], v[28:31], v153, v153 op_sel_hi:[0,0,0]
	v_mfma_scale_f32_16x16x128_f8f6f4 v[16:19], v[210:217], v[202:209], v[16:19], v153, v153 op_sel_hi:[0,0,0]
	v_mfma_scale_f32_16x16x128_f8f6f4 v[12:15], v[224:231], v[202:209], v[12:15], v153, v153 op_sel_hi:[0,0,0]
	s_setprio 0
	s_barrier
	ds_read_b128 v[162:165], v156
	ds_read_b128 v[166:169], v156 offset:1024
	ds_read_b128 v[170:173], v156 offset:2048
	ds_read_b128 v[174:177], v156 offset:3072
	s_add_u32 s30, s30, 0x10180
	s_addc_u32 s31, s31, 0
	s_mov_b32 m0, s57
	v_lshl_add_u64 v[144:145], s[30:31], 0, v[134:135]
	ds_read_b128 v[178:181], v157
	ds_read_b128 v[182:185], v157 offset:1024
	ds_read_b128 v[186:189], v157 offset:2048
	ds_read_b128 v[190:193], v157 offset:3072
	ds_read_b128 v[194:197], v157 offset:4096
	ds_read_b128 v[198:201], v157 offset:5120
	ds_read_b128 v[202:205], v157 offset:6144
	ds_read_b128 v[206:209], v157 offset:7168
	global_load_lds_dwordx4 v[144:145], off
	v_lshl_add_u64 v[144:145], s[30:31], 0, v[138:139]
	s_mov_b32 m0, s58
	s_nop 0
	global_load_lds_dwordx4 v[144:145], off
	s_waitcnt lgkmcnt(8)
	s_barrier
	s_waitcnt lgkmcnt(0)
	s_setprio 1
	s_waitcnt lgkmcnt(0)
	v_mfma_scale_f32_16x16x128_f8f6f4 v[108:111], v[162:169], v[178:185], v[108:111], v153, v153 op_sel_hi:[0,0,0]
	v_mfma_scale_f32_16x16x128_f8f6f4 v[112:115], v[170:177], v[178:185], v[112:115], v153, v153 op_sel_hi:[0,0,0]
	v_mfma_scale_f32_16x16x128_f8f6f4 v[104:107], v[162:169], v[186:193], v[104:107], v153, v153 op_sel_hi:[0,0,0]
	v_mfma_scale_f32_16x16x128_f8f6f4 v[100:103], v[170:177], v[186:193], v[100:103], v153, v153 op_sel_hi:[0,0,0]
	v_mfma_scale_f32_16x16x128_f8f6f4 v[80:83], v[162:169], v[194:201], v[80:83], v153, v153 op_sel_hi:[0,0,0]
	v_mfma_scale_f32_16x16x128_f8f6f4 v[76:79], v[170:177], v[194:201], v[76:79], v153, v153 op_sel_hi:[0,0,0]
	v_mfma_scale_f32_16x16x128_f8f6f4 v[48:51], v[162:169], v[202:209], v[48:51], v153, v153 op_sel_hi:[0,0,0]
	v_mfma_scale_f32_16x16x128_f8f6f4 v[44:47], v[170:177], v[202:209], v[44:47], v153, v153 op_sel_hi:[0,0,0]
	s_setprio 0
	s_barrier
	s_mov_b32 m0, s71
	v_lshl_add_u64 v[144:145], s[2:3], 0, v[132:133]
	ds_read_b128 v[210:213], v158
	ds_read_b128 v[214:217], v158 offset:1024
	ds_read_b128 v[224:227], v158 offset:2048
	ds_read_b128 v[228:231], v158 offset:3072
	global_load_lds_dwordx4 v[144:145], off
	v_lshl_add_u64 v[146:147], s[2:3], 0, v[136:137]
	s_mov_b32 m0, s69
	s_nop 0
	global_load_lds_dwordx4 v[146:147], off
	s_barrier
	s_waitcnt lgkmcnt(0)
	s_setprio 1
	s_waitcnt lgkmcnt(0)
	v_mfma_scale_f32_16x16x128_f8f6f4 v[124:127], v[210:217], v[178:185], v[124:127], v153, v153 op_sel_hi:[0,0,0]
	v_mfma_scale_f32_16x16x128_f8f6f4 v[128:131], v[224:231], v[178:185], v[128:131], v153, v153 op_sel_hi:[0,0,0]
	v_mfma_scale_f32_16x16x128_f8f6f4 v[120:123], v[210:217], v[186:193], v[120:123], v153, v153 op_sel_hi:[0,0,0]
	v_mfma_scale_f32_16x16x128_f8f6f4 v[116:119], v[224:231], v[186:193], v[116:119], v153, v153 op_sel_hi:[0,0,0]
	v_mfma_scale_f32_16x16x128_f8f6f4 v[96:99], v[210:217], v[194:201], v[96:99], v153, v153 op_sel_hi:[0,0,0]
	v_mfma_scale_f32_16x16x128_f8f6f4 v[92:95], v[224:231], v[194:201], v[92:95], v153, v153 op_sel_hi:[0,0,0]
	v_mfma_scale_f32_16x16x128_f8f6f4 v[64:67], v[210:217], v[202:209], v[64:67], v153, v153 op_sel_hi:[0,0,0]
	v_mfma_scale_f32_16x16x128_f8f6f4 v[60:63], v[224:231], v[202:209], v[60:63], v153, v153 op_sel_hi:[0,0,0]
	s_setprio 0
	s_mov_b32 m0, s27
	v_lshl_add_u64 v[148:149], s[28:29], 0, v[134:135]
	s_barrier
	ds_read_b128 v[178:181], v157 offset:16384
	ds_read_b128 v[182:185], v157 offset:17408
	ds_read_b128 v[186:189], v157 offset:18432
	ds_read_b128 v[190:193], v157 offset:19456
	ds_read_b128 v[194:197], v157 offset:20480
	ds_read_b128 v[198:201], v157 offset:21504
	ds_read_b128 v[202:205], v157 offset:22528
	ds_read_b128 v[206:209], v157 offset:23552
	global_load_lds_dwordx4 v[148:149], off
	v_lshl_add_u64 v[150:151], s[28:29], 0, v[138:139]
	s_mov_b32 m0, s48
	s_nop 0
	global_load_lds_dwordx4 v[150:151], off
	s_barrier
	s_waitcnt lgkmcnt(0)
	s_setprio 1
	s_waitcnt lgkmcnt(0)
	v_mfma_scale_f32_16x16x128_f8f6f4 v[72:75], v[162:169], v[178:185], v[72:75], v153, v153 op_sel_hi:[0,0,0]
	v_mfma_scale_f32_16x16x128_f8f6f4 v[68:71], v[170:177], v[178:185], v[68:71], v153, v153 op_sel_hi:[0,0,0]
	v_mfma_scale_f32_16x16x128_f8f6f4 v[40:43], v[162:169], v[186:193], v[40:43], v153, v153 op_sel_hi:[0,0,0]
	v_mfma_scale_f32_16x16x128_f8f6f4 v[36:39], v[170:177], v[186:193], v[36:39], v153, v153 op_sel_hi:[0,0,0]
	v_mfma_scale_f32_16x16x128_f8f6f4 v[24:27], v[162:169], v[194:201], v[24:27], v153, v153 op_sel_hi:[0,0,0]
	v_mfma_scale_f32_16x16x128_f8f6f4 v[20:23], v[170:177], v[194:201], v[20:23], v153, v153 op_sel_hi:[0,0,0]
	v_mfma_scale_f32_16x16x128_f8f6f4 v[8:11], v[162:169], v[202:209], v[8:11], v153, v153 op_sel_hi:[0,0,0]
	v_mfma_scale_f32_16x16x128_f8f6f4 v[4:7], v[170:177], v[202:209], v[4:7], v153, v153 op_sel_hi:[0,0,0]
	s_setprio 0
	s_barrier
	s_add_u32 s30, s2, 0x10000
	s_addc_u32 s31, s3, 0
	s_mov_b32 m0, s72
	v_lshl_add_u64 v[162:163], s[30:31], 0, v[132:133]
	global_load_lds_dwordx4 v[162:163], off
	v_lshl_add_u64 v[162:163], s[30:31], 0, v[136:137]
	s_mov_b32 m0, s70
	s_nop 0
	global_load_lds_dwordx4 v[162:163], off
	s_waitcnt vmcnt(6)
	s_barrier
	s_setprio 1
	v_mfma_scale_f32_16x16x128_f8f6f4 v[88:91], v[210:217], v[178:185], v[88:91], v153, v153 op_sel_hi:[0,0,0]
	v_mfma_scale_f32_16x16x128_f8f6f4 v[84:87], v[224:231], v[178:185], v[84:87], v153, v153 op_sel_hi:[0,0,0]
	v_mfma_scale_f32_16x16x128_f8f6f4 v[56:59], v[210:217], v[186:193], v[56:59], v153, v153 op_sel_hi:[0,0,0]
	v_mfma_scale_f32_16x16x128_f8f6f4 v[52:55], v[224:231], v[186:193], v[52:55], v153, v153 op_sel_hi:[0,0,0]
	v_mfma_scale_f32_16x16x128_f8f6f4 v[32:35], v[210:217], v[194:201], v[32:35], v153, v153 op_sel_hi:[0,0,0]
	v_mfma_scale_f32_16x16x128_f8f6f4 v[28:31], v[224:231], v[194:201], v[28:31], v153, v153 op_sel_hi:[0,0,0]
	v_mfma_scale_f32_16x16x128_f8f6f4 v[16:19], v[210:217], v[202:209], v[16:19], v153, v153 op_sel_hi:[0,0,0]
	v_mfma_scale_f32_16x16x128_f8f6f4 v[12:15], v[224:231], v[202:209], v[12:15], v153, v153 op_sel_hi:[0,0,0]
	s_setprio 0
	s_barrier
	ds_read_b128 v[162:165], v159
	ds_read_b128 v[166:169], v159 offset:1024
	ds_read_b128 v[170:173], v159 offset:2048
	ds_read_b128 v[174:177], v159 offset:3072
	s_add_u32 s28, s28, 0x10000
	s_addc_u32 s29, s29, 0
	s_mov_b32 m0, s49
	v_lshl_add_u64 v[210:211], s[28:29], 0, v[134:135]
	ds_read_b128 v[178:181], v157 offset:32768
	ds_read_b128 v[182:185], v157 offset:33792
	ds_read_b128 v[186:189], v157 offset:34816
	ds_read_b128 v[190:193], v157 offset:35840
	ds_read_b128 v[194:197], v157 offset:36864
	ds_read_b128 v[198:201], v157 offset:37888
	ds_read_b128 v[202:205], v157 offset:38912
	ds_read_b128 v[206:209], v157 offset:39936
	global_load_lds_dwordx4 v[210:211], off
	v_lshl_add_u64 v[210:211], s[28:29], 0, v[138:139]
	s_mov_b32 m0, s50
	s_nop 0
	global_load_lds_dwordx4 v[210:211], off
	s_waitcnt lgkmcnt(8)
	s_barrier
	s_waitcnt lgkmcnt(0)
	s_setprio 1
	s_waitcnt lgkmcnt(0)
	v_mfma_scale_f32_16x16x128_f8f6f4 v[108:111], v[162:169], v[178:185], v[108:111], v153, v153 op_sel_hi:[0,0,0]
	v_mfma_scale_f32_16x16x128_f8f6f4 v[112:115], v[170:177], v[178:185], v[112:115], v153, v153 op_sel_hi:[0,0,0]
	v_mfma_scale_f32_16x16x128_f8f6f4 v[104:107], v[162:169], v[186:193], v[104:107], v153, v153 op_sel_hi:[0,0,0]
	v_mfma_scale_f32_16x16x128_f8f6f4 v[100:103], v[170:177], v[186:193], v[100:103], v153, v153 op_sel_hi:[0,0,0]
	v_mfma_scale_f32_16x16x128_f8f6f4 v[80:83], v[162:169], v[194:201], v[80:83], v153, v153 op_sel_hi:[0,0,0]
	v_mfma_scale_f32_16x16x128_f8f6f4 v[76:79], v[170:177], v[194:201], v[76:79], v153, v153 op_sel_hi:[0,0,0]
	v_mfma_scale_f32_16x16x128_f8f6f4 v[48:51], v[162:169], v[202:209], v[48:51], v153, v153 op_sel_hi:[0,0,0]
	v_mfma_scale_f32_16x16x128_f8f6f4 v[44:47], v[170:177], v[202:209], v[44:47], v153, v153 op_sel_hi:[0,0,0]
	s_setprio 0
	s_barrier
	s_mov_b32 m0, s74
	v_lshl_add_u64 v[144:145], v[144:145], 0, s[12:13]
	ds_read_b128 v[210:213], v160
	ds_read_b128 v[214:217], v160 offset:1024
	ds_read_b128 v[224:227], v160 offset:2048
	ds_read_b128 v[228:231], v160 offset:3072
	global_load_lds_dwordx4 v[144:145], off
	v_lshl_add_u64 v[144:145], v[146:147], 0, s[12:13]
	s_mov_b32 m0, s73
	s_nop 0
	global_load_lds_dwordx4 v[144:145], off
	s_barrier
	s_waitcnt lgkmcnt(0)
	s_setprio 1
	s_waitcnt lgkmcnt(0)
	v_mfma_scale_f32_16x16x128_f8f6f4 v[124:127], v[210:217], v[178:185], v[124:127], v153, v153 op_sel_hi:[0,0,0]
	v_mfma_scale_f32_16x16x128_f8f6f4 v[128:131], v[224:231], v[178:185], v[128:131], v153, v153 op_sel_hi:[0,0,0]
	v_mfma_scale_f32_16x16x128_f8f6f4 v[120:123], v[210:217], v[186:193], v[120:123], v153, v153 op_sel_hi:[0,0,0]
	v_mfma_scale_f32_16x16x128_f8f6f4 v[116:119], v[224:231], v[186:193], v[116:119], v153, v153 op_sel_hi:[0,0,0]
	v_mfma_scale_f32_16x16x128_f8f6f4 v[96:99], v[210:217], v[194:201], v[96:99], v153, v153 op_sel_hi:[0,0,0]
	v_mfma_scale_f32_16x16x128_f8f6f4 v[92:95], v[224:231], v[194:201], v[92:95], v153, v153 op_sel_hi:[0,0,0]
	v_mfma_scale_f32_16x16x128_f8f6f4 v[64:67], v[210:217], v[202:209], v[64:67], v153, v153 op_sel_hi:[0,0,0]
	v_mfma_scale_f32_16x16x128_f8f6f4 v[60:63], v[224:231], v[202:209], v[60:63], v153, v153 op_sel_hi:[0,0,0]
	s_setprio 0
	s_mov_b32 m0, s52
	v_lshl_add_u64 v[144:145], v[148:149], 0, s[12:13]
	s_barrier
	ds_read_b128 v[178:181], v157 offset:49152
	ds_read_b128 v[182:185], v157 offset:50176
	ds_read_b128 v[186:189], v157 offset:51200
	ds_read_b128 v[190:193], v157 offset:52224
	ds_read_b128 v[194:197], v157 offset:53248
	ds_read_b128 v[198:201], v157 offset:54272
	ds_read_b128 v[202:205], v157 offset:55296
	ds_read_b128 v[206:209], v157 offset:56320
	global_load_lds_dwordx4 v[144:145], off
	v_lshl_add_u64 v[144:145], v[150:151], 0, s[12:13]
	s_mov_b32 m0, s53
	s_nop 0
	global_load_lds_dwordx4 v[144:145], off
	s_barrier
	s_waitcnt lgkmcnt(0)
	s_setprio 1
	s_waitcnt lgkmcnt(0)
	v_mfma_scale_f32_16x16x128_f8f6f4 v[72:75], v[162:169], v[178:185], v[72:75], v153, v153 op_sel_hi:[0,0,0]
	v_mfma_scale_f32_16x16x128_f8f6f4 v[68:71], v[170:177], v[178:185], v[68:71], v153, v153 op_sel_hi:[0,0,0]
	v_mfma_scale_f32_16x16x128_f8f6f4 v[40:43], v[162:169], v[186:193], v[40:43], v153, v153 op_sel_hi:[0,0,0]
	v_mfma_scale_f32_16x16x128_f8f6f4 v[36:39], v[170:177], v[186:193], v[36:39], v153, v153 op_sel_hi:[0,0,0]
	v_mfma_scale_f32_16x16x128_f8f6f4 v[24:27], v[162:169], v[194:201], v[24:27], v153, v153 op_sel_hi:[0,0,0]
	v_mfma_scale_f32_16x16x128_f8f6f4 v[20:23], v[170:177], v[194:201], v[20:23], v153, v153 op_sel_hi:[0,0,0]
	v_mfma_scale_f32_16x16x128_f8f6f4 v[8:11], v[162:169], v[202:209], v[8:11], v153, v153 op_sel_hi:[0,0,0]
	v_mfma_scale_f32_16x16x128_f8f6f4 v[4:7], v[170:177], v[202:209], v[4:7], v153, v153 op_sel_hi:[0,0,0]
	s_setprio 0
	s_barrier
	s_add_u32 s2, s2, 0x10080
	s_addc_u32 s3, s3, 0
	s_mov_b32 m0, s39
	v_lshl_add_u64 v[144:145], s[2:3], 0, v[132:133]
	global_load_lds_dwordx4 v[144:145], off
	v_lshl_add_u64 v[144:145], s[2:3], 0, v[136:137]
	s_mov_b32 m0, s38
	s_nop 0
	global_load_lds_dwordx4 v[144:145], off
	s_waitcnt vmcnt(6)
	s_barrier
	s_setprio 1
	v_mfma_scale_f32_16x16x128_f8f6f4 v[88:91], v[210:217], v[178:185], v[88:91], v153, v153 op_sel_hi:[0,0,0]
	v_mfma_scale_f32_16x16x128_f8f6f4 v[84:87], v[224:231], v[178:185], v[84:87], v153, v153 op_sel_hi:[0,0,0]
	v_mfma_scale_f32_16x16x128_f8f6f4 v[56:59], v[210:217], v[186:193], v[56:59], v153, v153 op_sel_hi:[0,0,0]
	v_mfma_scale_f32_16x16x128_f8f6f4 v[52:55], v[224:231], v[186:193], v[52:55], v153, v153 op_sel_hi:[0,0,0]
	v_mfma_scale_f32_16x16x128_f8f6f4 v[32:35], v[210:217], v[194:201], v[32:35], v153, v153 op_sel_hi:[0,0,0]
	v_mfma_scale_f32_16x16x128_f8f6f4 v[28:31], v[224:231], v[194:201], v[28:31], v153, v153 op_sel_hi:[0,0,0]
	v_mfma_scale_f32_16x16x128_f8f6f4 v[16:19], v[210:217], v[202:209], v[16:19], v153, v153 op_sel_hi:[0,0,0]
	v_mfma_scale_f32_16x16x128_f8f6f4 v[12:15], v[224:231], v[202:209], v[12:15], v153, v153 op_sel_hi:[0,0,0]
	s_setprio 0
	v_lshl_add_u32 v144, s26, 8, v154
	v_ashrrev_i32_e32 v145, 31, v144
	v_lshlrev_b64 v[144:145], 12, v[144:145]
	s_lshl_b32 s2, s68, 8
	v_lshl_add_u64 v[144:145], s[10:11], 0, v[144:145]
	s_ashr_i32 s3, s2, 31
	v_lshl_add_u64 v[144:145], s[2:3], 1, v[144:145]
	v_lshl_add_u64 v[144:145], v[144:145], 0, s[4:5]
	v_pk_mul_f32 v[108:109], v[108:109], s[18:19] op_sel_hi:[1,0]
	s_barrier
	s_nop 7
	s_nop 7
	s_nop 7
	v_lshl_add_u64 v[144:145], v[144:145], 0, v[142:143]
	v_pk_mul_f32 v[110:111], v[110:111], s[18:19] op_sel_hi:[1,0]
	v_cvt_pk_bf16_f32 v108, v108, v109
	v_pk_mul_f32 v[114:115], v[114:115], s[18:19] op_sel_hi:[1,0]
	v_cvt_pk_bf16_f32 v109, v110, v111
	v_pk_mul_f32 v[112:113], v[112:113], s[18:19] op_sel_hi:[1,0]
	v_pk_mul_f32 v[104:105], v[104:105], s[18:19] op_sel_hi:[1,0]
	v_cvt_pk_bf16_f32 v110, v112, v113
	v_cvt_pk_bf16_f32 v111, v114, v115
	global_store_dwordx4 v[144:145], v[108:111], off sc1
	v_pk_mul_f32 v[112:113], v[130:131], s[18:19] op_sel_hi:[1,0]
	v_pk_mul_f32 v[114:115], v[128:129], s[18:19] op_sel_hi:[1,0]
	v_pk_mul_f32 v[108:109], v[124:125], s[18:19] op_sel_hi:[1,0]
	v_pk_mul_f32 v[110:111], v[126:127], s[18:19] op_sel_hi:[1,0]
	v_cvt_pk_bf16_f32 v108, v108, v109
	v_pk_mul_f32 v[106:107], v[106:107], s[18:19] op_sel_hi:[1,0]
	v_cvt_pk_bf16_f32 v109, v110, v111
	v_cvt_pk_bf16_f32 v110, v114, v115
	v_cvt_pk_bf16_f32 v111, v112, v113
	global_store_dwordx4 v[144:145], v[108:111], off offset:256 sc1
	v_pk_mul_f32 v[80:81], v[80:81], s[18:19] op_sel_hi:[1,0]
	v_pk_mul_f32 v[82:83], v[82:83], s[18:19] op_sel_hi:[1,0]
	v_pk_mul_f32 v[108:109], v[102:103], s[18:19] op_sel_hi:[1,0]
	v_pk_mul_f32 v[102:103], v[100:101], s[18:19] op_sel_hi:[1,0]
	v_cvt_pk_bf16_f32 v100, v104, v105
	v_add_co_u32_e32 v104, vcc, s51, v144
	v_cvt_pk_bf16_f32 v101, v106, v107
	v_cvt_pk_bf16_f32 v102, v102, v103
	v_cvt_pk_bf16_f32 v103, v108, v109
	v_pk_mul_f32 v[106:107], v[118:119], s[18:19] op_sel_hi:[1,0]
	s_nop 0
	v_addc_co_u32_e32 v105, vcc, 0, v145, vcc
	global_store_dwordx4 v[104:105], v[100:103], off sc1
	v_pk_mul_f32 v[108:109], v[116:117], s[18:19] op_sel_hi:[1,0]
	v_pk_mul_f32 v[48:49], v[48:49], s[18:19] op_sel_hi:[1,0]
	v_pk_mul_f32 v[100:101], v[120:121], s[18:19] op_sel_hi:[1,0]
	v_pk_mul_f32 v[102:103], v[122:123], s[18:19] op_sel_hi:[1,0]
	v_cvt_pk_bf16_f32 v100, v100, v101
	v_pk_mul_f32 v[92:93], v[92:93], s[18:19] op_sel_hi:[1,0]
	v_cvt_pk_bf16_f32 v101, v102, v103
	v_cvt_pk_bf16_f32 v102, v108, v109
	v_cvt_pk_bf16_f32 v103, v106, v107
	global_store_dwordx4 v[104:105], v[100:103], off offset:256 sc1
	v_pk_mul_f32 v[50:51], v[50:51], s[18:19] op_sel_hi:[1,0]
	v_pk_mul_f32 v[60:61], v[60:61], s[18:19] op_sel_hi:[1,0]
	v_pk_mul_f32 v[100:101], v[78:79], s[18:19] op_sel_hi:[1,0]
	v_pk_mul_f32 v[78:79], v[76:77], s[18:19] op_sel_hi:[1,0]
	v_cvt_pk_bf16_f32 v76, v80, v81
	v_add_co_u32_e32 v80, vcc, s60, v144
	v_cvt_pk_bf16_f32 v77, v82, v83
	v_cvt_pk_bf16_f32 v78, v78, v79
	v_cvt_pk_bf16_f32 v79, v100, v101
	v_pk_mul_f32 v[82:83], v[94:95], s[18:19] op_sel_hi:[1,0]
	s_nop 0
	v_addc_co_u32_e32 v81, vcc, 0, v145, vcc
	global_store_dwordx4 v[80:81], v[76:79], off sc1
	v_pk_mul_f32 v[40:41], v[40:41], s[18:19] op_sel_hi:[1,0]
	v_pk_mul_f32 v[42:43], v[42:43], s[18:19] op_sel_hi:[1,0]
	v_pk_mul_f32 v[76:77], v[96:97], s[18:19] op_sel_hi:[1,0]
	v_pk_mul_f32 v[78:79], v[98:99], s[18:19] op_sel_hi:[1,0]
	v_cvt_pk_bf16_f32 v76, v76, v77
	v_pk_mul_f32 v[24:25], v[24:25], s[18:19] op_sel_hi:[1,0]
	v_cvt_pk_bf16_f32 v77, v78, v79
	v_cvt_pk_bf16_f32 v78, v92, v93
	v_cvt_pk_bf16_f32 v79, v82, v83
	global_store_dwordx4 v[80:81], v[76:79], off offset:256 sc1
	v_pk_mul_f32 v[26:27], v[26:27], s[18:19] op_sel_hi:[1,0]
	v_pk_mul_f32 v[8:9], v[8:9], s[18:19] op_sel_hi:[1,0]
	v_pk_mul_f32 v[76:77], v[46:47], s[18:19] op_sel_hi:[1,0]
	v_pk_mul_f32 v[46:47], v[44:45], s[18:19] op_sel_hi:[1,0]
	v_cvt_pk_bf16_f32 v44, v48, v49
	v_add_co_u32_e32 v48, vcc, s61, v144
	v_cvt_pk_bf16_f32 v45, v50, v51
	v_cvt_pk_bf16_f32 v46, v46, v47
	v_cvt_pk_bf16_f32 v47, v76, v77
	v_pk_mul_f32 v[50:51], v[62:63], s[18:19] op_sel_hi:[1,0]
	s_nop 0
	v_addc_co_u32_e32 v49, vcc, 0, v145, vcc
	global_store_dwordx4 v[48:49], v[44:47], off sc1
	v_pk_mul_f32 v[28:29], v[28:29], s[18:19] op_sel_hi:[1,0]
	v_pk_mul_f32 v[10:11], v[10:11], s[18:19] op_sel_hi:[1,0]
	v_pk_mul_f32 v[46:47], v[66:67], s[18:19] op_sel_hi:[1,0]
	v_pk_mul_f32 v[44:45], v[64:65], s[18:19] op_sel_hi:[1,0]
	s_add_i32 s55, s55, s19
	v_cvt_pk_bf16_f32 v44, v44, v45
	v_cvt_pk_bf16_f32 v45, v46, v47
	v_cvt_pk_bf16_f32 v46, v60, v61
	v_cvt_pk_bf16_f32 v47, v50, v51
	global_store_dwordx4 v[48:49], v[44:47], off offset:256 sc1
	v_pk_mul_f32 v[48:49], v[70:71], s[18:19] op_sel_hi:[1,0]
	v_pk_mul_f32 v[50:51], v[68:69], s[18:19] op_sel_hi:[1,0]
	v_pk_mul_f32 v[46:47], v[74:75], s[18:19] op_sel_hi:[1,0]
	v_pk_mul_f32 v[44:45], v[72:73], s[18:19] op_sel_hi:[1,0]
	v_pk_mul_f32 v[60:61], v[84:85], s[18:19] op_sel_hi:[1,0]
	v_cvt_pk_bf16_f32 v44, v44, v45
	v_cvt_pk_bf16_f32 v45, v46, v47
	v_cvt_pk_bf16_f32 v46, v50, v51
	v_cvt_pk_bf16_f32 v47, v48, v49
	v_add_co_u32_e32 v48, vcc, s62, v144
	v_pk_mul_f32 v[50:51], v[86:87], s[18:19] op_sel_hi:[1,0]
	s_nop 0
	v_addc_co_u32_e32 v49, vcc, 0, v145, vcc
	global_store_dwordx4 v[48:49], v[44:47], off sc1
	s_mov_b32 s68, s66
	s_mov_b32 s26, s20
	v_pk_mul_f32 v[44:45], v[88:89], s[18:19] op_sel_hi:[1,0]
	v_pk_mul_f32 v[46:47], v[90:91], s[18:19] op_sel_hi:[1,0]
	v_cvt_pk_bf16_f32 v44, v44, v45
	s_mov_b64 s[38:39], s[24:25]
	v_cvt_pk_bf16_f32 v45, v46, v47
	v_cvt_pk_bf16_f32 v46, v60, v61
	v_cvt_pk_bf16_f32 v47, v50, v51
	global_store_dwordx4 v[48:49], v[44:47], off offset:256 sc1
	s_mov_b64 s[30:31], s[22:23]
	v_pk_mul_f32 v[12:13], v[12:13], s[18:19] op_sel_hi:[1,0]
	v_pk_mul_f32 v[44:45], v[38:39], s[18:19] op_sel_hi:[1,0]
	v_pk_mul_f32 v[38:39], v[36:37], s[18:19] op_sel_hi:[1,0]
	v_cvt_pk_bf16_f32 v36, v40, v41
	v_add_co_u32_e32 v40, vcc, s63, v144
	v_cvt_pk_bf16_f32 v37, v42, v43
	v_cvt_pk_bf16_f32 v38, v38, v39
	v_cvt_pk_bf16_f32 v39, v44, v45
	v_pk_mul_f32 v[42:43], v[54:55], s[18:19] op_sel_hi:[1,0]
	s_nop 0
	v_addc_co_u32_e32 v41, vcc, 0, v145, vcc
	global_store_dwordx4 v[40:41], v[36:39], off sc1
	v_pk_mul_f32 v[44:45], v[52:53], s[18:19] op_sel_hi:[1,0]
	s_nop 0
	v_pk_mul_f32 v[36:37], v[56:57], s[18:19] op_sel_hi:[1,0]
	v_pk_mul_f32 v[38:39], v[58:59], s[18:19] op_sel_hi:[1,0]
	v_cvt_pk_bf16_f32 v36, v36, v37
	s_nop 0
	v_cvt_pk_bf16_f32 v37, v38, v39
	v_cvt_pk_bf16_f32 v38, v44, v45
	v_cvt_pk_bf16_f32 v39, v42, v43
	global_store_dwordx4 v[40:41], v[36:39], off offset:256 sc1
	s_nop 1
	v_pk_mul_f32 v[36:37], v[22:23], s[18:19] op_sel_hi:[1,0]
	v_pk_mul_f32 v[22:23], v[20:21], s[18:19] op_sel_hi:[1,0]
	v_cvt_pk_bf16_f32 v20, v24, v25
	v_add_co_u32_e32 v24, vcc, s64, v144
	v_cvt_pk_bf16_f32 v21, v26, v27
	v_cvt_pk_bf16_f32 v22, v22, v23
	v_cvt_pk_bf16_f32 v23, v36, v37
	v_pk_mul_f32 v[26:27], v[30:31], s[18:19] op_sel_hi:[1,0]
	s_nop 0
	v_addc_co_u32_e32 v25, vcc, 0, v145, vcc
	global_store_dwordx4 v[24:25], v[20:23], off sc1
	s_nop 1
	v_pk_mul_f32 v[20:21], v[32:33], s[18:19] op_sel_hi:[1,0]
	v_pk_mul_f32 v[22:23], v[34:35], s[18:19] op_sel_hi:[1,0]
	v_cvt_pk_bf16_f32 v20, v20, v21
	s_nop 0
	v_cvt_pk_bf16_f32 v21, v22, v23
	v_cvt_pk_bf16_f32 v22, v28, v29
	v_cvt_pk_bf16_f32 v23, v26, v27
	global_store_dwordx4 v[24:25], v[20:23], off offset:256 sc1
	s_nop 1
	v_pk_mul_f32 v[20:21], v[6:7], s[18:19] op_sel_hi:[1,0]
	v_pk_mul_f32 v[6:7], v[4:5], s[18:19] op_sel_hi:[1,0]
	v_cvt_pk_bf16_f32 v4, v8, v9
	v_add_co_u32_e32 v8, vcc, s65, v144
	v_cvt_pk_bf16_f32 v5, v10, v11
	v_cvt_pk_bf16_f32 v6, v6, v7
	v_cvt_pk_bf16_f32 v7, v20, v21
	v_pk_mul_f32 v[10:11], v[14:15], s[18:19] op_sel_hi:[1,0]
	s_nop 0
	v_addc_co_u32_e32 v9, vcc, 0, v145, vcc
	global_store_dwordx4 v[8:9], v[4:7], off sc1
	s_andn2_b64 vcc, exec, s[0:1]
	s_nop 0
	v_pk_mul_f32 v[6:7], v[18:19], s[18:19] op_sel_hi:[1,0]
	v_pk_mul_f32 v[4:5], v[16:17], s[18:19] op_sel_hi:[1,0]
	s_nop 0
	v_cvt_pk_bf16_f32 v4, v4, v5
	v_cvt_pk_bf16_f32 v5, v6, v7
	v_cvt_pk_bf16_f32 v6, v12, v13
	v_cvt_pk_bf16_f32 v7, v10, v11
	global_store_dwordx4 v[8:9], v[4:7], off offset:256 sc1
	s_cbranch_vccz .LBB0_1350

.LBB0_1414:
	s_waitcnt vmcnt(3)
	v_mul_f32_e32 v4, 0x42800000, v4
	s_waitcnt vmcnt(2)
	v_mul_f32_e32 v8, 0x42800000, v8
	v_med3_f32 v4, v4, s67, v91
	v_med3_f32 v8, v8, s67, v91
	v_mov_b32_e32 v67, v69
	v_cvt_pk_fp8_f32 v67, v4, v8
	s_waitcnt vmcnt(1)
	v_mul_f32_e32 v12, 0x42800000, v12
	s_waitcnt vmcnt(0)
	v_mul_f32_e32 v0, 0x42800000, v0
	v_med3_f32 v4, v12, s67, v91
	v_med3_f32 v0, v0, s67, v91
	v_cvt_pk_fp8_f32 v67, v4, v0 op_sel:[0,0,1]
	v_mul_f32_e32 v0, 0x42800000, v57
	v_mul_f32_e32 v4, 0x42800000, v53
	v_med3_f32 v0, v0, s67, v91
	v_med3_f32 v4, v4, s67, v91
	v_mov_b32_e32 v98, v69
	v_cvt_pk_fp8_f32 v98, v0, v4
	v_mul_f32_e32 v8, 0x42800000, v61
	v_mul_f32_e32 v0, 0x42800000, v45
	v_med3_f32 v4, v8, s67, v91
	v_med3_f32 v0, v0, s67, v91
	v_cvt_pk_fp8_f32 v98, v4, v0 op_sel:[0,0,1]
	v_mul_f32_e32 v0, 0x42800000, v41
	v_mul_f32_e32 v4, 0x42800000, v37
	v_med3_f32 v0, v0, s67, v91
	v_med3_f32 v4, v4, s67, v91
	v_mov_b32_e32 v99, v69
	v_cvt_pk_fp8_f32 v99, v0, v4
	v_mul_f32_e32 v8, 0x42800000, v49
	v_mul_f32_e32 v0, 0x42800000, v33
	v_med3_f32 v4, v8, s67, v91
	v_med3_f32 v0, v0, s67, v91
	v_cvt_pk_fp8_f32 v99, v4, v0 op_sel:[0,0,1]
	v_mul_f32_e32 v0, 0x42800000, v21
	v_mul_f32_e32 v4, 0x42800000, v25
	v_med3_f32 v0, v0, s67, v91
	v_med3_f32 v4, v4, s67, v91
	v_mov_b32_e32 v100, v69
	v_cvt_pk_fp8_f32 v100, v0, v4
	v_mul_f32_e32 v8, 0x42800000, v29
	v_mul_f32_e32 v0, 0x42800000, v17
	v_med3_f32 v4, v8, s67, v91
	v_med3_f32 v0, v0, s67, v91
	v_cvt_pk_fp8_f32 v100, v4, v0 op_sel:[0,0,1]
	v_mul_f32_e32 v0, 0x42800000, v5
	v_mul_f32_e32 v4, 0x42800000, v9
	v_med3_f32 v0, v0, s67, v91
	v_med3_f32 v4, v4, s67, v91
	v_mov_b32_e32 v101, v69
	v_cvt_pk_fp8_f32 v101, v0, v4
	v_mul_f32_e32 v5, 0x42800000, v13
	v_mul_f32_e32 v0, 0x42800000, v1
	v_med3_f32 v1, v5, s67, v91
	v_med3_f32 v0, v0, s67, v91
	v_cvt_pk_fp8_f32 v101, v1, v0 op_sel:[0,0,1]
	v_mul_f32_e32 v0, 0x42800000, v58
	v_mul_f32_e32 v1, 0x42800000, v54
	v_med3_f32 v0, v0, s67, v91
	v_med3_f32 v1, v1, s67, v91
	v_mov_b32_e32 v102, v69
	v_cvt_pk_fp8_f32 v102, v0, v1
	v_mul_f32_e32 v4, 0x42800000, v62
	v_mul_f32_e32 v0, 0x42800000, v46
	v_med3_f32 v1, v4, s67, v91
	v_med3_f32 v0, v0, s67, v91
	v_cvt_pk_fp8_f32 v102, v1, v0 op_sel:[0,0,1]
	v_mul_f32_e32 v0, 0x42800000, v42
	v_mul_f32_e32 v1, 0x42800000, v38
	v_med3_f32 v0, v0, s67, v91
	v_med3_f32 v1, v1, s67, v91
	v_mov_b32_e32 v103, v69
	v_cvt_pk_fp8_f32 v103, v0, v1
	v_mul_f32_e32 v4, 0x42800000, v50
	v_mul_f32_e32 v0, 0x42800000, v34
	v_med3_f32 v1, v4, s67, v91
	v_med3_f32 v0, v0, s67, v91
	v_cvt_pk_fp8_f32 v103, v1, v0 op_sel:[0,0,1]
	v_mul_f32_e32 v0, 0x42800000, v22
	v_mul_f32_e32 v1, 0x42800000, v26
	v_med3_f32 v0, v0, s67, v91
	v_med3_f32 v1, v1, s67, v91
	v_mov_b32_e32 v104, v69
	v_cvt_pk_fp8_f32 v104, v0, v1
	v_mul_f32_e32 v4, 0x42800000, v30
	v_mul_f32_e32 v0, 0x42800000, v18
	v_med3_f32 v1, v4, s67, v91
	v_med3_f32 v0, v0, s67, v91
	v_cvt_pk_fp8_f32 v104, v1, v0 op_sel:[0,0,1]
	v_mul_f32_e32 v0, 0x42800000, v6
	v_mul_f32_e32 v1, 0x42800000, v10
	v_med3_f32 v0, v0, s67, v91
	v_med3_f32 v1, v1, s67, v91
	v_mov_b32_e32 v105, v69
	v_cvt_pk_fp8_f32 v105, v0, v1
	v_mul_f32_e32 v4, 0x42800000, v14
	v_mul_f32_e32 v0, 0x42800000, v2
	v_med3_f32 v1, v4, s67, v91
	v_med3_f32 v0, v0, s67, v91
	v_cvt_pk_fp8_f32 v105, v1, v0 op_sel:[0,0,1]
	v_mul_f32_e32 v0, 0x42800000, v59
	v_mul_f32_e32 v1, 0x42800000, v55
	v_med3_f32 v0, v0, s67, v91
	v_med3_f32 v1, v1, s67, v91
	v_mov_b32_e32 v4, v69
	v_cvt_pk_fp8_f32 v4, v0, v1
	v_mul_f32_e32 v2, 0x42800000, v63
	v_mul_f32_e32 v0, 0x42800000, v47
	v_med3_f32 v1, v2, s67, v91
	v_med3_f32 v0, v0, s67, v91
	v_cvt_pk_fp8_f32 v4, v1, v0 op_sel:[0,0,1]
	v_mul_f32_e32 v0, 0x42800000, v43
	v_mul_f32_e32 v1, 0x42800000, v39
	v_med3_f32 v0, v0, s67, v91
	v_med3_f32 v1, v1, s67, v91
	v_mov_b32_e32 v5, v69
	v_cvt_pk_fp8_f32 v5, v0, v1
	v_mul_f32_e32 v2, 0x42800000, v51
	v_mul_f32_e32 v0, 0x42800000, v35
	v_med3_f32 v1, v2, s67, v91
	v_med3_f32 v0, v0, s67, v91
	v_cvt_pk_fp8_f32 v5, v1, v0 op_sel:[0,0,1]
	v_mul_f32_e32 v0, 0x42800000, v23
	v_mul_f32_e32 v1, 0x42800000, v27
	v_mul_f32_e32 v56, 0x42800000, v56
	v_mul_f32_e32 v52, 0x42800000, v52
	v_med3_f32 v0, v0, s67, v91
	v_med3_f32 v1, v1, s67, v91
	v_mov_b32_e32 v6, v69
	v_med3_f32 v56, v56, s67, v91
	v_med3_f32 v52, v52, s67, v91
	v_mov_b32_e32 v64, v69
	v_cvt_pk_fp8_f32 v6, v0, v1
	v_cvt_pk_fp8_f32 v64, v56, v52
	v_mul_f32_e32 v40, 0x42800000, v40
	v_mul_f32_e32 v36, 0x42800000, v36
	v_mul_f32_e32 v20, 0x42800000, v20
	v_mul_f32_e32 v24, 0x42800000, v24
	v_med3_f32 v40, v40, s67, v91
	v_med3_f32 v36, v36, s67, v91
	v_mov_b32_e32 v65, v69
	v_med3_f32 v20, v20, s67, v91
	v_med3_f32 v24, v24, s67, v91
	v_mov_b32_e32 v66, v69
	v_mul_f32_e32 v2, 0x42800000, v31
	v_mul_f32_e32 v0, 0x42800000, v19
	v_mul_f32_e32 v60, 0x42800000, v60
	v_mul_f32_e32 v44, 0x42800000, v44
	v_cvt_pk_fp8_f32 v65, v40, v36
	v_cvt_pk_fp8_f32 v66, v20, v24
	v_med3_f32 v1, v2, s67, v91
	v_med3_f32 v0, v0, s67, v91
	v_med3_f32 v52, v60, s67, v91
	v_med3_f32 v44, v44, s67, v91
	v_cvt_pk_fp8_f32 v6, v1, v0 op_sel:[0,0,1]
	v_mul_f32_e32 v0, 0x42800000, v7
	v_mul_f32_e32 v1, 0x42800000, v11
	v_cvt_pk_fp8_f32 v64, v52, v44 op_sel:[0,0,1]
	v_mul_f32_e32 v44, 0x42800000, v48
	v_mul_f32_e32 v32, 0x42800000, v32
	v_mul_f32_e32 v28, 0x42800000, v28
	v_mul_f32_e32 v16, 0x42800000, v16
	v_med3_f32 v0, v0, s67, v91
	v_med3_f32 v1, v1, s67, v91
	v_mov_b32_e32 v7, v69
	v_med3_f32 v36, v44, s67, v91
	v_med3_f32 v32, v32, s67, v91
	v_med3_f32 v20, v28, s67, v91
	v_med3_f32 v16, v16, s67, v91
	v_cvt_pk_fp8_f32 v7, v0, v1
	v_cvt_pk_fp8_f32 v65, v36, v32 op_sel:[0,0,1]
	v_cvt_pk_fp8_f32 v66, v20, v16 op_sel:[0,0,1]
	v_mul_f32_e32 v2, 0x42800000, v15
	v_mul_f32_e32 v0, 0x42800000, v3
	v_med3_f32 v1, v2, s67, v91
	v_med3_f32 v0, v0, s67, v91
	v_cvt_pk_fp8_f32 v7, v1, v0 op_sel:[0,0,1]
	s_mul_hi_i32 s7, s6, 0x380000
	s_mul_i32 s6, s6, 0x380000
	ds_write_b128 v88, v[64:67] offset:40960
	ds_write_b128 v88, v[98:101] offset:41040
	ds_write_b128 v88, v[102:105] offset:41120
	ds_write_b128 v88, v[4:7] offset:41200
	s_add_u32 s6, s47, s6
	s_waitcnt lgkmcnt(0)
	s_addc_u32 s7, s48, s7
	s_add_i32 s17, s17, s4
	s_ashr_i32 s4, s24, 31
	ds_read_b128 v[0:3], v89 offset:40960
	s_add_u32 s6, s6, s24
	v_add_u32_e32 v4, s17, v76
	s_addc_u32 s7, s7, s4
	v_ashrrev_i32_e32 v5, 31, v4
	v_lshl_add_u64 v[8:9], s[6:7], 0, v[70:71]
	v_lshlrev_b64 v[4:5], 9, v[4:5]
	v_lshl_add_u64 v[10:11], v[8:9], 0, v[4:5]
	ds_read_b128 v[4:7], v89 offset:42240
	s_waitcnt lgkmcnt(1)
	global_store_dwordx4 v[10:11], v[0:3], off sc1
	s_nop 1
	v_add_u32_e32 v0, s17, v77
	v_ashrrev_i32_e32 v1, 31, v0
	v_lshlrev_b64 v[0:1], 9, v[0:1]
	v_lshl_add_u64 v[0:1], v[8:9], 0, v[0:1]
	s_waitcnt lgkmcnt(0)
	global_store_dwordx4 v[0:1], v[4:7], off sc1
	ds_read_b128 v[0:3], v89 offset:43520
	s_nop 0
	v_add_u32_e32 v4, s17, v78
	v_ashrrev_i32_e32 v5, 31, v4
	v_lshlrev_b64 v[4:5], 9, v[4:5]
	v_lshl_add_u64 v[10:11], v[8:9], 0, v[4:5]
	ds_read_b128 v[4:7], v89 offset:44800
	s_waitcnt lgkmcnt(1)
	global_store_dwordx4 v[10:11], v[0:3], off sc1
	s_nop 1
	v_add_u32_e32 v0, s17, v79
	v_ashrrev_i32_e32 v1, 31, v0
	v_lshlrev_b64 v[0:1], 9, v[0:1]
	v_lshl_add_u64 v[0:1], v[8:9], 0, v[0:1]
	s_waitcnt lgkmcnt(0)
	global_store_dwordx4 v[0:1], v[4:7], off sc1
	s_waitcnt lgkmcnt(0)

.LBB0_1416:
	s_add_i32 s4, s57, 0xffff8341
	s_mul_hi_i32 s6, s4, 0x20d56b39
	s_lshr_b32 s7, s6, 31
	s_ashr_i32 s6, s6, 12
	s_add_i32 s6, s6, s7
	s_mul_i32 s7, s6, 0x7cc0
	s_sub_i32 s38, s4, s7
	s_cmpk_gt_i32 s38, 0x1cbf
	s_mov_b64 s[8:9], -1
	s_cbranch_scc0 .LBB0_1422
	s_add_i32 s11, s38, 0xffffe340
	s_and_b32 s10, s11, 0xff
	s_cmpk_gt_u32 s38, 0x5cbf
	s_cbranch_scc0 .LBB0_1419
	v_mov_b32_e32 v0, s58
	s_add_i32 s4, s38, 0xffffa340
	s_ashr_i32 s7, s6, 31
	ds_read_b64 v[0:1], v0
	s_lshr_b32 s4, s4, 8
	s_lshl_b64 s[8:9], s[6:7], 26
	s_add_u32 s12, s3, s8
	s_addc_u32 s13, s40, s9
	s_lshl_b64 s[8:9], s[4:5], 20
	s_add_u32 s8, s12, s8
	s_addc_u32 s9, s13, s9
	s_waitcnt lgkmcnt(0)
	v_readfirstlane_b32 s16, v0
	s_lshl_b64 s[12:13], s[6:7], 27
	v_readfirstlane_b32 s17, v1
	s_add_u32 s7, s16, s12
	s_addc_u32 s17, s17, s13
	s_lshl_b64 s[12:13], s[4:5], 22
	s_add_u32 s16, s7, s12
	s_addc_u32 s17, s17, s13
	s_lshl_b32 s4, s10, 3
	s_and_b32 s7, s4, 0x7c0
	s_lshl_b32 s4, s38, 6
	s_and_b32 s12, s4, 0x1c0
	v_or_b32_e32 v0, s12, v75
	v_lshlrev_b32_e32 v0, 13, v0
	v_mov_b32_e32 v1, v69
	v_lshl_add_u64 v[0:1], s[16:17], 0, v[0:1]
	s_lshl_b32 s4, s7, 2
	v_lshl_add_u64 v[0:1], v[0:1], 0, s[4:5]
	v_mov_b32_e32 v73, v69
	v_lshl_add_u64 v[60:61], v[0:1], 0, v[72:73]
	v_add_co_u32_e32 v4, vcc, s59, v60
	s_mov_b32 s4, 0x8000
	s_nop 0
	v_addc_co_u32_e32 v5, vcc, 0, v61, vcc
	v_add_co_u32_e32 v8, vcc, s60, v60
	global_load_dwordx4 v[0:3], v[60:61], off nt
	s_nop 0
	global_load_dwordx4 v[4:7], v[4:5], off nt
	v_addc_co_u32_e32 v9, vcc, 0, v61, vcc
	v_add_co_u32_e32 v10, vcc, s61, v60
	v_mov_b32_e32 v64, v69
	s_nop 0
	v_addc_co_u32_e32 v11, vcc, 0, v61, vcc
	v_add_co_u32_e32 v16, vcc, s4, v60
	s_mov_b32 s4, 0xa000
	s_nop 0
	v_addc_co_u32_e32 v17, vcc, 0, v61, vcc
	v_add_co_u32_e32 v20, vcc, s4, v60
	s_mov_b32 s4, 0xc000
	s_nop 0
	v_addc_co_u32_e32 v21, vcc, 0, v61, vcc
	v_add_co_u32_e32 v24, vcc, s4, v60
	s_mov_b32 s4, 0xe000
	s_nop 0
	v_addc_co_u32_e32 v25, vcc, 0, v61, vcc
	global_load_dwordx4 v[12:15], v[8:9], off nt
	s_nop 0
	global_load_dwordx4 v[8:11], v[10:11], off nt
	v_add_co_u32_e32 v26, vcc, s4, v60
	s_mov_b32 s4, 0x10000
	s_nop 0
	v_addc_co_u32_e32 v27, vcc, 0, v61, vcc
	global_load_dwordx4 v[16:19], v[16:17], off nt
	s_nop 0
	global_load_dwordx4 v[20:23], v[20:21], off nt
	v_add_co_u32_e32 v28, vcc, s4, v60
	s_mov_b32 s4, 0x14000
	s_nop 0
	v_addc_co_u32_e32 v29, vcc, 0, v61, vcc
	v_add_co_u32_e32 v36, vcc, s62, v60
	global_load_dwordx4 v[32:35], v[24:25], off nt
	s_nop 0
	global_load_dwordx4 v[24:27], v[26:27], off nt
	v_addc_co_u32_e32 v37, vcc, 0, v61, vcc
	v_add_co_u32_e32 v40, vcc, s4, v60
	s_mov_b32 s4, 0x16000
	s_nop 0
	v_addc_co_u32_e32 v41, vcc, 0, v61, vcc
	global_load_dwordx4 v[28:31], v[28:29], off nt
	s_nop 0
	global_load_dwordx4 v[36:39], v[36:37], off nt
	v_add_co_u32_e32 v42, vcc, s4, v60
	v_mov_b32_e32 v65, v69
	s_nop 0
	v_addc_co_u32_e32 v43, vcc, 0, v61, vcc
	v_add_co_u32_e32 v44, vcc, s63, v60
	global_load_dwordx4 v[48:51], v[40:41], off nt
	s_nop 0
	global_load_dwordx4 v[40:43], v[42:43], off nt
	v_addc_co_u32_e32 v45, vcc, 0, v61, vcc
	v_add_co_u32_e32 v52, vcc, s64, v60
	v_mov_b32_e32 v66, v69
	s_nop 0
	v_addc_co_u32_e32 v53, vcc, 0, v61, vcc
	global_load_dwordx4 v[44:47], v[44:45], off nt
	s_nop 0
	global_load_dwordx4 v[52:55], v[52:53], off nt
	v_add_co_u32_e32 v56, vcc, s65, v60
	v_mov_b32_e32 v67, v69
	s_nop 0
	v_addc_co_u32_e32 v57, vcc, 0, v61, vcc
	v_add_co_u32_e32 v60, vcc, s66, v60
	global_load_dwordx4 v[56:59], v[56:57], off nt
	s_nop 0
	v_addc_co_u32_e32 v61, vcc, 0, v61, vcc
	global_load_dwordx4 v[60:63], v[60:61], off nt
	v_mov_b32_e32 v98, v69
	v_mov_b32_e32 v99, v69
	v_mov_b32_e32 v100, v69
	v_mov_b32_e32 v101, v69
	v_mov_b32_e32 v102, v69
	v_mov_b32_e32 v103, v69
	s_waitcnt vmcnt(15)
	v_mul_f32_e32 v0, 0x42000000, v0
	s_waitcnt vmcnt(14)
	v_mul_f32_e32 v4, 0x42000000, v4
	v_med3_f32 v0, v0, s67, v91
	v_med3_f32 v4, v4, s67, v91
	v_cvt_pk_fp8_f32 v64, v0, v4
	v_mov_b32_e32 v104, v69
	v_mov_b32_e32 v105, v69
	s_add_u32 s8, s8, s12
	s_addc_u32 s9, s9, 0
	s_waitcnt vmcnt(13)
	v_mul_f32_e32 v12, 0x42000000, v12
	s_waitcnt vmcnt(12)
	v_mul_f32_e32 v0, 0x42000000, v8
	v_med3_f32 v4, v12, s67, v91
	v_med3_f32 v0, v0, s67, v91
	v_cvt_pk_fp8_f32 v64, v4, v0 op_sel:[0,0,1]
	s_waitcnt vmcnt(11)
	v_mul_f32_e32 v0, 0x42000000, v16
	s_waitcnt vmcnt(10)
	v_mul_f32_e32 v4, 0x42000000, v20
	v_med3_f32 v0, v0, s67, v91
	v_med3_f32 v4, v4, s67, v91
	v_cvt_pk_fp8_f32 v65, v0, v4
	s_waitcnt vmcnt(9)
	v_mul_f32_e32 v8, 0x42000000, v32
	s_waitcnt vmcnt(8)
	v_mul_f32_e32 v0, 0x42000000, v24
	v_med3_f32 v4, v8, s67, v91
	v_med3_f32 v0, v0, s67, v91
	v_cvt_pk_fp8_f32 v65, v4, v0 op_sel:[0,0,1]
	s_waitcnt vmcnt(7)
	v_mul_f32_e32 v0, 0x42000000, v28
	s_waitcnt vmcnt(6)
	v_mul_f32_e32 v4, 0x42000000, v36
	v_med3_f32 v0, v0, s67, v91
	v_med3_f32 v4, v4, s67, v91
	v_cvt_pk_fp8_f32 v66, v0, v4
	s_waitcnt vmcnt(5)
	v_mul_f32_e32 v8, 0x42000000, v48
	s_waitcnt vmcnt(4)
	v_mul_f32_e32 v0, 0x42000000, v40
	v_med3_f32 v4, v8, s67, v91
	v_med3_f32 v0, v0, s67, v91
	v_cvt_pk_fp8_f32 v66, v4, v0 op_sel:[0,0,1]
	s_waitcnt vmcnt(3)
	v_mul_f32_e32 v0, 0x42000000, v44
	s_waitcnt vmcnt(2)
	v_mul_f32_e32 v4, 0x42000000, v52
	v_med3_f32 v0, v0, s67, v91
	v_med3_f32 v4, v4, s67, v91
	v_cvt_pk_fp8_f32 v67, v0, v4
	s_waitcnt vmcnt(1)
	v_mul_f32_e32 v8, 0x42000000, v56
	v_med3_f32 v4, v8, s67, v91
	s_waitcnt vmcnt(0)
	v_mul_f32_e32 v0, 0x42000000, v60
	v_med3_f32 v0, v0, s67, v91
	v_cvt_pk_fp8_f32 v67, v4, v0 op_sel:[0,0,1]
	v_mul_f32_e32 v0, 0x42000000, v1
	v_mul_f32_e32 v1, 0x42000000, v5
	v_med3_f32 v0, v0, s67, v91
	v_med3_f32 v1, v1, s67, v91
	v_cvt_pk_fp8_f32 v98, v0, v1
	v_mul_f32_e32 v4, 0x42000000, v13
	v_mul_f32_e32 v0, 0x42000000, v9
	v_med3_f32 v1, v4, s67, v91
	v_med3_f32 v0, v0, s67, v91
	v_cvt_pk_fp8_f32 v98, v1, v0 op_sel:[0,0,1]
	v_mul_f32_e32 v0, 0x42000000, v17
	v_mul_f32_e32 v1, 0x42000000, v21
	v_med3_f32 v0, v0, s67, v91
	v_med3_f32 v1, v1, s67, v91
	v_cvt_pk_fp8_f32 v99, v0, v1
	v_mul_f32_e32 v4, 0x42000000, v33
	v_mul_f32_e32 v0, 0x42000000, v25
	v_med3_f32 v1, v4, s67, v91
	v_med3_f32 v0, v0, s67, v91
	v_cvt_pk_fp8_f32 v99, v1, v0 op_sel:[0,0,1]
	v_mul_f32_e32 v0, 0x42000000, v29
	v_mul_f32_e32 v1, 0x42000000, v37
	v_med3_f32 v0, v0, s67, v91
	v_med3_f32 v1, v1, s67, v91
	v_cvt_pk_fp8_f32 v100, v0, v1
	v_mul_f32_e32 v4, 0x42000000, v49
	v_mul_f32_e32 v0, 0x42000000, v41
	v_med3_f32 v1, v4, s67, v91
	v_med3_f32 v0, v0, s67, v91
	v_cvt_pk_fp8_f32 v100, v1, v0 op_sel:[0,0,1]
	v_mul_f32_e32 v0, 0x42000000, v45
	v_mul_f32_e32 v1, 0x42000000, v53
	v_med3_f32 v0, v0, s67, v91
	v_med3_f32 v1, v1, s67, v91
	v_cvt_pk_fp8_f32 v101, v0, v1
	v_mul_f32_e32 v4, 0x42000000, v57
	v_mul_f32_e32 v0, 0x42000000, v61
	v_med3_f32 v1, v4, s67, v91
	v_med3_f32 v0, v0, s67, v91
	v_cvt_pk_fp8_f32 v101, v1, v0 op_sel:[0,0,1]
	v_mul_f32_e32 v0, 0x42000000, v2
	v_mul_f32_e32 v1, 0x42000000, v6
	v_med3_f32 v0, v0, s67, v91
	v_med3_f32 v1, v1, s67, v91
	v_cvt_pk_fp8_f32 v102, v0, v1
	v_mul_f32_e32 v2, 0x42000000, v14
	v_mul_f32_e32 v0, 0x42000000, v10
	v_med3_f32 v1, v2, s67, v91
	v_med3_f32 v0, v0, s67, v91
	v_cvt_pk_fp8_f32 v102, v1, v0 op_sel:[0,0,1]
	v_mul_f32_e32 v0, 0x42000000, v18
	v_mul_f32_e32 v1, 0x42000000, v22
	v_med3_f32 v0, v0, s67, v91
	v_med3_f32 v1, v1, s67, v91
	v_cvt_pk_fp8_f32 v103, v0, v1
	v_mul_f32_e32 v2, 0x42000000, v34
	v_mul_f32_e32 v0, 0x42000000, v26
	v_med3_f32 v1, v2, s67, v91
	v_med3_f32 v0, v0, s67, v91
	v_cvt_pk_fp8_f32 v103, v1, v0 op_sel:[0,0,1]
	v_mul_f32_e32 v0, 0x42000000, v30
	v_mul_f32_e32 v1, 0x42000000, v38
	v_med3_f32 v0, v0, s67, v91
	v_med3_f32 v1, v1, s67, v91
	v_cvt_pk_fp8_f32 v104, v0, v1
	v_mul_f32_e32 v2, 0x42000000, v50
	v_mul_f32_e32 v0, 0x42000000, v42
	v_med3_f32 v1, v2, s67, v91
	v_med3_f32 v0, v0, s67, v91
	v_cvt_pk_fp8_f32 v104, v1, v0 op_sel:[0,0,1]
	v_mul_f32_e32 v0, 0x42000000, v46
	v_mul_f32_e32 v1, 0x42000000, v54
	v_med3_f32 v0, v0, s67, v91
	v_med3_f32 v1, v1, s67, v91
	v_cvt_pk_fp8_f32 v105, v0, v1
	v_mul_f32_e32 v2, 0x42000000, v58
	v_mul_f32_e32 v0, 0x42000000, v62
	v_med3_f32 v1, v2, s67, v91
	v_med3_f32 v0, v0, s67, v91
	v_cvt_pk_fp8_f32 v105, v1, v0 op_sel:[0,0,1]
	v_mul_f32_e32 v0, 0x42000000, v3
	v_mul_f32_e32 v1, 0x42000000, v7
	v_med3_f32 v3, v0, s67, v91
	v_med3_f32 v1, v1, s67, v91
	v_mov_b32_e32 v0, v69
	v_cvt_pk_fp8_f32 v0, v3, v1
	v_mul_f32_e32 v2, 0x42000000, v15
	v_mul_f32_e32 v1, 0x42000000, v11
	v_med3_f32 v2, v2, s67, v91
	v_med3_f32 v1, v1, s67, v91
	v_cvt_pk_fp8_f32 v0, v2, v1 op_sel:[0,0,1]
	v_mul_f32_e32 v1, 0x42000000, v19
	v_mul_f32_e32 v2, 0x42000000, v23
	v_med3_f32 v4, v1, s67, v91
	v_med3_f32 v2, v2, s67, v91
	v_mov_b32_e32 v1, v69
	v_cvt_pk_fp8_f32 v1, v4, v2
	v_mul_f32_e32 v3, 0x42000000, v35
	v_mul_f32_e32 v2, 0x42000000, v27
	v_med3_f32 v3, v3, s67, v91
	v_med3_f32 v2, v2, s67, v91
	v_cvt_pk_fp8_f32 v1, v3, v2 op_sel:[0,0,1]
	v_mul_f32_e32 v2, 0x42000000, v31
	v_mul_f32_e32 v3, 0x42000000, v39
	v_med3_f32 v5, v2, s67, v91
	v_med3_f32 v3, v3, s67, v91
	v_mov_b32_e32 v2, v69
	v_cvt_pk_fp8_f32 v2, v5, v3
	v_mul_f32_e32 v4, 0x42000000, v51
	v_mul_f32_e32 v3, 0x42000000, v43
	v_med3_f32 v4, v4, s67, v91
	v_med3_f32 v3, v3, s67, v91
	v_cvt_pk_fp8_f32 v2, v4, v3 op_sel:[0,0,1]
	v_mul_f32_e32 v3, 0x42000000, v47
	v_mul_f32_e32 v4, 0x42000000, v55
	v_med3_f32 v6, v3, s67, v91
	v_med3_f32 v4, v4, s67, v91
	v_mov_b32_e32 v3, v69
	v_cvt_pk_fp8_f32 v3, v6, v4
	v_mul_f32_e32 v5, 0x42000000, v59
	v_mul_f32_e32 v4, 0x42000000, v63
	v_med3_f32 v5, v5, s67, v91
	v_med3_f32 v4, v4, s67, v91
	v_cvt_pk_fp8_f32 v3, v5, v4 op_sel:[0,0,1]
	ds_write_b128 v88, v[64:67] offset:40960
	ds_write_b128 v88, v[98:101] offset:41040
	ds_write_b128 v88, v[102:105] offset:41120
	ds_write_b128 v88, v[0:3] offset:41200
	s_waitcnt lgkmcnt(0)
	ds_read_b128 v[0:3], v89 offset:40960
	v_or_b32_e32 v4, s7, v76
	v_lshl_add_u64 v[8:9], s[8:9], 0, v[70:71]
	v_lshlrev_b32_e32 v4, 9, v4
	v_mov_b32_e32 v5, v69
	v_lshl_add_u64 v[10:11], v[8:9], 0, v[4:5]
	ds_read_b128 v[4:7], v89 offset:42240
	s_waitcnt lgkmcnt(1)
	global_store_dwordx4 v[10:11], v[0:3], off sc1
	s_mov_b64 s[8:9], 0
	s_nop 0
	v_or_b32_e32 v0, s7, v77
	v_lshlrev_b32_e32 v0, 9, v0
	v_mov_b32_e32 v1, v69
	v_lshl_add_u64 v[0:1], v[8:9], 0, v[0:1]
	s_waitcnt lgkmcnt(0)
	global_store_dwordx4 v[0:1], v[4:7], off sc1
	ds_read_b128 v[0:3], v89 offset:43520
	s_nop 0
	v_or_b32_e32 v4, s7, v78
	v_lshlrev_b32_e32 v4, 9, v4
	v_mov_b32_e32 v5, v69
	v_lshl_add_u64 v[10:11], v[8:9], 0, v[4:5]
	ds_read_b128 v[4:7], v89 offset:44800
	s_waitcnt lgkmcnt(1)
	global_store_dwordx4 v[10:11], v[0:3], off sc1
	s_nop 1
	v_or_b32_e32 v0, s7, v79
	v_lshlrev_b32_e32 v0, 9, v0
	v_mov_b32_e32 v1, v69
	v_lshl_add_u64 v[0:1], v[8:9], 0, v[0:1]
	s_waitcnt lgkmcnt(0)
	global_store_dwordx4 v[0:1], v[4:7], off sc1
	s_waitcnt lgkmcnt(0)
.LBB0_1419:
	s_andn2_b64 vcc, exec, s[8:9]
	s_cbranch_vccnz .LBB0_1421
	s_ashr_i32 s7, s6, 31
	s_lshr_b32 s4, s11, 9
	s_bfe_u32 s11, s11, 0x10008
	s_lshl_b64 s[12:13], s[6:7], 27
	s_add_u32 s7, s41, s12
	s_addc_u32 s16, s42, s13
	s_lshl_b32 s17, s11, 18
	s_lshl_b64 s[8:9], s[4:5], 21
	s_add_u32 s7, s7, s8
	s_addc_u32 s8, s16, s9
	s_add_u32 s7, s7, s17
	s_addc_u32 s8, s8, 0
	s_lshl_b32 s9, s11, 3
	s_add_i32 s9, s9, 0
	s_add_i32 s9, s9, 0x204e8
	v_mov_b32_e32 v0, s9
	ds_read_b64 v[0:1], v0
	v_mov_b32_e32 v73, v69
	v_mov_b32_e32 v12, v69
	v_mov_b32_e32 v14, v69
	v_mov_b32_e32 v13, v69
	s_waitcnt lgkmcnt(0)
	v_readfirstlane_b32 s9, v0
	v_readfirstlane_b32 s11, v1
	s_add_u32 s9, s9, s12
	s_addc_u32 s11, s11, s13
	s_lshl_b64 s[12:13], s[4:5], 22
	s_add_u32 s12, s9, s12
	s_addc_u32 s13, s11, s13
	s_lshl_b32 s4, s38, 6
	s_and_b32 s9, s4, 0x7c0
	v_or_b32_e32 v0, s9, v75
	v_lshlrev_b32_e32 v0, 11, v0
	v_mov_b32_e32 v1, v69
	s_lshl_b32 s4, s10, 3
	v_lshl_add_u64 v[0:1], s[12:13], 0, v[0:1]
	s_and_b32 s4, s4, 0x700
	v_lshl_add_u64 v[0:1], v[0:1], 0, s[4:5]
	v_lshl_add_u64 v[0:1], v[0:1], 0, v[72:73]
	v_add_co_u32_e32 v2, vcc, s68, v0
	global_load_dwordx4 v[40:43], v[0:1], off nt
	global_load_dwordx4 v[44:47], v[0:1], off offset:2048 nt
	v_addc_co_u32_e32 v3, vcc, 0, v1, vcc
	v_add_co_u32_e32 v4, vcc, s59, v0
	v_mov_b32_e32 v98, v69
	s_nop 0
	v_addc_co_u32_e32 v5, vcc, 0, v1, vcc
	global_load_dwordx4 v[56:59], v[4:5], off offset:-4096 nt
	global_load_dwordx4 v[20:23], v[4:5], off nt
	global_load_dwordx4 v[24:27], v[4:5], off offset:2048 nt
	v_add_co_u32_e32 v4, vcc, s69, v0
	v_mov_b32_e32 v99, v69
	s_nop 0
	v_addc_co_u32_e32 v5, vcc, 0, v1, vcc
	v_add_co_u32_e32 v6, vcc, s60, v0
	v_mov_b32_e32 v100, v69
	s_nop 0
	v_addc_co_u32_e32 v7, vcc, 0, v1, vcc
	global_load_dwordx4 v[64:67], v[2:3], off offset:2048 nt
	global_load_dwordx4 v[36:39], v[4:5], off offset:2048 nt
	global_load_dwordx4 v[60:63], v[6:7], off offset:-4096 nt
	global_load_dwordx4 v[16:19], v[6:7], off nt
	v_add_co_u32_e32 v2, vcc, s70, v0
	v_mov_b32_e32 v101, v69
	s_nop 0
	v_addc_co_u32_e32 v3, vcc, 0, v1, vcc
	v_add_co_u32_e32 v8, vcc, s61, v0
	v_mov_b32_e32 v102, v69
	s_nop 0
	v_addc_co_u32_e32 v9, vcc, 0, v1, vcc
	global_load_dwordx4 v[48:51], v[6:7], off offset:2048 nt
	global_load_dwordx4 v[52:55], v[8:9], off offset:-4096 nt
	global_load_dwordx4 v[28:31], v[2:3], off offset:2048 nt
	s_nop 0
	global_load_dwordx4 v[4:7], v[8:9], off nt
	s_nop 0
	global_load_dwordx4 v[8:11], v[8:9], off offset:2048 nt
	v_add_co_u32_e32 v0, vcc, s71, v0
	v_mov_b32_e32 v103, v69
	s_nop 0
	v_addc_co_u32_e32 v1, vcc, 0, v1, vcc
	global_load_dwordx4 v[32:35], v[0:1], off nt
	s_nop 0
	global_load_dwordx4 v[0:3], v[0:1], off offset:2048 nt
	v_mov_b32_e32 v104, v69
	v_mov_b32_e32 v105, v69
	s_lshl_b32 s4, s10, 1
	s_add_u32 s12, s7, s9
	s_addc_u32 s13, s8, 0
	s_lshl_b32 s7, s10, 2
	s_and_b32 s7, s7, 0x300
	s_and_b32 s4, s4, 64
	s_or_b32 s4, s4, s7
	s_waitcnt vmcnt(15)
	v_mul_f32_e32 v15, 0x42800000, v40
	s_waitcnt vmcnt(14)
	v_mul_f32_e32 v40, 0x42800000, v44
	v_med3_f32 v15, v15, s67, v91
	v_med3_f32 v40, v40, s67, v91
	v_cvt_pk_fp8_f32 v12, v15, v40
	s_waitcnt vmcnt(13)
	v_mul_f32_e32 v44, 0x42800000, v56
	s_waitcnt vmcnt(12)
	v_mul_f32_e32 v20, 0x42800000, v20
	s_waitcnt vmcnt(11)
	v_mul_f32_e32 v24, 0x42800000, v24
	v_med3_f32 v15, v20, s67, v91
	v_med3_f32 v20, v24, s67, v91
	v_cvt_pk_fp8_f32 v13, v15, v20
	v_med3_f32 v44, v44, s67, v91
	s_waitcnt vmcnt(10)
	v_mul_f32_e32 v56, 0x42800000, v64
	s_waitcnt vmcnt(9)
	v_mul_f32_e32 v36, 0x42800000, v36
	s_waitcnt vmcnt(8)
	v_mul_f32_e32 v60, 0x42800000, v60
	s_waitcnt vmcnt(7)
	v_mul_f32_e32 v16, 0x42800000, v16
	v_med3_f32 v16, v16, s67, v91
	v_med3_f32 v56, v56, s67, v91
	v_med3_f32 v24, v60, s67, v91
	v_med3_f32 v36, v36, s67, v91
	v_cvt_pk_fp8_f32 v12, v44, v56 op_sel:[0,0,1]
	v_cvt_pk_fp8_f32 v13, v24, v36 op_sel:[0,0,1]
	s_waitcnt vmcnt(6)
	v_mul_f32_e32 v48, 0x42800000, v48
	v_med3_f32 v40, v48, s67, v91
	v_cvt_pk_fp8_f32 v14, v16, v40
	s_waitcnt vmcnt(5)
	v_mul_f32_e32 v52, 0x42800000, v52
	s_waitcnt vmcnt(4)
	v_mul_f32_e32 v28, 0x42800000, v28
	s_waitcnt vmcnt(3)
	v_mul_f32_e32 v4, 0x42800000, v4
	s_waitcnt vmcnt(2)
	v_mul_f32_e32 v8, 0x42800000, v8
	v_med3_f32 v48, v52, s67, v91
	v_med3_f32 v15, v28, s67, v91
	v_cvt_pk_fp8_f32 v14, v48, v15 op_sel:[0,0,1]
	v_med3_f32 v4, v4, s67, v91
	v_med3_f32 v8, v8, s67, v91
	v_mov_b32_e32 v15, v69
	v_cvt_pk_fp8_f32 v15, v4, v8
	s_waitcnt vmcnt(1)
	v_mul_f32_e32 v16, 0x42800000, v32
	s_waitcnt vmcnt(0)
	v_mul_f32_e32 v0, 0x42800000, v0
	v_med3_f32 v4, v16, s67, v91
	v_med3_f32 v0, v0, s67, v91
	v_cvt_pk_fp8_f32 v15, v4, v0 op_sel:[0,0,1]
	v_mul_f32_e32 v0, 0x42800000, v41
	v_mul_f32_e32 v4, 0x42800000, v45
	v_med3_f32 v0, v0, s67, v91
	v_med3_f32 v4, v4, s67, v91
	v_cvt_pk_fp8_f32 v98, v0, v4
	v_mul_f32_e32 v8, 0x42800000, v57
	v_mul_f32_e32 v0, 0x42800000, v65
	v_med3_f32 v4, v8, s67, v91
	v_med3_f32 v0, v0, s67, v91
	v_cvt_pk_fp8_f32 v98, v4, v0 op_sel:[0,0,1]
	v_mul_f32_e32 v0, 0x42800000, v21
	v_mul_f32_e32 v4, 0x42800000, v25
	v_med3_f32 v0, v0, s67, v91
	v_med3_f32 v4, v4, s67, v91
	v_cvt_pk_fp8_f32 v99, v0, v4
	v_mul_f32_e32 v8, 0x42800000, v61
	v_mul_f32_e32 v0, 0x42800000, v37
	v_med3_f32 v4, v8, s67, v91
	v_med3_f32 v0, v0, s67, v91
	v_cvt_pk_fp8_f32 v99, v4, v0 op_sel:[0,0,1]
	v_mul_f32_e32 v0, 0x42800000, v17
	v_mul_f32_e32 v4, 0x42800000, v49
	v_med3_f32 v0, v0, s67, v91
	v_med3_f32 v4, v4, s67, v91
	v_cvt_pk_fp8_f32 v100, v0, v4
	v_mul_f32_e32 v8, 0x42800000, v53
	v_mul_f32_e32 v0, 0x42800000, v29
	v_med3_f32 v4, v8, s67, v91
	v_med3_f32 v0, v0, s67, v91
	v_cvt_pk_fp8_f32 v100, v4, v0 op_sel:[0,0,1]
	v_mul_f32_e32 v0, 0x42800000, v5
	v_mul_f32_e32 v4, 0x42800000, v9
	v_med3_f32 v0, v0, s67, v91
	v_med3_f32 v4, v4, s67, v91
	v_cvt_pk_fp8_f32 v101, v0, v4
	v_mul_f32_e32 v5, 0x42800000, v33
	v_mul_f32_e32 v0, 0x42800000, v1
	v_med3_f32 v1, v5, s67, v91
	v_med3_f32 v0, v0, s67, v91
	v_cvt_pk_fp8_f32 v101, v1, v0 op_sel:[0,0,1]
	v_mul_f32_e32 v0, 0x42800000, v42
	v_mul_f32_e32 v1, 0x42800000, v46
	v_med3_f32 v0, v0, s67, v91
	v_med3_f32 v1, v1, s67, v91
	v_cvt_pk_fp8_f32 v102, v0, v1
	v_mul_f32_e32 v4, 0x42800000, v58
	v_mul_f32_e32 v0, 0x42800000, v66
	v_med3_f32 v1, v4, s67, v91
	v_med3_f32 v0, v0, s67, v91
	v_cvt_pk_fp8_f32 v102, v1, v0 op_sel:[0,0,1]
	v_mul_f32_e32 v0, 0x42800000, v22
	v_mul_f32_e32 v1, 0x42800000, v26
	v_med3_f32 v0, v0, s67, v91
	v_med3_f32 v1, v1, s67, v91
	v_cvt_pk_fp8_f32 v103, v0, v1
	v_mul_f32_e32 v4, 0x42800000, v62
	v_mul_f32_e32 v0, 0x42800000, v38
	v_med3_f32 v1, v4, s67, v91
	v_med3_f32 v0, v0, s67, v91
	v_cvt_pk_fp8_f32 v103, v1, v0 op_sel:[0,0,1]
	v_mul_f32_e32 v0, 0x42800000, v18
	v_mul_f32_e32 v1, 0x42800000, v50
	v_med3_f32 v0, v0, s67, v91
	v_med3_f32 v1, v1, s67, v91
	v_cvt_pk_fp8_f32 v104, v0, v1
	v_mul_f32_e32 v4, 0x42800000, v54
	v_mul_f32_e32 v0, 0x42800000, v30
	v_med3_f32 v1, v4, s67, v91
	v_med3_f32 v0, v0, s67, v91
	v_cvt_pk_fp8_f32 v104, v1, v0 op_sel:[0,0,1]
	v_mul_f32_e32 v0, 0x42800000, v6
	v_mul_f32_e32 v1, 0x42800000, v10
	v_med3_f32 v0, v0, s67, v91
	v_med3_f32 v1, v1, s67, v91
	v_cvt_pk_fp8_f32 v105, v0, v1
	v_mul_f32_e32 v4, 0x42800000, v34
	v_mul_f32_e32 v0, 0x42800000, v2
	v_med3_f32 v1, v4, s67, v91
	v_med3_f32 v0, v0, s67, v91
	v_cvt_pk_fp8_f32 v105, v1, v0 op_sel:[0,0,1]
	v_mul_f32_e32 v0, 0x42800000, v43
	v_mul_f32_e32 v1, 0x42800000, v47
	v_med3_f32 v0, v0, s67, v91
	v_med3_f32 v1, v1, s67, v91
	v_mov_b32_e32 v4, v69
	v_cvt_pk_fp8_f32 v4, v0, v1
	v_mul_f32_e32 v2, 0x42800000, v59
	v_mul_f32_e32 v0, 0x42800000, v67
	v_med3_f32 v1, v2, s67, v91
	v_med3_f32 v0, v0, s67, v91
	v_cvt_pk_fp8_f32 v4, v1, v0 op_sel:[0,0,1]
	v_mul_f32_e32 v0, 0x42800000, v23
	v_mul_f32_e32 v1, 0x42800000, v27
	v_med3_f32 v0, v0, s67, v91
	v_med3_f32 v1, v1, s67, v91
	v_mov_b32_e32 v5, v69
	v_cvt_pk_fp8_f32 v5, v0, v1
	v_mul_f32_e32 v2, 0x42800000, v63
	v_mul_f32_e32 v0, 0x42800000, v39
	v_med3_f32 v1, v2, s67, v91
	v_med3_f32 v0, v0, s67, v91
	v_cvt_pk_fp8_f32 v5, v1, v0 op_sel:[0,0,1]
	v_mul_f32_e32 v0, 0x42800000, v19
	v_mul_f32_e32 v1, 0x42800000, v51
	v_med3_f32 v0, v0, s67, v91
	v_med3_f32 v1, v1, s67, v91
	v_mov_b32_e32 v6, v69
	v_cvt_pk_fp8_f32 v6, v0, v1
	v_mul_f32_e32 v2, 0x42800000, v55
	v_mul_f32_e32 v0, 0x42800000, v31
	v_med3_f32 v1, v2, s67, v91
	v_med3_f32 v0, v0, s67, v91
	v_cvt_pk_fp8_f32 v6, v1, v0 op_sel:[0,0,1]
	v_mul_f32_e32 v0, 0x42800000, v7
	v_mul_f32_e32 v1, 0x42800000, v11
	v_med3_f32 v0, v0, s67, v91
	v_med3_f32 v1, v1, s67, v91
	v_mov_b32_e32 v7, v69
	v_cvt_pk_fp8_f32 v7, v0, v1
	v_mul_f32_e32 v2, 0x42800000, v35
	v_mul_f32_e32 v0, 0x42800000, v3
	v_med3_f32 v1, v2, s67, v91
	v_med3_f32 v0, v0, s67, v91
	v_cvt_pk_fp8_f32 v7, v1, v0 op_sel:[0,0,1]
	ds_write_b128 v88, v[12:15] offset:40960
	ds_write_b128 v88, v[98:101] offset:41040
	ds_write_b128 v88, v[102:105] offset:41120
	ds_write_b128 v88, v[4:7] offset:41200
	s_waitcnt lgkmcnt(0)
	ds_read_b128 v[0:3], v89 offset:40960
	v_or_b32_e32 v4, s4, v76
	v_lshl_add_u64 v[8:9], s[12:13], 0, v[70:71]
	v_lshlrev_b32_e32 v4, 11, v4
	v_mov_b32_e32 v5, v69
	v_lshl_add_u64 v[10:11], v[8:9], 0, v[4:5]
	ds_read_b128 v[4:7], v89 offset:42240
	s_waitcnt lgkmcnt(1)
	global_store_dwordx4 v[10:11], v[0:3], off sc1
	s_nop 1
	v_or_b32_e32 v0, s4, v77
	v_lshlrev_b32_e32 v0, 11, v0
	v_mov_b32_e32 v1, v69
	v_lshl_add_u64 v[0:1], v[8:9], 0, v[0:1]
	s_waitcnt lgkmcnt(0)
	global_store_dwordx4 v[0:1], v[4:7], off sc1
	ds_read_b128 v[0:3], v89 offset:43520
	s_nop 0
	v_or_b32_e32 v4, s4, v78
	v_lshlrev_b32_e32 v4, 11, v4
	v_mov_b32_e32 v5, v69
	v_lshl_add_u64 v[10:11], v[8:9], 0, v[4:5]
	ds_read_b128 v[4:7], v89 offset:44800
	s_waitcnt lgkmcnt(1)
	global_store_dwordx4 v[10:11], v[0:3], off sc1
	s_nop 1
	v_or_b32_e32 v0, s4, v79
	v_lshlrev_b32_e32 v0, 11, v0
	v_mov_b32_e32 v1, v69
	v_lshl_add_u64 v[0:1], v[8:9], 0, v[0:1]
	s_waitcnt lgkmcnt(0)
	global_store_dwordx4 v[0:1], v[4:7], off sc1
	s_waitcnt lgkmcnt(0)

.LBB0_1451:
	s_cmpk_gt_i32 s94, 0x93
	s_cbranch_scc1 .LBB0_1453
	s_lshl_b32 s30, s7, 6
	s_mul_i32 s31, s6, 0x1280000
	v_or_b32_e32 v0, s30, v75
	s_mul_hi_i32 s23, s6, 0x1280000
	s_add_u32 s31, s51, s31
	v_mul_hi_i32_i24_e32 v1, 0x9500, v0
	v_mul_i32_i24_e32 v0, 0x9500, v0
	s_addc_u32 s38, s52, s23
	v_lshl_add_u64 v[0:1], s[8:9], 0, v[0:1]
	s_ashr_i32 s23, s22, 31
	v_lshl_add_u64 v[0:1], s[22:23], 2, v[0:1]
	v_mov_b32_e32 v73, v69
	v_lshl_add_u64 v[56:57], v[0:1], 0, v[72:73]
	v_add_co_u32_e32 v4, vcc, s79, v56
	global_load_dwordx4 v[0:3], v[56:57], off nt
	s_nop 0
	v_addc_co_u32_e32 v5, vcc, 0, v57, vcc
	global_load_dwordx4 v[16:19], v[4:5], off offset:1280 nt
	v_add_co_u32_e32 v4, vcc, s62, v56
	v_mov_b32_e32 v64, v69
	s_nop 0
	v_addc_co_u32_e32 v5, vcc, 0, v57, vcc
	global_load_dwordx4 v[20:23], v[4:5], off offset:2560 nt
	v_add_co_u32_e32 v4, vcc, s80, v56
	v_mov_b32_e32 v65, v69
	s_nop 0
	v_addc_co_u32_e32 v5, vcc, 0, v57, vcc
	global_load_dwordx4 v[44:47], v[4:5], off offset:3840 nt
	v_add_co_u32_e32 v4, vcc, s81, v56
	v_mov_b32_e32 v66, v69
	s_nop 0
	v_addc_co_u32_e32 v5, vcc, 0, v57, vcc
	v_add_co_u32_e32 v8, vcc, s82, v56
	global_load_dwordx4 v[4:7], v[4:5], off offset:1024 nt
	s_nop 0
	v_addc_co_u32_e32 v9, vcc, 0, v57, vcc
	global_load_dwordx4 v[24:27], v[8:9], off offset:2304 nt
	v_add_co_u32_e32 v8, vcc, s83, v56
	v_mov_b32_e32 v67, v69
	s_nop 0
	v_addc_co_u32_e32 v9, vcc, 0, v57, vcc
	global_load_dwordx4 v[28:31], v[8:9], off offset:3584 nt
	v_add_co_u32_e32 v8, vcc, s84, v56
	s_ashr_i32 s23, s30, 31
	s_nop 0
	v_addc_co_u32_e32 v9, vcc, 0, v57, vcc
	global_load_dwordx4 v[52:55], v[8:9], off offset:768 nt
	v_add_co_u32_e32 v8, vcc, s85, v56
	s_add_u32 s30, s31, s30
	s_nop 0
	v_addc_co_u32_e32 v9, vcc, 0, v57, vcc
	v_add_co_u32_e32 v12, vcc, s86, v56
	global_load_dwordx4 v[8:11], v[8:9], off offset:2048 nt
	s_nop 0
	v_addc_co_u32_e32 v13, vcc, 0, v57, vcc
	global_load_dwordx4 v[32:35], v[12:13], off offset:3328 nt
	v_add_co_u32_e32 v12, vcc, s87, v56
	s_addc_u32 s31, s38, s23
	s_nop 0
	v_addc_co_u32_e32 v13, vcc, 0, v57, vcc
	global_load_dwordx4 v[36:39], v[12:13], off offset:512 nt
	v_add_co_u32_e32 v12, vcc, s88, v56
	s_mov_b64 s[38:39], 0
	s_nop 0
	v_addc_co_u32_e32 v13, vcc, 0, v57, vcc
	global_load_dwordx4 v[60:63], v[12:13], off offset:1792 nt
	v_add_co_u32_e32 v12, vcc, s89, v56
	s_waitcnt vmcnt(11)
	v_mul_f32_e32 v0, 0x42800000, v0
	v_addc_co_u32_e32 v13, vcc, 0, v57, vcc
	v_add_co_u32_e32 v40, vcc, s90, v56
	global_load_dwordx4 v[12:15], v[12:13], off offset:3072 nt
	s_nop 0
	v_addc_co_u32_e32 v41, vcc, 0, v57, vcc
	global_load_dwordx4 v[40:43], v[40:41], off offset:256 nt
	v_add_co_u32_e32 v48, vcc, s91, v56
	s_waitcnt vmcnt(12)
	v_mul_f32_e32 v16, 0x42800000, v16
	v_addc_co_u32_e32 v49, vcc, 0, v57, vcc
	v_add_co_u32_e32 v56, vcc, s92, v56
	global_load_dwordx4 v[48:51], v[48:49], off offset:1536 nt
	s_nop 0
	v_addc_co_u32_e32 v57, vcc, 0, v57, vcc
	global_load_dwordx4 v[56:59], v[56:57], off offset:2816 nt
	v_med3_f32 v0, v0, s67, v91
	v_med3_f32 v16, v16, s67, v91
	v_cvt_pk_fp8_f32 v64, v0, v16
	s_waitcnt vmcnt(11)
	v_mul_f32_e32 v0, 0x42800000, v4
	v_med3_f32 v0, v0, s67, v91
	v_mul_f32_e32 v20, 0x42800000, v20
	s_waitcnt vmcnt(10)
	v_mul_f32_e32 v4, 0x42800000, v24
	v_med3_f32 v4, v4, s67, v91
	v_mul_f32_e32 v44, 0x42800000, v44
	v_cvt_pk_fp8_f32 v65, v0, v4
	v_med3_f32 v20, v20, s67, v91
	v_med3_f32 v44, v44, s67, v91
	v_cvt_pk_fp8_f32 v64, v20, v44 op_sel:[0,0,1]
	s_waitcnt vmcnt(9)
	v_mul_f32_e32 v16, 0x42800000, v28
	v_med3_f32 v16, v16, s67, v91
	s_waitcnt vmcnt(8)
	v_mul_f32_e32 v20, 0x42800000, v52
	v_med3_f32 v20, v20, s67, v91
	v_cvt_pk_fp8_f32 v65, v16, v20 op_sel:[0,0,1]
	s_waitcnt vmcnt(7)
	v_mul_f32_e32 v0, 0x42800000, v8
	v_med3_f32 v0, v0, s67, v91
	s_waitcnt vmcnt(6)
	v_mul_f32_e32 v4, 0x42800000, v32
	v_med3_f32 v4, v4, s67, v91
	v_cvt_pk_fp8_f32 v66, v0, v4
	s_waitcnt vmcnt(5)
	v_mul_f32_e32 v8, 0x42800000, v36
	v_med3_f32 v8, v8, s67, v91
	s_waitcnt vmcnt(4)
	v_mul_f32_e32 v16, 0x42800000, v60
	v_med3_f32 v16, v16, s67, v91
	v_cvt_pk_fp8_f32 v66, v8, v16 op_sel:[0,0,1]
	s_waitcnt vmcnt(3)
	v_mul_f32_e32 v0, 0x42800000, v12
	v_med3_f32 v0, v0, s67, v91
	s_waitcnt vmcnt(2)
	v_mul_f32_e32 v4, 0x42800000, v40
	v_med3_f32 v4, v4, s67, v91
	v_cvt_pk_fp8_f32 v67, v0, v4
	v_mul_f32_e32 v0, 0x42800000, v1
	v_mul_f32_e32 v1, 0x42800000, v17
	v_med3_f32 v0, v0, s67, v91
	v_med3_f32 v1, v1, s67, v91
	v_mul_f32_e32 v4, 0x42800000, v21
	s_waitcnt vmcnt(1)
	v_mul_f32_e32 v8, 0x42800000, v48
	v_med3_f32 v8, v8, s67, v91
	v_med3_f32 v4, v4, s67, v91
	s_waitcnt vmcnt(0)
	v_mul_f32_e32 v12, 0x42800000, v56
	v_med3_f32 v12, v12, s67, v91
	v_cvt_pk_fp8_f32 v67, v8, v12 op_sel:[0,0,1]
	v_mul_f32_e32 v8, 0x42800000, v45
	v_med3_f32 v8, v8, s67, v91
	ds_write_b128 v88, v[64:67] offset:40960
	v_mov_b32_e32 v64, v69
	v_cvt_pk_fp8_f32 v64, v0, v1
	v_mul_f32_e32 v0, 0x42800000, v5
	v_mul_f32_e32 v1, 0x42800000, v25
	v_med3_f32 v0, v0, s67, v91
	v_med3_f32 v1, v1, s67, v91
	v_mov_b32_e32 v65, v69
	v_cvt_pk_fp8_f32 v65, v0, v1
	v_mul_f32_e32 v0, 0x42800000, v9
	v_mul_f32_e32 v1, 0x42800000, v33
	v_med3_f32 v0, v0, s67, v91
	v_med3_f32 v1, v1, s67, v91
	v_mov_b32_e32 v66, v69
	v_cvt_pk_fp8_f32 v64, v4, v8 op_sel:[0,0,1]
	v_mul_f32_e32 v4, 0x42800000, v29
	v_mul_f32_e32 v5, 0x42800000, v53
	v_cvt_pk_fp8_f32 v66, v0, v1
	v_mul_f32_e32 v0, 0x42800000, v13
	v_mul_f32_e32 v1, 0x42800000, v41
	v_med3_f32 v4, v4, s67, v91
	v_med3_f32 v5, v5, s67, v91
	v_med3_f32 v0, v0, s67, v91
	v_med3_f32 v1, v1, s67, v91
	v_mov_b32_e32 v67, v69
	v_cvt_pk_fp8_f32 v65, v4, v5 op_sel:[0,0,1]
	v_mul_f32_e32 v4, 0x42800000, v37
	v_mul_f32_e32 v5, 0x42800000, v61
	v_cvt_pk_fp8_f32 v67, v0, v1
	v_med3_f32 v4, v4, s67, v91
	v_med3_f32 v5, v5, s67, v91
	v_cvt_pk_fp8_f32 v66, v4, v5 op_sel:[0,0,1]
	v_mul_f32_e32 v4, 0x42800000, v49
	v_mul_f32_e32 v5, 0x42800000, v57
	v_med3_f32 v4, v4, s67, v91
	v_med3_f32 v5, v5, s67, v91
	v_cvt_pk_fp8_f32 v67, v4, v5 op_sel:[0,0,1]
	v_mul_f32_e32 v0, 0x42800000, v2
	v_mul_f32_e32 v1, 0x42800000, v18
	v_med3_f32 v0, v0, s67, v91
	ds_write_b128 v88, v[64:67] offset:41040
	v_med3_f32 v1, v1, s67, v91
	v_mov_b32_e32 v64, v69
	v_cvt_pk_fp8_f32 v64, v0, v1
	v_mul_f32_e32 v0, 0x42800000, v6
	v_mul_f32_e32 v1, 0x42800000, v26
	v_med3_f32 v0, v0, s67, v91
	v_med3_f32 v1, v1, s67, v91
	v_mov_b32_e32 v65, v69
	v_mul_f32_e32 v2, 0x42800000, v22
	v_mul_f32_e32 v4, 0x42800000, v46
	v_cvt_pk_fp8_f32 v65, v0, v1
	v_mul_f32_e32 v0, 0x42800000, v10
	v_mul_f32_e32 v1, 0x42800000, v34
	v_med3_f32 v2, v2, s67, v91
	v_med3_f32 v4, v4, s67, v91
	v_med3_f32 v0, v0, s67, v91
	v_med3_f32 v1, v1, s67, v91
	v_mov_b32_e32 v66, v69
	v_cvt_pk_fp8_f32 v64, v2, v4 op_sel:[0,0,1]
	v_mul_f32_e32 v2, 0x42800000, v30
	v_mul_f32_e32 v4, 0x42800000, v54
	v_cvt_pk_fp8_f32 v66, v0, v1
	v_mul_f32_e32 v0, 0x42800000, v14
	v_mul_f32_e32 v1, 0x42800000, v42
	v_med3_f32 v2, v2, s67, v91
	v_med3_f32 v4, v4, s67, v91
	v_med3_f32 v0, v0, s67, v91
	v_med3_f32 v1, v1, s67, v91
	v_mov_b32_e32 v67, v69
	v_cvt_pk_fp8_f32 v65, v2, v4 op_sel:[0,0,1]
	v_mul_f32_e32 v2, 0x42800000, v38
	v_mul_f32_e32 v4, 0x42800000, v62
	v_cvt_pk_fp8_f32 v67, v0, v1
	v_med3_f32 v2, v2, s67, v91
	v_med3_f32 v4, v4, s67, v91
	v_cvt_pk_fp8_f32 v66, v2, v4 op_sel:[0,0,1]
	v_mul_f32_e32 v2, 0x42800000, v50
	v_mul_f32_e32 v4, 0x42800000, v58
	v_med3_f32 v2, v2, s67, v91
	v_med3_f32 v4, v4, s67, v91
	v_mul_f32_e32 v0, 0x42800000, v3
	v_mul_f32_e32 v1, 0x42800000, v19
	v_cvt_pk_fp8_f32 v67, v2, v4 op_sel:[0,0,1]
	v_med3_f32 v4, v0, s67, v91
	v_med3_f32 v1, v1, s67, v91
	v_mov_b32_e32 v0, v69
	v_cvt_pk_fp8_f32 v0, v4, v1
	v_mul_f32_e32 v2, 0x42800000, v23
	v_mul_f32_e32 v3, 0x42800000, v47
	v_med3_f32 v2, v2, s67, v91
	v_med3_f32 v3, v3, s67, v91
	v_cvt_pk_fp8_f32 v0, v2, v3 op_sel:[0,0,1]
	v_mul_f32_e32 v1, 0x42800000, v7
	v_mul_f32_e32 v2, 0x42800000, v27
	v_med3_f32 v5, v1, s67, v91
	v_med3_f32 v2, v2, s67, v91
	v_mov_b32_e32 v1, v69
	v_cvt_pk_fp8_f32 v1, v5, v2
	v_mul_f32_e32 v3, 0x42800000, v31
	v_mul_f32_e32 v4, 0x42800000, v55
	v_med3_f32 v3, v3, s67, v91
	v_med3_f32 v4, v4, s67, v91
	v_cvt_pk_fp8_f32 v1, v3, v4 op_sel:[0,0,1]
	v_mul_f32_e32 v2, 0x42800000, v11
	v_mul_f32_e32 v3, 0x42800000, v35
	v_med3_f32 v6, v2, s67, v91
	v_med3_f32 v3, v3, s67, v91
	v_mov_b32_e32 v2, v69
	v_cvt_pk_fp8_f32 v2, v6, v3
	v_mul_f32_e32 v4, 0x42800000, v39
	v_mul_f32_e32 v5, 0x42800000, v63
	v_med3_f32 v4, v4, s67, v91
	v_med3_f32 v5, v5, s67, v91
	v_cvt_pk_fp8_f32 v2, v4, v5 op_sel:[0,0,1]
	v_mul_f32_e32 v3, 0x42800000, v15
	v_mul_f32_e32 v4, 0x42800000, v43
	v_med3_f32 v7, v3, s67, v91
	v_med3_f32 v4, v4, s67, v91
	v_mov_b32_e32 v3, v69
	v_cvt_pk_fp8_f32 v3, v7, v4
	v_mul_f32_e32 v5, 0x42800000, v51
	v_mul_f32_e32 v6, 0x42800000, v59
	v_med3_f32 v5, v5, s67, v91
	v_med3_f32 v6, v6, s67, v91
	v_cvt_pk_fp8_f32 v3, v5, v6 op_sel:[0,0,1]
	ds_write_b128 v88, v[64:67] offset:41120
	v_or_b32_e32 v6, s17, v76
	v_ashrrev_i32_e32 v7, 31, v6
	ds_write_b128 v88, v[0:3] offset:41200
	s_waitcnt lgkmcnt(0)
	ds_read_b128 v[0:3], v89 offset:40960
	v_lshl_add_u64 v[4:5], s[30:31], 0, v[70:71]
	v_lshlrev_b64 v[6:7], 11, v[6:7]
	v_lshl_add_u64 v[6:7], v[4:5], 0, v[6:7]
	s_waitcnt lgkmcnt(0)
	global_store_dwordx4 v[6:7], v[0:3], off sc1
	ds_read_b128 v[0:3], v89 offset:42240
	v_or_b32_e32 v6, s17, v77
	v_ashrrev_i32_e32 v7, 31, v6
	v_lshlrev_b64 v[6:7], 11, v[6:7]
	v_lshl_add_u64 v[6:7], v[4:5], 0, v[6:7]
	s_waitcnt lgkmcnt(0)
	global_store_dwordx4 v[6:7], v[0:3], off sc1
	ds_read_b128 v[0:3], v89 offset:43520
	v_or_b32_e32 v6, s17, v78
	v_ashrrev_i32_e32 v7, 31, v6
	v_lshlrev_b64 v[6:7], 11, v[6:7]
	v_lshl_add_u64 v[6:7], v[4:5], 0, v[6:7]
	s_waitcnt lgkmcnt(0)
	global_store_dwordx4 v[6:7], v[0:3], off sc1
	ds_read_b128 v[0:3], v89 offset:44800
	v_or_b32_e32 v6, s17, v79
	v_ashrrev_i32_e32 v7, 31, v6
	v_lshlrev_b64 v[6:7], 11, v[6:7]
	v_lshl_add_u64 v[4:5], v[4:5], 0, v[6:7]
	s_waitcnt lgkmcnt(0)
	global_store_dwordx4 v[4:5], v[0:3], off sc1
	s_waitcnt lgkmcnt(0)
.LBB0_1453:
	s_and_b64 vcc, exec, s[38:39]
	s_cbranch_vccz .LBB0_1415
	s_xor_b64 s[38:39], s[24:25], -1
	s_lshl_b32 s24, s7, 6
	s_mov_b64 s[30:31], -1
	s_and_b64 vcc, exec, s[38:39]
	s_cbranch_vccz .LBB0_1484
	s_andn2_b64 vcc, exec, s[28:29]
	s_cbranch_vccnz .LBB0_1458
	s_ashr_i32 s7, s6, 31
	s_lshl_b64 s[28:29], s[6:7], 22
	v_or_b32_e32 v0, s24, v75
	s_add_u32 s7, s53, s28
	v_mul_hi_i32_i24_e32 v1, s18, v0
	v_mul_i32_i24_e32 v0, s18, v0
	s_addc_u32 s25, s54, s29
	v_lshl_add_u64 v[0:1], v[0:1], 2, s[8:9]
	s_ashr_i32 s23, s22, 31
	v_lshl_add_u64 v[0:1], s[22:23], 2, v[0:1]
	v_mov_b32_e32 v73, v69
	v_lshl_add_u64 v[0:1], v[0:1], 0, v[72:73]
	s_lshl_b64 s[28:29], s[18:19], 2
	global_load_dwordx4 v[56:59], v[0:1], off nt
	v_lshl_add_u64 v[0:1], v[0:1], 0, s[28:29]
	global_load_dwordx4 v[60:63], v[0:1], off nt
	v_lshl_add_u64 v[0:1], v[0:1], 0, s[28:29]
	global_load_dwordx4 v[64:67], v[0:1], off nt
	v_lshl_add_u64 v[0:1], v[0:1], 0, s[28:29]
	global_load_dwordx4 v[52:55], v[0:1], off nt
	v_lshl_add_u64 v[0:1], v[0:1], 0, s[28:29]
	global_load_dwordx4 v[40:43], v[0:1], off nt
	v_lshl_add_u64 v[0:1], v[0:1], 0, s[28:29]
	global_load_dwordx4 v[44:47], v[0:1], off nt
	v_lshl_add_u64 v[0:1], v[0:1], 0, s[28:29]
	global_load_dwordx4 v[48:51], v[0:1], off nt
	v_lshl_add_u64 v[0:1], v[0:1], 0, s[28:29]
	global_load_dwordx4 v[36:39], v[0:1], off nt
	v_lshl_add_u64 v[0:1], v[0:1], 0, s[28:29]
	global_load_dwordx4 v[24:27], v[0:1], off nt
	v_lshl_add_u64 v[0:1], v[0:1], 0, s[28:29]
	global_load_dwordx4 v[28:31], v[0:1], off nt
	v_lshl_add_u64 v[0:1], v[0:1], 0, s[28:29]
	global_load_dwordx4 v[32:35], v[0:1], off nt
	v_lshl_add_u64 v[0:1], v[0:1], 0, s[28:29]
	global_load_dwordx4 v[20:23], v[0:1], off nt
	v_lshl_add_u64 v[0:1], v[0:1], 0, s[28:29]
	global_load_dwordx4 v[4:7], v[0:1], off nt
	v_lshl_add_u64 v[0:1], v[0:1], 0, s[28:29]
	global_load_dwordx4 v[12:15], v[0:1], off nt
	v_lshl_add_u64 v[0:1], v[0:1], 0, s[28:29]
	global_load_dwordx4 v[16:19], v[0:1], off nt
	v_lshl_add_u64 v[0:1], v[0:1], 0, s[28:29]
	global_load_dwordx4 v[0:3], v[0:1], off nt
	v_mov_b32_e32 v11, v69
	v_mov_b32_e32 v99, v69
	v_mov_b32_e32 v100, v69
	v_mov_b32_e32 v101, v69
	v_mov_b32_e32 v102, v69
	v_mov_b32_e32 v103, v69
	v_mov_b32_e32 v104, v69
	v_mov_b32_e32 v105, v69
	v_mov_b32_e32 v8, v69
	v_mov_b32_e32 v9, v69
	v_mov_b32_e32 v10, v69
	v_mov_b32_e32 v98, v69
	s_ashr_i32 s23, s24, 31
	s_add_u32 s28, s7, s24
	s_addc_u32 s29, s25, s23
	s_cmpk_lt_u32 s57, 0xf97f
	s_waitcnt vmcnt(15)
	v_mul_f32_e32 v56, 0x42800000, v56
	v_mul_f32_e32 v57, 0x42800000, v57
	s_waitcnt vmcnt(14)
	v_mul_f32_e32 v60, 0x42800000, v60
	v_med3_f32 v56, v56, s67, v91
	v_mul_f32_e32 v61, 0x42800000, v61
	v_med3_f32 v60, v60, s67, v91
	v_med3_f32 v57, v57, s67, v91
	v_med3_f32 v61, v61, s67, v91
	s_waitcnt vmcnt(11)
	v_mul_f32_e32 v41, 0x42800000, v41
	v_med3_f32 v41, v41, s67, v91
	s_waitcnt vmcnt(10)
	v_mul_f32_e32 v45, 0x42800000, v45
	v_med3_f32 v45, v45, s67, v91
	v_cvt_pk_fp8_f32 v99, v41, v45
	s_waitcnt vmcnt(9)
	v_mul_f32_e32 v49, 0x42800000, v49
	v_mul_f32_e32 v40, 0x42800000, v40
	v_mul_f32_e32 v44, 0x42800000, v44
	s_waitcnt vmcnt(7)
	v_mul_f32_e32 v24, 0x42800000, v24
	v_med3_f32 v40, v40, s67, v91
	s_waitcnt vmcnt(6)
	v_mul_f32_e32 v28, 0x42800000, v28
	v_med3_f32 v44, v44, s67, v91
	v_med3_f32 v24, v24, s67, v91
	v_med3_f32 v28, v28, s67, v91
	v_cvt_pk_fp8_f32 v8, v56, v60
	v_cvt_pk_fp8_f32 v9, v40, v44
	s_waitcnt vmcnt(3)
	v_mul_f32_e32 v4, 0x42800000, v4
	v_med3_f32 v4, v4, s67, v91
	s_waitcnt vmcnt(2)
	v_mul_f32_e32 v12, 0x42800000, v12
	v_med3_f32 v12, v12, s67, v91
	v_cvt_pk_fp8_f32 v11, v4, v12
	s_waitcnt vmcnt(1)
	v_mul_f32_e32 v16, 0x42800000, v16
	s_waitcnt vmcnt(0)
	v_mul_f32_e32 v0, 0x42800000, v0
	v_med3_f32 v4, v16, s67, v91
	v_med3_f32 v0, v0, s67, v91
	v_cvt_pk_fp8_f32 v11, v4, v0 op_sel:[0,0,1]
	v_mul_f32_e32 v0, 0x42800000, v37
	v_med3_f32 v4, v49, s67, v91
	v_med3_f32 v0, v0, s67, v91
	v_cvt_pk_fp8_f32 v99, v4, v0 op_sel:[0,0,1]
	v_mul_f32_e32 v0, 0x42800000, v25
	v_mul_f32_e32 v4, 0x42800000, v29
	v_med3_f32 v0, v0, s67, v91
	v_med3_f32 v4, v4, s67, v91
	v_cvt_pk_fp8_f32 v100, v0, v4
	v_mul_f32_e32 v12, 0x42800000, v33
	v_mul_f32_e32 v0, 0x42800000, v21
	v_med3_f32 v4, v12, s67, v91
	v_med3_f32 v0, v0, s67, v91
	v_cvt_pk_fp8_f32 v100, v4, v0 op_sel:[0,0,1]
	v_mul_f32_e32 v0, 0x42800000, v5
	v_mul_f32_e32 v4, 0x42800000, v13
	v_med3_f32 v0, v0, s67, v91
	v_med3_f32 v4, v4, s67, v91
	v_cvt_pk_fp8_f32 v101, v0, v4
	v_mul_f32_e32 v5, 0x42800000, v17
	v_mul_f32_e32 v0, 0x42800000, v1
	v_med3_f32 v1, v5, s67, v91
	v_med3_f32 v0, v0, s67, v91
	v_cvt_pk_fp8_f32 v101, v1, v0 op_sel:[0,0,1]
	v_mul_f32_e32 v0, 0x42800000, v58
	v_mul_f32_e32 v1, 0x42800000, v62
	v_med3_f32 v0, v0, s67, v91
	v_med3_f32 v1, v1, s67, v91
	v_cvt_pk_fp8_f32 v102, v0, v1
	v_mul_f32_e32 v4, 0x42800000, v66
	v_mul_f32_e32 v0, 0x42800000, v54
	v_med3_f32 v1, v4, s67, v91
	v_med3_f32 v0, v0, s67, v91
	v_cvt_pk_fp8_f32 v102, v1, v0 op_sel:[0,0,1]
	v_mul_f32_e32 v0, 0x42800000, v42
	v_mul_f32_e32 v1, 0x42800000, v46
	v_med3_f32 v0, v0, s67, v91
	v_med3_f32 v1, v1, s67, v91
	v_cvt_pk_fp8_f32 v103, v0, v1
	v_mul_f32_e32 v4, 0x42800000, v50
	v_mul_f32_e32 v0, 0x42800000, v38
	v_med3_f32 v1, v4, s67, v91
	v_med3_f32 v0, v0, s67, v91
	v_cvt_pk_fp8_f32 v103, v1, v0 op_sel:[0,0,1]
	v_mul_f32_e32 v0, 0x42800000, v26
	v_mul_f32_e32 v1, 0x42800000, v30
	v_med3_f32 v0, v0, s67, v91
	v_med3_f32 v1, v1, s67, v91
	v_cvt_pk_fp8_f32 v104, v0, v1
	v_mul_f32_e32 v4, 0x42800000, v34
	v_mul_f32_e32 v0, 0x42800000, v22
	v_med3_f32 v1, v4, s67, v91
	v_med3_f32 v0, v0, s67, v91
	v_cvt_pk_fp8_f32 v104, v1, v0 op_sel:[0,0,1]
	v_mul_f32_e32 v0, 0x42800000, v6
	v_mul_f32_e32 v1, 0x42800000, v14
	v_med3_f32 v0, v0, s67, v91
	v_med3_f32 v1, v1, s67, v91
	v_cvt_pk_fp8_f32 v105, v0, v1
	v_mul_f32_e32 v4, 0x42800000, v18
	v_mul_f32_e32 v0, 0x42800000, v2
	v_med3_f32 v1, v4, s67, v91
	v_med3_f32 v0, v0, s67, v91
	v_cvt_pk_fp8_f32 v105, v1, v0 op_sel:[0,0,1]
	v_mul_f32_e32 v0, 0x42800000, v59
	v_mul_f32_e32 v1, 0x42800000, v63
	v_med3_f32 v0, v0, s67, v91
	v_med3_f32 v1, v1, s67, v91
	v_mov_b32_e32 v4, v69
	v_cvt_pk_fp8_f32 v4, v0, v1
	v_mul_f32_e32 v2, 0x42800000, v67
	v_mul_f32_e32 v0, 0x42800000, v55
	v_med3_f32 v1, v2, s67, v91
	v_med3_f32 v0, v0, s67, v91
	v_cvt_pk_fp8_f32 v4, v1, v0 op_sel:[0,0,1]
	v_mul_f32_e32 v0, 0x42800000, v43
	v_mul_f32_e32 v1, 0x42800000, v47
	v_med3_f32 v0, v0, s67, v91
	v_med3_f32 v1, v1, s67, v91
	v_mov_b32_e32 v5, v69
	v_cvt_pk_fp8_f32 v5, v0, v1
	v_mul_f32_e32 v2, 0x42800000, v51
	v_mul_f32_e32 v0, 0x42800000, v39
	v_med3_f32 v1, v2, s67, v91
	v_med3_f32 v0, v0, s67, v91
	v_cvt_pk_fp8_f32 v5, v1, v0 op_sel:[0,0,1]
	v_mul_f32_e32 v0, 0x42800000, v27
	v_mul_f32_e32 v1, 0x42800000, v31
	v_med3_f32 v0, v0, s67, v91
	v_med3_f32 v1, v1, s67, v91
	v_mov_b32_e32 v6, v69
	v_cvt_pk_fp8_f32 v6, v0, v1
	v_mul_f32_e32 v2, 0x42800000, v35
	v_mul_f32_e32 v0, 0x42800000, v23
	v_cvt_pk_fp8_f32 v10, v24, v28
	v_med3_f32 v1, v2, s67, v91
	v_med3_f32 v0, v0, s67, v91
	v_cvt_pk_fp8_f32 v98, v57, v61
	v_cvt_pk_fp8_f32 v6, v1, v0 op_sel:[0,0,1]
	v_mul_f32_e32 v0, 0x42800000, v7
	v_mul_f32_e32 v1, 0x42800000, v15
	v_mul_f32_e32 v64, 0x42800000, v64
	v_mul_f32_e32 v52, 0x42800000, v52
	v_mul_f32_e32 v48, 0x42800000, v48
	v_mul_f32_e32 v36, 0x42800000, v36
	v_mul_f32_e32 v32, 0x42800000, v32
	v_mul_f32_e32 v20, 0x42800000, v20
	v_med3_f32 v0, v0, s67, v91
	v_med3_f32 v1, v1, s67, v91
	v_mov_b32_e32 v7, v69
	v_mul_f32_e32 v65, 0x42800000, v65
	v_med3_f32 v64, v64, s67, v91
	v_mul_f32_e32 v53, 0x42800000, v53
	v_med3_f32 v52, v52, s67, v91
	v_med3_f32 v48, v48, s67, v91
	v_med3_f32 v36, v36, s67, v91
	v_med3_f32 v32, v32, s67, v91
	v_med3_f32 v20, v20, s67, v91
	v_cvt_pk_fp8_f32 v7, v0, v1
	v_med3_f32 v56, v65, s67, v91
	v_med3_f32 v53, v53, s67, v91
	v_cvt_pk_fp8_f32 v8, v64, v52 op_sel:[0,0,1]
	v_cvt_pk_fp8_f32 v9, v48, v36 op_sel:[0,0,1]
	v_cvt_pk_fp8_f32 v10, v32, v20 op_sel:[0,0,1]
	v_cvt_pk_fp8_f32 v98, v56, v53 op_sel:[0,0,1]
	v_mul_f32_e32 v2, 0x42800000, v19
	v_mul_f32_e32 v0, 0x42800000, v3
	v_med3_f32 v1, v2, s67, v91
	v_med3_f32 v0, v0, s67, v91
	v_cvt_pk_fp8_f32 v7, v1, v0 op_sel:[0,0,1]
	ds_write_b128 v88, v[8:11] offset:40960
	ds_write_b128 v88, v[98:101] offset:41040
	ds_write_b128 v88, v[102:105] offset:41120
	ds_write_b128 v88, v[4:7] offset:41200
	s_waitcnt lgkmcnt(0)
	ds_read_b128 v[0:3], v89 offset:40960
	v_or_b32_e32 v4, s17, v76
	v_ashrrev_i32_e32 v5, 31, v4
	v_lshl_add_u64 v[8:9], s[28:29], 0, v[70:71]
	v_lshlrev_b64 v[4:5], 11, v[4:5]
	v_lshl_add_u64 v[10:11], v[8:9], 0, v[4:5]
	ds_read_b128 v[4:7], v89 offset:42240
	s_waitcnt lgkmcnt(1)
	global_store_dwordx4 v[10:11], v[0:3], off sc1
	s_cselect_b64 s[28:29], -1, 0
	s_nop 0
	v_or_b32_e32 v0, s17, v77
	v_ashrrev_i32_e32 v1, 31, v0
	v_lshlrev_b64 v[0:1], 11, v[0:1]
	v_lshl_add_u64 v[0:1], v[8:9], 0, v[0:1]
	s_waitcnt lgkmcnt(0)
	global_store_dwordx4 v[0:1], v[4:7], off sc1
	ds_read_b128 v[0:3], v89 offset:43520
	s_nop 0
	v_or_b32_e32 v4, s17, v78
	v_ashrrev_i32_e32 v5, 31, v4
	v_lshlrev_b64 v[4:5], 11, v[4:5]
	v_lshl_add_u64 v[10:11], v[8:9], 0, v[4:5]
	ds_read_b128 v[4:7], v89 offset:44800
	s_waitcnt lgkmcnt(1)
	global_store_dwordx4 v[10:11], v[0:3], off sc1
	s_nop 1
	v_or_b32_e32 v0, s17, v79
	v_ashrrev_i32_e32 v1, 31, v0
	v_lshlrev_b64 v[0:1], 11, v[0:1]
	v_lshl_add_u64 v[0:1], v[8:9], 0, v[0:1]
	s_waitcnt lgkmcnt(0)
	global_store_dwordx4 v[0:1], v[4:7], off sc1
	s_waitcnt lgkmcnt(0)
	s_andn2_b64 vcc, exec, s[28:29]
	s_cbranch_vccz .LBB0_1459
	s_branch .LBB0_1483

.LBB0_1459:
	s_andn2_b64 vcc, exec, s[26:27]
	s_cbranch_vccnz .LBB0_1461
	s_ashr_i32 s7, s6, 31
	s_lshl_b64 s[26:27], s[6:7], 22
	s_add_u32 s7, s55, s26
	s_addc_u32 s23, s56, s27
	v_or_b32_e32 v0, s24, v75
	s_add_u32 s7, s7, s20
	v_mul_hi_i32_i24_e32 v1, s18, v0
	v_mul_i32_i24_e32 v0, s18, v0
	s_addc_u32 s25, s23, s21
	v_lshl_add_u64 v[0:1], v[0:1], 2, s[8:9]
	s_ashr_i32 s23, s22, 31
	v_lshl_add_u64 v[0:1], s[22:23], 2, v[0:1]
	v_mov_b32_e32 v73, v69
	v_lshl_add_u64 v[0:1], v[0:1], 0, v[72:73]
	s_lshl_b64 s[26:27], s[18:19], 2
	global_load_dwordx4 v[56:59], v[0:1], off nt
	v_lshl_add_u64 v[0:1], v[0:1], 0, s[26:27]
	global_load_dwordx4 v[60:63], v[0:1], off nt
	v_lshl_add_u64 v[0:1], v[0:1], 0, s[26:27]
	global_load_dwordx4 v[64:67], v[0:1], off nt
	v_lshl_add_u64 v[0:1], v[0:1], 0, s[26:27]
	global_load_dwordx4 v[52:55], v[0:1], off nt
	v_lshl_add_u64 v[0:1], v[0:1], 0, s[26:27]
	global_load_dwordx4 v[40:43], v[0:1], off nt
	v_lshl_add_u64 v[0:1], v[0:1], 0, s[26:27]
	global_load_dwordx4 v[44:47], v[0:1], off nt
	v_lshl_add_u64 v[0:1], v[0:1], 0, s[26:27]
	global_load_dwordx4 v[48:51], v[0:1], off nt
	v_lshl_add_u64 v[0:1], v[0:1], 0, s[26:27]
	global_load_dwordx4 v[36:39], v[0:1], off nt
	v_lshl_add_u64 v[0:1], v[0:1], 0, s[26:27]
	global_load_dwordx4 v[24:27], v[0:1], off nt
	v_lshl_add_u64 v[0:1], v[0:1], 0, s[26:27]
	global_load_dwordx4 v[28:31], v[0:1], off nt
	v_lshl_add_u64 v[0:1], v[0:1], 0, s[26:27]
	global_load_dwordx4 v[32:35], v[0:1], off nt
	v_lshl_add_u64 v[0:1], v[0:1], 0, s[26:27]
	global_load_dwordx4 v[20:23], v[0:1], off nt
	v_lshl_add_u64 v[0:1], v[0:1], 0, s[26:27]
	global_load_dwordx4 v[4:7], v[0:1], off nt
	v_lshl_add_u64 v[0:1], v[0:1], 0, s[26:27]
	global_load_dwordx4 v[12:15], v[0:1], off nt
	v_lshl_add_u64 v[0:1], v[0:1], 0, s[26:27]
	global_load_dwordx4 v[16:19], v[0:1], off nt
	v_lshl_add_u64 v[0:1], v[0:1], 0, s[26:27]
	global_load_dwordx4 v[0:3], v[0:1], off nt
	v_mov_b32_e32 v11, v69
	v_mov_b32_e32 v99, v69
	v_mov_b32_e32 v100, v69
	v_mov_b32_e32 v101, v69
	v_mov_b32_e32 v102, v69
	v_mov_b32_e32 v103, v69
	v_mov_b32_e32 v104, v69
	v_mov_b32_e32 v105, v69
	v_mov_b32_e32 v8, v69
	v_mov_b32_e32 v9, v69
	v_mov_b32_e32 v10, v69
	v_mov_b32_e32 v98, v69
	s_ashr_i32 s23, s24, 31
	s_add_u32 s26, s7, s24
	s_addc_u32 s27, s25, s23
	s_cmpk_lt_u32 s57, 0xf97f
	s_waitcnt vmcnt(15)
	v_mul_f32_e32 v56, 0x42800000, v56
	v_mul_f32_e32 v57, 0x42800000, v57
	s_waitcnt vmcnt(14)
	v_mul_f32_e32 v60, 0x42800000, v60
	v_med3_f32 v56, v56, s67, v91
	v_mul_f32_e32 v61, 0x42800000, v61
	v_med3_f32 v60, v60, s67, v91
	v_med3_f32 v57, v57, s67, v91
	v_med3_f32 v61, v61, s67, v91
	s_waitcnt vmcnt(11)
	v_mul_f32_e32 v41, 0x42800000, v41
	v_med3_f32 v41, v41, s67, v91
	s_waitcnt vmcnt(10)
	v_mul_f32_e32 v45, 0x42800000, v45
	v_med3_f32 v45, v45, s67, v91
	v_cvt_pk_fp8_f32 v99, v41, v45
	s_waitcnt vmcnt(9)
	v_mul_f32_e32 v49, 0x42800000, v49
	v_mul_f32_e32 v40, 0x42800000, v40
	v_mul_f32_e32 v44, 0x42800000, v44
	s_waitcnt vmcnt(7)
	v_mul_f32_e32 v24, 0x42800000, v24
	v_med3_f32 v40, v40, s67, v91
	s_waitcnt vmcnt(6)
	v_mul_f32_e32 v28, 0x42800000, v28
	v_med3_f32 v44, v44, s67, v91
	v_med3_f32 v24, v24, s67, v91
	v_med3_f32 v28, v28, s67, v91
	v_cvt_pk_fp8_f32 v8, v56, v60
	v_cvt_pk_fp8_f32 v9, v40, v44
	s_waitcnt vmcnt(3)
	v_mul_f32_e32 v4, 0x42800000, v4
	v_med3_f32 v4, v4, s67, v91
	s_waitcnt vmcnt(2)
	v_mul_f32_e32 v12, 0x42800000, v12
	v_med3_f32 v12, v12, s67, v91
	v_cvt_pk_fp8_f32 v11, v4, v12
	s_waitcnt vmcnt(1)
	v_mul_f32_e32 v16, 0x42800000, v16
	s_waitcnt vmcnt(0)
	v_mul_f32_e32 v0, 0x42800000, v0
	v_med3_f32 v4, v16, s67, v91
	v_med3_f32 v0, v0, s67, v91
	v_cvt_pk_fp8_f32 v11, v4, v0 op_sel:[0,0,1]
	v_mul_f32_e32 v0, 0x42800000, v37
	v_med3_f32 v4, v49, s67, v91
	v_med3_f32 v0, v0, s67, v91
	v_cvt_pk_fp8_f32 v99, v4, v0 op_sel:[0,0,1]
	v_mul_f32_e32 v0, 0x42800000, v25
	v_mul_f32_e32 v4, 0x42800000, v29
	v_med3_f32 v0, v0, s67, v91
	v_med3_f32 v4, v4, s67, v91
	v_cvt_pk_fp8_f32 v100, v0, v4
	v_mul_f32_e32 v12, 0x42800000, v33
	v_mul_f32_e32 v0, 0x42800000, v21
	v_med3_f32 v4, v12, s67, v91
	v_med3_f32 v0, v0, s67, v91
	v_cvt_pk_fp8_f32 v100, v4, v0 op_sel:[0,0,1]
	v_mul_f32_e32 v0, 0x42800000, v5
	v_mul_f32_e32 v4, 0x42800000, v13
	v_med3_f32 v0, v0, s67, v91
	v_med3_f32 v4, v4, s67, v91
	v_cvt_pk_fp8_f32 v101, v0, v4
	v_mul_f32_e32 v5, 0x42800000, v17
	v_mul_f32_e32 v0, 0x42800000, v1
	v_med3_f32 v1, v5, s67, v91
	v_med3_f32 v0, v0, s67, v91
	v_cvt_pk_fp8_f32 v101, v1, v0 op_sel:[0,0,1]
	v_mul_f32_e32 v0, 0x42800000, v58
	v_mul_f32_e32 v1, 0x42800000, v62
	v_med3_f32 v0, v0, s67, v91
	v_med3_f32 v1, v1, s67, v91
	v_cvt_pk_fp8_f32 v102, v0, v1
	v_mul_f32_e32 v4, 0x42800000, v66
	v_mul_f32_e32 v0, 0x42800000, v54
	v_med3_f32 v1, v4, s67, v91
	v_med3_f32 v0, v0, s67, v91
	v_cvt_pk_fp8_f32 v102, v1, v0 op_sel:[0,0,1]
	v_mul_f32_e32 v0, 0x42800000, v42
	v_mul_f32_e32 v1, 0x42800000, v46
	v_med3_f32 v0, v0, s67, v91
	v_med3_f32 v1, v1, s67, v91
	v_cvt_pk_fp8_f32 v103, v0, v1
	v_mul_f32_e32 v4, 0x42800000, v50
	v_mul_f32_e32 v0, 0x42800000, v38
	v_med3_f32 v1, v4, s67, v91
	v_med3_f32 v0, v0, s67, v91
	v_cvt_pk_fp8_f32 v103, v1, v0 op_sel:[0,0,1]
	v_mul_f32_e32 v0, 0x42800000, v26
	v_mul_f32_e32 v1, 0x42800000, v30
	v_med3_f32 v0, v0, s67, v91
	v_med3_f32 v1, v1, s67, v91
	v_cvt_pk_fp8_f32 v104, v0, v1
	v_mul_f32_e32 v4, 0x42800000, v34
	v_mul_f32_e32 v0, 0x42800000, v22
	v_med3_f32 v1, v4, s67, v91
	v_med3_f32 v0, v0, s67, v91
	v_cvt_pk_fp8_f32 v104, v1, v0 op_sel:[0,0,1]
	v_mul_f32_e32 v0, 0x42800000, v6
	v_mul_f32_e32 v1, 0x42800000, v14
	v_med3_f32 v0, v0, s67, v91
	v_med3_f32 v1, v1, s67, v91
	v_cvt_pk_fp8_f32 v105, v0, v1
	v_mul_f32_e32 v4, 0x42800000, v18
	v_mul_f32_e32 v0, 0x42800000, v2
	v_med3_f32 v1, v4, s67, v91
	v_med3_f32 v0, v0, s67, v91
	v_cvt_pk_fp8_f32 v105, v1, v0 op_sel:[0,0,1]
	v_mul_f32_e32 v0, 0x42800000, v59
	v_mul_f32_e32 v1, 0x42800000, v63
	v_med3_f32 v0, v0, s67, v91
	v_med3_f32 v1, v1, s67, v91
	v_mov_b32_e32 v4, v69
	v_cvt_pk_fp8_f32 v4, v0, v1
	v_mul_f32_e32 v2, 0x42800000, v67
	v_mul_f32_e32 v0, 0x42800000, v55
	v_med3_f32 v1, v2, s67, v91
	v_med3_f32 v0, v0, s67, v91
	v_cvt_pk_fp8_f32 v4, v1, v0 op_sel:[0,0,1]
	v_mul_f32_e32 v0, 0x42800000, v43
	v_mul_f32_e32 v1, 0x42800000, v47
	v_med3_f32 v0, v0, s67, v91
	v_med3_f32 v1, v1, s67, v91
	v_mov_b32_e32 v5, v69
	v_cvt_pk_fp8_f32 v5, v0, v1
	v_mul_f32_e32 v2, 0x42800000, v51
	v_mul_f32_e32 v0, 0x42800000, v39
	v_med3_f32 v1, v2, s67, v91
	v_med3_f32 v0, v0, s67, v91
	v_cvt_pk_fp8_f32 v5, v1, v0 op_sel:[0,0,1]
	v_mul_f32_e32 v0, 0x42800000, v27
	v_mul_f32_e32 v1, 0x42800000, v31
	v_med3_f32 v0, v0, s67, v91
	v_med3_f32 v1, v1, s67, v91
	v_mov_b32_e32 v6, v69
	v_cvt_pk_fp8_f32 v6, v0, v1
	v_mul_f32_e32 v2, 0x42800000, v35
	v_mul_f32_e32 v0, 0x42800000, v23
	v_cvt_pk_fp8_f32 v10, v24, v28
	v_med3_f32 v1, v2, s67, v91
	v_med3_f32 v0, v0, s67, v91
	v_cvt_pk_fp8_f32 v98, v57, v61
	v_cvt_pk_fp8_f32 v6, v1, v0 op_sel:[0,0,1]
	v_mul_f32_e32 v0, 0x42800000, v7
	v_mul_f32_e32 v1, 0x42800000, v15
	v_mul_f32_e32 v64, 0x42800000, v64
	v_mul_f32_e32 v52, 0x42800000, v52
	v_mul_f32_e32 v48, 0x42800000, v48
	v_mul_f32_e32 v36, 0x42800000, v36
	v_mul_f32_e32 v32, 0x42800000, v32
	v_mul_f32_e32 v20, 0x42800000, v20
	v_med3_f32 v0, v0, s67, v91
	v_med3_f32 v1, v1, s67, v91
	v_mov_b32_e32 v7, v69
	v_mul_f32_e32 v65, 0x42800000, v65
	v_med3_f32 v64, v64, s67, v91
	v_mul_f32_e32 v53, 0x42800000, v53
	v_med3_f32 v52, v52, s67, v91
	v_med3_f32 v48, v48, s67, v91
	v_med3_f32 v36, v36, s67, v91
	v_med3_f32 v32, v32, s67, v91
	v_med3_f32 v20, v20, s67, v91
	v_cvt_pk_fp8_f32 v7, v0, v1
	v_med3_f32 v56, v65, s67, v91
	v_med3_f32 v53, v53, s67, v91
	v_cvt_pk_fp8_f32 v8, v64, v52 op_sel:[0,0,1]
	v_cvt_pk_fp8_f32 v9, v48, v36 op_sel:[0,0,1]
	v_cvt_pk_fp8_f32 v10, v32, v20 op_sel:[0,0,1]
	v_cvt_pk_fp8_f32 v98, v56, v53 op_sel:[0,0,1]
	v_mul_f32_e32 v2, 0x42800000, v19
	v_mul_f32_e32 v0, 0x42800000, v3
	v_med3_f32 v1, v2, s67, v91
	v_med3_f32 v0, v0, s67, v91
	v_cvt_pk_fp8_f32 v7, v1, v0 op_sel:[0,0,1]
	ds_write_b128 v88, v[8:11] offset:40960
	ds_write_b128 v88, v[98:101] offset:41040
	ds_write_b128 v88, v[102:105] offset:41120
	ds_write_b128 v88, v[4:7] offset:41200
	s_waitcnt lgkmcnt(0)
	ds_read_b128 v[0:3], v89 offset:40960
	v_or_b32_e32 v4, s17, v76
	v_ashrrev_i32_e32 v5, 31, v4
	v_lshl_add_u64 v[8:9], s[26:27], 0, v[70:71]
	v_lshlrev_b64 v[4:5], 11, v[4:5]
	v_lshl_add_u64 v[10:11], v[8:9], 0, v[4:5]
	ds_read_b128 v[4:7], v89 offset:42240
	s_waitcnt lgkmcnt(1)
	global_store_dwordx4 v[10:11], v[0:3], off sc1
	s_cselect_b64 s[26:27], -1, 0
	s_nop 0
	v_or_b32_e32 v0, s17, v77
	v_ashrrev_i32_e32 v1, 31, v0
	v_lshlrev_b64 v[0:1], 11, v[0:1]
	v_lshl_add_u64 v[0:1], v[8:9], 0, v[0:1]
	s_waitcnt lgkmcnt(0)
	global_store_dwordx4 v[0:1], v[4:7], off sc1
	ds_read_b128 v[0:3], v89 offset:43520
	s_nop 0
	v_or_b32_e32 v4, s17, v78
	v_ashrrev_i32_e32 v5, 31, v4
	v_lshlrev_b64 v[4:5], 11, v[4:5]
	v_lshl_add_u64 v[10:11], v[8:9], 0, v[4:5]
	ds_read_b128 v[4:7], v89 offset:44800
	s_waitcnt lgkmcnt(1)
	global_store_dwordx4 v[10:11], v[0:3], off sc1
	s_nop 1
	v_or_b32_e32 v0, s17, v79
	v_ashrrev_i32_e32 v1, 31, v0
	v_lshlrev_b64 v[0:1], 11, v[0:1]
	v_lshl_add_u64 v[0:1], v[8:9], 0, v[0:1]
	s_waitcnt lgkmcnt(0)
	global_store_dwordx4 v[0:1], v[4:7], off sc1
	s_waitcnt lgkmcnt(0)
	s_andn2_b64 vcc, exec, s[26:27]
	s_cbranch_vccz .LBB0_1462
	s_branch .LBB0_1483

.LBB0_1466:
	s_lshl_b64 s[20:21], s[20:21], 1
	s_add_u32 s7, s12, s20
	s_addc_u32 s20, s13, s21
	s_ashr_i32 s25, s24, 31
	s_lshl_b64 s[12:13], s[24:25], 1
	s_waitcnt lgkmcnt(0)
	s_add_u32 s12, s7, s12
	s_addc_u32 s13, s20, s13
	v_or_b32_e32 v0, s17, v80
	v_lshl_add_u64 v[4:5], s[12:13], 0, v[68:69]
	s_mov_b64 s[12:13], -1
	s_and_b64 vcc, exec, s[26:27]
	v_mul_hi_i32_i24_e32 v7, s16, v0
	v_mul_i32_i24_e32 v6, s16, v0
	s_cbranch_vccz .LBB0_1468
	v_lshl_add_u64 v[0:1], v[6:7], 1, v[4:5]
	global_store_dwordx4 v[0:1], v[94:97], off sc1
	s_mov_b64 s[12:13], 0
.LBB0_1468:
	v_mov_b32_e32 v0, 0
	s_andn2_b64 vcc, exec, s[12:13]
	v_mov_b32_e32 v1, 0
	v_mov_b32_e32 v2, 0
	v_mov_b32_e32 v3, 0
	s_cbranch_vccnz .LBB0_1470
	ds_read_b128 v[8:11], v92 offset:40960
	ds_read_b128 v[0:3], v92 offset:42112
	v_lshl_add_u64 v[6:7], v[6:7], 1, v[4:5]
	s_waitcnt lgkmcnt(1)
	global_store_dwordx4 v[6:7], v[8:11], off sc1
.LBB0_1470:
	v_or_b32_e32 v6, s17, v81
	v_mul_hi_i32_i24_e32 v7, s16, v6
	v_mul_i32_i24_e32 v6, s16, v6
	v_lshl_add_u64 v[6:7], v[6:7], 1, v[4:5]
	s_waitcnt lgkmcnt(0)
	global_store_dwordx4 v[6:7], v[0:3], off sc1
	s_mov_b64 s[12:13], -1
	s_and_b64 vcc, exec, s[26:27]
	v_or_b32_e32 v0, s17, v82
	v_mul_hi_i32_i24_e32 v7, s16, v0
	v_mul_i32_i24_e32 v6, s16, v0
	s_cbranch_vccz .LBB0_1472
	v_lshl_add_u64 v[0:1], v[6:7], 1, v[4:5]
	global_store_dwordx4 v[0:1], v[94:97], off sc1
	s_mov_b64 s[12:13], 0
.LBB0_1472:
	v_mov_b32_e32 v0, 0
	s_andn2_b64 vcc, exec, s[12:13]
	v_mov_b32_e32 v1, 0
	v_mov_b32_e32 v2, 0
	v_mov_b32_e32 v3, 0
	s_cbranch_vccnz .LBB0_1474
	ds_read_b128 v[8:11], v92 offset:43264
	ds_read_b128 v[0:3], v92 offset:44416
	v_lshl_add_u64 v[6:7], v[6:7], 1, v[4:5]
	s_waitcnt lgkmcnt(1)
	global_store_dwordx4 v[6:7], v[8:11], off sc1
.LBB0_1474:
	v_or_b32_e32 v6, s17, v83
	v_mul_hi_i32_i24_e32 v7, s16, v6
	v_mul_i32_i24_e32 v6, s16, v6
	v_lshl_add_u64 v[6:7], v[6:7], 1, v[4:5]
	s_waitcnt lgkmcnt(0)
	global_store_dwordx4 v[6:7], v[0:3], off sc1
	s_mov_b64 s[12:13], -1
	s_and_b64 vcc, exec, s[26:27]
	v_or_b32_e32 v0, s17, v84
	v_mul_hi_i32_i24_e32 v7, s16, v0
	v_mul_i32_i24_e32 v6, s16, v0
	s_cbranch_vccz .LBB0_1476
	v_lshl_add_u64 v[0:1], v[6:7], 1, v[4:5]
	global_store_dwordx4 v[0:1], v[94:97], off sc1
	s_mov_b64 s[12:13], 0
.LBB0_1476:
	v_mov_b32_e32 v0, 0
	s_andn2_b64 vcc, exec, s[12:13]
	v_mov_b32_e32 v1, 0
	v_mov_b32_e32 v2, 0
	v_mov_b32_e32 v3, 0
	s_cbranch_vccnz .LBB0_1478
	ds_read_b128 v[8:11], v92 offset:45568
	ds_read_b128 v[0:3], v92 offset:46720
	v_lshl_add_u64 v[6:7], v[6:7], 1, v[4:5]
	s_waitcnt lgkmcnt(1)
	global_store_dwordx4 v[6:7], v[8:11], off sc1
.LBB0_1478:
	v_or_b32_e32 v6, s17, v85
	v_mul_hi_i32_i24_e32 v7, s16, v6
	v_mul_i32_i24_e32 v6, s16, v6
	v_lshl_add_u64 v[6:7], v[6:7], 1, v[4:5]
	s_waitcnt lgkmcnt(0)
	global_store_dwordx4 v[6:7], v[0:3], off sc1
	s_mov_b64 s[12:13], -1
	s_and_b64 vcc, exec, s[26:27]
	v_or_b32_e32 v0, s17, v86
	v_mul_hi_i32_i24_e32 v7, s16, v0
	v_mul_i32_i24_e32 v6, s16, v0
	s_cbranch_vccz .LBB0_1480
	v_lshl_add_u64 v[0:1], v[6:7], 1, v[4:5]
	global_store_dwordx4 v[0:1], v[94:97], off sc1
	s_mov_b64 s[12:13], 0
.LBB0_1480:
	v_mov_b32_e32 v0, 0
	s_andn2_b64 vcc, exec, s[12:13]
	v_mov_b32_e32 v1, 0
	v_mov_b32_e32 v2, 0
	v_mov_b32_e32 v3, 0
	s_cbranch_vccnz .LBB0_1482
	ds_read_b128 v[8:11], v92 offset:47872
	ds_read_b128 v[0:3], v92 offset:49024
	v_lshl_add_u64 v[6:7], v[6:7], 1, v[4:5]
	s_waitcnt lgkmcnt(1)
	global_store_dwordx4 v[6:7], v[8:11], off sc1
.LBB0_1482:
	v_or_b32_e32 v6, s17, v87
	v_mul_hi_i32_i24_e32 v7, s16, v6
	v_mul_i32_i24_e32 v6, s16, v6
	v_lshl_add_u64 v[4:5], v[6:7], 1, v[4:5]
	s_waitcnt lgkmcnt(0)
	global_store_dwordx4 v[4:5], v[0:3], off sc1
	s_waitcnt lgkmcnt(0)

.LBB0_1680:
	ds_read_b128 v[12:15], v176
	ds_read_b128 v[16:19], v176 offset:1024
	ds_read_b128 v[28:31], v176 offset:2048
	ds_read_b128 v[32:35], v176 offset:3072
	s_add_u32 s18, s29, s57
	v_cmp_lt_i64_e32 vcc, s[6:7], v[144:145]
	s_addc_u32 s19, s30, 0
	s_and_b64 s[2:3], vcc, exec
	s_cselect_b32 s25, s19, s23
	s_cselect_b32 s24, s18, s22
	s_add_u32 s20, s31, s58
	s_addc_u32 s21, s38, 0
	s_and_b64 s[2:3], vcc, exec
	s_cselect_b32 s3, s21, s27
	s_cselect_b32 s2, s20, s26
	s_add_u32 s62, s22, 0x20080
	s_addc_u32 s63, s23, 0
	s_add_i32 s67, s40, 0xc000
	v_lshl_add_u64 v[44:45], s[62:63], 0, v[136:137]
	s_mov_b32 m0, s67
	s_add_i32 s61, s40, 0xe000
	ds_read_b128 v[4:7], v177
	ds_read_b128 v[8:11], v177 offset:1024
	ds_read_b128 v[20:23], v177 offset:2048
	ds_read_b128 v[24:27], v177 offset:3072
	ds_read_b128 v[36:39], v177 offset:4096
	ds_read_b128 v[40:43], v177 offset:5120
	ds_read_b128 v[52:55], v177 offset:6144
	ds_read_b128 v[56:59], v177 offset:7168
	global_load_lds_dwordx4 v[44:45], off
	v_lshl_add_u64 v[44:45], s[62:63], 0, v[140:141]
	s_mov_b32 m0, s61
	s_nop 0
	global_load_lds_dwordx4 v[44:45], off
	s_waitcnt lgkmcnt(8)
	s_barrier
	s_waitcnt lgkmcnt(0)
	s_setprio 1
	v_mov_b64_e32 v[110:111], v[2:3]
	v_mov_b64_e32 v[114:115], v[2:3]
	v_mov_b64_e32 v[106:107], v[2:3]
	v_mov_b64_e32 v[102:103], v[2:3]
	v_mov_b64_e32 v[82:83], v[2:3]
	v_mov_b64_e32 v[78:79], v[2:3]
	v_mov_b64_e32 v[50:51], v[2:3]
	v_mov_b64_e32 v[46:47], v[2:3]
	v_mov_b64_e32 v[108:109], v[0:1]
	v_mov_b64_e32 v[112:113], v[0:1]
	v_mov_b64_e32 v[104:105], v[0:1]
	v_mov_b64_e32 v[100:101], v[0:1]
	v_mov_b64_e32 v[80:81], v[0:1]
	v_mov_b64_e32 v[76:77], v[0:1]
	v_mov_b64_e32 v[48:49], v[0:1]
	v_mov_b64_e32 v[44:45], v[0:1]
	s_waitcnt lgkmcnt(0)
	v_mfma_scale_f32_16x16x128_f8f6f4 v[108:111], v[12:19], v[4:11], v[108:111], v171, v171 op_sel_hi:[0,0,0]
	v_mfma_scale_f32_16x16x128_f8f6f4 v[112:115], v[28:35], v[4:11], v[112:115], v171, v171 op_sel_hi:[0,0,0]
	v_mfma_scale_f32_16x16x128_f8f6f4 v[104:107], v[12:19], v[20:27], v[104:107], v171, v171 op_sel_hi:[0,0,0]
	v_mfma_scale_f32_16x16x128_f8f6f4 v[100:103], v[28:35], v[20:27], v[100:103], v171, v171 op_sel_hi:[0,0,0]
	v_mfma_scale_f32_16x16x128_f8f6f4 v[80:83], v[12:19], v[36:43], v[80:83], v171, v171 op_sel_hi:[0,0,0]
	v_mfma_scale_f32_16x16x128_f8f6f4 v[76:79], v[28:35], v[36:43], v[76:79], v171, v171 op_sel_hi:[0,0,0]
	v_mfma_scale_f32_16x16x128_f8f6f4 v[48:51], v[12:19], v[52:59], v[48:51], v171, v171 op_sel_hi:[0,0,0]
	v_mfma_scale_f32_16x16x128_f8f6f4 v[44:47], v[28:35], v[52:59], v[44:47], v171, v171 op_sel_hi:[0,0,0]
	s_setprio 0
	s_barrier
	v_lshl_add_u64 v[132:133], s[26:27], 0, v[138:139]
	s_add_i32 s64, s50, s39
	v_lshl_add_u64 v[60:61], v[132:133], 0, s[10:11]
	s_mov_b32 m0, s64
	v_lshl_add_u64 v[134:135], s[26:27], 0, v[142:143]
	s_add_i32 s62, s64, 0x2000
	ds_read_b128 v[154:157], v178
	ds_read_b128 v[158:161], v178 offset:1024
	ds_read_b128 v[180:183], v178 offset:2048
	ds_read_b128 v[184:187], v178 offset:3072
	global_load_lds_dwordx4 v[60:61], off
	v_lshl_add_u64 v[60:61], v[134:135], 0, s[10:11]
	s_mov_b32 m0, s62
	s_nop 0
	global_load_lds_dwordx4 v[60:61], off
	s_barrier
	s_waitcnt lgkmcnt(0)
	s_setprio 1
	v_mov_b64_e32 v[126:127], v[2:3]
	v_mov_b64_e32 v[130:131], v[2:3]
	v_mov_b64_e32 v[122:123], v[2:3]
	v_mov_b64_e32 v[118:119], v[2:3]
	v_mov_b64_e32 v[98:99], v[2:3]
	v_mov_b64_e32 v[94:95], v[2:3]
	v_mov_b64_e32 v[66:67], v[2:3]
	v_mov_b64_e32 v[62:63], v[2:3]
	v_mov_b64_e32 v[124:125], v[0:1]
	v_mov_b64_e32 v[128:129], v[0:1]
	v_mov_b64_e32 v[120:121], v[0:1]
	v_mov_b64_e32 v[116:117], v[0:1]
	v_mov_b64_e32 v[96:97], v[0:1]
	v_mov_b64_e32 v[92:93], v[0:1]
	v_mov_b64_e32 v[64:65], v[0:1]
	v_mov_b64_e32 v[60:61], v[0:1]
	s_waitcnt lgkmcnt(0)
	v_mfma_scale_f32_16x16x128_f8f6f4 v[124:127], v[154:161], v[4:11], v[124:127], v171, v171 op_sel_hi:[0,0,0]
	v_mfma_scale_f32_16x16x128_f8f6f4 v[128:131], v[180:187], v[4:11], v[128:131], v171, v171 op_sel_hi:[0,0,0]
	v_mfma_scale_f32_16x16x128_f8f6f4 v[120:123], v[154:161], v[20:27], v[120:123], v171, v171 op_sel_hi:[0,0,0]
	v_mfma_scale_f32_16x16x128_f8f6f4 v[116:119], v[180:187], v[20:27], v[116:119], v171, v171 op_sel_hi:[0,0,0]
	v_mfma_scale_f32_16x16x128_f8f6f4 v[96:99], v[154:161], v[36:43], v[96:99], v171, v171 op_sel_hi:[0,0,0]
	v_mfma_scale_f32_16x16x128_f8f6f4 v[92:95], v[180:187], v[36:43], v[92:95], v171, v171 op_sel_hi:[0,0,0]
	v_mfma_scale_f32_16x16x128_f8f6f4 v[64:67], v[154:161], v[52:59], v[64:67], v171, v171 op_sel_hi:[0,0,0]
	v_mfma_scale_f32_16x16x128_f8f6f4 v[60:63], v[180:187], v[52:59], v[60:63], v171, v171 op_sel_hi:[0,0,0]
	s_setprio 0
	v_lshl_add_u64 v[150:151], s[22:23], 0, v[136:137]
	s_mov_b32 m0, s40
	v_lshl_add_u64 v[4:5], v[150:151], 0, s[10:11]
	v_lshl_add_u64 v[152:153], s[22:23], 0, v[140:141]
	s_barrier
	ds_read_b128 v[52:55], v177 offset:16384
	ds_read_b128 v[56:59], v177 offset:17408
	ds_read_b128 v[188:191], v177 offset:18432
	ds_read_b128 v[192:195], v177 offset:19456
	ds_read_b128 v[196:199], v177 offset:20480
	ds_read_b128 v[200:203], v177 offset:21504
	ds_read_b128 v[204:207], v177 offset:22528
	ds_read_b128 v[208:211], v177 offset:23552
	global_load_lds_dwordx4 v[4:5], off
	v_lshl_add_u64 v[4:5], v[152:153], 0, s[10:11]
	s_mov_b32 m0, s41
	s_nop 0
	global_load_lds_dwordx4 v[4:5], off
	s_barrier
	s_waitcnt lgkmcnt(0)
	s_setprio 1
	v_mov_b64_e32 v[74:75], v[2:3]
	v_mov_b64_e32 v[70:71], v[2:3]
	v_mov_b64_e32 v[42:43], v[2:3]
	v_mov_b64_e32 v[38:39], v[2:3]
	v_mov_b64_e32 v[26:27], v[2:3]
	v_mov_b64_e32 v[22:23], v[2:3]
	v_mov_b64_e32 v[10:11], v[2:3]
	v_mov_b64_e32 v[6:7], v[2:3]
	v_mov_b64_e32 v[72:73], v[0:1]
	v_mov_b64_e32 v[68:69], v[0:1]
	v_mov_b64_e32 v[40:41], v[0:1]
	v_mov_b64_e32 v[36:37], v[0:1]
	v_mov_b64_e32 v[24:25], v[0:1]
	v_mov_b64_e32 v[20:21], v[0:1]
	v_mov_b64_e32 v[8:9], v[0:1]
	v_mov_b64_e32 v[4:5], v[0:1]
	s_waitcnt lgkmcnt(0)
	v_mfma_scale_f32_16x16x128_f8f6f4 v[72:75], v[12:19], v[52:59], v[72:75], v171, v171 op_sel_hi:[0,0,0]
	v_mfma_scale_f32_16x16x128_f8f6f4 v[68:71], v[28:35], v[52:59], v[68:71], v171, v171 op_sel_hi:[0,0,0]
	v_mfma_scale_f32_16x16x128_f8f6f4 v[40:43], v[12:19], v[188:195], v[40:43], v171, v171 op_sel_hi:[0,0,0]
	v_mfma_scale_f32_16x16x128_f8f6f4 v[36:39], v[28:35], v[188:195], v[36:39], v171, v171 op_sel_hi:[0,0,0]
	v_mfma_scale_f32_16x16x128_f8f6f4 v[24:27], v[12:19], v[196:203], v[24:27], v171, v171 op_sel_hi:[0,0,0]
	v_mfma_scale_f32_16x16x128_f8f6f4 v[20:23], v[28:35], v[196:203], v[20:23], v171, v171 op_sel_hi:[0,0,0]
	v_mfma_scale_f32_16x16x128_f8f6f4 v[8:11], v[12:19], v[204:211], v[8:11], v171, v171 op_sel_hi:[0,0,0]
	v_mfma_scale_f32_16x16x128_f8f6f4 v[4:7], v[28:35], v[204:211], v[4:7], v171, v171 op_sel_hi:[0,0,0]
	s_setprio 0
	s_barrier
	s_add_u32 s68, s26, 0x10100
	s_addc_u32 s69, s27, 0
	s_add_i32 s65, s51, s39
	v_lshl_add_u64 v[12:13], s[68:69], 0, v[138:139]
	s_mov_b32 m0, s65
	s_add_i32 s63, s65, 0x2000
	global_load_lds_dwordx4 v[12:13], off
	v_lshl_add_u64 v[12:13], s[68:69], 0, v[142:143]
	s_mov_b32 m0, s63
	s_nop 0
	global_load_lds_dwordx4 v[12:13], off
	s_waitcnt vmcnt(6)
	s_barrier
	s_setprio 1
	v_mov_b64_e32 v[90:91], v[2:3]
	v_mov_b64_e32 v[86:87], v[2:3]
	v_mov_b64_e32 v[88:89], v[0:1]
	v_mov_b64_e32 v[84:85], v[0:1]
	v_mfma_scale_f32_16x16x128_f8f6f4 v[88:91], v[154:161], v[52:59], v[88:91], v171, v171 op_sel_hi:[0,0,0]
	v_mfma_scale_f32_16x16x128_f8f6f4 v[84:87], v[180:187], v[52:59], v[84:87], v171, v171 op_sel_hi:[0,0,0]
	v_mov_b64_e32 v[58:59], v[2:3]
	v_mov_b64_e32 v[54:55], v[2:3]
	v_mov_b64_e32 v[34:35], v[2:3]
	v_mov_b64_e32 v[30:31], v[2:3]
	v_mov_b64_e32 v[18:19], v[2:3]
	v_mov_b64_e32 v[14:15], v[2:3]
	v_mov_b64_e32 v[56:57], v[0:1]
	v_mov_b64_e32 v[52:53], v[0:1]
	v_mov_b64_e32 v[32:33], v[0:1]
	v_mov_b64_e32 v[28:29], v[0:1]
	v_mov_b64_e32 v[16:17], v[0:1]
	v_mov_b64_e32 v[12:13], v[0:1]
	v_mfma_scale_f32_16x16x128_f8f6f4 v[56:59], v[154:161], v[188:195], v[56:59], v171, v171 op_sel_hi:[0,0,0]
	v_mfma_scale_f32_16x16x128_f8f6f4 v[52:55], v[180:187], v[188:195], v[52:55], v171, v171 op_sel_hi:[0,0,0]
	v_mfma_scale_f32_16x16x128_f8f6f4 v[32:35], v[154:161], v[196:203], v[32:35], v171, v171 op_sel_hi:[0,0,0]
	v_mfma_scale_f32_16x16x128_f8f6f4 v[28:31], v[180:187], v[196:203], v[28:31], v171, v171 op_sel_hi:[0,0,0]
	v_mfma_scale_f32_16x16x128_f8f6f4 v[16:19], v[154:161], v[204:211], v[16:19], v171, v171 op_sel_hi:[0,0,0]
	v_mfma_scale_f32_16x16x128_f8f6f4 v[12:15], v[180:187], v[204:211], v[12:15], v171, v171 op_sel_hi:[0,0,0]
	s_setprio 0
	s_add_i32 s66, 0, 0x18000
	v_add_u32_e32 v154, s66, v174
	s_barrier
	ds_read_b128 v[156:159], v154
	ds_read_b128 v[160:163], v154 offset:1024
	ds_read_b128 v[180:183], v154 offset:2048
	ds_read_b128 v[184:187], v154 offset:3072
	s_add_u32 s68, s22, 0x20100
	s_addc_u32 s69, s23, 0
	s_mov_b32 m0, s42
	v_lshl_add_u64 v[164:165], s[68:69], 0, v[136:137]
	ds_read_b128 v[188:191], v177 offset:32768
	ds_read_b128 v[192:195], v177 offset:33792
	ds_read_b128 v[196:199], v177 offset:34816
	ds_read_b128 v[200:203], v177 offset:35840
	ds_read_b128 v[204:207], v177 offset:36864
	ds_read_b128 v[208:211], v177 offset:37888
	ds_read_b128 v[212:215], v177 offset:38912
	ds_read_b128 v[216:219], v177 offset:39936
	global_load_lds_dwordx4 v[164:165], off
	v_lshl_add_u64 v[164:165], s[68:69], 0, v[140:141]
	s_mov_b32 m0, s43
	s_nop 0
	global_load_lds_dwordx4 v[164:165], off
	s_waitcnt lgkmcnt(8)
	s_barrier
	s_waitcnt lgkmcnt(0)
	s_setprio 1
	s_waitcnt lgkmcnt(0)
	v_mfma_scale_f32_16x16x128_f8f6f4 v[108:111], v[156:163], v[188:195], v[108:111], v171, v171 op_sel_hi:[0,0,0]
	v_mfma_scale_f32_16x16x128_f8f6f4 v[112:115], v[180:187], v[188:195], v[112:115], v171, v171 op_sel_hi:[0,0,0]
	v_mfma_scale_f32_16x16x128_f8f6f4 v[104:107], v[156:163], v[196:203], v[104:107], v171, v171 op_sel_hi:[0,0,0]
	v_mfma_scale_f32_16x16x128_f8f6f4 v[100:103], v[180:187], v[196:203], v[100:103], v171, v171 op_sel_hi:[0,0,0]
	v_mfma_scale_f32_16x16x128_f8f6f4 v[80:83], v[156:163], v[204:211], v[80:83], v171, v171 op_sel_hi:[0,0,0]
	v_mfma_scale_f32_16x16x128_f8f6f4 v[76:79], v[180:187], v[204:211], v[76:79], v171, v171 op_sel_hi:[0,0,0]
	v_mfma_scale_f32_16x16x128_f8f6f4 v[48:51], v[156:163], v[212:219], v[48:51], v171, v171 op_sel_hi:[0,0,0]
	v_mfma_scale_f32_16x16x128_f8f6f4 v[44:47], v[180:187], v[212:219], v[44:47], v171, v171 op_sel_hi:[0,0,0]
	s_setprio 0
	s_barrier
	s_add_i32 s69, 0, 0x1c000
	s_add_i32 s68, s66, s39
	v_add_u32_e32 v155, s69, v174
	v_lshl_add_u64 v[132:133], v[132:133], 0, s[12:13]
	s_mov_b32 m0, s68
	s_add_i32 s66, s68, 0x2000
	ds_read_b128 v[224:227], v155
	ds_read_b128 v[228:231], v155 offset:1024
	ds_read_b128 v[232:235], v155 offset:2048
	ds_read_b128 v[236:239], v155 offset:3072
	global_load_lds_dwordx4 v[132:133], off
	v_lshl_add_u64 v[132:133], v[134:135], 0, s[12:13]
	s_mov_b32 m0, s66
	s_nop 0
	global_load_lds_dwordx4 v[132:133], off
	s_barrier
	s_waitcnt lgkmcnt(0)
	s_setprio 1
	s_waitcnt lgkmcnt(0)
	v_mfma_scale_f32_16x16x128_f8f6f4 v[124:127], v[224:231], v[188:195], v[124:127], v171, v171 op_sel_hi:[0,0,0]
	v_mfma_scale_f32_16x16x128_f8f6f4 v[128:131], v[232:239], v[188:195], v[128:131], v171, v171 op_sel_hi:[0,0,0]
	v_mfma_scale_f32_16x16x128_f8f6f4 v[120:123], v[224:231], v[196:203], v[120:123], v171, v171 op_sel_hi:[0,0,0]
	v_mfma_scale_f32_16x16x128_f8f6f4 v[116:119], v[232:239], v[196:203], v[116:119], v171, v171 op_sel_hi:[0,0,0]
	v_mfma_scale_f32_16x16x128_f8f6f4 v[96:99], v[224:231], v[204:211], v[96:99], v171, v171 op_sel_hi:[0,0,0]
	v_mfma_scale_f32_16x16x128_f8f6f4 v[92:95], v[232:239], v[204:211], v[92:95], v171, v171 op_sel_hi:[0,0,0]
	v_mfma_scale_f32_16x16x128_f8f6f4 v[64:67], v[224:231], v[212:219], v[64:67], v171, v171 op_sel_hi:[0,0,0]
	v_mfma_scale_f32_16x16x128_f8f6f4 v[60:63], v[232:239], v[212:219], v[60:63], v171, v171 op_sel_hi:[0,0,0]
	s_setprio 0
	s_mov_b32 m0, s46
	v_lshl_add_u64 v[132:133], v[150:151], 0, s[12:13]
	s_barrier
	ds_read_b128 v[188:191], v177 offset:49152
	ds_read_b128 v[192:195], v177 offset:50176
	ds_read_b128 v[196:199], v177 offset:51200
	ds_read_b128 v[200:203], v177 offset:52224
	ds_read_b128 v[204:207], v177 offset:53248
	ds_read_b128 v[208:211], v177 offset:54272
	ds_read_b128 v[212:215], v177 offset:55296
	ds_read_b128 v[216:219], v177 offset:56320
	global_load_lds_dwordx4 v[132:133], off
	v_lshl_add_u64 v[132:133], v[152:153], 0, s[12:13]
	s_mov_b32 m0, s47
	s_nop 0
	global_load_lds_dwordx4 v[132:133], off
	s_barrier
	s_waitcnt lgkmcnt(0)
	s_setprio 1
	s_waitcnt lgkmcnt(0)
	v_mfma_scale_f32_16x16x128_f8f6f4 v[72:75], v[156:163], v[188:195], v[72:75], v171, v171 op_sel_hi:[0,0,0]
	v_mfma_scale_f32_16x16x128_f8f6f4 v[68:71], v[180:187], v[188:195], v[68:71], v171, v171 op_sel_hi:[0,0,0]
	v_mfma_scale_f32_16x16x128_f8f6f4 v[40:43], v[156:163], v[196:203], v[40:43], v171, v171 op_sel_hi:[0,0,0]
	v_mfma_scale_f32_16x16x128_f8f6f4 v[36:39], v[180:187], v[196:203], v[36:39], v171, v171 op_sel_hi:[0,0,0]
	v_mfma_scale_f32_16x16x128_f8f6f4 v[24:27], v[156:163], v[204:211], v[24:27], v171, v171 op_sel_hi:[0,0,0]
	v_mfma_scale_f32_16x16x128_f8f6f4 v[20:23], v[180:187], v[204:211], v[20:23], v171, v171 op_sel_hi:[0,0,0]
	v_mfma_scale_f32_16x16x128_f8f6f4 v[8:11], v[156:163], v[212:219], v[8:11], v171, v171 op_sel_hi:[0,0,0]
	v_mfma_scale_f32_16x16x128_f8f6f4 v[4:7], v[180:187], v[212:219], v[4:7], v171, v171 op_sel_hi:[0,0,0]
	s_setprio 0
	s_barrier
	s_add_u32 s70, s26, 0x10180
	s_addc_u32 s71, s27, 0
	s_add_i32 s27, s69, s39
	v_lshl_add_u64 v[132:133], s[70:71], 0, v[138:139]
	s_mov_b32 m0, s27
	s_add_i32 s26, s27, 0x2000
	global_load_lds_dwordx4 v[132:133], off
	v_lshl_add_u64 v[132:133], s[70:71], 0, v[142:143]
	s_mov_b32 m0, s26
	s_nop 0
	global_load_lds_dwordx4 v[132:133], off
	s_waitcnt vmcnt(6)
	s_barrier
	s_setprio 1
	v_mfma_scale_f32_16x16x128_f8f6f4 v[88:91], v[224:231], v[188:195], v[88:91], v171, v171 op_sel_hi:[0,0,0]
	v_mfma_scale_f32_16x16x128_f8f6f4 v[84:87], v[232:239], v[188:195], v[84:87], v171, v171 op_sel_hi:[0,0,0]
	v_mfma_scale_f32_16x16x128_f8f6f4 v[56:59], v[224:231], v[196:203], v[56:59], v171, v171 op_sel_hi:[0,0,0]
	v_mfma_scale_f32_16x16x128_f8f6f4 v[52:55], v[232:239], v[196:203], v[52:55], v171, v171 op_sel_hi:[0,0,0]
	v_mfma_scale_f32_16x16x128_f8f6f4 v[32:35], v[224:231], v[204:211], v[32:35], v171, v171 op_sel_hi:[0,0,0]
	v_mfma_scale_f32_16x16x128_f8f6f4 v[28:31], v[232:239], v[204:211], v[28:31], v171, v171 op_sel_hi:[0,0,0]
	v_mfma_scale_f32_16x16x128_f8f6f4 v[16:19], v[224:231], v[212:219], v[16:19], v171, v171 op_sel_hi:[0,0,0]
	v_mfma_scale_f32_16x16x128_f8f6f4 v[12:15], v[232:239], v[212:219], v[12:15], v171, v171 op_sel_hi:[0,0,0]
	s_setprio 0
	s_barrier
	ds_read_b128 v[156:159], v176
	ds_read_b128 v[160:163], v176 offset:1024
	ds_read_b128 v[180:183], v176 offset:2048
	ds_read_b128 v[184:187], v176 offset:3072
	s_add_u32 s22, s22, 0x20180
	s_addc_u32 s23, s23, 0
	s_mov_b32 m0, s67
	v_lshl_add_u64 v[132:133], s[22:23], 0, v[136:137]
	ds_read_b128 v[188:191], v177
	ds_read_b128 v[192:195], v177 offset:1024
	ds_read_b128 v[196:199], v177 offset:2048
	ds_read_b128 v[200:203], v177 offset:3072
	ds_read_b128 v[204:207], v177 offset:4096
	ds_read_b128 v[208:211], v177 offset:5120
	ds_read_b128 v[212:215], v177 offset:6144
	ds_read_b128 v[216:219], v177 offset:7168
	global_load_lds_dwordx4 v[132:133], off
	v_lshl_add_u64 v[132:133], s[22:23], 0, v[140:141]
	s_mov_b32 m0, s61
	s_nop 0
	global_load_lds_dwordx4 v[132:133], off
	s_waitcnt lgkmcnt(8)
	s_barrier
	s_waitcnt lgkmcnt(0)
	s_setprio 1
	s_waitcnt lgkmcnt(0)
	v_mfma_scale_f32_16x16x128_f8f6f4 v[108:111], v[156:163], v[188:195], v[108:111], v171, v171 op_sel_hi:[0,0,0]
	v_mfma_scale_f32_16x16x128_f8f6f4 v[112:115], v[180:187], v[188:195], v[112:115], v171, v171 op_sel_hi:[0,0,0]
	v_mfma_scale_f32_16x16x128_f8f6f4 v[104:107], v[156:163], v[196:203], v[104:107], v171, v171 op_sel_hi:[0,0,0]
	v_mfma_scale_f32_16x16x128_f8f6f4 v[100:103], v[180:187], v[196:203], v[100:103], v171, v171 op_sel_hi:[0,0,0]
	v_mfma_scale_f32_16x16x128_f8f6f4 v[80:83], v[156:163], v[204:211], v[80:83], v171, v171 op_sel_hi:[0,0,0]
	v_mfma_scale_f32_16x16x128_f8f6f4 v[76:79], v[180:187], v[204:211], v[76:79], v171, v171 op_sel_hi:[0,0,0]
	v_mfma_scale_f32_16x16x128_f8f6f4 v[48:51], v[156:163], v[212:219], v[48:51], v171, v171 op_sel_hi:[0,0,0]
	v_mfma_scale_f32_16x16x128_f8f6f4 v[44:47], v[180:187], v[212:219], v[44:47], v171, v171 op_sel_hi:[0,0,0]
	s_setprio 0
	s_barrier
	s_mov_b32 m0, s64
	v_lshl_add_u64 v[132:133], s[2:3], 0, v[138:139]
	ds_read_b128 v[224:227], v178
	ds_read_b128 v[228:231], v178 offset:1024
	ds_read_b128 v[232:235], v178 offset:2048
	ds_read_b128 v[236:239], v178 offset:3072
	global_load_lds_dwordx4 v[132:133], off
	v_lshl_add_u64 v[134:135], s[2:3], 0, v[142:143]
	s_mov_b32 m0, s62
	s_nop 0
	global_load_lds_dwordx4 v[134:135], off
	s_barrier
	s_waitcnt lgkmcnt(0)
	s_setprio 1
	s_waitcnt lgkmcnt(0)
	v_mfma_scale_f32_16x16x128_f8f6f4 v[124:127], v[224:231], v[188:195], v[124:127], v171, v171 op_sel_hi:[0,0,0]
	v_mfma_scale_f32_16x16x128_f8f6f4 v[128:131], v[232:239], v[188:195], v[128:131], v171, v171 op_sel_hi:[0,0,0]
	v_mfma_scale_f32_16x16x128_f8f6f4 v[120:123], v[224:231], v[196:203], v[120:123], v171, v171 op_sel_hi:[0,0,0]
	v_mfma_scale_f32_16x16x128_f8f6f4 v[116:119], v[232:239], v[196:203], v[116:119], v171, v171 op_sel_hi:[0,0,0]
	v_mfma_scale_f32_16x16x128_f8f6f4 v[96:99], v[224:231], v[204:211], v[96:99], v171, v171 op_sel_hi:[0,0,0]
	v_mfma_scale_f32_16x16x128_f8f6f4 v[92:95], v[232:239], v[204:211], v[92:95], v171, v171 op_sel_hi:[0,0,0]
	v_mfma_scale_f32_16x16x128_f8f6f4 v[64:67], v[224:231], v[212:219], v[64:67], v171, v171 op_sel_hi:[0,0,0]
	v_mfma_scale_f32_16x16x128_f8f6f4 v[60:63], v[232:239], v[212:219], v[60:63], v171, v171 op_sel_hi:[0,0,0]
	s_setprio 0
	s_mov_b32 m0, s40
	v_lshl_add_u64 v[150:151], s[24:25], 0, v[136:137]
	s_barrier
	ds_read_b128 v[188:191], v177 offset:16384
	ds_read_b128 v[192:195], v177 offset:17408
	ds_read_b128 v[196:199], v177 offset:18432
	ds_read_b128 v[200:203], v177 offset:19456
	ds_read_b128 v[204:207], v177 offset:20480
	ds_read_b128 v[208:211], v177 offset:21504
	ds_read_b128 v[212:215], v177 offset:22528
	ds_read_b128 v[216:219], v177 offset:23552
	global_load_lds_dwordx4 v[150:151], off
	v_lshl_add_u64 v[152:153], s[24:25], 0, v[140:141]
	s_mov_b32 m0, s41
	s_nop 0
	global_load_lds_dwordx4 v[152:153], off
	s_barrier
	s_waitcnt lgkmcnt(0)
	s_setprio 1
	s_waitcnt lgkmcnt(0)
	v_mfma_scale_f32_16x16x128_f8f6f4 v[72:75], v[156:163], v[188:195], v[72:75], v171, v171 op_sel_hi:[0,0,0]
	v_mfma_scale_f32_16x16x128_f8f6f4 v[68:71], v[180:187], v[188:195], v[68:71], v171, v171 op_sel_hi:[0,0,0]
	v_mfma_scale_f32_16x16x128_f8f6f4 v[40:43], v[156:163], v[196:203], v[40:43], v171, v171 op_sel_hi:[0,0,0]
	v_mfma_scale_f32_16x16x128_f8f6f4 v[36:39], v[180:187], v[196:203], v[36:39], v171, v171 op_sel_hi:[0,0,0]
	v_mfma_scale_f32_16x16x128_f8f6f4 v[24:27], v[156:163], v[204:211], v[24:27], v171, v171 op_sel_hi:[0,0,0]
	v_mfma_scale_f32_16x16x128_f8f6f4 v[20:23], v[180:187], v[204:211], v[20:23], v171, v171 op_sel_hi:[0,0,0]
	v_mfma_scale_f32_16x16x128_f8f6f4 v[8:11], v[156:163], v[212:219], v[8:11], v171, v171 op_sel_hi:[0,0,0]
	v_mfma_scale_f32_16x16x128_f8f6f4 v[4:7], v[180:187], v[212:219], v[4:7], v171, v171 op_sel_hi:[0,0,0]
	s_setprio 0
	s_barrier
	s_add_u32 s22, s2, 0x10000
	s_addc_u32 s23, s3, 0
	s_mov_b32 m0, s65
	v_lshl_add_u64 v[156:157], s[22:23], 0, v[138:139]
	global_load_lds_dwordx4 v[156:157], off
	v_lshl_add_u64 v[156:157], s[22:23], 0, v[142:143]
	s_mov_b32 m0, s63
	s_nop 0
	global_load_lds_dwordx4 v[156:157], off
	s_waitcnt vmcnt(6)
	s_barrier
	s_setprio 1
	v_mfma_scale_f32_16x16x128_f8f6f4 v[88:91], v[224:231], v[188:195], v[88:91], v171, v171 op_sel_hi:[0,0,0]
	v_mfma_scale_f32_16x16x128_f8f6f4 v[84:87], v[232:239], v[188:195], v[84:87], v171, v171 op_sel_hi:[0,0,0]
	v_mfma_scale_f32_16x16x128_f8f6f4 v[56:59], v[224:231], v[196:203], v[56:59], v171, v171 op_sel_hi:[0,0,0]
	v_mfma_scale_f32_16x16x128_f8f6f4 v[52:55], v[232:239], v[196:203], v[52:55], v171, v171 op_sel_hi:[0,0,0]
	v_mfma_scale_f32_16x16x128_f8f6f4 v[32:35], v[224:231], v[204:211], v[32:35], v171, v171 op_sel_hi:[0,0,0]
	v_mfma_scale_f32_16x16x128_f8f6f4 v[28:31], v[232:239], v[204:211], v[28:31], v171, v171 op_sel_hi:[0,0,0]
	v_mfma_scale_f32_16x16x128_f8f6f4 v[16:19], v[224:231], v[212:219], v[16:19], v171, v171 op_sel_hi:[0,0,0]
	v_mfma_scale_f32_16x16x128_f8f6f4 v[12:15], v[232:239], v[212:219], v[12:15], v171, v171 op_sel_hi:[0,0,0]
	s_setprio 0
	s_barrier
	ds_read_b128 v[156:159], v154
	ds_read_b128 v[160:163], v154 offset:1024
	ds_read_b128 v[180:183], v154 offset:2048
	ds_read_b128 v[184:187], v154 offset:3072
	s_add_u32 s22, s24, 0x20000
	s_addc_u32 s23, s25, 0
	s_mov_b32 m0, s42
	v_lshl_add_u64 v[164:165], s[22:23], 0, v[136:137]
	ds_read_b128 v[188:191], v177 offset:32768
	ds_read_b128 v[192:195], v177 offset:33792
	ds_read_b128 v[196:199], v177 offset:34816
	ds_read_b128 v[200:203], v177 offset:35840
	ds_read_b128 v[204:207], v177 offset:36864
	ds_read_b128 v[208:211], v177 offset:37888
	ds_read_b128 v[212:215], v177 offset:38912
	ds_read_b128 v[216:219], v177 offset:39936
	global_load_lds_dwordx4 v[164:165], off
	v_lshl_add_u64 v[164:165], s[22:23], 0, v[140:141]
	s_mov_b32 m0, s43
	s_nop 0
	global_load_lds_dwordx4 v[164:165], off
	s_waitcnt lgkmcnt(8)
	s_barrier
	s_waitcnt lgkmcnt(0)
	s_setprio 1
	s_waitcnt lgkmcnt(0)
	v_mfma_scale_f32_16x16x128_f8f6f4 v[108:111], v[156:163], v[188:195], v[108:111], v171, v171 op_sel_hi:[0,0,0]
	v_mfma_scale_f32_16x16x128_f8f6f4 v[112:115], v[180:187], v[188:195], v[112:115], v171, v171 op_sel_hi:[0,0,0]
	v_mfma_scale_f32_16x16x128_f8f6f4 v[104:107], v[156:163], v[196:203], v[104:107], v171, v171 op_sel_hi:[0,0,0]
	v_mfma_scale_f32_16x16x128_f8f6f4 v[100:103], v[180:187], v[196:203], v[100:103], v171, v171 op_sel_hi:[0,0,0]
	v_mfma_scale_f32_16x16x128_f8f6f4 v[80:83], v[156:163], v[204:211], v[80:83], v171, v171 op_sel_hi:[0,0,0]
	v_mfma_scale_f32_16x16x128_f8f6f4 v[76:79], v[180:187], v[204:211], v[76:79], v171, v171 op_sel_hi:[0,0,0]
	v_mfma_scale_f32_16x16x128_f8f6f4 v[48:51], v[156:163], v[212:219], v[48:51], v171, v171 op_sel_hi:[0,0,0]
	v_mfma_scale_f32_16x16x128_f8f6f4 v[44:47], v[180:187], v[212:219], v[44:47], v171, v171 op_sel_hi:[0,0,0]
	s_setprio 0
	s_barrier
	s_mov_b32 m0, s68
	v_lshl_add_u64 v[132:133], v[132:133], 0, s[8:9]
	ds_read_b128 v[224:227], v155
	ds_read_b128 v[228:231], v155 offset:1024
	ds_read_b128 v[232:235], v155 offset:2048
	ds_read_b128 v[236:239], v155 offset:3072
	global_load_lds_dwordx4 v[132:133], off
	v_lshl_add_u64 v[132:133], v[134:135], 0, s[8:9]
	s_mov_b32 m0, s66
	s_nop 0
	global_load_lds_dwordx4 v[132:133], off
	s_barrier
	s_waitcnt lgkmcnt(0)
	s_setprio 1
	s_waitcnt lgkmcnt(0)
	v_mfma_scale_f32_16x16x128_f8f6f4 v[124:127], v[224:231], v[188:195], v[124:127], v171, v171 op_sel_hi:[0,0,0]
	v_mfma_scale_f32_16x16x128_f8f6f4 v[128:131], v[232:239], v[188:195], v[128:131], v171, v171 op_sel_hi:[0,0,0]
	v_mfma_scale_f32_16x16x128_f8f6f4 v[120:123], v[224:231], v[196:203], v[120:123], v171, v171 op_sel_hi:[0,0,0]
	v_mfma_scale_f32_16x16x128_f8f6f4 v[116:119], v[232:239], v[196:203], v[116:119], v171, v171 op_sel_hi:[0,0,0]
	v_mfma_scale_f32_16x16x128_f8f6f4 v[96:99], v[224:231], v[204:211], v[96:99], v171, v171 op_sel_hi:[0,0,0]
	v_mfma_scale_f32_16x16x128_f8f6f4 v[92:95], v[232:239], v[204:211], v[92:95], v171, v171 op_sel_hi:[0,0,0]
	v_mfma_scale_f32_16x16x128_f8f6f4 v[64:67], v[224:231], v[212:219], v[64:67], v171, v171 op_sel_hi:[0,0,0]
	v_mfma_scale_f32_16x16x128_f8f6f4 v[60:63], v[232:239], v[212:219], v[60:63], v171, v171 op_sel_hi:[0,0,0]
	s_setprio 0
	s_mov_b32 m0, s46
	v_lshl_add_u64 v[132:133], v[150:151], 0, s[8:9]
	s_barrier
	ds_read_b128 v[188:191], v177 offset:49152
	ds_read_b128 v[192:195], v177 offset:50176
	ds_read_b128 v[196:199], v177 offset:51200
	ds_read_b128 v[200:203], v177 offset:52224
	ds_read_b128 v[204:207], v177 offset:53248
	ds_read_b128 v[208:211], v177 offset:54272
	ds_read_b128 v[212:215], v177 offset:55296
	ds_read_b128 v[216:219], v177 offset:56320
	global_load_lds_dwordx4 v[132:133], off
	v_lshl_add_u64 v[132:133], v[152:153], 0, s[8:9]
	s_mov_b32 m0, s47
	s_nop 0
	global_load_lds_dwordx4 v[132:133], off
	s_barrier
	s_waitcnt lgkmcnt(0)
	s_setprio 1
	s_waitcnt lgkmcnt(0)
	v_mfma_scale_f32_16x16x128_f8f6f4 v[72:75], v[156:163], v[188:195], v[72:75], v171, v171 op_sel_hi:[0,0,0]
	v_mfma_scale_f32_16x16x128_f8f6f4 v[68:71], v[180:187], v[188:195], v[68:71], v171, v171 op_sel_hi:[0,0,0]
	v_mfma_scale_f32_16x16x128_f8f6f4 v[40:43], v[156:163], v[196:203], v[40:43], v171, v171 op_sel_hi:[0,0,0]
	v_mfma_scale_f32_16x16x128_f8f6f4 v[36:39], v[180:187], v[196:203], v[36:39], v171, v171 op_sel_hi:[0,0,0]
	v_mfma_scale_f32_16x16x128_f8f6f4 v[24:27], v[156:163], v[204:211], v[24:27], v171, v171 op_sel_hi:[0,0,0]
	v_mfma_scale_f32_16x16x128_f8f6f4 v[20:23], v[180:187], v[204:211], v[20:23], v171, v171 op_sel_hi:[0,0,0]
	v_mfma_scale_f32_16x16x128_f8f6f4 v[8:11], v[156:163], v[212:219], v[8:11], v171, v171 op_sel_hi:[0,0,0]
	v_mfma_scale_f32_16x16x128_f8f6f4 v[4:7], v[180:187], v[212:219], v[4:7], v171, v171 op_sel_hi:[0,0,0]
	s_setprio 0
	s_barrier
	s_add_u32 s2, s2, 0x10080
	s_addc_u32 s3, s3, 0
	s_mov_b32 m0, s27
	v_lshl_add_u64 v[132:133], s[2:3], 0, v[138:139]
	global_load_lds_dwordx4 v[132:133], off
	v_lshl_add_u64 v[132:133], s[2:3], 0, v[142:143]
	s_mov_b32 m0, s26
	s_nop 0
	global_load_lds_dwordx4 v[132:133], off
	s_waitcnt vmcnt(6)
	s_barrier
	s_setprio 1
	v_mfma_scale_f32_16x16x128_f8f6f4 v[88:91], v[224:231], v[188:195], v[88:91], v171, v171 op_sel_hi:[0,0,0]
	v_mfma_scale_f32_16x16x128_f8f6f4 v[84:87], v[232:239], v[188:195], v[84:87], v171, v171 op_sel_hi:[0,0,0]
	v_mfma_scale_f32_16x16x128_f8f6f4 v[56:59], v[224:231], v[196:203], v[56:59], v171, v171 op_sel_hi:[0,0,0]
	v_mfma_scale_f32_16x16x128_f8f6f4 v[52:55], v[232:239], v[196:203], v[52:55], v171, v171 op_sel_hi:[0,0,0]
	v_mfma_scale_f32_16x16x128_f8f6f4 v[32:35], v[224:231], v[204:211], v[32:35], v171, v171 op_sel_hi:[0,0,0]
	v_mfma_scale_f32_16x16x128_f8f6f4 v[28:31], v[232:239], v[204:211], v[28:31], v171, v171 op_sel_hi:[0,0,0]
	v_mfma_scale_f32_16x16x128_f8f6f4 v[16:19], v[224:231], v[212:219], v[16:19], v171, v171 op_sel_hi:[0,0,0]
	v_mfma_scale_f32_16x16x128_f8f6f4 v[12:15], v[232:239], v[212:219], v[12:15], v171, v171 op_sel_hi:[0,0,0]
	s_setprio 0
	v_lshl_add_u32 v164, s60, 8, v173
	s_cmp_lt_i32 s59, 6
	s_cselect_b32 s2, 0, 32
	v_or_b32_e32 v162, 16, v164
	s_cselect_b32 s24, s52, 0x47b1c000
	s_cselect_b32 s22, s53, 0x800
	s_cselect_b32 s23, 0, -6
	s_add_u32 s2, s44, s2
	v_ashrrev_i32_e32 v165, 31, v164
	v_ashrrev_i32_e32 v163, 31, v162
	s_addc_u32 s3, s45, 0
	v_lshlrev_b64 v[132:133], 6, v[164:165]
	v_lshlrev_b64 v[150:151], 6, v[162:163]
	s_barrier
	s_nop 7
	s_nop 7
	s_nop 7
	v_lshl_add_u64 v[132:133], s[2:3], 0, v[132:133]
	v_lshl_add_u64 v[150:151], s[2:3], 0, v[150:151]
	global_load_dwordx4 v[180:183], v[132:133], off
	s_nop 0
	global_load_dwordx4 v[132:135], v[132:133], off offset:16
	s_nop 0
	global_load_dwordx4 v[184:187], v[150:151], off
	global_load_dwordx4 v[188:191], v[150:151], off offset:16
	v_or_b32_e32 v160, 32, v164
	v_ashrrev_i32_e32 v161, 31, v160
	v_lshlrev_b64 v[150:151], 6, v[160:161]
	v_or_b32_e32 v158, 48, v164
	v_lshl_add_u64 v[150:151], s[2:3], 0, v[150:151]
	v_ashrrev_i32_e32 v159, 31, v158
	global_load_dwordx4 v[192:195], v[150:151], off
	global_load_dwordx4 v[196:199], v[150:151], off offset:16
	v_lshlrev_b64 v[150:151], 6, v[158:159]
	v_lshl_add_u64 v[150:151], s[2:3], 0, v[150:151]
	global_load_dwordx4 v[200:203], v[150:151], off
	global_load_dwordx4 v[204:207], v[150:151], off offset:16
	v_add_u32_e32 v156, 0x80, v164
	v_add_u32_e32 v150, 0xb0, v164
	v_add_u32_e32 v154, 0x90, v164
	v_add_u32_e32 v152, 0xa0, v164
	v_ashrrev_i32_e32 v157, 31, v156
	v_ashrrev_i32_e32 v151, 31, v150
	v_ashrrev_i32_e32 v155, 31, v154
	v_ashrrev_i32_e32 v153, 31, v152
	v_lshlrev_b64 v[208:209], 6, v[156:157]
	v_lshlrev_b64 v[214:215], 6, v[150:151]
	v_lshlrev_b64 v[210:211], 6, v[154:155]
	v_lshlrev_b64 v[212:213], 6, v[152:153]
	v_lshl_add_u64 v[216:217], s[2:3], 0, v[208:209]
	v_lshl_add_u64 v[240:241], s[2:3], 0, v[214:215]
	v_lshl_add_u64 v[220:221], s[2:3], 0, v[210:211]
	v_lshl_add_u64 v[222:223], s[2:3], 0, v[212:213]
	global_load_dwordx4 v[208:211], v[216:217], off
	global_load_dwordx4 v[212:215], v[216:217], off offset:16
	s_nop 0
	global_load_dwordx4 v[216:219], v[220:221], off
	global_load_dwordx4 v[224:227], v[220:221], off offset:16
	global_load_dwordx4 v[228:231], v[222:223], off
	global_load_dwordx4 v[232:235], v[222:223], off offset:16
	global_load_dwordx4 v[236:239], v[240:241], off
	s_nop 0
	global_load_dwordx4 v[240:243], v[240:241], off offset:16
	s_mov_b32 s60, s56
	s_mov_b64 s[26:27], s[20:21]
	s_waitcnt vmcnt(0)
	v_mov_b32_e32 v220, v180
	v_mov_b32_e32 v221, v132
	v_mov_b32_e32 v132, v181
	v_mov_b32_e32 v180, v182
	v_mov_b32_e32 v181, v134
	v_mov_b32_e32 v134, v183
	v_mov_b32_e32 v182, v184
	v_mov_b32_e32 v183, v188
	v_mov_b32_e32 v188, v185
	v_mov_b32_e32 v184, v186
	v_mov_b32_e32 v185, v190
	v_mov_b32_e32 v190, v187
	v_pk_add_f32 v[132:133], v[220:221], v[132:133]
	v_pk_add_f32 v[134:135], v[180:181], v[134:135]
	v_pk_add_f32 v[180:181], v[182:183], v[188:189]
	v_pk_add_f32 v[182:183], v[184:185], v[190:191]
	v_pk_add_f32 v[132:133], v[132:133], v[134:135]
	v_pk_add_f32 v[134:135], v[180:181], v[182:183]
	v_mov_b32_e32 v181, v132
	v_mov_b32_e32 v180, v134
	v_mov_b32_e32 v132, v135
	v_pk_add_f32 v[132:133], v[180:181], v[132:133]
	v_mov_b32_e32 v186, v192
	v_pk_fma_f32 v[132:133], v[132:133], s[16:17], v[148:149] op_sel_hi:[1,0,0]
	v_mov_b32_e32 v187, v196
	v_mul_f32_e32 v134, 0x4b800000, v133
	v_mul_f32_e32 v135, 0x4b800000, v132
	v_cmp_gt_f32_e32 vcc, s54, v133
	v_cmp_gt_f32_e64 s[2:3], s54, v132
	v_mov_b32_e32 v196, v193
	v_cndmask_b32_e32 v133, v133, v134, vcc
	v_cndmask_b32_e64 v132, v132, v135, s[2:3]
	v_rsq_f32_e32 v134, v133
	v_rsq_f32_e32 v135, v132
	v_mov_b32_e32 v192, v194
	v_mov_b32_e32 v193, v198
	v_mul_f32_e32 v151, 0x45800000, v134
	v_mul_f32_e32 v153, 0x45800000, v135
	v_cndmask_b32_e32 v134, v134, v151, vcc
	v_cndmask_b32_e64 v135, v135, v153, s[2:3]
	v_mov_b32_e32 v198, v195
	v_pk_add_f32 v[132:133], v[186:187], v[196:197]
	v_mul_f32_e32 v180, 0x3c800000, v134
	v_mul_f32_e32 v182, 0x3c800000, v135
	v_pk_add_f32 v[134:135], v[192:193], v[198:199]
	v_mov_b32_e32 v184, v202
	v_pk_add_f32 v[132:133], v[132:133], v[134:135]
	v_mov_b32_e32 v134, v200
	v_mov_b32_e32 v135, v204
	v_mov_b32_e32 v204, v201
	v_mov_b32_e32 v185, v206
	v_mov_b32_e32 v206, v203
	v_pk_add_f32 v[134:135], v[134:135], v[204:205]
	v_pk_add_f32 v[184:185], v[184:185], v[206:207]
	v_mov_b32_e32 v186, v218
	v_pk_add_f32 v[134:135], v[134:135], v[184:185]
	v_mov_b32_e32 v185, v132
	v_mov_b32_e32 v184, v134
	v_mov_b32_e32 v132, v135
	v_pk_add_f32 v[132:133], v[184:185], v[132:133]
	v_mov_b32_e32 v135, v214
	v_pk_fma_f32 v[132:133], v[132:133], s[16:17], v[148:149] op_sel_hi:[1,0,0]
	v_mov_b32_e32 v214, v211
	v_mul_f32_e32 v134, 0x4b800000, v133
	v_cmp_gt_f32_e32 vcc, s54, v133
	v_cmp_gt_f32_e64 s[2:3], s54, v132
	v_mov_b32_e32 v187, v226
	v_cndmask_b32_e32 v133, v133, v134, vcc
	v_rsq_f32_e32 v133, v133
	v_mul_f32_e32 v134, 0x4b800000, v132
	v_cndmask_b32_e64 v132, v132, v134, s[2:3]
	v_rsq_f32_e32 v132, v132
	v_mul_f32_e32 v134, 0x45800000, v133
	v_cndmask_b32_e32 v133, v133, v134, vcc
	v_mul_f32_e32 v184, 0x3c800000, v133
	v_mul_f32_e32 v133, 0x45800000, v132
	v_cndmask_b32_e64 v132, v132, v133, s[2:3]
	v_mul_f32_e32 v172, 0x3c800000, v132
	v_mov_b32_e32 v132, v208
	v_mov_b32_e32 v133, v212
	v_mov_b32_e32 v212, v209
	v_mov_b32_e32 v134, v210
	v_pk_add_f32 v[132:133], v[132:133], v[212:213]
	v_pk_add_f32 v[134:135], v[134:135], v[214:215]
	v_mov_b32_e32 v226, v219
	v_pk_add_f32 v[132:133], v[132:133], v[134:135]
	v_mov_b32_e32 v134, v216
	v_mov_b32_e32 v135, v224
	v_mov_b32_e32 v224, v217
	v_pk_add_f32 v[134:135], v[134:135], v[224:225]
	v_pk_add_f32 v[186:187], v[186:187], v[226:227]
	v_pk_mul_f32 v[108:109], v[108:109], v[180:181] op_sel_hi:[1,0]
	v_pk_add_f32 v[134:135], v[134:135], v[186:187]
	v_mov_b32_e32 v187, v132
	v_mov_b32_e32 v186, v134
	v_mov_b32_e32 v132, v135
	v_pk_add_f32 v[132:133], v[186:187], v[132:133]
	v_mov_b32_e32 v135, v234
	v_pk_fma_f32 v[132:133], v[132:133], s[16:17], v[148:149] op_sel_hi:[1,0,0]
	v_mov_b32_e32 v234, v231
	v_mul_f32_e32 v134, 0x4b800000, v133
	v_cmp_gt_f32_e32 vcc, s54, v133
	v_cmp_gt_f32_e64 s[2:3], s54, v132
	v_mov_b32_e32 v186, v238
	v_cndmask_b32_e32 v133, v133, v134, vcc
	v_rsq_f32_e32 v133, v133
	v_mul_f32_e32 v134, 0x4b800000, v132
	v_cndmask_b32_e64 v132, v132, v134, s[2:3]
	v_rsq_f32_e32 v132, v132
	v_mul_f32_e32 v134, 0x45800000, v133
	v_cndmask_b32_e32 v133, v133, v134, vcc
	v_mul_f32_e32 v170, 0x3c800000, v133
	v_mul_f32_e32 v133, 0x45800000, v132
	v_cndmask_b32_e64 v132, v132, v133, s[2:3]
	v_mul_f32_e32 v168, 0x3c800000, v132
	v_mov_b32_e32 v132, v228
	v_mov_b32_e32 v133, v232
	v_mov_b32_e32 v232, v229
	v_mov_b32_e32 v134, v230
	v_pk_add_f32 v[132:133], v[132:133], v[232:233]
	v_pk_add_f32 v[134:135], v[134:135], v[234:235]
	v_mov_b32_e32 v187, v242
	v_pk_add_f32 v[132:133], v[132:133], v[134:135]
	v_mov_b32_e32 v134, v236
	v_mov_b32_e32 v135, v240
	v_mov_b32_e32 v240, v237
	v_mov_b32_e32 v242, v239
	v_pk_add_f32 v[134:135], v[134:135], v[240:241]
	v_pk_add_f32 v[186:187], v[186:187], v[242:243]
	v_pk_mul_f32 v[110:111], v[110:111], v[180:181] op_sel_hi:[1,0]
	v_pk_add_f32 v[134:135], v[134:135], v[186:187]
	v_mov_b32_e32 v187, v132
	v_mov_b32_e32 v186, v134
	v_mov_b32_e32 v132, v135
	v_pk_add_f32 v[132:133], v[186:187], v[132:133]
	v_cvt_pk_bf16_f32 v108, v108, v109
	v_cvt_pk_bf16_f32 v109, v110, v111
	v_pk_mul_f32 v[114:115], v[114:115], v[180:181] op_sel_hi:[1,0]
	v_pk_fma_f32 v[132:133], v[132:133], s[16:17], v[148:149] op_sel_hi:[1,0,0]
	v_pk_mul_f32 v[112:113], v[112:113], v[180:181] op_sel_hi:[1,0]
	v_mul_f32_e32 v134, 0x4b800000, v133
	v_cmp_gt_f32_e32 vcc, s54, v133
	v_cmp_gt_f32_e64 s[2:3], s54, v132
	v_cvt_pk_bf16_f32 v110, v112, v113
	v_cvt_pk_bf16_f32 v111, v114, v115
	v_pk_mul_f32 v[112:113], v[130:131], v[180:181] op_sel_hi:[1,0]
	v_cndmask_b32_e32 v133, v133, v134, vcc
	v_rsq_f32_e32 v133, v133
	v_mul_f32_e32 v134, 0x4b800000, v132
	v_cndmask_b32_e64 v132, v132, v134, s[2:3]
	v_rsq_f32_e32 v132, v132
	v_mul_f32_e32 v134, 0x45800000, v133
	v_cndmask_b32_e32 v133, v133, v134, vcc
	v_mul_f32_e32 v166, 0x3c800000, v133
	v_mul_f32_e32 v133, 0x45800000, v132
	v_cndmask_b32_e64 v132, v132, v133, s[2:3]
	s_add_u32 s2, s4, s24
	s_addc_u32 s3, s5, 0
	s_add_i32 s23, s23, s59
	v_lshl_or_b32 v134, s23, 8, v175
	v_ashrrev_i32_e32 v135, 31, v134
	v_lshl_add_u64 v[134:135], v[134:135], 1, s[2:3]
	v_mad_i64_i32 v[164:165], s[2:3], s22, v164, 0
	v_lshl_add_u64 v[164:165], v[164:165], 1, v[134:135]
	global_store_dwordx4 v[164:165], v[108:111], off sc1
	v_pk_mul_f32 v[114:115], v[128:129], v[180:181] op_sel_hi:[1,0]
	v_pk_mul_f32 v[106:107], v[106:107], v[182:183] op_sel_hi:[1,0]
	v_pk_mul_f32 v[108:109], v[124:125], v[180:181] op_sel_hi:[1,0]
	v_pk_mul_f32 v[110:111], v[126:127], v[180:181] op_sel_hi:[1,0]
	v_cvt_pk_bf16_f32 v108, v108, v109
	v_pk_mul_f32 v[104:105], v[104:105], v[182:183] op_sel_hi:[1,0]
	v_cvt_pk_bf16_f32 v109, v110, v111
	v_cvt_pk_bf16_f32 v110, v114, v115
	v_cvt_pk_bf16_f32 v111, v112, v113
	global_store_dwordx4 v[164:165], v[108:111], off offset:256 sc1
	v_pk_mul_f32 v[82:83], v[82:83], v[184:185] op_sel_hi:[1,0]
	v_pk_mul_f32 v[80:81], v[80:81], v[184:185] op_sel_hi:[1,0]
	v_mad_i64_i32 v[108:109], s[2:3], s22, v162, 0
	v_lshl_add_u64 v[108:109], v[108:109], 1, v[134:135]
	v_pk_mul_f32 v[110:111], v[102:103], v[182:183] op_sel_hi:[1,0]
	v_pk_mul_f32 v[102:103], v[100:101], v[182:183] op_sel_hi:[1,0]
	v_cvt_pk_bf16_f32 v100, v104, v105
	v_cvt_pk_bf16_f32 v101, v106, v107
	v_pk_mul_f32 v[104:105], v[118:119], v[182:183] op_sel_hi:[1,0]
	v_cvt_pk_bf16_f32 v102, v102, v103
	v_cvt_pk_bf16_f32 v103, v110, v111
	global_store_dwordx4 v[108:109], v[100:103], off sc1
	v_pk_mul_f32 v[106:107], v[116:117], v[182:183] op_sel_hi:[1,0]
	v_pk_mul_f32 v[50:51], v[50:51], v[172:173] op_sel_hi:[1,0]
	v_pk_mul_f32 v[100:101], v[120:121], v[182:183] op_sel_hi:[1,0]
	v_pk_mul_f32 v[102:103], v[122:123], v[182:183] op_sel_hi:[1,0]
	v_cvt_pk_bf16_f32 v100, v100, v101
	v_pk_mul_f32 v[48:49], v[48:49], v[172:173] op_sel_hi:[1,0]
	v_cvt_pk_bf16_f32 v101, v102, v103
	v_cvt_pk_bf16_f32 v102, v106, v107
	v_cvt_pk_bf16_f32 v103, v104, v105
	global_store_dwordx4 v[108:109], v[100:103], off offset:256 sc1
	v_pk_mul_f32 v[42:43], v[42:43], v[168:169] op_sel_hi:[1,0]
	v_pk_mul_f32 v[40:41], v[40:41], v[168:169] op_sel_hi:[1,0]
	v_mad_i64_i32 v[100:101], s[2:3], s22, v160, 0
	v_lshl_add_u64 v[100:101], v[100:101], 1, v[134:135]
	v_pk_mul_f32 v[102:103], v[78:79], v[184:185] op_sel_hi:[1,0]
	v_pk_mul_f32 v[78:79], v[76:77], v[184:185] op_sel_hi:[1,0]
	v_cvt_pk_bf16_f32 v76, v80, v81
	v_cvt_pk_bf16_f32 v77, v82, v83
	v_pk_mul_f32 v[80:81], v[94:95], v[184:185] op_sel_hi:[1,0]
	v_cvt_pk_bf16_f32 v78, v78, v79
	v_cvt_pk_bf16_f32 v79, v102, v103
	global_store_dwordx4 v[100:101], v[76:79], off sc1
	v_pk_mul_f32 v[82:83], v[92:93], v[184:185] op_sel_hi:[1,0]
	v_pk_mul_f32 v[26:27], v[26:27], v[166:167] op_sel_hi:[1,0]
	v_pk_mul_f32 v[76:77], v[96:97], v[184:185] op_sel_hi:[1,0]
	v_pk_mul_f32 v[78:79], v[98:99], v[184:185] op_sel_hi:[1,0]
	v_cvt_pk_bf16_f32 v76, v76, v77
	v_pk_mul_f32 v[24:25], v[24:25], v[166:167] op_sel_hi:[1,0]
	v_cvt_pk_bf16_f32 v77, v78, v79
	v_cvt_pk_bf16_f32 v78, v82, v83
	v_cvt_pk_bf16_f32 v79, v80, v81
	global_store_dwordx4 v[100:101], v[76:79], off offset:256 sc1
	v_mul_f32_e32 v132, 0x3c800000, v132
	v_pk_mul_f32 v[10:11], v[10:11], v[132:133] op_sel_hi:[1,0]
	v_mad_i64_i32 v[76:77], s[2:3], s22, v158, 0
	v_lshl_add_u64 v[76:77], v[76:77], 1, v[134:135]
	v_pk_mul_f32 v[78:79], v[46:47], v[172:173] op_sel_hi:[1,0]
	v_pk_mul_f32 v[46:47], v[44:45], v[172:173] op_sel_hi:[1,0]
	v_cvt_pk_bf16_f32 v44, v48, v49
	v_cvt_pk_bf16_f32 v45, v50, v51
	v_pk_mul_f32 v[48:49], v[62:63], v[172:173] op_sel_hi:[1,0]
	v_cvt_pk_bf16_f32 v46, v46, v47
	v_cvt_pk_bf16_f32 v47, v78, v79
	global_store_dwordx4 v[76:77], v[44:47], off sc1
	v_pk_mul_f32 v[50:51], v[60:61], v[172:173] op_sel_hi:[1,0]
	v_pk_mul_f32 v[60:61], v[68:69], v[170:171] op_sel_hi:[1,0]
	v_pk_mul_f32 v[44:45], v[64:65], v[172:173] op_sel_hi:[1,0]
	v_pk_mul_f32 v[46:47], v[66:67], v[172:173] op_sel_hi:[1,0]
	v_cvt_pk_bf16_f32 v44, v44, v45
	v_pk_mul_f32 v[8:9], v[8:9], v[132:133] op_sel_hi:[1,0]
	v_cvt_pk_bf16_f32 v45, v46, v47
	v_cvt_pk_bf16_f32 v46, v50, v51
	v_cvt_pk_bf16_f32 v47, v48, v49
	global_store_dwordx4 v[76:77], v[44:47], off offset:256 sc1
	v_pk_mul_f32 v[50:51], v[70:71], v[170:171] op_sel_hi:[1,0]
	s_add_i32 s49, s49, s17
	v_mad_i64_i32 v[44:45], s[2:3], s22, v156, 0
	v_lshl_add_u64 v[48:49], v[44:45], 1, v[134:135]
	v_pk_mul_f32 v[46:47], v[74:75], v[170:171] op_sel_hi:[1,0]
	v_pk_mul_f32 v[44:45], v[72:73], v[170:171] op_sel_hi:[1,0]
	s_andn2_b64 vcc, exec, s[0:1]
	v_cvt_pk_bf16_f32 v44, v44, v45
	v_cvt_pk_bf16_f32 v45, v46, v47
	v_cvt_pk_bf16_f32 v46, v60, v61
	v_cvt_pk_bf16_f32 v47, v50, v51
	global_store_dwordx4 v[48:49], v[44:47], off sc1
	v_pk_mul_f32 v[50:51], v[86:87], v[170:171] op_sel_hi:[1,0]
	v_pk_mul_f32 v[60:61], v[84:85], v[170:171] op_sel_hi:[1,0]
	v_pk_mul_f32 v[46:47], v[90:91], v[170:171] op_sel_hi:[1,0]
	v_pk_mul_f32 v[44:45], v[88:89], v[170:171] op_sel_hi:[1,0]
	s_mov_b32 s59, s55
	v_cvt_pk_bf16_f32 v44, v44, v45
	v_cvt_pk_bf16_f32 v45, v46, v47
	v_cvt_pk_bf16_f32 v46, v60, v61
	v_cvt_pk_bf16_f32 v47, v50, v51
	global_store_dwordx4 v[48:49], v[44:47], off offset:256 sc1
	s_nop 1
	v_mad_i64_i32 v[44:45], s[2:3], s22, v154, 0
	v_pk_mul_f32 v[46:47], v[38:39], v[168:169] op_sel_hi:[1,0]
	v_pk_mul_f32 v[38:39], v[36:37], v[168:169] op_sel_hi:[1,0]
	v_lshl_add_u64 v[44:45], v[44:45], 1, v[134:135]
	v_cvt_pk_bf16_f32 v36, v40, v41
	v_cvt_pk_bf16_f32 v37, v42, v43
	v_cvt_pk_bf16_f32 v38, v38, v39
	v_cvt_pk_bf16_f32 v39, v46, v47
	global_store_dwordx4 v[44:45], v[36:39], off sc1
	v_pk_mul_f32 v[40:41], v[54:55], v[168:169] op_sel_hi:[1,0]
	v_pk_mul_f32 v[42:43], v[52:53], v[168:169] op_sel_hi:[1,0]
	v_pk_mul_f32 v[38:39], v[58:59], v[168:169] op_sel_hi:[1,0]
	v_pk_mul_f32 v[36:37], v[56:57], v[168:169] op_sel_hi:[1,0]
	s_nop 0
	v_cvt_pk_bf16_f32 v36, v36, v37
	v_cvt_pk_bf16_f32 v37, v38, v39
	v_cvt_pk_bf16_f32 v38, v42, v43
	v_cvt_pk_bf16_f32 v39, v40, v41
	global_store_dwordx4 v[44:45], v[36:39], off offset:256 sc1
	s_nop 1
	v_mad_i64_i32 v[36:37], s[2:3], s22, v152, 0
	v_pk_mul_f32 v[38:39], v[22:23], v[166:167] op_sel_hi:[1,0]
	v_pk_mul_f32 v[22:23], v[20:21], v[166:167] op_sel_hi:[1,0]
	v_lshl_add_u64 v[36:37], v[36:37], 1, v[134:135]
	v_cvt_pk_bf16_f32 v20, v24, v25
	v_cvt_pk_bf16_f32 v21, v26, v27
	v_cvt_pk_bf16_f32 v22, v22, v23
	v_cvt_pk_bf16_f32 v23, v38, v39
	global_store_dwordx4 v[36:37], v[20:23], off sc1
	v_pk_mul_f32 v[24:25], v[30:31], v[166:167] op_sel_hi:[1,0]
	v_pk_mul_f32 v[26:27], v[28:29], v[166:167] op_sel_hi:[1,0]
	v_pk_mul_f32 v[22:23], v[34:35], v[166:167] op_sel_hi:[1,0]
	v_pk_mul_f32 v[20:21], v[32:33], v[166:167] op_sel_hi:[1,0]
	s_nop 0
	v_cvt_pk_bf16_f32 v20, v20, v21
	v_cvt_pk_bf16_f32 v21, v22, v23
	v_cvt_pk_bf16_f32 v22, v26, v27
	v_cvt_pk_bf16_f32 v23, v24, v25
	global_store_dwordx4 v[36:37], v[20:23], off offset:256 sc1
	s_nop 1
	v_mad_i64_i32 v[20:21], s[2:3], s22, v150, 0
	v_pk_mul_f32 v[22:23], v[6:7], v[132:133] op_sel_hi:[1,0]
	v_pk_mul_f32 v[6:7], v[4:5], v[132:133] op_sel_hi:[1,0]
	v_lshl_add_u64 v[20:21], v[20:21], 1, v[134:135]
	v_cvt_pk_bf16_f32 v4, v8, v9
	v_cvt_pk_bf16_f32 v5, v10, v11
	v_cvt_pk_bf16_f32 v6, v6, v7
	v_cvt_pk_bf16_f32 v7, v22, v23
	global_store_dwordx4 v[20:21], v[4:7], off sc1
	s_mov_b64 s[22:23], s[18:19]
	v_pk_mul_f32 v[8:9], v[14:15], v[132:133] op_sel_hi:[1,0]
	v_pk_mul_f32 v[6:7], v[18:19], v[132:133] op_sel_hi:[1,0]
	v_pk_mul_f32 v[4:5], v[16:17], v[132:133] op_sel_hi:[1,0]
	v_pk_mul_f32 v[10:11], v[12:13], v[132:133] op_sel_hi:[1,0]
	v_cvt_pk_bf16_f32 v4, v4, v5
	v_cvt_pk_bf16_f32 v5, v6, v7
	s_nop 0
	v_cvt_pk_bf16_f32 v6, v10, v11
	v_cvt_pk_bf16_f32 v7, v8, v9
	global_store_dwordx4 v[20:21], v[4:7], off offset:256 sc1
	s_cbranch_vccz .LBB0_1686

.LBB0_1696:
	v_lshl_add_u64 v[64:65], s[6:7], 0, v[44:45]
	global_load_dwordx4 v[0:3], v[64:65], off
	global_load_dwordx4 v[50:53], v[34:35], off offset:528
	global_load_dwordx4 v[54:57], v[34:35], off offset:512
	s_add_i32 s47, s23, s22
	s_cmpk_lt_i32 s47, 0x2200
	s_cselect_b64 s[20:21], -1, 0
	s_and_b64 s[4:5], s[20:21], exec
	s_cselect_b32 s4, s47, s22
	s_mul_hi_i32 s5, s4, 0x4c00
	s_mulk_i32 s4, 0x4c00
	s_add_u32 s4, s8, s4
	s_addc_u32 s5, s9, s5
	s_add_i32 s46, s27, s22
	s_cmpk_lt_i32 s46, 0x2200
	s_cselect_b64 s[18:19], -1, 0
	s_and_b64 s[12:13], s[18:19], exec
	v_lshl_add_u64 v[48:49], s[6:7], 0, v[46:47]
	s_cselect_b32 s10, s46, s22
	global_load_dwordx4 v[60:63], v[48:49], off
	s_mul_hi_i32 s13, s10, 0x4c00
	s_mulk_i32 s10, 0x4c00
	s_add_u32 s12, s8, s10
	s_addc_u32 s13, s9, s13
	s_add_i32 s45, s29, s22
	s_cmpk_lt_i32 s45, 0x2200
	s_cselect_b64 s[16:17], -1, 0
	v_lshl_add_u64 v[4:5], s[4:5], 0, v[32:33]
	global_load_dwordx4 v[28:31], v58, s[4:5] offset:3072
	global_load_dwordx4 v[20:23], v58, s[12:13] offset:3072
	s_and_b64 s[4:5], s[16:17], exec
	s_cselect_b32 s4, s45, s22
	v_add_co_u32_e32 v4, vcc, s42, v4
	s_mul_hi_i32 s5, s4, 0x4c00
	s_mulk_i32 s4, 0x4c00
	v_addc_co_u32_e32 v5, vcc, 0, v5, vcc
	v_lshl_add_u64 v[6:7], s[12:13], 0, v[32:33]
	s_add_u32 s4, s8, s4
	v_add_co_u32_e32 v6, vcc, s42, v6
	s_addc_u32 s5, s9, s5
	s_nop 0
	v_addc_co_u32_e32 v7, vcc, 0, v7, vcc
	global_load_dwordx4 v[24:27], v[4:5], off offset:2048
	global_load_dwordx4 v[16:19], v[6:7], off offset:2048
	v_lshl_add_u64 v[4:5], s[4:5], 0, v[32:33]
	v_add_co_u32_e32 v8, vcc, s42, v4
	s_add_i32 s44, s31, s22
	s_nop 0
	v_addc_co_u32_e32 v9, vcc, 0, v5, vcc
	s_cmpk_lt_i32 s44, 0x2200
	s_cselect_b64 s[12:13], -1, 0
	s_and_b64 s[48:49], s[12:13], exec
	s_cselect_b32 s10, s44, s22
	s_mul_hi_i32 s49, s10, 0x4c00
	s_mulk_i32 s10, 0x4c00
	s_add_u32 s48, s8, s10
	s_addc_u32 s49, s9, s49
	v_lshl_add_u64 v[10:11], s[48:49], 0, v[32:33]
	global_load_dwordx4 v[12:15], v58, s[4:5] offset:3072
	global_load_dwordx4 v[4:7], v58, s[48:49] offset:3072
	s_cmpk_gt_i32 s22, 0x1fff
	s_waitcnt vmcnt(9)
	v_and_b32_e32 v75, 0xffff0000, v0
	v_lshlrev_b32_e32 v74, 16, v0
	v_and_b32_e32 v66, 0xffff0000, v1
	v_lshlrev_b32_e32 v67, 16, v1
	v_mul_f32_e32 v76, v75, v75
	v_pk_mul_f32 v[0:1], v[66:67], v[66:67]
	v_fmac_f32_e32 v76, v74, v74
	v_and_b32_e32 v68, 0xffff0000, v2
	v_lshlrev_b32_e32 v69, 16, v2
	v_add_f32_e32 v1, v1, v76
	v_and_b32_e32 v70, 0xffff0000, v3
	v_lshlrev_b32_e32 v71, 16, v3
	v_pk_mul_f32 v[2:3], v[68:69], v[68:69]
	v_add_f32_e32 v0, v0, v1
	v_add_f32_e32 v0, v3, v0
	v_pk_mul_f32 v[72:73], v[70:71], v[70:71]
	v_add_f32_e32 v0, v2, v0
	v_add_f32_e32 v0, v73, v0
	v_add_f32_e32 v0, v72, v0
	v_mov_b32_e32 v1, v0
	s_nop 1
	v_mov_b32_dpp v1, v1 quad_perm:[1,0,3,2] row_mask:0xf bank_mask:0xf
	v_add_f32_e32 v0, v0, v1
	v_mov_b32_e32 v1, v0
	s_nop 1
	v_mov_b32_dpp v1, v1 quad_perm:[2,3,0,1] row_mask:0xf bank_mask:0xf
	v_add_f32_e32 v0, v0, v1
	v_mov_b32_e32 v1, v0
	s_nop 1
	v_mov_b32_dpp v1, v1 row_half_mirror row_mask:0xf bank_mask:0xf
	v_add_f32_e32 v0, v0, v1
	v_mov_b32_e32 v1, v0
	s_nop 1
	v_mov_b32_dpp v1, v1 row_mirror row_mask:0xf bank_mask:0xf
	v_add_f32_e32 v0, v0, v1
	v_fmamk_f32 v0, v0, 0x3c000000, v59
	v_mul_f32_e32 v1, 0x4b800000, v0
	v_cmp_gt_f32_e32 vcc, s43, v0
	s_nop 1
	v_cndmask_b32_e32 v0, v0, v1, vcc
	v_rsq_f32_e32 v72, v0
	v_add_co_u32_e64 v0, s[4:5], s42, v10
	v_mul_f32_e32 v73, 0x45800000, v72
	v_cndmask_b32_e32 v72, v72, v73, vcc
	v_mul_f32_e32 v66, v72, v66
	s_waitcnt vmcnt(7)
	v_mul_f32_e32 v57, v57, v66
	v_mul_f32_e32 v66, v72, v69
	v_mul_f32_e32 v67, v72, v67
	v_mul_f32_e32 v66, v50, v66
	v_mul_f32_e32 v50, v72, v68
	v_mul_f32_e32 v56, v56, v67
	v_mul_f32_e32 v67, v51, v50
	v_mul_f32_e32 v50, v72, v71
	v_mul_f32_e32 v68, v52, v50
	v_mul_f32_e32 v50, v72, v70
	v_addc_co_u32_e64 v1, s[4:5], 0, v11, s[4:5]
	v_mul_f32_e32 v73, v72, v74
	v_mul_f32_e32 v74, v72, v75
	v_mul_f32_e32 v53, v53, v50
	global_load_dwordx4 v[8:11], v[8:9], off offset:2048
	s_nop 0
	global_load_dwordx4 v[0:3], v[0:1], off offset:2048
	v_mul_f32_e32 v54, v54, v73
	v_mul_f32_e32 v55, v55, v74
	v_cvt_pk_bf16_f32 v50, v54, v55
	v_cvt_pk_bf16_f32 v51, v56, v57
	v_cvt_pk_bf16_f32 v52, v66, v67
	v_cvt_pk_bf16_f32 v53, v68, v53
	global_store_dwordx4 v[64:65], v[50:53], off sc1
	global_load_dwordx4 v[50:53], v[36:37], off offset:256
	s_nop 0
	global_load_dwordx4 v[64:67], v[36:37], off offset:272
	s_waitcnt vmcnt(11)
	v_lshlrev_b32_e32 v56, 16, v60
	v_and_b32_e32 v57, 0xffff0000, v60
	v_lshlrev_b32_e32 v60, 16, v61
	v_and_b32_e32 v61, 0xffff0000, v61
	v_pk_mul_f32 v[70:71], v[56:57], v[56:57]
	v_pk_mul_f32 v[72:73], v[60:61], v[60:61]
	v_add_f32_e32 v70, v70, v71
	v_lshlrev_b32_e32 v68, 16, v62
	v_and_b32_e32 v69, 0xffff0000, v62
	v_add_f32_e32 v70, v72, v70
	v_pk_mul_f32 v[74:75], v[68:69], v[68:69]
	v_add_f32_e32 v70, v73, v70
	v_and_b32_e32 v54, 0xffff0000, v63
	v_lshlrev_b32_e32 v55, 16, v63
	v_add_f32_e32 v70, v74, v70
	v_pk_mul_f32 v[62:63], v[54:55], v[54:55]
	v_add_f32_e32 v70, v75, v70
	v_add_f32_e32 v63, v63, v70
	v_add_f32_e32 v62, v62, v63
	v_mov_b32_e32 v63, v62
	s_nop 1
	v_mov_b32_dpp v63, v63 quad_perm:[1,0,3,2] row_mask:0xf bank_mask:0xf
	v_add_f32_e32 v62, v62, v63
	v_mov_b32_e32 v63, v62
	s_nop 1
	v_mov_b32_dpp v63, v63 quad_perm:[2,3,0,1] row_mask:0xf bank_mask:0xf
	v_add_f32_e32 v62, v62, v63
	v_mov_b32_e32 v63, v62
	s_nop 1
	v_mov_b32_dpp v63, v63 row_half_mirror row_mask:0xf bank_mask:0xf
	v_add_f32_e32 v62, v62, v63
	v_fmamk_f32 v62, v62, 0x3c800000, v59
	v_mul_f32_e32 v63, 0x4b800000, v62
	v_cmp_gt_f32_e32 vcc, s43, v62
	s_nop 1
	v_cndmask_b32_e32 v62, v62, v63, vcc
	v_rsq_f32_e32 v62, v62
	s_nop 0
	v_mul_f32_e32 v63, 0x45800000, v62
	v_cndmask_b32_e32 v62, v62, v63, vcc
	v_pk_mul_f32 v[56:57], v[62:63], v[56:57] op_sel_hi:[0,1]
	v_pk_mul_f32 v[60:61], v[62:63], v[60:61] op_sel_hi:[0,1]
	v_pk_mul_f32 v[68:69], v[62:63], v[68:69] op_sel_hi:[0,1]
	v_pk_mul_f32 v[62:63], v[62:63], v[54:55] op_sel_hi:[0,1]
	s_waitcnt vmcnt(1)
	v_pk_mul_f32 v[56:57], v[50:51], v[56:57]
	v_pk_mul_f32 v[54:55], v[52:53], v[60:61]
	s_waitcnt vmcnt(0)
	v_pk_mul_f32 v[52:53], v[64:65], v[68:69]
	v_pk_mul_f32 v[50:51], v[66:67], v[62:63] op_sel:[0,1] op_sel_hi:[1,0]
	s_cbranch_scc0 .LBB0_1702
	s_and_saveexec_b64 s[4:5], s[2:3]
	s_cbranch_execnz .LBB0_1703

.LBB0_1704:
	global_load_dwordx4 v[48:51], v[34:35], off offset:512
	global_load_dwordx4 v[52:55], v[34:35], off offset:528
	v_and_b32_e32 v67, 0xffff0000, v28
	v_lshlrev_b32_e32 v66, 16, v28
	v_and_b32_e32 v28, 0xffff0000, v29
	v_lshlrev_b32_e32 v29, 16, v29
	v_mul_f32_e32 v68, v67, v67
	v_pk_mul_f32 v[60:61], v[28:29], v[28:29]
	v_fmac_f32_e32 v68, v66, v66
	v_and_b32_e32 v56, 0xffff0000, v30
	v_lshlrev_b32_e32 v57, 16, v30
	v_add_f32_e32 v61, v61, v68
	v_pk_mul_f32 v[62:63], v[56:57], v[56:57]
	v_add_f32_e32 v60, v60, v61
	v_and_b32_e32 v30, 0xffff0000, v31
	v_lshlrev_b32_e32 v31, 16, v31
	v_add_f32_e32 v60, v63, v60
	v_pk_mul_f32 v[64:65], v[30:31], v[30:31]
	v_add_f32_e32 v60, v62, v60
	v_add_f32_e32 v60, v65, v60
	v_add_f32_e32 v60, v64, v60
	v_mov_b32_e32 v61, v60
	s_cmpk_gt_i32 s47, 0x1fff
	s_nop 0
	v_mov_b32_dpp v61, v61 quad_perm:[1,0,3,2] row_mask:0xf bank_mask:0xf
	v_add_f32_e32 v60, v60, v61
	v_mov_b32_e32 v61, v60
	s_nop 1
	v_mov_b32_dpp v61, v61 quad_perm:[2,3,0,1] row_mask:0xf bank_mask:0xf
	v_add_f32_e32 v60, v60, v61
	v_mov_b32_e32 v61, v60
	s_nop 1
	v_mov_b32_dpp v61, v61 row_half_mirror row_mask:0xf bank_mask:0xf
	v_add_f32_e32 v60, v60, v61
	v_mov_b32_e32 v61, v60
	s_nop 1
	v_mov_b32_dpp v61, v61 row_mirror row_mask:0xf bank_mask:0xf
	v_add_f32_e32 v60, v60, v61
	v_fmamk_f32 v60, v60, 0x3c000000, v59
	v_mul_f32_e32 v61, 0x4b800000, v60
	v_cmp_gt_f32_e32 vcc, s43, v60
	s_nop 1
	v_cndmask_b32_e32 v60, v60, v61, vcc
	v_rsq_f32_e32 v62, v60
	v_lshl_add_u64 v[60:61], s[6:7], 0, v[40:41]
	v_mul_f32_e32 v63, 0x45800000, v62
	v_cndmask_b32_e32 v62, v62, v63, vcc
	v_mul_f32_e32 v29, v62, v29
	v_mul_f32_e32 v31, v62, v31
	v_mul_f32_e32 v63, v62, v66
	v_mul_f32_e32 v64, v62, v67
	v_mul_f32_e32 v28, v62, v28
	v_mul_f32_e32 v57, v62, v57
	v_mul_f32_e32 v56, v62, v56
	v_mul_f32_e32 v30, v62, v30
	s_waitcnt vmcnt(1)
	v_mul_f32_e32 v29, v50, v29
	s_waitcnt vmcnt(0)
	v_mul_f32_e32 v31, v54, v31
	v_mul_f32_e32 v48, v48, v63
	v_mul_f32_e32 v49, v49, v64
	v_mul_f32_e32 v50, v51, v28
	v_mul_f32_e32 v51, v52, v57
	v_mul_f32_e32 v52, v53, v56
	v_mul_f32_e32 v53, v55, v30
	v_cvt_pk_bf16_f32 v28, v48, v49
	v_cvt_pk_bf16_f32 v29, v29, v50
	v_cvt_pk_bf16_f32 v30, v51, v52
	v_cvt_pk_bf16_f32 v31, v31, v53
	global_store_dwordx4 v[60:61], v[28:31], off sc1
	global_load_dwordx4 v[48:51], v[36:37], off offset:256
	global_load_dwordx4 v[52:55], v[36:37], off offset:272
	v_lshlrev_b32_e32 v30, 16, v24
	v_and_b32_e32 v31, 0xffff0000, v24
	v_lshlrev_b32_e32 v24, 16, v25
	v_and_b32_e32 v25, 0xffff0000, v25
	v_pk_mul_f32 v[60:61], v[30:31], v[30:31]
	v_pk_mul_f32 v[62:63], v[24:25], v[24:25]
	v_add_f32_e32 v60, v60, v61
	v_lshlrev_b32_e32 v56, 16, v26
	v_and_b32_e32 v57, 0xffff0000, v26
	v_add_f32_e32 v60, v62, v60
	v_pk_mul_f32 v[64:65], v[56:57], v[56:57]
	v_add_f32_e32 v60, v63, v60
	v_and_b32_e32 v28, 0xffff0000, v27
	v_lshlrev_b32_e32 v29, 16, v27
	v_add_f32_e32 v60, v64, v60
	v_pk_mul_f32 v[26:27], v[28:29], v[28:29]
	v_add_f32_e32 v60, v65, v60
	v_add_f32_e32 v27, v27, v60
	v_add_f32_e32 v26, v26, v27
	v_mov_b32_e32 v27, v26
	s_nop 1
	v_mov_b32_dpp v27, v27 quad_perm:[1,0,3,2] row_mask:0xf bank_mask:0xf
	v_add_f32_e32 v26, v26, v27
	v_mov_b32_e32 v27, v26
	s_nop 1
	v_mov_b32_dpp v27, v27 quad_perm:[2,3,0,1] row_mask:0xf bank_mask:0xf
	v_add_f32_e32 v26, v26, v27
	v_mov_b32_e32 v27, v26
	s_nop 1
	v_mov_b32_dpp v27, v27 row_half_mirror row_mask:0xf bank_mask:0xf
	v_add_f32_e32 v26, v26, v27
	v_fmamk_f32 v26, v26, 0x3c800000, v59
	v_mul_f32_e32 v27, 0x4b800000, v26
	v_cmp_gt_f32_e32 vcc, s43, v26
	s_nop 1
	v_cndmask_b32_e32 v26, v26, v27, vcc
	v_rsq_f32_e32 v26, v26
	s_nop 0
	v_mul_f32_e32 v27, 0x45800000, v26
	v_cndmask_b32_e32 v26, v26, v27, vcc
	v_pk_mul_f32 v[30:31], v[26:27], v[30:31] op_sel_hi:[0,1]
	v_pk_mul_f32 v[24:25], v[26:27], v[24:25] op_sel_hi:[0,1]
	v_pk_mul_f32 v[56:57], v[26:27], v[56:57] op_sel_hi:[0,1]
	v_pk_mul_f32 v[60:61], v[26:27], v[28:29] op_sel_hi:[0,1]
	s_waitcnt vmcnt(1)
	v_pk_mul_f32 v[30:31], v[48:49], v[30:31]
	v_pk_mul_f32 v[28:29], v[50:51], v[24:25]
	s_waitcnt vmcnt(0)
	v_pk_mul_f32 v[26:27], v[52:53], v[56:57]
	v_pk_mul_f32 v[24:25], v[54:55], v[60:61] op_sel:[0,1] op_sel_hi:[1,0]
	s_cbranch_scc1 .LBB0_1706
	s_add_i32 s4, s39, s25
	s_and_b32 s4, s4, 0x1ffe0
	s_lshl_b32 s10, s4, 3
	v_lshl_add_u64 v[56:57], v[38:39], 0, s[10:11]
	global_load_dwordx4 v[48:51], v[56:57], off
	global_load_dwordx4 v[52:55], v[56:57], off offset:16
	global_load_dwordx4 v[60:63], v[56:57], off offset:32
	global_load_dwordx4 v[64:67], v[56:57], off offset:48
	v_mov_b32_e32 v56, v30
	v_mov_b32_e32 v57, v31
	v_mov_b32_e32 v68, v28
	v_mov_b32_e32 v69, v29
	v_mov_b32_e32 v70, v26
	v_mov_b32_e32 v71, v27
	v_mov_b32_e32 v72, v24
	v_mov_b32_e32 v73, v25
	v_mov_b32_dpp v56, v56 row_shl:4 row_mask:0xf bank_mask:0x5
	v_mov_b32_dpp v57, v57 row_shl:4 row_mask:0xf bank_mask:0x5
	v_mov_b32_dpp v68, v68 row_shl:4 row_mask:0xf bank_mask:0x5
	v_mov_b32_dpp v69, v69 row_shl:4 row_mask:0xf bank_mask:0x5
	v_mov_b32_dpp v70, v70 row_shl:4 row_mask:0xf bank_mask:0x5
	v_mov_b32_dpp v71, v71 row_shl:4 row_mask:0xf bank_mask:0x5
	v_mov_b32_dpp v72, v72 row_shl:4 row_mask:0xf bank_mask:0x5
	v_mov_b32_dpp v73, v73 row_shl:4 row_mask:0xf bank_mask:0x5
	v_mov_b32_dpp v56, v30 row_shr:4 row_mask:0xf bank_mask:0xa
	v_mov_b32_dpp v57, v31 row_shr:4 row_mask:0xf bank_mask:0xa
	v_mov_b32_dpp v68, v28 row_shr:4 row_mask:0xf bank_mask:0xa
	v_mov_b32_dpp v69, v29 row_shr:4 row_mask:0xf bank_mask:0xa
	v_mov_b32_dpp v70, v26 row_shr:4 row_mask:0xf bank_mask:0xa
	v_mov_b32_dpp v71, v27 row_shr:4 row_mask:0xf bank_mask:0xa
	v_mov_b32_dpp v72, v24 row_shr:4 row_mask:0xf bank_mask:0xa
	v_mov_b32_dpp v73, v25 row_shr:4 row_mask:0xf bank_mask:0xa
	s_waitcnt vmcnt(3)
	v_mov_b32_e32 v75, v50
	v_mov_b32_e32 v50, v49
	s_waitcnt vmcnt(2)
	v_mov_b32_e32 v49, v54
	v_mov_b32_e32 v54, v53
	s_waitcnt vmcnt(1)
	v_mov_b32_e32 v53, v62
	v_mov_b32_e32 v62, v61
	s_waitcnt vmcnt(0)
	v_mov_b32_e32 v61, v66
	v_mov_b32_e32 v66, v65
	v_pk_mul_f32 v[50:51], v[50:51], v[56:57]
	v_pk_mul_f32 v[54:55], v[54:55], v[68:69]
	v_pk_mul_f32 v[56:57], v[62:63], v[70:71]
	v_pk_mul_f32 v[62:63], v[66:67], v[72:73]
	v_mov_b32_e32 v74, v48
	v_mov_b32_e32 v48, v52
	v_mov_b32_e32 v52, v60
	v_mov_b32_e32 v60, v64
	v_cndmask_b32_e64 v51, v51, -v51, s[0:1]
	v_cndmask_b32_e64 v50, v50, -v50, s[0:1]
	v_cndmask_b32_e64 v55, v55, -v55, s[0:1]
	v_cndmask_b32_e64 v54, v54, -v54, s[0:1]
	v_cndmask_b32_e64 v57, v57, -v57, s[0:1]
	v_cndmask_b32_e64 v56, v56, -v56, s[0:1]
	v_cndmask_b32_e64 v63, v63, -v63, s[0:1]
	v_cndmask_b32_e64 v62, v62, -v62, s[0:1]
	v_pk_fma_f32 v[30:31], v[30:31], v[74:75], v[50:51]
	v_pk_fma_f32 v[28:29], v[28:29], v[48:49], v[54:55]
	v_pk_fma_f32 v[26:27], v[26:27], v[52:53], v[56:57]
	v_pk_fma_f32 v[24:25], v[24:25], v[60:61], v[62:63]

.LBB0_1709:
	global_load_dwordx4 v[24:27], v[34:35], off offset:512
	global_load_dwordx4 v[28:31], v[34:35], off offset:528
	v_and_b32_e32 v57, 0xffff0000, v20
	v_lshlrev_b32_e32 v56, 16, v20
	v_and_b32_e32 v20, 0xffff0000, v21
	v_lshlrev_b32_e32 v21, 16, v21
	v_mul_f32_e32 v60, v57, v57
	v_pk_mul_f32 v[50:51], v[20:21], v[20:21]
	v_fmac_f32_e32 v60, v56, v56
	v_and_b32_e32 v48, 0xffff0000, v22
	v_lshlrev_b32_e32 v49, 16, v22
	v_add_f32_e32 v51, v51, v60
	v_pk_mul_f32 v[52:53], v[48:49], v[48:49]
	v_add_f32_e32 v50, v50, v51
	v_and_b32_e32 v22, 0xffff0000, v23
	v_lshlrev_b32_e32 v23, 16, v23
	v_add_f32_e32 v50, v53, v50
	v_pk_mul_f32 v[54:55], v[22:23], v[22:23]
	v_add_f32_e32 v50, v52, v50
	v_add_f32_e32 v50, v55, v50
	v_add_f32_e32 v50, v54, v50
	v_mov_b32_e32 v51, v50
	s_mul_i32 s4, s46, 0x4c00
	s_mul_hi_i32 s5, s46, 0x4c00
	v_mov_b32_dpp v51, v51 quad_perm:[1,0,3,2] row_mask:0xf bank_mask:0xf
	v_add_f32_e32 v50, v50, v51
	v_mov_b32_e32 v51, v50
	s_add_u32 s4, s8, s4
	s_addc_u32 s5, s9, s5
	v_mov_b32_dpp v51, v51 quad_perm:[2,3,0,1] row_mask:0xf bank_mask:0xf
	v_add_f32_e32 v50, v50, v51
	v_mov_b32_e32 v51, v50
	s_cmpk_gt_i32 s46, 0x1fff
	s_nop 0
	v_mov_b32_dpp v51, v51 row_half_mirror row_mask:0xf bank_mask:0xf
	v_add_f32_e32 v50, v50, v51
	v_mov_b32_e32 v51, v50
	s_nop 1
	v_mov_b32_dpp v51, v51 row_mirror row_mask:0xf bank_mask:0xf
	v_add_f32_e32 v50, v50, v51
	v_fmamk_f32 v50, v50, 0x3c000000, v59
	v_mul_f32_e32 v51, 0x4b800000, v50
	v_cmp_gt_f32_e32 vcc, s43, v50
	s_nop 1
	v_cndmask_b32_e32 v50, v50, v51, vcc
	v_rsq_f32_e32 v50, v50
	s_nop 0
	v_mul_f32_e32 v51, 0x45800000, v50
	v_cndmask_b32_e32 v50, v50, v51, vcc
	v_mul_f32_e32 v21, v50, v21
	v_mul_f32_e32 v23, v50, v23
	v_mul_f32_e32 v51, v50, v56
	v_mul_f32_e32 v52, v50, v57
	v_mul_f32_e32 v20, v50, v20
	v_mul_f32_e32 v49, v50, v49
	v_mul_f32_e32 v48, v50, v48
	v_mul_f32_e32 v22, v50, v22
	s_waitcnt vmcnt(1)
	v_mul_f32_e32 v21, v26, v21
	s_waitcnt vmcnt(0)
	v_mul_f32_e32 v23, v30, v23
	v_mul_f32_e32 v24, v24, v51
	v_mul_f32_e32 v25, v25, v52
	v_mul_f32_e32 v26, v27, v20
	v_mul_f32_e32 v27, v28, v49
	v_mul_f32_e32 v28, v29, v48
	v_mul_f32_e32 v29, v31, v22
	v_cvt_pk_bf16_f32 v20, v24, v25
	v_cvt_pk_bf16_f32 v21, v21, v26
	v_cvt_pk_bf16_f32 v22, v27, v28
	v_cvt_pk_bf16_f32 v23, v23, v29
	global_store_dwordx4 v58, v[20:23], s[4:5] offset:3072 sc1
	global_load_dwordx4 v[22:25], v[36:37], off offset:256
	s_nop 0
	global_load_dwordx4 v[26:29], v[36:37], off offset:272
	v_lshlrev_b32_e32 v30, 16, v16
	v_and_b32_e32 v31, 0xffff0000, v16
	v_lshlrev_b32_e32 v16, 16, v17
	v_and_b32_e32 v17, 0xffff0000, v17
	v_pk_mul_f32 v[50:51], v[30:31], v[30:31]
	v_pk_mul_f32 v[52:53], v[16:17], v[16:17]
	v_add_f32_e32 v50, v50, v51
	v_lshlrev_b32_e32 v48, 16, v18
	v_and_b32_e32 v49, 0xffff0000, v18
	v_add_f32_e32 v50, v52, v50
	v_pk_mul_f32 v[54:55], v[48:49], v[48:49]
	v_add_f32_e32 v50, v53, v50
	v_and_b32_e32 v20, 0xffff0000, v19
	v_lshlrev_b32_e32 v21, 16, v19
	v_add_f32_e32 v50, v54, v50
	v_pk_mul_f32 v[18:19], v[20:21], v[20:21]
	v_add_f32_e32 v50, v55, v50
	v_add_f32_e32 v19, v19, v50
	v_add_f32_e32 v18, v18, v19
	v_mov_b32_e32 v19, v18
	s_nop 1
	v_mov_b32_dpp v19, v19 quad_perm:[1,0,3,2] row_mask:0xf bank_mask:0xf
	v_add_f32_e32 v18, v18, v19
	v_mov_b32_e32 v19, v18
	s_nop 1
	v_mov_b32_dpp v19, v19 quad_perm:[2,3,0,1] row_mask:0xf bank_mask:0xf
	v_add_f32_e32 v18, v18, v19
	v_mov_b32_e32 v19, v18
	s_nop 1
	v_mov_b32_dpp v19, v19 row_half_mirror row_mask:0xf bank_mask:0xf
	v_add_f32_e32 v18, v18, v19
	v_fmamk_f32 v18, v18, 0x3c800000, v59
	v_mul_f32_e32 v19, 0x4b800000, v18
	v_cmp_gt_f32_e32 vcc, s43, v18
	s_nop 1
	v_cndmask_b32_e32 v18, v18, v19, vcc
	v_rsq_f32_e32 v18, v18
	s_nop 0
	v_mul_f32_e32 v19, 0x45800000, v18
	v_cndmask_b32_e32 v18, v18, v19, vcc
	v_pk_mul_f32 v[30:31], v[18:19], v[30:31] op_sel_hi:[0,1]
	v_pk_mul_f32 v[16:17], v[18:19], v[16:17] op_sel_hi:[0,1]
	v_pk_mul_f32 v[48:49], v[18:19], v[48:49] op_sel_hi:[0,1]
	v_pk_mul_f32 v[50:51], v[18:19], v[20:21] op_sel_hi:[0,1]
	s_waitcnt vmcnt(1)
	v_pk_mul_f32 v[22:23], v[22:23], v[30:31]
	v_pk_mul_f32 v[20:21], v[24:25], v[16:17]
	s_waitcnt vmcnt(0)
	v_pk_mul_f32 v[18:19], v[26:27], v[48:49]
	v_pk_mul_f32 v[16:17], v[28:29], v[50:51] op_sel:[0,1] op_sel_hi:[1,0]
	s_cbranch_scc1 .LBB0_1711
	s_add_i32 s10, s28, s25
	s_and_b32 s10, s10, 0x1ffe0
	s_lshl_b32 s10, s10, 3
	v_lshl_add_u64 v[56:57], v[38:39], 0, s[10:11]
	global_load_dwordx4 v[24:27], v[56:57], off
	global_load_dwordx4 v[28:31], v[56:57], off offset:16
	global_load_dwordx4 v[48:51], v[56:57], off offset:32
	global_load_dwordx4 v[52:55], v[56:57], off offset:48
	v_mov_b32_e32 v56, v22
	v_mov_b32_e32 v57, v23
	v_mov_b32_e32 v60, v20
	v_mov_b32_e32 v61, v21
	v_mov_b32_e32 v62, v18
	v_mov_b32_e32 v63, v19
	v_mov_b32_e32 v64, v16
	v_mov_b32_e32 v65, v17
	v_mov_b32_dpp v56, v56 row_shl:4 row_mask:0xf bank_mask:0x5
	v_mov_b32_dpp v57, v57 row_shl:4 row_mask:0xf bank_mask:0x5
	v_mov_b32_dpp v60, v60 row_shl:4 row_mask:0xf bank_mask:0x5
	v_mov_b32_dpp v61, v61 row_shl:4 row_mask:0xf bank_mask:0x5
	v_mov_b32_dpp v62, v62 row_shl:4 row_mask:0xf bank_mask:0x5
	v_mov_b32_dpp v63, v63 row_shl:4 row_mask:0xf bank_mask:0x5
	v_mov_b32_dpp v64, v64 row_shl:4 row_mask:0xf bank_mask:0x5
	v_mov_b32_dpp v65, v65 row_shl:4 row_mask:0xf bank_mask:0x5
	v_mov_b32_dpp v56, v22 row_shr:4 row_mask:0xf bank_mask:0xa
	v_mov_b32_dpp v57, v23 row_shr:4 row_mask:0xf bank_mask:0xa
	v_mov_b32_dpp v60, v20 row_shr:4 row_mask:0xf bank_mask:0xa
	v_mov_b32_dpp v61, v21 row_shr:4 row_mask:0xf bank_mask:0xa
	v_mov_b32_dpp v62, v18 row_shr:4 row_mask:0xf bank_mask:0xa
	v_mov_b32_dpp v63, v19 row_shr:4 row_mask:0xf bank_mask:0xa
	v_mov_b32_dpp v64, v16 row_shr:4 row_mask:0xf bank_mask:0xa
	v_mov_b32_dpp v65, v17 row_shr:4 row_mask:0xf bank_mask:0xa
	s_waitcnt vmcnt(3)
	v_mov_b32_e32 v67, v26
	v_mov_b32_e32 v26, v25
	s_waitcnt vmcnt(2)
	v_mov_b32_e32 v25, v30
	v_mov_b32_e32 v30, v29
	s_waitcnt vmcnt(1)
	v_mov_b32_e32 v29, v50
	v_mov_b32_e32 v50, v49
	s_waitcnt vmcnt(0)
	v_mov_b32_e32 v49, v54
	v_mov_b32_e32 v54, v53
	v_mov_b32_e32 v66, v24
	v_mov_b32_e32 v24, v28
	v_mov_b32_e32 v28, v48
	v_mov_b32_e32 v48, v52
	v_pk_mul_f32 v[26:27], v[26:27], v[56:57]
	v_pk_mul_f32 v[30:31], v[30:31], v[60:61]
	v_pk_mul_f32 v[50:51], v[50:51], v[62:63]
	v_pk_mul_f32 v[52:53], v[54:55], v[64:65]
	v_cndmask_b32_e64 v27, v27, -v27, s[0:1]
	v_cndmask_b32_e64 v26, v26, -v26, s[0:1]
	v_cndmask_b32_e64 v31, v31, -v31, s[0:1]
	v_cndmask_b32_e64 v30, v30, -v30, s[0:1]
	v_cndmask_b32_e64 v51, v51, -v51, s[0:1]
	v_cndmask_b32_e64 v50, v50, -v50, s[0:1]
	v_cndmask_b32_e64 v53, v53, -v53, s[0:1]
	v_cndmask_b32_e64 v52, v52, -v52, s[0:1]
	v_pk_fma_f32 v[22:23], v[22:23], v[66:67], v[26:27]
	v_pk_fma_f32 v[20:21], v[20:21], v[24:25], v[30:31]
	v_pk_fma_f32 v[18:19], v[18:19], v[28:29], v[50:51]
	v_pk_fma_f32 v[16:17], v[16:17], v[48:49], v[52:53]

.LBB0_1714:
	global_load_dwordx4 v[16:19], v[34:35], off offset:512
	global_load_dwordx4 v[20:23], v[34:35], off offset:528
	v_and_b32_e32 v49, 0xffff0000, v12
	v_lshlrev_b32_e32 v48, 16, v12
	v_and_b32_e32 v12, 0xffff0000, v13
	v_lshlrev_b32_e32 v13, 16, v13
	v_mul_f32_e32 v50, v49, v49
	v_pk_mul_f32 v[26:27], v[12:13], v[12:13]
	v_fmac_f32_e32 v50, v48, v48
	v_and_b32_e32 v24, 0xffff0000, v14
	v_lshlrev_b32_e32 v25, 16, v14
	v_add_f32_e32 v27, v27, v50
	v_pk_mul_f32 v[28:29], v[24:25], v[24:25]
	v_add_f32_e32 v26, v26, v27
	v_and_b32_e32 v14, 0xffff0000, v15
	v_lshlrev_b32_e32 v15, 16, v15
	v_add_f32_e32 v26, v29, v26
	v_pk_mul_f32 v[30:31], v[14:15], v[14:15]
	v_add_f32_e32 v26, v28, v26
	v_add_f32_e32 v26, v31, v26
	v_add_f32_e32 v26, v30, v26
	v_mov_b32_e32 v27, v26
	s_mul_i32 s4, s45, 0x4c00
	s_mul_hi_i32 s5, s45, 0x4c00
	v_mov_b32_dpp v27, v27 quad_perm:[1,0,3,2] row_mask:0xf bank_mask:0xf
	v_add_f32_e32 v26, v26, v27
	v_mov_b32_e32 v27, v26
	s_add_u32 s4, s8, s4
	s_addc_u32 s5, s9, s5
	v_mov_b32_dpp v27, v27 quad_perm:[2,3,0,1] row_mask:0xf bank_mask:0xf
	v_add_f32_e32 v26, v26, v27
	v_mov_b32_e32 v27, v26
	s_cmpk_gt_i32 s45, 0x1fff
	s_nop 0
	v_mov_b32_dpp v27, v27 row_half_mirror row_mask:0xf bank_mask:0xf
	v_add_f32_e32 v26, v26, v27
	v_mov_b32_e32 v27, v26
	s_nop 1
	v_mov_b32_dpp v27, v27 row_mirror row_mask:0xf bank_mask:0xf
	v_add_f32_e32 v26, v26, v27
	v_fmamk_f32 v26, v26, 0x3c000000, v59
	v_mul_f32_e32 v27, 0x4b800000, v26
	v_cmp_gt_f32_e32 vcc, s43, v26
	s_nop 1
	v_cndmask_b32_e32 v26, v26, v27, vcc
	v_rsq_f32_e32 v26, v26
	s_nop 0
	v_mul_f32_e32 v27, 0x45800000, v26
	v_cndmask_b32_e32 v26, v26, v27, vcc
	v_mul_f32_e32 v13, v26, v13
	v_mul_f32_e32 v15, v26, v15
	v_mul_f32_e32 v27, v26, v48
	v_mul_f32_e32 v28, v26, v49
	v_mul_f32_e32 v12, v26, v12
	v_mul_f32_e32 v25, v26, v25
	v_mul_f32_e32 v24, v26, v24
	v_mul_f32_e32 v14, v26, v14
	s_waitcnt vmcnt(1)
	v_mul_f32_e32 v13, v18, v13
	s_waitcnt vmcnt(0)
	v_mul_f32_e32 v15, v22, v15
	v_mul_f32_e32 v16, v16, v27
	v_mul_f32_e32 v17, v17, v28
	v_mul_f32_e32 v18, v19, v12
	v_mul_f32_e32 v19, v20, v25
	v_mul_f32_e32 v20, v21, v24
	v_mul_f32_e32 v21, v23, v14
	v_cvt_pk_bf16_f32 v12, v16, v17
	v_cvt_pk_bf16_f32 v13, v13, v18
	v_cvt_pk_bf16_f32 v14, v19, v20
	v_cvt_pk_bf16_f32 v15, v15, v21
	global_store_dwordx4 v58, v[12:15], s[4:5] offset:3072 sc1
	global_load_dwordx4 v[14:17], v[36:37], off offset:256
	s_nop 0
	global_load_dwordx4 v[18:21], v[36:37], off offset:272
	v_lshlrev_b32_e32 v22, 16, v8
	v_and_b32_e32 v23, 0xffff0000, v8
	v_lshlrev_b32_e32 v8, 16, v9
	v_and_b32_e32 v9, 0xffff0000, v9
	v_pk_mul_f32 v[26:27], v[22:23], v[22:23]
	v_pk_mul_f32 v[28:29], v[8:9], v[8:9]
	v_add_f32_e32 v26, v26, v27
	v_lshlrev_b32_e32 v24, 16, v10
	v_and_b32_e32 v25, 0xffff0000, v10
	v_add_f32_e32 v26, v28, v26
	v_pk_mul_f32 v[30:31], v[24:25], v[24:25]
	v_add_f32_e32 v26, v29, v26
	v_and_b32_e32 v12, 0xffff0000, v11
	v_lshlrev_b32_e32 v13, 16, v11
	v_add_f32_e32 v26, v30, v26
	v_pk_mul_f32 v[10:11], v[12:13], v[12:13]
	v_add_f32_e32 v26, v31, v26
	v_add_f32_e32 v11, v11, v26
	v_add_f32_e32 v10, v10, v11
	v_mov_b32_e32 v11, v10
	s_nop 1
	v_mov_b32_dpp v11, v11 quad_perm:[1,0,3,2] row_mask:0xf bank_mask:0xf
	v_add_f32_e32 v10, v10, v11
	v_mov_b32_e32 v11, v10
	s_nop 1
	v_mov_b32_dpp v11, v11 quad_perm:[2,3,0,1] row_mask:0xf bank_mask:0xf
	v_add_f32_e32 v10, v10, v11
	v_mov_b32_e32 v11, v10
	s_nop 1
	v_mov_b32_dpp v11, v11 row_half_mirror row_mask:0xf bank_mask:0xf
	v_add_f32_e32 v10, v10, v11
	v_fmamk_f32 v10, v10, 0x3c800000, v59
	v_mul_f32_e32 v11, 0x4b800000, v10
	v_cmp_gt_f32_e32 vcc, s43, v10
	s_nop 1
	v_cndmask_b32_e32 v10, v10, v11, vcc
	v_rsq_f32_e32 v10, v10
	s_nop 0
	v_mul_f32_e32 v11, 0x45800000, v10
	v_cndmask_b32_e32 v10, v10, v11, vcc
	v_pk_mul_f32 v[22:23], v[10:11], v[22:23] op_sel_hi:[0,1]
	v_pk_mul_f32 v[8:9], v[10:11], v[8:9] op_sel_hi:[0,1]
	v_pk_mul_f32 v[24:25], v[10:11], v[24:25] op_sel_hi:[0,1]
	v_pk_mul_f32 v[26:27], v[10:11], v[12:13] op_sel_hi:[0,1]
	s_waitcnt vmcnt(1)
	v_pk_mul_f32 v[14:15], v[14:15], v[22:23]
	v_pk_mul_f32 v[12:13], v[16:17], v[8:9]
	s_waitcnt vmcnt(0)
	v_pk_mul_f32 v[10:11], v[18:19], v[24:25]
	v_pk_mul_f32 v[8:9], v[20:21], v[26:27] op_sel:[0,1] op_sel_hi:[1,0]
	s_cbranch_scc1 .LBB0_1716
	s_add_i32 s10, s30, s25
	s_and_b32 s10, s10, 0x1ffe0
	s_lshl_b32 s10, s10, 3
	v_lshl_add_u64 v[48:49], v[38:39], 0, s[10:11]
	global_load_dwordx4 v[16:19], v[48:49], off
	global_load_dwordx4 v[20:23], v[48:49], off offset:16
	global_load_dwordx4 v[24:27], v[48:49], off offset:32
	global_load_dwordx4 v[28:31], v[48:49], off offset:48
	v_mov_b32_e32 v48, v14
	v_mov_b32_e32 v49, v15
	v_mov_b32_e32 v50, v12
	v_mov_b32_e32 v51, v13
	v_mov_b32_e32 v52, v10
	v_mov_b32_e32 v53, v11
	v_mov_b32_e32 v54, v8
	v_mov_b32_e32 v55, v9
	v_mov_b32_dpp v48, v48 row_shl:4 row_mask:0xf bank_mask:0x5
	v_mov_b32_dpp v49, v49 row_shl:4 row_mask:0xf bank_mask:0x5
	v_mov_b32_dpp v50, v50 row_shl:4 row_mask:0xf bank_mask:0x5
	v_mov_b32_dpp v51, v51 row_shl:4 row_mask:0xf bank_mask:0x5
	v_mov_b32_dpp v52, v52 row_shl:4 row_mask:0xf bank_mask:0x5
	v_mov_b32_dpp v53, v53 row_shl:4 row_mask:0xf bank_mask:0x5
	v_mov_b32_dpp v54, v54 row_shl:4 row_mask:0xf bank_mask:0x5
	v_mov_b32_dpp v55, v55 row_shl:4 row_mask:0xf bank_mask:0x5
	v_mov_b32_dpp v48, v14 row_shr:4 row_mask:0xf bank_mask:0xa
	v_mov_b32_dpp v49, v15 row_shr:4 row_mask:0xf bank_mask:0xa
	v_mov_b32_dpp v50, v12 row_shr:4 row_mask:0xf bank_mask:0xa
	v_mov_b32_dpp v51, v13 row_shr:4 row_mask:0xf bank_mask:0xa
	v_mov_b32_dpp v52, v10 row_shr:4 row_mask:0xf bank_mask:0xa
	v_mov_b32_dpp v53, v11 row_shr:4 row_mask:0xf bank_mask:0xa
	v_mov_b32_dpp v54, v8 row_shr:4 row_mask:0xf bank_mask:0xa
	v_mov_b32_dpp v55, v9 row_shr:4 row_mask:0xf bank_mask:0xa
	s_waitcnt vmcnt(3)
	v_mov_b32_e32 v57, v18
	v_mov_b32_e32 v18, v17
	s_waitcnt vmcnt(2)
	v_mov_b32_e32 v17, v22
	v_mov_b32_e32 v22, v21
	s_waitcnt vmcnt(1)
	v_mov_b32_e32 v21, v26
	v_mov_b32_e32 v26, v25
	s_waitcnt vmcnt(0)
	v_mov_b32_e32 v25, v30
	v_mov_b32_e32 v30, v29
	v_mov_b32_e32 v56, v16
	v_mov_b32_e32 v16, v20
	v_mov_b32_e32 v20, v24
	v_mov_b32_e32 v24, v28
	v_pk_mul_f32 v[18:19], v[18:19], v[48:49]
	v_pk_mul_f32 v[22:23], v[22:23], v[50:51]
	v_pk_mul_f32 v[26:27], v[26:27], v[52:53]
	v_pk_mul_f32 v[28:29], v[30:31], v[54:55]
	v_cndmask_b32_e64 v19, v19, -v19, s[0:1]
	v_cndmask_b32_e64 v18, v18, -v18, s[0:1]
	v_cndmask_b32_e64 v23, v23, -v23, s[0:1]
	v_cndmask_b32_e64 v22, v22, -v22, s[0:1]
	v_cndmask_b32_e64 v27, v27, -v27, s[0:1]
	v_cndmask_b32_e64 v26, v26, -v26, s[0:1]
	v_cndmask_b32_e64 v29, v29, -v29, s[0:1]
	v_cndmask_b32_e64 v28, v28, -v28, s[0:1]
	v_pk_fma_f32 v[14:15], v[14:15], v[56:57], v[18:19]
	v_pk_fma_f32 v[12:13], v[12:13], v[16:17], v[22:23]
	v_pk_fma_f32 v[10:11], v[10:11], v[20:21], v[26:27]
	v_pk_fma_f32 v[8:9], v[8:9], v[24:25], v[28:29]

.LBB0_1719:
	global_load_dwordx4 v[8:11], v[34:35], off offset:512
	global_load_dwordx4 v[12:15], v[34:35], off offset:528
	v_and_b32_e32 v25, 0xffff0000, v4
	v_lshlrev_b32_e32 v24, 16, v4
	v_and_b32_e32 v4, 0xffff0000, v5
	v_lshlrev_b32_e32 v5, 16, v5
	v_mul_f32_e32 v26, v25, v25
	v_pk_mul_f32 v[18:19], v[4:5], v[4:5]
	v_fmac_f32_e32 v26, v24, v24
	v_and_b32_e32 v16, 0xffff0000, v6
	v_lshlrev_b32_e32 v17, 16, v6
	v_add_f32_e32 v19, v19, v26
	v_pk_mul_f32 v[20:21], v[16:17], v[16:17]
	v_add_f32_e32 v18, v18, v19
	v_and_b32_e32 v6, 0xffff0000, v7
	v_lshlrev_b32_e32 v7, 16, v7
	v_add_f32_e32 v18, v21, v18
	v_pk_mul_f32 v[22:23], v[6:7], v[6:7]
	v_add_f32_e32 v18, v20, v18
	v_add_f32_e32 v18, v23, v18
	v_add_f32_e32 v18, v22, v18
	v_mov_b32_e32 v19, v18
	s_mul_i32 s4, s44, 0x4c00
	s_mul_hi_i32 s5, s44, 0x4c00
	v_mov_b32_dpp v19, v19 quad_perm:[1,0,3,2] row_mask:0xf bank_mask:0xf
	v_add_f32_e32 v18, v18, v19
	v_mov_b32_e32 v19, v18
	s_add_u32 s4, s8, s4
	s_addc_u32 s5, s9, s5
	v_mov_b32_dpp v19, v19 quad_perm:[2,3,0,1] row_mask:0xf bank_mask:0xf
	v_add_f32_e32 v18, v18, v19
	v_mov_b32_e32 v19, v18
	s_cmpk_gt_i32 s44, 0x1fff
	s_nop 0
	v_mov_b32_dpp v19, v19 row_half_mirror row_mask:0xf bank_mask:0xf
	v_add_f32_e32 v18, v18, v19
	v_mov_b32_e32 v19, v18
	s_nop 1
	v_mov_b32_dpp v19, v19 row_mirror row_mask:0xf bank_mask:0xf
	v_add_f32_e32 v18, v18, v19
	v_fmamk_f32 v18, v18, 0x3c000000, v59
	v_mul_f32_e32 v19, 0x4b800000, v18
	v_cmp_gt_f32_e32 vcc, s43, v18
	s_nop 1
	v_cndmask_b32_e32 v18, v18, v19, vcc
	v_rsq_f32_e32 v18, v18
	s_nop 0
	v_mul_f32_e32 v19, 0x45800000, v18
	v_cndmask_b32_e32 v18, v18, v19, vcc
	v_mul_f32_e32 v5, v18, v5
	v_mul_f32_e32 v7, v18, v7
	v_mul_f32_e32 v19, v18, v24
	v_mul_f32_e32 v20, v18, v25
	v_mul_f32_e32 v4, v18, v4
	v_mul_f32_e32 v17, v18, v17
	v_mul_f32_e32 v16, v18, v16
	v_mul_f32_e32 v6, v18, v6
	s_waitcnt vmcnt(1)
	v_mul_f32_e32 v5, v10, v5
	s_waitcnt vmcnt(0)
	v_mul_f32_e32 v7, v14, v7
	v_mul_f32_e32 v8, v8, v19
	v_mul_f32_e32 v9, v9, v20
	v_mul_f32_e32 v10, v11, v4
	v_mul_f32_e32 v11, v12, v17
	v_mul_f32_e32 v12, v13, v16
	v_mul_f32_e32 v13, v15, v6
	v_cvt_pk_bf16_f32 v4, v8, v9
	v_cvt_pk_bf16_f32 v5, v5, v10
	v_cvt_pk_bf16_f32 v6, v11, v12
	v_cvt_pk_bf16_f32 v7, v7, v13
	global_store_dwordx4 v58, v[4:7], s[4:5] offset:3072 sc1
	global_load_dwordx4 v[6:9], v[36:37], off offset:256
	s_nop 0
	global_load_dwordx4 v[10:13], v[36:37], off offset:272
	v_lshlrev_b32_e32 v14, 16, v0
	v_and_b32_e32 v15, 0xffff0000, v0
	v_lshlrev_b32_e32 v0, 16, v1
	v_and_b32_e32 v1, 0xffff0000, v1
	v_pk_mul_f32 v[18:19], v[14:15], v[14:15]
	v_pk_mul_f32 v[20:21], v[0:1], v[0:1]
	v_add_f32_e32 v18, v18, v19
	v_lshlrev_b32_e32 v16, 16, v2
	v_and_b32_e32 v17, 0xffff0000, v2
	v_add_f32_e32 v18, v20, v18
	v_pk_mul_f32 v[22:23], v[16:17], v[16:17]
	v_add_f32_e32 v18, v21, v18
	v_and_b32_e32 v4, 0xffff0000, v3
	v_lshlrev_b32_e32 v5, 16, v3
	v_add_f32_e32 v18, v22, v18
	v_pk_mul_f32 v[2:3], v[4:5], v[4:5]
	v_add_f32_e32 v18, v23, v18
	v_add_f32_e32 v3, v3, v18
	v_add_f32_e32 v2, v2, v3
	v_mov_b32_e32 v3, v2
	s_nop 1
	v_mov_b32_dpp v3, v3 quad_perm:[1,0,3,2] row_mask:0xf bank_mask:0xf
	v_add_f32_e32 v2, v2, v3
	v_mov_b32_e32 v3, v2
	s_nop 1
	v_mov_b32_dpp v3, v3 quad_perm:[2,3,0,1] row_mask:0xf bank_mask:0xf
	v_add_f32_e32 v2, v2, v3
	v_mov_b32_e32 v3, v2
	s_nop 1
	v_mov_b32_dpp v3, v3 row_half_mirror row_mask:0xf bank_mask:0xf
	v_add_f32_e32 v2, v2, v3
	v_fmamk_f32 v2, v2, 0x3c800000, v59
	v_mul_f32_e32 v3, 0x4b800000, v2
	v_cmp_gt_f32_e32 vcc, s43, v2
	s_nop 1
	v_cndmask_b32_e32 v2, v2, v3, vcc
	v_rsq_f32_e32 v2, v2
	s_nop 0
	v_mul_f32_e32 v3, 0x45800000, v2
	v_cndmask_b32_e32 v2, v2, v3, vcc
	v_pk_mul_f32 v[14:15], v[2:3], v[14:15] op_sel_hi:[0,1]
	v_pk_mul_f32 v[0:1], v[2:3], v[0:1] op_sel_hi:[0,1]
	v_pk_mul_f32 v[16:17], v[2:3], v[16:17] op_sel_hi:[0,1]
	v_pk_mul_f32 v[18:19], v[2:3], v[4:5] op_sel_hi:[0,1]
	s_waitcnt vmcnt(1)
	v_pk_mul_f32 v[6:7], v[6:7], v[14:15]
	v_pk_mul_f32 v[4:5], v[8:9], v[0:1]
	s_waitcnt vmcnt(0)
	v_pk_mul_f32 v[2:3], v[10:11], v[16:17]
	v_pk_mul_f32 v[0:1], v[12:13], v[18:19] op_sel:[0,1] op_sel_hi:[1,0]
	s_cbranch_scc1 .LBB0_1721
	s_add_i32 s10, s38, s25
	s_and_b32 s10, s10, 0x1ffe0
	s_lshl_b32 s10, s10, 3
	v_lshl_add_u64 v[24:25], v[38:39], 0, s[10:11]
	global_load_dwordx4 v[8:11], v[24:25], off
	global_load_dwordx4 v[12:15], v[24:25], off offset:16
	global_load_dwordx4 v[16:19], v[24:25], off offset:32
	global_load_dwordx4 v[20:23], v[24:25], off offset:48
	v_mov_b32_e32 v24, v6
	v_mov_b32_e32 v25, v7
	v_mov_b32_e32 v26, v4
	v_mov_b32_e32 v27, v5
	v_mov_b32_e32 v28, v2
	v_mov_b32_e32 v29, v3
	v_mov_b32_e32 v30, v0
	v_mov_b32_e32 v31, v1
	v_mov_b32_dpp v24, v24 row_shl:4 row_mask:0xf bank_mask:0x5
	v_mov_b32_dpp v25, v25 row_shl:4 row_mask:0xf bank_mask:0x5
	v_mov_b32_dpp v26, v26 row_shl:4 row_mask:0xf bank_mask:0x5
	v_mov_b32_dpp v27, v27 row_shl:4 row_mask:0xf bank_mask:0x5
	v_mov_b32_dpp v28, v28 row_shl:4 row_mask:0xf bank_mask:0x5
	v_mov_b32_dpp v29, v29 row_shl:4 row_mask:0xf bank_mask:0x5
	v_mov_b32_dpp v30, v30 row_shl:4 row_mask:0xf bank_mask:0x5
	v_mov_b32_dpp v31, v31 row_shl:4 row_mask:0xf bank_mask:0x5
	v_mov_b32_dpp v24, v6 row_shr:4 row_mask:0xf bank_mask:0xa
	v_mov_b32_dpp v25, v7 row_shr:4 row_mask:0xf bank_mask:0xa
	v_mov_b32_dpp v26, v4 row_shr:4 row_mask:0xf bank_mask:0xa
	v_mov_b32_dpp v27, v5 row_shr:4 row_mask:0xf bank_mask:0xa
	v_mov_b32_dpp v28, v2 row_shr:4 row_mask:0xf bank_mask:0xa
	v_mov_b32_dpp v29, v3 row_shr:4 row_mask:0xf bank_mask:0xa
	v_mov_b32_dpp v30, v0 row_shr:4 row_mask:0xf bank_mask:0xa
	v_mov_b32_dpp v31, v1 row_shr:4 row_mask:0xf bank_mask:0xa
	s_waitcnt vmcnt(3)
	v_mov_b32_e32 v49, v10
	v_mov_b32_e32 v10, v9
	s_waitcnt vmcnt(2)
	v_mov_b32_e32 v9, v14
	v_mov_b32_e32 v14, v13
	s_waitcnt vmcnt(1)
	v_mov_b32_e32 v13, v18
	v_mov_b32_e32 v18, v17
	s_waitcnt vmcnt(0)
	v_mov_b32_e32 v17, v22
	v_mov_b32_e32 v22, v21
	v_mov_b32_e32 v48, v8
	v_mov_b32_e32 v8, v12
	v_mov_b32_e32 v12, v16
	v_mov_b32_e32 v16, v20
	v_pk_mul_f32 v[10:11], v[10:11], v[24:25]
	v_pk_mul_f32 v[14:15], v[14:15], v[26:27]
	v_pk_mul_f32 v[18:19], v[18:19], v[28:29]
	v_pk_mul_f32 v[20:21], v[22:23], v[30:31]
	v_cndmask_b32_e64 v11, v11, -v11, s[0:1]
	v_cndmask_b32_e64 v10, v10, -v10, s[0:1]
	v_cndmask_b32_e64 v15, v15, -v15, s[0:1]
	v_cndmask_b32_e64 v14, v14, -v14, s[0:1]
	v_cndmask_b32_e64 v19, v19, -v19, s[0:1]
	v_cndmask_b32_e64 v18, v18, -v18, s[0:1]
	v_cndmask_b32_e64 v21, v21, -v21, s[0:1]
	v_cndmask_b32_e64 v20, v20, -v20, s[0:1]
	v_pk_fma_f32 v[6:7], v[6:7], v[48:49], v[10:11]
	v_pk_fma_f32 v[4:5], v[4:5], v[8:9], v[14:15]
	v_pk_fma_f32 v[2:3], v[2:3], v[12:13], v[18:19]
	v_pk_fma_f32 v[0:1], v[0:1], v[16:17], v[20:21]

.LBB0_1939:
	s_add_i32 s92, s38, s65
	s_add_i32 s0, s92, 0x9989
	s_mul_hi_i32 s2, s0, 0x20d56b39
	s_lshr_b32 s3, s2, 31
	s_ashr_i32 s2, s2, 12
	s_add_i32 s2, s2, s3
	s_mul_i32 s3, s2, 0x7cc0
	s_sub_i32 s30, s0, s3
	s_cmpk_gt_i32 s30, 0x1cbf
	s_mov_b64 s[4:5], -1
	s_cbranch_scc0 .LBB0_1945
	s_add_i32 s9, s30, 0xffffe340
	s_and_b32 s8, s9, 0xff
	s_cmpk_gt_u32 s30, 0x5cbf
	s_cbranch_scc0 .LBB0_1942
	v_mov_b32_e32 v0, s61
	s_add_i32 s0, s30, 0xffffa340
	s_ashr_i32 s3, s2, 31
	ds_read_b64 v[0:1], v0
	s_lshr_b32 s0, s0, 8
	s_lshl_b64 s[4:5], s[2:3], 26
	s_add_u32 s10, s41, s4
	s_addc_u32 s11, s44, s5
	s_lshl_b64 s[4:5], s[0:1], 20
	s_add_u32 s4, s10, s4
	s_addc_u32 s5, s11, s5
	s_waitcnt lgkmcnt(0)
	v_readfirstlane_b32 s12, v0
	s_lshl_b64 s[10:11], s[2:3], 27
	v_readfirstlane_b32 s13, v1
	s_add_u32 s3, s12, s10
	s_addc_u32 s13, s13, s11
	s_lshl_b64 s[10:11], s[0:1], 22
	s_add_u32 s12, s3, s10
	s_addc_u32 s13, s13, s11
	s_lshl_b32 s0, s8, 3
	s_and_b32 s3, s0, 0x7c0
	s_lshl_b32 s0, s30, 6
	s_and_b32 s10, s0, 0x1c0
	v_or_b32_e32 v0, s10, v82
	v_lshlrev_b32_e32 v0, 13, v0
	v_mov_b32_e32 v1, v77
	v_lshl_add_u64 v[0:1], s[12:13], 0, v[0:1]
	s_lshl_b32 s0, s3, 2
	v_lshl_add_u64 v[0:1], v[0:1], 0, s[0:1]
	v_mov_b32_e32 v81, v77
	v_lshl_add_u64 v[60:61], v[0:1], 0, v[80:81]
	v_add_co_u32_e32 v4, vcc, s62, v60
	s_mov_b32 s0, 0x8000
	s_nop 0
	v_addc_co_u32_e32 v5, vcc, 0, v61, vcc
	v_add_co_u32_e32 v8, vcc, s63, v60
	global_load_dwordx4 v[0:3], v[60:61], off nt
	s_nop 0
	global_load_dwordx4 v[4:7], v[4:5], off nt
	v_addc_co_u32_e32 v9, vcc, 0, v61, vcc
	v_add_co_u32_e32 v10, vcc, s64, v60
	v_mov_b32_e32 v64, v77
	s_nop 0
	v_addc_co_u32_e32 v11, vcc, 0, v61, vcc
	v_add_co_u32_e32 v16, vcc, s0, v60
	s_mov_b32 s0, 0xa000
	s_nop 0
	v_addc_co_u32_e32 v17, vcc, 0, v61, vcc
	v_add_co_u32_e32 v20, vcc, s0, v60
	s_mov_b32 s0, 0xc000
	s_nop 0
	v_addc_co_u32_e32 v21, vcc, 0, v61, vcc
	v_add_co_u32_e32 v24, vcc, s0, v60
	s_mov_b32 s0, 0xe000
	s_nop 0
	v_addc_co_u32_e32 v25, vcc, 0, v61, vcc
	global_load_dwordx4 v[12:15], v[8:9], off nt
	s_nop 0
	global_load_dwordx4 v[8:11], v[10:11], off nt
	v_add_co_u32_e32 v26, vcc, s0, v60
	s_mov_b32 s0, 0x10000
	s_nop 0
	v_addc_co_u32_e32 v27, vcc, 0, v61, vcc
	global_load_dwordx4 v[16:19], v[16:17], off nt
	s_nop 0
	global_load_dwordx4 v[20:23], v[20:21], off nt
	v_add_co_u32_e32 v28, vcc, s0, v60
	s_mov_b32 s0, 0x14000
	s_nop 0
	v_addc_co_u32_e32 v29, vcc, 0, v61, vcc
	v_add_co_u32_e32 v36, vcc, s66, v60
	global_load_dwordx4 v[32:35], v[24:25], off nt
	s_nop 0
	global_load_dwordx4 v[24:27], v[26:27], off nt
	v_addc_co_u32_e32 v37, vcc, 0, v61, vcc
	v_add_co_u32_e32 v40, vcc, s0, v60
	s_mov_b32 s0, 0x16000
	s_nop 0
	v_addc_co_u32_e32 v41, vcc, 0, v61, vcc
	global_load_dwordx4 v[28:31], v[28:29], off nt
	s_nop 0
	global_load_dwordx4 v[36:39], v[36:37], off nt
	v_add_co_u32_e32 v42, vcc, s0, v60
	s_mov_b32 s0, 0x18000
	s_nop 0
	v_addc_co_u32_e32 v43, vcc, 0, v61, vcc
	v_add_co_u32_e32 v48, vcc, s0, v60
	s_mov_b32 s0, 0x1a000
	s_nop 0
	v_addc_co_u32_e32 v49, vcc, 0, v61, vcc
	global_load_dwordx4 v[44:47], v[40:41], off nt
	s_nop 0
	global_load_dwordx4 v[40:43], v[42:43], off nt
	v_add_co_u32_e32 v52, vcc, s0, v60
	s_mov_b32 s0, 0x1c000
	s_nop 0
	v_addc_co_u32_e32 v53, vcc, 0, v61, vcc
	global_load_dwordx4 v[48:51], v[48:49], off nt
	s_nop 0
	global_load_dwordx4 v[52:55], v[52:53], off nt
	v_add_co_u32_e32 v56, vcc, s0, v60
	s_mov_b32 s0, 0x1e000
	s_nop 0
	v_addc_co_u32_e32 v57, vcc, 0, v61, vcc
	v_add_co_u32_e32 v60, vcc, s0, v60
	global_load_dwordx4 v[56:59], v[56:57], off nt
	s_nop 0
	v_addc_co_u32_e32 v61, vcc, 0, v61, vcc
	global_load_dwordx4 v[60:63], v[60:61], off nt
	v_mov_b32_e32 v65, v77
	v_mov_b32_e32 v66, v77
	v_mov_b32_e32 v67, v77
	v_mov_b32_e32 v68, v77
	v_mov_b32_e32 v69, v77
	s_waitcnt vmcnt(15)
	v_mul_f32_e32 v0, 0x42000000, v0
	s_waitcnt vmcnt(14)
	v_mul_f32_e32 v4, 0x42000000, v4
	v_med3_f32 v0, v0, s67, v98
	v_med3_f32 v4, v4, s67, v98
	v_cvt_pk_fp8_f32 v64, v0, v4
	v_mov_b32_e32 v70, v77
	v_mov_b32_e32 v71, v77
	v_mov_b32_e32 v72, v77
	v_mov_b32_e32 v73, v77
	v_mov_b32_e32 v74, v77
	v_mov_b32_e32 v75, v77
	s_add_u32 s4, s4, s10
	s_addc_u32 s5, s5, 0
	s_waitcnt vmcnt(13)
	v_mul_f32_e32 v12, 0x42000000, v12
	s_waitcnt vmcnt(12)
	v_mul_f32_e32 v0, 0x42000000, v8
	v_med3_f32 v4, v12, s67, v98
	v_med3_f32 v0, v0, s67, v98
	v_cvt_pk_fp8_f32 v64, v4, v0 op_sel:[0,0,1]
	s_waitcnt vmcnt(11)
	v_mul_f32_e32 v0, 0x42000000, v16
	s_waitcnt vmcnt(10)
	v_mul_f32_e32 v4, 0x42000000, v20
	v_med3_f32 v0, v0, s67, v98
	v_med3_f32 v4, v4, s67, v98
	v_cvt_pk_fp8_f32 v65, v0, v4
	s_waitcnt vmcnt(9)
	v_mul_f32_e32 v8, 0x42000000, v32
	s_waitcnt vmcnt(8)
	v_mul_f32_e32 v0, 0x42000000, v24
	v_med3_f32 v4, v8, s67, v98
	v_med3_f32 v0, v0, s67, v98
	v_cvt_pk_fp8_f32 v65, v4, v0 op_sel:[0,0,1]
	s_waitcnt vmcnt(7)
	v_mul_f32_e32 v0, 0x42000000, v28
	s_waitcnt vmcnt(6)
	v_mul_f32_e32 v4, 0x42000000, v36
	v_med3_f32 v0, v0, s67, v98
	v_med3_f32 v4, v4, s67, v98
	v_cvt_pk_fp8_f32 v66, v0, v4
	s_waitcnt vmcnt(5)
	v_mul_f32_e32 v8, 0x42000000, v44
	s_waitcnt vmcnt(4)
	v_mul_f32_e32 v0, 0x42000000, v40
	v_med3_f32 v4, v8, s67, v98
	v_med3_f32 v0, v0, s67, v98
	v_cvt_pk_fp8_f32 v66, v4, v0 op_sel:[0,0,1]
	s_waitcnt vmcnt(3)
	v_mul_f32_e32 v0, 0x42000000, v48
	s_waitcnt vmcnt(2)
	v_mul_f32_e32 v4, 0x42000000, v52
	v_med3_f32 v0, v0, s67, v98
	v_med3_f32 v4, v4, s67, v98
	v_cvt_pk_fp8_f32 v67, v0, v4
	s_waitcnt vmcnt(1)
	v_mul_f32_e32 v8, 0x42000000, v56
	v_med3_f32 v4, v8, s67, v98
	s_waitcnt vmcnt(0)
	v_mul_f32_e32 v0, 0x42000000, v60
	v_med3_f32 v0, v0, s67, v98
	v_cvt_pk_fp8_f32 v67, v4, v0 op_sel:[0,0,1]
	v_mul_f32_e32 v0, 0x42000000, v1
	v_mul_f32_e32 v1, 0x42000000, v5
	v_med3_f32 v0, v0, s67, v98
	v_med3_f32 v1, v1, s67, v98
	v_cvt_pk_fp8_f32 v68, v0, v1
	v_mul_f32_e32 v4, 0x42000000, v13
	v_mul_f32_e32 v0, 0x42000000, v9
	v_med3_f32 v1, v4, s67, v98
	v_med3_f32 v0, v0, s67, v98
	v_cvt_pk_fp8_f32 v68, v1, v0 op_sel:[0,0,1]
	v_mul_f32_e32 v0, 0x42000000, v17
	v_mul_f32_e32 v1, 0x42000000, v21
	v_med3_f32 v0, v0, s67, v98
	v_med3_f32 v1, v1, s67, v98
	v_cvt_pk_fp8_f32 v69, v0, v1
	v_mul_f32_e32 v4, 0x42000000, v33
	v_mul_f32_e32 v0, 0x42000000, v25
	v_med3_f32 v1, v4, s67, v98
	v_med3_f32 v0, v0, s67, v98
	v_cvt_pk_fp8_f32 v69, v1, v0 op_sel:[0,0,1]
	v_mul_f32_e32 v0, 0x42000000, v29
	v_mul_f32_e32 v1, 0x42000000, v37
	v_med3_f32 v0, v0, s67, v98
	v_med3_f32 v1, v1, s67, v98
	v_cvt_pk_fp8_f32 v70, v0, v1
	v_mul_f32_e32 v4, 0x42000000, v45
	v_mul_f32_e32 v0, 0x42000000, v41
	v_med3_f32 v1, v4, s67, v98
	v_med3_f32 v0, v0, s67, v98
	v_cvt_pk_fp8_f32 v70, v1, v0 op_sel:[0,0,1]
	v_mul_f32_e32 v0, 0x42000000, v49
	v_mul_f32_e32 v1, 0x42000000, v53
	v_med3_f32 v0, v0, s67, v98
	v_med3_f32 v1, v1, s67, v98
	v_cvt_pk_fp8_f32 v71, v0, v1
	v_mul_f32_e32 v4, 0x42000000, v57
	v_mul_f32_e32 v0, 0x42000000, v61
	v_med3_f32 v1, v4, s67, v98
	v_med3_f32 v0, v0, s67, v98
	v_cvt_pk_fp8_f32 v71, v1, v0 op_sel:[0,0,1]
	v_mul_f32_e32 v0, 0x42000000, v2
	v_mul_f32_e32 v1, 0x42000000, v6
	v_med3_f32 v0, v0, s67, v98
	v_med3_f32 v1, v1, s67, v98
	v_cvt_pk_fp8_f32 v72, v0, v1
	v_mul_f32_e32 v2, 0x42000000, v14
	v_mul_f32_e32 v0, 0x42000000, v10
	v_med3_f32 v1, v2, s67, v98
	v_med3_f32 v0, v0, s67, v98
	v_cvt_pk_fp8_f32 v72, v1, v0 op_sel:[0,0,1]
	v_mul_f32_e32 v0, 0x42000000, v18
	v_mul_f32_e32 v1, 0x42000000, v22
	v_med3_f32 v0, v0, s67, v98
	v_med3_f32 v1, v1, s67, v98
	v_cvt_pk_fp8_f32 v73, v0, v1
	v_mul_f32_e32 v2, 0x42000000, v34
	v_mul_f32_e32 v0, 0x42000000, v26
	v_med3_f32 v1, v2, s67, v98
	v_med3_f32 v0, v0, s67, v98
	v_cvt_pk_fp8_f32 v73, v1, v0 op_sel:[0,0,1]
	v_mul_f32_e32 v0, 0x42000000, v30
	v_mul_f32_e32 v1, 0x42000000, v38
	v_med3_f32 v0, v0, s67, v98
	v_med3_f32 v1, v1, s67, v98
	v_cvt_pk_fp8_f32 v74, v0, v1
	v_mul_f32_e32 v2, 0x42000000, v46
	v_mul_f32_e32 v0, 0x42000000, v42
	v_med3_f32 v1, v2, s67, v98
	v_med3_f32 v0, v0, s67, v98
	v_cvt_pk_fp8_f32 v74, v1, v0 op_sel:[0,0,1]
	v_mul_f32_e32 v0, 0x42000000, v50
	v_mul_f32_e32 v1, 0x42000000, v54
	v_med3_f32 v0, v0, s67, v98
	v_med3_f32 v1, v1, s67, v98
	v_cvt_pk_fp8_f32 v75, v0, v1
	v_mul_f32_e32 v2, 0x42000000, v58
	v_mul_f32_e32 v0, 0x42000000, v62
	v_med3_f32 v1, v2, s67, v98
	v_med3_f32 v0, v0, s67, v98
	v_cvt_pk_fp8_f32 v75, v1, v0 op_sel:[0,0,1]
	v_mul_f32_e32 v0, 0x42000000, v3
	v_mul_f32_e32 v1, 0x42000000, v7
	v_med3_f32 v3, v0, s67, v98
	v_med3_f32 v1, v1, s67, v98
	v_mov_b32_e32 v0, v77
	v_cvt_pk_fp8_f32 v0, v3, v1
	v_mul_f32_e32 v2, 0x42000000, v15
	v_mul_f32_e32 v1, 0x42000000, v11
	v_med3_f32 v2, v2, s67, v98
	v_med3_f32 v1, v1, s67, v98
	v_cvt_pk_fp8_f32 v0, v2, v1 op_sel:[0,0,1]
	v_mul_f32_e32 v1, 0x42000000, v19
	v_mul_f32_e32 v2, 0x42000000, v23
	v_med3_f32 v4, v1, s67, v98
	v_med3_f32 v2, v2, s67, v98
	v_mov_b32_e32 v1, v77
	v_cvt_pk_fp8_f32 v1, v4, v2
	v_mul_f32_e32 v3, 0x42000000, v35
	v_mul_f32_e32 v2, 0x42000000, v27
	v_med3_f32 v3, v3, s67, v98
	v_med3_f32 v2, v2, s67, v98
	v_cvt_pk_fp8_f32 v1, v3, v2 op_sel:[0,0,1]
	v_mul_f32_e32 v2, 0x42000000, v31
	v_mul_f32_e32 v3, 0x42000000, v39
	v_med3_f32 v5, v2, s67, v98
	v_med3_f32 v3, v3, s67, v98
	v_mov_b32_e32 v2, v77
	v_cvt_pk_fp8_f32 v2, v5, v3
	v_mul_f32_e32 v4, 0x42000000, v47
	v_mul_f32_e32 v3, 0x42000000, v43
	v_med3_f32 v4, v4, s67, v98
	v_med3_f32 v3, v3, s67, v98
	v_cvt_pk_fp8_f32 v2, v4, v3 op_sel:[0,0,1]
	v_mul_f32_e32 v3, 0x42000000, v51
	v_mul_f32_e32 v4, 0x42000000, v55
	v_med3_f32 v6, v3, s67, v98
	v_med3_f32 v4, v4, s67, v98
	v_mov_b32_e32 v3, v77
	v_cvt_pk_fp8_f32 v3, v6, v4
	v_mul_f32_e32 v5, 0x42000000, v59
	v_mul_f32_e32 v4, 0x42000000, v63
	v_med3_f32 v5, v5, s67, v98
	v_med3_f32 v4, v4, s67, v98
	v_cvt_pk_fp8_f32 v3, v5, v4 op_sel:[0,0,1]
	ds_write_b128 v95, v[64:67] offset:40960
	ds_write_b128 v95, v[68:71] offset:41040
	ds_write_b128 v95, v[72:75] offset:41120
	ds_write_b128 v95, v[0:3] offset:41200
	s_waitcnt lgkmcnt(0)
	ds_read_b128 v[0:3], v96 offset:40960
	v_or_b32_e32 v4, s3, v83
	v_lshl_add_u64 v[8:9], s[4:5], 0, v[78:79]
	v_lshlrev_b32_e32 v4, 9, v4
	v_mov_b32_e32 v5, v77
	v_lshl_add_u64 v[10:11], v[8:9], 0, v[4:5]
	ds_read_b128 v[4:7], v96 offset:42240
	s_waitcnt lgkmcnt(1)
	global_store_dwordx4 v[10:11], v[0:3], off sc1
	s_mov_b64 s[4:5], 0
	s_nop 0
	v_or_b32_e32 v0, s3, v84
	v_lshlrev_b32_e32 v0, 9, v0
	v_mov_b32_e32 v1, v77
	v_lshl_add_u64 v[0:1], v[8:9], 0, v[0:1]
	s_waitcnt lgkmcnt(0)
	global_store_dwordx4 v[0:1], v[4:7], off sc1
	ds_read_b128 v[0:3], v96 offset:43520
	s_nop 0
	v_or_b32_e32 v4, s3, v85
	v_lshlrev_b32_e32 v4, 9, v4
	v_mov_b32_e32 v5, v77
	v_lshl_add_u64 v[10:11], v[8:9], 0, v[4:5]
	ds_read_b128 v[4:7], v96 offset:44800
	s_waitcnt lgkmcnt(1)
	global_store_dwordx4 v[10:11], v[0:3], off sc1
	s_nop 1
	v_or_b32_e32 v0, s3, v86
	v_lshlrev_b32_e32 v0, 9, v0
	v_mov_b32_e32 v1, v77
	v_lshl_add_u64 v[0:1], v[8:9], 0, v[0:1]
	s_waitcnt lgkmcnt(0)
	global_store_dwordx4 v[0:1], v[4:7], off sc1
	s_waitcnt lgkmcnt(0)
.LBB0_1942:
	s_andn2_b64 vcc, exec, s[4:5]
	s_cbranch_vccnz .LBB0_1944
	s_ashr_i32 s3, s2, 31
	s_lshr_b32 s0, s9, 9
	s_bfe_u32 s9, s9, 0x10008
	s_lshl_b64 s[10:11], s[2:3], 27
	s_add_u32 s3, s45, s10
	s_addc_u32 s12, s46, s11
	s_lshl_b32 s13, s9, 18
	s_lshl_b64 s[4:5], s[0:1], 21
	s_add_u32 s3, s3, s4
	s_addc_u32 s4, s12, s5
	s_add_u32 s3, s3, s13
	s_addc_u32 s4, s4, 0
	s_lshl_b32 s5, s9, 3
	s_add_i32 s5, s5, 0
	s_add_i32 s5, s5, 0x204e8
	v_mov_b32_e32 v0, s5
	ds_read_b64 v[0:1], v0
	v_mov_b32_e32 v81, v77
	v_mov_b32_e32 v12, v77
	v_mov_b32_e32 v14, v77
	v_mov_b32_e32 v13, v77
	s_waitcnt lgkmcnt(0)
	v_readfirstlane_b32 s5, v0
	v_readfirstlane_b32 s9, v1
	s_add_u32 s5, s5, s10
	s_addc_u32 s9, s9, s11
	s_lshl_b64 s[10:11], s[0:1], 22
	s_add_u32 s10, s5, s10
	s_addc_u32 s11, s9, s11
	s_lshl_b32 s0, s30, 6
	s_and_b32 s5, s0, 0x7c0
	v_or_b32_e32 v0, s5, v82
	v_lshlrev_b32_e32 v0, 11, v0
	v_mov_b32_e32 v1, v77
	s_lshl_b32 s0, s8, 3
	v_lshl_add_u64 v[0:1], s[10:11], 0, v[0:1]
	s_and_b32 s0, s0, 0x700
	v_lshl_add_u64 v[0:1], v[0:1], 0, s[0:1]
	v_lshl_add_u64 v[0:1], v[0:1], 0, v[80:81]
	s_movk_i32 s0, 0x1000
	v_add_co_u32_e32 v2, vcc, s0, v0
	global_load_dwordx4 v[36:39], v[0:1], off nt
	global_load_dwordx4 v[40:43], v[0:1], off offset:2048 nt
	v_addc_co_u32_e32 v3, vcc, 0, v1, vcc
	v_add_co_u32_e32 v4, vcc, s62, v0
	v_mov_b32_e32 v68, v77
	s_nop 0
	v_addc_co_u32_e32 v5, vcc, 0, v1, vcc
	global_load_dwordx4 v[56:59], v[4:5], off offset:-4096 nt
	global_load_dwordx4 v[20:23], v[4:5], off nt
	global_load_dwordx4 v[24:27], v[4:5], off offset:2048 nt
	v_add_co_u32_e32 v4, vcc, s68, v0
	v_mov_b32_e32 v69, v77
	s_nop 0
	v_addc_co_u32_e32 v5, vcc, 0, v1, vcc
	v_add_co_u32_e32 v6, vcc, s63, v0
	v_mov_b32_e32 v70, v77
	s_nop 0
	v_addc_co_u32_e32 v7, vcc, 0, v1, vcc
	global_load_dwordx4 v[64:67], v[2:3], off offset:2048 nt
	global_load_dwordx4 v[44:47], v[4:5], off offset:2048 nt
	global_load_dwordx4 v[60:63], v[6:7], off offset:-4096 nt
	global_load_dwordx4 v[16:19], v[6:7], off nt
	v_add_co_u32_e32 v2, vcc, s69, v0
	v_mov_b32_e32 v71, v77
	s_nop 0
	v_addc_co_u32_e32 v3, vcc, 0, v1, vcc
	v_add_co_u32_e32 v8, vcc, s64, v0
	v_mov_b32_e32 v72, v77
	s_nop 0
	v_addc_co_u32_e32 v9, vcc, 0, v1, vcc
	global_load_dwordx4 v[48:51], v[6:7], off offset:2048 nt
	global_load_dwordx4 v[52:55], v[8:9], off offset:-4096 nt
	global_load_dwordx4 v[28:31], v[2:3], off offset:2048 nt
	s_nop 0
	global_load_dwordx4 v[4:7], v[8:9], off nt
	s_nop 0
	global_load_dwordx4 v[8:11], v[8:9], off offset:2048 nt
	v_add_co_u32_e32 v0, vcc, s70, v0
	v_mov_b32_e32 v73, v77
	s_nop 0
	v_addc_co_u32_e32 v1, vcc, 0, v1, vcc
	global_load_dwordx4 v[32:35], v[0:1], off nt
	s_nop 0
	global_load_dwordx4 v[0:3], v[0:1], off offset:2048 nt
	v_mov_b32_e32 v74, v77
	v_mov_b32_e32 v75, v77
	s_lshl_b32 s0, s8, 1
	s_add_u32 s10, s3, s5
	s_addc_u32 s11, s4, 0
	s_lshl_b32 s3, s8, 2
	s_and_b32 s3, s3, 0x300
	s_and_b32 s0, s0, 64
	s_or_b32 s0, s0, s3
	s_waitcnt vmcnt(15)
	v_mul_f32_e32 v15, 0x42800000, v36
	s_waitcnt vmcnt(14)
	v_mul_f32_e32 v36, 0x42800000, v40
	v_med3_f32 v15, v15, s67, v98
	v_med3_f32 v36, v36, s67, v98
	v_cvt_pk_fp8_f32 v12, v15, v36
	s_waitcnt vmcnt(13)
	v_mul_f32_e32 v40, 0x42800000, v56
	s_waitcnt vmcnt(12)
	v_mul_f32_e32 v20, 0x42800000, v20
	s_waitcnt vmcnt(11)
	v_mul_f32_e32 v24, 0x42800000, v24
	v_med3_f32 v15, v20, s67, v98
	v_med3_f32 v20, v24, s67, v98
	v_cvt_pk_fp8_f32 v13, v15, v20
	v_med3_f32 v40, v40, s67, v98
	s_waitcnt vmcnt(10)
	v_mul_f32_e32 v56, 0x42800000, v64
	s_waitcnt vmcnt(9)
	v_mul_f32_e32 v44, 0x42800000, v44
	v_med3_f32 v36, v44, s67, v98
	s_waitcnt vmcnt(7)
	v_mul_f32_e32 v16, 0x42800000, v16
	v_med3_f32 v16, v16, s67, v98
	v_mul_f32_e32 v60, 0x42800000, v60
	v_med3_f32 v56, v56, s67, v98
	v_med3_f32 v24, v60, s67, v98
	v_cvt_pk_fp8_f32 v12, v40, v56 op_sel:[0,0,1]
	v_cvt_pk_fp8_f32 v13, v24, v36 op_sel:[0,0,1]
	s_waitcnt vmcnt(6)
	v_mul_f32_e32 v48, 0x42800000, v48
	v_med3_f32 v44, v48, s67, v98
	v_cvt_pk_fp8_f32 v14, v16, v44
	s_waitcnt vmcnt(5)
	v_mul_f32_e32 v52, 0x42800000, v52
	s_waitcnt vmcnt(4)
	v_mul_f32_e32 v28, 0x42800000, v28
	s_waitcnt vmcnt(3)
	v_mul_f32_e32 v4, 0x42800000, v4
	s_waitcnt vmcnt(2)
	v_mul_f32_e32 v8, 0x42800000, v8
	v_med3_f32 v48, v52, s67, v98
	v_med3_f32 v15, v28, s67, v98
	v_cvt_pk_fp8_f32 v14, v48, v15 op_sel:[0,0,1]
	v_med3_f32 v4, v4, s67, v98
	v_med3_f32 v8, v8, s67, v98
	v_mov_b32_e32 v15, v77
	v_cvt_pk_fp8_f32 v15, v4, v8
	s_waitcnt vmcnt(1)
	v_mul_f32_e32 v16, 0x42800000, v32
	s_waitcnt vmcnt(0)
	v_mul_f32_e32 v0, 0x42800000, v0
	v_med3_f32 v4, v16, s67, v98
	v_med3_f32 v0, v0, s67, v98
	v_cvt_pk_fp8_f32 v15, v4, v0 op_sel:[0,0,1]
	v_mul_f32_e32 v0, 0x42800000, v37
	v_mul_f32_e32 v4, 0x42800000, v41
	v_med3_f32 v0, v0, s67, v98
	v_med3_f32 v4, v4, s67, v98
	v_cvt_pk_fp8_f32 v68, v0, v4
	v_mul_f32_e32 v8, 0x42800000, v57
	v_mul_f32_e32 v0, 0x42800000, v65
	v_med3_f32 v4, v8, s67, v98
	v_med3_f32 v0, v0, s67, v98
	v_cvt_pk_fp8_f32 v68, v4, v0 op_sel:[0,0,1]
	v_mul_f32_e32 v0, 0x42800000, v21
	v_mul_f32_e32 v4, 0x42800000, v25
	v_med3_f32 v0, v0, s67, v98
	v_med3_f32 v4, v4, s67, v98
	v_cvt_pk_fp8_f32 v69, v0, v4
	v_mul_f32_e32 v8, 0x42800000, v61
	v_mul_f32_e32 v0, 0x42800000, v45
	v_med3_f32 v4, v8, s67, v98
	v_med3_f32 v0, v0, s67, v98
	v_cvt_pk_fp8_f32 v69, v4, v0 op_sel:[0,0,1]
	v_mul_f32_e32 v0, 0x42800000, v17
	v_mul_f32_e32 v4, 0x42800000, v49
	v_med3_f32 v0, v0, s67, v98
	v_med3_f32 v4, v4, s67, v98
	v_cvt_pk_fp8_f32 v70, v0, v4
	v_mul_f32_e32 v8, 0x42800000, v53
	v_mul_f32_e32 v0, 0x42800000, v29
	v_med3_f32 v4, v8, s67, v98
	v_med3_f32 v0, v0, s67, v98
	v_cvt_pk_fp8_f32 v70, v4, v0 op_sel:[0,0,1]
	v_mul_f32_e32 v0, 0x42800000, v5
	v_mul_f32_e32 v4, 0x42800000, v9
	v_med3_f32 v0, v0, s67, v98
	v_med3_f32 v4, v4, s67, v98
	v_cvt_pk_fp8_f32 v71, v0, v4
	v_mul_f32_e32 v5, 0x42800000, v33
	v_mul_f32_e32 v0, 0x42800000, v1
	v_med3_f32 v1, v5, s67, v98
	v_med3_f32 v0, v0, s67, v98
	v_cvt_pk_fp8_f32 v71, v1, v0 op_sel:[0,0,1]
	v_mul_f32_e32 v0, 0x42800000, v38
	v_mul_f32_e32 v1, 0x42800000, v42
	v_med3_f32 v0, v0, s67, v98
	v_med3_f32 v1, v1, s67, v98
	v_cvt_pk_fp8_f32 v72, v0, v1
	v_mul_f32_e32 v4, 0x42800000, v58
	v_mul_f32_e32 v0, 0x42800000, v66
	v_med3_f32 v1, v4, s67, v98
	v_med3_f32 v0, v0, s67, v98
	v_cvt_pk_fp8_f32 v72, v1, v0 op_sel:[0,0,1]
	v_mul_f32_e32 v0, 0x42800000, v22
	v_mul_f32_e32 v1, 0x42800000, v26
	v_med3_f32 v0, v0, s67, v98
	v_med3_f32 v1, v1, s67, v98
	v_cvt_pk_fp8_f32 v73, v0, v1
	v_mul_f32_e32 v4, 0x42800000, v62
	v_mul_f32_e32 v0, 0x42800000, v46
	v_med3_f32 v1, v4, s67, v98
	v_med3_f32 v0, v0, s67, v98
	v_cvt_pk_fp8_f32 v73, v1, v0 op_sel:[0,0,1]
	v_mul_f32_e32 v0, 0x42800000, v18
	v_mul_f32_e32 v1, 0x42800000, v50
	v_med3_f32 v0, v0, s67, v98
	v_med3_f32 v1, v1, s67, v98
	v_cvt_pk_fp8_f32 v74, v0, v1
	v_mul_f32_e32 v4, 0x42800000, v54
	v_mul_f32_e32 v0, 0x42800000, v30
	v_med3_f32 v1, v4, s67, v98
	v_med3_f32 v0, v0, s67, v98
	v_cvt_pk_fp8_f32 v74, v1, v0 op_sel:[0,0,1]
	v_mul_f32_e32 v0, 0x42800000, v6
	v_mul_f32_e32 v1, 0x42800000, v10
	v_med3_f32 v0, v0, s67, v98
	v_med3_f32 v1, v1, s67, v98
	v_cvt_pk_fp8_f32 v75, v0, v1
	v_mul_f32_e32 v4, 0x42800000, v34
	v_mul_f32_e32 v0, 0x42800000, v2
	v_med3_f32 v1, v4, s67, v98
	v_med3_f32 v0, v0, s67, v98
	v_cvt_pk_fp8_f32 v75, v1, v0 op_sel:[0,0,1]
	v_mul_f32_e32 v0, 0x42800000, v39
	v_mul_f32_e32 v1, 0x42800000, v43
	v_med3_f32 v0, v0, s67, v98
	v_med3_f32 v1, v1, s67, v98
	v_mov_b32_e32 v4, v77
	v_cvt_pk_fp8_f32 v4, v0, v1
	v_mul_f32_e32 v2, 0x42800000, v59
	v_mul_f32_e32 v0, 0x42800000, v67
	v_med3_f32 v1, v2, s67, v98
	v_med3_f32 v0, v0, s67, v98
	v_cvt_pk_fp8_f32 v4, v1, v0 op_sel:[0,0,1]
	v_mul_f32_e32 v0, 0x42800000, v23
	v_mul_f32_e32 v1, 0x42800000, v27
	v_med3_f32 v0, v0, s67, v98
	v_med3_f32 v1, v1, s67, v98
	v_mov_b32_e32 v5, v77
	v_cvt_pk_fp8_f32 v5, v0, v1
	v_mul_f32_e32 v2, 0x42800000, v63
	v_mul_f32_e32 v0, 0x42800000, v47
	v_med3_f32 v1, v2, s67, v98
	v_med3_f32 v0, v0, s67, v98
	v_cvt_pk_fp8_f32 v5, v1, v0 op_sel:[0,0,1]
	v_mul_f32_e32 v0, 0x42800000, v19
	v_mul_f32_e32 v1, 0x42800000, v51
	v_med3_f32 v0, v0, s67, v98
	v_med3_f32 v1, v1, s67, v98
	v_mov_b32_e32 v6, v77
	v_cvt_pk_fp8_f32 v6, v0, v1
	v_mul_f32_e32 v2, 0x42800000, v55
	v_mul_f32_e32 v0, 0x42800000, v31
	v_med3_f32 v1, v2, s67, v98
	v_med3_f32 v0, v0, s67, v98
	v_cvt_pk_fp8_f32 v6, v1, v0 op_sel:[0,0,1]
	v_mul_f32_e32 v0, 0x42800000, v7
	v_mul_f32_e32 v1, 0x42800000, v11
	v_med3_f32 v0, v0, s67, v98
	v_med3_f32 v1, v1, s67, v98
	v_mov_b32_e32 v7, v77
	v_cvt_pk_fp8_f32 v7, v0, v1
	v_mul_f32_e32 v2, 0x42800000, v35
	v_mul_f32_e32 v0, 0x42800000, v3
	v_med3_f32 v1, v2, s67, v98
	v_med3_f32 v0, v0, s67, v98
	v_cvt_pk_fp8_f32 v7, v1, v0 op_sel:[0,0,1]
	ds_write_b128 v95, v[12:15] offset:40960
	ds_write_b128 v95, v[68:71] offset:41040
	ds_write_b128 v95, v[72:75] offset:41120
	ds_write_b128 v95, v[4:7] offset:41200
	s_waitcnt lgkmcnt(0)
	ds_read_b128 v[0:3], v96 offset:40960
	v_or_b32_e32 v4, s0, v83
	v_lshl_add_u64 v[8:9], s[10:11], 0, v[78:79]
	v_lshlrev_b32_e32 v4, 11, v4
	v_mov_b32_e32 v5, v77
	v_lshl_add_u64 v[10:11], v[8:9], 0, v[4:5]
	ds_read_b128 v[4:7], v96 offset:42240
	s_waitcnt lgkmcnt(1)
	global_store_dwordx4 v[10:11], v[0:3], off sc1
	s_nop 1
	v_or_b32_e32 v0, s0, v84
	v_lshlrev_b32_e32 v0, 11, v0
	v_mov_b32_e32 v1, v77
	v_lshl_add_u64 v[0:1], v[8:9], 0, v[0:1]
	s_waitcnt lgkmcnt(0)
	global_store_dwordx4 v[0:1], v[4:7], off sc1
	ds_read_b128 v[0:3], v96 offset:43520
	s_nop 0
	v_or_b32_e32 v4, s0, v85
	v_lshlrev_b32_e32 v4, 11, v4
	v_mov_b32_e32 v5, v77
	v_lshl_add_u64 v[10:11], v[8:9], 0, v[4:5]
	ds_read_b128 v[4:7], v96 offset:44800
	s_waitcnt lgkmcnt(1)
	global_store_dwordx4 v[10:11], v[0:3], off sc1
	s_nop 1
	v_or_b32_e32 v0, s0, v86
	v_lshlrev_b32_e32 v0, 11, v0
	v_mov_b32_e32 v1, v77
	v_lshl_add_u64 v[0:1], v[8:9], 0, v[0:1]
	s_waitcnt lgkmcnt(0)
	global_store_dwordx4 v[0:1], v[4:7], off sc1
	s_waitcnt lgkmcnt(0)

.LBB0_1976:
	s_and_b64 vcc, exec, s[30:31]
	s_cbranch_vccz .LBB0_1938
	s_xor_b64 s[30:31], s[22:23], -1
	s_lshl_b32 s22, s3, 6
	s_mov_b64 s[28:29], -1
	s_and_b64 vcc, exec, s[30:31]
	s_cbranch_vccz .LBB0_2007
	s_andn2_b64 vcc, exec, s[26:27]
	s_cbranch_vccnz .LBB0_1981
	s_ashr_i32 s3, s2, 31
	s_lshl_b64 s[26:27], s[2:3], 22
	v_or_b32_e32 v0, s22, v82
	s_add_u32 s3, s57, s26
	v_mul_hi_i32_i24_e32 v1, s16, v0
	v_mul_i32_i24_e32 v0, s16, v0
	s_addc_u32 s23, s58, s27
	v_lshl_add_u64 v[0:1], v[0:1], 2, s[4:5]
	s_ashr_i32 s21, s20, 31
	v_lshl_add_u64 v[0:1], s[20:21], 2, v[0:1]
	v_mov_b32_e32 v81, v77
	v_lshl_add_u64 v[0:1], v[0:1], 0, v[80:81]
	s_lshl_b64 s[26:27], s[16:17], 2
	global_load_dwordx4 v[56:59], v[0:1], off nt
	v_lshl_add_u64 v[0:1], v[0:1], 0, s[26:27]
	global_load_dwordx4 v[60:63], v[0:1], off nt
	v_lshl_add_u64 v[0:1], v[0:1], 0, s[26:27]
	global_load_dwordx4 v[64:67], v[0:1], off nt
	v_lshl_add_u64 v[0:1], v[0:1], 0, s[26:27]
	global_load_dwordx4 v[52:55], v[0:1], off nt
	v_lshl_add_u64 v[0:1], v[0:1], 0, s[26:27]
	global_load_dwordx4 v[40:43], v[0:1], off nt
	v_lshl_add_u64 v[0:1], v[0:1], 0, s[26:27]
	global_load_dwordx4 v[44:47], v[0:1], off nt
	v_lshl_add_u64 v[0:1], v[0:1], 0, s[26:27]
	global_load_dwordx4 v[48:51], v[0:1], off nt
	v_lshl_add_u64 v[0:1], v[0:1], 0, s[26:27]
	global_load_dwordx4 v[36:39], v[0:1], off nt
	v_lshl_add_u64 v[0:1], v[0:1], 0, s[26:27]
	global_load_dwordx4 v[24:27], v[0:1], off nt
	v_lshl_add_u64 v[0:1], v[0:1], 0, s[26:27]
	global_load_dwordx4 v[28:31], v[0:1], off nt
	v_lshl_add_u64 v[0:1], v[0:1], 0, s[26:27]
	global_load_dwordx4 v[32:35], v[0:1], off nt
	v_lshl_add_u64 v[0:1], v[0:1], 0, s[26:27]
	global_load_dwordx4 v[20:23], v[0:1], off nt
	v_lshl_add_u64 v[0:1], v[0:1], 0, s[26:27]
	global_load_dwordx4 v[4:7], v[0:1], off nt
	v_lshl_add_u64 v[0:1], v[0:1], 0, s[26:27]
	global_load_dwordx4 v[8:11], v[0:1], off nt
	v_lshl_add_u64 v[0:1], v[0:1], 0, s[26:27]
	global_load_dwordx4 v[12:15], v[0:1], off nt
	v_lshl_add_u64 v[0:1], v[0:1], 0, s[26:27]
	global_load_dwordx4 v[0:3], v[0:1], off nt
	v_mov_b32_e32 v19, v77
	v_mov_b32_e32 v69, v77
	v_mov_b32_e32 v70, v77
	v_mov_b32_e32 v71, v77
	v_mov_b32_e32 v72, v77
	v_mov_b32_e32 v73, v77
	v_mov_b32_e32 v74, v77
	v_mov_b32_e32 v75, v77
	v_mov_b32_e32 v16, v77
	v_mov_b32_e32 v17, v77
	v_mov_b32_e32 v18, v77
	v_mov_b32_e32 v68, v77
	s_ashr_i32 s21, s22, 31
	s_add_u32 s26, s3, s22
	s_addc_u32 s27, s23, s21
	s_add_i32 s3, s92, 0x11648
	s_cmpk_lt_u32 s3, 0xf97f
	s_waitcnt vmcnt(15)
	v_mul_f32_e32 v56, 0x42800000, v56
	v_mul_f32_e32 v57, 0x42800000, v57
	s_waitcnt vmcnt(14)
	v_mul_f32_e32 v60, 0x42800000, v60
	v_med3_f32 v56, v56, s67, v98
	v_mul_f32_e32 v61, 0x42800000, v61
	v_med3_f32 v60, v60, s67, v98
	v_med3_f32 v57, v57, s67, v98
	v_med3_f32 v61, v61, s67, v98
	s_waitcnt vmcnt(11)
	v_mul_f32_e32 v41, 0x42800000, v41
	v_med3_f32 v41, v41, s67, v98
	s_waitcnt vmcnt(10)
	v_mul_f32_e32 v45, 0x42800000, v45
	v_med3_f32 v45, v45, s67, v98
	v_cvt_pk_fp8_f32 v69, v41, v45
	s_waitcnt vmcnt(9)
	v_mul_f32_e32 v49, 0x42800000, v49
	v_mul_f32_e32 v40, 0x42800000, v40
	v_mul_f32_e32 v44, 0x42800000, v44
	s_waitcnt vmcnt(7)
	v_mul_f32_e32 v24, 0x42800000, v24
	v_med3_f32 v40, v40, s67, v98
	s_waitcnt vmcnt(6)
	v_mul_f32_e32 v28, 0x42800000, v28
	v_med3_f32 v44, v44, s67, v98
	v_med3_f32 v24, v24, s67, v98
	v_med3_f32 v28, v28, s67, v98
	v_cvt_pk_fp8_f32 v16, v56, v60
	v_cvt_pk_fp8_f32 v17, v40, v44
	s_waitcnt vmcnt(3)
	v_mul_f32_e32 v4, 0x42800000, v4
	v_med3_f32 v4, v4, s67, v98
	s_waitcnt vmcnt(2)
	v_mul_f32_e32 v8, 0x42800000, v8
	v_med3_f32 v8, v8, s67, v98
	v_cvt_pk_fp8_f32 v19, v4, v8
	s_waitcnt vmcnt(1)
	v_mul_f32_e32 v12, 0x42800000, v12
	s_waitcnt vmcnt(0)
	v_mul_f32_e32 v0, 0x42800000, v0
	v_med3_f32 v4, v12, s67, v98
	v_med3_f32 v0, v0, s67, v98
	v_cvt_pk_fp8_f32 v19, v4, v0 op_sel:[0,0,1]
	v_mul_f32_e32 v0, 0x42800000, v37
	v_med3_f32 v4, v49, s67, v98
	v_med3_f32 v0, v0, s67, v98
	v_cvt_pk_fp8_f32 v69, v4, v0 op_sel:[0,0,1]
	v_mul_f32_e32 v0, 0x42800000, v25
	v_mul_f32_e32 v4, 0x42800000, v29
	v_med3_f32 v0, v0, s67, v98
	v_med3_f32 v4, v4, s67, v98
	v_cvt_pk_fp8_f32 v70, v0, v4
	v_mul_f32_e32 v8, 0x42800000, v33
	v_mul_f32_e32 v0, 0x42800000, v21
	v_med3_f32 v4, v8, s67, v98
	v_med3_f32 v0, v0, s67, v98
	v_cvt_pk_fp8_f32 v70, v4, v0 op_sel:[0,0,1]
	v_mul_f32_e32 v0, 0x42800000, v5
	v_mul_f32_e32 v4, 0x42800000, v9
	v_med3_f32 v0, v0, s67, v98
	v_med3_f32 v4, v4, s67, v98
	v_cvt_pk_fp8_f32 v71, v0, v4
	v_mul_f32_e32 v5, 0x42800000, v13
	v_mul_f32_e32 v0, 0x42800000, v1
	v_med3_f32 v1, v5, s67, v98
	v_med3_f32 v0, v0, s67, v98
	v_cvt_pk_fp8_f32 v71, v1, v0 op_sel:[0,0,1]
	v_mul_f32_e32 v0, 0x42800000, v58
	v_mul_f32_e32 v1, 0x42800000, v62
	v_med3_f32 v0, v0, s67, v98
	v_med3_f32 v1, v1, s67, v98
	v_cvt_pk_fp8_f32 v72, v0, v1
	v_mul_f32_e32 v4, 0x42800000, v66
	v_mul_f32_e32 v0, 0x42800000, v54
	v_med3_f32 v1, v4, s67, v98
	v_med3_f32 v0, v0, s67, v98
	v_cvt_pk_fp8_f32 v72, v1, v0 op_sel:[0,0,1]
	v_mul_f32_e32 v0, 0x42800000, v42
	v_mul_f32_e32 v1, 0x42800000, v46
	v_med3_f32 v0, v0, s67, v98
	v_med3_f32 v1, v1, s67, v98
	v_cvt_pk_fp8_f32 v73, v0, v1
	v_mul_f32_e32 v4, 0x42800000, v50
	v_mul_f32_e32 v0, 0x42800000, v38
	v_med3_f32 v1, v4, s67, v98
	v_med3_f32 v0, v0, s67, v98
	v_cvt_pk_fp8_f32 v73, v1, v0 op_sel:[0,0,1]
	v_mul_f32_e32 v0, 0x42800000, v26
	v_mul_f32_e32 v1, 0x42800000, v30
	v_med3_f32 v0, v0, s67, v98
	v_med3_f32 v1, v1, s67, v98
	v_cvt_pk_fp8_f32 v74, v0, v1
	v_mul_f32_e32 v4, 0x42800000, v34
	v_mul_f32_e32 v0, 0x42800000, v22
	v_med3_f32 v1, v4, s67, v98
	v_med3_f32 v0, v0, s67, v98
	v_cvt_pk_fp8_f32 v74, v1, v0 op_sel:[0,0,1]
	v_mul_f32_e32 v0, 0x42800000, v6
	v_mul_f32_e32 v1, 0x42800000, v10
	v_med3_f32 v0, v0, s67, v98
	v_med3_f32 v1, v1, s67, v98
	v_cvt_pk_fp8_f32 v75, v0, v1
	v_mul_f32_e32 v4, 0x42800000, v14
	v_mul_f32_e32 v0, 0x42800000, v2
	v_med3_f32 v1, v4, s67, v98
	v_med3_f32 v0, v0, s67, v98
	v_cvt_pk_fp8_f32 v75, v1, v0 op_sel:[0,0,1]
	v_mul_f32_e32 v0, 0x42800000, v59
	v_mul_f32_e32 v1, 0x42800000, v63
	v_med3_f32 v0, v0, s67, v98
	v_med3_f32 v1, v1, s67, v98
	v_mov_b32_e32 v4, v77
	v_cvt_pk_fp8_f32 v4, v0, v1
	v_mul_f32_e32 v2, 0x42800000, v67
	v_mul_f32_e32 v0, 0x42800000, v55
	v_med3_f32 v1, v2, s67, v98
	v_med3_f32 v0, v0, s67, v98
	v_cvt_pk_fp8_f32 v4, v1, v0 op_sel:[0,0,1]
	v_mul_f32_e32 v0, 0x42800000, v43
	v_mul_f32_e32 v1, 0x42800000, v47
	v_med3_f32 v0, v0, s67, v98
	v_med3_f32 v1, v1, s67, v98
	v_mov_b32_e32 v5, v77
	v_cvt_pk_fp8_f32 v5, v0, v1
	v_mul_f32_e32 v2, 0x42800000, v51
	v_mul_f32_e32 v0, 0x42800000, v39
	v_med3_f32 v1, v2, s67, v98
	v_med3_f32 v0, v0, s67, v98
	v_cvt_pk_fp8_f32 v5, v1, v0 op_sel:[0,0,1]
	v_mul_f32_e32 v0, 0x42800000, v27
	v_mul_f32_e32 v1, 0x42800000, v31
	v_med3_f32 v0, v0, s67, v98
	v_med3_f32 v1, v1, s67, v98
	v_mov_b32_e32 v6, v77
	v_cvt_pk_fp8_f32 v6, v0, v1
	v_mul_f32_e32 v2, 0x42800000, v35
	v_mul_f32_e32 v0, 0x42800000, v23
	v_cvt_pk_fp8_f32 v18, v24, v28
	v_med3_f32 v1, v2, s67, v98
	v_med3_f32 v0, v0, s67, v98
	v_cvt_pk_fp8_f32 v68, v57, v61
	v_cvt_pk_fp8_f32 v6, v1, v0 op_sel:[0,0,1]
	v_mul_f32_e32 v0, 0x42800000, v7
	v_mul_f32_e32 v1, 0x42800000, v11
	v_mul_f32_e32 v64, 0x42800000, v64
	v_mul_f32_e32 v52, 0x42800000, v52
	v_mul_f32_e32 v48, 0x42800000, v48
	v_mul_f32_e32 v36, 0x42800000, v36
	v_mul_f32_e32 v32, 0x42800000, v32
	v_mul_f32_e32 v20, 0x42800000, v20
	v_med3_f32 v0, v0, s67, v98
	v_med3_f32 v1, v1, s67, v98
	v_mov_b32_e32 v7, v77
	v_mul_f32_e32 v65, 0x42800000, v65
	v_med3_f32 v64, v64, s67, v98
	v_mul_f32_e32 v53, 0x42800000, v53
	v_med3_f32 v52, v52, s67, v98
	v_med3_f32 v48, v48, s67, v98
	v_med3_f32 v36, v36, s67, v98
	v_med3_f32 v32, v32, s67, v98
	v_med3_f32 v20, v20, s67, v98
	v_cvt_pk_fp8_f32 v7, v0, v1
	v_med3_f32 v56, v65, s67, v98
	v_med3_f32 v53, v53, s67, v98
	v_cvt_pk_fp8_f32 v16, v64, v52 op_sel:[0,0,1]
	v_cvt_pk_fp8_f32 v17, v48, v36 op_sel:[0,0,1]
	v_cvt_pk_fp8_f32 v18, v32, v20 op_sel:[0,0,1]
	v_cvt_pk_fp8_f32 v68, v56, v53 op_sel:[0,0,1]
	v_mul_f32_e32 v2, 0x42800000, v15
	v_mul_f32_e32 v0, 0x42800000, v3
	v_med3_f32 v1, v2, s67, v98
	v_med3_f32 v0, v0, s67, v98
	v_cvt_pk_fp8_f32 v7, v1, v0 op_sel:[0,0,1]
	ds_write_b128 v95, v[16:19] offset:40960
	ds_write_b128 v95, v[68:71] offset:41040
	ds_write_b128 v95, v[72:75] offset:41120
	ds_write_b128 v95, v[4:7] offset:41200
	s_waitcnt lgkmcnt(0)
	ds_read_b128 v[0:3], v96 offset:40960
	v_or_b32_e32 v4, s13, v83
	v_ashrrev_i32_e32 v5, 31, v4
	v_lshl_add_u64 v[8:9], s[26:27], 0, v[78:79]
	v_lshlrev_b64 v[4:5], 11, v[4:5]
	v_lshl_add_u64 v[10:11], v[8:9], 0, v[4:5]
	ds_read_b128 v[4:7], v96 offset:42240
	s_waitcnt lgkmcnt(1)
	global_store_dwordx4 v[10:11], v[0:3], off sc1
	s_cselect_b64 s[26:27], -1, 0
	s_nop 0
	v_or_b32_e32 v0, s13, v84
	v_ashrrev_i32_e32 v1, 31, v0
	v_lshlrev_b64 v[0:1], 11, v[0:1]
	v_lshl_add_u64 v[0:1], v[8:9], 0, v[0:1]
	s_waitcnt lgkmcnt(0)
	global_store_dwordx4 v[0:1], v[4:7], off sc1
	ds_read_b128 v[0:3], v96 offset:43520
	s_nop 0
	v_or_b32_e32 v4, s13, v85
	v_ashrrev_i32_e32 v5, 31, v4
	v_lshlrev_b64 v[4:5], 11, v[4:5]
	v_lshl_add_u64 v[10:11], v[8:9], 0, v[4:5]
	ds_read_b128 v[4:7], v96 offset:44800
	s_waitcnt lgkmcnt(1)
	global_store_dwordx4 v[10:11], v[0:3], off sc1
	s_nop 1
	v_or_b32_e32 v0, s13, v86
	v_ashrrev_i32_e32 v1, 31, v0
	v_lshlrev_b64 v[0:1], 11, v[0:1]
	v_lshl_add_u64 v[0:1], v[8:9], 0, v[0:1]
	s_waitcnt lgkmcnt(0)
	global_store_dwordx4 v[0:1], v[4:7], off sc1
	s_waitcnt lgkmcnt(0)
	s_andn2_b64 vcc, exec, s[26:27]
	s_cbranch_vccz .LBB0_1982
	s_branch .LBB0_2006

.LBB0_1982:
	s_andn2_b64 vcc, exec, s[24:25]
	s_cbranch_vccnz .LBB0_1984
	s_ashr_i32 s3, s2, 31
	s_lshl_b64 s[24:25], s[2:3], 22
	s_add_u32 s3, s59, s24
	s_addc_u32 s21, s60, s25
	v_or_b32_e32 v0, s22, v82
	s_add_u32 s3, s3, s18
	v_mul_hi_i32_i24_e32 v1, s16, v0
	v_mul_i32_i24_e32 v0, s16, v0
	s_addc_u32 s23, s21, s19
	v_lshl_add_u64 v[0:1], v[0:1], 2, s[4:5]
	s_ashr_i32 s21, s20, 31
	v_lshl_add_u64 v[0:1], s[20:21], 2, v[0:1]
	v_mov_b32_e32 v81, v77
	v_lshl_add_u64 v[0:1], v[0:1], 0, v[80:81]
	s_lshl_b64 s[24:25], s[16:17], 2
	global_load_dwordx4 v[56:59], v[0:1], off nt
	v_lshl_add_u64 v[0:1], v[0:1], 0, s[24:25]
	global_load_dwordx4 v[60:63], v[0:1], off nt
	v_lshl_add_u64 v[0:1], v[0:1], 0, s[24:25]
	global_load_dwordx4 v[64:67], v[0:1], off nt
	v_lshl_add_u64 v[0:1], v[0:1], 0, s[24:25]
	global_load_dwordx4 v[52:55], v[0:1], off nt
	v_lshl_add_u64 v[0:1], v[0:1], 0, s[24:25]
	global_load_dwordx4 v[40:43], v[0:1], off nt
	v_lshl_add_u64 v[0:1], v[0:1], 0, s[24:25]
	global_load_dwordx4 v[44:47], v[0:1], off nt
	v_lshl_add_u64 v[0:1], v[0:1], 0, s[24:25]
	global_load_dwordx4 v[48:51], v[0:1], off nt
	v_lshl_add_u64 v[0:1], v[0:1], 0, s[24:25]
	global_load_dwordx4 v[36:39], v[0:1], off nt
	v_lshl_add_u64 v[0:1], v[0:1], 0, s[24:25]
	global_load_dwordx4 v[24:27], v[0:1], off nt
	v_lshl_add_u64 v[0:1], v[0:1], 0, s[24:25]
	global_load_dwordx4 v[28:31], v[0:1], off nt
	v_lshl_add_u64 v[0:1], v[0:1], 0, s[24:25]
	global_load_dwordx4 v[32:35], v[0:1], off nt
	v_lshl_add_u64 v[0:1], v[0:1], 0, s[24:25]
	global_load_dwordx4 v[20:23], v[0:1], off nt
	v_lshl_add_u64 v[0:1], v[0:1], 0, s[24:25]
	global_load_dwordx4 v[4:7], v[0:1], off nt
	v_lshl_add_u64 v[0:1], v[0:1], 0, s[24:25]
	global_load_dwordx4 v[12:15], v[0:1], off nt
	v_lshl_add_u64 v[0:1], v[0:1], 0, s[24:25]
	global_load_dwordx4 v[16:19], v[0:1], off nt
	v_lshl_add_u64 v[0:1], v[0:1], 0, s[24:25]
	global_load_dwordx4 v[0:3], v[0:1], off nt
	v_mov_b32_e32 v11, v77
	v_mov_b32_e32 v69, v77
	v_mov_b32_e32 v70, v77
	v_mov_b32_e32 v71, v77
	v_mov_b32_e32 v72, v77
	v_mov_b32_e32 v73, v77
	v_mov_b32_e32 v74, v77
	v_mov_b32_e32 v75, v77
	v_mov_b32_e32 v8, v77
	v_mov_b32_e32 v9, v77
	v_mov_b32_e32 v10, v77
	v_mov_b32_e32 v68, v77
	s_ashr_i32 s21, s22, 31
	s_add_u32 s24, s3, s22
	s_addc_u32 s25, s23, s21
	s_add_i32 s92, s92, 0x11648
	s_cmpk_lt_u32 s92, 0xf97f
	s_waitcnt vmcnt(15)
	v_mul_f32_e32 v56, 0x42800000, v56
	v_mul_f32_e32 v57, 0x42800000, v57
	s_waitcnt vmcnt(14)
	v_mul_f32_e32 v60, 0x42800000, v60
	v_med3_f32 v56, v56, s67, v98
	v_mul_f32_e32 v61, 0x42800000, v61
	v_med3_f32 v60, v60, s67, v98
	v_med3_f32 v57, v57, s67, v98
	v_med3_f32 v61, v61, s67, v98
	s_waitcnt vmcnt(11)
	v_mul_f32_e32 v41, 0x42800000, v41
	v_med3_f32 v41, v41, s67, v98
	s_waitcnt vmcnt(10)
	v_mul_f32_e32 v45, 0x42800000, v45
	v_med3_f32 v45, v45, s67, v98
	v_cvt_pk_fp8_f32 v69, v41, v45
	s_waitcnt vmcnt(9)
	v_mul_f32_e32 v49, 0x42800000, v49
	v_mul_f32_e32 v40, 0x42800000, v40
	v_mul_f32_e32 v44, 0x42800000, v44
	s_waitcnt vmcnt(7)
	v_mul_f32_e32 v24, 0x42800000, v24
	v_med3_f32 v40, v40, s67, v98
	s_waitcnt vmcnt(6)
	v_mul_f32_e32 v28, 0x42800000, v28
	v_med3_f32 v44, v44, s67, v98
	v_med3_f32 v24, v24, s67, v98
	v_med3_f32 v28, v28, s67, v98
	v_cvt_pk_fp8_f32 v8, v56, v60
	v_cvt_pk_fp8_f32 v9, v40, v44
	s_waitcnt vmcnt(3)
	v_mul_f32_e32 v4, 0x42800000, v4
	v_med3_f32 v4, v4, s67, v98
	s_waitcnt vmcnt(2)
	v_mul_f32_e32 v12, 0x42800000, v12
	v_med3_f32 v12, v12, s67, v98
	v_cvt_pk_fp8_f32 v11, v4, v12
	s_waitcnt vmcnt(1)
	v_mul_f32_e32 v16, 0x42800000, v16
	s_waitcnt vmcnt(0)
	v_mul_f32_e32 v0, 0x42800000, v0
	v_med3_f32 v4, v16, s67, v98
	v_med3_f32 v0, v0, s67, v98
	v_cvt_pk_fp8_f32 v11, v4, v0 op_sel:[0,0,1]
	v_mul_f32_e32 v0, 0x42800000, v37
	v_med3_f32 v4, v49, s67, v98
	v_med3_f32 v0, v0, s67, v98
	v_cvt_pk_fp8_f32 v69, v4, v0 op_sel:[0,0,1]
	v_mul_f32_e32 v0, 0x42800000, v25
	v_mul_f32_e32 v4, 0x42800000, v29
	v_med3_f32 v0, v0, s67, v98
	v_med3_f32 v4, v4, s67, v98
	v_cvt_pk_fp8_f32 v70, v0, v4
	v_mul_f32_e32 v12, 0x42800000, v33
	v_mul_f32_e32 v0, 0x42800000, v21
	v_med3_f32 v4, v12, s67, v98
	v_med3_f32 v0, v0, s67, v98
	v_cvt_pk_fp8_f32 v70, v4, v0 op_sel:[0,0,1]
	v_mul_f32_e32 v0, 0x42800000, v5
	v_mul_f32_e32 v4, 0x42800000, v13
	v_med3_f32 v0, v0, s67, v98
	v_med3_f32 v4, v4, s67, v98
	v_cvt_pk_fp8_f32 v71, v0, v4
	v_mul_f32_e32 v5, 0x42800000, v17
	v_mul_f32_e32 v0, 0x42800000, v1
	v_med3_f32 v1, v5, s67, v98
	v_med3_f32 v0, v0, s67, v98
	v_cvt_pk_fp8_f32 v71, v1, v0 op_sel:[0,0,1]
	v_mul_f32_e32 v0, 0x42800000, v58
	v_mul_f32_e32 v1, 0x42800000, v62
	v_med3_f32 v0, v0, s67, v98
	v_med3_f32 v1, v1, s67, v98
	v_cvt_pk_fp8_f32 v72, v0, v1
	v_mul_f32_e32 v4, 0x42800000, v66
	v_mul_f32_e32 v0, 0x42800000, v54
	v_med3_f32 v1, v4, s67, v98
	v_med3_f32 v0, v0, s67, v98
	v_cvt_pk_fp8_f32 v72, v1, v0 op_sel:[0,0,1]
	v_mul_f32_e32 v0, 0x42800000, v42
	v_mul_f32_e32 v1, 0x42800000, v46
	v_med3_f32 v0, v0, s67, v98
	v_med3_f32 v1, v1, s67, v98
	v_cvt_pk_fp8_f32 v73, v0, v1
	v_mul_f32_e32 v4, 0x42800000, v50
	v_mul_f32_e32 v0, 0x42800000, v38
	v_med3_f32 v1, v4, s67, v98
	v_med3_f32 v0, v0, s67, v98
	v_cvt_pk_fp8_f32 v73, v1, v0 op_sel:[0,0,1]
	v_mul_f32_e32 v0, 0x42800000, v26
	v_mul_f32_e32 v1, 0x42800000, v30
	v_med3_f32 v0, v0, s67, v98
	v_med3_f32 v1, v1, s67, v98
	v_cvt_pk_fp8_f32 v74, v0, v1
	v_mul_f32_e32 v4, 0x42800000, v34
	v_mul_f32_e32 v0, 0x42800000, v22
	v_med3_f32 v1, v4, s67, v98
	v_med3_f32 v0, v0, s67, v98
	v_cvt_pk_fp8_f32 v74, v1, v0 op_sel:[0,0,1]
	v_mul_f32_e32 v0, 0x42800000, v6
	v_mul_f32_e32 v1, 0x42800000, v14
	v_med3_f32 v0, v0, s67, v98
	v_med3_f32 v1, v1, s67, v98
	v_cvt_pk_fp8_f32 v75, v0, v1
	v_mul_f32_e32 v4, 0x42800000, v18
	v_mul_f32_e32 v0, 0x42800000, v2
	v_med3_f32 v1, v4, s67, v98
	v_med3_f32 v0, v0, s67, v98
	v_cvt_pk_fp8_f32 v75, v1, v0 op_sel:[0,0,1]
	v_mul_f32_e32 v0, 0x42800000, v59
	v_mul_f32_e32 v1, 0x42800000, v63
	v_med3_f32 v0, v0, s67, v98
	v_med3_f32 v1, v1, s67, v98
	v_mov_b32_e32 v4, v77
	v_cvt_pk_fp8_f32 v4, v0, v1
	v_mul_f32_e32 v2, 0x42800000, v67
	v_mul_f32_e32 v0, 0x42800000, v55
	v_med3_f32 v1, v2, s67, v98
	v_med3_f32 v0, v0, s67, v98
	v_cvt_pk_fp8_f32 v4, v1, v0 op_sel:[0,0,1]
	v_mul_f32_e32 v0, 0x42800000, v43
	v_mul_f32_e32 v1, 0x42800000, v47
	v_med3_f32 v0, v0, s67, v98
	v_med3_f32 v1, v1, s67, v98
	v_mov_b32_e32 v5, v77
	v_cvt_pk_fp8_f32 v5, v0, v1
	v_mul_f32_e32 v2, 0x42800000, v51
	v_mul_f32_e32 v0, 0x42800000, v39
	v_med3_f32 v1, v2, s67, v98
	v_med3_f32 v0, v0, s67, v98
	v_cvt_pk_fp8_f32 v5, v1, v0 op_sel:[0,0,1]
	v_mul_f32_e32 v0, 0x42800000, v27
	v_mul_f32_e32 v1, 0x42800000, v31
	v_med3_f32 v0, v0, s67, v98
	v_med3_f32 v1, v1, s67, v98
	v_mov_b32_e32 v6, v77
	v_cvt_pk_fp8_f32 v6, v0, v1
	v_mul_f32_e32 v2, 0x42800000, v35
	v_mul_f32_e32 v0, 0x42800000, v23
	v_cvt_pk_fp8_f32 v10, v24, v28
	v_med3_f32 v1, v2, s67, v98
	v_med3_f32 v0, v0, s67, v98
	v_cvt_pk_fp8_f32 v68, v57, v61
	v_cvt_pk_fp8_f32 v6, v1, v0 op_sel:[0,0,1]
	v_mul_f32_e32 v0, 0x42800000, v7
	v_mul_f32_e32 v1, 0x42800000, v15
	v_mul_f32_e32 v64, 0x42800000, v64
	v_mul_f32_e32 v52, 0x42800000, v52
	v_mul_f32_e32 v48, 0x42800000, v48
	v_mul_f32_e32 v36, 0x42800000, v36
	v_mul_f32_e32 v32, 0x42800000, v32
	v_mul_f32_e32 v20, 0x42800000, v20
	v_med3_f32 v0, v0, s67, v98
	v_med3_f32 v1, v1, s67, v98
	v_mov_b32_e32 v7, v77
	v_mul_f32_e32 v65, 0x42800000, v65
	v_med3_f32 v64, v64, s67, v98
	v_mul_f32_e32 v53, 0x42800000, v53
	v_med3_f32 v52, v52, s67, v98
	v_med3_f32 v48, v48, s67, v98
	v_med3_f32 v36, v36, s67, v98
	v_med3_f32 v32, v32, s67, v98
	v_med3_f32 v20, v20, s67, v98
	v_cvt_pk_fp8_f32 v7, v0, v1
	v_med3_f32 v56, v65, s67, v98
	v_med3_f32 v53, v53, s67, v98
	v_cvt_pk_fp8_f32 v8, v64, v52 op_sel:[0,0,1]
	v_cvt_pk_fp8_f32 v9, v48, v36 op_sel:[0,0,1]
	v_cvt_pk_fp8_f32 v10, v32, v20 op_sel:[0,0,1]
	v_cvt_pk_fp8_f32 v68, v56, v53 op_sel:[0,0,1]
	v_mul_f32_e32 v2, 0x42800000, v19
	v_mul_f32_e32 v0, 0x42800000, v3
	v_med3_f32 v1, v2, s67, v98
	v_med3_f32 v0, v0, s67, v98
	v_cvt_pk_fp8_f32 v7, v1, v0 op_sel:[0,0,1]
	ds_write_b128 v95, v[8:11] offset:40960
	ds_write_b128 v95, v[68:71] offset:41040
	ds_write_b128 v95, v[72:75] offset:41120
	ds_write_b128 v95, v[4:7] offset:41200
	s_waitcnt lgkmcnt(0)
	ds_read_b128 v[0:3], v96 offset:40960
	v_or_b32_e32 v4, s13, v83
	v_ashrrev_i32_e32 v5, 31, v4
	v_lshl_add_u64 v[8:9], s[24:25], 0, v[78:79]
	v_lshlrev_b64 v[4:5], 11, v[4:5]
	v_lshl_add_u64 v[10:11], v[8:9], 0, v[4:5]
	ds_read_b128 v[4:7], v96 offset:42240
	s_waitcnt lgkmcnt(1)
	global_store_dwordx4 v[10:11], v[0:3], off sc1
	s_cselect_b64 s[24:25], -1, 0
	s_nop 0
	v_or_b32_e32 v0, s13, v84
	v_ashrrev_i32_e32 v1, 31, v0
	v_lshlrev_b64 v[0:1], 11, v[0:1]
	v_lshl_add_u64 v[0:1], v[8:9], 0, v[0:1]
	s_waitcnt lgkmcnt(0)
	global_store_dwordx4 v[0:1], v[4:7], off sc1
	ds_read_b128 v[0:3], v96 offset:43520
	s_nop 0
	v_or_b32_e32 v4, s13, v85
	v_ashrrev_i32_e32 v5, 31, v4
	v_lshlrev_b64 v[4:5], 11, v[4:5]
	v_lshl_add_u64 v[10:11], v[8:9], 0, v[4:5]
	ds_read_b128 v[4:7], v96 offset:44800
	s_waitcnt lgkmcnt(1)
	global_store_dwordx4 v[10:11], v[0:3], off sc1
	s_nop 1
	v_or_b32_e32 v0, s13, v86
	v_ashrrev_i32_e32 v1, 31, v0
	v_lshlrev_b64 v[0:1], 11, v[0:1]
	v_lshl_add_u64 v[0:1], v[8:9], 0, v[0:1]
	s_waitcnt lgkmcnt(0)
	global_store_dwordx4 v[0:1], v[4:7], off sc1
	s_waitcnt lgkmcnt(0)
	s_andn2_b64 vcc, exec, s[24:25]
	s_cbranch_vccz .LBB0_1985
	s_branch .LBB0_2006

.LBB0_2262:
	ds_read_b128 v[8:11], v179
	ds_read_b128 v[12:15], v179 offset:1024
	ds_read_b128 v[0:3], v179 offset:2048
	ds_read_b128 v[4:7], v179 offset:3072
	s_add_u32 s18, s16, 0xfffc0080
	s_addc_u32 s19, s17, -1
	s_cmp_eq_u32 s62, 12
	s_cselect_b32 s21, s56, s19
	s_cselect_b32 s20, s57, s18
	s_cselect_b32 s19, s58, s61
	s_cselect_b32 s18, s59, s60
	v_lshl_add_u64 v[162:163], s[16:17], 0, v[156:157]
	s_add_i32 m0, s30, 0xc000
	ds_read_b128 v[166:169], v180
	ds_read_b128 v[170:173], v180 offset:1024
	ds_read_b128 v[182:185], v180 offset:2048
	ds_read_b128 v[186:189], v180 offset:3072
	ds_read_b128 v[190:193], v180 offset:4096
	ds_read_b128 v[194:197], v180 offset:5120
	ds_read_b128 v[198:201], v180 offset:6144
	ds_read_b128 v[202:205], v180 offset:7168
	global_load_lds_dwordx4 v[162:163], off
	v_lshl_add_u64 v[162:163], s[16:17], 0, v[154:155]
	s_add_i32 m0, s30, 0xe000
	s_nop 0
	global_load_lds_dwordx4 v[162:163], off
	s_waitcnt lgkmcnt(8)
	s_barrier
	s_waitcnt lgkmcnt(0)
	s_setprio 1
	s_waitcnt lgkmcnt(0)
	v_mfma_scale_f32_16x16x128_f8f6f4 v[140:143], v[8:15], v[166:173], v[140:143], v175, v175 op_sel_hi:[0,0,0]
	v_mfma_scale_f32_16x16x128_f8f6f4 v[136:139], v[0:7], v[166:173], v[136:139], v175, v175 op_sel_hi:[0,0,0]
	v_mfma_scale_f32_16x16x128_f8f6f4 v[128:131], v[8:15], v[182:189], v[128:131], v175, v175 op_sel_hi:[0,0,0]
	v_mfma_scale_f32_16x16x128_f8f6f4 v[120:123], v[0:7], v[182:189], v[120:123], v175, v175 op_sel_hi:[0,0,0]
	v_mfma_scale_f32_16x16x128_f8f6f4 v[112:115], v[8:15], v[190:197], v[112:115], v175, v175 op_sel_hi:[0,0,0]
	v_mfma_scale_f32_16x16x128_f8f6f4 v[104:107], v[0:7], v[190:197], v[104:107], v175, v175 op_sel_hi:[0,0,0]
	v_mfma_scale_f32_16x16x128_f8f6f4 v[96:99], v[8:15], v[198:205], v[96:99], v175, v175 op_sel_hi:[0,0,0]
	v_mfma_scale_f32_16x16x128_f8f6f4 v[88:91], v[0:7], v[198:205], v[88:91], v175, v175 op_sel_hi:[0,0,0]
	s_setprio 0
	s_barrier
	s_add_i32 s63, s46, s29
	v_lshl_add_u64 v[162:163], s[18:19], 0, v[146:147]
	s_mov_b32 m0, s63
	ds_read_b128 v[206:209], v181
	ds_read_b128 v[210:213], v181 offset:1024
	ds_read_b128 v[214:217], v181 offset:2048
	ds_read_b128 v[218:221], v181 offset:3072
	global_load_lds_dwordx4 v[162:163], off
	v_lshl_add_u64 v[164:165], s[18:19], 0, v[150:151]
	s_add_i32 m0, s63, 0x2000
	s_nop 0
	global_load_lds_dwordx4 v[164:165], off
	s_barrier
	s_waitcnt lgkmcnt(0)
	s_setprio 1
	s_waitcnt lgkmcnt(0)
	v_mfma_scale_f32_16x16x128_f8f6f4 v[132:135], v[206:213], v[166:173], v[132:135], v175, v175 op_sel_hi:[0,0,0]
	v_mfma_scale_f32_16x16x128_f8f6f4 v[124:127], v[214:221], v[166:173], v[124:127], v175, v175 op_sel_hi:[0,0,0]
	v_mfma_scale_f32_16x16x128_f8f6f4 v[116:119], v[206:213], v[182:189], v[116:119], v175, v175 op_sel_hi:[0,0,0]
	v_mfma_scale_f32_16x16x128_f8f6f4 v[108:111], v[214:221], v[182:189], v[108:111], v175, v175 op_sel_hi:[0,0,0]
	v_mfma_scale_f32_16x16x128_f8f6f4 v[100:103], v[206:213], v[190:197], v[100:103], v175, v175 op_sel_hi:[0,0,0]
	v_mfma_scale_f32_16x16x128_f8f6f4 v[92:95], v[214:221], v[190:197], v[92:95], v175, v175 op_sel_hi:[0,0,0]
	v_mfma_scale_f32_16x16x128_f8f6f4 v[84:87], v[206:213], v[198:205], v[84:87], v175, v175 op_sel_hi:[0,0,0]
	v_mfma_scale_f32_16x16x128_f8f6f4 v[80:83], v[214:221], v[198:205], v[80:83], v175, v175 op_sel_hi:[0,0,0]
	s_setprio 0
	s_mov_b32 m0, s30
	v_lshl_add_u64 v[166:167], s[20:21], 0, v[144:145]
	s_barrier
	ds_read_b128 v[182:185], v180 offset:16384
	ds_read_b128 v[186:189], v180 offset:17408
	ds_read_b128 v[190:193], v180 offset:18432
	ds_read_b128 v[194:197], v180 offset:19456
	ds_read_b128 v[198:201], v180 offset:20480
	ds_read_b128 v[202:205], v180 offset:21504
	ds_read_b128 v[224:227], v180 offset:22528
	ds_read_b128 v[228:231], v180 offset:23552
	global_load_lds_dwordx4 v[166:167], off
	v_lshl_add_u64 v[168:169], s[20:21], 0, v[148:149]
	s_mov_b32 m0, s31
	s_nop 0
	global_load_lds_dwordx4 v[168:169], off
	s_barrier
	s_waitcnt lgkmcnt(0)
	s_setprio 1
	s_waitcnt lgkmcnt(0)
	v_mfma_scale_f32_16x16x128_f8f6f4 v[76:79], v[8:15], v[182:189], v[76:79], v175, v175 op_sel_hi:[0,0,0]
	v_mfma_scale_f32_16x16x128_f8f6f4 v[72:75], v[0:7], v[182:189], v[72:75], v175, v175 op_sel_hi:[0,0,0]
	v_mfma_scale_f32_16x16x128_f8f6f4 v[64:67], v[8:15], v[190:197], v[64:67], v175, v175 op_sel_hi:[0,0,0]
	v_mfma_scale_f32_16x16x128_f8f6f4 v[56:59], v[0:7], v[190:197], v[56:59], v175, v175 op_sel_hi:[0,0,0]
	v_mfma_scale_f32_16x16x128_f8f6f4 v[48:51], v[8:15], v[198:205], v[48:51], v175, v175 op_sel_hi:[0,0,0]
	v_mfma_scale_f32_16x16x128_f8f6f4 v[40:43], v[0:7], v[198:205], v[40:43], v175, v175 op_sel_hi:[0,0,0]
	v_mfma_scale_f32_16x16x128_f8f6f4 v[32:35], v[8:15], v[224:231], v[32:35], v175, v175 op_sel_hi:[0,0,0]
	v_mfma_scale_f32_16x16x128_f8f6f4 v[24:27], v[0:7], v[224:231], v[24:27], v175, v175 op_sel_hi:[0,0,0]
	s_setprio 0
	s_barrier
	s_add_u32 s64, s18, 0x40000
	s_addc_u32 s65, s19, 0
	s_add_i32 s63, s47, s29
	v_lshl_add_u64 v[0:1], s[64:65], 0, v[146:147]
	s_mov_b32 m0, s63
	s_nop 0
	global_load_lds_dwordx4 v[0:1], off
	v_lshl_add_u64 v[0:1], s[64:65], 0, v[150:151]
	s_add_i32 m0, s63, 0x2000
	s_nop 0
	global_load_lds_dwordx4 v[0:1], off
	s_waitcnt vmcnt(6)
	s_barrier
	s_setprio 1
	v_mfma_scale_f32_16x16x128_f8f6f4 v[68:71], v[206:213], v[182:189], v[68:71], v175, v175 op_sel_hi:[0,0,0]
	v_mfma_scale_f32_16x16x128_f8f6f4 v[60:63], v[214:221], v[182:189], v[60:63], v175, v175 op_sel_hi:[0,0,0]
	v_mfma_scale_f32_16x16x128_f8f6f4 v[52:55], v[206:213], v[190:197], v[52:55], v175, v175 op_sel_hi:[0,0,0]
	v_mfma_scale_f32_16x16x128_f8f6f4 v[44:47], v[214:221], v[190:197], v[44:47], v175, v175 op_sel_hi:[0,0,0]
	v_mfma_scale_f32_16x16x128_f8f6f4 v[36:39], v[206:213], v[198:205], v[36:39], v175, v175 op_sel_hi:[0,0,0]
	v_mfma_scale_f32_16x16x128_f8f6f4 v[28:31], v[214:221], v[198:205], v[28:31], v175, v175 op_sel_hi:[0,0,0]
	v_mfma_scale_f32_16x16x128_f8f6f4 v[20:23], v[206:213], v[224:231], v[20:23], v175, v175 op_sel_hi:[0,0,0]
	v_mfma_scale_f32_16x16x128_f8f6f4 v[16:19], v[214:221], v[224:231], v[16:19], v175, v175 op_sel_hi:[0,0,0]
	s_setprio 0
	s_add_i32 s63, 0, 0x18000
	v_add_u32_e32 v12, s63, v176
	s_barrier
	ds_read_b128 v[0:3], v12
	ds_read_b128 v[4:7], v12 offset:1024
	ds_read_b128 v[8:11], v12 offset:2048
	ds_read_b128 v[12:15], v12 offset:3072
	s_add_u32 s20, s20, 0x40000
	s_addc_u32 s21, s21, 0
	s_mov_b32 m0, s38
	v_lshl_add_u64 v[170:171], s[20:21], 0, v[144:145]
	ds_read_b128 v[182:185], v180 offset:32768
	ds_read_b128 v[186:189], v180 offset:33792
	ds_read_b128 v[190:193], v180 offset:34816
	ds_read_b128 v[194:197], v180 offset:35840
	ds_read_b128 v[198:201], v180 offset:36864
	ds_read_b128 v[202:205], v180 offset:37888
	ds_read_b128 v[206:209], v180 offset:38912
	ds_read_b128 v[210:213], v180 offset:39936
	global_load_lds_dwordx4 v[170:171], off
	v_lshl_add_u64 v[170:171], s[20:21], 0, v[148:149]
	s_mov_b32 m0, s39
	s_nop 0
	global_load_lds_dwordx4 v[170:171], off
	s_waitcnt lgkmcnt(8)
	s_barrier
	s_waitcnt lgkmcnt(0)
	s_setprio 1
	s_waitcnt lgkmcnt(0)
	v_mfma_scale_f32_16x16x128_f8f6f4 v[140:143], v[0:7], v[182:189], v[140:143], v175, v175 op_sel_hi:[0,0,0]
	v_mfma_scale_f32_16x16x128_f8f6f4 v[136:139], v[8:15], v[182:189], v[136:139], v175, v175 op_sel_hi:[0,0,0]
	v_mfma_scale_f32_16x16x128_f8f6f4 v[128:131], v[0:7], v[190:197], v[128:131], v175, v175 op_sel_hi:[0,0,0]
	v_mfma_scale_f32_16x16x128_f8f6f4 v[120:123], v[8:15], v[190:197], v[120:123], v175, v175 op_sel_hi:[0,0,0]
	v_mfma_scale_f32_16x16x128_f8f6f4 v[112:115], v[0:7], v[198:205], v[112:115], v175, v175 op_sel_hi:[0,0,0]
	v_mfma_scale_f32_16x16x128_f8f6f4 v[104:107], v[8:15], v[198:205], v[104:107], v175, v175 op_sel_hi:[0,0,0]
	v_mfma_scale_f32_16x16x128_f8f6f4 v[96:99], v[0:7], v[206:213], v[96:99], v175, v175 op_sel_hi:[0,0,0]
	v_mfma_scale_f32_16x16x128_f8f6f4 v[88:91], v[8:15], v[206:213], v[88:91], v175, v175 op_sel_hi:[0,0,0]
	s_setprio 0
	s_barrier
	s_add_i32 s20, 0, 0x1c000
	s_add_i32 s21, s63, s29
	v_add_u32_e32 v152, s20, v176
	v_lshl_add_u64 v[162:163], v[162:163], 0, s[4:5]
	s_mov_b32 m0, s21
	ds_read_b128 v[214:217], v152
	ds_read_b128 v[218:221], v152 offset:1024
	ds_read_b128 v[224:227], v152 offset:2048
	ds_read_b128 v[228:231], v152 offset:3072
	global_load_lds_dwordx4 v[162:163], off
	v_lshl_add_u64 v[162:163], v[164:165], 0, s[4:5]
	s_add_i32 m0, s21, 0x2000
	s_nop 0
	global_load_lds_dwordx4 v[162:163], off
	s_barrier
	s_waitcnt lgkmcnt(0)
	s_setprio 1
	s_waitcnt lgkmcnt(0)
	v_mfma_scale_f32_16x16x128_f8f6f4 v[132:135], v[214:221], v[182:189], v[132:135], v175, v175 op_sel_hi:[0,0,0]
	v_mfma_scale_f32_16x16x128_f8f6f4 v[124:127], v[224:231], v[182:189], v[124:127], v175, v175 op_sel_hi:[0,0,0]
	v_mfma_scale_f32_16x16x128_f8f6f4 v[116:119], v[214:221], v[190:197], v[116:119], v175, v175 op_sel_hi:[0,0,0]
	v_mfma_scale_f32_16x16x128_f8f6f4 v[108:111], v[224:231], v[190:197], v[108:111], v175, v175 op_sel_hi:[0,0,0]
	v_mfma_scale_f32_16x16x128_f8f6f4 v[100:103], v[214:221], v[198:205], v[100:103], v175, v175 op_sel_hi:[0,0,0]
	v_mfma_scale_f32_16x16x128_f8f6f4 v[92:95], v[224:231], v[198:205], v[92:95], v175, v175 op_sel_hi:[0,0,0]
	v_mfma_scale_f32_16x16x128_f8f6f4 v[84:87], v[214:221], v[206:213], v[84:87], v175, v175 op_sel_hi:[0,0,0]
	v_mfma_scale_f32_16x16x128_f8f6f4 v[80:83], v[224:231], v[206:213], v[80:83], v175, v175 op_sel_hi:[0,0,0]
	s_setprio 0
	s_mov_b32 m0, s43
	v_lshl_add_u64 v[162:163], v[166:167], 0, s[4:5]
	s_barrier
	ds_read_b128 v[182:185], v180 offset:49152
	ds_read_b128 v[186:189], v180 offset:50176
	ds_read_b128 v[190:193], v180 offset:51200
	ds_read_b128 v[194:197], v180 offset:52224
	ds_read_b128 v[198:201], v180 offset:53248
	ds_read_b128 v[202:205], v180 offset:54272
	ds_read_b128 v[206:209], v180 offset:55296
	ds_read_b128 v[210:213], v180 offset:56320
	global_load_lds_dwordx4 v[162:163], off
	v_lshl_add_u64 v[162:163], v[168:169], 0, s[4:5]
	s_mov_b32 m0, s44
	s_nop 0
	global_load_lds_dwordx4 v[162:163], off
	s_barrier
	s_waitcnt lgkmcnt(0)
	s_setprio 1
	s_waitcnt lgkmcnt(0)
	v_mfma_scale_f32_16x16x128_f8f6f4 v[76:79], v[0:7], v[182:189], v[76:79], v175, v175 op_sel_hi:[0,0,0]
	v_mfma_scale_f32_16x16x128_f8f6f4 v[72:75], v[8:15], v[182:189], v[72:75], v175, v175 op_sel_hi:[0,0,0]
	v_mfma_scale_f32_16x16x128_f8f6f4 v[64:67], v[0:7], v[190:197], v[64:67], v175, v175 op_sel_hi:[0,0,0]
	v_mfma_scale_f32_16x16x128_f8f6f4 v[56:59], v[8:15], v[190:197], v[56:59], v175, v175 op_sel_hi:[0,0,0]
	v_mfma_scale_f32_16x16x128_f8f6f4 v[48:51], v[0:7], v[198:205], v[48:51], v175, v175 op_sel_hi:[0,0,0]
	v_mfma_scale_f32_16x16x128_f8f6f4 v[40:43], v[8:15], v[198:205], v[40:43], v175, v175 op_sel_hi:[0,0,0]
	v_mfma_scale_f32_16x16x128_f8f6f4 v[32:35], v[0:7], v[206:213], v[32:35], v175, v175 op_sel_hi:[0,0,0]
	v_mfma_scale_f32_16x16x128_f8f6f4 v[24:27], v[8:15], v[206:213], v[24:27], v175, v175 op_sel_hi:[0,0,0]
	s_setprio 0
	s_barrier
	s_add_u32 s18, s18, 0x40080
	s_addc_u32 s19, s19, 0
	s_add_i32 s20, s20, s29
	v_lshl_add_u64 v[0:1], s[18:19], 0, v[146:147]
	s_mov_b32 m0, s20
	s_nop 0
	global_load_lds_dwordx4 v[0:1], off
	v_lshl_add_u64 v[0:1], s[18:19], 0, v[150:151]
	s_add_i32 m0, s20, 0x2000
	s_nop 0
	global_load_lds_dwordx4 v[0:1], off
	s_waitcnt vmcnt(6)
	s_barrier
	s_setprio 1
	v_mfma_scale_f32_16x16x128_f8f6f4 v[68:71], v[214:221], v[182:189], v[68:71], v175, v175 op_sel_hi:[0,0,0]
	v_mfma_scale_f32_16x16x128_f8f6f4 v[60:63], v[224:231], v[182:189], v[60:63], v175, v175 op_sel_hi:[0,0,0]
	v_mfma_scale_f32_16x16x128_f8f6f4 v[52:55], v[214:221], v[190:197], v[52:55], v175, v175 op_sel_hi:[0,0,0]
	v_mfma_scale_f32_16x16x128_f8f6f4 v[44:47], v[224:231], v[190:197], v[44:47], v175, v175 op_sel_hi:[0,0,0]
	v_mfma_scale_f32_16x16x128_f8f6f4 v[36:39], v[214:221], v[198:205], v[36:39], v175, v175 op_sel_hi:[0,0,0]
	v_mfma_scale_f32_16x16x128_f8f6f4 v[28:31], v[224:231], v[198:205], v[28:31], v175, v175 op_sel_hi:[0,0,0]
	v_mfma_scale_f32_16x16x128_f8f6f4 v[20:23], v[214:221], v[206:213], v[20:23], v175, v175 op_sel_hi:[0,0,0]
	v_mfma_scale_f32_16x16x128_f8f6f4 v[16:19], v[224:231], v[206:213], v[16:19], v175, v175 op_sel_hi:[0,0,0]
	s_setprio 0
	s_add_i32 s62, s62, 2
	s_add_u32 s60, s60, 0x100
	s_addc_u32 s61, s61, 0
	s_add_u32 s16, s16, 0x100
	s_addc_u32 s17, s17, 0
	s_cmp_gt_u32 s62, 13
	s_barrier
	s_cbranch_scc0 .LBB0_2262
	s_lshl_b32 s16, s55, 8
	s_min_i32 s17, s55, 32
	s_ashr_i32 s20, s17, 4
	s_add_i32 s17, s16, 0xffffe000
	s_cmp_lt_i32 s55, 32
	s_cselect_b32 s19, s48, 0x302b8000
	s_cselect_b32 s18, s16, s17
	s_add_u32 s55, s2, s19
	s_mul_i32 s20, s20, 6
	s_addc_u32 s56, s3, 0
	s_ashr_i32 s19, s18, 31
	s_ashr_i32 s17, s16, 31
	s_ashr_i32 s21, s20, 31
	s_lshl_b64 s[18:19], s[18:19], 12
	s_lshl_b64 s[16:17], s[16:17], 12
	s_lshl_b64 s[20:21], s[20:21], 13
	v_lshl_or_b32 v8, s54, 8, v178
	s_add_u32 s20, s2, s20
	s_addc_u32 s21, s3, s21
	v_ashrrev_i32_e32 v9, 31, v8
	v_lshl_add_u64 v[0:1], v[8:9], 2, s[20:21]
	v_lshl_add_u64 v[10:11], v[0:1], 0, s[6:7]
	v_add_co_u32_e32 v0, vcc, s49, v0
	s_nop 7
	s_nop 7
	s_nop 7
	s_add_u32 s18, s55, s18
	s_nop 0
	v_addc_co_u32_e32 v1, vcc, 0, v1, vcc
	v_add_u32_e32 v152, v177, v8
	global_load_dwordx4 v[0:3], v[0:1], off
	s_nop 0
	global_load_dwordx4 v[182:185], v[10:11], off offset:528
	global_load_dwordx4 v[4:7], v[10:11], off offset:16
	global_load_dwordx4 v[186:189], v[10:11], off offset:512
	s_addc_u32 s19, s56, s19
	s_add_u32 s16, s41, s16
	v_lshlrev_b64 v[222:223], 1, v[152:153]
	v_lshl_add_u64 v[8:9], s[18:19], 0, v[222:223]
	global_load_dwordx4 v[190:193], v[8:9], off
	v_add_u32_e32 v8, 0x80, v152
	v_mov_b32_e32 v9, v153
	v_lshlrev_b64 v[224:225], 1, v[8:9]
	v_lshl_add_u64 v[8:9], s[18:19], 0, v[224:225]
	global_load_dwordx4 v[194:197], v[8:9], off
	v_add_u32_e32 v8, 0x8000, v152
	v_mov_b32_e32 v9, v153
	v_lshlrev_b64 v[226:227], 1, v[8:9]
	v_lshl_add_u64 v[8:9], s[18:19], 0, v[226:227]
	global_load_dwordx4 v[198:201], v[8:9], off
	v_add_u32_e32 v8, 0x8080, v152
	v_mov_b32_e32 v9, v153
	v_lshlrev_b64 v[170:171], 1, v[8:9]
	v_lshl_add_u64 v[8:9], s[18:19], 0, v[170:171]
	global_load_dwordx4 v[202:205], v[8:9], off
	v_add_u32_e32 v8, 0x10000, v152
	v_mov_b32_e32 v9, v153
	v_lshlrev_b64 v[168:169], 1, v[8:9]
	v_lshl_add_u64 v[8:9], s[18:19], 0, v[168:169]
	global_load_dwordx4 v[206:209], v[8:9], off
	v_add_u32_e32 v8, 0x10080, v152
	v_mov_b32_e32 v9, v153
	v_lshlrev_b64 v[166:167], 1, v[8:9]
	v_lshl_add_u64 v[8:9], s[18:19], 0, v[166:167]
	global_load_dwordx4 v[210:213], v[8:9], off
	v_mov_b32_e32 v9, v153
	v_add_u32_e32 v8, 0x18000, v152
	v_lshlrev_b64 v[164:165], 1, v[8:9]
	v_lshl_add_u64 v[8:9], s[18:19], 0, v[164:165]
	global_load_dwordx4 v[214:217], v[8:9], off
	v_mov_b32_e32 v9, v153
	v_add_u32_e32 v8, 0x18080, v152
	v_lshlrev_b64 v[162:163], 1, v[8:9]
	v_lshl_add_u64 v[8:9], s[18:19], 0, v[162:163]
	global_load_dwordx4 v[218:221], v[8:9], off
	s_addc_u32 s17, s42, s17
	s_and_b64 vcc, exec, s[0:1]
	s_mov_b32 s54, s50
	s_mov_b32 s55, s51
	s_waitcnt vmcnt(0)
	v_pk_mul_f32 v[12:13], v[0:1], s[8:9] op_sel_hi:[1,0]
	v_pk_mul_f32 v[0:1], v[182:183], s[8:9] op_sel_hi:[1,0]
	v_pk_mul_f32 v[14:15], v[2:3], s[8:9] op_sel_hi:[1,0]
	v_pk_mul_f32 v[10:11], v[6:7], s[8:9] op_sel_hi:[1,0]
	v_pk_mul_f32 v[8:9], v[4:5], s[8:9] op_sel_hi:[1,0]
	v_pk_mul_f32 v[6:7], v[188:189], s[8:9] op_sel_hi:[1,0]
	v_pk_mul_f32 v[4:5], v[186:187], s[8:9] op_sel_hi:[1,0]
	v_pk_mul_f32 v[2:3], v[184:185], s[8:9] op_sel_hi:[1,0]
	v_lshlrev_b32_e32 v182, 16, v190
	v_and_b32_e32 v183, 0xffff0000, v190
	v_lshlrev_b32_e32 v184, 16, v191
	v_and_b32_e32 v185, 0xffff0000, v191
	v_lshlrev_b32_e32 v186, 16, v192
	v_and_b32_e32 v187, 0xffff0000, v192
	v_lshlrev_b32_e32 v188, 16, v193
	v_and_b32_e32 v189, 0xffff0000, v193
	v_lshlrev_b32_e32 v190, 16, v194
	v_and_b32_e32 v191, 0xffff0000, v194
	v_pk_fma_f32 v[140:141], v[140:141], v[12:13], v[182:183]
	v_lshlrev_b32_e32 v192, 16, v195
	v_and_b32_e32 v193, 0xffff0000, v195
	v_lshlrev_b32_e32 v194, 16, v196
	v_and_b32_e32 v195, 0xffff0000, v196
	v_lshlrev_b32_e32 v196, 16, v197
	v_and_b32_e32 v197, 0xffff0000, v197
	v_pk_fma_f32 v[142:143], v[142:143], v[14:15], v[184:185]
	v_pk_fma_f32 v[182:183], v[138:139], v[10:11], v[188:189]
	v_pk_fma_f32 v[138:139], v[136:137], v[8:9], v[186:187]
	v_cvt_pk_bf16_f32 v136, v140, v141
	v_cvt_pk_bf16_f32 v137, v142, v143
	v_lshl_add_u64 v[140:141], s[16:17], 0, v[222:223]
	v_pk_fma_f32 v[132:133], v[132:133], v[4:5], v[190:191]
	v_lshlrev_b32_e32 v228, 16, v198
	v_and_b32_e32 v229, 0xffff0000, v198
	v_lshlrev_b32_e32 v198, 16, v199
	v_and_b32_e32 v199, 0xffff0000, v199
	v_cvt_pk_bf16_f32 v138, v138, v139
	v_cvt_pk_bf16_f32 v139, v182, v183
	global_store_dwordx4 v[140:141], v[136:139], off sc1
	v_pk_fma_f32 v[134:135], v[134:135], v[6:7], v[192:193]
	v_lshlrev_b32_e32 v230, 16, v200
	v_pk_fma_f32 v[136:137], v[126:127], v[2:3], v[196:197]
	v_pk_fma_f32 v[126:127], v[124:125], v[0:1], v[194:195]
	v_cvt_pk_bf16_f32 v124, v132, v133
	v_cvt_pk_bf16_f32 v125, v134, v135
	v_lshl_add_u64 v[132:133], s[16:17], 0, v[224:225]
	v_and_b32_e32 v231, 0xffff0000, v200
	v_lshlrev_b32_e32 v200, 16, v201
	v_and_b32_e32 v201, 0xffff0000, v201
	v_lshlrev_b32_e32 v232, 16, v202
	v_and_b32_e32 v233, 0xffff0000, v202
	v_cvt_pk_bf16_f32 v126, v126, v127
	v_cvt_pk_bf16_f32 v127, v136, v137
	global_store_dwordx4 v[132:133], v[124:127], off sc1
	v_lshlrev_b32_e32 v202, 16, v203
	v_and_b32_e32 v203, 0xffff0000, v203
	v_pk_fma_f32 v[124:125], v[130:131], v[14:15], v[198:199]
	v_lshlrev_b32_e32 v234, 16, v204
	v_and_b32_e32 v235, 0xffff0000, v204
	v_lshlrev_b32_e32 v204, 16, v205
	v_and_b32_e32 v205, 0xffff0000, v205
	v_pk_fma_f32 v[126:127], v[128:129], v[12:13], v[228:229]
	v_pk_fma_f32 v[128:129], v[122:123], v[10:11], v[200:201]
	v_pk_fma_f32 v[122:123], v[120:121], v[8:9], v[230:231]
	v_cvt_pk_bf16_f32 v120, v126, v127
	v_cvt_pk_bf16_f32 v121, v124, v125
	v_lshl_add_u64 v[124:125], s[16:17], 0, v[226:227]
	v_pk_fma_f32 v[116:117], v[116:117], v[4:5], v[232:233]
	v_lshlrev_b32_e32 v236, 16, v206
	v_and_b32_e32 v237, 0xffff0000, v206
	v_lshlrev_b32_e32 v206, 16, v207
	v_and_b32_e32 v207, 0xffff0000, v207
	v_cvt_pk_bf16_f32 v122, v122, v123
	v_cvt_pk_bf16_f32 v123, v128, v129
	global_store_dwordx4 v[124:125], v[120:123], off sc1
	v_pk_fma_f32 v[118:119], v[118:119], v[6:7], v[202:203]
	v_lshlrev_b32_e32 v238, 16, v208
	v_pk_fma_f32 v[120:121], v[110:111], v[2:3], v[204:205]
	v_pk_fma_f32 v[110:111], v[108:109], v[0:1], v[234:235]
	v_cvt_pk_bf16_f32 v108, v116, v117
	v_cvt_pk_bf16_f32 v109, v118, v119
	v_lshl_add_u64 v[116:117], s[16:17], 0, v[170:171]
	v_and_b32_e32 v239, 0xffff0000, v208
	v_lshlrev_b32_e32 v208, 16, v209
	v_and_b32_e32 v209, 0xffff0000, v209
	v_lshlrev_b32_e32 v240, 16, v210
	v_and_b32_e32 v241, 0xffff0000, v210
	v_cvt_pk_bf16_f32 v110, v110, v111
	v_cvt_pk_bf16_f32 v111, v120, v121
	global_store_dwordx4 v[116:117], v[108:111], off sc1
	v_lshlrev_b32_e32 v210, 16, v211
	v_and_b32_e32 v211, 0xffff0000, v211
	v_pk_fma_f32 v[108:109], v[114:115], v[14:15], v[206:207]
	v_lshlrev_b32_e32 v242, 16, v212
	v_and_b32_e32 v243, 0xffff0000, v212
	v_lshlrev_b32_e32 v212, 16, v213
	v_and_b32_e32 v213, 0xffff0000, v213
	v_pk_fma_f32 v[110:111], v[112:113], v[12:13], v[236:237]
	v_pk_fma_f32 v[112:113], v[106:107], v[10:11], v[208:209]
	v_pk_fma_f32 v[106:107], v[104:105], v[8:9], v[238:239]
	v_cvt_pk_bf16_f32 v104, v110, v111
	v_cvt_pk_bf16_f32 v105, v108, v109
	v_lshl_add_u64 v[108:109], s[16:17], 0, v[168:169]
	v_pk_fma_f32 v[100:101], v[100:101], v[4:5], v[240:241]
	v_lshlrev_b32_e32 v244, 16, v214
	v_and_b32_e32 v245, 0xffff0000, v214
	v_lshlrev_b32_e32 v214, 16, v215
	v_and_b32_e32 v215, 0xffff0000, v215
	v_cvt_pk_bf16_f32 v106, v106, v107
	v_cvt_pk_bf16_f32 v107, v112, v113
	global_store_dwordx4 v[108:109], v[104:107], off sc1
	v_pk_fma_f32 v[102:103], v[102:103], v[6:7], v[210:211]
	v_lshlrev_b32_e32 v246, 16, v216
	v_pk_fma_f32 v[104:105], v[94:95], v[2:3], v[212:213]
	v_pk_fma_f32 v[94:95], v[92:93], v[0:1], v[242:243]
	v_cvt_pk_bf16_f32 v92, v100, v101
	v_cvt_pk_bf16_f32 v93, v102, v103
	v_lshl_add_u64 v[100:101], s[16:17], 0, v[166:167]
	v_and_b32_e32 v247, 0xffff0000, v216
	v_lshlrev_b32_e32 v216, 16, v217
	v_and_b32_e32 v217, 0xffff0000, v217
	v_lshlrev_b32_e32 v248, 16, v218
	v_and_b32_e32 v249, 0xffff0000, v218
	v_cvt_pk_bf16_f32 v94, v94, v95
	v_cvt_pk_bf16_f32 v95, v104, v105
	global_store_dwordx4 v[100:101], v[92:95], off sc1
	v_lshlrev_b32_e32 v218, 16, v219
	v_and_b32_e32 v219, 0xffff0000, v219
	v_pk_fma_f32 v[92:93], v[98:99], v[14:15], v[214:215]
	v_lshlrev_b32_e32 v172, 16, v220
	v_and_b32_e32 v173, 0xffff0000, v220
	v_lshlrev_b32_e32 v220, 16, v221
	v_and_b32_e32 v221, 0xffff0000, v221
	v_pk_fma_f32 v[94:95], v[96:97], v[12:13], v[244:245]
	v_pk_fma_f32 v[96:97], v[90:91], v[10:11], v[216:217]
	v_pk_fma_f32 v[90:91], v[88:89], v[8:9], v[246:247]
	v_cvt_pk_bf16_f32 v88, v94, v95
	v_cvt_pk_bf16_f32 v89, v92, v93
	v_lshl_add_u64 v[92:93], s[16:17], 0, v[164:165]
	v_pk_fma_f32 v[84:85], v[84:85], v[4:5], v[248:249]
	v_cvt_pk_bf16_f32 v90, v90, v91
	v_cvt_pk_bf16_f32 v91, v96, v97
	global_store_dwordx4 v[92:93], v[88:91], off sc1
	v_pk_fma_f32 v[86:87], v[86:87], v[6:7], v[218:219]
	s_nop 0
	v_pk_fma_f32 v[88:89], v[82:83], v[2:3], v[220:221]
	v_pk_fma_f32 v[82:83], v[80:81], v[0:1], v[172:173]
	v_cvt_pk_bf16_f32 v80, v84, v85
	v_cvt_pk_bf16_f32 v81, v86, v87
	v_lshl_add_u64 v[84:85], s[16:17], 0, v[162:163]
	v_cvt_pk_bf16_f32 v82, v82, v83
	v_cvt_pk_bf16_f32 v83, v88, v89
	global_store_dwordx4 v[84:85], v[80:83], off sc1
	s_nop 1
	v_add_u32_e32 v80, 0x40000, v152
	v_mov_b32_e32 v81, v153
	v_lshlrev_b64 v[122:123], 1, v[80:81]
	v_lshl_add_u64 v[80:81], s[18:19], 0, v[122:123]
	global_load_dwordx4 v[90:93], v[80:81], off
	v_add_u32_e32 v80, 0x40080, v152
	v_mov_b32_e32 v81, v153
	v_lshlrev_b64 v[124:125], 1, v[80:81]
	v_lshl_add_u64 v[80:81], s[18:19], 0, v[124:125]
	global_load_dwordx4 v[94:97], v[80:81], off
	v_add_u32_e32 v80, 0x48000, v152
	v_mov_b32_e32 v81, v153
	v_lshlrev_b64 v[126:127], 1, v[80:81]
	v_lshl_add_u64 v[80:81], s[18:19], 0, v[126:127]
	global_load_dwordx4 v[98:101], v[80:81], off
	v_add_u32_e32 v80, 0x48080, v152
	v_mov_b32_e32 v81, v153
	v_lshlrev_b64 v[88:89], 1, v[80:81]
	v_lshl_add_u64 v[80:81], s[18:19], 0, v[88:89]
	global_load_dwordx4 v[102:105], v[80:81], off
	v_add_u32_e32 v80, 0x50000, v152
	v_mov_b32_e32 v81, v153
	v_lshlrev_b64 v[86:87], 1, v[80:81]
	v_lshl_add_u64 v[80:81], s[18:19], 0, v[86:87]
	global_load_dwordx4 v[106:109], v[80:81], off
	v_add_u32_e32 v80, 0x50080, v152
	v_mov_b32_e32 v81, v153
	v_lshlrev_b64 v[84:85], 1, v[80:81]
	v_lshl_add_u64 v[80:81], s[18:19], 0, v[84:85]
	global_load_dwordx4 v[110:113], v[80:81], off
	v_add_u32_e32 v80, 0x58000, v152
	v_mov_b32_e32 v81, v153
	v_lshlrev_b64 v[82:83], 1, v[80:81]
	v_lshl_add_u64 v[80:81], s[18:19], 0, v[82:83]
	v_add_u32_e32 v152, 0x58080, v152
	global_load_dwordx4 v[114:117], v[80:81], off
	v_lshlrev_b64 v[80:81], 1, v[152:153]
	v_lshl_add_u64 v[118:119], s[18:19], 0, v[80:81]
	global_load_dwordx4 v[118:121], v[118:119], off
	s_mov_b64 s[18:19], s[10:11]
	s_waitcnt vmcnt(0)
	v_lshlrev_b32_e32 v128, 16, v90
	v_and_b32_e32 v129, 0xffff0000, v90
	v_lshlrev_b32_e32 v130, 16, v91
	v_and_b32_e32 v131, 0xffff0000, v91
	v_lshlrev_b32_e32 v132, 16, v92
	v_and_b32_e32 v133, 0xffff0000, v92
	v_lshlrev_b32_e32 v92, 16, v93
	v_and_b32_e32 v93, 0xffff0000, v93
	v_lshlrev_b32_e32 v134, 16, v94
	v_and_b32_e32 v135, 0xffff0000, v94
	v_pk_fma_f32 v[76:77], v[76:77], v[12:13], v[128:129]
	v_lshlrev_b32_e32 v94, 16, v95
	v_and_b32_e32 v95, 0xffff0000, v95
	v_lshlrev_b32_e32 v136, 16, v96
	v_and_b32_e32 v137, 0xffff0000, v96
	v_lshlrev_b32_e32 v96, 16, v97
	v_and_b32_e32 v97, 0xffff0000, v97
	v_pk_fma_f32 v[78:79], v[78:79], v[14:15], v[130:131]
	v_pk_fma_f32 v[92:93], v[74:75], v[10:11], v[92:93]
	v_pk_fma_f32 v[74:75], v[72:73], v[8:9], v[132:133]
	v_cvt_pk_bf16_f32 v72, v76, v77
	v_cvt_pk_bf16_f32 v73, v78, v79
	v_lshl_add_u64 v[76:77], s[16:17], 0, v[122:123]
	v_pk_fma_f32 v[68:69], v[68:69], v[4:5], v[134:135]
	v_lshlrev_b32_e32 v138, 16, v98
	v_and_b32_e32 v139, 0xffff0000, v98
	v_lshlrev_b32_e32 v98, 16, v99
	v_and_b32_e32 v99, 0xffff0000, v99
	v_cvt_pk_bf16_f32 v74, v74, v75
	v_cvt_pk_bf16_f32 v75, v92, v93
	global_store_dwordx4 v[76:77], v[72:75], off sc1
	v_pk_fma_f32 v[70:71], v[70:71], v[6:7], v[94:95]
	v_lshlrev_b32_e32 v140, 16, v100
	v_pk_fma_f32 v[72:73], v[62:63], v[2:3], v[96:97]
	v_pk_fma_f32 v[62:63], v[60:61], v[0:1], v[136:137]
	v_cvt_pk_bf16_f32 v60, v68, v69
	v_cvt_pk_bf16_f32 v61, v70, v71
	v_lshl_add_u64 v[68:69], s[16:17], 0, v[124:125]
	v_and_b32_e32 v141, 0xffff0000, v100
	v_lshlrev_b32_e32 v100, 16, v101
	v_and_b32_e32 v101, 0xffff0000, v101
	v_lshlrev_b32_e32 v142, 16, v102
	v_and_b32_e32 v143, 0xffff0000, v102
	v_cvt_pk_bf16_f32 v62, v62, v63
	v_cvt_pk_bf16_f32 v63, v72, v73
	global_store_dwordx4 v[68:69], v[60:63], off sc1
	v_lshlrev_b32_e32 v102, 16, v103
	v_and_b32_e32 v103, 0xffff0000, v103
	v_pk_fma_f32 v[60:61], v[66:67], v[14:15], v[98:99]
	v_lshlrev_b32_e32 v162, 16, v104
	v_and_b32_e32 v163, 0xffff0000, v104
	v_lshlrev_b32_e32 v104, 16, v105
	v_and_b32_e32 v105, 0xffff0000, v105
	v_pk_fma_f32 v[62:63], v[64:65], v[12:13], v[138:139]
	v_pk_fma_f32 v[64:65], v[58:59], v[10:11], v[100:101]
	v_pk_fma_f32 v[58:59], v[56:57], v[8:9], v[140:141]
	v_cvt_pk_bf16_f32 v56, v62, v63
	v_cvt_pk_bf16_f32 v57, v60, v61
	v_lshl_add_u64 v[60:61], s[16:17], 0, v[126:127]
	v_pk_fma_f32 v[52:53], v[52:53], v[4:5], v[142:143]
	v_lshlrev_b32_e32 v164, 16, v106
	v_and_b32_e32 v165, 0xffff0000, v106
	v_lshlrev_b32_e32 v106, 16, v107
	v_and_b32_e32 v107, 0xffff0000, v107
	v_cvt_pk_bf16_f32 v58, v58, v59
	v_cvt_pk_bf16_f32 v59, v64, v65
	global_store_dwordx4 v[60:61], v[56:59], off sc1
	v_pk_fma_f32 v[54:55], v[54:55], v[6:7], v[102:103]
	v_lshlrev_b32_e32 v166, 16, v108
	v_pk_fma_f32 v[56:57], v[46:47], v[2:3], v[104:105]
	v_pk_fma_f32 v[46:47], v[44:45], v[0:1], v[162:163]
	v_cvt_pk_bf16_f32 v44, v52, v53
	v_cvt_pk_bf16_f32 v45, v54, v55
	v_lshl_add_u64 v[52:53], s[16:17], 0, v[88:89]
	v_and_b32_e32 v167, 0xffff0000, v108
	v_lshlrev_b32_e32 v108, 16, v109
	v_and_b32_e32 v109, 0xffff0000, v109
	v_lshlrev_b32_e32 v168, 16, v110
	v_and_b32_e32 v169, 0xffff0000, v110
	v_cvt_pk_bf16_f32 v46, v46, v47
	v_cvt_pk_bf16_f32 v47, v56, v57
	global_store_dwordx4 v[52:53], v[44:47], off sc1
	v_lshlrev_b32_e32 v170, 16, v112
	v_and_b32_e32 v171, 0xffff0000, v112
	v_pk_fma_f32 v[44:45], v[50:51], v[14:15], v[106:107]
	v_lshlrev_b32_e32 v112, 16, v113
	v_and_b32_e32 v113, 0xffff0000, v113
	v_lshlrev_b32_e32 v172, 16, v114
	v_and_b32_e32 v173, 0xffff0000, v114
	v_pk_fma_f32 v[46:47], v[48:49], v[12:13], v[164:165]
	v_pk_fma_f32 v[48:49], v[42:43], v[10:11], v[108:109]
	v_pk_fma_f32 v[42:43], v[40:41], v[8:9], v[166:167]
	v_cvt_pk_bf16_f32 v40, v46, v47
	v_cvt_pk_bf16_f32 v41, v44, v45
	v_lshl_add_u64 v[44:45], s[16:17], 0, v[86:87]
	v_pk_fma_f32 v[36:37], v[36:37], v[4:5], v[168:169]
	v_lshlrev_b32_e32 v110, 16, v111
	v_and_b32_e32 v111, 0xffff0000, v111
	v_lshlrev_b32_e32 v114, 16, v115
	v_and_b32_e32 v115, 0xffff0000, v115
	v_lshlrev_b32_e32 v182, 16, v116
	v_and_b32_e32 v183, 0xffff0000, v116
	v_lshlrev_b32_e32 v116, 16, v117
	v_and_b32_e32 v117, 0xffff0000, v117
	v_lshlrev_b32_e32 v184, 16, v118
	v_and_b32_e32 v185, 0xffff0000, v118
	v_cvt_pk_bf16_f32 v42, v42, v43
	v_cvt_pk_bf16_f32 v43, v48, v49
	global_store_dwordx4 v[44:45], v[40:43], off sc1
	v_pk_fma_f32 v[12:13], v[32:33], v[12:13], v[172:173]
	v_lshlrev_b32_e32 v90, 16, v120
	v_pk_fma_f32 v[40:41], v[30:31], v[2:3], v[112:113]
	v_pk_fma_f32 v[30:31], v[28:29], v[0:1], v[170:171]
	v_cvt_pk_bf16_f32 v28, v36, v37
	v_lshl_add_u64 v[36:37], s[16:17], 0, v[84:85]
	v_and_b32_e32 v91, 0xffff0000, v120
	v_lshlrev_b32_e32 v120, 16, v121
	v_and_b32_e32 v121, 0xffff0000, v121
	v_pk_fma_f32 v[38:39], v[38:39], v[6:7], v[110:111]
	v_pk_fma_f32 v[14:15], v[34:35], v[14:15], v[114:115]
	v_cvt_pk_bf16_f32 v29, v38, v39
	v_cvt_pk_bf16_f32 v30, v30, v31
	v_cvt_pk_bf16_f32 v31, v40, v41
	global_store_dwordx4 v[36:37], v[28:31], off sc1
	v_pk_fma_f32 v[26:27], v[26:27], v[10:11], v[116:117]
	v_pk_fma_f32 v[10:11], v[24:25], v[8:9], v[182:183]
	v_cvt_pk_bf16_f32 v8, v12, v13
	v_cvt_pk_bf16_f32 v9, v14, v15
	v_lshl_add_u64 v[12:13], s[16:17], 0, v[82:83]
	v_pk_fma_f32 v[4:5], v[20:21], v[4:5], v[184:185]
	v_lshlrev_b32_e32 v118, 16, v119
	v_and_b32_e32 v119, 0xffff0000, v119
	v_cvt_pk_bf16_f32 v10, v10, v11
	v_cvt_pk_bf16_f32 v11, v26, v27
	global_store_dwordx4 v[12:13], v[8:11], off sc1
	v_pk_fma_f32 v[6:7], v[22:23], v[6:7], v[118:119]
	s_nop 0
	v_pk_fma_f32 v[8:9], v[18:19], v[2:3], v[120:121]
	v_pk_fma_f32 v[2:3], v[16:17], v[0:1], v[90:91]
	v_cvt_pk_bf16_f32 v0, v4, v5
	v_lshl_add_u64 v[4:5], s[16:17], 0, v[80:81]
	v_cvt_pk_bf16_f32 v1, v6, v7
	v_cvt_pk_bf16_f32 v2, v2, v3
	v_cvt_pk_bf16_f32 v3, v8, v9
	global_store_dwordx4 v[4:5], v[0:3], off sc1
	s_mov_b64 s[16:17], s[12:13]
	s_cbranch_vccz .LBB0_2255
	s_waitcnt vmcnt(0)
	s_cmpk_gt_u32 s23, 0xff
	s_cbranch_scc1 .LBB0_2266
	s_barrier

.LBB0_2334:
	s_waitcnt vmcnt(3)
	v_mul_f32_e32 v4, 0x42800000, v4
	s_waitcnt vmcnt(2)
	v_mul_f32_e32 v8, 0x42800000, v8
	v_med3_f32 v4, v4, s74, v101
	v_med3_f32 v8, v8, s74, v101
	v_mov_b32_e32 v67, v79
	v_cvt_pk_fp8_f32 v67, v4, v8
	s_waitcnt vmcnt(1)
	v_mul_f32_e32 v12, 0x42800000, v12
	s_waitcnt vmcnt(0)
	v_mul_f32_e32 v0, 0x42800000, v0
	v_med3_f32 v4, v12, s74, v101
	v_med3_f32 v0, v0, s74, v101
	v_cvt_pk_fp8_f32 v67, v4, v0 op_sel:[0,0,1]
	v_mul_f32_e32 v0, 0x42800000, v57
	v_mul_f32_e32 v4, 0x42800000, v53
	v_med3_f32 v0, v0, s74, v101
	v_med3_f32 v4, v4, s74, v101
	v_mov_b32_e32 v68, v79
	v_cvt_pk_fp8_f32 v68, v0, v4
	v_mul_f32_e32 v8, 0x42800000, v61
	v_mul_f32_e32 v0, 0x42800000, v45
	v_med3_f32 v4, v8, s74, v101
	v_med3_f32 v0, v0, s74, v101
	v_cvt_pk_fp8_f32 v68, v4, v0 op_sel:[0,0,1]
	v_mul_f32_e32 v0, 0x42800000, v41
	v_mul_f32_e32 v4, 0x42800000, v37
	v_med3_f32 v0, v0, s74, v101
	v_med3_f32 v4, v4, s74, v101
	v_mov_b32_e32 v69, v79
	v_cvt_pk_fp8_f32 v69, v0, v4
	v_mul_f32_e32 v8, 0x42800000, v49
	v_mul_f32_e32 v0, 0x42800000, v33
	v_med3_f32 v4, v8, s74, v101
	v_med3_f32 v0, v0, s74, v101
	v_cvt_pk_fp8_f32 v69, v4, v0 op_sel:[0,0,1]
	v_mul_f32_e32 v0, 0x42800000, v21
	v_mul_f32_e32 v4, 0x42800000, v25
	v_med3_f32 v0, v0, s74, v101
	v_med3_f32 v4, v4, s74, v101
	v_mov_b32_e32 v70, v79
	v_cvt_pk_fp8_f32 v70, v0, v4
	v_mul_f32_e32 v8, 0x42800000, v29
	v_mul_f32_e32 v0, 0x42800000, v17
	v_med3_f32 v4, v8, s74, v101
	v_med3_f32 v0, v0, s74, v101
	v_cvt_pk_fp8_f32 v70, v4, v0 op_sel:[0,0,1]
	v_mul_f32_e32 v0, 0x42800000, v5
	v_mul_f32_e32 v4, 0x42800000, v9
	v_med3_f32 v0, v0, s74, v101
	v_med3_f32 v4, v4, s74, v101
	v_mov_b32_e32 v71, v79
	v_cvt_pk_fp8_f32 v71, v0, v4
	v_mul_f32_e32 v5, 0x42800000, v13
	v_mul_f32_e32 v0, 0x42800000, v1
	v_med3_f32 v1, v5, s74, v101
	v_med3_f32 v0, v0, s74, v101
	v_cvt_pk_fp8_f32 v71, v1, v0 op_sel:[0,0,1]
	v_mul_f32_e32 v0, 0x42800000, v58
	v_mul_f32_e32 v1, 0x42800000, v54
	v_med3_f32 v0, v0, s74, v101
	v_med3_f32 v1, v1, s74, v101
	v_mov_b32_e32 v72, v79
	v_cvt_pk_fp8_f32 v72, v0, v1
	v_mul_f32_e32 v4, 0x42800000, v62
	v_mul_f32_e32 v0, 0x42800000, v46
	v_med3_f32 v1, v4, s74, v101
	v_med3_f32 v0, v0, s74, v101
	v_cvt_pk_fp8_f32 v72, v1, v0 op_sel:[0,0,1]
	v_mul_f32_e32 v0, 0x42800000, v42
	v_mul_f32_e32 v1, 0x42800000, v38
	v_med3_f32 v0, v0, s74, v101
	v_med3_f32 v1, v1, s74, v101
	v_mov_b32_e32 v73, v79
	v_cvt_pk_fp8_f32 v73, v0, v1
	v_mul_f32_e32 v4, 0x42800000, v50
	v_mul_f32_e32 v0, 0x42800000, v34
	v_med3_f32 v1, v4, s74, v101
	v_med3_f32 v0, v0, s74, v101
	v_cvt_pk_fp8_f32 v73, v1, v0 op_sel:[0,0,1]
	v_mul_f32_e32 v0, 0x42800000, v22
	v_mul_f32_e32 v1, 0x42800000, v26
	v_med3_f32 v0, v0, s74, v101
	v_med3_f32 v1, v1, s74, v101
	v_mov_b32_e32 v74, v79
	v_cvt_pk_fp8_f32 v74, v0, v1
	v_mul_f32_e32 v4, 0x42800000, v30
	v_mul_f32_e32 v0, 0x42800000, v18
	v_med3_f32 v1, v4, s74, v101
	v_med3_f32 v0, v0, s74, v101
	v_cvt_pk_fp8_f32 v74, v1, v0 op_sel:[0,0,1]
	v_mul_f32_e32 v0, 0x42800000, v6
	v_mul_f32_e32 v1, 0x42800000, v10
	v_med3_f32 v0, v0, s74, v101
	v_med3_f32 v1, v1, s74, v101
	v_mov_b32_e32 v75, v79
	v_cvt_pk_fp8_f32 v75, v0, v1
	v_mul_f32_e32 v4, 0x42800000, v14
	v_mul_f32_e32 v0, 0x42800000, v2
	v_med3_f32 v1, v4, s74, v101
	v_med3_f32 v0, v0, s74, v101
	v_cvt_pk_fp8_f32 v75, v1, v0 op_sel:[0,0,1]
	v_mul_f32_e32 v0, 0x42800000, v59
	v_mul_f32_e32 v1, 0x42800000, v55
	v_med3_f32 v0, v0, s74, v101
	v_med3_f32 v1, v1, s74, v101
	v_mov_b32_e32 v4, v79
	v_cvt_pk_fp8_f32 v4, v0, v1
	v_mul_f32_e32 v2, 0x42800000, v63
	v_mul_f32_e32 v0, 0x42800000, v47
	v_med3_f32 v1, v2, s74, v101
	v_med3_f32 v0, v0, s74, v101
	v_cvt_pk_fp8_f32 v4, v1, v0 op_sel:[0,0,1]
	v_mul_f32_e32 v0, 0x42800000, v43
	v_mul_f32_e32 v1, 0x42800000, v39
	v_med3_f32 v0, v0, s74, v101
	v_med3_f32 v1, v1, s74, v101
	v_mov_b32_e32 v5, v79
	v_cvt_pk_fp8_f32 v5, v0, v1
	v_mul_f32_e32 v2, 0x42800000, v51
	v_mul_f32_e32 v0, 0x42800000, v35
	v_med3_f32 v1, v2, s74, v101
	v_med3_f32 v0, v0, s74, v101
	v_cvt_pk_fp8_f32 v5, v1, v0 op_sel:[0,0,1]
	v_mul_f32_e32 v0, 0x42800000, v23
	v_mul_f32_e32 v1, 0x42800000, v27
	v_mul_f32_e32 v56, 0x42800000, v56
	v_mul_f32_e32 v52, 0x42800000, v52
	v_med3_f32 v0, v0, s74, v101
	v_med3_f32 v1, v1, s74, v101
	v_mov_b32_e32 v6, v79
	v_med3_f32 v56, v56, s74, v101
	v_med3_f32 v52, v52, s74, v101
	v_mov_b32_e32 v64, v79
	v_cvt_pk_fp8_f32 v6, v0, v1
	v_cvt_pk_fp8_f32 v64, v56, v52
	v_mul_f32_e32 v40, 0x42800000, v40
	v_mul_f32_e32 v36, 0x42800000, v36
	v_mul_f32_e32 v20, 0x42800000, v20
	v_mul_f32_e32 v24, 0x42800000, v24
	v_med3_f32 v40, v40, s74, v101
	v_med3_f32 v36, v36, s74, v101
	v_mov_b32_e32 v65, v79
	v_med3_f32 v20, v20, s74, v101
	v_med3_f32 v24, v24, s74, v101
	v_mov_b32_e32 v66, v79
	v_mul_f32_e32 v2, 0x42800000, v31
	v_mul_f32_e32 v0, 0x42800000, v19
	v_mul_f32_e32 v60, 0x42800000, v60
	v_mul_f32_e32 v44, 0x42800000, v44
	v_cvt_pk_fp8_f32 v65, v40, v36
	v_cvt_pk_fp8_f32 v66, v20, v24
	v_med3_f32 v1, v2, s74, v101
	v_med3_f32 v0, v0, s74, v101
	v_med3_f32 v52, v60, s74, v101
	v_med3_f32 v44, v44, s74, v101
	v_cvt_pk_fp8_f32 v6, v1, v0 op_sel:[0,0,1]
	v_mul_f32_e32 v0, 0x42800000, v7
	v_mul_f32_e32 v1, 0x42800000, v11
	v_cvt_pk_fp8_f32 v64, v52, v44 op_sel:[0,0,1]
	v_mul_f32_e32 v44, 0x42800000, v48
	v_mul_f32_e32 v32, 0x42800000, v32
	v_mul_f32_e32 v28, 0x42800000, v28
	v_mul_f32_e32 v16, 0x42800000, v16
	v_med3_f32 v0, v0, s74, v101
	v_med3_f32 v1, v1, s74, v101
	v_mov_b32_e32 v7, v79
	v_med3_f32 v36, v44, s74, v101
	v_med3_f32 v32, v32, s74, v101
	v_med3_f32 v20, v28, s74, v101
	v_med3_f32 v16, v16, s74, v101
	v_cvt_pk_fp8_f32 v7, v0, v1
	v_cvt_pk_fp8_f32 v65, v36, v32 op_sel:[0,0,1]
	v_cvt_pk_fp8_f32 v66, v20, v16 op_sel:[0,0,1]
	v_mul_f32_e32 v2, 0x42800000, v15
	v_mul_f32_e32 v0, 0x42800000, v3
	v_med3_f32 v1, v2, s74, v101
	v_med3_f32 v0, v0, s74, v101
	v_cvt_pk_fp8_f32 v7, v1, v0 op_sel:[0,0,1]
	s_mul_hi_i32 s3, s2, 0x380000
	s_mul_i32 s2, s2, 0x380000
	ds_write_b128 v98, v[64:67] offset:40960
	ds_write_b128 v98, v[68:71] offset:41040
	ds_write_b128 v98, v[72:75] offset:41120
	ds_write_b128 v98, v[4:7] offset:41200
	s_add_u32 s2, s55, s2
	s_waitcnt lgkmcnt(0)
	s_addc_u32 s3, s56, s3
	s_add_i32 s17, s17, s0
	s_ashr_i32 s0, s24, 31
	ds_read_b128 v[0:3], v99 offset:40960
	s_add_u32 s2, s2, s24
	v_add_u32_e32 v4, s17, v87
	s_addc_u32 s3, s3, s0
	v_ashrrev_i32_e32 v5, 31, v4
	v_lshl_add_u64 v[8:9], s[2:3], 0, v[80:81]
	v_lshlrev_b64 v[4:5], 9, v[4:5]
	v_lshl_add_u64 v[10:11], v[8:9], 0, v[4:5]
	ds_read_b128 v[4:7], v99 offset:42240
	s_waitcnt lgkmcnt(1)
	global_store_dwordx4 v[10:11], v[0:3], off sc1
	s_nop 1
	v_add_u32_e32 v0, s17, v77
	v_ashrrev_i32_e32 v1, 31, v0
	v_lshlrev_b64 v[0:1], 9, v[0:1]
	v_lshl_add_u64 v[0:1], v[8:9], 0, v[0:1]
	s_waitcnt lgkmcnt(0)
	global_store_dwordx4 v[0:1], v[4:7], off sc1
	ds_read_b128 v[0:3], v99 offset:43520
	s_nop 0
	v_add_u32_e32 v4, s17, v88
	v_ashrrev_i32_e32 v5, 31, v4
	v_lshlrev_b64 v[4:5], 9, v[4:5]
	v_lshl_add_u64 v[10:11], v[8:9], 0, v[4:5]
	ds_read_b128 v[4:7], v99 offset:44800
	s_waitcnt lgkmcnt(1)
	global_store_dwordx4 v[10:11], v[0:3], off sc1
	s_nop 1
	v_add_u32_e32 v0, s17, v89
	v_ashrrev_i32_e32 v1, 31, v0
	v_lshlrev_b64 v[0:1], 9, v[0:1]
	v_lshl_add_u64 v[0:1], v[8:9], 0, v[0:1]
	s_waitcnt lgkmcnt(0)
	global_store_dwordx4 v[0:1], v[4:7], off sc1
	s_waitcnt lgkmcnt(0)

.LBB0_2336:
	s_add_i32 s0, s68, 0xffff8341
	s_mul_hi_i32 s2, s0, 0x20d56b39
	s_lshr_b32 s3, s2, 31
	s_ashr_i32 s2, s2, 12
	s_add_i32 s2, s2, s3
	s_mul_i32 s3, s2, 0x7cc0
	s_sub_i32 s38, s0, s3
	s_cmpk_gt_i32 s38, 0x1cbf
	s_mov_b64 s[4:5], -1
	s_cbranch_scc0 .LBB0_2342
	s_add_i32 s7, s38, 0xffffe340
	s_and_b32 s6, s7, 0xff
	s_cmpk_gt_u32 s38, 0x5cbf
	s_cbranch_scc0 .LBB0_2339
	v_mov_b32_e32 v0, s69
	s_add_i32 s0, s38, 0xffffa340
	s_ashr_i32 s3, s2, 31
	ds_read_b64 v[0:1], v0
	s_lshr_b32 s0, s0, 8
	s_lshl_b64 s[4:5], s[2:3], 26
	s_add_u32 s8, s45, s4
	s_addc_u32 s9, s46, s5
	s_lshl_b64 s[4:5], s[0:1], 20
	s_add_u32 s4, s8, s4
	s_addc_u32 s5, s9, s5
	s_waitcnt lgkmcnt(0)
	v_readfirstlane_b32 s16, v0
	s_lshl_b64 s[8:9], s[2:3], 27
	v_readfirstlane_b32 s17, v1
	s_add_u32 s3, s16, s8
	s_addc_u32 s17, s17, s9
	s_lshl_b64 s[8:9], s[0:1], 22
	s_add_u32 s16, s3, s8
	s_addc_u32 s17, s17, s9
	s_lshl_b32 s0, s6, 3
	s_and_b32 s3, s0, 0x7c0
	s_lshl_b32 s0, s38, 6
	s_and_b32 s8, s0, 0x1c0
	v_or_b32_e32 v0, s8, v76
	v_lshlrev_b32_e32 v0, 13, v0
	v_mov_b32_e32 v1, v79
	v_lshl_add_u64 v[0:1], s[16:17], 0, v[0:1]
	s_lshl_b32 s0, s3, 2
	v_lshl_add_u64 v[0:1], v[0:1], 0, s[0:1]
	v_mov_b32_e32 v83, v79
	v_lshl_add_u64 v[60:61], v[0:1], 0, v[82:83]
	v_add_co_u32_e32 v4, vcc, s70, v60
	s_mov_b32 s0, 0x8000
	s_nop 0
	v_addc_co_u32_e32 v5, vcc, 0, v61, vcc
	v_add_co_u32_e32 v8, vcc, s71, v60
	global_load_dwordx4 v[0:3], v[60:61], off nt
	s_nop 0
	global_load_dwordx4 v[4:7], v[4:5], off nt
	v_addc_co_u32_e32 v9, vcc, 0, v61, vcc
	v_add_co_u32_e32 v10, vcc, s72, v60
	v_mov_b32_e32 v64, v79
	s_nop 0
	v_addc_co_u32_e32 v11, vcc, 0, v61, vcc
	v_add_co_u32_e32 v16, vcc, s0, v60
	s_mov_b32 s0, 0xa000
	s_nop 0
	v_addc_co_u32_e32 v17, vcc, 0, v61, vcc
	v_add_co_u32_e32 v20, vcc, s0, v60
	s_mov_b32 s0, 0xc000
	s_nop 0
	v_addc_co_u32_e32 v21, vcc, 0, v61, vcc
	v_add_co_u32_e32 v24, vcc, s0, v60
	s_mov_b32 s0, 0xe000
	s_nop 0
	v_addc_co_u32_e32 v25, vcc, 0, v61, vcc
	global_load_dwordx4 v[12:15], v[8:9], off nt
	s_nop 0
	global_load_dwordx4 v[8:11], v[10:11], off nt
	v_add_co_u32_e32 v26, vcc, s0, v60
	s_mov_b32 s0, 0x10000
	s_nop 0
	v_addc_co_u32_e32 v27, vcc, 0, v61, vcc
	global_load_dwordx4 v[16:19], v[16:17], off nt
	s_nop 0
	global_load_dwordx4 v[20:23], v[20:21], off nt
	v_add_co_u32_e32 v28, vcc, s0, v60
	s_mov_b32 s0, 0x14000
	s_nop 0
	v_addc_co_u32_e32 v29, vcc, 0, v61, vcc
	v_add_co_u32_e32 v36, vcc, s73, v60
	global_load_dwordx4 v[32:35], v[24:25], off nt
	s_nop 0
	global_load_dwordx4 v[24:27], v[26:27], off nt
	v_addc_co_u32_e32 v37, vcc, 0, v61, vcc
	v_add_co_u32_e32 v40, vcc, s0, v60
	s_mov_b32 s0, 0x16000
	s_nop 0
	v_addc_co_u32_e32 v41, vcc, 0, v61, vcc
	global_load_dwordx4 v[28:31], v[28:29], off nt
	s_nop 0
	global_load_dwordx4 v[36:39], v[36:37], off nt
	v_add_co_u32_e32 v42, vcc, s0, v60
	s_mov_b32 s0, 0x18000
	s_nop 0
	v_addc_co_u32_e32 v43, vcc, 0, v61, vcc
	v_add_co_u32_e32 v48, vcc, s0, v60
	s_mov_b32 s0, 0x1a000
	s_nop 0
	v_addc_co_u32_e32 v49, vcc, 0, v61, vcc
	global_load_dwordx4 v[44:47], v[40:41], off nt
	s_nop 0
	global_load_dwordx4 v[40:43], v[42:43], off nt
	v_add_co_u32_e32 v52, vcc, s0, v60
	s_mov_b32 s0, 0x1c000
	s_nop 0
	v_addc_co_u32_e32 v53, vcc, 0, v61, vcc
	global_load_dwordx4 v[48:51], v[48:49], off nt
	s_nop 0
	global_load_dwordx4 v[52:55], v[52:53], off nt
	v_add_co_u32_e32 v56, vcc, s0, v60
	s_mov_b32 s0, 0x1e000
	s_nop 0
	v_addc_co_u32_e32 v57, vcc, 0, v61, vcc
	v_add_co_u32_e32 v60, vcc, s0, v60
	global_load_dwordx4 v[56:59], v[56:57], off nt
	s_nop 0
	v_addc_co_u32_e32 v61, vcc, 0, v61, vcc
	global_load_dwordx4 v[60:63], v[60:61], off nt
	v_mov_b32_e32 v65, v79
	v_mov_b32_e32 v66, v79
	v_mov_b32_e32 v67, v79
	v_mov_b32_e32 v68, v79
	v_mov_b32_e32 v69, v79
	s_waitcnt vmcnt(15)
	v_mul_f32_e32 v0, 0x42000000, v0
	s_waitcnt vmcnt(14)
	v_mul_f32_e32 v4, 0x42000000, v4
	v_med3_f32 v0, v0, s74, v101
	v_med3_f32 v4, v4, s74, v101
	v_cvt_pk_fp8_f32 v64, v0, v4
	v_mov_b32_e32 v70, v79
	v_mov_b32_e32 v71, v79
	v_mov_b32_e32 v72, v79
	v_mov_b32_e32 v73, v79
	v_mov_b32_e32 v74, v79
	v_mov_b32_e32 v75, v79
	s_add_u32 s4, s4, s8
	s_addc_u32 s5, s5, 0
	s_waitcnt vmcnt(13)
	v_mul_f32_e32 v12, 0x42000000, v12
	s_waitcnt vmcnt(12)
	v_mul_f32_e32 v0, 0x42000000, v8
	v_med3_f32 v4, v12, s74, v101
	v_med3_f32 v0, v0, s74, v101
	v_cvt_pk_fp8_f32 v64, v4, v0 op_sel:[0,0,1]
	s_waitcnt vmcnt(11)
	v_mul_f32_e32 v0, 0x42000000, v16
	s_waitcnt vmcnt(10)
	v_mul_f32_e32 v4, 0x42000000, v20
	v_med3_f32 v0, v0, s74, v101
	v_med3_f32 v4, v4, s74, v101
	v_cvt_pk_fp8_f32 v65, v0, v4
	s_waitcnt vmcnt(9)
	v_mul_f32_e32 v8, 0x42000000, v32
	s_waitcnt vmcnt(8)
	v_mul_f32_e32 v0, 0x42000000, v24
	v_med3_f32 v4, v8, s74, v101
	v_med3_f32 v0, v0, s74, v101
	v_cvt_pk_fp8_f32 v65, v4, v0 op_sel:[0,0,1]
	s_waitcnt vmcnt(7)
	v_mul_f32_e32 v0, 0x42000000, v28
	s_waitcnt vmcnt(6)
	v_mul_f32_e32 v4, 0x42000000, v36
	v_med3_f32 v0, v0, s74, v101
	v_med3_f32 v4, v4, s74, v101
	v_cvt_pk_fp8_f32 v66, v0, v4
	s_waitcnt vmcnt(5)
	v_mul_f32_e32 v8, 0x42000000, v44
	s_waitcnt vmcnt(4)
	v_mul_f32_e32 v0, 0x42000000, v40
	v_med3_f32 v4, v8, s74, v101
	v_med3_f32 v0, v0, s74, v101
	v_cvt_pk_fp8_f32 v66, v4, v0 op_sel:[0,0,1]
	s_waitcnt vmcnt(3)
	v_mul_f32_e32 v0, 0x42000000, v48
	s_waitcnt vmcnt(2)
	v_mul_f32_e32 v4, 0x42000000, v52
	v_med3_f32 v0, v0, s74, v101
	v_med3_f32 v4, v4, s74, v101
	v_cvt_pk_fp8_f32 v67, v0, v4
	s_waitcnt vmcnt(1)
	v_mul_f32_e32 v8, 0x42000000, v56
	v_med3_f32 v4, v8, s74, v101
	s_waitcnt vmcnt(0)
	v_mul_f32_e32 v0, 0x42000000, v60
	v_med3_f32 v0, v0, s74, v101
	v_cvt_pk_fp8_f32 v67, v4, v0 op_sel:[0,0,1]
	v_mul_f32_e32 v0, 0x42000000, v1
	v_mul_f32_e32 v1, 0x42000000, v5
	v_med3_f32 v0, v0, s74, v101
	v_med3_f32 v1, v1, s74, v101
	v_cvt_pk_fp8_f32 v68, v0, v1
	v_mul_f32_e32 v4, 0x42000000, v13
	v_mul_f32_e32 v0, 0x42000000, v9
	v_med3_f32 v1, v4, s74, v101
	v_med3_f32 v0, v0, s74, v101
	v_cvt_pk_fp8_f32 v68, v1, v0 op_sel:[0,0,1]
	v_mul_f32_e32 v0, 0x42000000, v17
	v_mul_f32_e32 v1, 0x42000000, v21
	v_med3_f32 v0, v0, s74, v101
	v_med3_f32 v1, v1, s74, v101
	v_cvt_pk_fp8_f32 v69, v0, v1
	v_mul_f32_e32 v4, 0x42000000, v33
	v_mul_f32_e32 v0, 0x42000000, v25
	v_med3_f32 v1, v4, s74, v101
	v_med3_f32 v0, v0, s74, v101
	v_cvt_pk_fp8_f32 v69, v1, v0 op_sel:[0,0,1]
	v_mul_f32_e32 v0, 0x42000000, v29
	v_mul_f32_e32 v1, 0x42000000, v37
	v_med3_f32 v0, v0, s74, v101
	v_med3_f32 v1, v1, s74, v101
	v_cvt_pk_fp8_f32 v70, v0, v1
	v_mul_f32_e32 v4, 0x42000000, v45
	v_mul_f32_e32 v0, 0x42000000, v41
	v_med3_f32 v1, v4, s74, v101
	v_med3_f32 v0, v0, s74, v101
	v_cvt_pk_fp8_f32 v70, v1, v0 op_sel:[0,0,1]
	v_mul_f32_e32 v0, 0x42000000, v49
	v_mul_f32_e32 v1, 0x42000000, v53
	v_med3_f32 v0, v0, s74, v101
	v_med3_f32 v1, v1, s74, v101
	v_cvt_pk_fp8_f32 v71, v0, v1
	v_mul_f32_e32 v4, 0x42000000, v57
	v_mul_f32_e32 v0, 0x42000000, v61
	v_med3_f32 v1, v4, s74, v101
	v_med3_f32 v0, v0, s74, v101
	v_cvt_pk_fp8_f32 v71, v1, v0 op_sel:[0,0,1]
	v_mul_f32_e32 v0, 0x42000000, v2
	v_mul_f32_e32 v1, 0x42000000, v6
	v_med3_f32 v0, v0, s74, v101
	v_med3_f32 v1, v1, s74, v101
	v_cvt_pk_fp8_f32 v72, v0, v1
	v_mul_f32_e32 v2, 0x42000000, v14
	v_mul_f32_e32 v0, 0x42000000, v10
	v_med3_f32 v1, v2, s74, v101
	v_med3_f32 v0, v0, s74, v101
	v_cvt_pk_fp8_f32 v72, v1, v0 op_sel:[0,0,1]
	v_mul_f32_e32 v0, 0x42000000, v18
	v_mul_f32_e32 v1, 0x42000000, v22
	v_med3_f32 v0, v0, s74, v101
	v_med3_f32 v1, v1, s74, v101
	v_cvt_pk_fp8_f32 v73, v0, v1
	v_mul_f32_e32 v2, 0x42000000, v34
	v_mul_f32_e32 v0, 0x42000000, v26
	v_med3_f32 v1, v2, s74, v101
	v_med3_f32 v0, v0, s74, v101
	v_cvt_pk_fp8_f32 v73, v1, v0 op_sel:[0,0,1]
	v_mul_f32_e32 v0, 0x42000000, v30
	v_mul_f32_e32 v1, 0x42000000, v38
	v_med3_f32 v0, v0, s74, v101
	v_med3_f32 v1, v1, s74, v101
	v_cvt_pk_fp8_f32 v74, v0, v1
	v_mul_f32_e32 v2, 0x42000000, v46
	v_mul_f32_e32 v0, 0x42000000, v42
	v_med3_f32 v1, v2, s74, v101
	v_med3_f32 v0, v0, s74, v101
	v_cvt_pk_fp8_f32 v74, v1, v0 op_sel:[0,0,1]
	v_mul_f32_e32 v0, 0x42000000, v50
	v_mul_f32_e32 v1, 0x42000000, v54
	v_med3_f32 v0, v0, s74, v101
	v_med3_f32 v1, v1, s74, v101
	v_cvt_pk_fp8_f32 v75, v0, v1
	v_mul_f32_e32 v2, 0x42000000, v58
	v_mul_f32_e32 v0, 0x42000000, v62
	v_med3_f32 v1, v2, s74, v101
	v_med3_f32 v0, v0, s74, v101
	v_cvt_pk_fp8_f32 v75, v1, v0 op_sel:[0,0,1]
	v_mul_f32_e32 v0, 0x42000000, v3
	v_mul_f32_e32 v1, 0x42000000, v7
	v_med3_f32 v3, v0, s74, v101
	v_med3_f32 v1, v1, s74, v101
	v_mov_b32_e32 v0, v79
	v_cvt_pk_fp8_f32 v0, v3, v1
	v_mul_f32_e32 v2, 0x42000000, v15
	v_mul_f32_e32 v1, 0x42000000, v11
	v_med3_f32 v2, v2, s74, v101
	v_med3_f32 v1, v1, s74, v101
	v_cvt_pk_fp8_f32 v0, v2, v1 op_sel:[0,0,1]
	v_mul_f32_e32 v1, 0x42000000, v19
	v_mul_f32_e32 v2, 0x42000000, v23
	v_med3_f32 v4, v1, s74, v101
	v_med3_f32 v2, v2, s74, v101
	v_mov_b32_e32 v1, v79
	v_cvt_pk_fp8_f32 v1, v4, v2
	v_mul_f32_e32 v3, 0x42000000, v35
	v_mul_f32_e32 v2, 0x42000000, v27
	v_med3_f32 v3, v3, s74, v101
	v_med3_f32 v2, v2, s74, v101
	v_cvt_pk_fp8_f32 v1, v3, v2 op_sel:[0,0,1]
	v_mul_f32_e32 v2, 0x42000000, v31
	v_mul_f32_e32 v3, 0x42000000, v39
	v_med3_f32 v5, v2, s74, v101
	v_med3_f32 v3, v3, s74, v101
	v_mov_b32_e32 v2, v79
	v_cvt_pk_fp8_f32 v2, v5, v3
	v_mul_f32_e32 v4, 0x42000000, v47
	v_mul_f32_e32 v3, 0x42000000, v43
	v_med3_f32 v4, v4, s74, v101
	v_med3_f32 v3, v3, s74, v101
	v_cvt_pk_fp8_f32 v2, v4, v3 op_sel:[0,0,1]
	v_mul_f32_e32 v3, 0x42000000, v51
	v_mul_f32_e32 v4, 0x42000000, v55
	v_med3_f32 v6, v3, s74, v101
	v_med3_f32 v4, v4, s74, v101
	v_mov_b32_e32 v3, v79
	v_cvt_pk_fp8_f32 v3, v6, v4
	v_mul_f32_e32 v5, 0x42000000, v59
	v_mul_f32_e32 v4, 0x42000000, v63
	v_med3_f32 v5, v5, s74, v101
	v_med3_f32 v4, v4, s74, v101
	v_cvt_pk_fp8_f32 v3, v5, v4 op_sel:[0,0,1]
	ds_write_b128 v98, v[64:67] offset:40960
	ds_write_b128 v98, v[68:71] offset:41040
	ds_write_b128 v98, v[72:75] offset:41120
	ds_write_b128 v98, v[0:3] offset:41200
	s_waitcnt lgkmcnt(0)
	ds_read_b128 v[0:3], v99 offset:40960
	v_or_b32_e32 v4, s3, v87
	v_lshl_add_u64 v[8:9], s[4:5], 0, v[80:81]
	v_lshlrev_b32_e32 v4, 9, v4
	v_mov_b32_e32 v5, v79
	v_lshl_add_u64 v[10:11], v[8:9], 0, v[4:5]
	ds_read_b128 v[4:7], v99 offset:42240
	s_waitcnt lgkmcnt(1)
	global_store_dwordx4 v[10:11], v[0:3], off sc1
	s_mov_b64 s[4:5], 0
	s_nop 0
	v_or_b32_e32 v0, s3, v77
	v_lshlrev_b32_e32 v0, 9, v0
	v_mov_b32_e32 v1, v79
	v_lshl_add_u64 v[0:1], v[8:9], 0, v[0:1]
	s_waitcnt lgkmcnt(0)
	global_store_dwordx4 v[0:1], v[4:7], off sc1
	ds_read_b128 v[0:3], v99 offset:43520
	s_nop 0
	v_or_b32_e32 v4, s3, v88
	v_lshlrev_b32_e32 v4, 9, v4
	v_mov_b32_e32 v5, v79
	v_lshl_add_u64 v[10:11], v[8:9], 0, v[4:5]
	ds_read_b128 v[4:7], v99 offset:44800
	s_waitcnt lgkmcnt(1)
	global_store_dwordx4 v[10:11], v[0:3], off sc1
	s_nop 1
	v_or_b32_e32 v0, s3, v89
	v_lshlrev_b32_e32 v0, 9, v0
	v_mov_b32_e32 v1, v79
	v_lshl_add_u64 v[0:1], v[8:9], 0, v[0:1]
	s_waitcnt lgkmcnt(0)
	global_store_dwordx4 v[0:1], v[4:7], off sc1
	s_waitcnt lgkmcnt(0)
.LBB0_2339:
	s_andn2_b64 vcc, exec, s[4:5]
	s_cbranch_vccnz .LBB0_2341
	s_ashr_i32 s3, s2, 31
	s_lshr_b32 s0, s7, 9
	s_bfe_u32 s7, s7, 0x10008
	s_lshl_b64 s[8:9], s[2:3], 27
	s_add_u32 s3, s47, s8
	s_addc_u32 s16, s48, s9
	s_lshl_b32 s17, s7, 18
	s_lshl_b64 s[4:5], s[0:1], 21
	s_add_u32 s3, s3, s4
	s_addc_u32 s4, s16, s5
	s_add_u32 s3, s3, s17
	s_addc_u32 s4, s4, 0
	s_lshl_b32 s5, s7, 3
	s_add_i32 s5, s5, 0
	s_add_i32 s5, s5, 0x204e8
	v_mov_b32_e32 v0, s5
	ds_read_b64 v[0:1], v0
	v_mov_b32_e32 v83, v79
	v_mov_b32_e32 v12, v79
	v_mov_b32_e32 v14, v79
	v_mov_b32_e32 v13, v79
	s_waitcnt lgkmcnt(0)
	v_readfirstlane_b32 s5, v0
	v_readfirstlane_b32 s7, v1
	s_add_u32 s5, s5, s8
	s_addc_u32 s7, s7, s9
	s_lshl_b64 s[8:9], s[0:1], 22
	s_add_u32 s8, s5, s8
	s_addc_u32 s9, s7, s9
	s_lshl_b32 s0, s38, 6
	s_and_b32 s5, s0, 0x7c0
	v_or_b32_e32 v0, s5, v76
	v_lshlrev_b32_e32 v0, 11, v0
	v_mov_b32_e32 v1, v79
	s_lshl_b32 s0, s6, 3
	v_lshl_add_u64 v[0:1], s[8:9], 0, v[0:1]
	s_and_b32 s0, s0, 0x700
	v_lshl_add_u64 v[0:1], v[0:1], 0, s[0:1]
	v_lshl_add_u64 v[0:1], v[0:1], 0, v[82:83]
	s_movk_i32 s0, 0x1000
	v_add_co_u32_e32 v2, vcc, s0, v0
	s_movk_i32 s0, 0x3000
	s_nop 0
	v_addc_co_u32_e32 v3, vcc, 0, v1, vcc
	v_add_co_u32_e32 v4, vcc, s70, v0
	global_load_dwordx4 v[28:31], v[0:1], off nt
	global_load_dwordx4 v[32:35], v[0:1], off offset:2048 nt
	v_addc_co_u32_e32 v5, vcc, 0, v1, vcc
	global_load_dwordx4 v[56:59], v[4:5], off offset:-4096 nt
	global_load_dwordx4 v[16:19], v[4:5], off nt
	global_load_dwordx4 v[20:23], v[4:5], off offset:2048 nt
	v_add_co_u32_e32 v4, vcc, s0, v0
	v_mov_b32_e32 v68, v79
	s_nop 0
	v_addc_co_u32_e32 v5, vcc, 0, v1, vcc
	v_add_co_u32_e32 v6, vcc, s71, v0
	v_mov_b32_e32 v69, v79
	s_nop 0
	v_addc_co_u32_e32 v7, vcc, 0, v1, vcc
	global_load_dwordx4 v[64:67], v[2:3], off offset:2048 nt
	global_load_dwordx4 v[44:47], v[4:5], off offset:2048 nt
	global_load_dwordx4 v[60:63], v[6:7], off offset:-4096 nt
	global_load_dwordx4 v[24:27], v[6:7], off nt
	v_add_co_u32_e32 v2, vcc, s75, v0
	v_mov_b32_e32 v70, v79
	s_nop 0
	v_addc_co_u32_e32 v3, vcc, 0, v1, vcc
	v_add_co_u32_e32 v8, vcc, s72, v0
	v_mov_b32_e32 v71, v79
	s_nop 0
	v_addc_co_u32_e32 v9, vcc, 0, v1, vcc
	global_load_dwordx4 v[48:51], v[6:7], off offset:2048 nt
	global_load_dwordx4 v[52:55], v[8:9], off offset:-4096 nt
	global_load_dwordx4 v[36:39], v[2:3], off offset:2048 nt
	s_nop 0
	global_load_dwordx4 v[4:7], v[8:9], off nt
	s_nop 0
	global_load_dwordx4 v[8:11], v[8:9], off offset:2048 nt
	v_add_co_u32_e32 v0, vcc, s76, v0
	v_mov_b32_e32 v72, v79
	s_nop 0
	v_addc_co_u32_e32 v1, vcc, 0, v1, vcc
	global_load_dwordx4 v[40:43], v[0:1], off nt
	s_nop 0
	global_load_dwordx4 v[0:3], v[0:1], off offset:2048 nt
	v_mov_b32_e32 v73, v79
	v_mov_b32_e32 v74, v79
	v_mov_b32_e32 v75, v79
	s_lshl_b32 s0, s6, 1
	s_add_u32 s8, s3, s5
	s_addc_u32 s9, s4, 0
	s_lshl_b32 s3, s6, 2
	s_and_b32 s3, s3, 0x300
	s_and_b32 s0, s0, 64
	s_or_b32 s0, s0, s3
	s_waitcnt vmcnt(15)
	v_mul_f32_e32 v15, 0x42800000, v28
	s_waitcnt vmcnt(14)
	v_mul_f32_e32 v28, 0x42800000, v32
	v_med3_f32 v15, v15, s74, v101
	v_med3_f32 v28, v28, s74, v101
	v_cvt_pk_fp8_f32 v12, v15, v28
	s_waitcnt vmcnt(12)
	v_mul_f32_e32 v16, 0x42800000, v16
	s_waitcnt vmcnt(11)
	v_mul_f32_e32 v20, 0x42800000, v20
	v_med3_f32 v15, v16, s74, v101
	v_med3_f32 v16, v20, s74, v101
	v_cvt_pk_fp8_f32 v13, v15, v16
	v_mul_f32_e32 v32, 0x42800000, v56
	v_med3_f32 v32, v32, s74, v101
	s_waitcnt vmcnt(10)
	v_mul_f32_e32 v56, 0x42800000, v64
	s_waitcnt vmcnt(9)
	v_mul_f32_e32 v44, 0x42800000, v44
	v_med3_f32 v28, v44, s74, v101
	s_waitcnt vmcnt(7)
	v_mul_f32_e32 v24, 0x42800000, v24
	v_med3_f32 v24, v24, s74, v101
	v_mul_f32_e32 v60, 0x42800000, v60
	v_med3_f32 v56, v56, s74, v101
	v_med3_f32 v20, v60, s74, v101
	v_cvt_pk_fp8_f32 v12, v32, v56 op_sel:[0,0,1]
	v_cvt_pk_fp8_f32 v13, v20, v28 op_sel:[0,0,1]
	s_waitcnt vmcnt(6)
	v_mul_f32_e32 v48, 0x42800000, v48
	v_med3_f32 v44, v48, s74, v101
	v_cvt_pk_fp8_f32 v14, v24, v44
	s_waitcnt vmcnt(5)
	v_mul_f32_e32 v52, 0x42800000, v52
	s_waitcnt vmcnt(4)
	v_mul_f32_e32 v36, 0x42800000, v36
	s_waitcnt vmcnt(3)
	v_mul_f32_e32 v4, 0x42800000, v4
	s_waitcnt vmcnt(2)
	v_mul_f32_e32 v8, 0x42800000, v8
	v_med3_f32 v48, v52, s74, v101
	v_med3_f32 v15, v36, s74, v101
	v_cvt_pk_fp8_f32 v14, v48, v15 op_sel:[0,0,1]
	v_med3_f32 v4, v4, s74, v101
	v_med3_f32 v8, v8, s74, v101
	v_mov_b32_e32 v15, v79
	v_cvt_pk_fp8_f32 v15, v4, v8
	s_waitcnt vmcnt(1)
	v_mul_f32_e32 v16, 0x42800000, v40
	s_waitcnt vmcnt(0)
	v_mul_f32_e32 v0, 0x42800000, v0
	v_med3_f32 v4, v16, s74, v101
	v_med3_f32 v0, v0, s74, v101
	v_cvt_pk_fp8_f32 v15, v4, v0 op_sel:[0,0,1]
	v_mul_f32_e32 v0, 0x42800000, v29
	v_mul_f32_e32 v4, 0x42800000, v33
	v_med3_f32 v0, v0, s74, v101
	v_med3_f32 v4, v4, s74, v101
	v_cvt_pk_fp8_f32 v68, v0, v4
	v_mul_f32_e32 v8, 0x42800000, v57
	v_mul_f32_e32 v0, 0x42800000, v65
	v_med3_f32 v4, v8, s74, v101
	v_med3_f32 v0, v0, s74, v101
	v_cvt_pk_fp8_f32 v68, v4, v0 op_sel:[0,0,1]
	v_mul_f32_e32 v0, 0x42800000, v17
	v_mul_f32_e32 v4, 0x42800000, v21
	v_med3_f32 v0, v0, s74, v101
	v_med3_f32 v4, v4, s74, v101
	v_cvt_pk_fp8_f32 v69, v0, v4
	v_mul_f32_e32 v8, 0x42800000, v61
	v_mul_f32_e32 v0, 0x42800000, v45
	v_med3_f32 v4, v8, s74, v101
	v_med3_f32 v0, v0, s74, v101
	v_cvt_pk_fp8_f32 v69, v4, v0 op_sel:[0,0,1]
	v_mul_f32_e32 v0, 0x42800000, v25
	v_mul_f32_e32 v4, 0x42800000, v49
	v_med3_f32 v0, v0, s74, v101
	v_med3_f32 v4, v4, s74, v101
	v_cvt_pk_fp8_f32 v70, v0, v4
	v_mul_f32_e32 v8, 0x42800000, v53
	v_mul_f32_e32 v0, 0x42800000, v37
	v_med3_f32 v4, v8, s74, v101
	v_med3_f32 v0, v0, s74, v101
	v_cvt_pk_fp8_f32 v70, v4, v0 op_sel:[0,0,1]
	v_mul_f32_e32 v0, 0x42800000, v5
	v_mul_f32_e32 v4, 0x42800000, v9
	v_med3_f32 v0, v0, s74, v101
	v_med3_f32 v4, v4, s74, v101
	v_cvt_pk_fp8_f32 v71, v0, v4
	v_mul_f32_e32 v5, 0x42800000, v41
	v_mul_f32_e32 v0, 0x42800000, v1
	v_med3_f32 v1, v5, s74, v101
	v_med3_f32 v0, v0, s74, v101
	v_cvt_pk_fp8_f32 v71, v1, v0 op_sel:[0,0,1]
	v_mul_f32_e32 v0, 0x42800000, v30
	v_mul_f32_e32 v1, 0x42800000, v34
	v_med3_f32 v0, v0, s74, v101
	v_med3_f32 v1, v1, s74, v101
	v_cvt_pk_fp8_f32 v72, v0, v1
	v_mul_f32_e32 v4, 0x42800000, v58
	v_mul_f32_e32 v0, 0x42800000, v66
	v_med3_f32 v1, v4, s74, v101
	v_med3_f32 v0, v0, s74, v101
	v_cvt_pk_fp8_f32 v72, v1, v0 op_sel:[0,0,1]
	v_mul_f32_e32 v0, 0x42800000, v18
	v_mul_f32_e32 v1, 0x42800000, v22
	v_med3_f32 v0, v0, s74, v101
	v_med3_f32 v1, v1, s74, v101
	v_cvt_pk_fp8_f32 v73, v0, v1
	v_mul_f32_e32 v4, 0x42800000, v62
	v_mul_f32_e32 v0, 0x42800000, v46
	v_med3_f32 v1, v4, s74, v101
	v_med3_f32 v0, v0, s74, v101
	v_cvt_pk_fp8_f32 v73, v1, v0 op_sel:[0,0,1]
	v_mul_f32_e32 v0, 0x42800000, v26
	v_mul_f32_e32 v1, 0x42800000, v50
	v_med3_f32 v0, v0, s74, v101
	v_med3_f32 v1, v1, s74, v101
	v_cvt_pk_fp8_f32 v74, v0, v1
	v_mul_f32_e32 v4, 0x42800000, v54
	v_mul_f32_e32 v0, 0x42800000, v38
	v_med3_f32 v1, v4, s74, v101
	v_med3_f32 v0, v0, s74, v101
	v_cvt_pk_fp8_f32 v74, v1, v0 op_sel:[0,0,1]
	v_mul_f32_e32 v0, 0x42800000, v6
	v_mul_f32_e32 v1, 0x42800000, v10
	v_med3_f32 v0, v0, s74, v101
	v_med3_f32 v1, v1, s74, v101
	v_cvt_pk_fp8_f32 v75, v0, v1
	v_mul_f32_e32 v4, 0x42800000, v42
	v_mul_f32_e32 v0, 0x42800000, v2
	v_med3_f32 v1, v4, s74, v101
	v_med3_f32 v0, v0, s74, v101
	v_cvt_pk_fp8_f32 v75, v1, v0 op_sel:[0,0,1]
	v_mul_f32_e32 v0, 0x42800000, v31
	v_mul_f32_e32 v1, 0x42800000, v35
	v_med3_f32 v0, v0, s74, v101
	v_med3_f32 v1, v1, s74, v101
	v_mov_b32_e32 v4, v79
	v_cvt_pk_fp8_f32 v4, v0, v1
	v_mul_f32_e32 v2, 0x42800000, v59
	v_mul_f32_e32 v0, 0x42800000, v67
	v_med3_f32 v1, v2, s74, v101
	v_med3_f32 v0, v0, s74, v101
	v_cvt_pk_fp8_f32 v4, v1, v0 op_sel:[0,0,1]
	v_mul_f32_e32 v0, 0x42800000, v19
	v_mul_f32_e32 v1, 0x42800000, v23
	v_med3_f32 v0, v0, s74, v101
	v_med3_f32 v1, v1, s74, v101
	v_mov_b32_e32 v5, v79
	v_cvt_pk_fp8_f32 v5, v0, v1
	v_mul_f32_e32 v2, 0x42800000, v63
	v_mul_f32_e32 v0, 0x42800000, v47
	v_med3_f32 v1, v2, s74, v101
	v_med3_f32 v0, v0, s74, v101
	v_cvt_pk_fp8_f32 v5, v1, v0 op_sel:[0,0,1]
	v_mul_f32_e32 v0, 0x42800000, v27
	v_mul_f32_e32 v1, 0x42800000, v51
	v_med3_f32 v0, v0, s74, v101
	v_med3_f32 v1, v1, s74, v101
	v_mov_b32_e32 v6, v79
	v_cvt_pk_fp8_f32 v6, v0, v1
	v_mul_f32_e32 v2, 0x42800000, v55
	v_mul_f32_e32 v0, 0x42800000, v39
	v_med3_f32 v1, v2, s74, v101
	v_med3_f32 v0, v0, s74, v101
	v_cvt_pk_fp8_f32 v6, v1, v0 op_sel:[0,0,1]
	v_mul_f32_e32 v0, 0x42800000, v7
	v_mul_f32_e32 v1, 0x42800000, v11
	v_med3_f32 v0, v0, s74, v101
	v_med3_f32 v1, v1, s74, v101
	v_mov_b32_e32 v7, v79
	v_cvt_pk_fp8_f32 v7, v0, v1
	v_mul_f32_e32 v2, 0x42800000, v43
	v_mul_f32_e32 v0, 0x42800000, v3
	v_med3_f32 v1, v2, s74, v101
	v_med3_f32 v0, v0, s74, v101
	v_cvt_pk_fp8_f32 v7, v1, v0 op_sel:[0,0,1]
	ds_write_b128 v98, v[12:15] offset:40960
	ds_write_b128 v98, v[68:71] offset:41040
	ds_write_b128 v98, v[72:75] offset:41120
	ds_write_b128 v98, v[4:7] offset:41200
	s_waitcnt lgkmcnt(0)
	ds_read_b128 v[0:3], v99 offset:40960
	v_or_b32_e32 v4, s0, v87
	v_lshl_add_u64 v[8:9], s[8:9], 0, v[80:81]
	v_lshlrev_b32_e32 v4, 11, v4
	v_mov_b32_e32 v5, v79
	v_lshl_add_u64 v[10:11], v[8:9], 0, v[4:5]
	ds_read_b128 v[4:7], v99 offset:42240
	s_waitcnt lgkmcnt(1)
	global_store_dwordx4 v[10:11], v[0:3], off sc1
	s_nop 1
	v_or_b32_e32 v0, s0, v77
	v_lshlrev_b32_e32 v0, 11, v0
	v_mov_b32_e32 v1, v79
	v_lshl_add_u64 v[0:1], v[8:9], 0, v[0:1]
	s_waitcnt lgkmcnt(0)
	global_store_dwordx4 v[0:1], v[4:7], off sc1
	ds_read_b128 v[0:3], v99 offset:43520
	s_nop 0
	v_or_b32_e32 v4, s0, v88
	v_lshlrev_b32_e32 v4, 11, v4
	v_mov_b32_e32 v5, v79
	v_lshl_add_u64 v[10:11], v[8:9], 0, v[4:5]
	ds_read_b128 v[4:7], v99 offset:44800
	s_waitcnt lgkmcnt(1)
	global_store_dwordx4 v[10:11], v[0:3], off sc1
	s_nop 1
	v_or_b32_e32 v0, s0, v89
	v_lshlrev_b32_e32 v0, 11, v0
	v_mov_b32_e32 v1, v79
	v_lshl_add_u64 v[0:1], v[8:9], 0, v[0:1]
	s_waitcnt lgkmcnt(0)
	global_store_dwordx4 v[0:1], v[4:7], off sc1
	s_waitcnt lgkmcnt(0)

.LBB0_2371:
	s_cmpk_gt_i32 s53, 0x93
	s_cbranch_scc1 .LBB0_2373
	s_lshl_b32 s30, s3, 6
	s_mul_i32 s31, s2, 0x1280000
	v_or_b32_e32 v0, s30, v76
	s_mul_hi_i32 s23, s2, 0x1280000
	s_add_u32 s31, s59, s31
	v_mul_hi_i32_i24_e32 v1, 0x9500, v0
	v_mul_i32_i24_e32 v0, 0x9500, v0
	s_addc_u32 s38, s60, s23
	v_lshl_add_u64 v[0:1], s[4:5], 0, v[0:1]
	s_ashr_i32 s23, s22, 31
	v_lshl_add_u64 v[0:1], s[22:23], 2, v[0:1]
	v_mov_b32_e32 v83, v79
	v_lshl_add_u64 v[56:57], v[0:1], 0, v[82:83]
	v_add_co_u32_e32 v4, vcc, s84, v56
	global_load_dwordx4 v[0:3], v[56:57], off nt
	s_nop 0
	v_addc_co_u32_e32 v5, vcc, 0, v57, vcc
	global_load_dwordx4 v[16:19], v[4:5], off offset:1280 nt
	v_add_co_u32_e32 v4, vcc, s73, v56
	v_mov_b32_e32 v64, v79
	s_nop 0
	v_addc_co_u32_e32 v5, vcc, 0, v57, vcc
	global_load_dwordx4 v[20:23], v[4:5], off offset:2560 nt
	v_add_co_u32_e32 v4, vcc, s85, v56
	v_mov_b32_e32 v65, v79
	s_nop 0
	v_addc_co_u32_e32 v5, vcc, 0, v57, vcc
	global_load_dwordx4 v[44:47], v[4:5], off offset:3840 nt
	v_add_co_u32_e32 v4, vcc, s86, v56
	v_mov_b32_e32 v66, v79
	s_nop 0
	v_addc_co_u32_e32 v5, vcc, 0, v57, vcc
	v_add_co_u32_e32 v8, vcc, s87, v56
	global_load_dwordx4 v[4:7], v[4:5], off offset:1024 nt
	s_nop 0
	v_addc_co_u32_e32 v9, vcc, 0, v57, vcc
	global_load_dwordx4 v[24:27], v[8:9], off offset:2304 nt
	v_add_co_u32_e32 v8, vcc, s88, v56
	v_mov_b32_e32 v67, v79
	s_nop 0
	v_addc_co_u32_e32 v9, vcc, 0, v57, vcc
	global_load_dwordx4 v[28:31], v[8:9], off offset:3584 nt
	v_add_co_u32_e32 v8, vcc, s89, v56
	s_ashr_i32 s23, s30, 31
	s_nop 0
	v_addc_co_u32_e32 v9, vcc, 0, v57, vcc
	global_load_dwordx4 v[52:55], v[8:9], off offset:768 nt
	v_add_co_u32_e32 v8, vcc, s90, v56
	s_add_u32 s30, s31, s30
	s_nop 0
	v_addc_co_u32_e32 v9, vcc, 0, v57, vcc
	v_add_co_u32_e32 v12, vcc, s91, v56
	global_load_dwordx4 v[8:11], v[8:9], off offset:2048 nt
	s_nop 0
	v_addc_co_u32_e32 v13, vcc, 0, v57, vcc
	global_load_dwordx4 v[32:35], v[12:13], off offset:3328 nt
	v_add_co_u32_e32 v12, vcc, s92, v56
	s_addc_u32 s31, s38, s23
	s_nop 0
	v_addc_co_u32_e32 v13, vcc, 0, v57, vcc
	global_load_dwordx4 v[36:39], v[12:13], off offset:512 nt
	v_add_co_u32_e32 v12, vcc, s93, v56
	s_mov_b64 s[38:39], 0
	s_nop 0
	v_addc_co_u32_e32 v13, vcc, 0, v57, vcc
	global_load_dwordx4 v[60:63], v[12:13], off offset:1792 nt
	v_add_co_u32_e32 v12, vcc, s94, v56
	s_waitcnt vmcnt(11)
	v_mul_f32_e32 v0, 0x42800000, v0
	v_addc_co_u32_e32 v13, vcc, 0, v57, vcc
	v_add_co_u32_e32 v40, vcc, s95, v56
	global_load_dwordx4 v[12:15], v[12:13], off offset:3072 nt
	s_nop 0
	v_addc_co_u32_e32 v41, vcc, 0, v57, vcc
	global_load_dwordx4 v[40:43], v[40:41], off offset:256 nt
	v_add_co_u32_e32 v48, vcc, s96, v56
	s_waitcnt vmcnt(12)
	v_mul_f32_e32 v16, 0x42800000, v16
	v_addc_co_u32_e32 v49, vcc, 0, v57, vcc
	v_add_co_u32_e32 v56, vcc, s97, v56
	global_load_dwordx4 v[48:51], v[48:49], off offset:1536 nt
	s_nop 0
	v_addc_co_u32_e32 v57, vcc, 0, v57, vcc
	global_load_dwordx4 v[56:59], v[56:57], off offset:2816 nt
	v_med3_f32 v0, v0, s74, v101
	v_med3_f32 v16, v16, s74, v101
	v_cvt_pk_fp8_f32 v64, v0, v16
	s_waitcnt vmcnt(11)
	v_mul_f32_e32 v0, 0x42800000, v4
	v_med3_f32 v0, v0, s74, v101
	v_mul_f32_e32 v20, 0x42800000, v20
	s_waitcnt vmcnt(10)
	v_mul_f32_e32 v4, 0x42800000, v24
	v_med3_f32 v4, v4, s74, v101
	v_mul_f32_e32 v44, 0x42800000, v44
	v_cvt_pk_fp8_f32 v65, v0, v4
	v_med3_f32 v20, v20, s74, v101
	v_med3_f32 v44, v44, s74, v101
	v_cvt_pk_fp8_f32 v64, v20, v44 op_sel:[0,0,1]
	s_waitcnt vmcnt(9)
	v_mul_f32_e32 v16, 0x42800000, v28
	v_med3_f32 v16, v16, s74, v101
	s_waitcnt vmcnt(8)
	v_mul_f32_e32 v20, 0x42800000, v52
	v_med3_f32 v20, v20, s74, v101
	v_cvt_pk_fp8_f32 v65, v16, v20 op_sel:[0,0,1]
	s_waitcnt vmcnt(7)
	v_mul_f32_e32 v0, 0x42800000, v8
	v_med3_f32 v0, v0, s74, v101
	s_waitcnt vmcnt(6)
	v_mul_f32_e32 v4, 0x42800000, v32
	v_med3_f32 v4, v4, s74, v101
	v_cvt_pk_fp8_f32 v66, v0, v4
	s_waitcnt vmcnt(5)
	v_mul_f32_e32 v8, 0x42800000, v36
	v_med3_f32 v8, v8, s74, v101
	s_waitcnt vmcnt(4)
	v_mul_f32_e32 v16, 0x42800000, v60
	v_med3_f32 v16, v16, s74, v101
	v_cvt_pk_fp8_f32 v66, v8, v16 op_sel:[0,0,1]
	s_waitcnt vmcnt(3)
	v_mul_f32_e32 v0, 0x42800000, v12
	v_med3_f32 v0, v0, s74, v101
	s_waitcnt vmcnt(2)
	v_mul_f32_e32 v4, 0x42800000, v40
	v_med3_f32 v4, v4, s74, v101
	v_cvt_pk_fp8_f32 v67, v0, v4
	v_mul_f32_e32 v0, 0x42800000, v1
	v_mul_f32_e32 v1, 0x42800000, v17
	v_med3_f32 v0, v0, s74, v101
	v_med3_f32 v1, v1, s74, v101
	v_mul_f32_e32 v4, 0x42800000, v21
	s_waitcnt vmcnt(1)
	v_mul_f32_e32 v8, 0x42800000, v48
	v_med3_f32 v8, v8, s74, v101
	v_med3_f32 v4, v4, s74, v101
	s_waitcnt vmcnt(0)
	v_mul_f32_e32 v12, 0x42800000, v56
	v_med3_f32 v12, v12, s74, v101
	v_cvt_pk_fp8_f32 v67, v8, v12 op_sel:[0,0,1]
	v_mul_f32_e32 v8, 0x42800000, v45
	v_med3_f32 v8, v8, s74, v101
	ds_write_b128 v98, v[64:67] offset:40960
	v_mov_b32_e32 v64, v79
	v_cvt_pk_fp8_f32 v64, v0, v1
	v_mul_f32_e32 v0, 0x42800000, v5
	v_mul_f32_e32 v1, 0x42800000, v25
	v_med3_f32 v0, v0, s74, v101
	v_med3_f32 v1, v1, s74, v101
	v_mov_b32_e32 v65, v79
	v_cvt_pk_fp8_f32 v65, v0, v1
	v_mul_f32_e32 v0, 0x42800000, v9
	v_mul_f32_e32 v1, 0x42800000, v33
	v_med3_f32 v0, v0, s74, v101
	v_med3_f32 v1, v1, s74, v101
	v_mov_b32_e32 v66, v79
	v_cvt_pk_fp8_f32 v64, v4, v8 op_sel:[0,0,1]
	v_mul_f32_e32 v4, 0x42800000, v29
	v_mul_f32_e32 v5, 0x42800000, v53
	v_cvt_pk_fp8_f32 v66, v0, v1
	v_mul_f32_e32 v0, 0x42800000, v13
	v_mul_f32_e32 v1, 0x42800000, v41
	v_med3_f32 v4, v4, s74, v101
	v_med3_f32 v5, v5, s74, v101
	v_med3_f32 v0, v0, s74, v101
	v_med3_f32 v1, v1, s74, v101
	v_mov_b32_e32 v67, v79
	v_cvt_pk_fp8_f32 v65, v4, v5 op_sel:[0,0,1]
	v_mul_f32_e32 v4, 0x42800000, v37
	v_mul_f32_e32 v5, 0x42800000, v61
	v_cvt_pk_fp8_f32 v67, v0, v1
	v_med3_f32 v4, v4, s74, v101
	v_med3_f32 v5, v5, s74, v101
	v_cvt_pk_fp8_f32 v66, v4, v5 op_sel:[0,0,1]
	v_mul_f32_e32 v4, 0x42800000, v49
	v_mul_f32_e32 v5, 0x42800000, v57
	v_med3_f32 v4, v4, s74, v101
	v_med3_f32 v5, v5, s74, v101
	v_cvt_pk_fp8_f32 v67, v4, v5 op_sel:[0,0,1]
	v_mul_f32_e32 v0, 0x42800000, v2
	v_mul_f32_e32 v1, 0x42800000, v18
	v_med3_f32 v0, v0, s74, v101
	ds_write_b128 v98, v[64:67] offset:41040
	v_med3_f32 v1, v1, s74, v101
	v_mov_b32_e32 v64, v79
	v_cvt_pk_fp8_f32 v64, v0, v1
	v_mul_f32_e32 v0, 0x42800000, v6
	v_mul_f32_e32 v1, 0x42800000, v26
	v_med3_f32 v0, v0, s74, v101
	v_med3_f32 v1, v1, s74, v101
	v_mov_b32_e32 v65, v79
	v_mul_f32_e32 v2, 0x42800000, v22
	v_mul_f32_e32 v4, 0x42800000, v46
	v_cvt_pk_fp8_f32 v65, v0, v1
	v_mul_f32_e32 v0, 0x42800000, v10
	v_mul_f32_e32 v1, 0x42800000, v34
	v_med3_f32 v2, v2, s74, v101
	v_med3_f32 v4, v4, s74, v101
	v_med3_f32 v0, v0, s74, v101
	v_med3_f32 v1, v1, s74, v101
	v_mov_b32_e32 v66, v79
	v_cvt_pk_fp8_f32 v64, v2, v4 op_sel:[0,0,1]
	v_mul_f32_e32 v2, 0x42800000, v30
	v_mul_f32_e32 v4, 0x42800000, v54
	v_cvt_pk_fp8_f32 v66, v0, v1
	v_mul_f32_e32 v0, 0x42800000, v14
	v_mul_f32_e32 v1, 0x42800000, v42
	v_med3_f32 v2, v2, s74, v101
	v_med3_f32 v4, v4, s74, v101
	v_med3_f32 v0, v0, s74, v101
	v_med3_f32 v1, v1, s74, v101
	v_mov_b32_e32 v67, v79
	v_cvt_pk_fp8_f32 v65, v2, v4 op_sel:[0,0,1]
	v_mul_f32_e32 v2, 0x42800000, v38
	v_mul_f32_e32 v4, 0x42800000, v62
	v_cvt_pk_fp8_f32 v67, v0, v1
	v_med3_f32 v2, v2, s74, v101
	v_med3_f32 v4, v4, s74, v101
	v_cvt_pk_fp8_f32 v66, v2, v4 op_sel:[0,0,1]
	v_mul_f32_e32 v2, 0x42800000, v50
	v_mul_f32_e32 v4, 0x42800000, v58
	v_med3_f32 v2, v2, s74, v101
	v_med3_f32 v4, v4, s74, v101
	v_mul_f32_e32 v0, 0x42800000, v3
	v_mul_f32_e32 v1, 0x42800000, v19
	v_cvt_pk_fp8_f32 v67, v2, v4 op_sel:[0,0,1]
	v_med3_f32 v4, v0, s74, v101
	v_med3_f32 v1, v1, s74, v101
	v_mov_b32_e32 v0, v79
	v_cvt_pk_fp8_f32 v0, v4, v1
	v_mul_f32_e32 v2, 0x42800000, v23
	v_mul_f32_e32 v3, 0x42800000, v47
	v_med3_f32 v2, v2, s74, v101
	v_med3_f32 v3, v3, s74, v101
	v_cvt_pk_fp8_f32 v0, v2, v3 op_sel:[0,0,1]
	v_mul_f32_e32 v1, 0x42800000, v7
	v_mul_f32_e32 v2, 0x42800000, v27
	v_med3_f32 v5, v1, s74, v101
	v_med3_f32 v2, v2, s74, v101
	v_mov_b32_e32 v1, v79
	v_cvt_pk_fp8_f32 v1, v5, v2
	v_mul_f32_e32 v3, 0x42800000, v31
	v_mul_f32_e32 v4, 0x42800000, v55
	v_med3_f32 v3, v3, s74, v101
	v_med3_f32 v4, v4, s74, v101
	v_cvt_pk_fp8_f32 v1, v3, v4 op_sel:[0,0,1]
	v_mul_f32_e32 v2, 0x42800000, v11
	v_mul_f32_e32 v3, 0x42800000, v35
	v_med3_f32 v6, v2, s74, v101
	v_med3_f32 v3, v3, s74, v101
	v_mov_b32_e32 v2, v79
	v_cvt_pk_fp8_f32 v2, v6, v3
	v_mul_f32_e32 v4, 0x42800000, v39
	v_mul_f32_e32 v5, 0x42800000, v63
	v_med3_f32 v4, v4, s74, v101
	v_med3_f32 v5, v5, s74, v101
	v_cvt_pk_fp8_f32 v2, v4, v5 op_sel:[0,0,1]
	v_mul_f32_e32 v3, 0x42800000, v15
	v_mul_f32_e32 v4, 0x42800000, v43
	v_med3_f32 v7, v3, s74, v101
	v_med3_f32 v4, v4, s74, v101
	v_mov_b32_e32 v3, v79
	v_cvt_pk_fp8_f32 v3, v7, v4
	v_mul_f32_e32 v5, 0x42800000, v51
	v_mul_f32_e32 v6, 0x42800000, v59
	v_med3_f32 v5, v5, s74, v101
	v_med3_f32 v6, v6, s74, v101
	v_cvt_pk_fp8_f32 v3, v5, v6 op_sel:[0,0,1]
	ds_write_b128 v98, v[64:67] offset:41120
	v_or_b32_e32 v6, s17, v87
	v_ashrrev_i32_e32 v7, 31, v6
	ds_write_b128 v98, v[0:3] offset:41200
	s_waitcnt lgkmcnt(0)
	ds_read_b128 v[0:3], v99 offset:40960
	v_lshl_add_u64 v[4:5], s[30:31], 0, v[80:81]
	v_lshlrev_b64 v[6:7], 11, v[6:7]
	v_lshl_add_u64 v[6:7], v[4:5], 0, v[6:7]
	s_waitcnt lgkmcnt(0)
	global_store_dwordx4 v[6:7], v[0:3], off sc1
	ds_read_b128 v[0:3], v99 offset:42240
	v_or_b32_e32 v6, s17, v77
	v_ashrrev_i32_e32 v7, 31, v6
	v_lshlrev_b64 v[6:7], 11, v[6:7]
	v_lshl_add_u64 v[6:7], v[4:5], 0, v[6:7]
	s_waitcnt lgkmcnt(0)
	global_store_dwordx4 v[6:7], v[0:3], off sc1
	ds_read_b128 v[0:3], v99 offset:43520
	v_or_b32_e32 v6, s17, v88
	v_ashrrev_i32_e32 v7, 31, v6
	v_lshlrev_b64 v[6:7], 11, v[6:7]
	v_lshl_add_u64 v[6:7], v[4:5], 0, v[6:7]
	s_waitcnt lgkmcnt(0)
	global_store_dwordx4 v[6:7], v[0:3], off sc1
	ds_read_b128 v[0:3], v99 offset:44800
	v_or_b32_e32 v6, s17, v89
	v_ashrrev_i32_e32 v7, 31, v6
	v_lshlrev_b64 v[6:7], 11, v[6:7]
	v_lshl_add_u64 v[4:5], v[4:5], 0, v[6:7]
	s_waitcnt lgkmcnt(0)
	global_store_dwordx4 v[4:5], v[0:3], off sc1
	s_waitcnt lgkmcnt(0)
.LBB0_2373:
	s_and_b64 vcc, exec, s[38:39]
	s_cbranch_vccz .LBB0_2335
	s_xor_b64 s[38:39], s[24:25], -1
	s_lshl_b32 s24, s3, 6
	s_mov_b64 s[30:31], -1
	s_and_b64 vcc, exec, s[38:39]
	s_cbranch_vccz .LBB0_2404
	s_andn2_b64 vcc, exec, s[28:29]
	s_cbranch_vccnz .LBB0_2378
	s_ashr_i32 s3, s2, 31
	s_lshl_b64 s[28:29], s[2:3], 22
	v_or_b32_e32 v0, s24, v76
	s_add_u32 s3, s61, s28
	v_mul_hi_i32_i24_e32 v1, s18, v0
	v_mul_i32_i24_e32 v0, s18, v0
	s_addc_u32 s25, s65, s29
	v_lshl_add_u64 v[0:1], v[0:1], 2, s[4:5]
	s_ashr_i32 s23, s22, 31
	v_lshl_add_u64 v[0:1], s[22:23], 2, v[0:1]
	v_mov_b32_e32 v83, v79
	v_lshl_add_u64 v[0:1], v[0:1], 0, v[82:83]
	s_lshl_b64 s[28:29], s[18:19], 2
	global_load_dwordx4 v[56:59], v[0:1], off nt
	v_lshl_add_u64 v[0:1], v[0:1], 0, s[28:29]
	global_load_dwordx4 v[60:63], v[0:1], off nt
	v_lshl_add_u64 v[0:1], v[0:1], 0, s[28:29]
	global_load_dwordx4 v[64:67], v[0:1], off nt
	v_lshl_add_u64 v[0:1], v[0:1], 0, s[28:29]
	global_load_dwordx4 v[52:55], v[0:1], off nt
	v_lshl_add_u64 v[0:1], v[0:1], 0, s[28:29]
	global_load_dwordx4 v[40:43], v[0:1], off nt
	v_lshl_add_u64 v[0:1], v[0:1], 0, s[28:29]
	global_load_dwordx4 v[44:47], v[0:1], off nt
	v_lshl_add_u64 v[0:1], v[0:1], 0, s[28:29]
	global_load_dwordx4 v[48:51], v[0:1], off nt
	v_lshl_add_u64 v[0:1], v[0:1], 0, s[28:29]
	global_load_dwordx4 v[36:39], v[0:1], off nt
	v_lshl_add_u64 v[0:1], v[0:1], 0, s[28:29]
	global_load_dwordx4 v[24:27], v[0:1], off nt
	v_lshl_add_u64 v[0:1], v[0:1], 0, s[28:29]
	global_load_dwordx4 v[28:31], v[0:1], off nt
	v_lshl_add_u64 v[0:1], v[0:1], 0, s[28:29]
	global_load_dwordx4 v[32:35], v[0:1], off nt
	v_lshl_add_u64 v[0:1], v[0:1], 0, s[28:29]
	global_load_dwordx4 v[20:23], v[0:1], off nt
	v_lshl_add_u64 v[0:1], v[0:1], 0, s[28:29]
	global_load_dwordx4 v[4:7], v[0:1], off nt
	v_lshl_add_u64 v[0:1], v[0:1], 0, s[28:29]
	global_load_dwordx4 v[8:11], v[0:1], off nt
	v_lshl_add_u64 v[0:1], v[0:1], 0, s[28:29]
	global_load_dwordx4 v[12:15], v[0:1], off nt
	v_lshl_add_u64 v[0:1], v[0:1], 0, s[28:29]
	global_load_dwordx4 v[0:3], v[0:1], off nt
	v_mov_b32_e32 v19, v79
	v_mov_b32_e32 v69, v79
	v_mov_b32_e32 v70, v79
	v_mov_b32_e32 v71, v79
	v_mov_b32_e32 v72, v79
	v_mov_b32_e32 v73, v79
	v_mov_b32_e32 v74, v79
	v_mov_b32_e32 v75, v79
	v_mov_b32_e32 v16, v79
	v_mov_b32_e32 v17, v79
	v_mov_b32_e32 v18, v79
	v_mov_b32_e32 v68, v79
	s_ashr_i32 s23, s24, 31
	s_add_u32 s28, s3, s24
	s_addc_u32 s29, s25, s23
	s_cmpk_lt_u32 s68, 0xf97f
	s_waitcnt vmcnt(15)
	v_mul_f32_e32 v56, 0x42800000, v56
	v_mul_f32_e32 v57, 0x42800000, v57
	s_waitcnt vmcnt(14)
	v_mul_f32_e32 v60, 0x42800000, v60
	v_med3_f32 v56, v56, s74, v101
	v_mul_f32_e32 v61, 0x42800000, v61
	v_med3_f32 v60, v60, s74, v101
	v_med3_f32 v57, v57, s74, v101
	v_med3_f32 v61, v61, s74, v101
	s_waitcnt vmcnt(11)
	v_mul_f32_e32 v41, 0x42800000, v41
	v_med3_f32 v41, v41, s74, v101
	s_waitcnt vmcnt(10)
	v_mul_f32_e32 v45, 0x42800000, v45
	v_med3_f32 v45, v45, s74, v101
	v_cvt_pk_fp8_f32 v69, v41, v45
	s_waitcnt vmcnt(9)
	v_mul_f32_e32 v49, 0x42800000, v49
	v_mul_f32_e32 v40, 0x42800000, v40
	v_mul_f32_e32 v44, 0x42800000, v44
	s_waitcnt vmcnt(7)
	v_mul_f32_e32 v24, 0x42800000, v24
	v_med3_f32 v40, v40, s74, v101
	s_waitcnt vmcnt(6)
	v_mul_f32_e32 v28, 0x42800000, v28
	v_med3_f32 v44, v44, s74, v101
	v_med3_f32 v24, v24, s74, v101
	v_med3_f32 v28, v28, s74, v101
	v_cvt_pk_fp8_f32 v16, v56, v60
	v_cvt_pk_fp8_f32 v17, v40, v44
	s_waitcnt vmcnt(3)
	v_mul_f32_e32 v4, 0x42800000, v4
	v_med3_f32 v4, v4, s74, v101
	s_waitcnt vmcnt(2)
	v_mul_f32_e32 v8, 0x42800000, v8
	v_med3_f32 v8, v8, s74, v101
	v_cvt_pk_fp8_f32 v19, v4, v8
	s_waitcnt vmcnt(1)
	v_mul_f32_e32 v12, 0x42800000, v12
	s_waitcnt vmcnt(0)
	v_mul_f32_e32 v0, 0x42800000, v0
	v_med3_f32 v4, v12, s74, v101
	v_med3_f32 v0, v0, s74, v101
	v_cvt_pk_fp8_f32 v19, v4, v0 op_sel:[0,0,1]
	v_mul_f32_e32 v0, 0x42800000, v37
	v_med3_f32 v4, v49, s74, v101
	v_med3_f32 v0, v0, s74, v101
	v_cvt_pk_fp8_f32 v69, v4, v0 op_sel:[0,0,1]
	v_mul_f32_e32 v0, 0x42800000, v25
	v_mul_f32_e32 v4, 0x42800000, v29
	v_med3_f32 v0, v0, s74, v101
	v_med3_f32 v4, v4, s74, v101
	v_cvt_pk_fp8_f32 v70, v0, v4
	v_mul_f32_e32 v8, 0x42800000, v33
	v_mul_f32_e32 v0, 0x42800000, v21
	v_med3_f32 v4, v8, s74, v101
	v_med3_f32 v0, v0, s74, v101
	v_cvt_pk_fp8_f32 v70, v4, v0 op_sel:[0,0,1]
	v_mul_f32_e32 v0, 0x42800000, v5
	v_mul_f32_e32 v4, 0x42800000, v9
	v_med3_f32 v0, v0, s74, v101
	v_med3_f32 v4, v4, s74, v101
	v_cvt_pk_fp8_f32 v71, v0, v4
	v_mul_f32_e32 v5, 0x42800000, v13
	v_mul_f32_e32 v0, 0x42800000, v1
	v_med3_f32 v1, v5, s74, v101
	v_med3_f32 v0, v0, s74, v101
	v_cvt_pk_fp8_f32 v71, v1, v0 op_sel:[0,0,1]
	v_mul_f32_e32 v0, 0x42800000, v58
	v_mul_f32_e32 v1, 0x42800000, v62
	v_med3_f32 v0, v0, s74, v101
	v_med3_f32 v1, v1, s74, v101
	v_cvt_pk_fp8_f32 v72, v0, v1
	v_mul_f32_e32 v4, 0x42800000, v66
	v_mul_f32_e32 v0, 0x42800000, v54
	v_med3_f32 v1, v4, s74, v101
	v_med3_f32 v0, v0, s74, v101
	v_cvt_pk_fp8_f32 v72, v1, v0 op_sel:[0,0,1]
	v_mul_f32_e32 v0, 0x42800000, v42
	v_mul_f32_e32 v1, 0x42800000, v46
	v_med3_f32 v0, v0, s74, v101
	v_med3_f32 v1, v1, s74, v101
	v_cvt_pk_fp8_f32 v73, v0, v1
	v_mul_f32_e32 v4, 0x42800000, v50
	v_mul_f32_e32 v0, 0x42800000, v38
	v_med3_f32 v1, v4, s74, v101
	v_med3_f32 v0, v0, s74, v101
	v_cvt_pk_fp8_f32 v73, v1, v0 op_sel:[0,0,1]
	v_mul_f32_e32 v0, 0x42800000, v26
	v_mul_f32_e32 v1, 0x42800000, v30
	v_med3_f32 v0, v0, s74, v101
	v_med3_f32 v1, v1, s74, v101
	v_cvt_pk_fp8_f32 v74, v0, v1
	v_mul_f32_e32 v4, 0x42800000, v34
	v_mul_f32_e32 v0, 0x42800000, v22
	v_med3_f32 v1, v4, s74, v101
	v_med3_f32 v0, v0, s74, v101
	v_cvt_pk_fp8_f32 v74, v1, v0 op_sel:[0,0,1]
	v_mul_f32_e32 v0, 0x42800000, v6
	v_mul_f32_e32 v1, 0x42800000, v10
	v_med3_f32 v0, v0, s74, v101
	v_med3_f32 v1, v1, s74, v101
	v_cvt_pk_fp8_f32 v75, v0, v1
	v_mul_f32_e32 v4, 0x42800000, v14
	v_mul_f32_e32 v0, 0x42800000, v2
	v_med3_f32 v1, v4, s74, v101
	v_med3_f32 v0, v0, s74, v101
	v_cvt_pk_fp8_f32 v75, v1, v0 op_sel:[0,0,1]
	v_mul_f32_e32 v0, 0x42800000, v59
	v_mul_f32_e32 v1, 0x42800000, v63
	v_med3_f32 v0, v0, s74, v101
	v_med3_f32 v1, v1, s74, v101
	v_mov_b32_e32 v4, v79
	v_cvt_pk_fp8_f32 v4, v0, v1
	v_mul_f32_e32 v2, 0x42800000, v67
	v_mul_f32_e32 v0, 0x42800000, v55
	v_med3_f32 v1, v2, s74, v101
	v_med3_f32 v0, v0, s74, v101
	v_cvt_pk_fp8_f32 v4, v1, v0 op_sel:[0,0,1]
	v_mul_f32_e32 v0, 0x42800000, v43
	v_mul_f32_e32 v1, 0x42800000, v47
	v_med3_f32 v0, v0, s74, v101
	v_med3_f32 v1, v1, s74, v101
	v_mov_b32_e32 v5, v79
	v_cvt_pk_fp8_f32 v5, v0, v1
	v_mul_f32_e32 v2, 0x42800000, v51
	v_mul_f32_e32 v0, 0x42800000, v39
	v_med3_f32 v1, v2, s74, v101
	v_med3_f32 v0, v0, s74, v101
	v_cvt_pk_fp8_f32 v5, v1, v0 op_sel:[0,0,1]
	v_mul_f32_e32 v0, 0x42800000, v27
	v_mul_f32_e32 v1, 0x42800000, v31
	v_med3_f32 v0, v0, s74, v101
	v_med3_f32 v1, v1, s74, v101
	v_mov_b32_e32 v6, v79
	v_cvt_pk_fp8_f32 v6, v0, v1
	v_mul_f32_e32 v2, 0x42800000, v35
	v_mul_f32_e32 v0, 0x42800000, v23
	v_cvt_pk_fp8_f32 v18, v24, v28
	v_med3_f32 v1, v2, s74, v101
	v_med3_f32 v0, v0, s74, v101
	v_cvt_pk_fp8_f32 v68, v57, v61
	v_cvt_pk_fp8_f32 v6, v1, v0 op_sel:[0,0,1]
	v_mul_f32_e32 v0, 0x42800000, v7
	v_mul_f32_e32 v1, 0x42800000, v11
	v_mul_f32_e32 v64, 0x42800000, v64
	v_mul_f32_e32 v52, 0x42800000, v52
	v_mul_f32_e32 v48, 0x42800000, v48
	v_mul_f32_e32 v36, 0x42800000, v36
	v_mul_f32_e32 v32, 0x42800000, v32
	v_mul_f32_e32 v20, 0x42800000, v20
	v_med3_f32 v0, v0, s74, v101
	v_med3_f32 v1, v1, s74, v101
	v_mov_b32_e32 v7, v79
	v_mul_f32_e32 v65, 0x42800000, v65
	v_med3_f32 v64, v64, s74, v101
	v_mul_f32_e32 v53, 0x42800000, v53
	v_med3_f32 v52, v52, s74, v101
	v_med3_f32 v48, v48, s74, v101
	v_med3_f32 v36, v36, s74, v101
	v_med3_f32 v32, v32, s74, v101
	v_med3_f32 v20, v20, s74, v101
	v_cvt_pk_fp8_f32 v7, v0, v1
	v_med3_f32 v56, v65, s74, v101
	v_med3_f32 v53, v53, s74, v101
	v_cvt_pk_fp8_f32 v16, v64, v52 op_sel:[0,0,1]
	v_cvt_pk_fp8_f32 v17, v48, v36 op_sel:[0,0,1]
	v_cvt_pk_fp8_f32 v18, v32, v20 op_sel:[0,0,1]
	v_cvt_pk_fp8_f32 v68, v56, v53 op_sel:[0,0,1]
	v_mul_f32_e32 v2, 0x42800000, v15
	v_mul_f32_e32 v0, 0x42800000, v3
	v_med3_f32 v1, v2, s74, v101
	v_med3_f32 v0, v0, s74, v101
	v_cvt_pk_fp8_f32 v7, v1, v0 op_sel:[0,0,1]
	ds_write_b128 v98, v[16:19] offset:40960
	ds_write_b128 v98, v[68:71] offset:41040
	ds_write_b128 v98, v[72:75] offset:41120
	ds_write_b128 v98, v[4:7] offset:41200
	s_waitcnt lgkmcnt(0)
	ds_read_b128 v[0:3], v99 offset:40960
	v_or_b32_e32 v4, s17, v87
	v_ashrrev_i32_e32 v5, 31, v4
	v_lshl_add_u64 v[8:9], s[28:29], 0, v[80:81]
	v_lshlrev_b64 v[4:5], 11, v[4:5]
	v_lshl_add_u64 v[10:11], v[8:9], 0, v[4:5]
	ds_read_b128 v[4:7], v99 offset:42240
	s_waitcnt lgkmcnt(1)
	global_store_dwordx4 v[10:11], v[0:3], off sc1
	s_cselect_b64 s[28:29], -1, 0
	s_nop 0
	v_or_b32_e32 v0, s17, v77
	v_ashrrev_i32_e32 v1, 31, v0
	v_lshlrev_b64 v[0:1], 11, v[0:1]
	v_lshl_add_u64 v[0:1], v[8:9], 0, v[0:1]
	s_waitcnt lgkmcnt(0)
	global_store_dwordx4 v[0:1], v[4:7], off sc1
	ds_read_b128 v[0:3], v99 offset:43520
	s_nop 0
	v_or_b32_e32 v4, s17, v88
	v_ashrrev_i32_e32 v5, 31, v4
	v_lshlrev_b64 v[4:5], 11, v[4:5]
	v_lshl_add_u64 v[10:11], v[8:9], 0, v[4:5]
	ds_read_b128 v[4:7], v99 offset:44800
	s_waitcnt lgkmcnt(1)
	global_store_dwordx4 v[10:11], v[0:3], off sc1
	s_nop 1
	v_or_b32_e32 v0, s17, v89
	v_ashrrev_i32_e32 v1, 31, v0
	v_lshlrev_b64 v[0:1], 11, v[0:1]
	v_lshl_add_u64 v[0:1], v[8:9], 0, v[0:1]
	s_waitcnt lgkmcnt(0)
	global_store_dwordx4 v[0:1], v[4:7], off sc1
	s_waitcnt lgkmcnt(0)
	s_andn2_b64 vcc, exec, s[28:29]
	s_cbranch_vccz .LBB0_2379
	s_branch .LBB0_2403

.LBB0_2379:
	s_andn2_b64 vcc, exec, s[26:27]
	s_cbranch_vccnz .LBB0_2381
	s_ashr_i32 s3, s2, 31
	s_lshl_b64 s[26:27], s[2:3], 22
	s_add_u32 s3, s66, s26
	s_addc_u32 s23, s67, s27
	v_or_b32_e32 v0, s24, v76
	s_add_u32 s3, s3, s20
	v_mul_hi_i32_i24_e32 v1, s18, v0
	v_mul_i32_i24_e32 v0, s18, v0
	s_addc_u32 s25, s23, s21
	v_lshl_add_u64 v[0:1], v[0:1], 2, s[4:5]
	s_ashr_i32 s23, s22, 31
	v_lshl_add_u64 v[0:1], s[22:23], 2, v[0:1]
	v_mov_b32_e32 v83, v79
	v_lshl_add_u64 v[0:1], v[0:1], 0, v[82:83]
	s_lshl_b64 s[26:27], s[18:19], 2
	global_load_dwordx4 v[56:59], v[0:1], off nt
	v_lshl_add_u64 v[0:1], v[0:1], 0, s[26:27]
	global_load_dwordx4 v[60:63], v[0:1], off nt
	v_lshl_add_u64 v[0:1], v[0:1], 0, s[26:27]
	global_load_dwordx4 v[64:67], v[0:1], off nt
	v_lshl_add_u64 v[0:1], v[0:1], 0, s[26:27]
	global_load_dwordx4 v[52:55], v[0:1], off nt
	v_lshl_add_u64 v[0:1], v[0:1], 0, s[26:27]
	global_load_dwordx4 v[40:43], v[0:1], off nt
	v_lshl_add_u64 v[0:1], v[0:1], 0, s[26:27]
	global_load_dwordx4 v[44:47], v[0:1], off nt
	v_lshl_add_u64 v[0:1], v[0:1], 0, s[26:27]
	global_load_dwordx4 v[48:51], v[0:1], off nt
	v_lshl_add_u64 v[0:1], v[0:1], 0, s[26:27]
	global_load_dwordx4 v[36:39], v[0:1], off nt
	v_lshl_add_u64 v[0:1], v[0:1], 0, s[26:27]
	global_load_dwordx4 v[24:27], v[0:1], off nt
	v_lshl_add_u64 v[0:1], v[0:1], 0, s[26:27]
	global_load_dwordx4 v[28:31], v[0:1], off nt
	v_lshl_add_u64 v[0:1], v[0:1], 0, s[26:27]
	global_load_dwordx4 v[32:35], v[0:1], off nt
	v_lshl_add_u64 v[0:1], v[0:1], 0, s[26:27]
	global_load_dwordx4 v[20:23], v[0:1], off nt
	v_lshl_add_u64 v[0:1], v[0:1], 0, s[26:27]
	global_load_dwordx4 v[4:7], v[0:1], off nt
	v_lshl_add_u64 v[0:1], v[0:1], 0, s[26:27]
	global_load_dwordx4 v[8:11], v[0:1], off nt
	v_lshl_add_u64 v[0:1], v[0:1], 0, s[26:27]
	global_load_dwordx4 v[12:15], v[0:1], off nt
	v_lshl_add_u64 v[0:1], v[0:1], 0, s[26:27]
	global_load_dwordx4 v[0:3], v[0:1], off nt
	v_mov_b32_e32 v19, v79
	v_mov_b32_e32 v69, v79
	v_mov_b32_e32 v70, v79
	v_mov_b32_e32 v71, v79
	v_mov_b32_e32 v72, v79
	v_mov_b32_e32 v73, v79
	v_mov_b32_e32 v74, v79
	v_mov_b32_e32 v75, v79
	v_mov_b32_e32 v16, v79
	v_mov_b32_e32 v17, v79
	v_mov_b32_e32 v18, v79
	v_mov_b32_e32 v68, v79
	s_ashr_i32 s23, s24, 31
	s_add_u32 s26, s3, s24
	s_addc_u32 s27, s25, s23
	s_cmpk_lt_u32 s68, 0xf97f
	s_waitcnt vmcnt(15)
	v_mul_f32_e32 v56, 0x42800000, v56
	v_mul_f32_e32 v57, 0x42800000, v57
	s_waitcnt vmcnt(14)
	v_mul_f32_e32 v60, 0x42800000, v60
	v_med3_f32 v56, v56, s74, v101
	v_mul_f32_e32 v61, 0x42800000, v61
	v_med3_f32 v60, v60, s74, v101
	v_med3_f32 v57, v57, s74, v101
	v_med3_f32 v61, v61, s74, v101
	s_waitcnt vmcnt(11)
	v_mul_f32_e32 v41, 0x42800000, v41
	v_med3_f32 v41, v41, s74, v101
	s_waitcnt vmcnt(10)
	v_mul_f32_e32 v45, 0x42800000, v45
	v_med3_f32 v45, v45, s74, v101
	v_cvt_pk_fp8_f32 v69, v41, v45
	s_waitcnt vmcnt(9)
	v_mul_f32_e32 v49, 0x42800000, v49
	v_mul_f32_e32 v40, 0x42800000, v40
	v_mul_f32_e32 v44, 0x42800000, v44
	s_waitcnt vmcnt(7)
	v_mul_f32_e32 v24, 0x42800000, v24
	v_med3_f32 v40, v40, s74, v101
	s_waitcnt vmcnt(6)
	v_mul_f32_e32 v28, 0x42800000, v28
	v_med3_f32 v44, v44, s74, v101
	v_med3_f32 v24, v24, s74, v101
	v_med3_f32 v28, v28, s74, v101
	v_cvt_pk_fp8_f32 v16, v56, v60
	v_cvt_pk_fp8_f32 v17, v40, v44
	s_waitcnt vmcnt(3)
	v_mul_f32_e32 v4, 0x42800000, v4
	v_med3_f32 v4, v4, s74, v101
	s_waitcnt vmcnt(2)
	v_mul_f32_e32 v8, 0x42800000, v8
	v_med3_f32 v8, v8, s74, v101
	v_cvt_pk_fp8_f32 v19, v4, v8
	s_waitcnt vmcnt(1)
	v_mul_f32_e32 v12, 0x42800000, v12
	s_waitcnt vmcnt(0)
	v_mul_f32_e32 v0, 0x42800000, v0
	v_med3_f32 v4, v12, s74, v101
	v_med3_f32 v0, v0, s74, v101
	v_cvt_pk_fp8_f32 v19, v4, v0 op_sel:[0,0,1]
	v_mul_f32_e32 v0, 0x42800000, v37
	v_med3_f32 v4, v49, s74, v101
	v_med3_f32 v0, v0, s74, v101
	v_cvt_pk_fp8_f32 v69, v4, v0 op_sel:[0,0,1]
	v_mul_f32_e32 v0, 0x42800000, v25
	v_mul_f32_e32 v4, 0x42800000, v29
	v_med3_f32 v0, v0, s74, v101
	v_med3_f32 v4, v4, s74, v101
	v_cvt_pk_fp8_f32 v70, v0, v4
	v_mul_f32_e32 v8, 0x42800000, v33
	v_mul_f32_e32 v0, 0x42800000, v21
	v_med3_f32 v4, v8, s74, v101
	v_med3_f32 v0, v0, s74, v101
	v_cvt_pk_fp8_f32 v70, v4, v0 op_sel:[0,0,1]
	v_mul_f32_e32 v0, 0x42800000, v5
	v_mul_f32_e32 v4, 0x42800000, v9
	v_med3_f32 v0, v0, s74, v101
	v_med3_f32 v4, v4, s74, v101
	v_cvt_pk_fp8_f32 v71, v0, v4
	v_mul_f32_e32 v5, 0x42800000, v13
	v_mul_f32_e32 v0, 0x42800000, v1
	v_med3_f32 v1, v5, s74, v101
	v_med3_f32 v0, v0, s74, v101
	v_cvt_pk_fp8_f32 v71, v1, v0 op_sel:[0,0,1]
	v_mul_f32_e32 v0, 0x42800000, v58
	v_mul_f32_e32 v1, 0x42800000, v62
	v_med3_f32 v0, v0, s74, v101
	v_med3_f32 v1, v1, s74, v101
	v_cvt_pk_fp8_f32 v72, v0, v1
	v_mul_f32_e32 v4, 0x42800000, v66
	v_mul_f32_e32 v0, 0x42800000, v54
	v_med3_f32 v1, v4, s74, v101
	v_med3_f32 v0, v0, s74, v101
	v_cvt_pk_fp8_f32 v72, v1, v0 op_sel:[0,0,1]
	v_mul_f32_e32 v0, 0x42800000, v42
	v_mul_f32_e32 v1, 0x42800000, v46
	v_med3_f32 v0, v0, s74, v101
	v_med3_f32 v1, v1, s74, v101
	v_cvt_pk_fp8_f32 v73, v0, v1
	v_mul_f32_e32 v4, 0x42800000, v50
	v_mul_f32_e32 v0, 0x42800000, v38
	v_med3_f32 v1, v4, s74, v101
	v_med3_f32 v0, v0, s74, v101
	v_cvt_pk_fp8_f32 v73, v1, v0 op_sel:[0,0,1]
	v_mul_f32_e32 v0, 0x42800000, v26
	v_mul_f32_e32 v1, 0x42800000, v30
	v_med3_f32 v0, v0, s74, v101
	v_med3_f32 v1, v1, s74, v101
	v_cvt_pk_fp8_f32 v74, v0, v1
	v_mul_f32_e32 v4, 0x42800000, v34
	v_mul_f32_e32 v0, 0x42800000, v22
	v_med3_f32 v1, v4, s74, v101
	v_med3_f32 v0, v0, s74, v101
	v_cvt_pk_fp8_f32 v74, v1, v0 op_sel:[0,0,1]
	v_mul_f32_e32 v0, 0x42800000, v6
	v_mul_f32_e32 v1, 0x42800000, v10
	v_med3_f32 v0, v0, s74, v101
	v_med3_f32 v1, v1, s74, v101
	v_cvt_pk_fp8_f32 v75, v0, v1
	v_mul_f32_e32 v4, 0x42800000, v14
	v_mul_f32_e32 v0, 0x42800000, v2
	v_med3_f32 v1, v4, s74, v101
	v_med3_f32 v0, v0, s74, v101
	v_cvt_pk_fp8_f32 v75, v1, v0 op_sel:[0,0,1]
	v_mul_f32_e32 v0, 0x42800000, v59
	v_mul_f32_e32 v1, 0x42800000, v63
	v_med3_f32 v0, v0, s74, v101
	v_med3_f32 v1, v1, s74, v101
	v_mov_b32_e32 v4, v79
	v_cvt_pk_fp8_f32 v4, v0, v1
	v_mul_f32_e32 v2, 0x42800000, v67
	v_mul_f32_e32 v0, 0x42800000, v55
	v_med3_f32 v1, v2, s74, v101
	v_med3_f32 v0, v0, s74, v101
	v_cvt_pk_fp8_f32 v4, v1, v0 op_sel:[0,0,1]
	v_mul_f32_e32 v0, 0x42800000, v43
	v_mul_f32_e32 v1, 0x42800000, v47
	v_med3_f32 v0, v0, s74, v101
	v_med3_f32 v1, v1, s74, v101
	v_mov_b32_e32 v5, v79
	v_cvt_pk_fp8_f32 v5, v0, v1
	v_mul_f32_e32 v2, 0x42800000, v51
	v_mul_f32_e32 v0, 0x42800000, v39
	v_med3_f32 v1, v2, s74, v101
	v_med3_f32 v0, v0, s74, v101
	v_cvt_pk_fp8_f32 v5, v1, v0 op_sel:[0,0,1]
	v_mul_f32_e32 v0, 0x42800000, v27
	v_mul_f32_e32 v1, 0x42800000, v31
	v_med3_f32 v0, v0, s74, v101
	v_med3_f32 v1, v1, s74, v101
	v_mov_b32_e32 v6, v79
	v_cvt_pk_fp8_f32 v6, v0, v1
	v_mul_f32_e32 v2, 0x42800000, v35
	v_mul_f32_e32 v0, 0x42800000, v23
	v_cvt_pk_fp8_f32 v18, v24, v28
	v_med3_f32 v1, v2, s74, v101
	v_med3_f32 v0, v0, s74, v101
	v_cvt_pk_fp8_f32 v68, v57, v61
	v_cvt_pk_fp8_f32 v6, v1, v0 op_sel:[0,0,1]
	v_mul_f32_e32 v0, 0x42800000, v7
	v_mul_f32_e32 v1, 0x42800000, v11
	v_mul_f32_e32 v64, 0x42800000, v64
	v_mul_f32_e32 v52, 0x42800000, v52
	v_mul_f32_e32 v48, 0x42800000, v48
	v_mul_f32_e32 v36, 0x42800000, v36
	v_mul_f32_e32 v32, 0x42800000, v32
	v_mul_f32_e32 v20, 0x42800000, v20
	v_med3_f32 v0, v0, s74, v101
	v_med3_f32 v1, v1, s74, v101
	v_mov_b32_e32 v7, v79
	v_mul_f32_e32 v65, 0x42800000, v65
	v_med3_f32 v64, v64, s74, v101
	v_mul_f32_e32 v53, 0x42800000, v53
	v_med3_f32 v52, v52, s74, v101
	v_med3_f32 v48, v48, s74, v101
	v_med3_f32 v36, v36, s74, v101
	v_med3_f32 v32, v32, s74, v101
	v_med3_f32 v20, v20, s74, v101
	v_cvt_pk_fp8_f32 v7, v0, v1
	v_med3_f32 v56, v65, s74, v101
	v_med3_f32 v53, v53, s74, v101
	v_cvt_pk_fp8_f32 v16, v64, v52 op_sel:[0,0,1]
	v_cvt_pk_fp8_f32 v17, v48, v36 op_sel:[0,0,1]
	v_cvt_pk_fp8_f32 v18, v32, v20 op_sel:[0,0,1]
	v_cvt_pk_fp8_f32 v68, v56, v53 op_sel:[0,0,1]
	v_mul_f32_e32 v2, 0x42800000, v15
	v_mul_f32_e32 v0, 0x42800000, v3
	v_med3_f32 v1, v2, s74, v101
	v_med3_f32 v0, v0, s74, v101
	v_cvt_pk_fp8_f32 v7, v1, v0 op_sel:[0,0,1]
	ds_write_b128 v98, v[16:19] offset:40960
	ds_write_b128 v98, v[68:71] offset:41040
	ds_write_b128 v98, v[72:75] offset:41120
	ds_write_b128 v98, v[4:7] offset:41200
	s_waitcnt lgkmcnt(0)
	ds_read_b128 v[0:3], v99 offset:40960
	v_or_b32_e32 v4, s17, v87
	v_ashrrev_i32_e32 v5, 31, v4
	v_lshl_add_u64 v[8:9], s[26:27], 0, v[80:81]
	v_lshlrev_b64 v[4:5], 11, v[4:5]
	v_lshl_add_u64 v[10:11], v[8:9], 0, v[4:5]
	ds_read_b128 v[4:7], v99 offset:42240
	s_waitcnt lgkmcnt(1)
	global_store_dwordx4 v[10:11], v[0:3], off sc1
	s_cselect_b64 s[26:27], -1, 0
	s_nop 0
	v_or_b32_e32 v0, s17, v77
	v_ashrrev_i32_e32 v1, 31, v0
	v_lshlrev_b64 v[0:1], 11, v[0:1]
	v_lshl_add_u64 v[0:1], v[8:9], 0, v[0:1]
	s_waitcnt lgkmcnt(0)
	global_store_dwordx4 v[0:1], v[4:7], off sc1
	ds_read_b128 v[0:3], v99 offset:43520
	s_nop 0
	v_or_b32_e32 v4, s17, v88
	v_ashrrev_i32_e32 v5, 31, v4
	v_lshlrev_b64 v[4:5], 11, v[4:5]
	v_lshl_add_u64 v[10:11], v[8:9], 0, v[4:5]
	ds_read_b128 v[4:7], v99 offset:44800
	s_waitcnt lgkmcnt(1)
	global_store_dwordx4 v[10:11], v[0:3], off sc1
	s_nop 1
	v_or_b32_e32 v0, s17, v89
	v_ashrrev_i32_e32 v1, 31, v0
	v_lshlrev_b64 v[0:1], 11, v[0:1]
	v_lshl_add_u64 v[0:1], v[8:9], 0, v[0:1]
	s_waitcnt lgkmcnt(0)
	global_store_dwordx4 v[0:1], v[4:7], off sc1
	s_waitcnt lgkmcnt(0)
	s_andn2_b64 vcc, exec, s[26:27]
	s_cbranch_vccz .LBB0_2382
	s_branch .LBB0_2403

.LBB0_2493:
	s_add_i32 s92, s56, s61
	s_add_i32 s0, s92, 0xc187
	s_mul_hi_i32 s2, s0, 0x20d56b39
	s_lshr_b32 s3, s2, 31
	s_ashr_i32 s2, s2, 12
	s_add_i32 s2, s2, s3
	s_mul_i32 s3, s2, 0x7cc0
	s_sub_i32 s30, s0, s3
	s_cmpk_gt_i32 s30, 0x1cbf
	s_mov_b64 s[6:7], -1
	s_cbranch_scc0 .LBB0_2499
	s_add_i32 s9, s30, 0xffffe340
	s_and_b32 s8, s9, 0xff
	s_cmpk_gt_u32 s30, 0x5cbf
	s_cbranch_scc0 .LBB0_2496
	v_mov_b32_e32 v0, s57
	s_add_i32 s0, s30, 0xffffa340
	s_ashr_i32 s3, s2, 31
	ds_read_b64 v[0:1], v0
	s_lshr_b32 s0, s0, 8
	s_lshl_b64 s[6:7], s[2:3], 26
	s_add_u32 s10, s38, s6
	s_addc_u32 s11, s39, s7
	s_lshl_b64 s[6:7], s[0:1], 20
	s_add_u32 s6, s10, s6
	s_addc_u32 s7, s11, s7
	s_waitcnt lgkmcnt(0)
	v_readfirstlane_b32 s12, v0
	s_lshl_b64 s[10:11], s[2:3], 27
	v_readfirstlane_b32 s13, v1
	s_add_u32 s3, s12, s10
	s_addc_u32 s13, s13, s11
	s_lshl_b64 s[10:11], s[0:1], 22
	s_add_u32 s12, s3, s10
	s_addc_u32 s13, s13, s11
	s_lshl_b32 s0, s8, 3
	s_and_b32 s3, s0, 0x7c0
	s_lshl_b32 s0, s30, 6
	s_and_b32 s10, s0, 0x1c0
	v_or_b32_e32 v0, s10, v74
	v_lshlrev_b32_e32 v0, 13, v0
	v_mov_b32_e32 v1, v69
	v_lshl_add_u64 v[0:1], s[12:13], 0, v[0:1]
	s_lshl_b32 s0, s3, 2
	v_lshl_add_u64 v[0:1], v[0:1], 0, s[0:1]
	v_mov_b32_e32 v73, v69
	v_lshl_add_u64 v[60:61], v[0:1], 0, v[72:73]
	v_add_co_u32_e32 v4, vcc, s58, v60
	s_mov_b32 s0, 0x8000
	s_nop 0
	v_addc_co_u32_e32 v5, vcc, 0, v61, vcc
	v_add_co_u32_e32 v8, vcc, s59, v60
	global_load_dwordx4 v[0:3], v[60:61], off nt
	s_nop 0
	global_load_dwordx4 v[4:7], v[4:5], off nt
	v_addc_co_u32_e32 v9, vcc, 0, v61, vcc
	v_add_co_u32_e32 v10, vcc, s60, v60
	v_mov_b32_e32 v64, v69
	s_nop 0
	v_addc_co_u32_e32 v11, vcc, 0, v61, vcc
	v_add_co_u32_e32 v16, vcc, s0, v60
	s_mov_b32 s0, 0xa000
	s_nop 0
	v_addc_co_u32_e32 v17, vcc, 0, v61, vcc
	v_add_co_u32_e32 v20, vcc, s0, v60
	s_mov_b32 s0, 0xc000
	s_nop 0
	v_addc_co_u32_e32 v21, vcc, 0, v61, vcc
	v_add_co_u32_e32 v24, vcc, s0, v60
	s_mov_b32 s0, 0xe000
	s_nop 0
	v_addc_co_u32_e32 v25, vcc, 0, v61, vcc
	global_load_dwordx4 v[12:15], v[8:9], off nt
	s_nop 0
	global_load_dwordx4 v[8:11], v[10:11], off nt
	v_add_co_u32_e32 v26, vcc, s0, v60
	s_mov_b32 s0, 0x10000
	s_nop 0
	v_addc_co_u32_e32 v27, vcc, 0, v61, vcc
	global_load_dwordx4 v[16:19], v[16:17], off nt
	s_nop 0
	global_load_dwordx4 v[20:23], v[20:21], off nt
	v_add_co_u32_e32 v28, vcc, s0, v60
	s_mov_b32 s0, 0x14000
	s_nop 0
	v_addc_co_u32_e32 v29, vcc, 0, v61, vcc
	v_add_co_u32_e32 v36, vcc, s62, v60
	global_load_dwordx4 v[32:35], v[24:25], off nt
	s_nop 0
	global_load_dwordx4 v[24:27], v[26:27], off nt
	v_addc_co_u32_e32 v37, vcc, 0, v61, vcc
	v_add_co_u32_e32 v40, vcc, s0, v60
	s_mov_b32 s0, 0x16000
	s_nop 0
	v_addc_co_u32_e32 v41, vcc, 0, v61, vcc
	global_load_dwordx4 v[28:31], v[28:29], off nt
	s_nop 0
	global_load_dwordx4 v[36:39], v[36:37], off nt
	v_add_co_u32_e32 v42, vcc, s0, v60
	s_mov_b32 s0, 0x18000
	s_nop 0
	v_addc_co_u32_e32 v43, vcc, 0, v61, vcc
	v_add_co_u32_e32 v44, vcc, s0, v60
	global_load_dwordx4 v[48:51], v[40:41], off nt
	s_nop 0
	global_load_dwordx4 v[40:43], v[42:43], off nt
	v_addc_co_u32_e32 v45, vcc, 0, v61, vcc
	v_add_co_u32_e32 v52, vcc, s63, v60
	v_mov_b32_e32 v65, v69
	s_nop 0
	v_addc_co_u32_e32 v53, vcc, 0, v61, vcc
	global_load_dwordx4 v[44:47], v[44:45], off nt
	s_nop 0
	global_load_dwordx4 v[52:55], v[52:53], off nt
	v_add_co_u32_e32 v56, vcc, s64, v60
	v_mov_b32_e32 v66, v69
	s_nop 0
	v_addc_co_u32_e32 v57, vcc, 0, v61, vcc
	v_add_co_u32_e32 v60, vcc, s65, v60
	global_load_dwordx4 v[56:59], v[56:57], off nt
	s_nop 0
	v_addc_co_u32_e32 v61, vcc, 0, v61, vcc
	global_load_dwordx4 v[60:63], v[60:61], off nt
	v_mov_b32_e32 v67, v69
	v_mov_b32_e32 v96, v69
	v_mov_b32_e32 v97, v69
	v_mov_b32_e32 v98, v69
	v_mov_b32_e32 v99, v69
	v_mov_b32_e32 v100, v69
	s_waitcnt vmcnt(0)
	v_mul_f32_e32 v0, 0x42000000, v0
	v_mul_f32_e32 v4, 0x42000000, v4
	v_med3_f32 v0, v0, s66, v90
	v_med3_f32 v4, v4, s66, v90
	v_cvt_pk_fp8_f32 v64, v0, v4
	v_mov_b32_e32 v101, v69
	v_mov_b32_e32 v102, v69
	v_mov_b32_e32 v103, v69
	s_add_u32 s6, s6, s10
	s_addc_u32 s7, s7, 0
	v_mul_f32_e32 v12, 0x42000000, v12
	v_mul_f32_e32 v0, 0x42000000, v8
	v_med3_f32 v4, v12, s66, v90
	v_med3_f32 v0, v0, s66, v90
	v_cvt_pk_fp8_f32 v64, v4, v0 op_sel:[0,0,1]
	v_mul_f32_e32 v0, 0x42000000, v16
	v_mul_f32_e32 v4, 0x42000000, v20
	v_med3_f32 v0, v0, s66, v90
	v_med3_f32 v4, v4, s66, v90
	v_cvt_pk_fp8_f32 v65, v0, v4
	v_mul_f32_e32 v8, 0x42000000, v32
	v_mul_f32_e32 v0, 0x42000000, v24
	v_med3_f32 v4, v8, s66, v90
	v_med3_f32 v0, v0, s66, v90
	v_cvt_pk_fp8_f32 v65, v4, v0 op_sel:[0,0,1]
	v_mul_f32_e32 v0, 0x42000000, v28
	v_mul_f32_e32 v4, 0x42000000, v36
	v_med3_f32 v0, v0, s66, v90
	v_med3_f32 v4, v4, s66, v90
	v_cvt_pk_fp8_f32 v66, v0, v4
	v_mul_f32_e32 v8, 0x42000000, v48
	v_mul_f32_e32 v0, 0x42000000, v40
	v_med3_f32 v4, v8, s66, v90
	v_med3_f32 v0, v0, s66, v90
	v_cvt_pk_fp8_f32 v66, v4, v0 op_sel:[0,0,1]
	v_mul_f32_e32 v0, 0x42000000, v44
	v_mul_f32_e32 v4, 0x42000000, v52
	v_med3_f32 v0, v0, s66, v90
	v_med3_f32 v4, v4, s66, v90
	v_cvt_pk_fp8_f32 v67, v0, v4
	v_mul_f32_e32 v8, 0x42000000, v56
	v_med3_f32 v4, v8, s66, v90
	v_mul_f32_e32 v0, 0x42000000, v60
	v_med3_f32 v0, v0, s66, v90
	v_cvt_pk_fp8_f32 v67, v4, v0 op_sel:[0,0,1]
	v_mul_f32_e32 v0, 0x42000000, v1
	v_mul_f32_e32 v1, 0x42000000, v5
	v_med3_f32 v0, v0, s66, v90
	v_med3_f32 v1, v1, s66, v90
	v_cvt_pk_fp8_f32 v96, v0, v1
	v_mul_f32_e32 v4, 0x42000000, v13
	v_mul_f32_e32 v0, 0x42000000, v9
	v_med3_f32 v1, v4, s66, v90
	v_med3_f32 v0, v0, s66, v90
	v_cvt_pk_fp8_f32 v96, v1, v0 op_sel:[0,0,1]
	v_mul_f32_e32 v0, 0x42000000, v17
	v_mul_f32_e32 v1, 0x42000000, v21
	v_med3_f32 v0, v0, s66, v90
	v_med3_f32 v1, v1, s66, v90
	v_cvt_pk_fp8_f32 v97, v0, v1
	v_mul_f32_e32 v4, 0x42000000, v33
	v_mul_f32_e32 v0, 0x42000000, v25
	v_med3_f32 v1, v4, s66, v90
	v_med3_f32 v0, v0, s66, v90
	v_cvt_pk_fp8_f32 v97, v1, v0 op_sel:[0,0,1]
	v_mul_f32_e32 v0, 0x42000000, v29
	v_mul_f32_e32 v1, 0x42000000, v37
	v_med3_f32 v0, v0, s66, v90
	v_med3_f32 v1, v1, s66, v90
	v_cvt_pk_fp8_f32 v98, v0, v1
	v_mul_f32_e32 v4, 0x42000000, v49
	v_mul_f32_e32 v0, 0x42000000, v41
	v_med3_f32 v1, v4, s66, v90
	v_med3_f32 v0, v0, s66, v90
	v_cvt_pk_fp8_f32 v98, v1, v0 op_sel:[0,0,1]
	v_mul_f32_e32 v0, 0x42000000, v45
	v_mul_f32_e32 v1, 0x42000000, v53
	v_med3_f32 v0, v0, s66, v90
	v_med3_f32 v1, v1, s66, v90
	v_cvt_pk_fp8_f32 v99, v0, v1
	v_mul_f32_e32 v4, 0x42000000, v57
	v_mul_f32_e32 v0, 0x42000000, v61
	v_med3_f32 v1, v4, s66, v90
	v_med3_f32 v0, v0, s66, v90
	v_cvt_pk_fp8_f32 v99, v1, v0 op_sel:[0,0,1]
	v_mul_f32_e32 v0, 0x42000000, v2
	v_mul_f32_e32 v1, 0x42000000, v6
	v_med3_f32 v0, v0, s66, v90
	v_med3_f32 v1, v1, s66, v90
	v_cvt_pk_fp8_f32 v100, v0, v1
	v_mul_f32_e32 v2, 0x42000000, v14
	v_mul_f32_e32 v0, 0x42000000, v10
	v_med3_f32 v1, v2, s66, v90
	v_med3_f32 v0, v0, s66, v90
	v_cvt_pk_fp8_f32 v100, v1, v0 op_sel:[0,0,1]
	v_mul_f32_e32 v0, 0x42000000, v18
	v_mul_f32_e32 v1, 0x42000000, v22
	v_med3_f32 v0, v0, s66, v90
	v_med3_f32 v1, v1, s66, v90
	v_cvt_pk_fp8_f32 v101, v0, v1
	v_mul_f32_e32 v2, 0x42000000, v34
	v_mul_f32_e32 v0, 0x42000000, v26
	v_med3_f32 v1, v2, s66, v90
	v_med3_f32 v0, v0, s66, v90
	v_cvt_pk_fp8_f32 v101, v1, v0 op_sel:[0,0,1]
	v_mul_f32_e32 v0, 0x42000000, v30
	v_mul_f32_e32 v1, 0x42000000, v38
	v_med3_f32 v0, v0, s66, v90
	v_med3_f32 v1, v1, s66, v90
	v_cvt_pk_fp8_f32 v102, v0, v1
	v_mul_f32_e32 v2, 0x42000000, v50
	v_mul_f32_e32 v0, 0x42000000, v42
	v_med3_f32 v1, v2, s66, v90
	v_med3_f32 v0, v0, s66, v90
	v_cvt_pk_fp8_f32 v102, v1, v0 op_sel:[0,0,1]
	v_mul_f32_e32 v0, 0x42000000, v46
	v_mul_f32_e32 v1, 0x42000000, v54
	v_med3_f32 v0, v0, s66, v90
	v_med3_f32 v1, v1, s66, v90
	v_cvt_pk_fp8_f32 v103, v0, v1
	v_mul_f32_e32 v2, 0x42000000, v58
	v_mul_f32_e32 v0, 0x42000000, v62
	v_med3_f32 v1, v2, s66, v90
	v_med3_f32 v0, v0, s66, v90
	v_cvt_pk_fp8_f32 v103, v1, v0 op_sel:[0,0,1]
	v_mul_f32_e32 v0, 0x42000000, v3
	v_mul_f32_e32 v1, 0x42000000, v7
	v_med3_f32 v3, v0, s66, v90
	v_med3_f32 v1, v1, s66, v90
	v_mov_b32_e32 v0, v69
	v_cvt_pk_fp8_f32 v0, v3, v1
	v_mul_f32_e32 v2, 0x42000000, v15
	v_mul_f32_e32 v1, 0x42000000, v11
	v_med3_f32 v2, v2, s66, v90
	v_med3_f32 v1, v1, s66, v90
	v_cvt_pk_fp8_f32 v0, v2, v1 op_sel:[0,0,1]
	v_mul_f32_e32 v1, 0x42000000, v19
	v_mul_f32_e32 v2, 0x42000000, v23
	v_med3_f32 v4, v1, s66, v90
	v_med3_f32 v2, v2, s66, v90
	v_mov_b32_e32 v1, v69
	v_cvt_pk_fp8_f32 v1, v4, v2
	v_mul_f32_e32 v3, 0x42000000, v35
	v_mul_f32_e32 v2, 0x42000000, v27
	v_med3_f32 v3, v3, s66, v90
	v_med3_f32 v2, v2, s66, v90
	v_cvt_pk_fp8_f32 v1, v3, v2 op_sel:[0,0,1]
	v_mul_f32_e32 v2, 0x42000000, v31
	v_mul_f32_e32 v3, 0x42000000, v39
	v_med3_f32 v5, v2, s66, v90
	v_med3_f32 v3, v3, s66, v90
	v_mov_b32_e32 v2, v69
	v_cvt_pk_fp8_f32 v2, v5, v3
	v_mul_f32_e32 v4, 0x42000000, v51
	v_mul_f32_e32 v3, 0x42000000, v43
	v_med3_f32 v4, v4, s66, v90
	v_med3_f32 v3, v3, s66, v90
	v_cvt_pk_fp8_f32 v2, v4, v3 op_sel:[0,0,1]
	v_mul_f32_e32 v3, 0x42000000, v47
	v_mul_f32_e32 v4, 0x42000000, v55
	v_med3_f32 v6, v3, s66, v90
	v_med3_f32 v4, v4, s66, v90
	v_mov_b32_e32 v3, v69
	v_cvt_pk_fp8_f32 v3, v6, v4
	v_mul_f32_e32 v5, 0x42000000, v59
	v_mul_f32_e32 v4, 0x42000000, v63
	v_med3_f32 v5, v5, s66, v90
	v_med3_f32 v4, v4, s66, v90
	v_cvt_pk_fp8_f32 v3, v5, v4 op_sel:[0,0,1]
	ds_write_b128 v87, v[64:67] offset:40960
	ds_write_b128 v87, v[96:99] offset:41040
	ds_write_b128 v87, v[100:103] offset:41120
	ds_write_b128 v87, v[0:3] offset:41200
	s_waitcnt lgkmcnt(0)
	ds_read_b128 v[0:3], v88 offset:40960
	v_or_b32_e32 v4, s3, v75
	v_lshl_add_u64 v[8:9], s[6:7], 0, v[70:71]
	v_lshlrev_b32_e32 v4, 9, v4
	v_mov_b32_e32 v5, v69
	v_lshl_add_u64 v[10:11], v[8:9], 0, v[4:5]
	ds_read_b128 v[4:7], v88 offset:42240
	s_waitcnt lgkmcnt(1)
	global_store_dwordx4 v[10:11], v[0:3], off sc1
	s_mov_b64 s[6:7], 0
	s_nop 0
	v_or_b32_e32 v0, s3, v76
	v_lshlrev_b32_e32 v0, 9, v0
	v_mov_b32_e32 v1, v69
	v_lshl_add_u64 v[0:1], v[8:9], 0, v[0:1]
	s_waitcnt lgkmcnt(0)
	global_store_dwordx4 v[0:1], v[4:7], off sc1
	ds_read_b128 v[0:3], v88 offset:43520
	s_nop 0
	v_or_b32_e32 v4, s3, v77
	v_lshlrev_b32_e32 v4, 9, v4
	v_mov_b32_e32 v5, v69
	v_lshl_add_u64 v[10:11], v[8:9], 0, v[4:5]
	ds_read_b128 v[4:7], v88 offset:44800
	s_waitcnt lgkmcnt(1)
	global_store_dwordx4 v[10:11], v[0:3], off sc1
	s_nop 1
	v_or_b32_e32 v0, s3, v78
	v_lshlrev_b32_e32 v0, 9, v0
	v_mov_b32_e32 v1, v69
	v_lshl_add_u64 v[0:1], v[8:9], 0, v[0:1]
	s_waitcnt lgkmcnt(0)
	global_store_dwordx4 v[0:1], v[4:7], off sc1
	s_waitcnt lgkmcnt(0)

.LBB0_2530:
	s_and_b64 vcc, exec, s[30:31]
	s_cbranch_vccz .LBB0_2492
	s_xor_b64 s[30:31], s[22:23], -1
	s_lshl_b32 s22, s3, 6
	s_mov_b64 s[28:29], -1
	s_and_b64 vcc, exec, s[30:31]
	s_cbranch_vccz .LBB0_2561
	s_andn2_b64 vcc, exec, s[26:27]
	s_cbranch_vccnz .LBB0_2535
	s_ashr_i32 s3, s2, 31
	s_lshl_b64 s[26:27], s[2:3], 22
	v_or_b32_e32 v0, s22, v74
	s_add_u32 s3, s52, s26
	v_mul_hi_i32_i24_e32 v1, s16, v0
	v_mul_i32_i24_e32 v0, s16, v0
	s_addc_u32 s23, s53, s27
	v_lshl_add_u64 v[0:1], v[0:1], 2, s[6:7]
	s_ashr_i32 s21, s20, 31
	v_lshl_add_u64 v[0:1], s[20:21], 2, v[0:1]
	v_mov_b32_e32 v73, v69
	v_lshl_add_u64 v[0:1], v[0:1], 0, v[72:73]
	s_lshl_b64 s[26:27], s[16:17], 2
	global_load_dwordx4 v[56:59], v[0:1], off nt
	v_lshl_add_u64 v[0:1], v[0:1], 0, s[26:27]
	global_load_dwordx4 v[60:63], v[0:1], off nt
	v_lshl_add_u64 v[0:1], v[0:1], 0, s[26:27]
	global_load_dwordx4 v[64:67], v[0:1], off nt
	v_lshl_add_u64 v[0:1], v[0:1], 0, s[26:27]
	global_load_dwordx4 v[52:55], v[0:1], off nt
	v_lshl_add_u64 v[0:1], v[0:1], 0, s[26:27]
	global_load_dwordx4 v[40:43], v[0:1], off nt
	v_lshl_add_u64 v[0:1], v[0:1], 0, s[26:27]
	global_load_dwordx4 v[44:47], v[0:1], off nt
	v_lshl_add_u64 v[0:1], v[0:1], 0, s[26:27]
	global_load_dwordx4 v[48:51], v[0:1], off nt
	v_lshl_add_u64 v[0:1], v[0:1], 0, s[26:27]
	global_load_dwordx4 v[36:39], v[0:1], off nt
	v_lshl_add_u64 v[0:1], v[0:1], 0, s[26:27]
	global_load_dwordx4 v[24:27], v[0:1], off nt
	v_lshl_add_u64 v[0:1], v[0:1], 0, s[26:27]
	global_load_dwordx4 v[28:31], v[0:1], off nt
	v_lshl_add_u64 v[0:1], v[0:1], 0, s[26:27]
	global_load_dwordx4 v[32:35], v[0:1], off nt
	v_lshl_add_u64 v[0:1], v[0:1], 0, s[26:27]
	global_load_dwordx4 v[20:23], v[0:1], off nt
	v_lshl_add_u64 v[0:1], v[0:1], 0, s[26:27]
	global_load_dwordx4 v[4:7], v[0:1], off nt
	v_lshl_add_u64 v[0:1], v[0:1], 0, s[26:27]
	global_load_dwordx4 v[12:15], v[0:1], off nt
	v_lshl_add_u64 v[0:1], v[0:1], 0, s[26:27]
	global_load_dwordx4 v[16:19], v[0:1], off nt
	v_lshl_add_u64 v[0:1], v[0:1], 0, s[26:27]
	global_load_dwordx4 v[0:3], v[0:1], off nt
	v_mov_b32_e32 v11, v69
	v_mov_b32_e32 v97, v69
	v_mov_b32_e32 v98, v69
	v_mov_b32_e32 v99, v69
	v_mov_b32_e32 v100, v69
	v_mov_b32_e32 v101, v69
	v_mov_b32_e32 v102, v69
	v_mov_b32_e32 v103, v69
	v_mov_b32_e32 v8, v69
	v_mov_b32_e32 v9, v69
	v_mov_b32_e32 v10, v69
	v_mov_b32_e32 v96, v69
	s_ashr_i32 s21, s22, 31
	s_add_u32 s26, s3, s22
	s_addc_u32 s27, s23, s21
	s_add_i32 s3, s92, 0x13e46
	s_cmpk_lt_u32 s3, 0xf97f
	s_waitcnt vmcnt(0)
	v_mul_f32_e32 v56, 0x42800000, v56
	v_mul_f32_e32 v57, 0x42800000, v57
	v_mul_f32_e32 v60, 0x42800000, v60
	v_med3_f32 v56, v56, s66, v90
	v_mul_f32_e32 v61, 0x42800000, v61
	v_med3_f32 v60, v60, s66, v90
	v_med3_f32 v57, v57, s66, v90
	v_med3_f32 v61, v61, s66, v90
	v_mul_f32_e32 v41, 0x42800000, v41
	v_med3_f32 v41, v41, s66, v90
	v_mul_f32_e32 v45, 0x42800000, v45
	v_med3_f32 v45, v45, s66, v90
	v_cvt_pk_fp8_f32 v97, v41, v45
	v_mul_f32_e32 v49, 0x42800000, v49
	v_mul_f32_e32 v40, 0x42800000, v40
	v_mul_f32_e32 v44, 0x42800000, v44
	v_mul_f32_e32 v24, 0x42800000, v24
	v_med3_f32 v40, v40, s66, v90
	v_mul_f32_e32 v28, 0x42800000, v28
	v_med3_f32 v44, v44, s66, v90
	v_med3_f32 v24, v24, s66, v90
	v_med3_f32 v28, v28, s66, v90
	v_cvt_pk_fp8_f32 v8, v56, v60
	v_cvt_pk_fp8_f32 v9, v40, v44
	v_mul_f32_e32 v4, 0x42800000, v4
	v_med3_f32 v4, v4, s66, v90
	v_mul_f32_e32 v12, 0x42800000, v12
	v_med3_f32 v12, v12, s66, v90
	v_cvt_pk_fp8_f32 v11, v4, v12
	v_mul_f32_e32 v16, 0x42800000, v16
	v_mul_f32_e32 v0, 0x42800000, v0
	v_med3_f32 v4, v16, s66, v90
	v_med3_f32 v0, v0, s66, v90
	v_cvt_pk_fp8_f32 v11, v4, v0 op_sel:[0,0,1]
	v_mul_f32_e32 v0, 0x42800000, v37
	v_med3_f32 v4, v49, s66, v90
	v_med3_f32 v0, v0, s66, v90
	v_cvt_pk_fp8_f32 v97, v4, v0 op_sel:[0,0,1]
	v_mul_f32_e32 v0, 0x42800000, v25
	v_mul_f32_e32 v4, 0x42800000, v29
	v_med3_f32 v0, v0, s66, v90
	v_med3_f32 v4, v4, s66, v90
	v_cvt_pk_fp8_f32 v98, v0, v4
	v_mul_f32_e32 v12, 0x42800000, v33
	v_mul_f32_e32 v0, 0x42800000, v21
	v_med3_f32 v4, v12, s66, v90
	v_med3_f32 v0, v0, s66, v90
	v_cvt_pk_fp8_f32 v98, v4, v0 op_sel:[0,0,1]
	v_mul_f32_e32 v0, 0x42800000, v5
	v_mul_f32_e32 v4, 0x42800000, v13
	v_med3_f32 v0, v0, s66, v90
	v_med3_f32 v4, v4, s66, v90
	v_cvt_pk_fp8_f32 v99, v0, v4
	v_mul_f32_e32 v5, 0x42800000, v17
	v_mul_f32_e32 v0, 0x42800000, v1
	v_med3_f32 v1, v5, s66, v90
	v_med3_f32 v0, v0, s66, v90
	v_cvt_pk_fp8_f32 v99, v1, v0 op_sel:[0,0,1]
	v_mul_f32_e32 v0, 0x42800000, v58
	v_mul_f32_e32 v1, 0x42800000, v62
	v_med3_f32 v0, v0, s66, v90
	v_med3_f32 v1, v1, s66, v90
	v_cvt_pk_fp8_f32 v100, v0, v1
	v_mul_f32_e32 v4, 0x42800000, v66
	v_mul_f32_e32 v0, 0x42800000, v54
	v_med3_f32 v1, v4, s66, v90
	v_med3_f32 v0, v0, s66, v90
	v_cvt_pk_fp8_f32 v100, v1, v0 op_sel:[0,0,1]
	v_mul_f32_e32 v0, 0x42800000, v42
	v_mul_f32_e32 v1, 0x42800000, v46
	v_med3_f32 v0, v0, s66, v90
	v_med3_f32 v1, v1, s66, v90
	v_cvt_pk_fp8_f32 v101, v0, v1
	v_mul_f32_e32 v4, 0x42800000, v50
	v_mul_f32_e32 v0, 0x42800000, v38
	v_med3_f32 v1, v4, s66, v90
	v_med3_f32 v0, v0, s66, v90
	v_cvt_pk_fp8_f32 v101, v1, v0 op_sel:[0,0,1]
	v_mul_f32_e32 v0, 0x42800000, v26
	v_mul_f32_e32 v1, 0x42800000, v30
	v_med3_f32 v0, v0, s66, v90
	v_med3_f32 v1, v1, s66, v90
	v_cvt_pk_fp8_f32 v102, v0, v1
	v_mul_f32_e32 v4, 0x42800000, v34
	v_mul_f32_e32 v0, 0x42800000, v22
	v_med3_f32 v1, v4, s66, v90
	v_med3_f32 v0, v0, s66, v90
	v_cvt_pk_fp8_f32 v102, v1, v0 op_sel:[0,0,1]
	v_mul_f32_e32 v0, 0x42800000, v6
	v_mul_f32_e32 v1, 0x42800000, v14
	v_med3_f32 v0, v0, s66, v90
	v_med3_f32 v1, v1, s66, v90
	v_cvt_pk_fp8_f32 v103, v0, v1
	v_mul_f32_e32 v4, 0x42800000, v18
	v_mul_f32_e32 v0, 0x42800000, v2
	v_med3_f32 v1, v4, s66, v90
	v_med3_f32 v0, v0, s66, v90
	v_cvt_pk_fp8_f32 v103, v1, v0 op_sel:[0,0,1]
	v_mul_f32_e32 v0, 0x42800000, v59
	v_mul_f32_e32 v1, 0x42800000, v63
	v_med3_f32 v0, v0, s66, v90
	v_med3_f32 v1, v1, s66, v90
	v_mov_b32_e32 v4, v69
	v_cvt_pk_fp8_f32 v4, v0, v1
	v_mul_f32_e32 v2, 0x42800000, v67
	v_mul_f32_e32 v0, 0x42800000, v55
	v_med3_f32 v1, v2, s66, v90
	v_med3_f32 v0, v0, s66, v90
	v_cvt_pk_fp8_f32 v4, v1, v0 op_sel:[0,0,1]
	v_mul_f32_e32 v0, 0x42800000, v43
	v_mul_f32_e32 v1, 0x42800000, v47
	v_med3_f32 v0, v0, s66, v90
	v_med3_f32 v1, v1, s66, v90
	v_mov_b32_e32 v5, v69
	v_cvt_pk_fp8_f32 v5, v0, v1
	v_mul_f32_e32 v2, 0x42800000, v51
	v_mul_f32_e32 v0, 0x42800000, v39
	v_med3_f32 v1, v2, s66, v90
	v_med3_f32 v0, v0, s66, v90
	v_cvt_pk_fp8_f32 v5, v1, v0 op_sel:[0,0,1]
	v_mul_f32_e32 v0, 0x42800000, v27
	v_mul_f32_e32 v1, 0x42800000, v31
	v_med3_f32 v0, v0, s66, v90
	v_med3_f32 v1, v1, s66, v90
	v_mov_b32_e32 v6, v69
	v_cvt_pk_fp8_f32 v6, v0, v1
	v_mul_f32_e32 v2, 0x42800000, v35
	v_mul_f32_e32 v0, 0x42800000, v23
	v_cvt_pk_fp8_f32 v10, v24, v28
	v_med3_f32 v1, v2, s66, v90
	v_med3_f32 v0, v0, s66, v90
	v_cvt_pk_fp8_f32 v96, v57, v61
	v_cvt_pk_fp8_f32 v6, v1, v0 op_sel:[0,0,1]
	v_mul_f32_e32 v0, 0x42800000, v7
	v_mul_f32_e32 v1, 0x42800000, v15
	v_mul_f32_e32 v64, 0x42800000, v64
	v_mul_f32_e32 v52, 0x42800000, v52
	v_mul_f32_e32 v48, 0x42800000, v48
	v_mul_f32_e32 v36, 0x42800000, v36
	v_mul_f32_e32 v32, 0x42800000, v32
	v_mul_f32_e32 v20, 0x42800000, v20
	v_med3_f32 v0, v0, s66, v90
	v_med3_f32 v1, v1, s66, v90
	v_mov_b32_e32 v7, v69
	v_mul_f32_e32 v65, 0x42800000, v65
	v_med3_f32 v64, v64, s66, v90
	v_mul_f32_e32 v53, 0x42800000, v53
	v_med3_f32 v52, v52, s66, v90
	v_med3_f32 v48, v48, s66, v90
	v_med3_f32 v36, v36, s66, v90
	v_med3_f32 v32, v32, s66, v90
	v_med3_f32 v20, v20, s66, v90
	v_cvt_pk_fp8_f32 v7, v0, v1
	v_med3_f32 v56, v65, s66, v90
	v_med3_f32 v53, v53, s66, v90
	v_cvt_pk_fp8_f32 v8, v64, v52 op_sel:[0,0,1]
	v_cvt_pk_fp8_f32 v9, v48, v36 op_sel:[0,0,1]
	v_cvt_pk_fp8_f32 v10, v32, v20 op_sel:[0,0,1]
	v_cvt_pk_fp8_f32 v96, v56, v53 op_sel:[0,0,1]
	v_mul_f32_e32 v2, 0x42800000, v19
	v_mul_f32_e32 v0, 0x42800000, v3
	v_med3_f32 v1, v2, s66, v90
	v_med3_f32 v0, v0, s66, v90
	v_cvt_pk_fp8_f32 v7, v1, v0 op_sel:[0,0,1]
	ds_write_b128 v87, v[8:11] offset:40960
	ds_write_b128 v87, v[96:99] offset:41040
	ds_write_b128 v87, v[100:103] offset:41120
	ds_write_b128 v87, v[4:7] offset:41200
	s_waitcnt lgkmcnt(0)
	ds_read_b128 v[0:3], v88 offset:40960
	v_or_b32_e32 v4, s13, v75
	v_ashrrev_i32_e32 v5, 31, v4
	v_lshl_add_u64 v[8:9], s[26:27], 0, v[70:71]
	v_lshlrev_b64 v[4:5], 11, v[4:5]
	v_lshl_add_u64 v[10:11], v[8:9], 0, v[4:5]
	ds_read_b128 v[4:7], v88 offset:42240
	s_waitcnt lgkmcnt(0)
	global_store_dwordx4 v[10:11], v[0:3], off sc1
	s_cselect_b64 s[26:27], -1, 0
	s_nop 0
	v_or_b32_e32 v0, s13, v76
	v_ashrrev_i32_e32 v1, 31, v0
	v_lshlrev_b64 v[0:1], 11, v[0:1]
	v_lshl_add_u64 v[0:1], v[8:9], 0, v[0:1]
	global_store_dwordx4 v[0:1], v[4:7], off sc1
	ds_read_b128 v[0:3], v88 offset:43520
	s_nop 0
	v_or_b32_e32 v4, s13, v77
	v_ashrrev_i32_e32 v5, 31, v4
	v_lshlrev_b64 v[4:5], 11, v[4:5]
	v_lshl_add_u64 v[10:11], v[8:9], 0, v[4:5]
	ds_read_b128 v[4:7], v88 offset:44800
	s_waitcnt lgkmcnt(1)
	global_store_dwordx4 v[10:11], v[0:3], off sc1
	s_nop 1
	v_or_b32_e32 v0, s13, v78
	v_ashrrev_i32_e32 v1, 31, v0
	v_lshlrev_b64 v[0:1], 11, v[0:1]
	v_lshl_add_u64 v[0:1], v[8:9], 0, v[0:1]
	s_waitcnt lgkmcnt(0)
	global_store_dwordx4 v[0:1], v[4:7], off sc1
	s_waitcnt lgkmcnt(0)
	s_andn2_b64 vcc, exec, s[26:27]
	s_cbranch_vccz .LBB0_2536
	s_branch .LBB0_2560

.LBB0_2536:
	s_andn2_b64 vcc, exec, s[24:25]
	s_cbranch_vccnz .LBB0_2538
	s_ashr_i32 s3, s2, 31
	s_lshl_b64 s[24:25], s[2:3], 22
	s_add_u32 s3, s54, s24
	s_addc_u32 s21, s55, s25
	v_or_b32_e32 v0, s22, v74
	s_add_u32 s3, s3, s18
	v_mul_hi_i32_i24_e32 v1, s16, v0
	v_mul_i32_i24_e32 v0, s16, v0
	s_addc_u32 s23, s21, s19
	v_lshl_add_u64 v[0:1], v[0:1], 2, s[6:7]
	s_ashr_i32 s21, s20, 31
	v_lshl_add_u64 v[0:1], s[20:21], 2, v[0:1]
	v_mov_b32_e32 v73, v69
	v_lshl_add_u64 v[0:1], v[0:1], 0, v[72:73]
	s_lshl_b64 s[24:25], s[16:17], 2
	global_load_dwordx4 v[56:59], v[0:1], off nt
	v_lshl_add_u64 v[0:1], v[0:1], 0, s[24:25]
	global_load_dwordx4 v[60:63], v[0:1], off nt
	v_lshl_add_u64 v[0:1], v[0:1], 0, s[24:25]
	global_load_dwordx4 v[64:67], v[0:1], off nt
	v_lshl_add_u64 v[0:1], v[0:1], 0, s[24:25]
	global_load_dwordx4 v[52:55], v[0:1], off nt
	v_lshl_add_u64 v[0:1], v[0:1], 0, s[24:25]
	global_load_dwordx4 v[40:43], v[0:1], off nt
	v_lshl_add_u64 v[0:1], v[0:1], 0, s[24:25]
	global_load_dwordx4 v[44:47], v[0:1], off nt
	v_lshl_add_u64 v[0:1], v[0:1], 0, s[24:25]
	global_load_dwordx4 v[48:51], v[0:1], off nt
	v_lshl_add_u64 v[0:1], v[0:1], 0, s[24:25]
	global_load_dwordx4 v[36:39], v[0:1], off nt
	v_lshl_add_u64 v[0:1], v[0:1], 0, s[24:25]
	global_load_dwordx4 v[24:27], v[0:1], off nt
	v_lshl_add_u64 v[0:1], v[0:1], 0, s[24:25]
	global_load_dwordx4 v[28:31], v[0:1], off nt
	v_lshl_add_u64 v[0:1], v[0:1], 0, s[24:25]
	global_load_dwordx4 v[32:35], v[0:1], off nt
	v_lshl_add_u64 v[0:1], v[0:1], 0, s[24:25]
	global_load_dwordx4 v[20:23], v[0:1], off nt
	v_lshl_add_u64 v[0:1], v[0:1], 0, s[24:25]
	global_load_dwordx4 v[4:7], v[0:1], off nt
	v_lshl_add_u64 v[0:1], v[0:1], 0, s[24:25]
	global_load_dwordx4 v[12:15], v[0:1], off nt
	v_lshl_add_u64 v[0:1], v[0:1], 0, s[24:25]
	global_load_dwordx4 v[16:19], v[0:1], off nt
	v_lshl_add_u64 v[0:1], v[0:1], 0, s[24:25]
	global_load_dwordx4 v[0:3], v[0:1], off nt
	v_mov_b32_e32 v11, v69
	v_mov_b32_e32 v97, v69
	v_mov_b32_e32 v98, v69
	v_mov_b32_e32 v99, v69
	v_mov_b32_e32 v100, v69
	v_mov_b32_e32 v101, v69
	v_mov_b32_e32 v102, v69
	v_mov_b32_e32 v103, v69
	v_mov_b32_e32 v8, v69
	v_mov_b32_e32 v9, v69
	v_mov_b32_e32 v10, v69
	v_mov_b32_e32 v96, v69
	s_ashr_i32 s21, s22, 31
	s_add_u32 s24, s3, s22
	s_addc_u32 s25, s23, s21
	s_add_i32 s92, s92, 0x13e46
	s_cmpk_lt_u32 s92, 0xf97f
	s_waitcnt vmcnt(0)
	v_mul_f32_e32 v56, 0x42800000, v56
	v_mul_f32_e32 v57, 0x42800000, v57
	v_mul_f32_e32 v60, 0x42800000, v60
	v_med3_f32 v56, v56, s66, v90
	v_mul_f32_e32 v61, 0x42800000, v61
	v_med3_f32 v60, v60, s66, v90
	v_med3_f32 v57, v57, s66, v90
	v_med3_f32 v61, v61, s66, v90
	v_mul_f32_e32 v41, 0x42800000, v41
	v_med3_f32 v41, v41, s66, v90
	v_mul_f32_e32 v45, 0x42800000, v45
	v_med3_f32 v45, v45, s66, v90
	v_cvt_pk_fp8_f32 v97, v41, v45
	v_mul_f32_e32 v49, 0x42800000, v49
	v_mul_f32_e32 v40, 0x42800000, v40
	v_mul_f32_e32 v44, 0x42800000, v44
	v_mul_f32_e32 v24, 0x42800000, v24
	v_med3_f32 v40, v40, s66, v90
	v_mul_f32_e32 v28, 0x42800000, v28
	v_med3_f32 v44, v44, s66, v90
	v_med3_f32 v24, v24, s66, v90
	v_med3_f32 v28, v28, s66, v90
	v_cvt_pk_fp8_f32 v8, v56, v60
	v_cvt_pk_fp8_f32 v9, v40, v44
	v_mul_f32_e32 v4, 0x42800000, v4
	v_med3_f32 v4, v4, s66, v90
	v_mul_f32_e32 v12, 0x42800000, v12
	v_med3_f32 v12, v12, s66, v90
	v_cvt_pk_fp8_f32 v11, v4, v12
	v_mul_f32_e32 v16, 0x42800000, v16
	v_mul_f32_e32 v0, 0x42800000, v0
	v_med3_f32 v4, v16, s66, v90
	v_med3_f32 v0, v0, s66, v90
	v_cvt_pk_fp8_f32 v11, v4, v0 op_sel:[0,0,1]
	v_mul_f32_e32 v0, 0x42800000, v37
	v_med3_f32 v4, v49, s66, v90
	v_med3_f32 v0, v0, s66, v90
	v_cvt_pk_fp8_f32 v97, v4, v0 op_sel:[0,0,1]
	v_mul_f32_e32 v0, 0x42800000, v25
	v_mul_f32_e32 v4, 0x42800000, v29
	v_med3_f32 v0, v0, s66, v90
	v_med3_f32 v4, v4, s66, v90
	v_cvt_pk_fp8_f32 v98, v0, v4
	v_mul_f32_e32 v12, 0x42800000, v33
	v_mul_f32_e32 v0, 0x42800000, v21
	v_med3_f32 v4, v12, s66, v90
	v_med3_f32 v0, v0, s66, v90
	v_cvt_pk_fp8_f32 v98, v4, v0 op_sel:[0,0,1]
	v_mul_f32_e32 v0, 0x42800000, v5
	v_mul_f32_e32 v4, 0x42800000, v13
	v_med3_f32 v0, v0, s66, v90
	v_med3_f32 v4, v4, s66, v90
	v_cvt_pk_fp8_f32 v99, v0, v4
	v_mul_f32_e32 v5, 0x42800000, v17
	v_mul_f32_e32 v0, 0x42800000, v1
	v_med3_f32 v1, v5, s66, v90
	v_med3_f32 v0, v0, s66, v90
	v_cvt_pk_fp8_f32 v99, v1, v0 op_sel:[0,0,1]
	v_mul_f32_e32 v0, 0x42800000, v58
	v_mul_f32_e32 v1, 0x42800000, v62
	v_med3_f32 v0, v0, s66, v90
	v_med3_f32 v1, v1, s66, v90
	v_cvt_pk_fp8_f32 v100, v0, v1
	v_mul_f32_e32 v4, 0x42800000, v66
	v_mul_f32_e32 v0, 0x42800000, v54
	v_med3_f32 v1, v4, s66, v90
	v_med3_f32 v0, v0, s66, v90
	v_cvt_pk_fp8_f32 v100, v1, v0 op_sel:[0,0,1]
	v_mul_f32_e32 v0, 0x42800000, v42
	v_mul_f32_e32 v1, 0x42800000, v46
	v_med3_f32 v0, v0, s66, v90
	v_med3_f32 v1, v1, s66, v90
	v_cvt_pk_fp8_f32 v101, v0, v1
	v_mul_f32_e32 v4, 0x42800000, v50
	v_mul_f32_e32 v0, 0x42800000, v38
	v_med3_f32 v1, v4, s66, v90
	v_med3_f32 v0, v0, s66, v90
	v_cvt_pk_fp8_f32 v101, v1, v0 op_sel:[0,0,1]
	v_mul_f32_e32 v0, 0x42800000, v26
	v_mul_f32_e32 v1, 0x42800000, v30
	v_med3_f32 v0, v0, s66, v90
	v_med3_f32 v1, v1, s66, v90
	v_cvt_pk_fp8_f32 v102, v0, v1
	v_mul_f32_e32 v4, 0x42800000, v34
	v_mul_f32_e32 v0, 0x42800000, v22
	v_med3_f32 v1, v4, s66, v90
	v_med3_f32 v0, v0, s66, v90
	v_cvt_pk_fp8_f32 v102, v1, v0 op_sel:[0,0,1]
	v_mul_f32_e32 v0, 0x42800000, v6
	v_mul_f32_e32 v1, 0x42800000, v14
	v_med3_f32 v0, v0, s66, v90
	v_med3_f32 v1, v1, s66, v90
	v_cvt_pk_fp8_f32 v103, v0, v1
	v_mul_f32_e32 v4, 0x42800000, v18
	v_mul_f32_e32 v0, 0x42800000, v2
	v_med3_f32 v1, v4, s66, v90
	v_med3_f32 v0, v0, s66, v90
	v_cvt_pk_fp8_f32 v103, v1, v0 op_sel:[0,0,1]
	v_mul_f32_e32 v0, 0x42800000, v59
	v_mul_f32_e32 v1, 0x42800000, v63
	v_med3_f32 v0, v0, s66, v90
	v_med3_f32 v1, v1, s66, v90
	v_mov_b32_e32 v4, v69
	v_cvt_pk_fp8_f32 v4, v0, v1
	v_mul_f32_e32 v2, 0x42800000, v67
	v_mul_f32_e32 v0, 0x42800000, v55
	v_med3_f32 v1, v2, s66, v90
	v_med3_f32 v0, v0, s66, v90
	v_cvt_pk_fp8_f32 v4, v1, v0 op_sel:[0,0,1]
	v_mul_f32_e32 v0, 0x42800000, v43
	v_mul_f32_e32 v1, 0x42800000, v47
	v_med3_f32 v0, v0, s66, v90
	v_med3_f32 v1, v1, s66, v90
	v_mov_b32_e32 v5, v69
	v_cvt_pk_fp8_f32 v5, v0, v1
	v_mul_f32_e32 v2, 0x42800000, v51
	v_mul_f32_e32 v0, 0x42800000, v39
	v_med3_f32 v1, v2, s66, v90
	v_med3_f32 v0, v0, s66, v90
	v_cvt_pk_fp8_f32 v5, v1, v0 op_sel:[0,0,1]
	v_mul_f32_e32 v0, 0x42800000, v27
	v_mul_f32_e32 v1, 0x42800000, v31
	v_med3_f32 v0, v0, s66, v90
	v_med3_f32 v1, v1, s66, v90
	v_mov_b32_e32 v6, v69
	v_cvt_pk_fp8_f32 v6, v0, v1
	v_mul_f32_e32 v2, 0x42800000, v35
	v_mul_f32_e32 v0, 0x42800000, v23
	v_cvt_pk_fp8_f32 v10, v24, v28
	v_med3_f32 v1, v2, s66, v90
	v_med3_f32 v0, v0, s66, v90
	v_cvt_pk_fp8_f32 v96, v57, v61
	v_cvt_pk_fp8_f32 v6, v1, v0 op_sel:[0,0,1]
	v_mul_f32_e32 v0, 0x42800000, v7
	v_mul_f32_e32 v1, 0x42800000, v15
	v_mul_f32_e32 v64, 0x42800000, v64
	v_mul_f32_e32 v52, 0x42800000, v52
	v_mul_f32_e32 v48, 0x42800000, v48
	v_mul_f32_e32 v36, 0x42800000, v36
	v_mul_f32_e32 v32, 0x42800000, v32
	v_mul_f32_e32 v20, 0x42800000, v20
	v_med3_f32 v0, v0, s66, v90
	v_med3_f32 v1, v1, s66, v90
	v_mov_b32_e32 v7, v69
	v_mul_f32_e32 v65, 0x42800000, v65
	v_med3_f32 v64, v64, s66, v90
	v_mul_f32_e32 v53, 0x42800000, v53
	v_med3_f32 v52, v52, s66, v90
	v_med3_f32 v48, v48, s66, v90
	v_med3_f32 v36, v36, s66, v90
	v_med3_f32 v32, v32, s66, v90
	v_med3_f32 v20, v20, s66, v90
	v_cvt_pk_fp8_f32 v7, v0, v1
	v_med3_f32 v56, v65, s66, v90
	v_med3_f32 v53, v53, s66, v90
	v_cvt_pk_fp8_f32 v8, v64, v52 op_sel:[0,0,1]
	v_cvt_pk_fp8_f32 v9, v48, v36 op_sel:[0,0,1]
	v_cvt_pk_fp8_f32 v10, v32, v20 op_sel:[0,0,1]
	v_cvt_pk_fp8_f32 v96, v56, v53 op_sel:[0,0,1]
	v_mul_f32_e32 v2, 0x42800000, v19
	v_mul_f32_e32 v0, 0x42800000, v3
	v_med3_f32 v1, v2, s66, v90
	v_med3_f32 v0, v0, s66, v90
	v_cvt_pk_fp8_f32 v7, v1, v0 op_sel:[0,0,1]
	ds_write_b128 v87, v[8:11] offset:40960
	ds_write_b128 v87, v[96:99] offset:41040
	ds_write_b128 v87, v[100:103] offset:41120
	ds_write_b128 v87, v[4:7] offset:41200
	s_waitcnt lgkmcnt(0)
	ds_read_b128 v[0:3], v88 offset:40960
	v_or_b32_e32 v4, s13, v75
	v_ashrrev_i32_e32 v5, 31, v4
	v_lshl_add_u64 v[8:9], s[24:25], 0, v[70:71]
	v_lshlrev_b64 v[4:5], 11, v[4:5]
	v_lshl_add_u64 v[10:11], v[8:9], 0, v[4:5]
	ds_read_b128 v[4:7], v88 offset:42240
	s_waitcnt lgkmcnt(0)
	global_store_dwordx4 v[10:11], v[0:3], off sc1
	s_cselect_b64 s[24:25], -1, 0
	s_nop 0
	v_or_b32_e32 v0, s13, v76
	v_ashrrev_i32_e32 v1, 31, v0
	v_lshlrev_b64 v[0:1], 11, v[0:1]
	v_lshl_add_u64 v[0:1], v[8:9], 0, v[0:1]
	global_store_dwordx4 v[0:1], v[4:7], off sc1
	ds_read_b128 v[0:3], v88 offset:43520
	s_nop 0
	v_or_b32_e32 v4, s13, v77
	v_ashrrev_i32_e32 v5, 31, v4
	v_lshlrev_b64 v[4:5], 11, v[4:5]
	v_lshl_add_u64 v[10:11], v[8:9], 0, v[4:5]
	ds_read_b128 v[4:7], v88 offset:44800
	s_waitcnt lgkmcnt(1)
	global_store_dwordx4 v[10:11], v[0:3], off sc1
	s_nop 1
	v_or_b32_e32 v0, s13, v78
	v_ashrrev_i32_e32 v1, 31, v0
	v_lshlrev_b64 v[0:1], 11, v[0:1]
	v_lshl_add_u64 v[0:1], v[8:9], 0, v[0:1]
	s_waitcnt lgkmcnt(0)
	global_store_dwordx4 v[0:1], v[4:7], off sc1
	s_waitcnt lgkmcnt(0)
	s_andn2_b64 vcc, exec, s[24:25]
	s_cbranch_vccz .LBB0_2539
	s_branch .LBB0_2560
